# taps GEMM epilogue: 8 decay-rate loads issued together (with the 2-wait-state pad after 128-bit stores); one missing VALU-SGPR wait state restored after the packed-op folding
# speedup vs baseline: 1.0129x; 1.0014x over previous
.LBB0_188:
	s_add_u32 s27, s18, s26
	s_addc_u32 s37, s19, 0
	s_add_u32 s30, s27, 0x100
	s_addc_u32 s31, s37, 0
	s_and_b64 s[28:29], s[24:25], exec
	s_cselect_b32 s31, s11, s31
	s_cselect_b32 s30, s57, s30
	s_add_u32 s26, s20, s26
	s_addc_u32 s28, s21, 0
	s_add_u32 s26, s26, 0x100
	s_addc_u32 s28, s28, 0
	s_and_b64 s[24:25], s[24:25], exec
	s_cselect_b32 s35, s9, s28
	s_cselect_b32 s34, s58, s26
	s_add_u32 s36, s27, 0x10080
	s_addc_u32 s37, s37, 0
	s_add_i32 s68, s54, s44
	s_add_i32 m0, s17, 0xc000
	s_add_i32 s69, s17, 0xe000
	s_add_i32 s67, s68, 0x2000
	s_add_u32 s28, s34, 0x10000
	s_addc_u32 s29, s35, 0
	s_add_i32 s66, s55, s44
	ds_read_b128 v[144:147], v151
	ds_read_b128 v[156:159], v151 offset:1024
	ds_read_b128 v[160:163], v151 offset:2048
	ds_read_b128 v[164:167], v151 offset:3072
	s_add_i32 s65, s66, 0x2000
	s_add_i32 s64, 0, 0x18000
	s_add_u32 s26, s30, 0x10000
	s_addc_u32 s27, s31, 0
	s_add_i32 s63, s64, s44
	s_add_i32 s62, 0, 0x1c000
	s_add_i32 s61, s63, 0x2000
	s_add_u32 s24, s34, 0x10080
	s_addc_u32 s25, s35, 0
	s_add_i32 s60, s62, s44
	s_add_i32 s59, s60, 0x2000
	v_lshl_add_u64 v[148:149], s[36:37], 0, v[136:137]
	ds_read_b128 v[168:171], v152
	ds_read_b128 v[172:175], v152 offset:1024
	ds_read_b128 v[176:179], v152 offset:2048
	ds_read_b128 v[180:183], v152 offset:3072
	ds_read_b128 v[184:187], v152 offset:4096
	ds_read_b128 v[192:195], v152 offset:5120
	ds_read_b128 v[196:199], v152 offset:6144
	ds_read_b128 v[200:203], v152 offset:7168
	global_load_lds_dwordx4 v[148:149], off
	v_lshl_add_u64 v[148:149], s[36:37], 0, v[132:133]
	s_mov_b32 m0, s69
	s_nop 0
	global_load_lds_dwordx4 v[148:149], off
	s_waitcnt lgkmcnt(8)
	s_barrier
	s_waitcnt lgkmcnt(0)
	s_setprio 1
	s_waitcnt lgkmcnt(0)
	v_mfma_f32_16x16x32_bf16 v[126:129], v[144:147], v[168:171], v[126:129]
	v_mfma_f32_16x16x32_bf16 v[122:125], v[160:163], v[168:171], v[122:125]
	v_mfma_f32_16x16x32_bf16 v[110:113], v[144:147], v[176:179], v[110:113]
	v_mfma_f32_16x16x32_bf16 v[106:109], v[160:163], v[176:179], v[106:109]
	v_mfma_f32_16x16x32_bf16 v[94:97], v[144:147], v[184:187], v[94:97]
	v_mfma_f32_16x16x32_bf16 v[90:93], v[160:163], v[184:187], v[90:93]
	v_mfma_f32_16x16x32_bf16 v[78:81], v[144:147], v[196:199], v[78:81]
	v_mfma_f32_16x16x32_bf16 v[74:77], v[160:163], v[196:199], v[74:77]
	v_mfma_f32_16x16x32_bf16 v[126:129], v[156:159], v[172:175], v[126:129]
	v_mfma_f32_16x16x32_bf16 v[122:125], v[164:167], v[172:175], v[122:125]
	v_mfma_f32_16x16x32_bf16 v[110:113], v[156:159], v[180:183], v[110:113]
	v_mfma_f32_16x16x32_bf16 v[106:109], v[164:167], v[180:183], v[106:109]
	v_mfma_f32_16x16x32_bf16 v[94:97], v[156:159], v[192:195], v[94:97]
	v_mfma_f32_16x16x32_bf16 v[90:93], v[164:167], v[192:195], v[90:93]
	v_mfma_f32_16x16x32_bf16 v[78:81], v[156:159], v[200:203], v[78:81]
	v_mfma_f32_16x16x32_bf16 v[74:77], v[164:167], v[200:203], v[74:77]
	s_setprio 0
	s_barrier
	s_mov_b32 m0, s68
	v_lshl_add_u64 v[148:149], s[34:35], 0, v[138:139]
	ds_read_b128 v[204:207], v153
	ds_read_b128 v[208:211], v153 offset:1024
	ds_read_b128 v[212:215], v153 offset:2048
	ds_read_b128 v[216:219], v153 offset:3072
	global_load_lds_dwordx4 v[148:149], off
	v_lshl_add_u64 v[188:189], s[34:35], 0, v[134:135]
	s_mov_b32 m0, s67
	s_nop 0
	global_load_lds_dwordx4 v[188:189], off
	s_barrier
	s_waitcnt lgkmcnt(0)
	s_setprio 1
	s_waitcnt lgkmcnt(0)
	v_mfma_f32_16x16x32_bf16 v[118:121], v[204:207], v[168:171], v[118:121]
	v_mfma_f32_16x16x32_bf16 v[114:117], v[212:215], v[168:171], v[114:117]
	v_mfma_f32_16x16x32_bf16 v[102:105], v[204:207], v[176:179], v[102:105]
	v_mfma_f32_16x16x32_bf16 v[98:101], v[212:215], v[176:179], v[98:101]
	v_mfma_f32_16x16x32_bf16 v[86:89], v[204:207], v[184:187], v[86:89]
	v_mfma_f32_16x16x32_bf16 v[82:85], v[212:215], v[184:187], v[82:85]
	v_mfma_f32_16x16x32_bf16 v[70:73], v[204:207], v[196:199], v[70:73]
	v_mfma_f32_16x16x32_bf16 v[66:69], v[212:215], v[196:199], v[66:69]
	v_mfma_f32_16x16x32_bf16 v[118:121], v[208:211], v[172:175], v[118:121]
	v_mfma_f32_16x16x32_bf16 v[114:117], v[216:219], v[172:175], v[114:117]
	v_mfma_f32_16x16x32_bf16 v[102:105], v[208:211], v[180:183], v[102:105]
	v_mfma_f32_16x16x32_bf16 v[98:101], v[216:219], v[180:183], v[98:101]
	v_mfma_f32_16x16x32_bf16 v[86:89], v[208:211], v[192:195], v[86:89]
	v_mfma_f32_16x16x32_bf16 v[82:85], v[216:219], v[192:195], v[82:85]
	v_mfma_f32_16x16x32_bf16 v[70:73], v[208:211], v[200:203], v[70:73]
	v_mfma_f32_16x16x32_bf16 v[66:69], v[216:219], v[200:203], v[66:69]
	s_setprio 0
	s_mov_b32 m0, s17
	v_lshl_add_u64 v[190:191], s[30:31], 0, v[136:137]
	s_barrier
	ds_read_b128 v[168:171], v152 offset:16384
	ds_read_b128 v[172:175], v152 offset:17408
	ds_read_b128 v[176:179], v152 offset:18432
	ds_read_b128 v[180:183], v152 offset:19456
	ds_read_b128 v[184:187], v152 offset:20480
	ds_read_b128 v[192:195], v152 offset:21504
	ds_read_b128 v[196:199], v152 offset:22528
	ds_read_b128 v[200:203], v152 offset:23552
	global_load_lds_dwordx4 v[190:191], off
	v_lshl_add_u64 v[220:221], s[30:31], 0, v[132:133]
	s_mov_b32 m0, s47
	s_nop 0
	global_load_lds_dwordx4 v[220:221], off
	s_barrier
	s_waitcnt lgkmcnt(0)
	s_setprio 1
	s_waitcnt lgkmcnt(0)
	v_mfma_f32_16x16x32_bf16 v[62:65], v[144:147], v[168:171], v[62:65]
	v_mfma_f32_16x16x32_bf16 v[58:61], v[160:163], v[168:171], v[58:61]
	v_mfma_f32_16x16x32_bf16 v[46:49], v[144:147], v[176:179], v[46:49]
	v_mfma_f32_16x16x32_bf16 v[42:45], v[160:163], v[176:179], v[42:45]
	v_mfma_f32_16x16x32_bf16 v[30:33], v[144:147], v[184:187], v[30:33]
	v_mfma_f32_16x16x32_bf16 v[26:29], v[160:163], v[184:187], v[26:29]
	v_mfma_f32_16x16x32_bf16 v[14:17], v[144:147], v[196:199], v[14:17]
	v_mfma_f32_16x16x32_bf16 v[10:13], v[160:163], v[196:199], v[10:13]
	v_mfma_f32_16x16x32_bf16 v[62:65], v[156:159], v[172:175], v[62:65]
	v_mfma_f32_16x16x32_bf16 v[58:61], v[164:167], v[172:175], v[58:61]
	v_mfma_f32_16x16x32_bf16 v[46:49], v[156:159], v[180:183], v[46:49]
	v_mfma_f32_16x16x32_bf16 v[42:45], v[164:167], v[180:183], v[42:45]
	v_mfma_f32_16x16x32_bf16 v[30:33], v[156:159], v[192:195], v[30:33]
	v_mfma_f32_16x16x32_bf16 v[26:29], v[164:167], v[192:195], v[26:29]
	v_mfma_f32_16x16x32_bf16 v[14:17], v[156:159], v[200:203], v[14:17]
	v_mfma_f32_16x16x32_bf16 v[10:13], v[164:167], v[200:203], v[10:13]
	s_setprio 0
	s_barrier
	s_mov_b32 m0, s66
	v_lshl_add_u64 v[144:145], s[28:29], 0, v[138:139]
	global_load_lds_dwordx4 v[144:145], off
	v_lshl_add_u64 v[144:145], s[28:29], 0, v[134:135]
	s_mov_b32 m0, s65
	s_nop 0
	global_load_lds_dwordx4 v[144:145], off
	s_waitcnt vmcnt(6)
	s_barrier
	s_setprio 1
	v_mfma_f32_16x16x32_bf16 v[54:57], v[204:207], v[168:171], v[54:57]
	v_mfma_f32_16x16x32_bf16 v[50:53], v[212:215], v[168:171], v[50:53]
	v_mfma_f32_16x16x32_bf16 v[38:41], v[204:207], v[176:179], v[38:41]
	v_mfma_f32_16x16x32_bf16 v[34:37], v[212:215], v[176:179], v[34:37]
	v_mfma_f32_16x16x32_bf16 v[22:25], v[204:207], v[184:187], v[22:25]
	v_mfma_f32_16x16x32_bf16 v[18:21], v[212:215], v[184:187], v[18:21]
	v_mfma_f32_16x16x32_bf16 v[6:9], v[204:207], v[196:199], v[6:9]
	v_mfma_f32_16x16x32_bf16 v[2:5], v[212:215], v[196:199], v[2:5]
	v_mfma_f32_16x16x32_bf16 v[54:57], v[208:211], v[172:175], v[54:57]
	v_mfma_f32_16x16x32_bf16 v[50:53], v[216:219], v[172:175], v[50:53]
	v_mfma_f32_16x16x32_bf16 v[38:41], v[208:211], v[180:183], v[38:41]
	v_mfma_f32_16x16x32_bf16 v[34:37], v[216:219], v[180:183], v[34:37]
	v_mfma_f32_16x16x32_bf16 v[22:25], v[208:211], v[192:195], v[22:25]
	v_mfma_f32_16x16x32_bf16 v[18:21], v[216:219], v[192:195], v[18:21]
	v_mfma_f32_16x16x32_bf16 v[6:9], v[208:211], v[200:203], v[6:9]
	v_mfma_f32_16x16x32_bf16 v[2:5], v[216:219], v[200:203], v[2:5]
	s_setprio 0
	v_add_u32_e32 v164, s64, v131
	s_barrier
	ds_read_b128 v[144:147], v164
	ds_read_b128 v[156:159], v164 offset:1024
	ds_read_b128 v[160:163], v164 offset:2048
	ds_read_b128 v[164:167], v164 offset:3072
	s_mov_b32 m0, s48
	v_lshl_add_u64 v[204:205], s[26:27], 0, v[136:137]
	ds_read_b128 v[168:171], v152 offset:32768
	ds_read_b128 v[172:175], v152 offset:33792
	ds_read_b128 v[176:179], v152 offset:34816
	ds_read_b128 v[180:183], v152 offset:35840
	ds_read_b128 v[184:187], v152 offset:36864
	ds_read_b128 v[192:195], v152 offset:37888
	ds_read_b128 v[196:199], v152 offset:38912
	ds_read_b128 v[200:203], v152 offset:39936
	global_load_lds_dwordx4 v[204:205], off
	v_lshl_add_u64 v[204:205], s[26:27], 0, v[132:133]
	s_mov_b32 m0, s49
	s_nop 0
	global_load_lds_dwordx4 v[204:205], off
	s_waitcnt lgkmcnt(8)
	s_barrier
	s_waitcnt lgkmcnt(0)
	s_setprio 1
	s_waitcnt lgkmcnt(0)
	v_mfma_f32_16x16x32_bf16 v[126:129], v[144:147], v[168:171], v[126:129]
	v_mfma_f32_16x16x32_bf16 v[122:125], v[160:163], v[168:171], v[122:125]
	v_mfma_f32_16x16x32_bf16 v[110:113], v[144:147], v[176:179], v[110:113]
	v_mfma_f32_16x16x32_bf16 v[106:109], v[160:163], v[176:179], v[106:109]
	v_mfma_f32_16x16x32_bf16 v[94:97], v[144:147], v[184:187], v[94:97]
	v_mfma_f32_16x16x32_bf16 v[90:93], v[160:163], v[184:187], v[90:93]
	v_mfma_f32_16x16x32_bf16 v[78:81], v[144:147], v[196:199], v[78:81]
	v_mfma_f32_16x16x32_bf16 v[74:77], v[160:163], v[196:199], v[74:77]
	v_mfma_f32_16x16x32_bf16 v[126:129], v[156:159], v[172:175], v[126:129]
	v_mfma_f32_16x16x32_bf16 v[122:125], v[164:167], v[172:175], v[122:125]
	v_mfma_f32_16x16x32_bf16 v[110:113], v[156:159], v[180:183], v[110:113]
	v_mfma_f32_16x16x32_bf16 v[106:109], v[164:167], v[180:183], v[106:109]
	v_mfma_f32_16x16x32_bf16 v[94:97], v[156:159], v[192:195], v[94:97]
	v_mfma_f32_16x16x32_bf16 v[90:93], v[164:167], v[192:195], v[90:93]
	v_mfma_f32_16x16x32_bf16 v[78:81], v[156:159], v[200:203], v[78:81]
	v_mfma_f32_16x16x32_bf16 v[74:77], v[164:167], v[200:203], v[74:77]
	s_setprio 0
	s_barrier
	s_mov_b32 m0, s63
	v_add_u32_e32 v216, s62, v131
	v_lshl_add_u64 v[148:149], v[148:149], 0, s[2:3]
	ds_read_b128 v[204:207], v216
	ds_read_b128 v[208:211], v216 offset:1024
	ds_read_b128 v[212:215], v216 offset:2048
	ds_read_b128 v[216:219], v216 offset:3072
	global_load_lds_dwordx4 v[148:149], off
	v_lshl_add_u64 v[148:149], v[188:189], 0, s[2:3]
	s_mov_b32 m0, s61
	s_nop 0
	global_load_lds_dwordx4 v[148:149], off
	s_barrier
	s_waitcnt lgkmcnt(0)
	s_setprio 1
	s_waitcnt lgkmcnt(0)
	v_mfma_f32_16x16x32_bf16 v[118:121], v[204:207], v[168:171], v[118:121]
	v_mfma_f32_16x16x32_bf16 v[114:117], v[212:215], v[168:171], v[114:117]
	v_mfma_f32_16x16x32_bf16 v[102:105], v[204:207], v[176:179], v[102:105]
	v_mfma_f32_16x16x32_bf16 v[98:101], v[212:215], v[176:179], v[98:101]
	v_mfma_f32_16x16x32_bf16 v[86:89], v[204:207], v[184:187], v[86:89]
	v_mfma_f32_16x16x32_bf16 v[82:85], v[212:215], v[184:187], v[82:85]
	v_mfma_f32_16x16x32_bf16 v[70:73], v[204:207], v[196:199], v[70:73]
	v_mfma_f32_16x16x32_bf16 v[66:69], v[212:215], v[196:199], v[66:69]
	v_mfma_f32_16x16x32_bf16 v[118:121], v[208:211], v[172:175], v[118:121]
	v_mfma_f32_16x16x32_bf16 v[114:117], v[216:219], v[172:175], v[114:117]
	v_mfma_f32_16x16x32_bf16 v[102:105], v[208:211], v[180:183], v[102:105]
	v_mfma_f32_16x16x32_bf16 v[98:101], v[216:219], v[180:183], v[98:101]
	v_mfma_f32_16x16x32_bf16 v[86:89], v[208:211], v[192:195], v[86:89]
	v_mfma_f32_16x16x32_bf16 v[82:85], v[216:219], v[192:195], v[82:85]
	v_mfma_f32_16x16x32_bf16 v[70:73], v[208:211], v[200:203], v[70:73]
	v_mfma_f32_16x16x32_bf16 v[66:69], v[216:219], v[200:203], v[66:69]
	s_setprio 0
	s_mov_b32 m0, s51
	v_lshl_add_u64 v[148:149], v[190:191], 0, s[2:3]
	s_barrier
	ds_read_b128 v[168:171], v152 offset:49152
	ds_read_b128 v[172:175], v152 offset:50176
	ds_read_b128 v[176:179], v152 offset:51200
	ds_read_b128 v[180:183], v152 offset:52224
	ds_read_b128 v[184:187], v152 offset:53248
	ds_read_b128 v[192:195], v152 offset:54272
	ds_read_b128 v[196:199], v152 offset:55296
	ds_read_b128 v[200:203], v152 offset:56320
	global_load_lds_dwordx4 v[148:149], off
	v_lshl_add_u64 v[148:149], v[220:221], 0, s[2:3]
	s_mov_b32 m0, s52
	s_nop 0
	global_load_lds_dwordx4 v[148:149], off
	s_barrier
	s_waitcnt lgkmcnt(0)
	s_setprio 1
	s_waitcnt lgkmcnt(0)
	v_mfma_f32_16x16x32_bf16 v[62:65], v[144:147], v[168:171], v[62:65]
	v_mfma_f32_16x16x32_bf16 v[58:61], v[160:163], v[168:171], v[58:61]
	v_mfma_f32_16x16x32_bf16 v[46:49], v[144:147], v[176:179], v[46:49]
	v_mfma_f32_16x16x32_bf16 v[42:45], v[160:163], v[176:179], v[42:45]
	v_mfma_f32_16x16x32_bf16 v[30:33], v[144:147], v[184:187], v[30:33]
	v_mfma_f32_16x16x32_bf16 v[26:29], v[160:163], v[184:187], v[26:29]
	v_mfma_f32_16x16x32_bf16 v[14:17], v[144:147], v[196:199], v[14:17]
	v_mfma_f32_16x16x32_bf16 v[10:13], v[160:163], v[196:199], v[10:13]
	v_mfma_f32_16x16x32_bf16 v[62:65], v[156:159], v[172:175], v[62:65]
	v_mfma_f32_16x16x32_bf16 v[58:61], v[164:167], v[172:175], v[58:61]
	v_mfma_f32_16x16x32_bf16 v[46:49], v[156:159], v[180:183], v[46:49]
	v_mfma_f32_16x16x32_bf16 v[42:45], v[164:167], v[180:183], v[42:45]
	v_mfma_f32_16x16x32_bf16 v[30:33], v[156:159], v[192:195], v[30:33]
	v_mfma_f32_16x16x32_bf16 v[26:29], v[164:167], v[192:195], v[26:29]
	v_mfma_f32_16x16x32_bf16 v[14:17], v[156:159], v[200:203], v[14:17]
	v_mfma_f32_16x16x32_bf16 v[10:13], v[164:167], v[200:203], v[10:13]
	s_setprio 0
	s_barrier
	s_mov_b32 m0, s60
	v_lshl_add_u64 v[144:145], s[24:25], 0, v[138:139]
	global_load_lds_dwordx4 v[144:145], off
	v_lshl_add_u64 v[144:145], s[24:25], 0, v[134:135]
	s_mov_b32 m0, s59
	s_nop 0
	global_load_lds_dwordx4 v[144:145], off
	s_waitcnt vmcnt(6)
	s_barrier
	s_setprio 1
	v_mfma_f32_16x16x32_bf16 v[54:57], v[204:207], v[168:171], v[54:57]
	v_mfma_f32_16x16x32_bf16 v[50:53], v[212:215], v[168:171], v[50:53]
	v_mfma_f32_16x16x32_bf16 v[38:41], v[204:207], v[176:179], v[38:41]
	v_mfma_f32_16x16x32_bf16 v[34:37], v[212:215], v[176:179], v[34:37]
	v_mfma_f32_16x16x32_bf16 v[22:25], v[204:207], v[184:187], v[22:25]
	v_mfma_f32_16x16x32_bf16 v[18:21], v[212:215], v[184:187], v[18:21]
	v_mfma_f32_16x16x32_bf16 v[6:9], v[204:207], v[196:199], v[6:9]
	v_mfma_f32_16x16x32_bf16 v[2:5], v[212:215], v[196:199], v[2:5]
	v_mfma_f32_16x16x32_bf16 v[54:57], v[208:211], v[172:175], v[54:57]
	v_mfma_f32_16x16x32_bf16 v[50:53], v[216:219], v[172:175], v[50:53]
	v_mfma_f32_16x16x32_bf16 v[38:41], v[208:211], v[180:183], v[38:41]
	v_mfma_f32_16x16x32_bf16 v[34:37], v[216:219], v[180:183], v[34:37]
	v_mfma_f32_16x16x32_bf16 v[22:25], v[208:211], v[192:195], v[22:25]
	v_mfma_f32_16x16x32_bf16 v[18:21], v[216:219], v[192:195], v[18:21]
	v_mfma_f32_16x16x32_bf16 v[6:9], v[208:211], v[200:203], v[6:9]
	v_mfma_f32_16x16x32_bf16 v[2:5], v[216:219], v[200:203], v[2:5]
	s_setprio 0
	s_movk_i32 s26, 0x100
	s_andn2_b64 vcc, exec, s[22:23]
	s_mov_b64 s[24:25], -1
	s_mov_b64 s[22:23], 0
	s_barrier
	s_cbranch_vccz .LBB0_188
	v_lshl_add_u32 v144, s16, 8, v1
	v_readlane_b32 s60, v250, 44
	v_ashrrev_i32_e32 v145, 31, v144
	v_readlane_b32 s61, v250, 45
	s_lshl_b32 s9, s56, 8
	s_cmp_eq_u32 s56, 64
	v_lshl_add_u64 v[146:147], v[144:145], 2, s[60:61]
	global_load_dword v168, v[146:147], off
	global_load_dword v178, v[146:147], off offset:64
	global_load_dword v179, v[146:147], off offset:128
	global_load_dword v180, v[146:147], off offset:192
	global_load_dword v181, v[146:147], off offset:512
	global_load_dword v182, v[146:147], off offset:576
	global_load_dword v183, v[146:147], off offset:640
	global_load_dword v184, v[146:147], off offset:704
	s_cselect_b64 vcc, -1, 0
	s_mov_b32 s11, 0x17c0000
	s_and_b64 s[18:19], vcc, exec
	s_cselect_b32 s16, 0, s9
	s_cselect_b32 s11, s11, 0x22940000
	s_cselect_b32 s9, 8, 14
	v_or_b32_e32 v164, s16, v150
	s_add_u32 s18, s6, s11
	v_lshlrev_b64 v[156:157], s9, v[144:145]
	s_addc_u32 s19, s7, 0
	v_ashrrev_i32_e32 v165, 31, v164
	v_cvt_f32_i32_e32 v145, v164
	v_or_b32_e32 v158, 1, v164
	v_or_b32_e32 v159, 2, v164
	v_or_b32_e32 v161, 4, v164
	v_or_b32_e32 v166, 7, v164
	v_or_b32_e32 v160, 3, v164
	v_or_b32_e32 v162, 5, v164
	v_or_b32_e32 v163, 6, v164
	v_or_b32_e32 v167, 0x80, v164
	v_lshl_add_u64 v[148:149], v[164:165], 1, s[18:19]
	v_cvt_f32_i32_e32 v158, v158
	v_cvt_f32_i32_e32 v159, v159
	v_cvt_f32_i32_e32 v165, v161
	v_cvt_f32_i32_e32 v172, v166
	v_cvt_f32_i32_e32 v160, v160
	v_cvt_f32_i32_e32 v170, v162
	v_cvt_f32_i32_e32 v171, v163
	v_cvt_f32_i32_e32 v173, v167
	v_cndmask_b32_e32 v169, v154, v155, vcc
	v_mul_f32_e64 v163, v169, -v145
	v_lshl_add_u64 v[166:167], v[156:157], 1, v[148:149]
	v_mul_f32_e64 v162, v169, -v158
	v_mul_f32_e64 v161, v169, -v159
	v_mul_f32_e64 v159, v169, -v165
	v_mul_f32_e64 v156, v169, -v172
	v_mul_f32_e64 v160, v169, -v160
	v_mul_f32_e64 v158, v169, -v170
	v_mul_f32_e64 v157, v169, -v171
	v_mul_f32_e64 v145, v169, -v173
	s_and_b64 vcc, exec, s[0:1]
	s_mov_b32 s56, s8
	s_mov_b32 s16, s10
	s_mov_b64 s[20:21], s[14:15]
	s_mov_b64 s[18:19], s[12:13]
	v_readlane_b32 s62, v250, 46
	v_readlane_b32 s63, v250, 47
	v_readlane_b32 s64, v250, 48
	v_readlane_b32 s65, v250, 49
	v_readlane_b32 s66, v250, 50
	v_readlane_b32 s67, v250, 51
	v_readlane_b32 s68, v250, 52
	v_readlane_b32 s69, v250, 53
	v_readlane_b32 s70, v250, 54
	v_readlane_b32 s71, v250, 55
	v_readlane_b32 s72, v250, 56
	v_readlane_b32 s73, v250, 57
	v_readlane_b32 s74, v250, 58
	v_readlane_b32 s75, v250, 59
	s_waitcnt vmcnt(0)
	v_mul_f32_e64 v165, v163, |v168|
	v_mul_f32_e64 v170, v162, |v168|
	v_mul_f32_e64 v173, v159, |v168|
	v_mul_f32_e64 v176, v156, |v168|
	v_mul_f32_e32 v165, 0x3fb8aa3b, v165
	v_mul_f32_e64 v171, v161, |v168|
	v_mul_f32_e64 v172, v160, |v168|
	v_mul_f32_e64 v174, v158, |v168|
	v_mul_f32_e64 v175, v157, |v168|
	v_mul_f32_e32 v170, 0x3fb8aa3b, v170
	v_mul_f32_e32 v173, 0x3fb8aa3b, v173
	v_mul_f32_e32 v176, 0x3fb8aa3b, v176
	v_exp_f32_e32 v165, v165
	v_mul_f32_e64 v177, v145, |v168|
	v_mul_f32_e32 v171, 0x3fb8aa3b, v171
	v_mul_f32_e32 v172, 0x3fb8aa3b, v172
	v_mul_f32_e32 v174, 0x3fb8aa3b, v174
	v_mul_f32_e32 v175, 0x3fb8aa3b, v175
	v_exp_f32_e32 v170, v170
	v_exp_f32_e32 v173, v173
	v_exp_f32_e32 v176, v176
	v_mul_f32_e32 v177, 0x3fb8aa3b, v177
	v_exp_f32_e32 v171, v171
	v_exp_f32_e32 v172, v172
	v_exp_f32_e32 v174, v174
	v_exp_f32_e32 v175, v175
	v_exp_f32_e32 v177, v177
	v_add_f32_e32 v165, 0x3d4ccccd, v165
	v_add_f32_e32 v170, 0x3d4ccccd, v170
	v_add_f32_e32 v173, 0x3d4ccccd, v173
	v_add_f32_e32 v176, 0x3d4ccccd, v176
	v_mul_f32_e32 v126, v126, v165
	v_add_f32_e32 v171, 0x3d4ccccd, v171
	v_add_f32_e32 v172, 0x3d4ccccd, v172
	v_add_f32_e32 v174, 0x3d4ccccd, v174
	v_add_f32_e32 v175, 0x3d4ccccd, v175
	v_mul_f32_e32 v127, v127, v170
	v_mul_f32_e32 v165, v122, v173
	v_mul_f32_e32 v125, v125, v176
	v_cvt_pk_bf16_f32 v122, v126, v127
	v_or_b32_e32 v126, 0x81, v164
	v_mul_f32_e32 v128, v128, v171
	v_mul_f32_e32 v129, v129, v172
	v_mul_f32_e32 v170, v123, v174
	v_mul_f32_e32 v171, v124, v175
	v_cvt_pk_bf16_f32 v123, v128, v129
	v_cvt_pk_bf16_f32 v124, v165, v170
	v_cvt_pk_bf16_f32 v125, v171, v125
	v_cvt_f32_i32_e32 v126, v126
	global_store_dwordx4 v[166:167], v[122:125], off
	v_or_b32_e32 v129, 0x86, v164
	v_cvt_f32_i32_e32 v129, v129
	v_add_f32_e32 v122, 0x3d4ccccd, v177
	v_mul_f32_e32 v124, v118, v122
	v_or_b32_e32 v122, 0x82, v164
	v_cvt_f32_i32_e32 v122, v122
	v_mul_f32_e64 v118, v169, -v126
	v_mul_f32_e64 v123, v118, |v168|
	v_mul_f32_e32 v123, 0x3fb8aa3b, v123
	v_mul_f32_e64 v122, v169, -v122
	v_exp_f32_e32 v123, v123
	v_mul_f32_e64 v125, v122, |v168|
	v_or_b32_e32 v126, 0x83, v164
	v_mul_f32_e32 v125, 0x3fb8aa3b, v125
	v_cvt_f32_i32_e32 v126, v126
	v_exp_f32_e32 v125, v125
	v_add_f32_e32 v123, 0x3d4ccccd, v123
	v_mul_f32_e32 v127, v119, v123
	v_mul_f32_e64 v119, v169, -v126
	v_add_f32_e32 v123, 0x3d4ccccd, v125
	v_mul_f32_e64 v125, v119, |v168|
	v_mul_f32_e32 v125, 0x3fb8aa3b, v125
	v_exp_f32_e32 v125, v125
	v_or_b32_e32 v126, 0x84, v164
	v_cvt_f32_i32_e32 v126, v126
	v_mul_f32_e32 v128, v120, v123
	v_add_f32_e32 v120, 0x3d4ccccd, v125
	v_mul_f32_e32 v125, v121, v120
	v_mul_f32_e64 v120, v169, -v126
	v_mul_f32_e64 v123, v120, |v168|
	v_mul_f32_e32 v123, 0x3fb8aa3b, v123
	v_exp_f32_e32 v123, v123
	v_or_b32_e32 v121, 0x85, v164
	v_cvt_f32_i32_e32 v121, v121
	v_cvt_pk_bf16_f32 v124, v124, v127
	v_add_f32_e32 v123, 0x3d4ccccd, v123
	v_mul_f32_e32 v165, v114, v123
	v_or_b32_e32 v114, 0x87, v164
	v_cvt_f32_i32_e32 v114, v114
	v_mul_f32_e64 v121, v169, -v121
	v_mul_f32_e64 v126, v121, |v168|
	v_mul_f32_e64 v123, v169, -v129
	v_mul_f32_e32 v126, 0x3fb8aa3b, v126
	v_mul_f32_e64 v129, v123, |v168|
	v_mul_f32_e64 v114, v169, -v114
	v_exp_f32_e32 v126, v126
	v_mul_f32_e32 v129, 0x3fb8aa3b, v129
	v_mul_f32_e64 v164, v114, |v168|
	v_exp_f32_e32 v129, v129
	v_mul_f32_e32 v164, 0x3fb8aa3b, v164
	v_exp_f32_e32 v164, v164
	v_add_f32_e32 v126, 0x3d4ccccd, v126
	v_mul_f32_e32 v115, v115, v126
	v_add_f32_e32 v126, 0x3d4ccccd, v129
	v_mul_f32_e32 v116, v116, v126
	v_add_f32_e32 v126, 0x3d4ccccd, v164
	v_mul_f32_e32 v117, v117, v126
	v_cvt_pk_bf16_f32 v125, v128, v125
	v_cvt_pk_bf16_f32 v126, v165, v115
	v_cvt_pk_bf16_f32 v127, v116, v117
	global_store_dwordx4 v[166:167], v[124:127], off offset:256
	s_nop 1
	v_mov_b32_e32 v115, v178
	v_or_b32_e32 v116, 16, v144
	v_ashrrev_i32_e32 v117, 31, v116
	v_lshlrev_b64 v[116:117], s9, v[116:117]
	v_lshl_add_u64 v[116:117], v[116:117], 1, v[148:149]
	s_nop 0
	v_mul_f32_e64 v125, v162, |v115|
	v_mul_f32_e64 v124, v163, |v115|
	v_mul_f32_e32 v125, 0x3fb8aa3b, v125
	v_mul_f32_e32 v124, 0x3fb8aa3b, v124
	v_exp_f32_e32 v125, v125
	v_exp_f32_e32 v124, v124
	v_mul_f32_e64 v128, v159, |v115|
	v_mul_f32_e64 v126, v161, |v115|
	v_add_f32_e32 v125, 0x3d4ccccd, v125
	v_mul_f32_e32 v128, 0x3fb8aa3b, v128
	v_add_f32_e32 v124, 0x3d4ccccd, v124
	v_mul_f32_e32 v111, v111, v125
	v_mul_f32_e64 v125, v158, |v115|
	v_mul_f32_e32 v126, 0x3fb8aa3b, v126
	v_mul_f32_e32 v110, v110, v124
	v_exp_f32_e32 v124, v128
	v_mul_f32_e32 v125, 0x3fb8aa3b, v125
	v_exp_f32_e32 v126, v126
	v_exp_f32_e32 v125, v125
	v_mul_f32_e64 v127, v160, |v115|
	v_add_f32_e32 v124, 0x3d4ccccd, v124
	v_mul_f32_e32 v127, 0x3fb8aa3b, v127
	v_add_f32_e32 v126, 0x3d4ccccd, v126
	v_mul_f32_e32 v124, v106, v124
	v_add_f32_e32 v106, 0x3d4ccccd, v125
	v_mul_f32_e64 v125, v157, |v115|
	v_exp_f32_e32 v127, v127
	v_mul_f32_e32 v112, v112, v126
	v_mul_f32_e32 v125, 0x3fb8aa3b, v125
	v_mul_f32_e64 v126, v156, |v115|
	v_exp_f32_e32 v125, v125
	v_mul_f32_e32 v126, 0x3fb8aa3b, v126
	v_exp_f32_e32 v126, v126
	v_add_f32_e32 v127, 0x3d4ccccd, v127
	v_mul_f32_e32 v113, v113, v127
	v_mul_f32_e32 v127, v107, v106
	v_add_f32_e32 v106, 0x3d4ccccd, v125
	v_mul_f32_e32 v125, v108, v106
	v_add_f32_e32 v106, 0x3d4ccccd, v126
	v_mul_f32_e32 v109, v109, v106
	v_cvt_pk_bf16_f32 v106, v110, v111
	v_mul_f32_e64 v110, v145, |v115|
	v_cvt_pk_bf16_f32 v107, v112, v113
	v_mul_f32_e32 v110, 0x3fb8aa3b, v110
	v_mul_f32_e64 v111, v118, |v115|
	v_cvt_pk_bf16_f32 v108, v124, v127
	v_cvt_pk_bf16_f32 v109, v125, v109
	v_exp_f32_e32 v110, v110
	v_mul_f32_e32 v111, 0x3fb8aa3b, v111
	global_store_dwordx4 v[116:117], v[106:109], off
	v_exp_f32_e32 v111, v111
	s_nop 0
	v_mul_f32_e64 v107, v122, |v115|
	v_mul_f32_e32 v107, 0x3fb8aa3b, v107
	v_mul_f32_e64 v108, v119, |v115|
	v_exp_f32_e32 v107, v107
	v_mul_f32_e32 v108, 0x3fb8aa3b, v108
	v_exp_f32_e32 v108, v108
	v_add_f32_e32 v106, 0x3d4ccccd, v110
	v_mul_f32_e32 v102, v102, v106
	v_add_f32_e32 v106, 0x3d4ccccd, v111
	v_mul_f32_e32 v103, v103, v106
	v_add_f32_e32 v106, 0x3d4ccccd, v107
	v_mul_f32_e64 v107, v120, |v115|
	v_mul_f32_e32 v104, v104, v106
	v_add_f32_e32 v106, 0x3d4ccccd, v108
	v_mul_f32_e32 v107, 0x3fb8aa3b, v107
	v_mul_f32_e64 v108, v121, |v115|
	v_exp_f32_e32 v107, v107
	v_mul_f32_e32 v108, 0x3fb8aa3b, v108
	v_exp_f32_e32 v108, v108
	v_mul_f32_e32 v105, v105, v106
	v_add_f32_e32 v106, 0x3d4ccccd, v107
	v_mul_f32_e64 v107, v123, |v115|
	v_mul_f32_e32 v106, v98, v106
	v_add_f32_e32 v98, 0x3d4ccccd, v108
	v_mul_f32_e32 v107, 0x3fb8aa3b, v107
	v_mul_f32_e64 v108, v114, |v115|
	v_exp_f32_e32 v107, v107
	v_mul_f32_e32 v108, 0x3fb8aa3b, v108
	v_exp_f32_e32 v108, v108
	v_mul_f32_e32 v109, v99, v98
	v_add_f32_e32 v98, 0x3d4ccccd, v107
	v_mul_f32_e32 v107, v100, v98
	v_add_f32_e32 v98, 0x3d4ccccd, v108
	v_mul_f32_e32 v101, v101, v98
	v_cvt_pk_bf16_f32 v98, v102, v103
	v_cvt_pk_bf16_f32 v99, v104, v105
	v_cvt_pk_bf16_f32 v100, v106, v109
	v_cvt_pk_bf16_f32 v101, v107, v101
	global_store_dwordx4 v[116:117], v[98:101], off offset:256
	s_nop 1
	v_mov_b32_e32 v100, v179
	s_nop 0
	v_mul_f32_e64 v102, v162, |v100|
	v_mul_f32_e64 v103, v161, |v100|
	v_mul_f32_e32 v102, 0x3fb8aa3b, v102
	v_mul_f32_e32 v103, 0x3fb8aa3b, v103
	v_exp_f32_e32 v102, v102
	v_exp_f32_e32 v103, v103
	v_mul_f32_e64 v101, v163, |v100|
	v_mul_f32_e64 v104, v160, |v100|
	v_mul_f32_e32 v101, 0x3fb8aa3b, v101
	v_add_f32_e32 v102, 0x3d4ccccd, v102
	v_mul_f32_e32 v104, 0x3fb8aa3b, v104
	v_exp_f32_e32 v101, v101
	v_add_f32_e32 v103, 0x3d4ccccd, v103
	v_mul_f32_e32 v95, v95, v102
	v_mul_f32_e64 v102, v159, |v100|
	v_exp_f32_e32 v104, v104
	v_mul_f32_e32 v96, v96, v103
	v_mul_f32_e32 v102, 0x3fb8aa3b, v102
	v_mul_f32_e64 v103, v158, |v100|
	v_exp_f32_e32 v102, v102
	v_mul_f32_e32 v103, 0x3fb8aa3b, v103
	v_exp_f32_e32 v103, v103
	v_add_f32_e32 v101, 0x3d4ccccd, v101
	v_mul_f32_e32 v94, v94, v101
	v_add_f32_e32 v101, 0x3d4ccccd, v104
	v_mul_f32_e32 v97, v97, v101
	v_add_f32_e32 v101, 0x3d4ccccd, v102
	v_mul_f32_e64 v102, v157, |v100|
	v_mul_f32_e32 v101, v90, v101
	v_add_f32_e32 v90, 0x3d4ccccd, v103
	v_mul_f32_e32 v102, 0x3fb8aa3b, v102
	v_mul_f32_e64 v103, v156, |v100|
	v_exp_f32_e32 v102, v102
	v_mul_f32_e32 v103, 0x3fb8aa3b, v103
	v_exp_f32_e32 v103, v103
	v_or_b32_e32 v98, 32, v144
	v_mul_f32_e32 v104, v91, v90
	v_add_f32_e32 v90, 0x3d4ccccd, v102
	v_ashrrev_i32_e32 v99, 31, v98
	v_mul_f32_e32 v102, v92, v90
	v_add_f32_e32 v90, 0x3d4ccccd, v103
	v_lshlrev_b64 v[98:99], s9, v[98:99]
	v_mul_f32_e32 v93, v93, v90
	v_cvt_pk_bf16_f32 v90, v94, v95
	v_mul_f32_e64 v94, v145, |v100|
	v_lshl_add_u64 v[98:99], v[98:99], 1, v[148:149]
	v_cvt_pk_bf16_f32 v91, v96, v97
	v_mul_f32_e32 v94, 0x3fb8aa3b, v94
	v_mul_f32_e64 v95, v118, |v100|
	v_cvt_pk_bf16_f32 v92, v101, v104
	v_cvt_pk_bf16_f32 v93, v102, v93
	v_exp_f32_e32 v94, v94
	v_mul_f32_e32 v95, 0x3fb8aa3b, v95
	global_store_dwordx4 v[98:99], v[90:93], off
	v_exp_f32_e32 v95, v95
	s_nop 0
	v_mul_f32_e64 v91, v122, |v100|
	v_mul_f32_e32 v91, 0x3fb8aa3b, v91
	v_mul_f32_e64 v92, v119, |v100|
	v_exp_f32_e32 v91, v91
	v_mul_f32_e32 v92, 0x3fb8aa3b, v92
	v_exp_f32_e32 v92, v92
	v_add_f32_e32 v90, 0x3d4ccccd, v94
	v_mul_f32_e32 v86, v86, v90
	v_add_f32_e32 v90, 0x3d4ccccd, v95
	v_mul_f32_e32 v87, v87, v90
	v_add_f32_e32 v90, 0x3d4ccccd, v91
	v_mul_f32_e64 v91, v120, |v100|
	v_mul_f32_e32 v88, v88, v90
	v_add_f32_e32 v90, 0x3d4ccccd, v92
	v_mul_f32_e32 v91, 0x3fb8aa3b, v91
	v_mul_f32_e64 v92, v121, |v100|
	v_exp_f32_e32 v91, v91
	v_mul_f32_e32 v92, 0x3fb8aa3b, v92
	v_exp_f32_e32 v92, v92
	v_mul_f32_e32 v89, v89, v90
	v_add_f32_e32 v90, 0x3d4ccccd, v91
	v_mul_f32_e64 v91, v123, |v100|
	v_mul_f32_e32 v90, v82, v90
	v_add_f32_e32 v82, 0x3d4ccccd, v92
	v_mul_f32_e32 v91, 0x3fb8aa3b, v91
	v_mul_f32_e64 v92, v114, |v100|
	v_exp_f32_e32 v91, v91
	v_mul_f32_e32 v92, 0x3fb8aa3b, v92
	v_exp_f32_e32 v92, v92
	v_mul_f32_e32 v93, v83, v82
	v_add_f32_e32 v82, 0x3d4ccccd, v91
	v_mul_f32_e32 v91, v84, v82
	v_add_f32_e32 v82, 0x3d4ccccd, v92
	v_mul_f32_e32 v85, v85, v82
	v_cvt_pk_bf16_f32 v82, v86, v87
	v_cvt_pk_bf16_f32 v83, v88, v89
	v_cvt_pk_bf16_f32 v84, v90, v93
	v_cvt_pk_bf16_f32 v85, v91, v85
	global_store_dwordx4 v[98:99], v[82:85], off offset:256
	s_nop 1
	v_mov_b32_e32 v84, v180
	s_nop 0
	v_mul_f32_e64 v86, v162, |v84|
	v_mul_f32_e64 v85, v163, |v84|
	v_mul_f32_e64 v87, v161, |v84|
	v_mul_f32_e32 v86, 0x3fb8aa3b, v86
	v_mul_f32_e32 v85, 0x3fb8aa3b, v85
	v_exp_f32_e32 v86, v86
	v_mul_f32_e32 v87, 0x3fb8aa3b, v87
	v_exp_f32_e32 v85, v85
	v_exp_f32_e32 v87, v87
	v_add_f32_e32 v86, 0x3d4ccccd, v86
	v_mul_f32_e64 v88, v160, |v84|
	v_add_f32_e32 v85, 0x3d4ccccd, v85
	v_mul_f32_e32 v79, v79, v86
	v_add_f32_e32 v86, 0x3d4ccccd, v87
	v_mul_f32_e32 v78, v78, v85
	v_mul_f32_e32 v85, 0x3fb8aa3b, v88
	v_mul_f32_e32 v80, v80, v86
	v_mul_f32_e64 v86, v159, |v84|
	v_exp_f32_e32 v85, v85
	v_mul_f32_e32 v86, 0x3fb8aa3b, v86
	v_mul_f32_e64 v87, v158, |v84|
	v_exp_f32_e32 v86, v86
	v_mul_f32_e32 v87, 0x3fb8aa3b, v87
	v_exp_f32_e32 v87, v87
	v_add_f32_e32 v85, 0x3d4ccccd, v85
	v_mul_f32_e32 v81, v81, v85
	v_add_f32_e32 v85, 0x3d4ccccd, v86
	v_mul_f32_e64 v86, v157, |v84|
	v_mul_f32_e32 v85, v74, v85
	v_add_f32_e32 v74, 0x3d4ccccd, v87
	v_mul_f32_e32 v86, 0x3fb8aa3b, v86
	v_mul_f32_e64 v87, v156, |v84|
	v_exp_f32_e32 v86, v86
	v_mul_f32_e32 v87, 0x3fb8aa3b, v87
	v_exp_f32_e32 v87, v87
	v_or_b32_e32 v82, 48, v144
	v_mul_f32_e32 v88, v75, v74
	v_add_f32_e32 v74, 0x3d4ccccd, v86
	v_ashrrev_i32_e32 v83, 31, v82
	v_mul_f32_e32 v86, v76, v74
	v_add_f32_e32 v74, 0x3d4ccccd, v87
	v_lshlrev_b64 v[82:83], s9, v[82:83]
	v_mul_f32_e32 v77, v77, v74
	v_cvt_pk_bf16_f32 v74, v78, v79
	v_mul_f32_e64 v78, v145, |v84|
	v_lshl_add_u64 v[82:83], v[82:83], 1, v[148:149]
	v_cvt_pk_bf16_f32 v75, v80, v81
	v_mul_f32_e32 v78, 0x3fb8aa3b, v78
	v_mul_f32_e64 v79, v118, |v84|
	v_cvt_pk_bf16_f32 v76, v85, v88
	v_cvt_pk_bf16_f32 v77, v86, v77
	v_exp_f32_e32 v78, v78
	v_mul_f32_e32 v79, 0x3fb8aa3b, v79
	global_store_dwordx4 v[82:83], v[74:77], off
	v_exp_f32_e32 v79, v79
	s_nop 0
	v_mul_f32_e64 v75, v122, |v84|
	v_mul_f32_e32 v75, 0x3fb8aa3b, v75
	v_mul_f32_e64 v76, v119, |v84|
	v_exp_f32_e32 v75, v75
	v_mul_f32_e32 v76, 0x3fb8aa3b, v76
	v_exp_f32_e32 v76, v76
	v_add_f32_e32 v74, 0x3d4ccccd, v78
	v_mul_f32_e32 v70, v70, v74
	v_add_f32_e32 v74, 0x3d4ccccd, v79
	v_mul_f32_e32 v71, v71, v74
	v_add_f32_e32 v74, 0x3d4ccccd, v75
	v_mul_f32_e64 v75, v120, |v84|
	v_mul_f32_e32 v72, v72, v74
	v_add_f32_e32 v74, 0x3d4ccccd, v76
	v_mul_f32_e32 v75, 0x3fb8aa3b, v75
	v_mul_f32_e64 v76, v121, |v84|
	v_exp_f32_e32 v75, v75
	v_mul_f32_e32 v76, 0x3fb8aa3b, v76
	v_exp_f32_e32 v76, v76
	v_mul_f32_e32 v73, v73, v74
	v_add_f32_e32 v74, 0x3d4ccccd, v75
	v_mul_f32_e64 v75, v123, |v84|
	v_mul_f32_e32 v74, v66, v74
	v_add_f32_e32 v66, 0x3d4ccccd, v76
	v_mul_f32_e32 v75, 0x3fb8aa3b, v75
	v_mul_f32_e64 v76, v114, |v84|
	v_exp_f32_e32 v75, v75
	v_mul_f32_e32 v76, 0x3fb8aa3b, v76
	v_exp_f32_e32 v76, v76
	v_mul_f32_e32 v77, v67, v66
	v_add_f32_e32 v66, 0x3d4ccccd, v75
	v_mul_f32_e32 v75, v68, v66
	v_add_f32_e32 v66, 0x3d4ccccd, v76
	v_mul_f32_e32 v69, v69, v66
	v_cvt_pk_bf16_f32 v66, v70, v71
	v_cvt_pk_bf16_f32 v67, v72, v73
	v_cvt_pk_bf16_f32 v68, v74, v77
	v_cvt_pk_bf16_f32 v69, v75, v69
	global_store_dwordx4 v[82:83], v[66:69], off offset:256
	s_nop 1
	v_mov_b32_e32 v68, v181
	s_nop 0
	v_mul_f32_e64 v70, v162, |v68|
	v_mul_f32_e64 v69, v163, |v68|
	v_mul_f32_e32 v69, 0x3fb8aa3b, v69
	v_exp_f32_e32 v69, v69
	v_mul_f32_e32 v70, 0x3fb8aa3b, v70
	v_exp_f32_e32 v70, v70
	v_mul_f32_e64 v71, v160, |v68|
	v_add_f32_e32 v69, 0x3d4ccccd, v69
	v_mul_f32_e32 v62, v62, v69
	v_mul_f32_e64 v69, v161, |v68|
	v_mul_f32_e32 v69, 0x3fb8aa3b, v69
	v_exp_f32_e32 v69, v69
	v_mul_f32_e32 v71, 0x3fb8aa3b, v71
	v_exp_f32_e32 v71, v71
	v_add_f32_e32 v70, 0x3d4ccccd, v70
	v_mul_f32_e32 v63, v63, v70
	v_add_f32_e32 v69, 0x3d4ccccd, v69
	v_mul_f32_e64 v70, v159, |v68|
	v_mul_f32_e32 v64, v64, v69
	v_add_f32_e32 v69, 0x3d4ccccd, v71
	v_mul_f32_e32 v70, 0x3fb8aa3b, v70
	v_mul_f32_e64 v71, v158, |v68|
	v_exp_f32_e32 v70, v70
	v_mul_f32_e32 v71, 0x3fb8aa3b, v71
	v_exp_f32_e32 v71, v71
	v_mul_f32_e32 v65, v65, v69
	v_add_f32_e32 v69, 0x3d4ccccd, v70
	v_mul_f32_e64 v70, v157, |v68|
	v_mul_f32_e32 v69, v58, v69
	v_add_f32_e32 v58, 0x3d4ccccd, v71
	v_mul_f32_e32 v70, 0x3fb8aa3b, v70
	v_mul_f32_e64 v71, v156, |v68|
	v_exp_f32_e32 v70, v70
	v_mul_f32_e32 v71, 0x3fb8aa3b, v71
	v_exp_f32_e32 v71, v71
	v_add_u32_e32 v66, 0x80, v144
	v_mul_f32_e32 v72, v59, v58
	v_add_f32_e32 v58, 0x3d4ccccd, v70
	v_ashrrev_i32_e32 v67, 31, v66
	v_mul_f32_e32 v70, v60, v58
	v_add_f32_e32 v58, 0x3d4ccccd, v71
	v_lshlrev_b64 v[66:67], s9, v[66:67]
	v_mul_f32_e32 v61, v61, v58
	v_cvt_pk_bf16_f32 v58, v62, v63
	v_mul_f32_e64 v62, v145, |v68|
	v_lshl_add_u64 v[66:67], v[66:67], 1, v[148:149]
	v_cvt_pk_bf16_f32 v59, v64, v65
	v_mul_f32_e32 v62, 0x3fb8aa3b, v62
	v_mul_f32_e64 v63, v118, |v68|
	v_cvt_pk_bf16_f32 v60, v69, v72
	v_cvt_pk_bf16_f32 v61, v70, v61
	v_exp_f32_e32 v62, v62
	v_mul_f32_e32 v63, 0x3fb8aa3b, v63
	global_store_dwordx4 v[66:67], v[58:61], off
	v_exp_f32_e32 v63, v63
	s_nop 0
	v_mul_f32_e64 v59, v122, |v68|
	v_mul_f32_e32 v59, 0x3fb8aa3b, v59
	v_mul_f32_e64 v60, v119, |v68|
	v_exp_f32_e32 v59, v59
	v_mul_f32_e32 v60, 0x3fb8aa3b, v60
	v_exp_f32_e32 v60, v60
	v_add_f32_e32 v58, 0x3d4ccccd, v62
	v_mul_f32_e32 v54, v54, v58
	v_add_f32_e32 v58, 0x3d4ccccd, v63
	v_mul_f32_e32 v55, v55, v58
	v_add_f32_e32 v58, 0x3d4ccccd, v59
	v_mul_f32_e64 v59, v120, |v68|
	v_mul_f32_e32 v56, v56, v58
	v_add_f32_e32 v58, 0x3d4ccccd, v60
	v_mul_f32_e32 v59, 0x3fb8aa3b, v59
	v_mul_f32_e64 v60, v121, |v68|
	v_exp_f32_e32 v59, v59
	v_mul_f32_e32 v60, 0x3fb8aa3b, v60
	v_exp_f32_e32 v60, v60
	v_mul_f32_e32 v57, v57, v58
	v_add_f32_e32 v58, 0x3d4ccccd, v59
	v_mul_f32_e64 v59, v123, |v68|
	v_mul_f32_e32 v58, v50, v58
	v_add_f32_e32 v50, 0x3d4ccccd, v60
	v_mul_f32_e32 v59, 0x3fb8aa3b, v59
	v_mul_f32_e64 v60, v114, |v68|
	v_exp_f32_e32 v59, v59
	v_mul_f32_e32 v60, 0x3fb8aa3b, v60
	v_exp_f32_e32 v60, v60
	v_mul_f32_e32 v61, v51, v50
	v_add_f32_e32 v50, 0x3d4ccccd, v59
	v_mul_f32_e32 v59, v52, v50
	v_add_f32_e32 v50, 0x3d4ccccd, v60
	v_mul_f32_e32 v53, v53, v50
	v_cvt_pk_bf16_f32 v50, v54, v55
	v_cvt_pk_bf16_f32 v51, v56, v57
	v_cvt_pk_bf16_f32 v52, v58, v61
	v_cvt_pk_bf16_f32 v53, v59, v53
	global_store_dwordx4 v[66:67], v[50:53], off offset:256
	s_nop 1
	v_mov_b32_e32 v52, v182
	s_nop 0
	v_mul_f32_e64 v54, v162, |v52|
	v_mul_f32_e64 v53, v163, |v52|
	v_mul_f32_e32 v53, 0x3fb8aa3b, v53
	v_exp_f32_e32 v53, v53
	v_mul_f32_e32 v54, 0x3fb8aa3b, v54
	v_exp_f32_e32 v54, v54
	v_mul_f32_e64 v55, v160, |v52|
	v_add_f32_e32 v53, 0x3d4ccccd, v53
	v_mul_f32_e32 v46, v46, v53
	v_add_f32_e32 v53, 0x3d4ccccd, v54
	v_mul_f32_e64 v54, v161, |v52|
	v_mul_f32_e32 v54, 0x3fb8aa3b, v54
	v_exp_f32_e32 v54, v54
	v_mul_f32_e32 v55, 0x3fb8aa3b, v55
	v_exp_f32_e32 v55, v55
	v_mul_f32_e32 v47, v47, v53
	v_add_f32_e32 v53, 0x3d4ccccd, v54
	v_mul_f32_e64 v54, v159, |v52|
	v_mul_f32_e32 v48, v48, v53
	v_add_f32_e32 v53, 0x3d4ccccd, v55
	v_mul_f32_e32 v54, 0x3fb8aa3b, v54
	v_mul_f32_e64 v55, v158, |v52|
	v_exp_f32_e32 v54, v54
	v_mul_f32_e32 v55, 0x3fb8aa3b, v55
	v_exp_f32_e32 v55, v55
	v_mul_f32_e32 v49, v49, v53
	v_add_f32_e32 v53, 0x3d4ccccd, v54
	v_mul_f32_e64 v54, v157, |v52|
	v_mul_f32_e32 v53, v42, v53
	v_add_f32_e32 v42, 0x3d4ccccd, v55
	v_mul_f32_e32 v54, 0x3fb8aa3b, v54
	v_mul_f32_e64 v55, v156, |v52|
	v_exp_f32_e32 v54, v54
	v_mul_f32_e32 v55, 0x3fb8aa3b, v55
	v_exp_f32_e32 v55, v55
	v_add_u32_e32 v50, 0x90, v144
	v_mul_f32_e32 v56, v43, v42
	v_add_f32_e32 v42, 0x3d4ccccd, v54
	v_ashrrev_i32_e32 v51, 31, v50
	v_mul_f32_e32 v54, v44, v42
	v_add_f32_e32 v42, 0x3d4ccccd, v55
	v_lshlrev_b64 v[50:51], s9, v[50:51]
	v_mul_f32_e32 v45, v45, v42
	v_cvt_pk_bf16_f32 v42, v46, v47
	v_mul_f32_e64 v46, v145, |v52|
	v_lshl_add_u64 v[50:51], v[50:51], 1, v[148:149]
	v_cvt_pk_bf16_f32 v43, v48, v49
	v_mul_f32_e32 v46, 0x3fb8aa3b, v46
	v_mul_f32_e64 v47, v118, |v52|
	v_cvt_pk_bf16_f32 v44, v53, v56
	v_cvt_pk_bf16_f32 v45, v54, v45
	v_exp_f32_e32 v46, v46
	v_mul_f32_e32 v47, 0x3fb8aa3b, v47
	global_store_dwordx4 v[50:51], v[42:45], off
	v_exp_f32_e32 v47, v47
	s_nop 0
	v_mul_f32_e64 v43, v122, |v52|
	v_mul_f32_e32 v43, 0x3fb8aa3b, v43
	v_mul_f32_e64 v44, v119, |v52|
	v_exp_f32_e32 v43, v43
	v_mul_f32_e32 v44, 0x3fb8aa3b, v44
	v_exp_f32_e32 v44, v44
	v_add_f32_e32 v42, 0x3d4ccccd, v46
	v_mul_f32_e32 v38, v38, v42
	v_add_f32_e32 v42, 0x3d4ccccd, v47
	v_mul_f32_e32 v39, v39, v42
	v_add_f32_e32 v42, 0x3d4ccccd, v43
	v_mul_f32_e64 v43, v120, |v52|
	v_mul_f32_e32 v40, v40, v42
	v_add_f32_e32 v42, 0x3d4ccccd, v44
	v_mul_f32_e32 v43, 0x3fb8aa3b, v43
	v_mul_f32_e64 v44, v121, |v52|
	v_exp_f32_e32 v43, v43
	v_mul_f32_e32 v44, 0x3fb8aa3b, v44
	v_exp_f32_e32 v44, v44
	v_mul_f32_e32 v41, v41, v42
	v_add_f32_e32 v42, 0x3d4ccccd, v43
	v_mul_f32_e64 v43, v123, |v52|
	v_mul_f32_e32 v42, v34, v42
	v_add_f32_e32 v34, 0x3d4ccccd, v44
	v_mul_f32_e32 v43, 0x3fb8aa3b, v43
	v_mul_f32_e64 v44, v114, |v52|
	v_exp_f32_e32 v43, v43
	v_mul_f32_e32 v44, 0x3fb8aa3b, v44
	v_exp_f32_e32 v44, v44
	v_mul_f32_e32 v45, v35, v34
	v_add_f32_e32 v34, 0x3d4ccccd, v43
	v_mul_f32_e32 v43, v36, v34
	v_add_f32_e32 v34, 0x3d4ccccd, v44
	v_mul_f32_e32 v37, v37, v34
	v_cvt_pk_bf16_f32 v34, v38, v39
	v_cvt_pk_bf16_f32 v35, v40, v41
	v_cvt_pk_bf16_f32 v36, v42, v45
	v_cvt_pk_bf16_f32 v37, v43, v37
	global_store_dwordx4 v[50:51], v[34:37], off offset:256
	s_nop 1
	v_mov_b32_e32 v36, v183
	s_nop 0
	v_mul_f32_e64 v38, v162, |v36|
	v_mul_f32_e64 v37, v163, |v36|
	v_mul_f32_e32 v37, 0x3fb8aa3b, v37
	v_exp_f32_e32 v37, v37
	v_mul_f32_e32 v38, 0x3fb8aa3b, v38
	v_exp_f32_e32 v38, v38
	v_mul_f32_e64 v39, v160, |v36|
	v_add_f32_e32 v37, 0x3d4ccccd, v37
	v_mul_f32_e32 v30, v30, v37
	v_add_f32_e32 v37, 0x3d4ccccd, v38
	v_mul_f32_e64 v38, v161, |v36|
	v_mul_f32_e32 v38, 0x3fb8aa3b, v38
	v_exp_f32_e32 v38, v38
	v_mul_f32_e32 v39, 0x3fb8aa3b, v39
	v_exp_f32_e32 v39, v39
	v_mul_f32_e32 v31, v31, v37
	v_add_f32_e32 v37, 0x3d4ccccd, v38
	v_mul_f32_e64 v38, v159, |v36|
	v_mul_f32_e32 v32, v32, v37
	v_add_f32_e32 v37, 0x3d4ccccd, v39
	v_mul_f32_e32 v38, 0x3fb8aa3b, v38
	v_mul_f32_e64 v39, v158, |v36|
	v_exp_f32_e32 v38, v38
	v_mul_f32_e32 v39, 0x3fb8aa3b, v39
	v_exp_f32_e32 v39, v39
	v_mul_f32_e32 v33, v33, v37
	v_add_f32_e32 v37, 0x3d4ccccd, v38
	v_mul_f32_e64 v38, v157, |v36|
	v_mul_f32_e32 v37, v26, v37
	v_add_f32_e32 v26, 0x3d4ccccd, v39
	v_mul_f32_e32 v38, 0x3fb8aa3b, v38
	v_mul_f32_e64 v39, v156, |v36|
	v_exp_f32_e32 v38, v38
	v_mul_f32_e32 v39, 0x3fb8aa3b, v39
	v_exp_f32_e32 v39, v39
	v_add_u32_e32 v34, 0xa0, v144
	v_mul_f32_e32 v40, v27, v26
	v_add_f32_e32 v26, 0x3d4ccccd, v38
	v_ashrrev_i32_e32 v35, 31, v34
	v_mul_f32_e32 v38, v28, v26
	v_add_f32_e32 v26, 0x3d4ccccd, v39
	v_lshlrev_b64 v[34:35], s9, v[34:35]
	v_mul_f32_e32 v29, v29, v26
	v_cvt_pk_bf16_f32 v26, v30, v31
	v_mul_f32_e64 v30, v145, |v36|
	v_lshl_add_u64 v[34:35], v[34:35], 1, v[148:149]
	v_cvt_pk_bf16_f32 v27, v32, v33
	v_mul_f32_e32 v30, 0x3fb8aa3b, v30
	v_mul_f32_e64 v31, v118, |v36|
	v_cvt_pk_bf16_f32 v28, v37, v40
	v_cvt_pk_bf16_f32 v29, v38, v29
	v_exp_f32_e32 v30, v30
	v_mul_f32_e32 v31, 0x3fb8aa3b, v31
	global_store_dwordx4 v[34:35], v[26:29], off
	v_exp_f32_e32 v31, v31
	s_nop 0
	v_mul_f32_e64 v27, v122, |v36|
	v_mul_f32_e32 v27, 0x3fb8aa3b, v27
	v_mul_f32_e64 v28, v119, |v36|
	v_exp_f32_e32 v27, v27
	v_mul_f32_e32 v28, 0x3fb8aa3b, v28
	v_exp_f32_e32 v28, v28
	v_add_f32_e32 v26, 0x3d4ccccd, v30
	v_mul_f32_e32 v22, v22, v26
	v_add_f32_e32 v26, 0x3d4ccccd, v31
	v_mul_f32_e32 v23, v23, v26
	v_add_f32_e32 v26, 0x3d4ccccd, v27
	v_mul_f32_e64 v27, v120, |v36|
	v_mul_f32_e32 v24, v24, v26
	v_add_f32_e32 v26, 0x3d4ccccd, v28
	v_mul_f32_e32 v27, 0x3fb8aa3b, v27
	v_mul_f32_e64 v28, v121, |v36|
	v_exp_f32_e32 v27, v27
	v_mul_f32_e32 v28, 0x3fb8aa3b, v28
	v_exp_f32_e32 v28, v28
	v_mul_f32_e32 v25, v25, v26
	v_add_f32_e32 v26, 0x3d4ccccd, v27
	v_mul_f32_e64 v27, v123, |v36|
	v_mul_f32_e32 v26, v18, v26
	v_add_f32_e32 v18, 0x3d4ccccd, v28
	v_mul_f32_e32 v27, 0x3fb8aa3b, v27
	v_mul_f32_e64 v28, v114, |v36|
	v_exp_f32_e32 v27, v27
	v_mul_f32_e32 v28, 0x3fb8aa3b, v28
	v_exp_f32_e32 v28, v28
	v_mul_f32_e32 v29, v19, v18
	v_add_f32_e32 v18, 0x3d4ccccd, v27
	v_mul_f32_e32 v27, v20, v18
	v_add_f32_e32 v18, 0x3d4ccccd, v28
	v_mul_f32_e32 v21, v21, v18
	v_cvt_pk_bf16_f32 v18, v22, v23
	v_cvt_pk_bf16_f32 v19, v24, v25
	v_cvt_pk_bf16_f32 v20, v26, v29
	v_cvt_pk_bf16_f32 v21, v27, v21
	global_store_dwordx4 v[34:35], v[18:21], off offset:256
	s_nop 1
	v_mov_b32_e32 v20, v184
	s_nop 0
	v_mul_f32_e64 v22, v162, |v20|
	v_mul_f32_e64 v21, v163, |v20|
	v_mul_f32_e32 v21, 0x3fb8aa3b, v21
	v_exp_f32_e32 v21, v21
	v_mul_f32_e32 v22, 0x3fb8aa3b, v22
	v_exp_f32_e32 v22, v22
	v_mul_f32_e64 v23, v160, |v20|
	v_add_f32_e32 v21, 0x3d4ccccd, v21
	v_mul_f32_e32 v14, v14, v21
	v_add_f32_e32 v21, 0x3d4ccccd, v22
	v_mul_f32_e64 v22, v161, |v20|
	v_mul_f32_e32 v22, 0x3fb8aa3b, v22
	v_exp_f32_e32 v22, v22
	v_mul_f32_e32 v23, 0x3fb8aa3b, v23
	v_exp_f32_e32 v23, v23
	v_mul_f32_e32 v15, v15, v21
	v_add_f32_e32 v21, 0x3d4ccccd, v22
	v_mul_f32_e64 v22, v159, |v20|
	v_mul_f32_e32 v16, v16, v21
	v_add_f32_e32 v21, 0x3d4ccccd, v23
	v_mul_f32_e32 v22, 0x3fb8aa3b, v22
	v_mul_f32_e64 v23, v158, |v20|
	v_exp_f32_e32 v22, v22
	v_mul_f32_e32 v23, 0x3fb8aa3b, v23
	v_exp_f32_e32 v23, v23
	v_mul_f32_e32 v17, v17, v21
	v_add_f32_e32 v21, 0x3d4ccccd, v22
	v_mul_f32_e64 v22, v157, |v20|
	v_mul_f32_e32 v21, v10, v21
	v_add_f32_e32 v10, 0x3d4ccccd, v23
	v_mul_f32_e32 v22, 0x3fb8aa3b, v22
	v_mul_f32_e64 v23, v156, |v20|
	v_exp_f32_e32 v22, v22
	v_mul_f32_e32 v23, 0x3fb8aa3b, v23
	v_exp_f32_e32 v23, v23
	v_add_u32_e32 v18, 0xb0, v144
	v_mul_f32_e32 v24, v11, v10
	v_add_f32_e32 v10, 0x3d4ccccd, v22
	v_ashrrev_i32_e32 v19, 31, v18
	v_mul_f32_e32 v22, v12, v10
	v_add_f32_e32 v10, 0x3d4ccccd, v23
	v_lshlrev_b64 v[18:19], s9, v[18:19]
	v_mul_f32_e32 v13, v13, v10
	v_cvt_pk_bf16_f32 v10, v14, v15
	v_mul_f32_e64 v14, v123, |v20|
	v_lshl_add_u64 v[18:19], v[18:19], 1, v[148:149]
	v_cvt_pk_bf16_f32 v11, v16, v17
	v_mul_f32_e32 v14, 0x3fb8aa3b, v14
	v_mul_f32_e64 v15, v121, |v20|
	v_cvt_pk_bf16_f32 v12, v21, v24
	v_cvt_pk_bf16_f32 v13, v22, v13
	v_exp_f32_e32 v14, v14
	v_mul_f32_e32 v15, 0x3fb8aa3b, v15
	global_store_dwordx4 v[18:19], v[10:13], off
	v_exp_f32_e32 v15, v15
	s_nop 0
	v_mul_f32_e64 v11, v120, |v20|
	v_mul_f32_e32 v11, 0x3fb8aa3b, v11
	v_exp_f32_e32 v11, v11
	v_mul_f32_e64 v12, v119, |v20|
	v_add_f32_e32 v10, 0x3d4ccccd, v14
	v_mul_f32_e32 v12, 0x3fb8aa3b, v12
	v_mul_f32_e32 v10, v4, v10
	v_add_f32_e32 v4, 0x3d4ccccd, v15
	v_exp_f32_e32 v12, v12
	v_mul_f32_e32 v4, v3, v4
	v_add_f32_e32 v3, 0x3d4ccccd, v11
	v_mul_f32_e32 v11, v2, v3
	v_mul_f32_e64 v3, v122, |v20|
	v_mul_f32_e32 v3, 0x3fb8aa3b, v3
	v_add_f32_e32 v2, 0x3d4ccccd, v12
	v_exp_f32_e32 v3, v3
	v_mul_f32_e64 v12, v118, |v20|
	v_mul_f32_e32 v12, 0x3fb8aa3b, v12
	v_exp_f32_e32 v12, v12
	v_mul_f32_e32 v9, v9, v2
	v_add_f32_e32 v2, 0x3d4ccccd, v3
	v_mul_f32_e32 v3, v8, v2
	v_mul_f32_e64 v8, v145, |v20|
	v_add_f32_e32 v2, 0x3d4ccccd, v12
	v_mul_f32_e32 v8, 0x3fb8aa3b, v8
	v_mul_f32_e64 v12, v114, |v20|
	v_exp_f32_e32 v8, v8
	v_mul_f32_e32 v12, 0x3fb8aa3b, v12
	v_exp_f32_e32 v12, v12
	v_mul_f32_e32 v2, v7, v2
	v_add_f32_e32 v7, 0x3d4ccccd, v8
	v_mul_f32_e32 v6, v6, v7
	v_add_f32_e32 v7, 0x3d4ccccd, v12
	v_mul_f32_e32 v5, v5, v7
	v_cvt_pk_bf16_f32 v2, v6, v2
	v_cvt_pk_bf16_f32 v3, v3, v9
	v_cvt_pk_bf16_f32 v4, v11, v4
	v_cvt_pk_bf16_f32 v5, v10, v5
	global_store_dwordx4 v[18:19], v[2:5], off offset:256
	s_cbranch_vccz .LBB0_185
	s_waitcnt vmcnt(0)
	v_readlane_b32 s52, v250, 40
	s_cmpk_gt_u32 s39, 0xff
	v_readlane_b32 s53, v250, 41
	v_readlane_b32 s54, v250, 42
	v_readlane_b32 s55, v250, 43
	s_cbranch_scc1 .LBB0_192
	s_barrier

.LBB0_634:
	s_or_b64 exec, exec, s[0:1]
	v_readlane_b32 s0, v251, 28
	v_mov_b32_e32 v90, v173
	s_nop 0
	v_mov_b32_e32 v2, s0
	v_readlane_b32 s0, v251, 34
	v_mov_b32_e32 v10, v1
	s_waitcnt lgkmcnt(0)
	v_mov_b32_e32 v3, s0
	s_barrier
	ds_read_b128 v[6:9], v2
	ds_read_b128 v[2:5], v3
	v_mov_b32_e32 v60, v164
	v_mov_b32_e32 v34, v165
	v_mov_b32_e32 v62, v166
	v_mov_b32_e32 v32, v167
	v_mov_b32_e32 v64, v168
	v_mov_b32_e32 v38, v169
	v_mov_b32_e32 v66, v170
	v_mov_b32_e32 v10, v171
	v_pk_add_f32 v[68:69], v[14:15], v[42:43]
	v_pk_add_f32 v[14:15], v[14:15], v[42:43] neg_lo:[0,1] neg_hi:[0,1]
	s_nop 0
	v_mov_b32_e32 v13, v15
	v_mov_b32_e32 v10, v14
	v_mov_b32_e32 v42, v15
	v_mov_b32_e32 v43, v11
	v_pk_mul_f32 v[14:15], v[12:13], v[66:67] op_sel_hi:[1,0] neg_lo:[0,1] neg_hi:[0,1]
	v_pk_add_f32 v[70:71], v[18:19], v[52:53]
	v_pk_fma_f32 v[42:43], v[42:43], v[60:61], v[14:15] op_sel_hi:[1,0,1]
	v_pk_add_f32 v[14:15], v[16:17], v[48:49]
	v_pk_add_f32 v[48:49], v[16:17], v[48:49] neg_lo:[0,1] neg_hi:[0,1]
	v_mov_b32_e32 v17, v11
	v_mov_b32_e32 v13, v48
	v_mov_b32_e32 v16, v48
	v_pk_mul_f32 v[54:55], v[12:13], v[38:39] op_sel_hi:[1,0] neg_lo:[0,1] neg_hi:[0,1]
	v_mov_b32_e32 v13, v49
	v_pk_add_f32 v[18:19], v[18:19], v[52:53] neg_lo:[0,1] neg_hi:[0,1]
	v_pk_fma_f32 v[16:17], v[16:17], v[34:35], v[54:55] op_sel_hi:[1,0,1]
	v_mov_b32_e32 v54, v49
	v_mov_b32_e32 v55, v11
	v_pk_mul_f32 v[48:49], v[12:13], v[64:65] op_sel_hi:[1,0] neg_lo:[0,1] neg_hi:[0,1]
	v_mov_b32_e32 v13, v18
	v_pk_fma_f32 v[48:49], v[54:55], v[62:63], v[48:49] op_sel_hi:[1,0,1]
	v_mov_b32_e32 v52, v18
	v_mov_b32_e32 v53, v11
	v_pk_mul_f32 v[54:55], v[12:13], v[32:33] op_sel_hi:[1,0] neg_lo:[0,1] neg_hi:[0,1]
	v_mov_b32_e32 v13, v19
	v_pk_fma_f32 v[52:53], v[52:53], v[32:33], v[54:55] op_sel_hi:[1,0,1]
	v_mov_b32_e32 v54, v19
	v_mov_b32_e32 v55, v11
	v_pk_add_f32 v[18:19], v[20:21], v[50:51]
	v_pk_add_f32 v[20:21], v[20:21], v[50:51] neg_lo:[0,1] neg_hi:[0,1]
	v_pk_mul_f32 v[54:55], v[54:55], v[64:65] op_sel_hi:[1,0]
	v_mov_b32_e32 v50, v20
	v_mov_b32_e32 v51, v11
	v_pk_fma_f32 v[54:55], v[12:13], v[62:63], v[54:55] op_sel_hi:[1,0,1] neg_lo:[0,1,0] neg_hi:[0,1,0]
	v_pk_mul_f32 v[50:51], v[50:51], v[38:39] op_sel_hi:[1,0]
	v_mov_b32_e32 v13, v20
	v_pk_fma_f32 v[58:59], v[12:13], v[34:35], v[50:51] op_sel_hi:[1,0,1] neg_lo:[0,1,0] neg_hi:[0,1,0]
	v_mov_b32_e32 v50, v21
	v_mov_b32_e32 v51, v11
	v_pk_mul_f32 v[50:51], v[50:51], v[66:67] op_sel_hi:[1,0]
	v_mov_b32_e32 v13, v21
	v_pk_add_f32 v[20:21], v[26:27], v[46:47]
	v_pk_add_f32 v[26:27], v[26:27], v[46:47] neg_lo:[0,1] neg_hi:[0,1]
	v_pk_fma_f32 v[56:57], v[12:13], v[60:61], v[50:51] op_sel_hi:[1,0,1] neg_lo:[0,1,0] neg_hi:[0,1,0]
	v_xor_b32_e32 v73, 0x80000000, v26
	v_mov_b32_e32 v46, v27
	v_mov_b32_e32 v47, v11
	v_mov_b32_e32 v13, v27
	v_pk_add_f32 v[26:27], v[30:31], v[44:45]
	v_pk_add_f32 v[30:31], v[30:31], v[44:45] neg_lo:[0,1] neg_hi:[0,1]
	v_pk_mul_f32 v[46:47], v[46:47], v[66:67] op_sel_hi:[1,0] neg_lo:[0,1] neg_hi:[0,1]
	v_mov_b32_e32 v44, v30
	v_mov_b32_e32 v45, v11
	v_pk_fma_f32 v[74:75], v[12:13], v[60:61], v[46:47] op_sel_hi:[1,0,1] neg_lo:[0,1,0] neg_hi:[0,1,0]
	v_pk_mul_f32 v[44:45], v[44:45], v[38:39] op_sel_hi:[1,0] neg_lo:[0,1] neg_hi:[0,1]
	v_mov_b32_e32 v13, v30
	v_pk_fma_f32 v[76:77], v[12:13], v[34:35], v[44:45] op_sel_hi:[1,0,1] neg_lo:[0,1,0] neg_hi:[0,1,0]
	v_mov_b32_e32 v44, v31
	v_mov_b32_e32 v45, v11
	v_pk_mul_f32 v[44:45], v[44:45], v[64:65] op_sel_hi:[1,0] neg_lo:[0,1] neg_hi:[0,1]
	v_mov_b32_e32 v13, v31
	v_pk_add_f32 v[30:31], v[28:29], v[40:41]
	v_pk_add_f32 v[28:29], v[28:29], v[40:41] neg_lo:[0,1] neg_hi:[0,1]
	v_pk_fma_f32 v[78:79], v[12:13], v[62:63], v[44:45] op_sel_hi:[1,0,1] neg_lo:[0,1,0] neg_hi:[0,1,0]
	v_mov_b32_e32 v13, v28
	v_mov_b32_e32 v40, v28
	v_mov_b32_e32 v41, v11
	v_pk_mul_f32 v[44:45], v[12:13], v[32:33] op_sel_hi:[1,0] neg_lo:[0,1] neg_hi:[0,1]
	v_mov_b32_e32 v13, v29
	v_pk_fma_f32 v[80:81], v[40:41], v[32:33], v[44:45] op_sel_hi:[1,0,1] neg_lo:[0,1,0] neg_hi:[0,1,0]
	v_mov_b32_e32 v40, v29
	v_pk_mul_f32 v[28:29], v[12:13], v[64:65] op_sel_hi:[1,0] neg_lo:[0,1] neg_hi:[0,1]
	v_mov_b32_e32 v45, v11
	v_pk_fma_f32 v[62:63], v[40:41], v[62:63], v[28:29] op_sel_hi:[1,0,1] neg_lo:[0,1,0] neg_hi:[0,1,0]
	v_pk_add_f32 v[28:29], v[24:25], v[36:37]
	v_pk_add_f32 v[24:25], v[24:25], v[36:37] neg_lo:[0,1] neg_hi:[0,1]
	v_mov_b32_e32 v37, v11
	v_mov_b32_e32 v13, v24
	v_mov_b32_e32 v36, v24
	v_pk_mul_f32 v[40:41], v[12:13], v[38:39] op_sel_hi:[1,0] neg_lo:[0,1] neg_hi:[0,1]
	v_mov_b32_e32 v13, v25
	v_pk_fma_f32 v[64:65], v[36:37], v[34:35], v[40:41] op_sel_hi:[1,0,1] neg_lo:[0,1,0] neg_hi:[0,1,0]
	v_mov_b32_e32 v36, v25
	v_pk_mul_f32 v[24:25], v[12:13], v[66:67] op_sel_hi:[1,0] neg_lo:[0,1] neg_hi:[0,1]
	v_mov_b32_e32 v41, v11
	v_pk_fma_f32 v[66:67], v[36:37], v[60:61], v[24:25] op_sel_hi:[1,0,1] neg_lo:[0,1,0] neg_hi:[0,1,0]
	v_pk_add_f32 v[24:25], v[68:69], v[20:21] neg_lo:[0,1] neg_hi:[0,1]
	v_pk_add_f32 v[20:21], v[68:69], v[20:21]
	v_mov_b32_e32 v13, v25
	v_mov_b32_e32 v36, v24
	v_mov_b32_e32 v40, v25
	v_pk_mul_f32 v[24:25], v[12:13], v[38:39] op_sel_hi:[1,0] neg_lo:[0,1] neg_hi:[0,1]
	v_mov_b32_e32 v69, v11
	v_pk_fma_f32 v[24:25], v[40:41], v[34:35], v[24:25] op_sel_hi:[1,0,1]
	v_pk_add_f32 v[40:41], v[14:15], v[26:27] neg_lo:[0,1] neg_hi:[0,1]
	v_pk_add_f32 v[14:15], v[14:15], v[26:27]
	v_mov_b32_e32 v13, v40
	v_mov_b32_e32 v44, v40
	v_pk_mul_f32 v[46:47], v[12:13], v[32:33] op_sel_hi:[1,0] neg_lo:[0,1] neg_hi:[0,1]
	v_mov_b32_e32 v13, v41
	v_pk_fma_f32 v[44:45], v[44:45], v[32:33], v[46:47] op_sel_hi:[1,0,1]
	v_mov_b32_e32 v46, v41
	v_mov_b32_e32 v47, v11
	v_pk_mul_f32 v[46:47], v[46:47], v[38:39] op_sel_hi:[1,0]
	v_pk_add_f32 v[40:41], v[70:71], v[30:31] neg_lo:[0,1] neg_hi:[0,1]
	v_pk_fma_f32 v[50:51], v[12:13], v[34:35], v[46:47] op_sel_hi:[1,0,1] neg_lo:[0,1,0] neg_hi:[0,1,0]
	v_mov_b32_e32 v46, v41
	v_mov_b32_e32 v47, v11
	v_xor_b32_e32 v83, 0x80000000, v40
	v_pk_mul_f32 v[46:47], v[46:47], v[38:39] op_sel_hi:[1,0] neg_lo:[0,1] neg_hi:[0,1]
	v_mov_b32_e32 v13, v41
	v_pk_add_f32 v[40:41], v[18:19], v[28:29] neg_lo:[0,1] neg_hi:[0,1]
	v_pk_fma_f32 v[84:85], v[12:13], v[34:35], v[46:47] op_sel_hi:[1,0,1] neg_lo:[0,1,0] neg_hi:[0,1,0]
	v_mov_b32_e32 v13, v40
	v_pk_add_f32 v[26:27], v[70:71], v[30:31]
	v_mov_b32_e32 v46, v40
	v_mov_b32_e32 v47, v11
	v_pk_mul_f32 v[60:61], v[12:13], v[32:33] op_sel_hi:[1,0] neg_lo:[0,1] neg_hi:[0,1]
	v_mov_b32_e32 v13, v41
	v_pk_add_f32 v[18:19], v[18:19], v[28:29]
	v_pk_add_f32 v[28:29], v[20:21], v[26:27] neg_lo:[0,1] neg_hi:[0,1]
	v_pk_fma_f32 v[86:87], v[46:47], v[32:33], v[60:61] op_sel_hi:[1,0,1] neg_lo:[0,1,0] neg_hi:[0,1,0]
	v_mov_b32_e32 v46, v41
	v_pk_mul_f32 v[40:41], v[12:13], v[38:39] op_sel_hi:[1,0] neg_lo:[0,1] neg_hi:[0,1]
	v_mov_b32_e32 v13, v29
	v_pk_fma_f32 v[88:89], v[46:47], v[34:35], v[40:41] op_sel_hi:[1,0,1] neg_lo:[0,1,0] neg_hi:[0,1,0]
	v_mov_b32_e32 v40, v28
	v_pk_add_f32 v[20:21], v[20:21], v[26:27]
	v_mov_b32_e32 v26, v29
	v_mov_b32_e32 v27, v11
	v_pk_mul_f32 v[28:29], v[12:13], v[32:33] op_sel_hi:[1,0] neg_lo:[0,1] neg_hi:[0,1]
	v_mov_b32_e32 v41, v11
	v_pk_fma_f32 v[26:27], v[26:27], v[32:33], v[28:29] op_sel_hi:[1,0,1]
	v_pk_add_f32 v[28:29], v[14:15], v[18:19] neg_lo:[0,1] neg_hi:[0,1]
	v_pk_add_f32 v[14:15], v[14:15], v[18:19]
	v_mov_b32_e32 v13, v29
	v_xor_b32_e32 v61, 0x80000000, v28
	v_mov_b32_e32 v18, v29
	v_mov_b32_e32 v19, v11
	v_pk_mul_f32 v[28:29], v[12:13], v[32:33] op_sel_hi:[1,0] neg_lo:[0,1] neg_hi:[0,1]
	v_pk_add_f32 v[30:31], v[20:21], v[14:15]
	v_pk_fma_f32 v[18:19], v[18:19], v[32:33], v[28:29] op_sel_hi:[1,0,1] neg_lo:[0,1,0] neg_hi:[0,1,0]
	v_pk_add_f32 v[28:29], v[20:21], v[14:15] neg_lo:[0,1] neg_hi:[0,1]
	v_mov_b32_e32 v60, v11
	v_pk_add_f32 v[14:15], v[28:29], 0 neg_lo:[1,1] neg_hi:[1,1]
	v_mov_b32_e32 v68, v28
	v_mov_b32_e32 v14, v11
	v_pk_add_f32 v[46:47], v[68:69], v[14:15]
	v_pk_add_f32 v[20:21], v[68:69], v[14:15] neg_lo:[0,1] neg_hi:[0,1]
	v_pk_add_f32 v[14:15], v[40:41], v[60:61]
	v_pk_add_f32 v[28:29], v[40:41], v[60:61] neg_lo:[0,1] neg_hi:[0,1]
	v_pk_add_f32 v[40:41], v[26:27], v[18:19]
	v_pk_add_f32 v[18:19], v[26:27], v[18:19] neg_lo:[0,1] neg_hi:[0,1]
	v_mov_b32_e32 v82, v11
	v_pk_add_f32 v[60:61], v[14:15], v[40:41]
	v_pk_add_f32 v[26:27], v[14:15], v[40:41] neg_lo:[0,1] neg_hi:[0,1]
	v_pk_add_f32 v[40:41], v[28:29], v[18:19] op_sel:[0,1] op_sel_hi:[1,0] neg_hi:[0,1]
	v_pk_add_f32 v[14:15], v[28:29], v[18:19] op_sel:[0,1] op_sel_hi:[1,0] neg_lo:[0,1]
	v_pk_add_f32 v[18:19], v[36:37], v[82:83]
	v_pk_add_f32 v[28:29], v[36:37], v[82:83] neg_lo:[0,1] neg_hi:[0,1]
	v_pk_add_f32 v[36:37], v[24:25], v[84:85]
	v_pk_add_f32 v[24:25], v[24:25], v[84:85] neg_lo:[0,1] neg_hi:[0,1]
	v_mov_b32_e32 v72, v11
	v_pk_mul_f32 v[68:69], v[32:33], v[24:25] op_sel:[0,1] op_sel_hi:[0,0] neg_lo:[1,1] neg_hi:[1,0]
	v_pk_fma_f32 v[68:69], v[32:33], v[24:25], v[68:69] op_sel_hi:[0,1,1]
	v_pk_add_f32 v[24:25], v[44:45], v[86:87]
	v_pk_add_f32 v[44:45], v[44:45], v[86:87] neg_lo:[0,1] neg_hi:[0,1]
	v_lshl_add_u32 v13, v90, 3, 0
	v_xor_b32_e32 v71, 0x80000000, v44
	v_mov_b32_e32 v70, v45
	v_pk_add_f32 v[44:45], v[50:51], v[88:89]
	v_pk_add_f32 v[50:51], v[50:51], v[88:89] neg_lo:[0,1] neg_hi:[0,1]
	s_nop 0
	v_pk_mul_f32 v[82:83], v[32:33], v[50:51] op_sel:[0,1] op_sel_hi:[0,0] neg_lo:[1,1] neg_hi:[1,0]
	v_pk_fma_f32 v[82:83], v[32:33], v[50:51], v[82:83] op_sel_hi:[0,1,1] neg_lo:[1,0,0] neg_hi:[1,0,0]
	v_pk_add_f32 v[50:51], v[18:19], v[24:25]
	v_pk_add_f32 v[18:19], v[18:19], v[24:25] neg_lo:[0,1] neg_hi:[0,1]
	v_pk_add_f32 v[24:25], v[36:37], v[44:45]
	v_pk_add_f32 v[36:37], v[36:37], v[44:45] neg_lo:[0,1] neg_hi:[0,1]
	v_pk_add_f32 v[84:85], v[50:51], v[24:25]
	v_xor_b32_e32 v45, 0x80000000, v36
	v_mov_b32_e32 v44, v37
	v_pk_add_f32 v[36:37], v[50:51], v[24:25] neg_lo:[0,1] neg_hi:[0,1]
	v_pk_add_f32 v[50:51], v[18:19], v[44:45]
	v_pk_add_f32 v[24:25], v[18:19], v[44:45] neg_lo:[0,1] neg_hi:[0,1]
	v_pk_add_f32 v[44:45], v[68:69], v[82:83] neg_lo:[0,1] neg_hi:[0,1]
	v_pk_add_f32 v[18:19], v[28:29], v[70:71]
	v_pk_add_f32 v[70:71], v[28:29], v[70:71] neg_lo:[0,1] neg_hi:[0,1]
	v_pk_add_f32 v[28:29], v[68:69], v[82:83]
	v_xor_b32_e32 v69, 0x80000000, v44
	v_mov_b32_e32 v68, v45
	v_pk_add_f32 v[82:83], v[18:19], v[28:29]
	v_pk_add_f32 v[28:29], v[18:19], v[28:29] neg_lo:[0,1] neg_hi:[0,1]
	v_pk_add_f32 v[44:45], v[70:71], v[68:69]
	v_pk_add_f32 v[18:19], v[70:71], v[68:69] neg_lo:[0,1] neg_hi:[0,1]
	v_pk_add_f32 v[68:69], v[10:11], v[72:73]
	v_pk_add_f32 v[70:71], v[10:11], v[72:73] neg_lo:[0,1] neg_hi:[0,1]
	v_pk_add_f32 v[72:73], v[42:43], v[74:75]
	v_pk_add_f32 v[42:43], v[42:43], v[74:75] neg_lo:[0,1] neg_hi:[0,1]
	v_add_f32_e32 v10, v30, v31
	v_pk_mul_f32 v[74:75], v[38:39], v[42:43] op_sel:[0,1] op_sel_hi:[0,0] neg_lo:[1,1] neg_hi:[1,0]
	v_pk_fma_f32 v[42:43], v[34:35], v[42:43], v[74:75] op_sel_hi:[0,1,1]
	v_pk_add_f32 v[74:75], v[16:17], v[76:77]
	v_pk_add_f32 v[16:17], v[16:17], v[76:77] neg_lo:[0,1] neg_hi:[0,1]
	s_nop 0
	v_pk_mul_f32 v[76:77], v[32:33], v[16:17] op_sel:[0,1] op_sel_hi:[0,0] neg_lo:[1,1] neg_hi:[1,0]
	v_pk_fma_f32 v[16:17], v[32:33], v[16:17], v[76:77] op_sel_hi:[0,1,1]
	v_pk_add_f32 v[76:77], v[48:49], v[78:79]
	v_pk_add_f32 v[48:49], v[48:49], v[78:79] neg_lo:[0,1] neg_hi:[0,1]
	s_nop 0
	v_pk_mul_f32 v[78:79], v[34:35], v[48:49] op_sel:[0,1] op_sel_hi:[0,0] neg_lo:[1,1] neg_hi:[1,0]
	v_pk_fma_f32 v[78:79], v[38:39], v[48:49], v[78:79] op_sel_hi:[0,1,1]
	v_pk_add_f32 v[48:49], v[52:53], v[80:81]
	v_pk_add_f32 v[52:53], v[52:53], v[80:81] neg_lo:[0,1] neg_hi:[0,1]
	s_nop 0
	v_xor_b32_e32 v81, 0x80000000, v52
	v_mov_b32_e32 v80, v53
	v_pk_add_f32 v[52:53], v[54:55], v[62:63]
	v_pk_add_f32 v[54:55], v[54:55], v[62:63] neg_lo:[0,1] neg_hi:[0,1]
	s_nop 0
	v_pk_mul_f32 v[62:63], v[34:35], v[54:55] op_sel:[0,1] op_sel_hi:[0,0] neg_lo:[1,1] neg_hi:[1,0]
	v_pk_fma_f32 v[62:63], v[38:39], v[54:55], v[62:63] op_sel_hi:[0,1,1] neg_lo:[1,0,0] neg_hi:[1,0,0]
	v_pk_add_f32 v[54:55], v[58:59], v[64:65]
	v_pk_add_f32 v[58:59], v[58:59], v[64:65] neg_lo:[0,1] neg_hi:[0,1]
	s_nop 0
	v_pk_mul_f32 v[64:65], v[32:33], v[58:59] op_sel:[0,1] op_sel_hi:[0,0] neg_lo:[1,1] neg_hi:[1,0]
	v_pk_fma_f32 v[58:59], v[32:33], v[58:59], v[64:65] op_sel_hi:[0,1,1] neg_lo:[1,0,0] neg_hi:[1,0,0]
	v_pk_add_f32 v[64:65], v[56:57], v[66:67]
	v_pk_add_f32 v[56:57], v[56:57], v[66:67] neg_lo:[0,1] neg_hi:[0,1]
	s_nop 0
	v_pk_mul_f32 v[38:39], v[38:39], v[56:57] op_sel:[0,1] op_sel_hi:[0,0] neg_lo:[1,1] neg_hi:[1,0]
	v_pk_fma_f32 v[56:57], v[34:35], v[56:57], v[38:39] op_sel_hi:[0,1,1] neg_lo:[1,0,0] neg_hi:[1,0,0]
	v_pk_add_f32 v[38:39], v[52:53], v[72:73]
	v_pk_add_f32 v[52:53], v[72:73], v[52:53] neg_lo:[0,1] neg_hi:[0,1]
	v_pk_add_f32 v[34:35], v[68:69], v[48:49]
	v_pk_mul_f32 v[66:67], v[32:33], v[52:53] op_sel:[0,1] op_sel_hi:[0,0] neg_lo:[1,1] neg_hi:[1,0]
	v_pk_fma_f32 v[52:53], v[32:33], v[52:53], v[66:67] op_sel_hi:[0,1,1]
	v_pk_add_f32 v[66:67], v[74:75], v[54:55]
	v_pk_add_f32 v[54:55], v[74:75], v[54:55] neg_lo:[0,1] neg_hi:[0,1]
	v_pk_add_f32 v[48:49], v[68:69], v[48:49] neg_lo:[0,1] neg_hi:[0,1]
	v_xor_b32_e32 v69, 0x80000000, v54
	v_mov_b32_e32 v68, v55
	v_pk_add_f32 v[54:55], v[76:77], v[64:65]
	v_pk_add_f32 v[64:65], v[76:77], v[64:65] neg_lo:[0,1] neg_hi:[0,1]
	s_nop 0
	v_pk_mul_f32 v[72:73], v[32:33], v[64:65] op_sel:[0,1] op_sel_hi:[0,0] neg_lo:[1,1] neg_hi:[1,0]
	v_pk_fma_f32 v[64:65], v[32:33], v[64:65], v[72:73] op_sel_hi:[0,1,1] neg_lo:[1,0,0] neg_hi:[1,0,0]
	v_pk_add_f32 v[72:73], v[34:35], v[66:67]
	v_pk_add_f32 v[34:35], v[34:35], v[66:67] neg_lo:[0,1] neg_hi:[0,1]
	v_pk_add_f32 v[66:67], v[38:39], v[54:55]
	v_pk_add_f32 v[38:39], v[38:39], v[54:55] neg_lo:[0,1] neg_hi:[0,1]
	v_pk_add_f32 v[76:77], v[72:73], v[66:67]
	v_pk_add_f32 v[54:55], v[72:73], v[66:67] neg_lo:[0,1] neg_hi:[0,1]
	v_pk_add_f32 v[66:67], v[34:35], v[38:39] op_sel:[0,1] op_sel_hi:[1,0] neg_hi:[0,1]
	v_pk_add_f32 v[38:39], v[34:35], v[38:39] op_sel:[0,1] op_sel_hi:[1,0] neg_lo:[0,1]
	v_pk_add_f32 v[34:35], v[48:49], v[68:69]
	v_pk_add_f32 v[68:69], v[48:49], v[68:69] neg_lo:[0,1] neg_hi:[0,1]
	v_pk_add_f32 v[48:49], v[52:53], v[64:65]
	v_pk_add_f32 v[52:53], v[52:53], v[64:65] neg_lo:[0,1] neg_hi:[0,1]
	v_pk_add_f32 v[72:73], v[34:35], v[48:49]
	v_pk_add_f32 v[48:49], v[34:35], v[48:49] neg_lo:[0,1] neg_hi:[0,1]
	v_pk_add_f32 v[74:75], v[68:69], v[52:53] op_sel:[0,1] op_sel_hi:[1,0] neg_hi:[0,1]
	v_pk_add_f32 v[34:35], v[68:69], v[52:53] op_sel:[0,1] op_sel_hi:[1,0] neg_lo:[0,1]
	v_pk_add_f32 v[68:69], v[62:63], v[42:43]
	v_pk_add_f32 v[42:43], v[42:43], v[62:63] neg_lo:[0,1] neg_hi:[0,1]
	v_pk_add_f32 v[52:53], v[70:71], v[80:81]
	v_pk_mul_f32 v[62:63], v[32:33], v[42:43] op_sel:[0,1] op_sel_hi:[0,0] neg_lo:[1,1] neg_hi:[1,0]
	v_pk_fma_f32 v[62:63], v[32:33], v[42:43], v[62:63] op_sel_hi:[0,1,1]
	v_pk_add_f32 v[42:43], v[16:17], v[58:59]
	v_pk_add_f32 v[16:17], v[16:17], v[58:59] neg_lo:[0,1] neg_hi:[0,1]
	v_pk_add_f32 v[64:65], v[70:71], v[80:81] neg_lo:[0,1] neg_hi:[0,1]
	v_xor_b32_e32 v59, 0x80000000, v16
	v_mov_b32_e32 v58, v17
	v_pk_add_f32 v[16:17], v[78:79], v[56:57]
	v_pk_add_f32 v[56:57], v[78:79], v[56:57] neg_lo:[0,1] neg_hi:[0,1]
	s_nop 0
	v_pk_mul_f32 v[70:71], v[32:33], v[56:57] op_sel:[0,1] op_sel_hi:[0,0] neg_lo:[1,1] neg_hi:[1,0]
	v_pk_fma_f32 v[32:33], v[32:33], v[56:57], v[70:71] op_sel_hi:[0,1,1] neg_lo:[1,0,0] neg_hi:[1,0,0]
	v_pk_add_f32 v[56:57], v[52:53], v[42:43]
	v_pk_add_f32 v[42:43], v[52:53], v[42:43] neg_lo:[0,1] neg_hi:[0,1]
	v_pk_add_f32 v[52:53], v[68:69], v[16:17]
	v_pk_add_f32 v[16:17], v[68:69], v[16:17] neg_lo:[0,1] neg_hi:[0,1]
	v_pk_add_f32 v[70:71], v[56:57], v[52:53]
	v_xor_b32_e32 v69, 0x80000000, v16
	v_mov_b32_e32 v68, v17
	v_pk_add_f32 v[56:57], v[56:57], v[52:53] neg_lo:[0,1] neg_hi:[0,1]
	v_pk_add_f32 v[16:17], v[64:65], v[58:59]
	v_pk_add_f32 v[52:53], v[62:63], v[32:33]
	v_pk_add_f32 v[32:33], v[62:63], v[32:33] neg_lo:[0,1] neg_hi:[0,1]
	v_pk_add_f32 v[58:59], v[64:65], v[58:59] neg_lo:[0,1] neg_hi:[0,1]
	v_pk_add_f32 v[64:65], v[16:17], v[52:53]
	v_pk_add_f32 v[52:53], v[16:17], v[52:53] neg_lo:[0,1] neg_hi:[0,1]
	v_mov_b64_e32 v[16:17], s[90:91]
	v_pk_add_f32 v[78:79], v[42:43], v[68:69]
	v_pk_add_f32 v[42:43], v[42:43], v[68:69] neg_lo:[0,1] neg_hi:[0,1]
	v_pk_add_f32 v[68:69], v[58:59], v[32:33] op_sel:[0,1] op_sel_hi:[1,0] neg_hi:[0,1]
	v_pk_add_f32 v[32:33], v[58:59], v[32:33] op_sel:[0,1] op_sel_hi:[1,0] neg_lo:[0,1]
	v_pk_fma_f32 v[58:59], v[10:11], s[94:95], v[16:17] op_sel_hi:[0,1,1]
	ds_write_b64 v13, v[58:59]
	v_pk_fma_f32 v[58:59], v[178:179], s[90:91], v[178:179] op_sel:[1,0,0] op_sel_hi:[0,1,1]
	v_pk_mul_f32 v[62:63], v[58:59], v[76:77] op_sel:[1,1] op_sel_hi:[0,1] neg_lo:[0,1]
	v_pk_fma_f32 v[62:63], v[58:59], v[76:77], v[62:63] op_sel_hi:[1,0,1]
	ds_write_b64 v13, v[62:63] offset:4224
	v_pk_mul_f32 v[62:63], v[178:179], v[58:59] op_sel:[1,1] op_sel_hi:[0,1] neg_lo:[0,1]
	v_pk_fma_f32 v[58:59], v[178:179], v[58:59], v[62:63] op_sel_hi:[1,0,1]
	s_nop 0
	v_pk_mul_f32 v[62:63], v[58:59], v[84:85] op_sel:[1,1] op_sel_hi:[0,1] neg_lo:[0,1]
	v_pk_fma_f32 v[62:63], v[58:59], v[84:85], v[62:63] op_sel_hi:[1,0,1]
	ds_write_b64 v13, v[62:63] offset:8448
	v_pk_mul_f32 v[62:63], v[178:179], v[58:59] op_sel:[1,1] op_sel_hi:[0,1] neg_lo:[0,1]
	v_pk_fma_f32 v[58:59], v[178:179], v[58:59], v[62:63] op_sel_hi:[1,0,1]
	s_nop 0
	v_pk_mul_f32 v[62:63], v[58:59], v[70:71] op_sel:[1,1] op_sel_hi:[0,1] neg_lo:[0,1]
	v_pk_fma_f32 v[62:63], v[58:59], v[70:71], v[62:63] op_sel_hi:[1,0,1]
	ds_write_b64 v13, v[62:63] offset:12672
	v_pk_mul_f32 v[62:63], v[178:179], v[58:59] op_sel:[1,1] op_sel_hi:[0,1] neg_lo:[0,1]
	v_pk_fma_f32 v[58:59], v[178:179], v[58:59], v[62:63] op_sel_hi:[1,0,1]
	s_nop 0
	v_pk_mul_f32 v[62:63], v[60:61], v[58:59] op_sel:[1,1] op_sel_hi:[1,0] neg_lo:[1,0]
	s_nop 0
	v_pk_fma_f32 v[60:61], v[60:61], v[58:59], v[62:63] op_sel_hi:[0,1,1]
	ds_write_b64 v13, v[60:61] offset:16896
	v_pk_mul_f32 v[60:61], v[178:179], v[58:59] op_sel:[1,1] op_sel_hi:[0,1] neg_lo:[0,1]
	v_pk_fma_f32 v[58:59], v[178:179], v[58:59], v[60:61] op_sel_hi:[1,0,1]
	s_nop 0
	v_pk_mul_f32 v[60:61], v[58:59], v[72:73] op_sel:[1,1] op_sel_hi:[0,1] neg_lo:[0,1]
	v_pk_fma_f32 v[60:61], v[58:59], v[72:73], v[60:61] op_sel_hi:[1,0,1]
	ds_write_b64 v13, v[60:61] offset:21120
	v_pk_mul_f32 v[60:61], v[178:179], v[58:59] op_sel:[1,1] op_sel_hi:[0,1] neg_lo:[0,1]
	v_pk_fma_f32 v[58:59], v[178:179], v[58:59], v[60:61] op_sel_hi:[1,0,1]
	s_nop 0
	v_pk_mul_f32 v[60:61], v[82:83], v[58:59] op_sel:[1,1] op_sel_hi:[1,0] neg_lo:[1,0]
	s_nop 0
	v_pk_fma_f32 v[60:61], v[82:83], v[58:59], v[60:61] op_sel_hi:[0,1,1]
	ds_write_b64 v13, v[60:61] offset:25344
	v_pk_mul_f32 v[60:61], v[178:179], v[58:59] op_sel:[1,1] op_sel_hi:[0,1] neg_lo:[0,1]
	v_pk_fma_f32 v[58:59], v[178:179], v[58:59], v[60:61] op_sel_hi:[1,0,1]
	s_nop 0
	v_pk_mul_f32 v[60:61], v[64:65], v[58:59] op_sel:[1,1] op_sel_hi:[1,0] neg_lo:[1,0]
	s_nop 0
	v_pk_fma_f32 v[60:61], v[64:65], v[58:59], v[60:61] op_sel_hi:[0,1,1]
	ds_write_b64 v13, v[60:61] offset:29568
	v_pk_mul_f32 v[60:61], v[178:179], v[58:59] op_sel:[1,1] op_sel_hi:[0,1] neg_lo:[0,1]
	v_pk_fma_f32 v[58:59], v[178:179], v[58:59], v[60:61] op_sel_hi:[1,0,1]
	s_nop 0
	v_pk_mul_f32 v[60:61], v[46:47], v[58:59] op_sel:[1,1] op_sel_hi:[1,0] neg_lo:[1,0]
	s_nop 0
	v_pk_fma_f32 v[46:47], v[46:47], v[58:59], v[60:61] op_sel_hi:[0,1,1]
	ds_write_b64 v13, v[46:47] offset:33792
	v_pk_mul_f32 v[46:47], v[178:179], v[58:59] op_sel:[1,1] op_sel_hi:[0,1] neg_lo:[0,1]
	v_pk_fma_f32 v[46:47], v[178:179], v[58:59], v[46:47] op_sel_hi:[1,0,1]
	s_nop 0
	v_pk_mul_f32 v[58:59], v[66:67], v[46:47] op_sel:[1,1] op_sel_hi:[1,0] neg_lo:[1,0]
	s_nop 0
	v_pk_fma_f32 v[58:59], v[66:67], v[46:47], v[58:59] op_sel_hi:[0,1,1]
	ds_write_b64 v13, v[58:59] offset:38016
	v_pk_mul_f32 v[58:59], v[178:179], v[46:47] op_sel:[1,1] op_sel_hi:[0,1] neg_lo:[0,1]
	v_pk_fma_f32 v[46:47], v[178:179], v[46:47], v[58:59] op_sel_hi:[1,0,1]
	s_nop 0
	v_pk_mul_f32 v[58:59], v[50:51], v[46:47] op_sel:[1,1] op_sel_hi:[1,0] neg_lo:[1,0]
	s_nop 0
	v_pk_fma_f32 v[50:51], v[50:51], v[46:47], v[58:59] op_sel_hi:[0,1,1]
	ds_write_b64 v13, v[50:51] offset:42240
	v_pk_mul_f32 v[50:51], v[178:179], v[46:47] op_sel:[1,1] op_sel_hi:[0,1] neg_lo:[0,1]
	v_pk_fma_f32 v[46:47], v[178:179], v[46:47], v[50:51] op_sel_hi:[1,0,1]
	s_nop 0
	v_pk_mul_f32 v[50:51], v[78:79], v[46:47] op_sel:[1,1] op_sel_hi:[1,0] neg_lo:[1,0]
	s_nop 0
	v_pk_fma_f32 v[50:51], v[78:79], v[46:47], v[50:51] op_sel_hi:[0,1,1]
	ds_write_b64 v13, v[50:51] offset:46464
	v_pk_mul_f32 v[50:51], v[178:179], v[46:47] op_sel:[1,1] op_sel_hi:[0,1] neg_lo:[0,1]
	v_pk_fma_f32 v[46:47], v[178:179], v[46:47], v[50:51] op_sel_hi:[1,0,1]
	s_nop 0
	v_pk_mul_f32 v[50:51], v[40:41], v[46:47] op_sel:[1,1] op_sel_hi:[1,0] neg_lo:[1,0]
	s_nop 0
	v_pk_fma_f32 v[40:41], v[40:41], v[46:47], v[50:51] op_sel_hi:[0,1,1]
	ds_write_b64 v13, v[40:41] offset:50688
	v_pk_mul_f32 v[40:41], v[178:179], v[46:47] op_sel:[1,1] op_sel_hi:[0,1] neg_lo:[0,1]
	v_pk_fma_f32 v[40:41], v[178:179], v[46:47], v[40:41] op_sel_hi:[1,0,1]
	s_nop 0
	v_pk_mul_f32 v[46:47], v[74:75], v[40:41] op_sel:[1,1] op_sel_hi:[1,0] neg_lo:[1,0]
	s_nop 0
	v_pk_fma_f32 v[46:47], v[74:75], v[40:41], v[46:47] op_sel_hi:[0,1,1]
	ds_write_b64 v13, v[46:47] offset:54912
	v_pk_mul_f32 v[46:47], v[178:179], v[40:41] op_sel:[1,1] op_sel_hi:[0,1] neg_lo:[0,1]
	v_pk_fma_f32 v[40:41], v[178:179], v[40:41], v[46:47] op_sel_hi:[1,0,1]
	s_nop 0
	v_pk_mul_f32 v[46:47], v[44:45], v[40:41] op_sel:[1,1] op_sel_hi:[1,0] neg_lo:[1,0]
	s_nop 0
	v_pk_fma_f32 v[44:45], v[44:45], v[40:41], v[46:47] op_sel_hi:[0,1,1]
	ds_write_b64 v13, v[44:45] offset:59136
	v_pk_mul_f32 v[44:45], v[178:179], v[40:41] op_sel:[1,1] op_sel_hi:[0,1] neg_lo:[0,1]
	v_pk_fma_f32 v[40:41], v[178:179], v[40:41], v[44:45] op_sel_hi:[1,0,1]
	s_nop 0
	v_pk_mul_f32 v[44:45], v[68:69], v[40:41] op_sel:[1,1] op_sel_hi:[1,0] neg_lo:[1,0]
	s_nop 0
	v_pk_fma_f32 v[44:45], v[68:69], v[40:41], v[44:45] op_sel_hi:[0,1,1]
	ds_write_b64 v13, v[44:45] offset:63360
	v_pk_mul_f32 v[44:45], v[178:179], v[40:41] op_sel:[1,1] op_sel_hi:[0,1] neg_lo:[0,1]
	v_pk_fma_f32 v[40:41], v[178:179], v[40:41], v[44:45] op_sel_hi:[1,0,1]
	s_mov_b32 s44, s95
	v_sub_f32_e32 v10, v30, v31
	v_pk_mul_f32 v[30:31], v[40:41], s[44:45]
	s_nop 0
	v_pk_fma_f32 v[30:31], v[10:11], v[40:41], v[30:31] op_sel:[0,0,1] op_sel_hi:[0,1,0]
	v_add_u32_e32 v10, 0x10800, v13
	ds_write_b64 v10, v[30:31]
	v_pk_mul_f32 v[30:31], v[178:179], v[40:41] op_sel:[1,1] op_sel_hi:[0,1] neg_lo:[0,1]
	v_pk_fma_f32 v[30:31], v[178:179], v[40:41], v[30:31] op_sel_hi:[1,0,1]
	s_nop 0
	v_pk_mul_f32 v[40:41], v[54:55], v[30:31] op_sel:[1,1] op_sel_hi:[1,0] neg_lo:[1,0]
	v_add_u32_e32 v10, 0x11880, v13
	v_pk_fma_f32 v[40:41], v[54:55], v[30:31], v[40:41] op_sel_hi:[0,1,1]
	ds_write_b64 v10, v[40:41]
	v_pk_mul_f32 v[40:41], v[178:179], v[30:31] op_sel:[1,1] op_sel_hi:[0,1] neg_lo:[0,1]
	v_pk_fma_f32 v[30:31], v[178:179], v[30:31], v[40:41] op_sel_hi:[1,0,1]
	s_nop 0
	v_pk_mul_f32 v[40:41], v[36:37], v[30:31] op_sel:[1,1] op_sel_hi:[1,0] neg_lo:[1,0]
	v_add_u32_e32 v10, 0x12900, v13
	v_pk_fma_f32 v[36:37], v[36:37], v[30:31], v[40:41] op_sel_hi:[0,1,1]
	ds_write_b64 v10, v[36:37]
	v_pk_mul_f32 v[36:37], v[178:179], v[30:31] op_sel:[1,1] op_sel_hi:[0,1] neg_lo:[0,1]
	v_pk_fma_f32 v[30:31], v[178:179], v[30:31], v[36:37] op_sel_hi:[1,0,1]
	s_nop 0
	v_pk_mul_f32 v[36:37], v[56:57], v[30:31] op_sel:[1,1] op_sel_hi:[1,0] neg_lo:[1,0]
	v_add_u32_e32 v10, 0x13980, v13
	v_pk_fma_f32 v[36:37], v[56:57], v[30:31], v[36:37] op_sel_hi:[0,1,1]
	ds_write_b64 v10, v[36:37]
	v_pk_mul_f32 v[36:37], v[178:179], v[30:31] op_sel:[1,1] op_sel_hi:[0,1] neg_lo:[0,1]
	v_pk_fma_f32 v[30:31], v[178:179], v[30:31], v[36:37] op_sel_hi:[1,0,1]
	s_nop 0
	v_pk_mul_f32 v[36:37], v[26:27], v[30:31] op_sel:[1,1] op_sel_hi:[1,0] neg_lo:[1,0]
	v_add_u32_e32 v10, 0x14a00, v13
	v_pk_fma_f32 v[26:27], v[26:27], v[30:31], v[36:37] op_sel_hi:[0,1,1]
	ds_write_b64 v10, v[26:27]
	v_pk_mul_f32 v[26:27], v[178:179], v[30:31] op_sel:[1,1] op_sel_hi:[0,1] neg_lo:[0,1]
	v_pk_fma_f32 v[26:27], v[178:179], v[30:31], v[26:27] op_sel_hi:[1,0,1]
	s_nop 0
	v_pk_mul_f32 v[30:31], v[48:49], v[26:27] op_sel:[1,1] op_sel_hi:[1,0] neg_lo:[1,0]
	v_add_u32_e32 v10, 0x15a80, v13
	v_pk_fma_f32 v[30:31], v[48:49], v[26:27], v[30:31] op_sel_hi:[0,1,1]
	ds_write_b64 v10, v[30:31]
	v_pk_mul_f32 v[30:31], v[178:179], v[26:27] op_sel:[1,1] op_sel_hi:[0,1] neg_lo:[0,1]
	v_pk_fma_f32 v[26:27], v[178:179], v[26:27], v[30:31] op_sel_hi:[1,0,1]
	s_nop 0
	v_pk_mul_f32 v[30:31], v[28:29], v[26:27] op_sel:[1,1] op_sel_hi:[1,0] neg_lo:[1,0]
	v_add_u32_e32 v10, 0x16b00, v13
	v_pk_fma_f32 v[28:29], v[28:29], v[26:27], v[30:31] op_sel_hi:[0,1,1]
	ds_write_b64 v10, v[28:29]
	v_pk_mul_f32 v[28:29], v[178:179], v[26:27] op_sel:[1,1] op_sel_hi:[0,1] neg_lo:[0,1]
	v_pk_fma_f32 v[26:27], v[178:179], v[26:27], v[28:29] op_sel_hi:[1,0,1]
	s_nop 0
	v_pk_mul_f32 v[28:29], v[52:53], v[26:27] op_sel:[1,1] op_sel_hi:[1,0] neg_lo:[1,0]
	v_add_u32_e32 v10, 0x17b80, v13
	v_pk_fma_f32 v[28:29], v[52:53], v[26:27], v[28:29] op_sel_hi:[0,1,1]
	ds_write_b64 v10, v[28:29]
	v_pk_mul_f32 v[28:29], v[178:179], v[26:27] op_sel:[1,1] op_sel_hi:[0,1] neg_lo:[0,1]
	v_pk_fma_f32 v[26:27], v[178:179], v[26:27], v[28:29] op_sel_hi:[1,0,1]
	s_nop 0
	v_pk_mul_f32 v[28:29], v[20:21], v[26:27] op_sel:[1,1] op_sel_hi:[1,0] neg_lo:[1,0]
	v_add_u32_e32 v10, 0x18c00, v13
	v_pk_fma_f32 v[20:21], v[20:21], v[26:27], v[28:29] op_sel_hi:[0,1,1]
	ds_write_b64 v10, v[20:21]
	v_pk_mul_f32 v[20:21], v[178:179], v[26:27] op_sel:[1,1] op_sel_hi:[0,1] neg_lo:[0,1]
	v_pk_fma_f32 v[20:21], v[178:179], v[26:27], v[20:21] op_sel_hi:[1,0,1]
	s_nop 0
	v_pk_mul_f32 v[26:27], v[38:39], v[20:21] op_sel:[1,1] op_sel_hi:[1,0] neg_lo:[1,0]
	v_add_u32_e32 v10, 0x19c80, v13
	v_pk_fma_f32 v[26:27], v[38:39], v[20:21], v[26:27] op_sel_hi:[0,1,1]
	ds_write_b64 v10, v[26:27]
	v_pk_mul_f32 v[26:27], v[178:179], v[20:21] op_sel:[1,1] op_sel_hi:[0,1] neg_lo:[0,1]
	v_pk_fma_f32 v[20:21], v[178:179], v[20:21], v[26:27] op_sel_hi:[1,0,1]
	s_nop 0
	v_pk_mul_f32 v[26:27], v[24:25], v[20:21] op_sel:[1,1] op_sel_hi:[1,0] neg_lo:[1,0]
	v_add_u32_e32 v10, 0x1ad00, v13
	v_pk_fma_f32 v[24:25], v[24:25], v[20:21], v[26:27] op_sel_hi:[0,1,1]
	ds_write_b64 v10, v[24:25]
	v_pk_mul_f32 v[24:25], v[178:179], v[20:21] op_sel:[1,1] op_sel_hi:[0,1] neg_lo:[0,1]
	v_pk_fma_f32 v[20:21], v[178:179], v[20:21], v[24:25] op_sel_hi:[1,0,1]
	s_nop 0
	v_pk_mul_f32 v[24:25], v[42:43], v[20:21] op_sel:[1,1] op_sel_hi:[1,0] neg_lo:[1,0]
	v_add_u32_e32 v10, 0x1bd80, v13
	v_pk_fma_f32 v[24:25], v[42:43], v[20:21], v[24:25] op_sel_hi:[0,1,1]
	ds_write_b64 v10, v[24:25]
	v_pk_mul_f32 v[24:25], v[178:179], v[20:21] op_sel:[1,1] op_sel_hi:[0,1] neg_lo:[0,1]
	v_pk_fma_f32 v[20:21], v[178:179], v[20:21], v[24:25] op_sel_hi:[1,0,1]
	s_nop 0
	v_pk_mul_f32 v[24:25], v[14:15], v[20:21] op_sel:[1,1] op_sel_hi:[1,0] neg_lo:[1,0]
	v_add_u32_e32 v10, 0x1ce00, v13
	v_pk_fma_f32 v[14:15], v[14:15], v[20:21], v[24:25] op_sel_hi:[0,1,1]
	ds_write_b64 v10, v[14:15]
	v_pk_mul_f32 v[14:15], v[178:179], v[20:21] op_sel:[1,1] op_sel_hi:[0,1] neg_lo:[0,1]
	v_pk_fma_f32 v[14:15], v[178:179], v[20:21], v[14:15] op_sel_hi:[1,0,1]
	s_nop 0
	v_pk_mul_f32 v[20:21], v[34:35], v[14:15] op_sel:[1,1] op_sel_hi:[1,0] neg_lo:[1,0]
	v_add_u32_e32 v10, 0x1de80, v13
	v_pk_fma_f32 v[20:21], v[34:35], v[14:15], v[20:21] op_sel_hi:[0,1,1]
	ds_write_b64 v10, v[20:21]
	v_pk_mul_f32 v[20:21], v[178:179], v[14:15] op_sel:[1,1] op_sel_hi:[0,1] neg_lo:[0,1]
	v_pk_fma_f32 v[14:15], v[178:179], v[14:15], v[20:21] op_sel_hi:[1,0,1]
	s_nop 0
	v_pk_mul_f32 v[20:21], v[18:19], v[14:15] op_sel:[1,1] op_sel_hi:[1,0] neg_lo:[1,0]
	v_add_u32_e32 v10, 0x1ef00, v13
	v_pk_fma_f32 v[18:19], v[18:19], v[14:15], v[20:21] op_sel_hi:[0,1,1]
	ds_write_b64 v10, v[18:19]
	v_pk_mul_f32 v[18:19], v[178:179], v[14:15] op_sel:[1,1] op_sel_hi:[0,1] neg_lo:[0,1]
	v_pk_fma_f32 v[14:15], v[178:179], v[14:15], v[18:19] op_sel_hi:[1,0,1]
	s_nop 0
	v_pk_mul_f32 v[18:19], v[32:33], v[14:15] op_sel:[1,1] op_sel_hi:[1,0] neg_lo:[1,0]
	v_add_u32_e32 v10, 0x1ff80, v13
	v_pk_fma_f32 v[14:15], v[32:33], v[14:15], v[18:19] op_sel_hi:[0,1,1]
	ds_write_b64 v10, v[14:15]
	v_mov_b32_e32 v10, v174
	v_mov_b32_e32 v13, v172
	s_waitcnt lgkmcnt(0)
	s_barrier
	v_mov_b32_e32 v14, v180
	v_xad_u32 v30, v13, 3, v10
	v_lshl_add_u32 v73, v30, 3, 0
	v_xad_u32 v30, v13, 4, v10
	v_lshl_add_u32 v72, v30, 3, 0
	v_xad_u32 v30, v13, 5, v10
	v_lshl_add_u32 v71, v30, 3, 0
	v_xad_u32 v30, v13, 6, v10
	v_lshl_add_u32 v70, v30, 3, 0
	v_xad_u32 v30, v13, 7, v10
	v_lshl_add_u32 v69, v30, 3, 0
	v_xad_u32 v30, v13, 8, v10
	v_lshl_add_u32 v30, v30, 3, 0
	v_add_u32_e32 v68, 0x800, v30
	v_xad_u32 v30, v13, 9, v10
	v_lshl_add_u32 v30, v30, 3, 0
	v_add_u32_e32 v67, 0x800, v30
	v_xad_u32 v30, v13, 10, v10
	v_lshl_add_u32 v30, v30, 3, 0
	v_add_u32_e32 v66, 0x800, v30
	v_xad_u32 v30, v13, 11, v10
	v_lshl_add_u32 v30, v30, 3, 0
	v_add_u32_e32 v18, v13, v10
	v_add_u32_e32 v65, 0x800, v30
	v_xad_u32 v30, v13, 12, v10
	v_mov_b32_e32 v15, v181
	v_lshl_add_u32 v76, v18, 3, 0
	v_lshl_add_u32 v30, v30, 3, 0
	ds_read2_b64 v[18:21], v76 offset1:16
	ds_read2_b64 v[40:43], v68 offset1:16
	v_add_u32_e32 v64, 0x800, v30
	v_xad_u32 v30, v13, 13, v10
	v_xad_u32 v22, v13, 1, v10
	v_lshl_add_u32 v30, v30, 3, 0
	v_lshl_add_u32 v75, v22, 3, 0
	v_xad_u32 v26, v13, 2, v10
	v_add_u32_e32 v63, 0x800, v30
	v_xad_u32 v30, v13, 14, v10
	v_xad_u32 v10, v13, 15, v10
	ds_read2_b64 v[22:25], v75 offset0:32 offset1:48
	ds_read2_b64 v[48:51], v67 offset0:32 offset1:48
	v_lshl_add_u32 v30, v30, 3, 0
	v_lshl_add_u32 v10, v10, 3, 0
	v_lshl_add_u32 v74, v26, 3, 0
	v_add_u32_e32 v62, 0x800, v30
	v_add_u32_e32 v13, 0x800, v10
	v_mov_b32_e32 v10, v1
	ds_read2_b64 v[26:29], v74 offset0:64 offset1:80
	ds_read2_b64 v[58:61], v73 offset0:96 offset1:112
	ds_read2_b64 v[78:81], v72 offset0:128 offset1:144
	ds_read2_b64 v[82:85], v71 offset0:160 offset1:176
	ds_read2_b64 v[86:89], v70 offset0:192 offset1:208
	ds_read2_b64 v[90:93], v69 offset0:224 offset1:240
	ds_read2_b64 v[54:57], v66 offset0:64 offset1:80
	ds_read2_b64 v[94:97], v65 offset0:96 offset1:112
	ds_read2_b64 v[98:101], v64 offset0:128 offset1:144
	ds_read2_b64 v[102:105], v63 offset0:160 offset1:176
	ds_read2_b64 v[106:109], v62 offset0:192 offset1:208
	ds_read2_b64 v[110:113], v13 offset0:224 offset1:240
	s_waitcnt lgkmcnt(14)
	v_pk_add_f32 v[114:115], v[18:19], v[40:41]
	v_pk_add_f32 v[40:41], v[18:19], v[40:41] neg_lo:[0,1] neg_hi:[0,1]
	v_pk_add_f32 v[18:19], v[20:21], v[42:43]
	v_pk_add_f32 v[20:21], v[20:21], v[42:43] neg_lo:[0,1] neg_hi:[0,1]
	v_mov_b32_e32 v30, v164
	v_mov_b32_e32 v32, v165
	v_mov_b32_e32 v34, v166
	v_mov_b32_e32 v10, v167
	v_mov_b32_e32 v38, v168
	v_mov_b32_e32 v36, v169
	v_mov_b32_e32 v46, v170
	v_mov_b32_e32 v31, v171
	v_pk_mul_f32 v[42:43], v[20:21], v[46:47] op_sel:[1,0] op_sel_hi:[0,0] neg_lo:[1,1] neg_hi:[0,1]
	s_mov_b32 s14, s95
	v_pk_fma_f32 v[44:45], v[20:21], v[30:31], v[42:43] op_sel_hi:[1,0,1]
	s_waitcnt lgkmcnt(12)
	v_pk_add_f32 v[20:21], v[22:23], v[48:49]
	v_pk_add_f32 v[22:23], v[22:23], v[48:49] neg_lo:[0,1] neg_hi:[0,1]
	s_mov_b32 s15, s94
	v_pk_mul_f32 v[42:43], v[22:23], v[36:37] op_sel:[1,0] op_sel_hi:[0,0] neg_lo:[1,1] neg_hi:[0,1]
	s_nop 0
	v_pk_fma_f32 v[48:49], v[22:23], v[32:33], v[42:43] op_sel_hi:[1,0,1]
	v_pk_add_f32 v[22:23], v[24:25], v[50:51]
	v_pk_add_f32 v[24:25], v[24:25], v[50:51] neg_lo:[0,1] neg_hi:[0,1]
	s_nop 0
	v_pk_mul_f32 v[42:43], v[24:25], v[38:39] op_sel:[1,0] op_sel_hi:[0,0] neg_lo:[1,1] neg_hi:[0,1]
	s_nop 0
	v_pk_fma_f32 v[52:53], v[24:25], v[34:35], v[42:43] op_sel_hi:[1,0,1]
	s_waitcnt lgkmcnt(5)
	v_pk_add_f32 v[24:25], v[26:27], v[54:55]
	v_pk_add_f32 v[26:27], v[26:27], v[54:55] neg_lo:[0,1] neg_hi:[0,1]
	s_nop 0
	v_pk_mul_f32 v[42:43], v[26:27], v[10:11] op_sel:[1,0] op_sel_hi:[0,0] neg_lo:[1,1] neg_hi:[0,1]
	s_nop 0
	v_pk_fma_f32 v[54:55], v[26:27], v[10:11], v[42:43] op_sel_hi:[1,0,1]
	v_pk_add_f32 v[26:27], v[28:29], v[56:57]
	v_pk_add_f32 v[28:29], v[28:29], v[56:57] neg_lo:[0,1] neg_hi:[0,1]
	s_nop 0
	v_pk_mul_f32 v[42:43], v[28:29], v[38:39] op_sel_hi:[1,0]
	s_nop 0
	v_pk_fma_f32 v[56:57], v[28:29], v[34:35], v[42:43] op_sel:[1,0,0] op_sel_hi:[0,0,1] neg_lo:[1,1,0] neg_hi:[0,1,0]
	s_waitcnt lgkmcnt(4)
	v_pk_add_f32 v[42:43], v[58:59], v[94:95] neg_lo:[0,1] neg_hi:[0,1]
	v_pk_add_f32 v[28:29], v[58:59], v[94:95]
	v_pk_mul_f32 v[50:51], v[42:43], v[36:37] op_sel_hi:[1,0]
	s_nop 0
	v_pk_fma_f32 v[58:59], v[42:43], v[32:33], v[50:51] op_sel:[1,0,0] op_sel_hi:[0,0,1] neg_lo:[1,1,0] neg_hi:[0,1,0]
	v_pk_add_f32 v[50:51], v[60:61], v[96:97] neg_lo:[0,1] neg_hi:[0,1]
	v_pk_add_f32 v[42:43], v[60:61], v[96:97]
	v_pk_mul_f32 v[60:61], v[50:51], v[46:47] op_sel_hi:[1,0]
	v_xor_b32_e32 v94, 0x80000000, v51
	v_mov_b32_e32 v95, v50
	s_waitcnt lgkmcnt(3)
	v_pk_add_f32 v[50:51], v[78:79], v[98:99]
	v_pk_add_f32 v[78:79], v[78:79], v[98:99] neg_lo:[0,1] neg_hi:[0,1]
	v_pk_fma_f32 v[60:61], v[94:95], v[30:31], v[60:61] op_sel_hi:[1,0,1] neg_lo:[0,1,0] neg_hi:[0,1,0]
	v_xor_b32_e32 v95, 0x80000000, v78
	v_mov_b32_e32 v94, v79
	v_pk_add_f32 v[78:79], v[80:81], v[100:101]
	v_pk_add_f32 v[80:81], v[80:81], v[100:101] neg_lo:[0,1] neg_hi:[0,1]
	s_nop 0
	v_pk_mul_f32 v[96:97], v[80:81], v[46:47] op_sel_hi:[1,0] neg_lo:[0,1] neg_hi:[0,1]
	s_nop 0
	v_pk_fma_f32 v[80:81], v[80:81], v[30:31], v[96:97] op_sel:[1,0,0] op_sel_hi:[0,0,1] neg_lo:[1,1,0] neg_hi:[0,1,0]
	s_waitcnt lgkmcnt(2)
	v_pk_add_f32 v[96:97], v[82:83], v[102:103]
	v_pk_add_f32 v[82:83], v[82:83], v[102:103] neg_lo:[0,1] neg_hi:[0,1]
	s_nop 0
	v_pk_mul_f32 v[98:99], v[82:83], v[36:37] op_sel_hi:[1,0] neg_lo:[0,1] neg_hi:[0,1]
	s_nop 0
	v_pk_fma_f32 v[82:83], v[82:83], v[32:33], v[98:99] op_sel:[1,0,0] op_sel_hi:[0,0,1] neg_lo:[1,1,0] neg_hi:[0,1,0]
	v_pk_add_f32 v[98:99], v[84:85], v[104:105]
	v_pk_add_f32 v[84:85], v[84:85], v[104:105] neg_lo:[0,1] neg_hi:[0,1]
	s_nop 0
	v_pk_mul_f32 v[100:101], v[84:85], v[38:39] op_sel_hi:[1,0] neg_lo:[0,1] neg_hi:[0,1]
	s_nop 0
	v_pk_fma_f32 v[84:85], v[84:85], v[34:35], v[100:101] op_sel:[1,0,0] op_sel_hi:[0,0,1] neg_lo:[1,1,0] neg_hi:[0,1,0]
	s_waitcnt lgkmcnt(1)
	v_pk_add_f32 v[100:101], v[86:87], v[106:107]
	v_pk_add_f32 v[86:87], v[86:87], v[106:107] neg_lo:[0,1] neg_hi:[0,1]
	s_nop 0
	v_pk_mul_f32 v[102:103], v[86:87], v[10:11] op_sel:[1,0] op_sel_hi:[0,0] neg_lo:[1,1] neg_hi:[0,1]
	s_nop 0
	v_pk_fma_f32 v[86:87], v[86:87], v[10:11], v[102:103] op_sel_hi:[1,0,1] neg_lo:[0,1,0] neg_hi:[0,1,0]
	v_pk_add_f32 v[102:103], v[88:89], v[108:109]
	v_pk_add_f32 v[88:89], v[88:89], v[108:109] neg_lo:[0,1] neg_hi:[0,1]
	s_nop 0
	v_pk_mul_f32 v[38:39], v[88:89], v[38:39] op_sel:[1,0] op_sel_hi:[0,0] neg_lo:[1,1] neg_hi:[0,1]
	s_nop 0
	v_pk_fma_f32 v[88:89], v[88:89], v[34:35], v[38:39] op_sel_hi:[1,0,1] neg_lo:[0,1,0] neg_hi:[0,1,0]
	s_waitcnt lgkmcnt(0)
	v_pk_add_f32 v[38:39], v[90:91], v[110:111] neg_lo:[0,1] neg_hi:[0,1]
	v_pk_add_f32 v[34:35], v[90:91], v[110:111]
	v_pk_mul_f32 v[90:91], v[38:39], v[36:37] op_sel:[1,0] op_sel_hi:[0,0] neg_lo:[1,1] neg_hi:[0,1]
	s_nop 0
	v_pk_fma_f32 v[90:91], v[38:39], v[32:33], v[90:91] op_sel_hi:[1,0,1] neg_lo:[0,1,0] neg_hi:[0,1,0]
	v_pk_add_f32 v[38:39], v[92:93], v[112:113]
	v_pk_add_f32 v[92:93], v[92:93], v[112:113] neg_lo:[0,1] neg_hi:[0,1]
	s_nop 0
	v_pk_mul_f32 v[46:47], v[92:93], v[46:47] op_sel:[1,0] op_sel_hi:[0,0] neg_lo:[1,1] neg_hi:[0,1]
	s_nop 0
	v_pk_fma_f32 v[92:93], v[92:93], v[30:31], v[46:47] op_sel_hi:[1,0,1] neg_lo:[0,1,0] neg_hi:[0,1,0]
	v_pk_add_f32 v[46:47], v[18:19], v[78:79]
	v_pk_add_f32 v[18:19], v[18:19], v[78:79] neg_lo:[0,1] neg_hi:[0,1]
	v_pk_add_f32 v[30:31], v[114:115], v[50:51]
	v_pk_mul_f32 v[78:79], v[18:19], v[36:37] op_sel:[1,0] op_sel_hi:[0,0] neg_lo:[1,1] neg_hi:[0,1]
	v_pk_add_f32 v[50:51], v[114:115], v[50:51] neg_lo:[0,1] neg_hi:[0,1]
	v_pk_fma_f32 v[78:79], v[18:19], v[32:33], v[78:79] op_sel_hi:[1,0,1]
	v_pk_add_f32 v[18:19], v[20:21], v[96:97]
	v_pk_add_f32 v[20:21], v[20:21], v[96:97] neg_lo:[0,1] neg_hi:[0,1]
	s_nop 0
	v_pk_mul_f32 v[96:97], v[20:21], v[10:11] op_sel:[1,0] op_sel_hi:[0,0] neg_lo:[1,1] neg_hi:[0,1]
	s_nop 0
	v_pk_fma_f32 v[20:21], v[20:21], v[10:11], v[96:97] op_sel_hi:[1,0,1]
	v_pk_add_f32 v[96:97], v[22:23], v[98:99]
	v_pk_add_f32 v[22:23], v[22:23], v[98:99] neg_lo:[0,1] neg_hi:[0,1]
	s_nop 0
	v_pk_mul_f32 v[98:99], v[22:23], v[36:37] op_sel_hi:[1,0]
	v_xor_b32_e32 v104, 0x80000000, v23
	v_mov_b32_e32 v105, v22
	v_pk_add_f32 v[22:23], v[24:25], v[100:101]
	v_pk_add_f32 v[24:25], v[24:25], v[100:101] neg_lo:[0,1] neg_hi:[0,1]
	v_pk_fma_f32 v[98:99], v[104:105], v[32:33], v[98:99] op_sel_hi:[1,0,1] neg_lo:[0,1,0] neg_hi:[0,1,0]
	v_xor_b32_e32 v101, 0x80000000, v24
	v_mov_b32_e32 v100, v25
	v_pk_add_f32 v[24:25], v[26:27], v[102:103]
	v_pk_add_f32 v[26:27], v[26:27], v[102:103] neg_lo:[0,1] neg_hi:[0,1]
	s_nop 0
	v_pk_mul_f32 v[102:103], v[26:27], v[36:37] op_sel_hi:[1,0] neg_lo:[0,1] neg_hi:[0,1]
	v_xor_b32_e32 v104, 0x80000000, v27
	v_mov_b32_e32 v105, v26
	v_pk_add_f32 v[26:27], v[28:29], v[34:35]
	v_pk_add_f32 v[28:29], v[28:29], v[34:35] neg_lo:[0,1] neg_hi:[0,1]
	v_pk_fma_f32 v[102:103], v[104:105], v[32:33], v[102:103] op_sel_hi:[1,0,1] neg_lo:[0,1,0] neg_hi:[0,1,0]
	v_pk_mul_f32 v[34:35], v[28:29], v[10:11] op_sel:[1,0] op_sel_hi:[0,0] neg_lo:[1,1] neg_hi:[0,1]
	v_pk_add_f32 v[104:105], v[30:31], v[22:23] neg_lo:[0,1] neg_hi:[0,1]
	v_pk_fma_f32 v[28:29], v[28:29], v[10:11], v[34:35] op_sel_hi:[1,0,1] neg_lo:[0,1,0] neg_hi:[0,1,0]
	v_pk_add_f32 v[34:35], v[42:43], v[38:39]
	v_pk_add_f32 v[38:39], v[42:43], v[38:39] neg_lo:[0,1] neg_hi:[0,1]
	s_nop 0
	v_pk_mul_f32 v[42:43], v[38:39], v[36:37] op_sel:[1,0] op_sel_hi:[0,0] neg_lo:[1,1] neg_hi:[0,1]
	s_nop 0
	v_pk_fma_f32 v[42:43], v[38:39], v[32:33], v[42:43] op_sel_hi:[1,0,1] neg_lo:[0,1,0] neg_hi:[0,1,0]
	v_pk_add_f32 v[38:39], v[30:31], v[22:23]
	v_pk_add_f32 v[22:23], v[46:47], v[24:25]
	v_pk_add_f32 v[24:25], v[46:47], v[24:25] neg_lo:[0,1] neg_hi:[0,1]
	s_nop 0
	v_pk_mul_f32 v[30:31], v[24:25], v[10:11] op_sel:[1,0] op_sel_hi:[0,0] neg_lo:[1,1] neg_hi:[0,1]
	s_nop 0
	v_pk_fma_f32 v[24:25], v[24:25], v[10:11], v[30:31] op_sel_hi:[1,0,1]
	v_pk_add_f32 v[30:31], v[18:19], v[26:27]
	v_pk_add_f32 v[18:19], v[18:19], v[26:27] neg_lo:[0,1] neg_hi:[0,1]
	s_nop 0
	v_xor_b32_e32 v27, 0x80000000, v18
	v_mov_b32_e32 v26, v19
	v_pk_add_f32 v[18:19], v[96:97], v[34:35]
	v_pk_add_f32 v[34:35], v[96:97], v[34:35] neg_lo:[0,1] neg_hi:[0,1]
	s_nop 0
	v_pk_mul_f32 v[46:47], v[34:35], v[10:11] op_sel:[1,0] op_sel_hi:[0,0] neg_lo:[1,1] neg_hi:[0,1]
	s_nop 0
	v_pk_fma_f32 v[34:35], v[34:35], v[10:11], v[46:47] op_sel_hi:[1,0,1] neg_lo:[0,1,0] neg_hi:[0,1,0]
	v_pk_add_f32 v[46:47], v[38:39], v[30:31]
	v_pk_add_f32 v[38:39], v[38:39], v[30:31] neg_lo:[0,1] neg_hi:[0,1]
	v_pk_add_f32 v[30:31], v[22:23], v[18:19]
	v_pk_add_f32 v[18:19], v[22:23], v[18:19] neg_lo:[0,1] neg_hi:[0,1]
	v_pk_add_f32 v[96:97], v[46:47], v[30:31]
	v_xor_b32_e32 v23, 0x80000000, v18
	v_mov_b32_e32 v22, v19
	v_pk_add_f32 v[18:19], v[104:105], v[26:27]
	v_pk_add_f32 v[104:105], v[104:105], v[26:27] neg_lo:[0,1] neg_hi:[0,1]
	v_pk_add_f32 v[26:27], v[24:25], v[34:35]
	v_pk_add_f32 v[24:25], v[24:25], v[34:35] neg_lo:[0,1] neg_hi:[0,1]
	v_pk_add_f32 v[30:31], v[46:47], v[30:31] neg_lo:[0,1] neg_hi:[0,1]
	v_xor_b32_e32 v35, 0x80000000, v24
	v_mov_b32_e32 v34, v25
	v_pk_add_f32 v[24:25], v[50:51], v[100:101]
	v_pk_add_f32 v[100:101], v[50:51], v[100:101] neg_lo:[0,1] neg_hi:[0,1]
	v_pk_add_f32 v[50:51], v[78:79], v[102:103] neg_lo:[0,1] neg_hi:[0,1]
	v_pk_add_f32 v[46:47], v[38:39], v[22:23]
	v_pk_add_f32 v[22:23], v[38:39], v[22:23] neg_lo:[0,1] neg_hi:[0,1]
	v_pk_add_f32 v[106:107], v[18:19], v[26:27]
	v_pk_add_f32 v[26:27], v[18:19], v[26:27] neg_lo:[0,1] neg_hi:[0,1]
	v_pk_add_f32 v[38:39], v[104:105], v[34:35]
	v_pk_add_f32 v[18:19], v[104:105], v[34:35] neg_lo:[0,1] neg_hi:[0,1]
	v_pk_add_f32 v[34:35], v[78:79], v[102:103]
	v_pk_mul_f32 v[78:79], v[10:11], v[50:51] op_sel:[0,1] op_sel_hi:[0,0] neg_lo:[1,1] neg_hi:[1,0]
	v_pk_fma_f32 v[78:79], v[10:11], v[50:51], v[78:79] op_sel_hi:[0,1,1]
	v_pk_add_f32 v[50:51], v[20:21], v[28:29]
	v_pk_add_f32 v[20:21], v[20:21], v[28:29] neg_lo:[0,1] neg_hi:[0,1]
	s_nop 0
	v_xor_b32_e32 v29, 0x80000000, v20
	v_mov_b32_e32 v28, v21
	v_pk_add_f32 v[20:21], v[98:99], v[42:43]
	v_pk_add_f32 v[42:43], v[98:99], v[42:43] neg_lo:[0,1] neg_hi:[0,1]
	s_nop 0
	v_pk_mul_f32 v[98:99], v[10:11], v[42:43] op_sel:[0,1] op_sel_hi:[0,0] neg_lo:[1,1] neg_hi:[1,0]
	v_pk_fma_f32 v[42:43], v[10:11], v[42:43], v[98:99] op_sel_hi:[0,1,1] neg_lo:[1,0,0] neg_hi:[1,0,0]
	v_pk_add_f32 v[98:99], v[24:25], v[50:51]
	v_pk_add_f32 v[24:25], v[24:25], v[50:51] neg_lo:[0,1] neg_hi:[0,1]
	v_pk_add_f32 v[50:51], v[34:35], v[20:21]
	v_pk_add_f32 v[20:21], v[34:35], v[20:21] neg_lo:[0,1] neg_hi:[0,1]
	v_pk_add_f32 v[104:105], v[98:99], v[50:51]
	v_xor_b32_e32 v103, 0x80000000, v20
	v_mov_b32_e32 v102, v21
	v_pk_add_f32 v[34:35], v[98:99], v[50:51] neg_lo:[0,1] neg_hi:[0,1]
	v_pk_add_f32 v[20:21], v[100:101], v[28:29]
	v_pk_add_f32 v[98:99], v[100:101], v[28:29] neg_lo:[0,1] neg_hi:[0,1]
	v_pk_add_f32 v[28:29], v[78:79], v[42:43]
	v_pk_add_f32 v[42:43], v[78:79], v[42:43] neg_lo:[0,1] neg_hi:[0,1]
	v_pk_add_f32 v[100:101], v[20:21], v[28:29]
	v_xor_b32_e32 v79, 0x80000000, v42
	v_mov_b32_e32 v78, v43
	v_pk_add_f32 v[28:29], v[20:21], v[28:29] neg_lo:[0,1] neg_hi:[0,1]
	v_pk_add_f32 v[42:43], v[98:99], v[78:79]
	v_pk_add_f32 v[20:21], v[98:99], v[78:79] neg_lo:[0,1] neg_hi:[0,1]
	v_pk_add_f32 v[78:79], v[40:41], v[94:95]
	v_pk_add_f32 v[94:95], v[40:41], v[94:95] neg_lo:[0,1] neg_hi:[0,1]
	v_pk_add_f32 v[40:41], v[44:45], v[80:81]
	v_pk_add_f32 v[44:45], v[44:45], v[80:81] neg_lo:[0,1] neg_hi:[0,1]
	v_pk_add_f32 v[50:51], v[24:25], v[102:103]
	v_pk_mul_f32 v[80:81], v[36:37], v[44:45] op_sel:[0,1] op_sel_hi:[0,0] neg_lo:[1,1] neg_hi:[1,0]
	v_pk_fma_f32 v[44:45], v[32:33], v[44:45], v[80:81] op_sel_hi:[0,1,1]
	v_pk_add_f32 v[80:81], v[48:49], v[82:83]
	v_pk_add_f32 v[48:49], v[48:49], v[82:83] neg_lo:[0,1] neg_hi:[0,1]
	v_pk_add_f32 v[24:25], v[24:25], v[102:103] neg_lo:[0,1] neg_hi:[0,1]
	v_pk_mul_f32 v[82:83], v[10:11], v[48:49] op_sel:[0,1] op_sel_hi:[0,0] neg_lo:[1,1] neg_hi:[1,0]
	v_pk_fma_f32 v[82:83], v[10:11], v[48:49], v[82:83] op_sel_hi:[0,1,1]
	v_pk_add_f32 v[48:49], v[52:53], v[84:85]
	v_pk_add_f32 v[52:53], v[52:53], v[84:85] neg_lo:[0,1] neg_hi:[0,1]
	s_nop 0
	v_pk_mul_f32 v[84:85], v[32:33], v[52:53] op_sel:[0,1] op_sel_hi:[0,0] neg_lo:[1,1] neg_hi:[1,0]
	v_pk_fma_f32 v[52:53], v[36:37], v[52:53], v[84:85] op_sel_hi:[0,1,1]
	v_pk_add_f32 v[84:85], v[54:55], v[86:87]
	v_pk_add_f32 v[54:55], v[54:55], v[86:87] neg_lo:[0,1] neg_hi:[0,1]
	s_nop 0
	v_xor_b32_e32 v87, 0x80000000, v54
	v_mov_b32_e32 v86, v55
	v_pk_add_f32 v[54:55], v[56:57], v[88:89]
	v_pk_add_f32 v[56:57], v[56:57], v[88:89] neg_lo:[0,1] neg_hi:[0,1]
	s_nop 0
	v_pk_mul_f32 v[88:89], v[32:33], v[56:57] op_sel:[0,1] op_sel_hi:[0,0] neg_lo:[1,1] neg_hi:[1,0]
	v_pk_fma_f32 v[56:57], v[36:37], v[56:57], v[88:89] op_sel_hi:[0,1,1] neg_lo:[1,0,0] neg_hi:[1,0,0]
	v_pk_add_f32 v[88:89], v[58:59], v[90:91]
	v_pk_add_f32 v[58:59], v[58:59], v[90:91] neg_lo:[0,1] neg_hi:[0,1]
	s_nop 0
	v_pk_mul_f32 v[90:91], v[10:11], v[58:59] op_sel:[0,1] op_sel_hi:[0,0] neg_lo:[1,1] neg_hi:[1,0]
	v_pk_fma_f32 v[58:59], v[10:11], v[58:59], v[90:91] op_sel_hi:[0,1,1] neg_lo:[1,0,0] neg_hi:[1,0,0]
	v_pk_add_f32 v[90:91], v[60:61], v[92:93]
	v_pk_add_f32 v[60:61], v[60:61], v[92:93] neg_lo:[0,1] neg_hi:[0,1]
	s_nop 0
	v_pk_mul_f32 v[36:37], v[36:37], v[60:61] op_sel:[0,1] op_sel_hi:[0,0] neg_lo:[1,1] neg_hi:[1,0]
	v_pk_fma_f32 v[36:37], v[32:33], v[60:61], v[36:37] op_sel_hi:[0,1,1] neg_lo:[1,0,0] neg_hi:[1,0,0]
	v_pk_add_f32 v[32:33], v[78:79], v[84:85]
	v_pk_add_f32 v[60:61], v[78:79], v[84:85] neg_lo:[0,1] neg_hi:[0,1]
	v_pk_add_f32 v[78:79], v[54:55], v[40:41]
	v_pk_add_f32 v[40:41], v[40:41], v[54:55] neg_lo:[0,1] neg_hi:[0,1]
	s_nop 0
	v_pk_mul_f32 v[54:55], v[10:11], v[40:41] op_sel:[0,1] op_sel_hi:[0,0] neg_lo:[1,1] neg_hi:[1,0]
	v_pk_fma_f32 v[54:55], v[10:11], v[40:41], v[54:55] op_sel_hi:[0,1,1]
	v_pk_add_f32 v[40:41], v[80:81], v[88:89]
	v_pk_add_f32 v[80:81], v[80:81], v[88:89] neg_lo:[0,1] neg_hi:[0,1]
	s_nop 0
	v_xor_b32_e32 v85, 0x80000000, v80
	v_mov_b32_e32 v84, v81
	v_pk_add_f32 v[80:81], v[48:49], v[90:91]
	v_pk_add_f32 v[48:49], v[48:49], v[90:91] neg_lo:[0,1] neg_hi:[0,1]
	v_pk_add_f32 v[90:91], v[78:79], v[80:81]
	v_pk_mul_f32 v[88:89], v[10:11], v[48:49] op_sel:[0,1] op_sel_hi:[0,0] neg_lo:[1,1] neg_hi:[1,0]
	v_pk_fma_f32 v[48:49], v[10:11], v[48:49], v[88:89] op_sel_hi:[0,1,1] neg_lo:[1,0,0] neg_hi:[1,0,0]
	v_pk_add_f32 v[88:89], v[32:33], v[40:41]
	v_pk_add_f32 v[32:33], v[32:33], v[40:41] neg_lo:[0,1] neg_hi:[0,1]
	v_pk_add_f32 v[40:41], v[78:79], v[80:81] neg_lo:[0,1] neg_hi:[0,1]
	v_pk_add_f32 v[80:81], v[88:89], v[90:91] neg_lo:[0,1] neg_hi:[0,1]
	v_pk_add_f32 v[92:93], v[32:33], v[40:41] op_sel:[0,1] op_sel_hi:[1,0] neg_hi:[0,1]
	v_pk_add_f32 v[40:41], v[32:33], v[40:41] op_sel:[0,1] op_sel_hi:[1,0] neg_lo:[0,1]
	v_pk_add_f32 v[78:79], v[54:55], v[48:49]
	v_pk_add_f32 v[48:49], v[54:55], v[48:49] neg_lo:[0,1] neg_hi:[0,1]
	v_pk_add_f32 v[32:33], v[60:61], v[84:85]
	v_pk_add_f32 v[60:61], v[60:61], v[84:85] neg_lo:[0,1] neg_hi:[0,1]
	v_xor_b32_e32 v55, 0x80000000, v48
	v_mov_b32_e32 v54, v49
	v_pk_add_f32 v[84:85], v[32:33], v[78:79]
	v_pk_add_f32 v[48:49], v[32:33], v[78:79] neg_lo:[0,1] neg_hi:[0,1]
	v_pk_add_f32 v[78:79], v[60:61], v[54:55]
	v_pk_add_f32 v[32:33], v[60:61], v[54:55] neg_lo:[0,1] neg_hi:[0,1]
	v_pk_add_f32 v[54:55], v[94:95], v[86:87]
	v_pk_add_f32 v[60:61], v[94:95], v[86:87] neg_lo:[0,1] neg_hi:[0,1]
	v_pk_add_f32 v[86:87], v[56:57], v[44:45]
	v_pk_add_f32 v[44:45], v[44:45], v[56:57] neg_lo:[0,1] neg_hi:[0,1]
	v_pk_add_f32 v[88:89], v[88:89], v[90:91]
	v_pk_mul_f32 v[56:57], v[10:11], v[44:45] op_sel:[0,1] op_sel_hi:[0,0] neg_lo:[1,1] neg_hi:[1,0]
	v_pk_fma_f32 v[56:57], v[10:11], v[44:45], v[56:57] op_sel_hi:[0,1,1]
	v_pk_add_f32 v[44:45], v[82:83], v[58:59]
	v_pk_add_f32 v[58:59], v[82:83], v[58:59] neg_lo:[0,1] neg_hi:[0,1]
	s_nop 0
	v_xor_b32_e32 v83, 0x80000000, v58
	v_mov_b32_e32 v82, v59
	v_pk_add_f32 v[58:59], v[52:53], v[36:37]
	v_pk_add_f32 v[36:37], v[52:53], v[36:37] neg_lo:[0,1] neg_hi:[0,1]
	s_nop 0
	v_pk_mul_f32 v[52:53], v[10:11], v[36:37] op_sel:[0,1] op_sel_hi:[0,0] neg_lo:[1,1] neg_hi:[1,0]
	v_pk_fma_f32 v[36:37], v[10:11], v[36:37], v[52:53] op_sel_hi:[0,1,1] neg_lo:[1,0,0] neg_hi:[1,0,0]
	v_pk_add_f32 v[52:53], v[54:55], v[44:45]
	v_pk_add_f32 v[44:45], v[54:55], v[44:45] neg_lo:[0,1] neg_hi:[0,1]
	v_pk_add_f32 v[54:55], v[86:87], v[58:59]
	v_pk_add_f32 v[58:59], v[86:87], v[58:59] neg_lo:[0,1] neg_hi:[0,1]
	s_nop 0
	v_xor_b32_e32 v87, 0x80000000, v58
	v_mov_b32_e32 v86, v59
	v_pk_add_f32 v[58:59], v[52:53], v[54:55]
	v_pk_add_f32 v[54:55], v[52:53], v[54:55] neg_lo:[0,1] neg_hi:[0,1]
	v_pk_add_f32 v[52:53], v[60:61], v[82:83]
	v_pk_add_f32 v[60:61], v[60:61], v[82:83] neg_lo:[0,1] neg_hi:[0,1]
	v_pk_add_f32 v[82:83], v[56:57], v[36:37]
	v_pk_add_f32 v[36:37], v[56:57], v[36:37] neg_lo:[0,1] neg_hi:[0,1]
	v_pk_add_f32 v[94:95], v[44:45], v[86:87]
	v_pk_add_f32 v[44:45], v[44:45], v[86:87] neg_lo:[0,1] neg_hi:[0,1]
	v_pk_add_f32 v[86:87], v[52:53], v[82:83]
	v_pk_add_f32 v[52:53], v[52:53], v[82:83] neg_lo:[0,1] neg_hi:[0,1]
	v_pk_add_f32 v[82:83], v[60:61], v[36:37] op_sel:[0,1] op_sel_hi:[1,0] neg_hi:[0,1]
	v_pk_add_f32 v[36:37], v[60:61], v[36:37] op_sel:[0,1] op_sel_hi:[1,0] neg_lo:[0,1]
	v_pk_fma_f32 v[60:61], v[14:15], s[90:91], v[14:15] op_sel:[1,0,0] op_sel_hi:[0,1,1]
	v_pk_mul_f32 v[56:57], v[96:97], s[14:15] op_sel:[1,0] neg_lo:[1,0]
	v_pk_mul_f32 v[90:91], v[60:61], v[88:89] op_sel:[1,1] op_sel_hi:[0,1] neg_lo:[0,1]
	v_pk_fma_f32 v[56:57], v[96:97], s[94:95], v[56:57] op_sel_hi:[0,1,1]
	v_pk_fma_f32 v[88:89], v[60:61], v[88:89], v[90:91] op_sel_hi:[1,0,1]
	ds_write2_b64 v76, v[56:57], v[88:89] offset1:16
	v_pk_mul_f32 v[56:57], v[14:15], v[60:61] op_sel:[1,1] op_sel_hi:[0,1] neg_lo:[0,1]
	v_pk_fma_f32 v[56:57], v[14:15], v[60:61], v[56:57] op_sel_hi:[1,0,1]
	s_nop 0
	v_pk_mul_f32 v[60:61], v[56:57], v[104:105] op_sel:[1,1] op_sel_hi:[0,1] neg_lo:[0,1]
	v_pk_mul_f32 v[76:77], v[14:15], v[56:57] op_sel:[1,1] op_sel_hi:[0,1] neg_lo:[0,1]
	v_pk_fma_f32 v[60:61], v[56:57], v[104:105], v[60:61] op_sel_hi:[1,0,1]
	v_pk_fma_f32 v[56:57], v[14:15], v[56:57], v[76:77] op_sel_hi:[1,0,1]
	s_nop 0
	v_pk_mul_f32 v[76:77], v[56:57], v[58:59] op_sel:[1,1] op_sel_hi:[0,1] neg_lo:[0,1]
	v_pk_fma_f32 v[58:59], v[56:57], v[58:59], v[76:77] op_sel_hi:[1,0,1]
	ds_write2_b64 v75, v[60:61], v[58:59] offset0:32 offset1:48
	v_pk_mul_f32 v[58:59], v[14:15], v[56:57] op_sel:[1,1] op_sel_hi:[0,1] neg_lo:[0,1]
	v_pk_fma_f32 v[56:57], v[14:15], v[56:57], v[58:59] op_sel_hi:[1,0,1]
	s_nop 0
	v_pk_mul_f32 v[58:59], v[56:57], v[106:107] op_sel:[1,1] op_sel_hi:[0,1] neg_lo:[0,1]
	v_pk_mul_f32 v[60:61], v[14:15], v[56:57] op_sel:[1,1] op_sel_hi:[0,1] neg_lo:[0,1]
	v_pk_fma_f32 v[58:59], v[56:57], v[106:107], v[58:59] op_sel_hi:[1,0,1]
	v_pk_fma_f32 v[56:57], v[14:15], v[56:57], v[60:61] op_sel_hi:[1,0,1]
	s_nop 0
	v_pk_mul_f32 v[60:61], v[56:57], v[84:85] op_sel:[1,1] op_sel_hi:[0,1] neg_lo:[0,1]
	v_pk_fma_f32 v[60:61], v[56:57], v[84:85], v[60:61] op_sel_hi:[1,0,1]
	ds_write2_b64 v74, v[58:59], v[60:61] offset0:64 offset1:80
	v_pk_mul_f32 v[58:59], v[14:15], v[56:57] op_sel:[1,1] op_sel_hi:[0,1] neg_lo:[0,1]
	v_pk_fma_f32 v[56:57], v[14:15], v[56:57], v[58:59] op_sel_hi:[1,0,1]
	s_nop 0
	v_pk_mul_f32 v[58:59], v[56:57], v[100:101] op_sel:[1,1] op_sel_hi:[0,1] neg_lo:[0,1]
	v_pk_mul_f32 v[60:61], v[14:15], v[56:57] op_sel:[1,1] op_sel_hi:[0,1] neg_lo:[0,1]
	v_pk_fma_f32 v[58:59], v[56:57], v[100:101], v[58:59] op_sel_hi:[1,0,1]
	v_pk_fma_f32 v[56:57], v[14:15], v[56:57], v[60:61] op_sel_hi:[1,0,1]
	s_nop 0
	v_pk_mul_f32 v[60:61], v[56:57], v[86:87] op_sel:[1,1] op_sel_hi:[0,1] neg_lo:[0,1]
	v_pk_fma_f32 v[60:61], v[56:57], v[86:87], v[60:61] op_sel_hi:[1,0,1]
	ds_write2_b64 v73, v[58:59], v[60:61] offset0:96 offset1:112
	v_pk_mul_f32 v[58:59], v[14:15], v[56:57] op_sel:[1,1] op_sel_hi:[0,1] neg_lo:[0,1]
	v_pk_fma_f32 v[56:57], v[14:15], v[56:57], v[58:59] op_sel_hi:[1,0,1]
	s_nop 0
	v_pk_mul_f32 v[58:59], v[56:57], v[46:47] op_sel:[1,1] op_sel_hi:[0,1] neg_lo:[0,1]
	v_pk_fma_f32 v[46:47], v[56:57], v[46:47], v[58:59] op_sel_hi:[1,0,1]
	v_pk_mul_f32 v[58:59], v[14:15], v[56:57] op_sel:[1,1] op_sel_hi:[0,1] neg_lo:[0,1]
	v_pk_fma_f32 v[56:57], v[14:15], v[56:57], v[58:59] op_sel_hi:[1,0,1]
	s_nop 0
	v_pk_mul_f32 v[58:59], v[56:57], v[92:93] op_sel:[1,1] op_sel_hi:[0,1] neg_lo:[0,1]
	v_pk_fma_f32 v[58:59], v[56:57], v[92:93], v[58:59] op_sel_hi:[1,0,1]
	ds_write2_b64 v72, v[46:47], v[58:59] offset0:128 offset1:144
	v_pk_mul_f32 v[46:47], v[14:15], v[56:57] op_sel:[1,1] op_sel_hi:[0,1] neg_lo:[0,1]
	v_pk_fma_f32 v[46:47], v[14:15], v[56:57], v[46:47] op_sel_hi:[1,0,1]
	s_nop 0
	v_pk_mul_f32 v[56:57], v[46:47], v[50:51] op_sel:[1,1] op_sel_hi:[0,1] neg_lo:[0,1]
	v_pk_fma_f32 v[50:51], v[46:47], v[50:51], v[56:57] op_sel_hi:[1,0,1]
	v_pk_mul_f32 v[56:57], v[14:15], v[46:47] op_sel:[1,1] op_sel_hi:[0,1] neg_lo:[0,1]
	v_pk_fma_f32 v[46:47], v[14:15], v[46:47], v[56:57] op_sel_hi:[1,0,1]
	s_nop 0
	v_pk_mul_f32 v[56:57], v[46:47], v[94:95] op_sel:[1,1] op_sel_hi:[0,1] neg_lo:[0,1]
	v_pk_fma_f32 v[56:57], v[46:47], v[94:95], v[56:57] op_sel_hi:[1,0,1]
	ds_write2_b64 v71, v[50:51], v[56:57] offset0:160 offset1:176
	v_pk_mul_f32 v[50:51], v[14:15], v[46:47] op_sel:[1,1] op_sel_hi:[0,1] neg_lo:[0,1]
	v_pk_fma_f32 v[46:47], v[14:15], v[46:47], v[50:51] op_sel_hi:[1,0,1]
	s_nop 0
	v_pk_mul_f32 v[50:51], v[38:39], v[46:47] op_sel:[1,1] op_sel_hi:[1,0] neg_lo:[1,0]
	s_nop 0
	v_pk_fma_f32 v[38:39], v[38:39], v[46:47], v[50:51] op_sel_hi:[0,1,1]
	v_pk_mul_f32 v[50:51], v[14:15], v[46:47] op_sel:[1,1] op_sel_hi:[0,1] neg_lo:[0,1]
	v_pk_fma_f32 v[46:47], v[14:15], v[46:47], v[50:51] op_sel_hi:[1,0,1]
	s_nop 0
	v_pk_mul_f32 v[50:51], v[46:47], v[78:79] op_sel:[1,1] op_sel_hi:[0,1] neg_lo:[0,1]
	v_pk_fma_f32 v[50:51], v[46:47], v[78:79], v[50:51] op_sel_hi:[1,0,1]
	ds_write2_b64 v70, v[38:39], v[50:51] offset0:192 offset1:208
	v_pk_mul_f32 v[38:39], v[14:15], v[46:47] op_sel:[1,1] op_sel_hi:[0,1] neg_lo:[0,1]
	v_pk_fma_f32 v[38:39], v[14:15], v[46:47], v[38:39] op_sel_hi:[1,0,1]
	s_nop 0
	v_pk_mul_f32 v[46:47], v[42:43], v[38:39] op_sel:[1,1] op_sel_hi:[1,0] neg_lo:[1,0]
	s_nop 0
	v_pk_fma_f32 v[42:43], v[42:43], v[38:39], v[46:47] op_sel_hi:[0,1,1]
	v_pk_mul_f32 v[46:47], v[14:15], v[38:39] op_sel:[1,1] op_sel_hi:[0,1] neg_lo:[0,1]
	v_pk_fma_f32 v[38:39], v[14:15], v[38:39], v[46:47] op_sel_hi:[1,0,1]
	s_nop 0
	v_pk_mul_f32 v[46:47], v[38:39], v[82:83] op_sel:[1,1] op_sel_hi:[0,1] neg_lo:[0,1]
	v_pk_fma_f32 v[46:47], v[38:39], v[82:83], v[46:47] op_sel_hi:[1,0,1]
	ds_write2_b64 v69, v[42:43], v[46:47] offset0:224 offset1:240
	v_pk_mul_f32 v[42:43], v[14:15], v[38:39] op_sel:[1,1] op_sel_hi:[0,1] neg_lo:[0,1]
	v_pk_fma_f32 v[38:39], v[14:15], v[38:39], v[42:43] op_sel_hi:[1,0,1]
	s_nop 0
	v_pk_mul_f32 v[42:43], v[30:31], v[38:39] op_sel:[1,1] op_sel_hi:[1,0] neg_lo:[1,0]
	s_nop 0
	v_pk_fma_f32 v[30:31], v[30:31], v[38:39], v[42:43] op_sel_hi:[0,1,1]
	v_pk_mul_f32 v[42:43], v[14:15], v[38:39] op_sel:[1,1] op_sel_hi:[0,1] neg_lo:[0,1]
	v_pk_fma_f32 v[38:39], v[14:15], v[38:39], v[42:43] op_sel_hi:[1,0,1]
	s_nop 0
	v_pk_mul_f32 v[42:43], v[80:81], v[38:39] op_sel:[1,1] op_sel_hi:[1,0] neg_lo:[1,0]
	s_nop 0
	v_pk_fma_f32 v[42:43], v[80:81], v[38:39], v[42:43] op_sel_hi:[0,1,1]
	ds_write2_b64 v68, v[30:31], v[42:43] offset1:16
	v_pk_mul_f32 v[30:31], v[14:15], v[38:39] op_sel:[1,1] op_sel_hi:[0,1] neg_lo:[0,1]
	v_pk_fma_f32 v[30:31], v[14:15], v[38:39], v[30:31] op_sel_hi:[1,0,1]
	s_nop 0
	v_pk_mul_f32 v[38:39], v[34:35], v[30:31] op_sel:[1,1] op_sel_hi:[1,0] neg_lo:[1,0]
	s_nop 0
	v_pk_fma_f32 v[34:35], v[34:35], v[30:31], v[38:39] op_sel_hi:[0,1,1]
	v_pk_mul_f32 v[38:39], v[14:15], v[30:31] op_sel:[1,1] op_sel_hi:[0,1] neg_lo:[0,1]
	v_pk_fma_f32 v[30:31], v[14:15], v[30:31], v[38:39] op_sel_hi:[1,0,1]
	s_nop 0
	v_pk_mul_f32 v[38:39], v[54:55], v[30:31] op_sel:[1,1] op_sel_hi:[1,0] neg_lo:[1,0]
	s_nop 0
	v_pk_fma_f32 v[38:39], v[54:55], v[30:31], v[38:39] op_sel_hi:[0,1,1]
	ds_write2_b64 v67, v[34:35], v[38:39] offset0:32 offset1:48
	v_pk_mul_f32 v[34:35], v[14:15], v[30:31] op_sel:[1,1] op_sel_hi:[0,1] neg_lo:[0,1]
	v_pk_fma_f32 v[30:31], v[14:15], v[30:31], v[34:35] op_sel_hi:[1,0,1]
	s_nop 0
	v_pk_mul_f32 v[34:35], v[26:27], v[30:31] op_sel:[1,1] op_sel_hi:[1,0] neg_lo:[1,0]
	s_nop 0
	v_pk_fma_f32 v[26:27], v[26:27], v[30:31], v[34:35] op_sel_hi:[0,1,1]
	v_pk_mul_f32 v[34:35], v[14:15], v[30:31] op_sel:[1,1] op_sel_hi:[0,1] neg_lo:[0,1]
	v_pk_fma_f32 v[30:31], v[14:15], v[30:31], v[34:35] op_sel_hi:[1,0,1]
	s_nop 0
	v_pk_mul_f32 v[34:35], v[48:49], v[30:31] op_sel:[1,1] op_sel_hi:[1,0] neg_lo:[1,0]
	s_nop 0
	v_pk_fma_f32 v[34:35], v[48:49], v[30:31], v[34:35] op_sel_hi:[0,1,1]
	ds_write2_b64 v66, v[26:27], v[34:35] offset0:64 offset1:80
	v_pk_mul_f32 v[26:27], v[14:15], v[30:31] op_sel:[1,1] op_sel_hi:[0,1] neg_lo:[0,1]
	v_pk_fma_f32 v[26:27], v[14:15], v[30:31], v[26:27] op_sel_hi:[1,0,1]
	s_nop 0
	v_pk_mul_f32 v[30:31], v[28:29], v[26:27] op_sel:[1,1] op_sel_hi:[1,0] neg_lo:[1,0]
	s_nop 0
	v_pk_fma_f32 v[28:29], v[28:29], v[26:27], v[30:31] op_sel_hi:[0,1,1]
	v_pk_mul_f32 v[30:31], v[14:15], v[26:27] op_sel:[1,1] op_sel_hi:[0,1] neg_lo:[0,1]
	v_pk_fma_f32 v[26:27], v[14:15], v[26:27], v[30:31] op_sel_hi:[1,0,1]
	s_nop 0
	v_pk_mul_f32 v[30:31], v[52:53], v[26:27] op_sel:[1,1] op_sel_hi:[1,0] neg_lo:[1,0]
	s_nop 0
	v_pk_fma_f32 v[30:31], v[52:53], v[26:27], v[30:31] op_sel_hi:[0,1,1]
	ds_write2_b64 v65, v[28:29], v[30:31] offset0:96 offset1:112
	v_pk_mul_f32 v[28:29], v[14:15], v[26:27] op_sel:[1,1] op_sel_hi:[0,1] neg_lo:[0,1]
	v_pk_fma_f32 v[26:27], v[14:15], v[26:27], v[28:29] op_sel_hi:[1,0,1]
	s_nop 0
	v_pk_mul_f32 v[28:29], v[22:23], v[26:27] op_sel:[1,1] op_sel_hi:[1,0] neg_lo:[1,0]
	s_nop 0
	v_pk_fma_f32 v[22:23], v[22:23], v[26:27], v[28:29] op_sel_hi:[0,1,1]
	v_pk_mul_f32 v[28:29], v[14:15], v[26:27] op_sel:[1,1] op_sel_hi:[0,1] neg_lo:[0,1]
	v_pk_fma_f32 v[26:27], v[14:15], v[26:27], v[28:29] op_sel_hi:[1,0,1]
	s_nop 0
	v_pk_mul_f32 v[28:29], v[40:41], v[26:27] op_sel:[1,1] op_sel_hi:[1,0] neg_lo:[1,0]
	s_nop 0
	v_pk_fma_f32 v[28:29], v[40:41], v[26:27], v[28:29] op_sel_hi:[0,1,1]
	ds_write2_b64 v64, v[22:23], v[28:29] offset0:128 offset1:144
	v_pk_mul_f32 v[22:23], v[14:15], v[26:27] op_sel:[1,1] op_sel_hi:[0,1] neg_lo:[0,1]
	v_pk_fma_f32 v[22:23], v[14:15], v[26:27], v[22:23] op_sel_hi:[1,0,1]
	s_nop 0
	v_pk_mul_f32 v[26:27], v[24:25], v[22:23] op_sel:[1,1] op_sel_hi:[1,0] neg_lo:[1,0]
	s_nop 0
	v_pk_fma_f32 v[24:25], v[24:25], v[22:23], v[26:27] op_sel_hi:[0,1,1]
	v_pk_mul_f32 v[26:27], v[14:15], v[22:23] op_sel:[1,1] op_sel_hi:[0,1] neg_lo:[0,1]
	v_pk_fma_f32 v[22:23], v[14:15], v[22:23], v[26:27] op_sel_hi:[1,0,1]
	s_nop 0
	v_pk_mul_f32 v[26:27], v[44:45], v[22:23] op_sel:[1,1] op_sel_hi:[1,0] neg_lo:[1,0]
	s_nop 0
	v_pk_fma_f32 v[26:27], v[44:45], v[22:23], v[26:27] op_sel_hi:[0,1,1]
	ds_write2_b64 v63, v[24:25], v[26:27] offset0:160 offset1:176
	v_pk_mul_f32 v[24:25], v[14:15], v[22:23] op_sel:[1,1] op_sel_hi:[0,1] neg_lo:[0,1]
	v_pk_fma_f32 v[22:23], v[14:15], v[22:23], v[24:25] op_sel_hi:[1,0,1]
	s_nop 0
	v_pk_mul_f32 v[24:25], v[18:19], v[22:23] op_sel:[1,1] op_sel_hi:[1,0] neg_lo:[1,0]
	s_nop 0
	v_pk_fma_f32 v[18:19], v[18:19], v[22:23], v[24:25] op_sel_hi:[0,1,1]
	v_pk_mul_f32 v[24:25], v[14:15], v[22:23] op_sel:[1,1] op_sel_hi:[0,1] neg_lo:[0,1]
	v_pk_fma_f32 v[22:23], v[14:15], v[22:23], v[24:25] op_sel_hi:[1,0,1]
	s_nop 0
	v_pk_mul_f32 v[24:25], v[32:33], v[22:23] op_sel:[1,1] op_sel_hi:[1,0] neg_lo:[1,0]
	s_nop 0
	v_pk_fma_f32 v[24:25], v[32:33], v[22:23], v[24:25] op_sel_hi:[0,1,1]
	ds_write2_b64 v62, v[18:19], v[24:25] offset0:192 offset1:208
	v_pk_mul_f32 v[18:19], v[14:15], v[22:23] op_sel:[1,1] op_sel_hi:[0,1] neg_lo:[0,1]
	v_pk_fma_f32 v[18:19], v[14:15], v[22:23], v[18:19] op_sel_hi:[1,0,1]
	s_nop 0
	v_pk_mul_f32 v[22:23], v[20:21], v[18:19] op_sel:[1,1] op_sel_hi:[1,0] neg_lo:[1,0]
	s_nop 0
	v_pk_fma_f32 v[20:21], v[20:21], v[18:19], v[22:23] op_sel_hi:[0,1,1]
	v_pk_mul_f32 v[22:23], v[14:15], v[18:19] op_sel:[1,1] op_sel_hi:[0,1] neg_lo:[0,1]
	v_pk_fma_f32 v[14:15], v[14:15], v[18:19], v[22:23] op_sel_hi:[1,0,1]
	s_nop 0
	v_pk_mul_f32 v[18:19], v[36:37], v[14:15] op_sel:[1,1] op_sel_hi:[1,0] neg_lo:[1,0]
	s_nop 0
	v_pk_fma_f32 v[14:15], v[36:37], v[14:15], v[18:19] op_sel_hi:[0,1,1]
	ds_write2_b64 v13, v[20:21], v[14:15] offset0:224 offset1:240
	v_mov_b32_e32 v14, v182
	v_mov_b32_e32 v10, v176
	v_mov_b32_e32 v13, v175
	s_waitcnt lgkmcnt(0)
	s_barrier
	v_mov_b32_e32 v50, v167
	v_xor_b32_e32 v18, 1, v13
	v_lshlrev_b32_e32 v10, 3, v10
	v_lshlrev_b32_e32 v18, 3, v18
	v_add3_u32 v20, 0, v18, v10
	v_xor_b32_e32 v18, 2, v13
	v_lshlrev_b32_e32 v18, 3, v18
	v_xor_b32_e32 v26, 5, v13
	v_add3_u32 v22, 0, v18, v10
	v_xor_b32_e32 v18, 3, v13
	v_lshlrev_b32_e32 v26, 3, v26
	v_lshlrev_b32_e32 v15, 3, v13
	v_lshlrev_b32_e32 v18, 3, v18
	v_add3_u32 v28, 0, v26, v10
	v_xor_b32_e32 v26, 6, v13
	v_add3_u32 v15, 0, v15, v10
	v_add3_u32 v24, 0, v18, v10
	v_lshlrev_b32_e32 v26, 3, v26
	v_xor_b32_e32 v34, 9, v13
	ds_read_b64 v[18:19], v15
	ds_read_b64 v[20:21], v20
	ds_read_b64 v[22:23], v22
	ds_read_b64 v[24:25], v24
	v_xor_b32_e32 v15, 4, v13
	v_add3_u32 v30, 0, v26, v10
	v_xor_b32_e32 v26, 7, v13
	v_lshlrev_b32_e32 v34, 3, v34
	v_lshlrev_b32_e32 v15, 3, v15
	v_lshlrev_b32_e32 v26, 3, v26
	v_add3_u32 v36, 0, v34, v10
	v_xor_b32_e32 v34, 10, v13
	v_add3_u32 v15, 0, v15, v10
	v_add3_u32 v32, 0, v26, v10
	v_lshlrev_b32_e32 v34, 3, v34
	ds_read_b64 v[26:27], v15
	ds_read_b64 v[28:29], v28
	ds_read_b64 v[30:31], v30
	ds_read_b64 v[32:33], v32
	v_xor_b32_e32 v15, 8, v13
	v_add3_u32 v38, 0, v34, v10
	v_xor_b32_e32 v34, 11, v13
	v_lshlrev_b32_e32 v15, 3, v15
	v_lshlrev_b32_e32 v34, 3, v34
	v_xor_b32_e32 v42, 13, v13
	v_add3_u32 v15, 0, v15, v10
	v_add3_u32 v40, 0, v34, v10
	v_lshlrev_b32_e32 v42, 3, v42
	ds_read_b64 v[34:35], v15
	ds_read_b64 v[36:37], v36
	ds_read_b64 v[38:39], v38
	ds_read_b64 v[40:41], v40
	v_xor_b32_e32 v15, 12, v13
	v_add3_u32 v44, 0, v42, v10
	v_xor_b32_e32 v42, 14, v13
	v_xor_b32_e32 v13, 15, v13
	v_lshlrev_b32_e32 v15, 3, v15
	v_lshlrev_b32_e32 v42, 3, v42
	v_lshlrev_b32_e32 v13, 3, v13
	v_add3_u32 v15, 0, v15, v10
	v_add3_u32 v46, 0, v42, v10
	v_add3_u32 v10, 0, v13, v10
	ds_read_b64 v[42:43], v15
	ds_read_b64 v[44:45], v44
	ds_read_b64 v[46:47], v46
	ds_read_b64 v[48:49], v10
	v_mov_b32_e32 v10, v1
	v_mov_b32_e32 v13, v166
	v_mov_b32_e32 v10, v164
	s_waitcnt lgkmcnt(7)
	v_pk_add_f32 v[54:55], v[18:19], v[34:35]
	v_mov_b32_e32 v10, v165
	v_pk_add_f32 v[18:19], v[18:19], v[34:35] neg_lo:[0,1] neg_hi:[0,1]
	s_waitcnt lgkmcnt(6)
	v_pk_add_f32 v[34:35], v[20:21], v[36:37]
	v_pk_add_f32 v[20:21], v[20:21], v[36:37] neg_lo:[0,1] neg_hi:[0,1]
	v_mov_b32_e32 v13, v168
	v_mov_b32_e32 v52, v169
	v_ashrrev_i32_e32 v15, 31, v14
	v_pk_mul_f32 v[36:37], v[20:21], v[52:53] op_sel:[1,0] op_sel_hi:[0,0] neg_lo:[1,1] neg_hi:[0,1]
	v_mov_b32_e32 v13, v170
	v_pk_fma_f32 v[20:21], v[20:21], v[10:11], v[36:37] op_sel_hi:[1,0,1]
	s_waitcnt lgkmcnt(5)
	v_pk_add_f32 v[36:37], v[22:23], v[38:39]
	v_pk_add_f32 v[22:23], v[22:23], v[38:39] neg_lo:[0,1] neg_hi:[0,1]
	s_movk_i32 s0, 0x1000
	v_pk_mul_f32 v[38:39], v[22:23], v[50:51] op_sel:[1,0] op_sel_hi:[0,0] neg_lo:[1,1] neg_hi:[0,1]
	v_mov_b32_e32 v13, v171
	v_pk_fma_f32 v[22:23], v[22:23], v[50:51], v[38:39] op_sel_hi:[1,0,1]
	s_waitcnt lgkmcnt(4)
	v_pk_add_f32 v[38:39], v[24:25], v[40:41]
	v_pk_add_f32 v[24:25], v[24:25], v[40:41] neg_lo:[0,1] neg_hi:[0,1]
	v_mov_b32_e32 v72, v164
	v_pk_mul_f32 v[40:41], v[24:25], v[52:53] op_sel_hi:[1,0]
	s_nop 0
	v_pk_fma_f32 v[24:25], v[24:25], v[10:11], v[40:41] op_sel:[1,0,0] op_sel_hi:[0,0,1] neg_lo:[1,1,0] neg_hi:[0,1,0]
	s_waitcnt lgkmcnt(3)
	v_pk_add_f32 v[40:41], v[26:27], v[42:43]
	v_pk_add_f32 v[26:27], v[26:27], v[42:43] neg_lo:[0,1] neg_hi:[0,1]
	v_mov_b32_e32 v13, v175
	v_xor_b32_e32 v43, 0x80000000, v26
	v_mov_b32_e32 v42, v27
	s_waitcnt lgkmcnt(2)
	v_pk_add_f32 v[26:27], v[28:29], v[44:45]
	v_pk_add_f32 v[28:29], v[28:29], v[44:45] neg_lo:[0,1] neg_hi:[0,1]
	v_mov_b32_e32 v74, v166
	v_pk_mul_f32 v[44:45], v[28:29], v[52:53] op_sel_hi:[1,0] neg_lo:[0,1] neg_hi:[0,1]
	s_nop 0
	v_pk_fma_f32 v[28:29], v[28:29], v[10:11], v[44:45] op_sel:[1,0,0] op_sel_hi:[0,0,1] neg_lo:[1,1,0] neg_hi:[0,1,0]
	s_waitcnt lgkmcnt(1)
	v_pk_add_f32 v[44:45], v[30:31], v[46:47]
	v_pk_add_f32 v[30:31], v[30:31], v[46:47] neg_lo:[0,1] neg_hi:[0,1]
	v_mov_b32_e32 v76, v168
	v_pk_mul_f32 v[46:47], v[30:31], v[50:51] op_sel:[1,0] op_sel_hi:[0,0] neg_lo:[1,1] neg_hi:[0,1]
	v_mov_b32_e32 v78, v170
	v_pk_fma_f32 v[30:31], v[30:31], v[50:51], v[46:47] op_sel_hi:[1,0,1] neg_lo:[0,1,0] neg_hi:[0,1,0]
	s_waitcnt lgkmcnt(0)
	v_pk_add_f32 v[46:47], v[32:33], v[48:49]
	v_pk_add_f32 v[32:33], v[32:33], v[48:49] neg_lo:[0,1] neg_hi:[0,1]
	v_mov_b32_e32 v83, v11
	v_pk_mul_f32 v[48:49], v[32:33], v[52:53] op_sel:[1,0] op_sel_hi:[0,0] neg_lo:[1,1] neg_hi:[0,1]
	v_pk_add_f32 v[52:53], v[34:35], v[26:27]
	v_pk_add_f32 v[26:27], v[34:35], v[26:27] neg_lo:[0,1] neg_hi:[0,1]
	v_pk_fma_f32 v[32:33], v[32:33], v[10:11], v[48:49] op_sel_hi:[1,0,1] neg_lo:[0,1,0] neg_hi:[0,1,0]
	v_pk_mul_f32 v[34:35], v[26:27], v[50:51] op_sel:[1,0] op_sel_hi:[0,0] neg_lo:[1,1] neg_hi:[0,1]
	v_pk_add_f32 v[48:49], v[54:55], v[40:41]
	v_pk_fma_f32 v[26:27], v[26:27], v[50:51], v[34:35] op_sel_hi:[1,0,1]
	v_pk_add_f32 v[34:35], v[36:37], v[44:45]
	v_pk_add_f32 v[36:37], v[36:37], v[44:45] neg_lo:[0,1] neg_hi:[0,1]
	v_pk_add_f32 v[40:41], v[54:55], v[40:41] neg_lo:[0,1] neg_hi:[0,1]
	v_xor_b32_e32 v45, 0x80000000, v36
	v_mov_b32_e32 v44, v37
	v_pk_add_f32 v[36:37], v[38:39], v[46:47]
	v_pk_add_f32 v[38:39], v[38:39], v[46:47] neg_lo:[0,1] neg_hi:[0,1]
	v_mov_b32_e32 v10, v177
	v_pk_mul_f32 v[46:47], v[38:39], v[50:51] op_sel:[1,0] op_sel_hi:[0,0] neg_lo:[1,1] neg_hi:[0,1]
	s_mov_b32 s7, 0xa000
	v_pk_fma_f32 v[38:39], v[38:39], v[50:51], v[46:47] op_sel_hi:[1,0,1] neg_lo:[0,1,0] neg_hi:[0,1,0]
	v_pk_add_f32 v[46:47], v[48:49], v[34:35]
	v_pk_add_f32 v[34:35], v[48:49], v[34:35] neg_lo:[0,1] neg_hi:[0,1]
	v_pk_add_f32 v[48:49], v[52:53], v[36:37]
	v_pk_add_f32 v[36:37], v[52:53], v[36:37] neg_lo:[0,1] neg_hi:[0,1]
	s_mov_b32 s6, 0xc000
	v_xor_b32_e32 v53, 0x80000000, v36
	v_mov_b32_e32 v52, v37
	v_pk_add_f32 v[36:37], v[46:47], v[48:49]
	v_pk_add_f32 v[46:47], v[46:47], v[48:49] neg_lo:[0,1] neg_hi:[0,1]
	v_pk_add_f32 v[48:49], v[34:35], v[52:53]
	v_pk_add_f32 v[34:35], v[34:35], v[52:53] neg_lo:[0,1] neg_hi:[0,1]
	v_pk_add_f32 v[52:53], v[40:41], v[44:45]
	v_pk_add_f32 v[40:41], v[40:41], v[44:45] neg_lo:[0,1] neg_hi:[0,1]
	v_pk_add_f32 v[44:45], v[26:27], v[38:39]
	v_pk_add_f32 v[26:27], v[26:27], v[38:39] neg_lo:[0,1] neg_hi:[0,1]
	s_mov_b32 s1, 0xe000
	v_xor_b32_e32 v39, 0x80000000, v26
	v_mov_b32_e32 v38, v27
	v_pk_add_f32 v[26:27], v[52:53], v[44:45]
	v_pk_add_f32 v[44:45], v[52:53], v[44:45] neg_lo:[0,1] neg_hi:[0,1]
	v_pk_add_f32 v[52:53], v[40:41], v[38:39]
	v_pk_add_f32 v[38:39], v[40:41], v[38:39] neg_lo:[0,1] neg_hi:[0,1]
	v_pk_add_f32 v[40:41], v[18:19], v[42:43]
	v_pk_add_f32 v[18:19], v[18:19], v[42:43] neg_lo:[0,1] neg_hi:[0,1]
	v_pk_add_f32 v[42:43], v[20:21], v[28:29]
	v_pk_add_f32 v[20:21], v[20:21], v[28:29] neg_lo:[0,1] neg_hi:[0,1]
	s_mov_b32 s8, 0x8000
	v_pk_mul_f32 v[28:29], v[50:51], v[20:21] op_sel:[0,1] op_sel_hi:[0,0] neg_lo:[1,1] neg_hi:[1,0]
	v_pk_fma_f32 v[20:21], v[50:51], v[20:21], v[28:29] op_sel_hi:[0,1,1]
	v_pk_add_f32 v[28:29], v[22:23], v[30:31]
	v_pk_add_f32 v[22:23], v[22:23], v[30:31] neg_lo:[0,1] neg_hi:[0,1]
	s_mov_b32 s9, 0x9000
	v_xor_b32_e32 v31, 0x80000000, v22
	v_mov_b32_e32 v30, v23
	v_pk_add_f32 v[22:23], v[24:25], v[32:33]
	v_pk_add_f32 v[24:25], v[24:25], v[32:33] neg_lo:[0,1] neg_hi:[0,1]
	s_mov_b32 s5, 0xb000
	v_pk_mul_f32 v[32:33], v[50:51], v[24:25] op_sel:[0,1] op_sel_hi:[0,0] neg_lo:[1,1] neg_hi:[1,0]
	v_pk_fma_f32 v[24:25], v[50:51], v[24:25], v[32:33] op_sel_hi:[0,1,1] neg_lo:[1,0,0] neg_hi:[1,0,0]
	v_pk_add_f32 v[32:33], v[40:41], v[28:29]
	v_pk_add_f32 v[28:29], v[40:41], v[28:29] neg_lo:[0,1] neg_hi:[0,1]
	v_pk_add_f32 v[40:41], v[42:43], v[22:23]
	v_pk_add_f32 v[22:23], v[42:43], v[22:23] neg_lo:[0,1] neg_hi:[0,1]
	v_mov_b32_e32 v50, v167
	v_xor_b32_e32 v43, 0x80000000, v22
	v_mov_b32_e32 v42, v23
	v_pk_add_f32 v[22:23], v[32:33], v[40:41]
	v_pk_add_f32 v[32:33], v[32:33], v[40:41] neg_lo:[0,1] neg_hi:[0,1]
	v_pk_add_f32 v[40:41], v[28:29], v[42:43]
	v_pk_add_f32 v[28:29], v[28:29], v[42:43] neg_lo:[0,1] neg_hi:[0,1]
	v_pk_add_f32 v[42:43], v[18:19], v[30:31]
	v_pk_add_f32 v[18:19], v[18:19], v[30:31] neg_lo:[0,1] neg_hi:[0,1]
	v_pk_add_f32 v[30:31], v[20:21], v[24:25]
	v_pk_add_f32 v[20:21], v[20:21], v[24:25] neg_lo:[0,1] neg_hi:[0,1]
	s_mov_b32 s4, 0xd000
	v_xor_b32_e32 v25, 0x80000000, v20
	v_mov_b32_e32 v24, v21
	v_pk_add_f32 v[20:21], v[42:43], v[30:31]
	v_pk_add_f32 v[30:31], v[42:43], v[30:31] neg_lo:[0,1] neg_hi:[0,1]
	v_pk_add_f32 v[42:43], v[18:19], v[24:25]
	v_pk_add_f32 v[18:19], v[18:19], v[24:25] neg_lo:[0,1] neg_hi:[0,1]
	v_lshl_add_u64 v[24:25], v[14:15], 3, s[46:47]
	global_store_dwordx2 v[24:25], v[36:37], off
	v_add_u32_e32 v24, 0x200, v14
	v_ashrrev_i32_e32 v25, 31, v24
	v_lshl_add_u64 v[24:25], v[24:25], 3, s[46:47]
	global_store_dwordx2 v[24:25], v[22:23], off
	v_add_u32_e32 v22, 0x400, v14
	v_ashrrev_i32_e32 v23, 31, v22
	v_lshl_add_u64 v[22:23], v[22:23], 3, s[46:47]
	global_store_dwordx2 v[22:23], v[26:27], off
	v_add_u32_e32 v22, 0x600, v14
	v_ashrrev_i32_e32 v23, 31, v22
	v_lshl_add_u64 v[22:23], v[22:23], 3, s[46:47]
	global_store_dwordx2 v[22:23], v[20:21], off
	v_add_u32_e32 v20, 0x800, v14
	v_ashrrev_i32_e32 v21, 31, v20
	v_lshl_add_u64 v[20:21], v[20:21], 3, s[46:47]
	global_store_dwordx2 v[20:21], v[48:49], off
	v_add_u32_e32 v20, 0xa00, v14
	v_ashrrev_i32_e32 v21, 31, v20
	v_lshl_add_u64 v[20:21], v[20:21], 3, s[46:47]
	global_store_dwordx2 v[20:21], v[40:41], off
	v_add_u32_e32 v20, 0xc00, v14
	v_ashrrev_i32_e32 v21, 31, v20
	v_lshl_add_u64 v[20:21], v[20:21], 3, s[46:47]
	global_store_dwordx2 v[20:21], v[52:53], off
	v_add_u32_e32 v20, 0xe00, v14
	v_ashrrev_i32_e32 v21, 31, v20
	v_lshl_add_u64 v[20:21], v[20:21], 3, s[46:47]
	global_store_dwordx2 v[20:21], v[42:43], off
	v_add_u32_e32 v20, 0x1000, v14
	v_ashrrev_i32_e32 v21, 31, v20
	v_lshl_add_u64 v[20:21], v[20:21], 3, s[46:47]
	global_store_dwordx2 v[20:21], v[46:47], off
	v_add_u32_e32 v20, 0x1200, v14
	v_ashrrev_i32_e32 v21, 31, v20
	v_lshl_add_u64 v[20:21], v[20:21], 3, s[46:47]
	global_store_dwordx2 v[20:21], v[32:33], off
	v_add_u32_e32 v20, 0x1400, v14
	v_ashrrev_i32_e32 v21, 31, v20
	v_lshl_add_u64 v[20:21], v[20:21], 3, s[46:47]
	global_store_dwordx2 v[20:21], v[44:45], off
	v_add_u32_e32 v20, 0x1600, v14
	v_ashrrev_i32_e32 v21, 31, v20
	v_lshl_add_u64 v[20:21], v[20:21], 3, s[46:47]
	global_store_dwordx2 v[20:21], v[30:31], off
	v_add_u32_e32 v20, 0x1800, v14
	v_ashrrev_i32_e32 v21, 31, v20
	v_lshl_add_u64 v[20:21], v[20:21], 3, s[46:47]
	global_store_dwordx2 v[20:21], v[34:35], off
	v_add_u32_e32 v20, 0x1a00, v14
	v_ashrrev_i32_e32 v21, 31, v20
	v_lshl_add_u64 v[20:21], v[20:21], 3, s[46:47]
	global_store_dwordx2 v[20:21], v[28:29], off
	v_add_u32_e32 v20, 0x1c00, v14
	v_ashrrev_i32_e32 v21, 31, v20
	v_lshl_add_u64 v[20:21], v[20:21], 3, s[46:47]
	global_store_dwordx2 v[20:21], v[38:39], off
	v_add_u32_e32 v20, 0x1e00, v14
	v_ashrrev_i32_e32 v21, 31, v20
	v_lshl_add_u64 v[20:21], v[20:21], 3, s[46:47]
	global_store_dwordx2 v[20:21], v[18:19], off
	v_mov_b32_e32 v52, v169
	v_xor_b32_e32 v18, 1, v13
	v_lshlrev_b32_e32 v10, 3, v10
	v_lshlrev_b32_e32 v18, 3, v18
	v_add3_u32 v20, 0, v18, v10
	v_xor_b32_e32 v18, 2, v13
	v_lshlrev_b32_e32 v18, 3, v18
	v_xor_b32_e32 v26, 5, v13
	v_add3_u32 v22, 0, v18, v10
	v_xor_b32_e32 v18, 3, v13
	v_lshlrev_b32_e32 v26, 3, v26
	v_lshlrev_b32_e32 v15, 3, v13
	v_lshlrev_b32_e32 v18, 3, v18
	v_add3_u32 v28, 0, v26, v10
	v_xor_b32_e32 v26, 6, v13
	v_add3_u32 v15, 0, v15, v10
	v_add3_u32 v24, 0, v18, v10
	v_lshlrev_b32_e32 v26, 3, v26
	v_xor_b32_e32 v34, 9, v13
	ds_read_b64 v[18:19], v15
	ds_read_b64 v[20:21], v20
	ds_read_b64 v[22:23], v22
	ds_read_b64 v[24:25], v24
	v_xor_b32_e32 v15, 4, v13
	v_add3_u32 v30, 0, v26, v10
	v_xor_b32_e32 v26, 7, v13
	v_lshlrev_b32_e32 v34, 3, v34
	v_lshlrev_b32_e32 v15, 3, v15
	v_lshlrev_b32_e32 v26, 3, v26
	v_add3_u32 v36, 0, v34, v10
	v_xor_b32_e32 v34, 10, v13
	v_add3_u32 v15, 0, v15, v10
	v_add3_u32 v32, 0, v26, v10
	v_lshlrev_b32_e32 v34, 3, v34
	ds_read_b64 v[26:27], v15
	ds_read_b64 v[28:29], v28
	ds_read_b64 v[30:31], v30
	ds_read_b64 v[32:33], v32
	v_xor_b32_e32 v15, 8, v13
	v_add3_u32 v38, 0, v34, v10
	v_xor_b32_e32 v34, 11, v13
	v_lshlrev_b32_e32 v15, 3, v15
	v_lshlrev_b32_e32 v34, 3, v34
	v_xor_b32_e32 v42, 13, v13
	v_add3_u32 v15, 0, v15, v10
	v_add3_u32 v40, 0, v34, v10
	v_lshlrev_b32_e32 v42, 3, v42
	ds_read_b64 v[34:35], v15
	ds_read_b64 v[36:37], v36
	ds_read_b64 v[38:39], v38
	ds_read_b64 v[40:41], v40
	v_xor_b32_e32 v15, 12, v13
	v_add3_u32 v44, 0, v42, v10
	v_xor_b32_e32 v42, 14, v13
	v_xor_b32_e32 v13, 15, v13
	v_lshlrev_b32_e32 v15, 3, v15
	v_lshlrev_b32_e32 v42, 3, v42
	v_lshlrev_b32_e32 v13, 3, v13
	v_add3_u32 v15, 0, v15, v10
	v_add3_u32 v46, 0, v42, v10
	v_add3_u32 v10, 0, v13, v10
	ds_read_b64 v[42:43], v15
	ds_read_b64 v[44:45], v44
	ds_read_b64 v[46:47], v46
	ds_read_b64 v[48:49], v10
	v_mov_b32_e32 v10, v1
	v_mov_b32_e32 v13, v166
	v_mov_b32_e32 v10, v164
	s_waitcnt lgkmcnt(7)
	v_pk_add_f32 v[54:55], v[18:19], v[34:35]
	v_mov_b32_e32 v10, v165
	v_pk_add_f32 v[18:19], v[18:19], v[34:35] neg_lo:[0,1] neg_hi:[0,1]
	s_waitcnt lgkmcnt(6)
	v_pk_add_f32 v[34:35], v[20:21], v[36:37]
	v_pk_add_f32 v[20:21], v[20:21], v[36:37] neg_lo:[0,1] neg_hi:[0,1]
	v_mov_b32_e32 v13, v168
	s_nop 0
	v_pk_mul_f32 v[36:37], v[20:21], v[52:53] op_sel:[1,0] op_sel_hi:[0,0] neg_lo:[1,1] neg_hi:[0,1]
	v_mov_b32_e32 v13, v170
	v_pk_fma_f32 v[20:21], v[20:21], v[10:11], v[36:37] op_sel_hi:[1,0,1]
	s_waitcnt lgkmcnt(5)
	v_pk_add_f32 v[36:37], v[22:23], v[38:39]
	v_pk_add_f32 v[22:23], v[22:23], v[38:39] neg_lo:[0,1] neg_hi:[0,1]
	s_nop 0
	v_pk_mul_f32 v[38:39], v[22:23], v[50:51] op_sel:[1,0] op_sel_hi:[0,0] neg_lo:[1,1] neg_hi:[0,1]
	v_mov_b32_e32 v13, v171
	v_pk_fma_f32 v[22:23], v[22:23], v[50:51], v[38:39] op_sel_hi:[1,0,1]
	s_waitcnt lgkmcnt(4)
	v_pk_add_f32 v[38:39], v[24:25], v[40:41]
	v_pk_add_f32 v[24:25], v[24:25], v[40:41] neg_lo:[0,1] neg_hi:[0,1]
	s_nop 0
	v_pk_mul_f32 v[40:41], v[24:25], v[52:53] op_sel_hi:[1,0]
	s_nop 0
	v_pk_fma_f32 v[24:25], v[24:25], v[10:11], v[40:41] op_sel:[1,0,0] op_sel_hi:[0,0,1] neg_lo:[1,1,0] neg_hi:[0,1,0]
	s_waitcnt lgkmcnt(3)
	v_pk_add_f32 v[40:41], v[26:27], v[42:43]
	v_pk_add_f32 v[26:27], v[26:27], v[42:43] neg_lo:[0,1] neg_hi:[0,1]
	s_nop 0
	v_xor_b32_e32 v43, 0x80000000, v26
	v_mov_b32_e32 v42, v27
	s_waitcnt lgkmcnt(2)
	v_pk_add_f32 v[26:27], v[28:29], v[44:45]
	v_pk_add_f32 v[28:29], v[28:29], v[44:45] neg_lo:[0,1] neg_hi:[0,1]
	s_nop 0
	v_pk_mul_f32 v[44:45], v[28:29], v[52:53] op_sel_hi:[1,0] neg_lo:[0,1] neg_hi:[0,1]
	s_nop 0
	v_pk_fma_f32 v[28:29], v[28:29], v[10:11], v[44:45] op_sel:[1,0,0] op_sel_hi:[0,0,1] neg_lo:[1,1,0] neg_hi:[0,1,0]
	s_waitcnt lgkmcnt(1)
	v_pk_add_f32 v[44:45], v[30:31], v[46:47]
	v_pk_add_f32 v[30:31], v[30:31], v[46:47] neg_lo:[0,1] neg_hi:[0,1]
	s_nop 0
	v_pk_mul_f32 v[46:47], v[30:31], v[50:51] op_sel:[1,0] op_sel_hi:[0,0] neg_lo:[1,1] neg_hi:[0,1]
	s_nop 0
	v_pk_fma_f32 v[30:31], v[30:31], v[50:51], v[46:47] op_sel_hi:[1,0,1] neg_lo:[0,1,0] neg_hi:[0,1,0]
	s_waitcnt lgkmcnt(0)
	v_pk_add_f32 v[46:47], v[32:33], v[48:49]
	v_pk_add_f32 v[32:33], v[32:33], v[48:49] neg_lo:[0,1] neg_hi:[0,1]
	s_nop 0
	v_pk_mul_f32 v[48:49], v[32:33], v[52:53] op_sel:[1,0] op_sel_hi:[0,0] neg_lo:[1,1] neg_hi:[0,1]
	v_pk_add_f32 v[52:53], v[34:35], v[26:27]
	v_pk_add_f32 v[26:27], v[34:35], v[26:27] neg_lo:[0,1] neg_hi:[0,1]
	v_pk_fma_f32 v[32:33], v[32:33], v[10:11], v[48:49] op_sel_hi:[1,0,1] neg_lo:[0,1,0] neg_hi:[0,1,0]
	v_pk_mul_f32 v[34:35], v[26:27], v[50:51] op_sel:[1,0] op_sel_hi:[0,0] neg_lo:[1,1] neg_hi:[0,1]
	v_pk_add_f32 v[48:49], v[54:55], v[40:41]
	v_pk_fma_f32 v[26:27], v[26:27], v[50:51], v[34:35] op_sel_hi:[1,0,1]
	v_pk_add_f32 v[34:35], v[36:37], v[44:45]
	v_pk_add_f32 v[36:37], v[36:37], v[44:45] neg_lo:[0,1] neg_hi:[0,1]
	v_pk_add_f32 v[40:41], v[54:55], v[40:41] neg_lo:[0,1] neg_hi:[0,1]
	v_xor_b32_e32 v45, 0x80000000, v36
	v_mov_b32_e32 v44, v37
	v_pk_add_f32 v[36:37], v[38:39], v[46:47]
	v_pk_add_f32 v[38:39], v[38:39], v[46:47] neg_lo:[0,1] neg_hi:[0,1]
	v_mov_b32_e32 v10, v1
	v_pk_mul_f32 v[46:47], v[38:39], v[50:51] op_sel:[1,0] op_sel_hi:[0,0] neg_lo:[1,1] neg_hi:[0,1]
	s_nop 0
	v_pk_fma_f32 v[38:39], v[38:39], v[50:51], v[46:47] op_sel_hi:[1,0,1] neg_lo:[0,1,0] neg_hi:[0,1,0]
	v_pk_add_f32 v[46:47], v[48:49], v[34:35]
	v_pk_add_f32 v[34:35], v[48:49], v[34:35] neg_lo:[0,1] neg_hi:[0,1]
	v_pk_add_f32 v[48:49], v[52:53], v[36:37]
	v_pk_add_f32 v[36:37], v[52:53], v[36:37] neg_lo:[0,1] neg_hi:[0,1]
	s_nop 0
	v_xor_b32_e32 v53, 0x80000000, v36
	v_mov_b32_e32 v52, v37
	v_pk_add_f32 v[36:37], v[46:47], v[48:49]
	v_pk_add_f32 v[46:47], v[46:47], v[48:49] neg_lo:[0,1] neg_hi:[0,1]
	v_pk_add_f32 v[48:49], v[34:35], v[52:53]
	v_pk_add_f32 v[34:35], v[34:35], v[52:53] neg_lo:[0,1] neg_hi:[0,1]
	v_pk_add_f32 v[52:53], v[40:41], v[44:45]
	v_pk_add_f32 v[40:41], v[40:41], v[44:45] neg_lo:[0,1] neg_hi:[0,1]
	v_pk_add_f32 v[44:45], v[26:27], v[38:39]
	v_pk_add_f32 v[26:27], v[26:27], v[38:39] neg_lo:[0,1] neg_hi:[0,1]
	s_nop 0
	v_xor_b32_e32 v39, 0x80000000, v26
	v_mov_b32_e32 v38, v27
	v_pk_add_f32 v[26:27], v[52:53], v[44:45]
	v_pk_add_f32 v[44:45], v[52:53], v[44:45] neg_lo:[0,1] neg_hi:[0,1]
	v_pk_add_f32 v[52:53], v[40:41], v[38:39]
	v_pk_add_f32 v[38:39], v[40:41], v[38:39] neg_lo:[0,1] neg_hi:[0,1]
	v_pk_add_f32 v[40:41], v[18:19], v[42:43]
	v_pk_add_f32 v[18:19], v[18:19], v[42:43] neg_lo:[0,1] neg_hi:[0,1]
	v_pk_add_f32 v[42:43], v[20:21], v[28:29]
	v_pk_add_f32 v[20:21], v[20:21], v[28:29] neg_lo:[0,1] neg_hi:[0,1]
	s_nop 0
	v_pk_mul_f32 v[28:29], v[50:51], v[20:21] op_sel:[0,1] op_sel_hi:[0,0] neg_lo:[1,1] neg_hi:[1,0]
	v_pk_fma_f32 v[20:21], v[50:51], v[20:21], v[28:29] op_sel_hi:[0,1,1]
	v_pk_add_f32 v[28:29], v[22:23], v[30:31]
	v_pk_add_f32 v[22:23], v[22:23], v[30:31] neg_lo:[0,1] neg_hi:[0,1]
	s_nop 0
	v_xor_b32_e32 v31, 0x80000000, v22
	v_mov_b32_e32 v30, v23
	v_pk_add_f32 v[22:23], v[24:25], v[32:33]
	v_pk_add_f32 v[24:25], v[24:25], v[32:33] neg_lo:[0,1] neg_hi:[0,1]
	s_nop 0
	v_pk_mul_f32 v[32:33], v[50:51], v[24:25] op_sel:[0,1] op_sel_hi:[0,0] neg_lo:[1,1] neg_hi:[1,0]
	v_pk_fma_f32 v[24:25], v[50:51], v[24:25], v[32:33] op_sel_hi:[0,1,1] neg_lo:[1,0,0] neg_hi:[1,0,0]
	v_pk_add_f32 v[32:33], v[40:41], v[28:29]
	v_pk_add_f32 v[28:29], v[40:41], v[28:29] neg_lo:[0,1] neg_hi:[0,1]
	v_pk_add_f32 v[40:41], v[42:43], v[22:23]
	v_pk_add_f32 v[22:23], v[42:43], v[22:23] neg_lo:[0,1] neg_hi:[0,1]
	s_nop 0
	v_xor_b32_e32 v43, 0x80000000, v22
	v_mov_b32_e32 v42, v23
	v_pk_add_f32 v[22:23], v[32:33], v[40:41]
	v_pk_add_f32 v[32:33], v[32:33], v[40:41] neg_lo:[0,1] neg_hi:[0,1]
	v_pk_add_f32 v[40:41], v[28:29], v[42:43]
	v_pk_add_f32 v[28:29], v[28:29], v[42:43] neg_lo:[0,1] neg_hi:[0,1]
	v_pk_add_f32 v[42:43], v[18:19], v[30:31]
	v_pk_add_f32 v[18:19], v[18:19], v[30:31] neg_lo:[0,1] neg_hi:[0,1]
	v_pk_add_f32 v[30:31], v[20:21], v[24:25]
	v_pk_add_f32 v[20:21], v[20:21], v[24:25] neg_lo:[0,1] neg_hi:[0,1]
	s_nop 0
	v_xor_b32_e32 v25, 0x80000000, v20
	v_mov_b32_e32 v24, v21
	v_pk_add_f32 v[20:21], v[42:43], v[30:31]
	v_pk_add_f32 v[30:31], v[42:43], v[30:31] neg_lo:[0,1] neg_hi:[0,1]
	v_pk_add_f32 v[42:43], v[18:19], v[24:25]
	v_pk_add_f32 v[18:19], v[18:19], v[24:25] neg_lo:[0,1] neg_hi:[0,1]
	v_add_u32_e32 v24, 0x2000, v14
	v_ashrrev_i32_e32 v25, 31, v24
	v_lshl_add_u64 v[24:25], v[24:25], 3, s[46:47]
	global_store_dwordx2 v[24:25], v[36:37], off
	v_add_u32_e32 v24, 0x2200, v14
	v_ashrrev_i32_e32 v25, 31, v24
	v_lshl_add_u64 v[24:25], v[24:25], 3, s[46:47]
	global_store_dwordx2 v[24:25], v[22:23], off
	v_add_u32_e32 v22, 0x2400, v14
	v_ashrrev_i32_e32 v23, 31, v22
	v_lshl_add_u64 v[22:23], v[22:23], 3, s[46:47]
	global_store_dwordx2 v[22:23], v[26:27], off
	v_add_u32_e32 v22, 0x2600, v14
	v_ashrrev_i32_e32 v23, 31, v22
	v_lshl_add_u64 v[22:23], v[22:23], 3, s[46:47]
	global_store_dwordx2 v[22:23], v[20:21], off
	v_add_u32_e32 v20, 0x2800, v14
	v_ashrrev_i32_e32 v21, 31, v20
	v_lshl_add_u64 v[20:21], v[20:21], 3, s[46:47]
	global_store_dwordx2 v[20:21], v[48:49], off
	v_add_u32_e32 v20, 0x2a00, v14
	v_ashrrev_i32_e32 v21, 31, v20
	v_lshl_add_u64 v[20:21], v[20:21], 3, s[46:47]
	global_store_dwordx2 v[20:21], v[40:41], off
	v_add_u32_e32 v20, 0x2c00, v14
	v_ashrrev_i32_e32 v21, 31, v20
	v_lshl_add_u64 v[20:21], v[20:21], 3, s[46:47]
	global_store_dwordx2 v[20:21], v[52:53], off
	v_add_u32_e32 v20, 0x2e00, v14
	v_ashrrev_i32_e32 v21, 31, v20
	v_lshl_add_u64 v[20:21], v[20:21], 3, s[46:47]
	global_store_dwordx2 v[20:21], v[42:43], off
	v_add_u32_e32 v20, 0x3000, v14
	v_ashrrev_i32_e32 v21, 31, v20
	v_lshl_add_u64 v[20:21], v[20:21], 3, s[46:47]
	global_store_dwordx2 v[20:21], v[46:47], off
	v_add_u32_e32 v20, 0x3200, v14
	v_ashrrev_i32_e32 v21, 31, v20
	v_lshl_add_u64 v[20:21], v[20:21], 3, s[46:47]
	global_store_dwordx2 v[20:21], v[32:33], off
	v_add_u32_e32 v20, 0x3400, v14
	v_ashrrev_i32_e32 v21, 31, v20
	v_lshl_add_u64 v[20:21], v[20:21], 3, s[46:47]
	global_store_dwordx2 v[20:21], v[44:45], off
	v_add_u32_e32 v20, 0x3600, v14
	v_ashrrev_i32_e32 v21, 31, v20
	v_lshl_add_u64 v[20:21], v[20:21], 3, s[46:47]
	global_store_dwordx2 v[20:21], v[30:31], off
	v_add_u32_e32 v20, 0x3800, v14
	v_ashrrev_i32_e32 v21, 31, v20
	v_lshl_add_u64 v[20:21], v[20:21], 3, s[46:47]
	global_store_dwordx2 v[20:21], v[34:35], off
	v_add_u32_e32 v20, 0x3a00, v14
	v_ashrrev_i32_e32 v21, 31, v20
	v_lshl_add_u64 v[20:21], v[20:21], 3, s[46:47]
	global_store_dwordx2 v[20:21], v[28:29], off
	v_add_u32_e32 v20, 0x3c00, v14
	v_add_u32_e32 v14, 0x3e00, v14
	v_ashrrev_i32_e32 v15, 31, v14
	v_ashrrev_i32_e32 v21, 31, v20
	v_lshl_add_u64 v[14:15], v[14:15], 3, s[46:47]
	v_lshl_add_u64 v[20:21], v[20:21], 3, s[46:47]
	global_store_dwordx2 v[14:15], v[18:19], off
	v_mov_b32_e32 v14, v182
	global_store_dwordx2 v[20:21], v[38:39], off
	s_barrier
	v_mov_b32_e32 v40, v169
	v_ashrrev_i32_e32 v15, 31, v14
	v_lshl_add_u64 v[18:19], v[14:15], 2, s[64:65]
	v_add_co_u32_e32 v28, vcc, s0, v18
	s_movk_i32 s0, 0x2000
	s_nop 0
	v_addc_co_u32_e32 v29, vcc, 0, v19, vcc
	v_add_co_u32_e32 v22, vcc, s0, v18
	s_movk_i32 s0, 0x6000
	s_nop 0
	v_addc_co_u32_e32 v23, vcc, 0, v19, vcc
	v_add_co_u32_e32 v30, vcc, s78, v18
	global_load_dword v20, v[18:19], off
	global_load_dword v21, v[18:19], off offset:2048
	v_addc_co_u32_e32 v31, vcc, 0, v19, vcc
	v_add_co_u32_e32 v32, vcc, s43, v18
	v_mov_b32_e32 v15, v173
	s_nop 0
	v_addc_co_u32_e32 v33, vcc, 0, v19, vcc
	v_add_co_u32_e32 v34, vcc, s0, v18
	s_mov_b32 s0, 0x8000
	s_nop 0
	v_addc_co_u32_e32 v35, vcc, 0, v19, vcc
	v_add_co_u32_e32 v36, vcc, s0, v18
	s_mov_b32 s0, 0xa000
	s_nop 0
	v_addc_co_u32_e32 v37, vcc, 0, v19, vcc
	v_add_co_u32_e32 v38, vcc, s0, v18
	global_load_dword v26, v[22:23], off offset:-4096
	global_load_dword v24, v[22:23], off
	global_load_dword v25, v[22:23], off offset:2048
	s_nop 0
	global_load_dword v22, v[32:33], off offset:-4096
	v_addc_co_u32_e32 v39, vcc, 0, v19, vcc
	global_load_dword v43, v[32:33], off offset:2048
	global_load_dword v46, v[34:35], off offset:-4096
	global_load_dword v48, v[36:37], off
	global_load_dword v49, v[36:37], off offset:2048
	global_load_dword v62, v[34:35], off
	global_load_dword v63, v[34:35], off offset:2048
	s_nop 0
	global_load_dword v34, v[38:39], off offset:-4096
	global_load_dword v64, v[36:37], off offset:-4096
	s_mov_b32 s0, 0x9000
	v_add_co_u32_e32 v36, vcc, s0, v18
	s_movk_i32 s0, 0x5000
	s_nop 0
	v_addc_co_u32_e32 v37, vcc, 0, v19, vcc
	global_load_dword v27, v[28:29], off offset:2048
	global_load_dword v35, v[36:37], off offset:2048
	v_add_co_u32_e32 v28, vcc, s0, v18
	s_mov_b32 s0, 0xb000
	s_nop 0
	v_addc_co_u32_e32 v29, vcc, 0, v19, vcc
	global_load_dword v66, v[38:39], off
	global_load_dword v67, v[38:39], off offset:2048
	v_add_co_u32_e32 v36, vcc, s0, v18
	s_mov_b32 s0, 0xc000
	s_nop 0
	v_addc_co_u32_e32 v37, vcc, 0, v19, vcc
	v_add_co_u32_e32 v38, vcc, s0, v18
	s_movk_i32 s0, 0x7000
	s_nop 0
	v_addc_co_u32_e32 v39, vcc, 0, v19, vcc
	global_load_dword v68, v[38:39], off offset:-4096
	global_load_dword v23, v[30:31], off offset:2048
	global_load_dword v69, v[36:37], off offset:2048
	v_add_co_u32_e32 v30, vcc, s0, v18
	s_mov_b32 s0, 0xe000
	s_nop 0
	v_addc_co_u32_e32 v31, vcc, 0, v19, vcc
	global_load_dword v47, v[28:29], off offset:2048
	global_load_dword v65, v[30:31], off offset:2048
	global_load_dword v42, v[32:33], off
	s_nop 0
	global_load_dword v30, v[38:39], off
	global_load_dword v31, v[38:39], off offset:2048
	v_add_co_u32_e32 v28, vcc, s0, v18
	s_mov_b32 s0, 0xd000
	s_nop 0
	v_addc_co_u32_e32 v29, vcc, 0, v19, vcc
	global_load_dword v32, v[28:29], off offset:-4096
	v_add_co_u32_e32 v36, vcc, s0, v18
	s_mov_b32 s0, 0xf000
	s_nop 0
	v_addc_co_u32_e32 v37, vcc, 0, v19, vcc
	global_load_dword v33, v[36:37], off offset:2048
	global_load_dword v38, v[28:29], off
	global_load_dword v39, v[28:29], off offset:2048
	v_add_co_u32_e32 v18, vcc, s0, v18
	v_mov_b32_e32 v36, v165
	s_nop 0
	v_addc_co_u32_e32 v19, vcc, 0, v19, vcc
	global_load_dword v70, v[18:19], off
	global_load_dword v71, v[18:19], off offset:2048
	v_mov_b32_e32 v28, v167
	v_mov_b32_e32 v45, v11
	v_mov_b32_e32 v10, v171
	s_waitcnt vmcnt(22)
	v_sub_f32_e32 v44, v21, v49
	v_mov_b32_e32 v13, v44
	v_pk_mul_f32 v[50:51], v[12:13], v[78:79] op_sel_hi:[1,0] neg_lo:[0,1] neg_hi:[0,1]
	v_sub_f32_e32 v10, v20, v48
	v_pk_fma_f32 v[44:45], v[44:45], v[72:73], v[50:51] op_sel_hi:[1,0,1]
	s_waitcnt vmcnt(19)
	v_sub_f32_e32 v50, v26, v34
	v_mov_b32_e32 v13, v50
	v_mov_b32_e32 v51, v11
	v_pk_mul_f32 v[52:53], v[12:13], v[40:41] op_sel_hi:[1,0] neg_lo:[0,1] neg_hi:[0,1]
	v_pk_add_f32 v[20:21], v[20:21], v[48:49]
	v_pk_fma_f32 v[50:51], v[50:51], v[36:37], v[52:53] op_sel_hi:[1,0,1]
	s_waitcnt vmcnt(16)
	v_sub_f32_e32 v52, v27, v35
	v_mov_b32_e32 v13, v52
	v_mov_b32_e32 v53, v11
	v_pk_mul_f32 v[54:55], v[12:13], v[76:77] op_sel_hi:[1,0] neg_lo:[0,1] neg_hi:[0,1]
	v_pk_add_f32 v[26:27], v[26:27], v[34:35]
	v_pk_fma_f32 v[54:55], v[52:53], v[74:75], v[54:55] op_sel_hi:[1,0,1]
	s_waitcnt vmcnt(15)
	v_sub_f32_e32 v52, v24, v66
	v_mov_b32_e32 v13, v52
	v_pk_mul_f32 v[56:57], v[12:13], v[28:29] op_sel_hi:[1,0] neg_lo:[0,1] neg_hi:[0,1]
	s_waitcnt vmcnt(6)
	v_sub_f32_e32 v82, v43, v31
	v_pk_fma_f32 v[56:57], v[52:53], v[28:29], v[56:57] op_sel_hi:[1,0,1]
	v_sub_f32_e32 v52, v25, v67
	v_pk_mul_f32 v[58:59], v[52:53], v[76:77] op_sel_hi:[1,0]
	v_mov_b32_e32 v13, v52
	v_sub_f32_e32 v52, v22, v68
	v_pk_fma_f32 v[60:61], v[12:13], v[74:75], v[58:59] op_sel_hi:[1,0,1] neg_lo:[0,1,0] neg_hi:[0,1,0]
	v_pk_mul_f32 v[58:59], v[52:53], v[40:41] op_sel_hi:[1,0]
	v_mov_b32_e32 v13, v52
	v_sub_f32_e32 v52, v23, v69
	v_pk_fma_f32 v[58:59], v[12:13], v[36:37], v[58:59] op_sel_hi:[1,0,1] neg_lo:[0,1,0] neg_hi:[0,1,0]
	v_pk_mul_f32 v[80:81], v[52:53], v[78:79] op_sel_hi:[1,0]
	v_mov_b32_e32 v13, v52
	v_pk_fma_f32 v[52:53], v[12:13], v[72:73], v[80:81] op_sel_hi:[1,0,1] neg_lo:[0,1,0] neg_hi:[0,1,0]
	v_sub_f32_e32 v13, v42, v30
	v_xor_b32_e32 v81, 0x80000000, v13
	v_pk_mul_f32 v[84:85], v[82:83], v[78:79] op_sel_hi:[1,0] neg_lo:[0,1] neg_hi:[0,1]
	v_mov_b32_e32 v13, v82
	v_pk_fma_f32 v[82:83], v[12:13], v[72:73], v[84:85] op_sel_hi:[1,0,1] neg_lo:[0,1,0] neg_hi:[0,1,0]
	s_waitcnt vmcnt(5)
	v_sub_f32_e32 v84, v46, v32
	v_mov_b32_e32 v85, v11
	v_pk_mul_f32 v[86:87], v[84:85], v[40:41] op_sel_hi:[1,0] neg_lo:[0,1] neg_hi:[0,1]
	v_mov_b32_e32 v13, v84
	v_pk_fma_f32 v[84:85], v[12:13], v[36:37], v[86:87] op_sel_hi:[1,0,1] neg_lo:[0,1,0] neg_hi:[0,1,0]
	s_waitcnt vmcnt(4)
	v_sub_f32_e32 v86, v47, v33
	v_mov_b32_e32 v87, v11
	v_pk_mul_f32 v[88:89], v[86:87], v[76:77] op_sel_hi:[1,0] neg_lo:[0,1] neg_hi:[0,1]
	v_mov_b32_e32 v13, v86
	v_pk_fma_f32 v[86:87], v[12:13], v[74:75], v[88:89] op_sel_hi:[1,0,1] neg_lo:[0,1,0] neg_hi:[0,1,0]
	s_waitcnt vmcnt(3)
	v_sub_f32_e32 v88, v62, v38
	v_mov_b32_e32 v13, v88
	v_mov_b32_e32 v89, v11
	v_pk_mul_f32 v[90:91], v[12:13], v[28:29] op_sel_hi:[1,0] neg_lo:[0,1] neg_hi:[0,1]
	v_pk_add_f32 v[30:31], v[42:43], v[30:31]
	v_pk_fma_f32 v[88:89], v[88:89], v[28:29], v[90:91] op_sel_hi:[1,0,1] neg_lo:[0,1,0] neg_hi:[0,1,0]
	s_waitcnt vmcnt(2)
	v_sub_f32_e32 v90, v63, v39
	v_mov_b32_e32 v13, v90
	v_mov_b32_e32 v91, v11
	v_pk_mul_f32 v[76:77], v[12:13], v[76:77] op_sel_hi:[1,0] neg_lo:[0,1] neg_hi:[0,1]
	v_pk_add_f32 v[42:43], v[20:21], v[30:31] neg_lo:[0,1] neg_hi:[0,1]
	v_pk_fma_f32 v[74:75], v[90:91], v[74:75], v[76:77] op_sel_hi:[1,0,1] neg_lo:[0,1,0] neg_hi:[0,1,0]
	s_waitcnt vmcnt(1)
	v_sub_f32_e32 v76, v64, v70
	v_mov_b32_e32 v13, v76
	v_mov_b32_e32 v77, v11
	v_pk_mul_f32 v[90:91], v[12:13], v[40:41] op_sel_hi:[1,0] neg_lo:[0,1] neg_hi:[0,1]
	v_pk_add_f32 v[32:33], v[46:47], v[32:33]
	v_pk_fma_f32 v[76:77], v[76:77], v[36:37], v[90:91] op_sel_hi:[1,0,1] neg_lo:[0,1,0] neg_hi:[0,1,0]
	s_waitcnt vmcnt(0)
	v_sub_f32_e32 v90, v65, v71
	v_mov_b32_e32 v13, v90
	v_pk_mul_f32 v[78:79], v[12:13], v[78:79] op_sel_hi:[1,0] neg_lo:[0,1] neg_hi:[0,1]
	v_mov_b32_e32 v13, v43
	v_mov_b32_e32 v46, v42
	v_pk_add_f32 v[20:21], v[20:21], v[30:31]
	v_mov_b32_e32 v30, v43
	v_mov_b32_e32 v31, v11
	v_pk_mul_f32 v[42:43], v[12:13], v[40:41] op_sel_hi:[1,0] neg_lo:[0,1] neg_hi:[0,1]
	v_pk_add_f32 v[34:35], v[62:63], v[38:39]
	v_pk_fma_f32 v[62:63], v[30:31], v[36:37], v[42:43] op_sel_hi:[1,0,1]
	v_pk_add_f32 v[30:31], v[26:27], v[32:33] neg_lo:[0,1] neg_hi:[0,1]
	v_pk_add_f32 v[24:25], v[24:25], v[66:67]
	v_mov_b32_e32 v13, v30
	v_mov_b32_e32 v42, v30
	v_pk_mul_f32 v[48:49], v[12:13], v[28:29] op_sel_hi:[1,0] neg_lo:[0,1] neg_hi:[0,1]
	v_pk_add_f32 v[26:27], v[26:27], v[32:33]
	v_mov_b32_e32 v32, v31
	v_mov_b32_e32 v33, v11
	v_mov_b32_e32 v13, v31
	v_pk_add_f32 v[30:31], v[24:25], v[34:35] neg_lo:[0,1] neg_hi:[0,1]
	v_pk_add_f32 v[22:23], v[22:23], v[68:69]
	v_pk_add_f32 v[38:39], v[64:65], v[70:71]
	v_pk_mul_f32 v[32:33], v[32:33], v[40:41] op_sel_hi:[1,0]
	v_pk_add_f32 v[24:25], v[24:25], v[34:35]
	v_mov_b32_e32 v34, v31
	v_mov_b32_e32 v35, v11
	v_pk_fma_f32 v[32:33], v[12:13], v[36:37], v[32:33] op_sel_hi:[1,0,1] neg_lo:[0,1,0] neg_hi:[0,1,0]
	v_xor_b32_e32 v67, 0x80000000, v30
	v_pk_mul_f32 v[34:35], v[34:35], v[40:41] op_sel_hi:[1,0] neg_lo:[0,1] neg_hi:[0,1]
	v_mov_b32_e32 v13, v31
	v_pk_add_f32 v[30:31], v[22:23], v[38:39] neg_lo:[0,1] neg_hi:[0,1]
	v_mov_b32_e32 v43, v11
	v_pk_fma_f32 v[68:69], v[12:13], v[36:37], v[34:35] op_sel_hi:[1,0,1] neg_lo:[0,1,0] neg_hi:[0,1,0]
	v_mov_b32_e32 v13, v30
	v_pk_fma_f32 v[64:65], v[42:43], v[28:29], v[48:49] op_sel_hi:[1,0,1]
	v_mov_b32_e32 v34, v30
	v_mov_b32_e32 v35, v11
	v_pk_mul_f32 v[42:43], v[12:13], v[28:29] op_sel_hi:[1,0] neg_lo:[0,1] neg_hi:[0,1]
	v_mov_b32_e32 v13, v31
	v_pk_fma_f32 v[70:71], v[34:35], v[28:29], v[42:43] op_sel_hi:[1,0,1] neg_lo:[0,1,0] neg_hi:[0,1,0]
	v_mov_b32_e32 v34, v31
	v_pk_mul_f32 v[30:31], v[12:13], v[40:41] op_sel_hi:[1,0] neg_lo:[0,1] neg_hi:[0,1]
	v_pk_add_f32 v[22:23], v[22:23], v[38:39]
	v_pk_fma_f32 v[38:39], v[34:35], v[36:37], v[30:31] op_sel_hi:[1,0,1] neg_lo:[0,1,0] neg_hi:[0,1,0]
	v_pk_add_f32 v[30:31], v[20:21], v[24:25] neg_lo:[0,1] neg_hi:[0,1]
	v_pk_add_f32 v[20:21], v[20:21], v[24:25]
	v_mov_b32_e32 v13, v31
	v_mov_b32_e32 v42, v30
	v_mov_b32_e32 v24, v31
	v_mov_b32_e32 v25, v11
	v_pk_mul_f32 v[30:31], v[12:13], v[28:29] op_sel_hi:[1,0] neg_lo:[0,1] neg_hi:[0,1]
	v_mov_b32_e32 v91, v11
	v_pk_fma_f32 v[30:31], v[24:25], v[28:29], v[30:31] op_sel_hi:[1,0,1]
	v_pk_add_f32 v[24:25], v[26:27], v[22:23] neg_lo:[0,1] neg_hi:[0,1]
	v_pk_fma_f32 v[72:73], v[90:91], v[72:73], v[78:79] op_sel_hi:[1,0,1] neg_lo:[0,1,0] neg_hi:[0,1,0]
	v_mov_b32_e32 v13, v25
	v_xor_b32_e32 v79, 0x80000000, v24
	v_pk_add_f32 v[22:23], v[26:27], v[22:23]
	v_mov_b32_e32 v26, v25
	v_mov_b32_e32 v27, v11
	v_pk_mul_f32 v[24:25], v[12:13], v[28:29] op_sel_hi:[1,0] neg_lo:[0,1] neg_hi:[0,1]
	v_pk_add_f32 v[34:35], v[20:21], v[22:23]
	v_pk_fma_f32 v[26:27], v[26:27], v[28:29], v[24:25] op_sel_hi:[1,0,1] neg_lo:[0,1,0] neg_hi:[0,1,0]
	v_pk_add_f32 v[24:25], v[20:21], v[22:23] neg_lo:[0,1] neg_hi:[0,1]
	v_mov_b32_e32 v43, v11
	v_pk_add_f32 v[20:21], v[24:25], 0 neg_lo:[1,1] neg_hi:[1,1]
	v_mov_b32_e32 v78, v11
	v_mov_b32_e32 v90, v24
	v_mov_b32_e32 v20, v11
	v_pk_add_f32 v[48:49], v[90:91], v[20:21]
	v_pk_add_f32 v[24:25], v[90:91], v[20:21] neg_lo:[0,1] neg_hi:[0,1]
	v_pk_add_f32 v[20:21], v[42:43], v[78:79]
	v_pk_add_f32 v[22:23], v[42:43], v[78:79] neg_lo:[0,1] neg_hi:[0,1]
	v_pk_add_f32 v[42:43], v[30:31], v[26:27]
	v_pk_add_f32 v[26:27], v[30:31], v[26:27] neg_lo:[0,1] neg_hi:[0,1]
	v_mov_b32_e32 v47, v11
	v_mov_b32_e32 v66, v11
	v_xor_b32_e32 v79, 0x80000000, v26
	v_mov_b32_e32 v78, v27
	v_pk_add_f32 v[26:27], v[62:63], v[68:69]
	v_pk_add_f32 v[62:63], v[62:63], v[68:69] neg_lo:[0,1] neg_hi:[0,1]
	v_pk_add_f32 v[90:91], v[20:21], v[42:43]
	v_pk_add_f32 v[30:31], v[20:21], v[42:43] neg_lo:[0,1] neg_hi:[0,1]
	v_pk_add_f32 v[42:43], v[22:23], v[78:79]
	v_pk_add_f32 v[20:21], v[22:23], v[78:79] neg_lo:[0,1] neg_hi:[0,1]
	v_pk_add_f32 v[22:23], v[46:47], v[66:67]
	v_pk_add_f32 v[46:47], v[46:47], v[66:67] neg_lo:[0,1] neg_hi:[0,1]
	v_pk_mul_f32 v[66:67], v[28:29], v[62:63] op_sel:[0,1] op_sel_hi:[0,0] neg_lo:[1,1] neg_hi:[1,0]
	v_pk_fma_f32 v[66:67], v[28:29], v[62:63], v[66:67] op_sel_hi:[0,1,1]
	v_pk_add_f32 v[62:63], v[64:65], v[70:71]
	v_pk_add_f32 v[64:65], v[64:65], v[70:71] neg_lo:[0,1] neg_hi:[0,1]
	v_mov_b32_e32 v80, v11
	v_xor_b32_e32 v69, 0x80000000, v64
	v_mov_b32_e32 v68, v65
	v_pk_add_f32 v[64:65], v[32:33], v[38:39]
	v_pk_add_f32 v[32:33], v[32:33], v[38:39] neg_lo:[0,1] neg_hi:[0,1]
	v_pk_add_f32 v[78:79], v[44:45], v[82:83]
	v_pk_mul_f32 v[38:39], v[28:29], v[32:33] op_sel:[0,1] op_sel_hi:[0,0] neg_lo:[1,1] neg_hi:[1,0]
	v_pk_fma_f32 v[32:33], v[28:29], v[32:33], v[38:39] op_sel_hi:[0,1,1] neg_lo:[1,0,0] neg_hi:[1,0,0]
	v_pk_add_f32 v[38:39], v[22:23], v[62:63]
	v_pk_add_f32 v[22:23], v[22:23], v[62:63] neg_lo:[0,1] neg_hi:[0,1]
	v_pk_add_f32 v[62:63], v[26:27], v[64:65]
	v_pk_add_f32 v[26:27], v[26:27], v[64:65] neg_lo:[0,1] neg_hi:[0,1]
	v_pk_add_f32 v[70:71], v[38:39], v[62:63]
	v_pk_add_f32 v[38:39], v[38:39], v[62:63] neg_lo:[0,1] neg_hi:[0,1]
	v_pk_add_f32 v[62:63], v[22:23], v[26:27] op_sel:[0,1] op_sel_hi:[1,0] neg_hi:[0,1]
	v_pk_add_f32 v[26:27], v[22:23], v[26:27] op_sel:[0,1] op_sel_hi:[1,0] neg_lo:[0,1]
	v_pk_add_f32 v[22:23], v[46:47], v[68:69]
	v_pk_add_f32 v[64:65], v[46:47], v[68:69] neg_lo:[0,1] neg_hi:[0,1]
	v_pk_add_f32 v[46:47], v[66:67], v[32:33]
	v_pk_add_f32 v[32:33], v[66:67], v[32:33] neg_lo:[0,1] neg_hi:[0,1]
	v_pk_add_f32 v[44:45], v[44:45], v[82:83] neg_lo:[0,1] neg_hi:[0,1]
	v_xor_b32_e32 v67, 0x80000000, v32
	v_mov_b32_e32 v66, v33
	v_pk_add_f32 v[68:69], v[22:23], v[46:47]
	v_pk_add_f32 v[32:33], v[22:23], v[46:47] neg_lo:[0,1] neg_hi:[0,1]
	v_pk_add_f32 v[46:47], v[64:65], v[66:67]
	v_pk_add_f32 v[22:23], v[64:65], v[66:67] neg_lo:[0,1] neg_hi:[0,1]
	v_pk_add_f32 v[64:65], v[10:11], v[80:81]
	v_pk_add_f32 v[66:67], v[10:11], v[80:81] neg_lo:[0,1] neg_hi:[0,1]
	v_pk_mul_f32 v[80:81], v[40:41], v[44:45] op_sel:[0,1] op_sel_hi:[0,0] neg_lo:[1,1] neg_hi:[1,0]
	v_pk_fma_f32 v[44:45], v[36:37], v[44:45], v[80:81] op_sel_hi:[0,1,1]
	v_pk_add_f32 v[80:81], v[50:51], v[84:85]
	v_pk_add_f32 v[50:51], v[50:51], v[84:85] neg_lo:[0,1] neg_hi:[0,1]
	v_add_f32_e32 v10, v34, v35
	v_pk_mul_f32 v[82:83], v[28:29], v[50:51] op_sel:[0,1] op_sel_hi:[0,0] neg_lo:[1,1] neg_hi:[1,0]
	v_pk_fma_f32 v[82:83], v[28:29], v[50:51], v[82:83] op_sel_hi:[0,1,1]
	v_pk_add_f32 v[50:51], v[54:55], v[86:87]
	v_pk_add_f32 v[54:55], v[54:55], v[86:87] neg_lo:[0,1] neg_hi:[0,1]
	v_pk_fma_f32 v[16:17], v[10:11], s[94:95], v[16:17] op_sel_hi:[0,1,1]
	v_pk_mul_f32 v[84:85], v[36:37], v[54:55] op_sel:[0,1] op_sel_hi:[0,0] neg_lo:[1,1] neg_hi:[1,0]
	v_pk_fma_f32 v[84:85], v[40:41], v[54:55], v[84:85] op_sel_hi:[0,1,1]
	v_pk_add_f32 v[54:55], v[56:57], v[88:89]
	v_pk_add_f32 v[56:57], v[56:57], v[88:89] neg_lo:[0,1] neg_hi:[0,1]
	v_lshl_add_u32 v13, v15, 3, 0
	v_xor_b32_e32 v87, 0x80000000, v56
	v_mov_b32_e32 v86, v57
	v_pk_add_f32 v[56:57], v[60:61], v[74:75]
	v_pk_add_f32 v[60:61], v[60:61], v[74:75] neg_lo:[0,1] neg_hi:[0,1]
	ds_write_b64 v13, v[16:17]
	v_pk_mul_f32 v[74:75], v[36:37], v[60:61] op_sel:[0,1] op_sel_hi:[0,0] neg_lo:[1,1] neg_hi:[1,0]
	v_pk_fma_f32 v[60:61], v[40:41], v[60:61], v[74:75] op_sel_hi:[0,1,1] neg_lo:[1,0,0] neg_hi:[1,0,0]
	v_pk_add_f32 v[74:75], v[58:59], v[76:77]
	v_pk_add_f32 v[58:59], v[58:59], v[76:77] neg_lo:[0,1] neg_hi:[0,1]
	v_pk_fma_f32 v[16:17], v[178:179], s[90:91], v[178:179] op_sel:[1,0,0] op_sel_hi:[0,1,1]
	v_pk_mul_f32 v[76:77], v[28:29], v[58:59] op_sel:[0,1] op_sel_hi:[0,0] neg_lo:[1,1] neg_hi:[1,0]
	v_pk_fma_f32 v[58:59], v[28:29], v[58:59], v[76:77] op_sel_hi:[0,1,1] neg_lo:[1,0,0] neg_hi:[1,0,0]
	v_pk_add_f32 v[76:77], v[52:53], v[72:73]
	v_pk_add_f32 v[52:53], v[52:53], v[72:73] neg_lo:[0,1] neg_hi:[0,1]
	s_nop 0
	v_pk_mul_f32 v[40:41], v[40:41], v[52:53] op_sel:[0,1] op_sel_hi:[0,0] neg_lo:[1,1] neg_hi:[1,0]
	v_pk_fma_f32 v[52:53], v[36:37], v[52:53], v[40:41] op_sel_hi:[0,1,1] neg_lo:[1,0,0] neg_hi:[1,0,0]
	v_pk_add_f32 v[36:37], v[64:65], v[54:55]
	v_pk_add_f32 v[64:65], v[64:65], v[54:55] neg_lo:[0,1] neg_hi:[0,1]
	v_pk_add_f32 v[54:55], v[78:79], v[56:57] neg_lo:[0,1] neg_hi:[0,1]
	v_pk_add_f32 v[40:41], v[56:57], v[78:79]
	v_pk_mul_f32 v[56:57], v[28:29], v[54:55] op_sel:[0,1] op_sel_hi:[0,0] neg_lo:[1,1] neg_hi:[1,0]
	v_pk_add_f32 v[72:73], v[80:81], v[74:75] neg_lo:[0,1] neg_hi:[0,1]
	v_pk_fma_f32 v[56:57], v[28:29], v[54:55], v[56:57] op_sel_hi:[0,1,1]
	v_pk_add_f32 v[54:55], v[80:81], v[74:75]
	v_xor_b32_e32 v75, 0x80000000, v72
	v_mov_b32_e32 v74, v73
	v_pk_add_f32 v[72:73], v[50:51], v[76:77]
	v_pk_add_f32 v[50:51], v[50:51], v[76:77] neg_lo:[0,1] neg_hi:[0,1]
	s_nop 0
	v_pk_mul_f32 v[76:77], v[28:29], v[50:51] op_sel:[0,1] op_sel_hi:[0,0] neg_lo:[1,1] neg_hi:[1,0]
	v_pk_fma_f32 v[50:51], v[28:29], v[50:51], v[76:77] op_sel_hi:[0,1,1] neg_lo:[1,0,0] neg_hi:[1,0,0]
	v_pk_add_f32 v[76:77], v[36:37], v[54:55]
	v_pk_add_f32 v[36:37], v[36:37], v[54:55] neg_lo:[0,1] neg_hi:[0,1]
	v_pk_add_f32 v[54:55], v[40:41], v[72:73]
	v_pk_add_f32 v[40:41], v[40:41], v[72:73] neg_lo:[0,1] neg_hi:[0,1]
	v_pk_add_f32 v[78:79], v[76:77], v[54:55]
	v_pk_add_f32 v[54:55], v[76:77], v[54:55] neg_lo:[0,1] neg_hi:[0,1]
	v_pk_add_f32 v[76:77], v[36:37], v[40:41] op_sel:[0,1] op_sel_hi:[1,0] neg_hi:[0,1]
	v_pk_add_f32 v[40:41], v[36:37], v[40:41] op_sel:[0,1] op_sel_hi:[1,0] neg_lo:[0,1]
	v_pk_add_f32 v[72:73], v[56:57], v[50:51]
	v_pk_add_f32 v[50:51], v[56:57], v[50:51] neg_lo:[0,1] neg_hi:[0,1]
	v_pk_add_f32 v[36:37], v[64:65], v[74:75]
	v_pk_add_f32 v[64:65], v[64:65], v[74:75] neg_lo:[0,1] neg_hi:[0,1]
	v_xor_b32_e32 v57, 0x80000000, v50
	v_mov_b32_e32 v56, v51
	v_pk_add_f32 v[74:75], v[36:37], v[72:73]
	v_pk_add_f32 v[50:51], v[36:37], v[72:73] neg_lo:[0,1] neg_hi:[0,1]
	v_pk_add_f32 v[72:73], v[64:65], v[56:57]
	v_pk_add_f32 v[36:37], v[64:65], v[56:57] neg_lo:[0,1] neg_hi:[0,1]
	v_pk_add_f32 v[56:57], v[66:67], v[86:87]
	v_pk_add_f32 v[64:65], v[66:67], v[86:87] neg_lo:[0,1] neg_hi:[0,1]
	v_pk_add_f32 v[66:67], v[60:61], v[44:45]
	v_pk_add_f32 v[44:45], v[44:45], v[60:61] neg_lo:[0,1] neg_hi:[0,1]
	s_nop 0
	v_pk_mul_f32 v[60:61], v[28:29], v[44:45] op_sel:[0,1] op_sel_hi:[0,0] neg_lo:[1,1] neg_hi:[1,0]
	v_pk_fma_f32 v[60:61], v[28:29], v[44:45], v[60:61] op_sel_hi:[0,1,1]
	v_pk_add_f32 v[44:45], v[82:83], v[58:59]
	v_pk_add_f32 v[58:59], v[82:83], v[58:59] neg_lo:[0,1] neg_hi:[0,1]
	s_nop 0
	v_xor_b32_e32 v81, 0x80000000, v58
	v_mov_b32_e32 v80, v59
	v_pk_add_f32 v[58:59], v[84:85], v[52:53]
	v_pk_add_f32 v[52:53], v[84:85], v[52:53] neg_lo:[0,1] neg_hi:[0,1]
	s_nop 0
	v_pk_mul_f32 v[82:83], v[28:29], v[52:53] op_sel:[0,1] op_sel_hi:[0,0] neg_lo:[1,1] neg_hi:[1,0]
	v_pk_fma_f32 v[28:29], v[28:29], v[52:53], v[82:83] op_sel_hi:[0,1,1] neg_lo:[1,0,0] neg_hi:[1,0,0]
	v_pk_add_f32 v[52:53], v[56:57], v[44:45]
	v_pk_add_f32 v[44:45], v[56:57], v[44:45] neg_lo:[0,1] neg_hi:[0,1]
	v_pk_add_f32 v[56:57], v[66:67], v[58:59]
	v_pk_add_f32 v[58:59], v[66:67], v[58:59] neg_lo:[0,1] neg_hi:[0,1]
	s_nop 0
	v_pk_add_f32 v[82:83], v[44:45], v[58:59] op_sel:[0,1] op_sel_hi:[1,0] neg_hi:[0,1]
	v_pk_add_f32 v[44:45], v[44:45], v[58:59] op_sel:[0,1] op_sel_hi:[1,0] neg_lo:[0,1]
	v_pk_add_f32 v[66:67], v[60:61], v[28:29]
	v_pk_add_f32 v[28:29], v[60:61], v[28:29] neg_lo:[0,1] neg_hi:[0,1]
	v_pk_add_f32 v[58:59], v[52:53], v[56:57]
	v_pk_add_f32 v[56:57], v[52:53], v[56:57] neg_lo:[0,1] neg_hi:[0,1]
	v_pk_add_f32 v[52:53], v[64:65], v[80:81]
	v_pk_add_f32 v[64:65], v[64:65], v[80:81] neg_lo:[0,1] neg_hi:[0,1]
	v_pk_add_f32 v[80:81], v[52:53], v[66:67]
	v_pk_add_f32 v[52:53], v[52:53], v[66:67] neg_lo:[0,1] neg_hi:[0,1]
	v_pk_add_f32 v[66:67], v[64:65], v[28:29] op_sel:[0,1] op_sel_hi:[1,0] neg_hi:[0,1]
	v_pk_add_f32 v[28:29], v[64:65], v[28:29] op_sel:[0,1] op_sel_hi:[1,0] neg_lo:[0,1]
	v_pk_mul_f32 v[60:61], v[16:17], v[78:79] op_sel:[1,1] op_sel_hi:[0,1] neg_lo:[0,1]
	v_pk_fma_f32 v[60:61], v[16:17], v[78:79], v[60:61] op_sel_hi:[1,0,1]
	ds_write_b64 v13, v[60:61] offset:4224
	v_pk_mul_f32 v[60:61], v[178:179], v[16:17] op_sel:[1,1] op_sel_hi:[0,1] neg_lo:[0,1]
	v_pk_fma_f32 v[16:17], v[178:179], v[16:17], v[60:61] op_sel_hi:[1,0,1]
	s_nop 0
	v_pk_mul_f32 v[60:61], v[16:17], v[70:71] op_sel:[1,1] op_sel_hi:[0,1] neg_lo:[0,1]
	v_pk_fma_f32 v[60:61], v[16:17], v[70:71], v[60:61] op_sel_hi:[1,0,1]
	ds_write_b64 v13, v[60:61] offset:8448
	v_pk_mul_f32 v[60:61], v[178:179], v[16:17] op_sel:[1,1] op_sel_hi:[0,1] neg_lo:[0,1]
	v_pk_fma_f32 v[16:17], v[178:179], v[16:17], v[60:61] op_sel_hi:[1,0,1]
	s_nop 0
	v_pk_mul_f32 v[60:61], v[16:17], v[58:59] op_sel:[1,1] op_sel_hi:[0,1] neg_lo:[0,1]
	v_pk_fma_f32 v[58:59], v[16:17], v[58:59], v[60:61] op_sel_hi:[1,0,1]
	ds_write_b64 v13, v[58:59] offset:12672
	v_pk_mul_f32 v[58:59], v[178:179], v[16:17] op_sel:[1,1] op_sel_hi:[0,1] neg_lo:[0,1]
	v_pk_fma_f32 v[16:17], v[178:179], v[16:17], v[58:59] op_sel_hi:[1,0,1]
	s_nop 0
	v_pk_mul_f32 v[58:59], v[90:91], v[16:17] op_sel:[1,1] op_sel_hi:[1,0] neg_lo:[1,0]
	s_nop 0
	v_pk_fma_f32 v[58:59], v[90:91], v[16:17], v[58:59] op_sel_hi:[0,1,1]
	ds_write_b64 v13, v[58:59] offset:16896
	v_pk_mul_f32 v[58:59], v[178:179], v[16:17] op_sel:[1,1] op_sel_hi:[0,1] neg_lo:[0,1]
	v_pk_fma_f32 v[16:17], v[178:179], v[16:17], v[58:59] op_sel_hi:[1,0,1]
	s_nop 0
	v_pk_mul_f32 v[58:59], v[16:17], v[74:75] op_sel:[1,1] op_sel_hi:[0,1] neg_lo:[0,1]
	v_pk_fma_f32 v[58:59], v[16:17], v[74:75], v[58:59] op_sel_hi:[1,0,1]
	ds_write_b64 v13, v[58:59] offset:21120
	v_pk_mul_f32 v[58:59], v[178:179], v[16:17] op_sel:[1,1] op_sel_hi:[0,1] neg_lo:[0,1]
	v_pk_fma_f32 v[16:17], v[178:179], v[16:17], v[58:59] op_sel_hi:[1,0,1]
	s_nop 0
	v_pk_mul_f32 v[58:59], v[68:69], v[16:17] op_sel:[1,1] op_sel_hi:[1,0] neg_lo:[1,0]
	s_nop 0
	v_pk_fma_f32 v[58:59], v[68:69], v[16:17], v[58:59] op_sel_hi:[0,1,1]
	ds_write_b64 v13, v[58:59] offset:25344
	v_pk_mul_f32 v[58:59], v[178:179], v[16:17] op_sel:[1,1] op_sel_hi:[0,1] neg_lo:[0,1]
	v_pk_fma_f32 v[16:17], v[178:179], v[16:17], v[58:59] op_sel_hi:[1,0,1]
	s_nop 0
	v_pk_mul_f32 v[58:59], v[80:81], v[16:17] op_sel:[1,1] op_sel_hi:[1,0] neg_lo:[1,0]
	s_nop 0
	v_pk_fma_f32 v[58:59], v[80:81], v[16:17], v[58:59] op_sel_hi:[0,1,1]
	ds_write_b64 v13, v[58:59] offset:29568
	v_pk_mul_f32 v[58:59], v[178:179], v[16:17] op_sel:[1,1] op_sel_hi:[0,1] neg_lo:[0,1]
	v_pk_fma_f32 v[16:17], v[178:179], v[16:17], v[58:59] op_sel_hi:[1,0,1]
	s_nop 0
	v_pk_mul_f32 v[58:59], v[48:49], v[16:17] op_sel:[1,1] op_sel_hi:[1,0] neg_lo:[1,0]
	s_nop 0
	v_pk_fma_f32 v[48:49], v[48:49], v[16:17], v[58:59] op_sel_hi:[0,1,1]
	ds_write_b64 v13, v[48:49] offset:33792
	v_pk_mul_f32 v[48:49], v[178:179], v[16:17] op_sel:[1,1] op_sel_hi:[0,1] neg_lo:[0,1]
	v_pk_fma_f32 v[16:17], v[178:179], v[16:17], v[48:49] op_sel_hi:[1,0,1]
	s_nop 0
	v_pk_mul_f32 v[48:49], v[76:77], v[16:17] op_sel:[1,1] op_sel_hi:[1,0] neg_lo:[1,0]
	s_nop 0
	v_pk_fma_f32 v[48:49], v[76:77], v[16:17], v[48:49] op_sel_hi:[0,1,1]
	ds_write_b64 v13, v[48:49] offset:38016
	v_pk_mul_f32 v[48:49], v[178:179], v[16:17] op_sel:[1,1] op_sel_hi:[0,1] neg_lo:[0,1]
	v_pk_fma_f32 v[16:17], v[178:179], v[16:17], v[48:49] op_sel_hi:[1,0,1]
	s_nop 0
	v_pk_mul_f32 v[48:49], v[62:63], v[16:17] op_sel:[1,1] op_sel_hi:[1,0] neg_lo:[1,0]
	s_nop 0
	v_pk_fma_f32 v[48:49], v[62:63], v[16:17], v[48:49] op_sel_hi:[0,1,1]
	ds_write_b64 v13, v[48:49] offset:42240
	v_pk_mul_f32 v[48:49], v[178:179], v[16:17] op_sel:[1,1] op_sel_hi:[0,1] neg_lo:[0,1]
	v_pk_fma_f32 v[16:17], v[178:179], v[16:17], v[48:49] op_sel_hi:[1,0,1]
	s_nop 0
	v_pk_mul_f32 v[48:49], v[82:83], v[16:17] op_sel:[1,1] op_sel_hi:[1,0] neg_lo:[1,0]
	s_nop 0
	v_pk_fma_f32 v[48:49], v[82:83], v[16:17], v[48:49] op_sel_hi:[0,1,1]
	ds_write_b64 v13, v[48:49] offset:46464
	v_pk_mul_f32 v[48:49], v[178:179], v[16:17] op_sel:[1,1] op_sel_hi:[0,1] neg_lo:[0,1]
	v_pk_fma_f32 v[16:17], v[178:179], v[16:17], v[48:49] op_sel_hi:[1,0,1]
	s_nop 0
	v_pk_mul_f32 v[48:49], v[42:43], v[16:17] op_sel:[1,1] op_sel_hi:[1,0] neg_lo:[1,0]
	s_nop 0
	v_pk_fma_f32 v[42:43], v[42:43], v[16:17], v[48:49] op_sel_hi:[0,1,1]
	ds_write_b64 v13, v[42:43] offset:50688
	v_pk_mul_f32 v[42:43], v[178:179], v[16:17] op_sel:[1,1] op_sel_hi:[0,1] neg_lo:[0,1]
	v_pk_fma_f32 v[16:17], v[178:179], v[16:17], v[42:43] op_sel_hi:[1,0,1]
	s_nop 0
	v_pk_mul_f32 v[42:43], v[72:73], v[16:17] op_sel:[1,1] op_sel_hi:[1,0] neg_lo:[1,0]
	s_nop 0
	v_pk_fma_f32 v[42:43], v[72:73], v[16:17], v[42:43] op_sel_hi:[0,1,1]
	ds_write_b64 v13, v[42:43] offset:54912
	v_pk_mul_f32 v[42:43], v[178:179], v[16:17] op_sel:[1,1] op_sel_hi:[0,1] neg_lo:[0,1]
	v_pk_fma_f32 v[16:17], v[178:179], v[16:17], v[42:43] op_sel_hi:[1,0,1]
	s_nop 0
	v_pk_mul_f32 v[42:43], v[46:47], v[16:17] op_sel:[1,1] op_sel_hi:[1,0] neg_lo:[1,0]
	s_nop 0
	v_pk_fma_f32 v[42:43], v[46:47], v[16:17], v[42:43] op_sel_hi:[0,1,1]
	ds_write_b64 v13, v[42:43] offset:59136
	v_pk_mul_f32 v[42:43], v[178:179], v[16:17] op_sel:[1,1] op_sel_hi:[0,1] neg_lo:[0,1]
	v_pk_fma_f32 v[16:17], v[178:179], v[16:17], v[42:43] op_sel_hi:[1,0,1]
	s_nop 0
	v_pk_mul_f32 v[42:43], v[66:67], v[16:17] op_sel:[1,1] op_sel_hi:[1,0] neg_lo:[1,0]
	s_nop 0
	v_pk_fma_f32 v[42:43], v[66:67], v[16:17], v[42:43] op_sel_hi:[0,1,1]
	ds_write_b64 v13, v[42:43] offset:63360
	v_pk_mul_f32 v[42:43], v[178:179], v[16:17] op_sel:[1,1] op_sel_hi:[0,1] neg_lo:[0,1]
	v_pk_fma_f32 v[16:17], v[178:179], v[16:17], v[42:43] op_sel_hi:[1,0,1]
	v_sub_f32_e32 v10, v34, v35
	v_pk_mul_f32 v[34:35], v[16:17], s[44:45]
	s_nop 0
	v_pk_fma_f32 v[34:35], v[10:11], v[16:17], v[34:35] op_sel:[0,0,1] op_sel_hi:[0,1,0]
	v_add_u32_e32 v10, 0x10800, v13
	ds_write_b64 v10, v[34:35]
	v_pk_mul_f32 v[34:35], v[178:179], v[16:17] op_sel:[1,1] op_sel_hi:[0,1] neg_lo:[0,1]
	v_pk_fma_f32 v[16:17], v[178:179], v[16:17], v[34:35] op_sel_hi:[1,0,1]
	s_nop 0
	v_pk_mul_f32 v[34:35], v[54:55], v[16:17] op_sel:[1,1] op_sel_hi:[1,0] neg_lo:[1,0]
	v_add_u32_e32 v10, 0x11880, v13
	v_pk_fma_f32 v[34:35], v[54:55], v[16:17], v[34:35] op_sel_hi:[0,1,1]
	ds_write_b64 v10, v[34:35]
	v_pk_mul_f32 v[34:35], v[178:179], v[16:17] op_sel:[1,1] op_sel_hi:[0,1] neg_lo:[0,1]
	v_pk_fma_f32 v[16:17], v[178:179], v[16:17], v[34:35] op_sel_hi:[1,0,1]
	s_nop 0
	v_pk_mul_f32 v[34:35], v[38:39], v[16:17] op_sel:[1,1] op_sel_hi:[1,0] neg_lo:[1,0]
	v_add_u32_e32 v10, 0x12900, v13
	v_pk_fma_f32 v[34:35], v[38:39], v[16:17], v[34:35] op_sel_hi:[0,1,1]
	ds_write_b64 v10, v[34:35]
	v_pk_mul_f32 v[34:35], v[178:179], v[16:17] op_sel:[1,1] op_sel_hi:[0,1] neg_lo:[0,1]
	v_pk_fma_f32 v[16:17], v[178:179], v[16:17], v[34:35] op_sel_hi:[1,0,1]
	s_nop 0
	v_pk_mul_f32 v[34:35], v[56:57], v[16:17] op_sel:[1,1] op_sel_hi:[1,0] neg_lo:[1,0]
	v_add_u32_e32 v10, 0x13980, v13
	v_pk_fma_f32 v[34:35], v[56:57], v[16:17], v[34:35] op_sel_hi:[0,1,1]
	ds_write_b64 v10, v[34:35]
	v_pk_mul_f32 v[34:35], v[178:179], v[16:17] op_sel:[1,1] op_sel_hi:[0,1] neg_lo:[0,1]
	v_pk_fma_f32 v[16:17], v[178:179], v[16:17], v[34:35] op_sel_hi:[1,0,1]
	s_nop 0
	v_pk_mul_f32 v[34:35], v[30:31], v[16:17] op_sel:[1,1] op_sel_hi:[1,0] neg_lo:[1,0]
	v_add_u32_e32 v10, 0x14a00, v13
	v_pk_fma_f32 v[30:31], v[30:31], v[16:17], v[34:35] op_sel_hi:[0,1,1]
	ds_write_b64 v10, v[30:31]
	v_pk_mul_f32 v[30:31], v[178:179], v[16:17] op_sel:[1,1] op_sel_hi:[0,1] neg_lo:[0,1]
	v_pk_fma_f32 v[16:17], v[178:179], v[16:17], v[30:31] op_sel_hi:[1,0,1]
	s_nop 0
	v_pk_mul_f32 v[30:31], v[50:51], v[16:17] op_sel:[1,1] op_sel_hi:[1,0] neg_lo:[1,0]
	v_add_u32_e32 v10, 0x15a80, v13
	v_pk_fma_f32 v[30:31], v[50:51], v[16:17], v[30:31] op_sel_hi:[0,1,1]
	ds_write_b64 v10, v[30:31]
	v_pk_mul_f32 v[30:31], v[178:179], v[16:17] op_sel:[1,1] op_sel_hi:[0,1] neg_lo:[0,1]
	v_pk_fma_f32 v[16:17], v[178:179], v[16:17], v[30:31] op_sel_hi:[1,0,1]
	s_nop 0
	v_pk_mul_f32 v[30:31], v[32:33], v[16:17] op_sel:[1,1] op_sel_hi:[1,0] neg_lo:[1,0]
	v_add_u32_e32 v10, 0x16b00, v13
	v_pk_fma_f32 v[30:31], v[32:33], v[16:17], v[30:31] op_sel_hi:[0,1,1]
	ds_write_b64 v10, v[30:31]
	v_pk_mul_f32 v[30:31], v[178:179], v[16:17] op_sel:[1,1] op_sel_hi:[0,1] neg_lo:[0,1]
	v_pk_fma_f32 v[16:17], v[178:179], v[16:17], v[30:31] op_sel_hi:[1,0,1]
	s_nop 0
	v_pk_mul_f32 v[30:31], v[52:53], v[16:17] op_sel:[1,1] op_sel_hi:[1,0] neg_lo:[1,0]
	v_add_u32_e32 v10, 0x17b80, v13
	v_pk_fma_f32 v[30:31], v[52:53], v[16:17], v[30:31] op_sel_hi:[0,1,1]
	ds_write_b64 v10, v[30:31]
	v_pk_mul_f32 v[30:31], v[178:179], v[16:17] op_sel:[1,1] op_sel_hi:[0,1] neg_lo:[0,1]
	v_pk_fma_f32 v[16:17], v[178:179], v[16:17], v[30:31] op_sel_hi:[1,0,1]
	s_nop 0
	v_pk_mul_f32 v[30:31], v[24:25], v[16:17] op_sel:[1,1] op_sel_hi:[1,0] neg_lo:[1,0]
	v_add_u32_e32 v10, 0x18c00, v13
	v_pk_fma_f32 v[24:25], v[24:25], v[16:17], v[30:31] op_sel_hi:[0,1,1]
	ds_write_b64 v10, v[24:25]
	v_pk_mul_f32 v[24:25], v[178:179], v[16:17] op_sel:[1,1] op_sel_hi:[0,1] neg_lo:[0,1]
	v_pk_fma_f32 v[16:17], v[178:179], v[16:17], v[24:25] op_sel_hi:[1,0,1]
	s_nop 0
	v_pk_mul_f32 v[24:25], v[40:41], v[16:17] op_sel:[1,1] op_sel_hi:[1,0] neg_lo:[1,0]
	v_add_u32_e32 v10, 0x19c80, v13
	v_pk_fma_f32 v[24:25], v[40:41], v[16:17], v[24:25] op_sel_hi:[0,1,1]
	ds_write_b64 v10, v[24:25]
	v_pk_mul_f32 v[24:25], v[178:179], v[16:17] op_sel:[1,1] op_sel_hi:[0,1] neg_lo:[0,1]
	v_pk_fma_f32 v[16:17], v[178:179], v[16:17], v[24:25] op_sel_hi:[1,0,1]
	s_nop 0
	v_pk_mul_f32 v[24:25], v[26:27], v[16:17] op_sel:[1,1] op_sel_hi:[1,0] neg_lo:[1,0]
	v_add_u32_e32 v10, 0x1ad00, v13
	v_pk_fma_f32 v[24:25], v[26:27], v[16:17], v[24:25] op_sel_hi:[0,1,1]
	ds_write_b64 v10, v[24:25]
	v_pk_mul_f32 v[24:25], v[178:179], v[16:17] op_sel:[1,1] op_sel_hi:[0,1] neg_lo:[0,1]
	v_pk_fma_f32 v[16:17], v[178:179], v[16:17], v[24:25] op_sel_hi:[1,0,1]
	s_nop 0
	v_pk_mul_f32 v[24:25], v[44:45], v[16:17] op_sel:[1,1] op_sel_hi:[1,0] neg_lo:[1,0]
	v_add_u32_e32 v10, 0x1bd80, v13
	v_pk_fma_f32 v[24:25], v[44:45], v[16:17], v[24:25] op_sel_hi:[0,1,1]
	ds_write_b64 v10, v[24:25]
	v_pk_mul_f32 v[24:25], v[178:179], v[16:17] op_sel:[1,1] op_sel_hi:[0,1] neg_lo:[0,1]
	v_pk_fma_f32 v[16:17], v[178:179], v[16:17], v[24:25] op_sel_hi:[1,0,1]
	s_nop 0
	v_pk_mul_f32 v[24:25], v[20:21], v[16:17] op_sel:[1,1] op_sel_hi:[1,0] neg_lo:[1,0]
	v_add_u32_e32 v10, 0x1ce00, v13
	v_pk_fma_f32 v[20:21], v[20:21], v[16:17], v[24:25] op_sel_hi:[0,1,1]
	ds_write_b64 v10, v[20:21]
	v_pk_mul_f32 v[20:21], v[178:179], v[16:17] op_sel:[1,1] op_sel_hi:[0,1] neg_lo:[0,1]
	v_pk_fma_f32 v[16:17], v[178:179], v[16:17], v[20:21] op_sel_hi:[1,0,1]
	s_nop 0
	v_pk_mul_f32 v[20:21], v[36:37], v[16:17] op_sel:[1,1] op_sel_hi:[1,0] neg_lo:[1,0]
	v_add_u32_e32 v10, 0x1de80, v13
	v_pk_fma_f32 v[20:21], v[36:37], v[16:17], v[20:21] op_sel_hi:[0,1,1]
	ds_write_b64 v10, v[20:21]
	v_pk_mul_f32 v[20:21], v[178:179], v[16:17] op_sel:[1,1] op_sel_hi:[0,1] neg_lo:[0,1]
	v_pk_fma_f32 v[16:17], v[178:179], v[16:17], v[20:21] op_sel_hi:[1,0,1]
	s_nop 0
	v_pk_mul_f32 v[20:21], v[22:23], v[16:17] op_sel:[1,1] op_sel_hi:[1,0] neg_lo:[1,0]
	v_add_u32_e32 v10, 0x1ef00, v13
	v_pk_fma_f32 v[20:21], v[22:23], v[16:17], v[20:21] op_sel_hi:[0,1,1]
	ds_write_b64 v10, v[20:21]
	v_pk_mul_f32 v[20:21], v[178:179], v[16:17] op_sel:[1,1] op_sel_hi:[0,1] neg_lo:[0,1]
	v_pk_fma_f32 v[16:17], v[178:179], v[16:17], v[20:21] op_sel_hi:[1,0,1]
	s_nop 0
	v_pk_mul_f32 v[18:19], v[28:29], v[16:17] op_sel:[1,1] op_sel_hi:[1,0] neg_lo:[1,0]
	v_add_u32_e32 v10, 0x1ff80, v13
	v_pk_fma_f32 v[16:17], v[28:29], v[16:17], v[18:19] op_sel_hi:[0,1,1]
	ds_write_b64 v10, v[16:17]
	v_mov_b32_e32 v10, v174
	v_mov_b32_e32 v13, v172
	s_waitcnt lgkmcnt(0)
	s_barrier
	v_mov_b32_e32 v16, v180
	v_add_u32_e32 v15, v13, v10
	v_lshl_add_u32 v75, v15, 3, 0
	v_xad_u32 v15, v13, 1, v10
	v_lshl_add_u32 v74, v15, 3, 0
	v_xad_u32 v15, v13, 2, v10
	v_lshl_add_u32 v73, v15, 3, 0
	v_xad_u32 v15, v13, 3, v10
	v_lshl_add_u32 v72, v15, 3, 0
	v_xad_u32 v15, v13, 4, v10
	v_lshl_add_u32 v71, v15, 3, 0
	v_xad_u32 v15, v13, 5, v10
	v_lshl_add_u32 v70, v15, 3, 0
	v_xad_u32 v15, v13, 6, v10
	v_lshl_add_u32 v69, v15, 3, 0
	v_xad_u32 v15, v13, 7, v10
	v_lshl_add_u32 v68, v15, 3, 0
	v_xad_u32 v15, v13, 8, v10
	v_lshl_add_u32 v15, v15, 3, 0
	v_add_u32_e32 v67, 0x800, v15
	v_xad_u32 v15, v13, 9, v10
	v_lshl_add_u32 v15, v15, 3, 0
	v_add_u32_e32 v66, 0x800, v15
	v_xad_u32 v15, v13, 10, v10
	v_lshl_add_u32 v15, v15, 3, 0
	v_add_u32_e32 v65, 0x800, v15
	v_xad_u32 v15, v13, 11, v10
	v_lshl_add_u32 v15, v15, 3, 0
	v_add_u32_e32 v64, 0x800, v15
	v_xad_u32 v15, v13, 12, v10
	v_mov_b32_e32 v17, v181
	v_lshl_add_u32 v15, v15, 3, 0
	ds_read2_b64 v[18:21], v75 offset1:16
	ds_read2_b64 v[40:43], v67 offset1:16
	v_add_u32_e32 v63, 0x800, v15
	v_xad_u32 v15, v13, 13, v10
	v_lshl_add_u32 v15, v15, 3, 0
	v_add_u32_e32 v62, 0x800, v15
	v_xad_u32 v15, v13, 14, v10
	v_xad_u32 v10, v13, 15, v10
	ds_read2_b64 v[22:25], v74 offset0:32 offset1:48
	ds_read2_b64 v[48:51], v66 offset0:32 offset1:48
	v_lshl_add_u32 v15, v15, 3, 0
	v_lshl_add_u32 v10, v10, 3, 0
	v_add_u32_e32 v15, 0x800, v15
	v_add_u32_e32 v13, 0x800, v10
	v_mov_b32_e32 v10, v1
	ds_read2_b64 v[26:29], v73 offset0:64 offset1:80
	ds_read2_b64 v[58:61], v72 offset0:96 offset1:112
	ds_read2_b64 v[76:79], v71 offset0:128 offset1:144
	ds_read2_b64 v[80:83], v70 offset0:160 offset1:176
	ds_read2_b64 v[84:87], v69 offset0:192 offset1:208
	ds_read2_b64 v[88:91], v68 offset0:224 offset1:240
	ds_read2_b64 v[54:57], v65 offset0:64 offset1:80
	ds_read2_b64 v[92:95], v64 offset0:96 offset1:112
	ds_read2_b64 v[96:99], v63 offset0:128 offset1:144
	ds_read2_b64 v[100:103], v62 offset0:160 offset1:176
	ds_read2_b64 v[104:107], v15 offset0:192 offset1:208
	ds_read2_b64 v[108:111], v13 offset0:224 offset1:240
	s_waitcnt lgkmcnt(14)
	v_pk_add_f32 v[112:113], v[18:19], v[40:41]
	v_pk_add_f32 v[40:41], v[18:19], v[40:41] neg_lo:[0,1] neg_hi:[0,1]
	v_pk_add_f32 v[18:19], v[20:21], v[42:43]
	v_pk_add_f32 v[20:21], v[20:21], v[42:43] neg_lo:[0,1] neg_hi:[0,1]
	v_mov_b32_e32 v30, v164
	v_mov_b32_e32 v32, v165
	v_mov_b32_e32 v34, v166
	v_mov_b32_e32 v10, v167
	v_mov_b32_e32 v38, v168
	v_mov_b32_e32 v36, v169
	v_mov_b32_e32 v46, v170
	v_mov_b32_e32 v31, v171
	v_pk_mul_f32 v[42:43], v[20:21], v[46:47] op_sel:[1,0] op_sel_hi:[0,0] neg_lo:[1,1] neg_hi:[0,1]
	s_nop 0
	v_pk_fma_f32 v[44:45], v[20:21], v[30:31], v[42:43] op_sel_hi:[1,0,1]
	s_waitcnt lgkmcnt(12)
	v_pk_add_f32 v[20:21], v[22:23], v[48:49]
	v_pk_add_f32 v[22:23], v[22:23], v[48:49] neg_lo:[0,1] neg_hi:[0,1]
	s_nop 0
	v_pk_mul_f32 v[42:43], v[22:23], v[36:37] op_sel:[1,0] op_sel_hi:[0,0] neg_lo:[1,1] neg_hi:[0,1]
	s_nop 0
	v_pk_fma_f32 v[48:49], v[22:23], v[32:33], v[42:43] op_sel_hi:[1,0,1]
	v_pk_add_f32 v[22:23], v[24:25], v[50:51]
	v_pk_add_f32 v[24:25], v[24:25], v[50:51] neg_lo:[0,1] neg_hi:[0,1]
	s_nop 0
	v_pk_mul_f32 v[42:43], v[24:25], v[38:39] op_sel:[1,0] op_sel_hi:[0,0] neg_lo:[1,1] neg_hi:[0,1]
	s_nop 0
	v_pk_fma_f32 v[52:53], v[24:25], v[34:35], v[42:43] op_sel_hi:[1,0,1]
	s_waitcnt lgkmcnt(5)
	v_pk_add_f32 v[24:25], v[26:27], v[54:55]
	v_pk_add_f32 v[26:27], v[26:27], v[54:55] neg_lo:[0,1] neg_hi:[0,1]
	s_nop 0
	v_pk_mul_f32 v[42:43], v[26:27], v[10:11] op_sel:[1,0] op_sel_hi:[0,0] neg_lo:[1,1] neg_hi:[0,1]
	s_nop 0
	v_pk_fma_f32 v[54:55], v[26:27], v[10:11], v[42:43] op_sel_hi:[1,0,1]
	v_pk_add_f32 v[26:27], v[28:29], v[56:57]
	v_pk_add_f32 v[28:29], v[28:29], v[56:57] neg_lo:[0,1] neg_hi:[0,1]
	s_nop 0
	v_pk_mul_f32 v[42:43], v[28:29], v[38:39] op_sel_hi:[1,0]
	s_nop 0
	v_pk_fma_f32 v[56:57], v[28:29], v[34:35], v[42:43] op_sel:[1,0,0] op_sel_hi:[0,0,1] neg_lo:[1,1,0] neg_hi:[0,1,0]
	s_waitcnt lgkmcnt(4)
	v_pk_add_f32 v[42:43], v[58:59], v[92:93] neg_lo:[0,1] neg_hi:[0,1]
	v_pk_add_f32 v[28:29], v[58:59], v[92:93]
	v_pk_mul_f32 v[50:51], v[42:43], v[36:37] op_sel_hi:[1,0]
	s_nop 0
	v_pk_fma_f32 v[58:59], v[42:43], v[32:33], v[50:51] op_sel:[1,0,0] op_sel_hi:[0,0,1] neg_lo:[1,1,0] neg_hi:[0,1,0]
	v_pk_add_f32 v[50:51], v[60:61], v[94:95] neg_lo:[0,1] neg_hi:[0,1]
	v_pk_add_f32 v[42:43], v[60:61], v[94:95]
	v_pk_mul_f32 v[60:61], v[50:51], v[46:47] op_sel_hi:[1,0]
	v_xor_b32_e32 v92, 0x80000000, v51
	v_mov_b32_e32 v93, v50
	s_waitcnt lgkmcnt(3)
	v_pk_add_f32 v[50:51], v[76:77], v[96:97]
	v_pk_add_f32 v[76:77], v[76:77], v[96:97] neg_lo:[0,1] neg_hi:[0,1]
	v_pk_fma_f32 v[60:61], v[92:93], v[30:31], v[60:61] op_sel_hi:[1,0,1] neg_lo:[0,1,0] neg_hi:[0,1,0]
	v_xor_b32_e32 v93, 0x80000000, v76
	v_mov_b32_e32 v92, v77
	v_pk_add_f32 v[76:77], v[78:79], v[98:99]
	v_pk_add_f32 v[78:79], v[78:79], v[98:99] neg_lo:[0,1] neg_hi:[0,1]
	s_nop 0
	v_pk_mul_f32 v[94:95], v[78:79], v[46:47] op_sel_hi:[1,0] neg_lo:[0,1] neg_hi:[0,1]
	s_nop 0
	v_pk_fma_f32 v[78:79], v[78:79], v[30:31], v[94:95] op_sel:[1,0,0] op_sel_hi:[0,0,1] neg_lo:[1,1,0] neg_hi:[0,1,0]
	s_waitcnt lgkmcnt(2)
	v_pk_add_f32 v[94:95], v[80:81], v[100:101]
	v_pk_add_f32 v[80:81], v[80:81], v[100:101] neg_lo:[0,1] neg_hi:[0,1]
	s_nop 0
	v_pk_mul_f32 v[96:97], v[80:81], v[36:37] op_sel_hi:[1,0] neg_lo:[0,1] neg_hi:[0,1]
	s_nop 0
	v_pk_fma_f32 v[80:81], v[80:81], v[32:33], v[96:97] op_sel:[1,0,0] op_sel_hi:[0,0,1] neg_lo:[1,1,0] neg_hi:[0,1,0]
	v_pk_add_f32 v[96:97], v[82:83], v[102:103]
	v_pk_add_f32 v[82:83], v[82:83], v[102:103] neg_lo:[0,1] neg_hi:[0,1]
	s_nop 0
	v_pk_mul_f32 v[98:99], v[82:83], v[38:39] op_sel_hi:[1,0] neg_lo:[0,1] neg_hi:[0,1]
	s_nop 0
	v_pk_fma_f32 v[82:83], v[82:83], v[34:35], v[98:99] op_sel:[1,0,0] op_sel_hi:[0,0,1] neg_lo:[1,1,0] neg_hi:[0,1,0]
	s_waitcnt lgkmcnt(1)
	v_pk_add_f32 v[98:99], v[84:85], v[104:105]
	v_pk_add_f32 v[84:85], v[84:85], v[104:105] neg_lo:[0,1] neg_hi:[0,1]
	s_nop 0
	v_pk_mul_f32 v[100:101], v[84:85], v[10:11] op_sel:[1,0] op_sel_hi:[0,0] neg_lo:[1,1] neg_hi:[0,1]
	s_nop 0
	v_pk_fma_f32 v[84:85], v[84:85], v[10:11], v[100:101] op_sel_hi:[1,0,1] neg_lo:[0,1,0] neg_hi:[0,1,0]
	v_pk_add_f32 v[100:101], v[86:87], v[106:107]
	v_pk_add_f32 v[86:87], v[86:87], v[106:107] neg_lo:[0,1] neg_hi:[0,1]
	s_nop 0
	v_pk_mul_f32 v[38:39], v[86:87], v[38:39] op_sel:[1,0] op_sel_hi:[0,0] neg_lo:[1,1] neg_hi:[0,1]
	s_nop 0
	v_pk_fma_f32 v[86:87], v[86:87], v[34:35], v[38:39] op_sel_hi:[1,0,1] neg_lo:[0,1,0] neg_hi:[0,1,0]
	s_waitcnt lgkmcnt(0)
	v_pk_add_f32 v[38:39], v[88:89], v[108:109] neg_lo:[0,1] neg_hi:[0,1]
	v_pk_add_f32 v[34:35], v[88:89], v[108:109]
	v_pk_mul_f32 v[88:89], v[38:39], v[36:37] op_sel:[1,0] op_sel_hi:[0,0] neg_lo:[1,1] neg_hi:[0,1]
	s_nop 0
	v_pk_fma_f32 v[88:89], v[38:39], v[32:33], v[88:89] op_sel_hi:[1,0,1] neg_lo:[0,1,0] neg_hi:[0,1,0]
	v_pk_add_f32 v[38:39], v[90:91], v[110:111]
	v_pk_add_f32 v[90:91], v[90:91], v[110:111] neg_lo:[0,1] neg_hi:[0,1]
	s_nop 0
	v_pk_mul_f32 v[46:47], v[90:91], v[46:47] op_sel:[1,0] op_sel_hi:[0,0] neg_lo:[1,1] neg_hi:[0,1]
	s_nop 0
	v_pk_fma_f32 v[90:91], v[90:91], v[30:31], v[46:47] op_sel_hi:[1,0,1] neg_lo:[0,1,0] neg_hi:[0,1,0]
	v_pk_add_f32 v[46:47], v[18:19], v[76:77]
	v_pk_add_f32 v[18:19], v[18:19], v[76:77] neg_lo:[0,1] neg_hi:[0,1]
	v_pk_add_f32 v[30:31], v[112:113], v[50:51]
	v_pk_mul_f32 v[76:77], v[18:19], v[36:37] op_sel:[1,0] op_sel_hi:[0,0] neg_lo:[1,1] neg_hi:[0,1]
	v_pk_add_f32 v[50:51], v[112:113], v[50:51] neg_lo:[0,1] neg_hi:[0,1]
	v_pk_fma_f32 v[76:77], v[18:19], v[32:33], v[76:77] op_sel_hi:[1,0,1]
	v_pk_add_f32 v[18:19], v[20:21], v[94:95]
	v_pk_add_f32 v[20:21], v[20:21], v[94:95] neg_lo:[0,1] neg_hi:[0,1]
	s_nop 0
	v_pk_mul_f32 v[94:95], v[20:21], v[10:11] op_sel:[1,0] op_sel_hi:[0,0] neg_lo:[1,1] neg_hi:[0,1]
	s_nop 0
	v_pk_fma_f32 v[20:21], v[20:21], v[10:11], v[94:95] op_sel_hi:[1,0,1]
	v_pk_add_f32 v[94:95], v[22:23], v[96:97]
	v_pk_add_f32 v[22:23], v[22:23], v[96:97] neg_lo:[0,1] neg_hi:[0,1]
	s_nop 0
	v_pk_mul_f32 v[96:97], v[22:23], v[36:37] op_sel_hi:[1,0]
	v_xor_b32_e32 v102, 0x80000000, v23
	v_mov_b32_e32 v103, v22
	v_pk_add_f32 v[22:23], v[24:25], v[98:99]
	v_pk_add_f32 v[24:25], v[24:25], v[98:99] neg_lo:[0,1] neg_hi:[0,1]
	v_pk_fma_f32 v[96:97], v[102:103], v[32:33], v[96:97] op_sel_hi:[1,0,1] neg_lo:[0,1,0] neg_hi:[0,1,0]
	v_xor_b32_e32 v99, 0x80000000, v24
	v_mov_b32_e32 v98, v25
	v_pk_add_f32 v[24:25], v[26:27], v[100:101]
	v_pk_add_f32 v[26:27], v[26:27], v[100:101] neg_lo:[0,1] neg_hi:[0,1]
	s_nop 0
	v_pk_mul_f32 v[100:101], v[26:27], v[36:37] op_sel_hi:[1,0] neg_lo:[0,1] neg_hi:[0,1]
	v_xor_b32_e32 v102, 0x80000000, v27
	v_mov_b32_e32 v103, v26
	v_pk_add_f32 v[26:27], v[28:29], v[34:35]
	v_pk_add_f32 v[28:29], v[28:29], v[34:35] neg_lo:[0,1] neg_hi:[0,1]
	v_pk_fma_f32 v[100:101], v[102:103], v[32:33], v[100:101] op_sel_hi:[1,0,1] neg_lo:[0,1,0] neg_hi:[0,1,0]
	v_pk_mul_f32 v[34:35], v[28:29], v[10:11] op_sel:[1,0] op_sel_hi:[0,0] neg_lo:[1,1] neg_hi:[0,1]
	v_pk_add_f32 v[102:103], v[30:31], v[22:23] neg_lo:[0,1] neg_hi:[0,1]
	v_pk_fma_f32 v[28:29], v[28:29], v[10:11], v[34:35] op_sel_hi:[1,0,1] neg_lo:[0,1,0] neg_hi:[0,1,0]
	v_pk_add_f32 v[34:35], v[42:43], v[38:39]
	v_pk_add_f32 v[38:39], v[42:43], v[38:39] neg_lo:[0,1] neg_hi:[0,1]
	s_nop 0
	v_pk_mul_f32 v[42:43], v[38:39], v[36:37] op_sel:[1,0] op_sel_hi:[0,0] neg_lo:[1,1] neg_hi:[0,1]
	s_nop 0
	v_pk_fma_f32 v[42:43], v[38:39], v[32:33], v[42:43] op_sel_hi:[1,0,1] neg_lo:[0,1,0] neg_hi:[0,1,0]
	v_pk_add_f32 v[38:39], v[30:31], v[22:23]
	v_pk_add_f32 v[22:23], v[46:47], v[24:25]
	v_pk_add_f32 v[24:25], v[46:47], v[24:25] neg_lo:[0,1] neg_hi:[0,1]
	s_nop 0
	v_pk_mul_f32 v[30:31], v[24:25], v[10:11] op_sel:[1,0] op_sel_hi:[0,0] neg_lo:[1,1] neg_hi:[0,1]
	s_nop 0
	v_pk_fma_f32 v[24:25], v[24:25], v[10:11], v[30:31] op_sel_hi:[1,0,1]
	v_pk_add_f32 v[30:31], v[18:19], v[26:27]
	v_pk_add_f32 v[18:19], v[18:19], v[26:27] neg_lo:[0,1] neg_hi:[0,1]
	s_nop 0
	v_xor_b32_e32 v27, 0x80000000, v18
	v_mov_b32_e32 v26, v19
	v_pk_add_f32 v[18:19], v[94:95], v[34:35]
	v_pk_add_f32 v[34:35], v[94:95], v[34:35] neg_lo:[0,1] neg_hi:[0,1]
	s_nop 0
	v_pk_mul_f32 v[46:47], v[34:35], v[10:11] op_sel:[1,0] op_sel_hi:[0,0] neg_lo:[1,1] neg_hi:[0,1]
	s_nop 0
	v_pk_fma_f32 v[34:35], v[34:35], v[10:11], v[46:47] op_sel_hi:[1,0,1] neg_lo:[0,1,0] neg_hi:[0,1,0]
	v_pk_add_f32 v[46:47], v[38:39], v[30:31]
	v_pk_add_f32 v[38:39], v[38:39], v[30:31] neg_lo:[0,1] neg_hi:[0,1]
	v_pk_add_f32 v[30:31], v[22:23], v[18:19]
	v_pk_add_f32 v[18:19], v[22:23], v[18:19] neg_lo:[0,1] neg_hi:[0,1]
	v_pk_add_f32 v[94:95], v[46:47], v[30:31]
	v_xor_b32_e32 v23, 0x80000000, v18
	v_mov_b32_e32 v22, v19
	v_pk_add_f32 v[18:19], v[102:103], v[26:27]
	v_pk_add_f32 v[102:103], v[102:103], v[26:27] neg_lo:[0,1] neg_hi:[0,1]
	v_pk_add_f32 v[26:27], v[24:25], v[34:35]
	v_pk_add_f32 v[24:25], v[24:25], v[34:35] neg_lo:[0,1] neg_hi:[0,1]
	v_pk_add_f32 v[30:31], v[46:47], v[30:31] neg_lo:[0,1] neg_hi:[0,1]
	v_xor_b32_e32 v35, 0x80000000, v24
	v_mov_b32_e32 v34, v25
	v_pk_add_f32 v[24:25], v[50:51], v[98:99]
	v_pk_add_f32 v[98:99], v[50:51], v[98:99] neg_lo:[0,1] neg_hi:[0,1]
	v_pk_add_f32 v[50:51], v[76:77], v[100:101] neg_lo:[0,1] neg_hi:[0,1]
	v_pk_add_f32 v[46:47], v[38:39], v[22:23]
	v_pk_add_f32 v[22:23], v[38:39], v[22:23] neg_lo:[0,1] neg_hi:[0,1]
	v_pk_add_f32 v[104:105], v[18:19], v[26:27]
	v_pk_add_f32 v[26:27], v[18:19], v[26:27] neg_lo:[0,1] neg_hi:[0,1]
	v_pk_add_f32 v[38:39], v[102:103], v[34:35]
	v_pk_add_f32 v[18:19], v[102:103], v[34:35] neg_lo:[0,1] neg_hi:[0,1]
	v_pk_add_f32 v[34:35], v[76:77], v[100:101]
	v_pk_mul_f32 v[76:77], v[10:11], v[50:51] op_sel:[0,1] op_sel_hi:[0,0] neg_lo:[1,1] neg_hi:[1,0]
	v_pk_fma_f32 v[76:77], v[10:11], v[50:51], v[76:77] op_sel_hi:[0,1,1]
	v_pk_add_f32 v[50:51], v[20:21], v[28:29]
	v_pk_add_f32 v[20:21], v[20:21], v[28:29] neg_lo:[0,1] neg_hi:[0,1]
	s_nop 0
	v_xor_b32_e32 v29, 0x80000000, v20
	v_mov_b32_e32 v28, v21
	v_pk_add_f32 v[20:21], v[96:97], v[42:43]
	v_pk_add_f32 v[42:43], v[96:97], v[42:43] neg_lo:[0,1] neg_hi:[0,1]
	s_nop 0
	v_pk_mul_f32 v[96:97], v[10:11], v[42:43] op_sel:[0,1] op_sel_hi:[0,0] neg_lo:[1,1] neg_hi:[1,0]
	v_pk_fma_f32 v[42:43], v[10:11], v[42:43], v[96:97] op_sel_hi:[0,1,1] neg_lo:[1,0,0] neg_hi:[1,0,0]
	v_pk_add_f32 v[96:97], v[24:25], v[50:51]
	v_pk_add_f32 v[24:25], v[24:25], v[50:51] neg_lo:[0,1] neg_hi:[0,1]
	v_pk_add_f32 v[50:51], v[34:35], v[20:21]
	v_pk_add_f32 v[20:21], v[34:35], v[20:21] neg_lo:[0,1] neg_hi:[0,1]
	v_pk_add_f32 v[102:103], v[96:97], v[50:51]
	v_xor_b32_e32 v101, 0x80000000, v20
	v_mov_b32_e32 v100, v21
	v_pk_add_f32 v[34:35], v[96:97], v[50:51] neg_lo:[0,1] neg_hi:[0,1]
	v_pk_add_f32 v[20:21], v[98:99], v[28:29]
	v_pk_add_f32 v[96:97], v[98:99], v[28:29] neg_lo:[0,1] neg_hi:[0,1]
	v_pk_add_f32 v[28:29], v[76:77], v[42:43]
	v_pk_add_f32 v[42:43], v[76:77], v[42:43] neg_lo:[0,1] neg_hi:[0,1]
	v_pk_add_f32 v[98:99], v[20:21], v[28:29]
	v_xor_b32_e32 v77, 0x80000000, v42
	v_mov_b32_e32 v76, v43
	v_pk_add_f32 v[28:29], v[20:21], v[28:29] neg_lo:[0,1] neg_hi:[0,1]
	v_pk_add_f32 v[42:43], v[96:97], v[76:77]
	v_pk_add_f32 v[20:21], v[96:97], v[76:77] neg_lo:[0,1] neg_hi:[0,1]
	v_pk_add_f32 v[76:77], v[40:41], v[92:93]
	v_pk_add_f32 v[92:93], v[40:41], v[92:93] neg_lo:[0,1] neg_hi:[0,1]
	v_pk_add_f32 v[40:41], v[44:45], v[78:79]
	v_pk_add_f32 v[44:45], v[44:45], v[78:79] neg_lo:[0,1] neg_hi:[0,1]
	v_pk_add_f32 v[50:51], v[24:25], v[100:101]
	v_pk_mul_f32 v[78:79], v[36:37], v[44:45] op_sel:[0,1] op_sel_hi:[0,0] neg_lo:[1,1] neg_hi:[1,0]
	v_pk_fma_f32 v[44:45], v[32:33], v[44:45], v[78:79] op_sel_hi:[0,1,1]
	v_pk_add_f32 v[78:79], v[48:49], v[80:81]
	v_pk_add_f32 v[48:49], v[48:49], v[80:81] neg_lo:[0,1] neg_hi:[0,1]
	v_pk_add_f32 v[24:25], v[24:25], v[100:101] neg_lo:[0,1] neg_hi:[0,1]
	v_pk_mul_f32 v[80:81], v[10:11], v[48:49] op_sel:[0,1] op_sel_hi:[0,0] neg_lo:[1,1] neg_hi:[1,0]
	v_pk_fma_f32 v[80:81], v[10:11], v[48:49], v[80:81] op_sel_hi:[0,1,1]
	v_pk_add_f32 v[48:49], v[52:53], v[82:83]
	v_pk_add_f32 v[52:53], v[52:53], v[82:83] neg_lo:[0,1] neg_hi:[0,1]
	s_nop 0
	v_pk_mul_f32 v[82:83], v[32:33], v[52:53] op_sel:[0,1] op_sel_hi:[0,0] neg_lo:[1,1] neg_hi:[1,0]
	v_pk_fma_f32 v[52:53], v[36:37], v[52:53], v[82:83] op_sel_hi:[0,1,1]
	v_pk_add_f32 v[82:83], v[54:55], v[84:85]
	v_pk_add_f32 v[54:55], v[54:55], v[84:85] neg_lo:[0,1] neg_hi:[0,1]
	s_nop 0
	v_xor_b32_e32 v85, 0x80000000, v54
	v_mov_b32_e32 v84, v55
	v_pk_add_f32 v[54:55], v[56:57], v[86:87]
	v_pk_add_f32 v[56:57], v[56:57], v[86:87] neg_lo:[0,1] neg_hi:[0,1]
	s_nop 0
	v_pk_mul_f32 v[86:87], v[32:33], v[56:57] op_sel:[0,1] op_sel_hi:[0,0] neg_lo:[1,1] neg_hi:[1,0]
	v_pk_fma_f32 v[56:57], v[36:37], v[56:57], v[86:87] op_sel_hi:[0,1,1] neg_lo:[1,0,0] neg_hi:[1,0,0]
	v_pk_add_f32 v[86:87], v[58:59], v[88:89]
	v_pk_add_f32 v[58:59], v[58:59], v[88:89] neg_lo:[0,1] neg_hi:[0,1]
	s_nop 0
	v_pk_mul_f32 v[88:89], v[10:11], v[58:59] op_sel:[0,1] op_sel_hi:[0,0] neg_lo:[1,1] neg_hi:[1,0]
	v_pk_fma_f32 v[58:59], v[10:11], v[58:59], v[88:89] op_sel_hi:[0,1,1] neg_lo:[1,0,0] neg_hi:[1,0,0]
	v_pk_add_f32 v[88:89], v[60:61], v[90:91]
	v_pk_add_f32 v[60:61], v[60:61], v[90:91] neg_lo:[0,1] neg_hi:[0,1]
	s_nop 0
	v_pk_mul_f32 v[36:37], v[36:37], v[60:61] op_sel:[0,1] op_sel_hi:[0,0] neg_lo:[1,1] neg_hi:[1,0]
	v_pk_fma_f32 v[36:37], v[32:33], v[60:61], v[36:37] op_sel_hi:[0,1,1] neg_lo:[1,0,0] neg_hi:[1,0,0]
	v_pk_add_f32 v[32:33], v[76:77], v[82:83]
	v_pk_add_f32 v[60:61], v[76:77], v[82:83] neg_lo:[0,1] neg_hi:[0,1]
	v_pk_add_f32 v[76:77], v[54:55], v[40:41]
	v_pk_add_f32 v[40:41], v[40:41], v[54:55] neg_lo:[0,1] neg_hi:[0,1]
	s_nop 0
	v_pk_mul_f32 v[54:55], v[10:11], v[40:41] op_sel:[0,1] op_sel_hi:[0,0] neg_lo:[1,1] neg_hi:[1,0]
	v_pk_fma_f32 v[54:55], v[10:11], v[40:41], v[54:55] op_sel_hi:[0,1,1]
	v_pk_add_f32 v[40:41], v[78:79], v[86:87]
	v_pk_add_f32 v[78:79], v[78:79], v[86:87] neg_lo:[0,1] neg_hi:[0,1]
	s_nop 0
	v_xor_b32_e32 v83, 0x80000000, v78
	v_mov_b32_e32 v82, v79
	v_pk_add_f32 v[78:79], v[48:49], v[88:89]
	v_pk_add_f32 v[48:49], v[48:49], v[88:89] neg_lo:[0,1] neg_hi:[0,1]
	v_pk_add_f32 v[88:89], v[76:77], v[78:79]
	v_pk_mul_f32 v[86:87], v[10:11], v[48:49] op_sel:[0,1] op_sel_hi:[0,0] neg_lo:[1,1] neg_hi:[1,0]
	v_pk_fma_f32 v[48:49], v[10:11], v[48:49], v[86:87] op_sel_hi:[0,1,1] neg_lo:[1,0,0] neg_hi:[1,0,0]
	v_pk_add_f32 v[86:87], v[32:33], v[40:41]
	v_pk_add_f32 v[32:33], v[32:33], v[40:41] neg_lo:[0,1] neg_hi:[0,1]
	v_pk_add_f32 v[40:41], v[76:77], v[78:79] neg_lo:[0,1] neg_hi:[0,1]
	v_pk_add_f32 v[78:79], v[86:87], v[88:89] neg_lo:[0,1] neg_hi:[0,1]
	v_pk_add_f32 v[90:91], v[32:33], v[40:41] op_sel:[0,1] op_sel_hi:[1,0] neg_hi:[0,1]
	v_pk_add_f32 v[40:41], v[32:33], v[40:41] op_sel:[0,1] op_sel_hi:[1,0] neg_lo:[0,1]
	v_pk_add_f32 v[76:77], v[54:55], v[48:49]
	v_pk_add_f32 v[48:49], v[54:55], v[48:49] neg_lo:[0,1] neg_hi:[0,1]
	v_pk_add_f32 v[32:33], v[60:61], v[82:83]
	v_pk_add_f32 v[60:61], v[60:61], v[82:83] neg_lo:[0,1] neg_hi:[0,1]
	v_xor_b32_e32 v55, 0x80000000, v48
	v_mov_b32_e32 v54, v49
	v_pk_add_f32 v[82:83], v[32:33], v[76:77]
	v_pk_add_f32 v[48:49], v[32:33], v[76:77] neg_lo:[0,1] neg_hi:[0,1]
	v_pk_add_f32 v[76:77], v[60:61], v[54:55]
	v_pk_add_f32 v[32:33], v[60:61], v[54:55] neg_lo:[0,1] neg_hi:[0,1]
	v_pk_add_f32 v[54:55], v[92:93], v[84:85]
	v_pk_add_f32 v[60:61], v[92:93], v[84:85] neg_lo:[0,1] neg_hi:[0,1]
	v_pk_add_f32 v[84:85], v[56:57], v[44:45]
	v_pk_add_f32 v[44:45], v[44:45], v[56:57] neg_lo:[0,1] neg_hi:[0,1]
	v_pk_add_f32 v[86:87], v[86:87], v[88:89]
	v_pk_mul_f32 v[56:57], v[10:11], v[44:45] op_sel:[0,1] op_sel_hi:[0,0] neg_lo:[1,1] neg_hi:[1,0]
	v_pk_fma_f32 v[56:57], v[10:11], v[44:45], v[56:57] op_sel_hi:[0,1,1]
	v_pk_add_f32 v[44:45], v[80:81], v[58:59]
	v_pk_add_f32 v[58:59], v[80:81], v[58:59] neg_lo:[0,1] neg_hi:[0,1]
	s_nop 0
	v_xor_b32_e32 v81, 0x80000000, v58
	v_mov_b32_e32 v80, v59
	v_pk_add_f32 v[58:59], v[52:53], v[36:37]
	v_pk_add_f32 v[36:37], v[52:53], v[36:37] neg_lo:[0,1] neg_hi:[0,1]
	s_nop 0
	v_pk_mul_f32 v[52:53], v[10:11], v[36:37] op_sel:[0,1] op_sel_hi:[0,0] neg_lo:[1,1] neg_hi:[1,0]
	v_pk_fma_f32 v[36:37], v[10:11], v[36:37], v[52:53] op_sel_hi:[0,1,1] neg_lo:[1,0,0] neg_hi:[1,0,0]
	v_pk_add_f32 v[52:53], v[54:55], v[44:45]
	v_pk_add_f32 v[44:45], v[54:55], v[44:45] neg_lo:[0,1] neg_hi:[0,1]
	v_pk_add_f32 v[54:55], v[84:85], v[58:59]
	v_pk_add_f32 v[58:59], v[84:85], v[58:59] neg_lo:[0,1] neg_hi:[0,1]
	s_nop 0
	v_xor_b32_e32 v85, 0x80000000, v58
	v_mov_b32_e32 v84, v59
	v_pk_add_f32 v[58:59], v[52:53], v[54:55]
	v_pk_add_f32 v[52:53], v[52:53], v[54:55] neg_lo:[0,1] neg_hi:[0,1]
	v_pk_add_f32 v[54:55], v[44:45], v[84:85]
	v_pk_add_f32 v[44:45], v[44:45], v[84:85] neg_lo:[0,1] neg_hi:[0,1]
	v_pk_add_f32 v[84:85], v[60:61], v[80:81]
	v_pk_add_f32 v[60:61], v[60:61], v[80:81] neg_lo:[0,1] neg_hi:[0,1]
	v_pk_add_f32 v[80:81], v[56:57], v[36:37]
	v_pk_add_f32 v[36:37], v[56:57], v[36:37] neg_lo:[0,1] neg_hi:[0,1]
	v_pk_add_f32 v[92:93], v[84:85], v[80:81]
	v_pk_add_f32 v[80:81], v[84:85], v[80:81] neg_lo:[0,1] neg_hi:[0,1]
	v_pk_add_f32 v[84:85], v[60:61], v[36:37] op_sel:[0,1] op_sel_hi:[1,0] neg_hi:[0,1]
	v_pk_add_f32 v[36:37], v[60:61], v[36:37] op_sel:[0,1] op_sel_hi:[1,0] neg_lo:[0,1]
	v_pk_fma_f32 v[60:61], v[16:17], s[90:91], v[16:17] op_sel:[1,0,0] op_sel_hi:[0,1,1]
	v_pk_mul_f32 v[56:57], v[94:95], s[14:15] op_sel:[1,0] neg_lo:[1,0]
	v_pk_mul_f32 v[88:89], v[60:61], v[86:87] op_sel:[1,1] op_sel_hi:[0,1] neg_lo:[0,1]
	v_pk_fma_f32 v[56:57], v[94:95], s[94:95], v[56:57] op_sel_hi:[0,1,1]
	v_pk_fma_f32 v[86:87], v[60:61], v[86:87], v[88:89] op_sel_hi:[1,0,1]
	ds_write2_b64 v75, v[56:57], v[86:87] offset1:16
	v_pk_mul_f32 v[56:57], v[16:17], v[60:61] op_sel:[1,1] op_sel_hi:[0,1] neg_lo:[0,1]
	v_pk_fma_f32 v[56:57], v[16:17], v[60:61], v[56:57] op_sel_hi:[1,0,1]
	s_nop 0
	v_pk_mul_f32 v[60:61], v[56:57], v[102:103] op_sel:[1,1] op_sel_hi:[0,1] neg_lo:[0,1]
	v_pk_mul_f32 v[86:87], v[16:17], v[56:57] op_sel:[1,1] op_sel_hi:[0,1] neg_lo:[0,1]
	v_pk_fma_f32 v[60:61], v[56:57], v[102:103], v[60:61] op_sel_hi:[1,0,1]
	v_pk_fma_f32 v[56:57], v[16:17], v[56:57], v[86:87] op_sel_hi:[1,0,1]
	s_nop 0
	v_pk_mul_f32 v[86:87], v[56:57], v[58:59] op_sel:[1,1] op_sel_hi:[0,1] neg_lo:[0,1]
	v_pk_fma_f32 v[58:59], v[56:57], v[58:59], v[86:87] op_sel_hi:[1,0,1]
	ds_write2_b64 v74, v[60:61], v[58:59] offset0:32 offset1:48
	v_pk_mul_f32 v[58:59], v[16:17], v[56:57] op_sel:[1,1] op_sel_hi:[0,1] neg_lo:[0,1]
	v_pk_fma_f32 v[56:57], v[16:17], v[56:57], v[58:59] op_sel_hi:[1,0,1]
	s_nop 0
	v_pk_mul_f32 v[58:59], v[56:57], v[104:105] op_sel:[1,1] op_sel_hi:[0,1] neg_lo:[0,1]
	v_pk_mul_f32 v[60:61], v[16:17], v[56:57] op_sel:[1,1] op_sel_hi:[0,1] neg_lo:[0,1]
	v_pk_fma_f32 v[58:59], v[56:57], v[104:105], v[58:59] op_sel_hi:[1,0,1]
	v_pk_fma_f32 v[56:57], v[16:17], v[56:57], v[60:61] op_sel_hi:[1,0,1]
	s_nop 0
	v_pk_mul_f32 v[60:61], v[56:57], v[82:83] op_sel:[1,1] op_sel_hi:[0,1] neg_lo:[0,1]
	v_pk_fma_f32 v[60:61], v[56:57], v[82:83], v[60:61] op_sel_hi:[1,0,1]
	ds_write2_b64 v73, v[58:59], v[60:61] offset0:64 offset1:80
	v_pk_mul_f32 v[58:59], v[16:17], v[56:57] op_sel:[1,1] op_sel_hi:[0,1] neg_lo:[0,1]
	v_pk_fma_f32 v[56:57], v[16:17], v[56:57], v[58:59] op_sel_hi:[1,0,1]
	s_nop 0
	v_pk_mul_f32 v[58:59], v[56:57], v[98:99] op_sel:[1,1] op_sel_hi:[0,1] neg_lo:[0,1]
	v_pk_mul_f32 v[60:61], v[16:17], v[56:57] op_sel:[1,1] op_sel_hi:[0,1] neg_lo:[0,1]
	v_pk_fma_f32 v[58:59], v[56:57], v[98:99], v[58:59] op_sel_hi:[1,0,1]
	v_pk_fma_f32 v[56:57], v[16:17], v[56:57], v[60:61] op_sel_hi:[1,0,1]
	s_nop 0
	v_pk_mul_f32 v[60:61], v[56:57], v[92:93] op_sel:[1,1] op_sel_hi:[0,1] neg_lo:[0,1]
	v_pk_fma_f32 v[60:61], v[56:57], v[92:93], v[60:61] op_sel_hi:[1,0,1]
	ds_write2_b64 v72, v[58:59], v[60:61] offset0:96 offset1:112
	v_pk_mul_f32 v[58:59], v[16:17], v[56:57] op_sel:[1,1] op_sel_hi:[0,1] neg_lo:[0,1]
	v_pk_fma_f32 v[56:57], v[16:17], v[56:57], v[58:59] op_sel_hi:[1,0,1]
	s_nop 0
	v_pk_mul_f32 v[58:59], v[56:57], v[46:47] op_sel:[1,1] op_sel_hi:[0,1] neg_lo:[0,1]
	v_pk_fma_f32 v[46:47], v[56:57], v[46:47], v[58:59] op_sel_hi:[1,0,1]
	v_pk_mul_f32 v[58:59], v[16:17], v[56:57] op_sel:[1,1] op_sel_hi:[0,1] neg_lo:[0,1]
	v_pk_fma_f32 v[56:57], v[16:17], v[56:57], v[58:59] op_sel_hi:[1,0,1]
	s_nop 0
	v_pk_mul_f32 v[58:59], v[56:57], v[90:91] op_sel:[1,1] op_sel_hi:[0,1] neg_lo:[0,1]
	v_pk_fma_f32 v[58:59], v[56:57], v[90:91], v[58:59] op_sel_hi:[1,0,1]
	ds_write2_b64 v71, v[46:47], v[58:59] offset0:128 offset1:144
	v_pk_mul_f32 v[46:47], v[16:17], v[56:57] op_sel:[1,1] op_sel_hi:[0,1] neg_lo:[0,1]
	v_pk_fma_f32 v[46:47], v[16:17], v[56:57], v[46:47] op_sel_hi:[1,0,1]
	s_nop 0
	v_pk_mul_f32 v[56:57], v[46:47], v[50:51] op_sel:[1,1] op_sel_hi:[0,1] neg_lo:[0,1]
	v_pk_fma_f32 v[50:51], v[46:47], v[50:51], v[56:57] op_sel_hi:[1,0,1]
	v_pk_mul_f32 v[56:57], v[16:17], v[46:47] op_sel:[1,1] op_sel_hi:[0,1] neg_lo:[0,1]
	v_pk_fma_f32 v[46:47], v[16:17], v[46:47], v[56:57] op_sel_hi:[1,0,1]
	s_nop 0
	v_pk_mul_f32 v[56:57], v[46:47], v[54:55] op_sel:[1,1] op_sel_hi:[0,1] neg_lo:[0,1]
	v_pk_fma_f32 v[54:55], v[46:47], v[54:55], v[56:57] op_sel_hi:[1,0,1]
	ds_write2_b64 v70, v[50:51], v[54:55] offset0:160 offset1:176
	v_pk_mul_f32 v[50:51], v[16:17], v[46:47] op_sel:[1,1] op_sel_hi:[0,1] neg_lo:[0,1]
	v_pk_fma_f32 v[46:47], v[16:17], v[46:47], v[50:51] op_sel_hi:[1,0,1]
	s_nop 0
	v_pk_mul_f32 v[50:51], v[38:39], v[46:47] op_sel:[1,1] op_sel_hi:[1,0] neg_lo:[1,0]
	s_nop 0
	v_pk_fma_f32 v[38:39], v[38:39], v[46:47], v[50:51] op_sel_hi:[0,1,1]
	v_pk_mul_f32 v[50:51], v[16:17], v[46:47] op_sel:[1,1] op_sel_hi:[0,1] neg_lo:[0,1]
	v_pk_fma_f32 v[46:47], v[16:17], v[46:47], v[50:51] op_sel_hi:[1,0,1]
	s_nop 0
	v_pk_mul_f32 v[50:51], v[46:47], v[76:77] op_sel:[1,1] op_sel_hi:[0,1] neg_lo:[0,1]
	v_pk_fma_f32 v[50:51], v[46:47], v[76:77], v[50:51] op_sel_hi:[1,0,1]
	ds_write2_b64 v69, v[38:39], v[50:51] offset0:192 offset1:208
	v_pk_mul_f32 v[38:39], v[16:17], v[46:47] op_sel:[1,1] op_sel_hi:[0,1] neg_lo:[0,1]
	v_pk_fma_f32 v[38:39], v[16:17], v[46:47], v[38:39] op_sel_hi:[1,0,1]
	s_nop 0
	v_pk_mul_f32 v[46:47], v[42:43], v[38:39] op_sel:[1,1] op_sel_hi:[1,0] neg_lo:[1,0]
	s_nop 0
	v_pk_fma_f32 v[42:43], v[42:43], v[38:39], v[46:47] op_sel_hi:[0,1,1]
	v_pk_mul_f32 v[46:47], v[16:17], v[38:39] op_sel:[1,1] op_sel_hi:[0,1] neg_lo:[0,1]
	v_pk_fma_f32 v[38:39], v[16:17], v[38:39], v[46:47] op_sel_hi:[1,0,1]
	s_nop 0
	v_pk_mul_f32 v[46:47], v[38:39], v[84:85] op_sel:[1,1] op_sel_hi:[0,1] neg_lo:[0,1]
	v_pk_fma_f32 v[46:47], v[38:39], v[84:85], v[46:47] op_sel_hi:[1,0,1]
	ds_write2_b64 v68, v[42:43], v[46:47] offset0:224 offset1:240
	v_pk_mul_f32 v[42:43], v[16:17], v[38:39] op_sel:[1,1] op_sel_hi:[0,1] neg_lo:[0,1]
	v_pk_fma_f32 v[38:39], v[16:17], v[38:39], v[42:43] op_sel_hi:[1,0,1]
	s_nop 0
	v_pk_mul_f32 v[42:43], v[30:31], v[38:39] op_sel:[1,1] op_sel_hi:[1,0] neg_lo:[1,0]
	s_nop 0
	v_pk_fma_f32 v[30:31], v[30:31], v[38:39], v[42:43] op_sel_hi:[0,1,1]
	v_pk_mul_f32 v[42:43], v[16:17], v[38:39] op_sel:[1,1] op_sel_hi:[0,1] neg_lo:[0,1]
	v_pk_fma_f32 v[38:39], v[16:17], v[38:39], v[42:43] op_sel_hi:[1,0,1]
	s_nop 0
	v_pk_mul_f32 v[42:43], v[78:79], v[38:39] op_sel:[1,1] op_sel_hi:[1,0] neg_lo:[1,0]
	s_nop 0
	v_pk_fma_f32 v[42:43], v[78:79], v[38:39], v[42:43] op_sel_hi:[0,1,1]
	ds_write2_b64 v67, v[30:31], v[42:43] offset1:16
	v_pk_mul_f32 v[30:31], v[16:17], v[38:39] op_sel:[1,1] op_sel_hi:[0,1] neg_lo:[0,1]
	v_pk_fma_f32 v[30:31], v[16:17], v[38:39], v[30:31] op_sel_hi:[1,0,1]
	s_nop 0
	v_pk_mul_f32 v[38:39], v[34:35], v[30:31] op_sel:[1,1] op_sel_hi:[1,0] neg_lo:[1,0]
	s_nop 0
	v_pk_fma_f32 v[34:35], v[34:35], v[30:31], v[38:39] op_sel_hi:[0,1,1]
	v_pk_mul_f32 v[38:39], v[16:17], v[30:31] op_sel:[1,1] op_sel_hi:[0,1] neg_lo:[0,1]
	v_pk_fma_f32 v[30:31], v[16:17], v[30:31], v[38:39] op_sel_hi:[1,0,1]
	s_nop 0
	v_pk_mul_f32 v[38:39], v[52:53], v[30:31] op_sel:[1,1] op_sel_hi:[1,0] neg_lo:[1,0]
	s_nop 0
	v_pk_fma_f32 v[38:39], v[52:53], v[30:31], v[38:39] op_sel_hi:[0,1,1]
	ds_write2_b64 v66, v[34:35], v[38:39] offset0:32 offset1:48
	v_pk_mul_f32 v[34:35], v[16:17], v[30:31] op_sel:[1,1] op_sel_hi:[0,1] neg_lo:[0,1]
	v_pk_fma_f32 v[30:31], v[16:17], v[30:31], v[34:35] op_sel_hi:[1,0,1]
	s_nop 0
	v_pk_mul_f32 v[34:35], v[26:27], v[30:31] op_sel:[1,1] op_sel_hi:[1,0] neg_lo:[1,0]
	s_nop 0
	v_pk_fma_f32 v[26:27], v[26:27], v[30:31], v[34:35] op_sel_hi:[0,1,1]
	v_pk_mul_f32 v[34:35], v[16:17], v[30:31] op_sel:[1,1] op_sel_hi:[0,1] neg_lo:[0,1]
	v_pk_fma_f32 v[30:31], v[16:17], v[30:31], v[34:35] op_sel_hi:[1,0,1]
	s_nop 0
	v_pk_mul_f32 v[34:35], v[48:49], v[30:31] op_sel:[1,1] op_sel_hi:[1,0] neg_lo:[1,0]
	s_nop 0
	v_pk_fma_f32 v[34:35], v[48:49], v[30:31], v[34:35] op_sel_hi:[0,1,1]
	ds_write2_b64 v65, v[26:27], v[34:35] offset0:64 offset1:80
	v_pk_mul_f32 v[26:27], v[16:17], v[30:31] op_sel:[1,1] op_sel_hi:[0,1] neg_lo:[0,1]
	v_pk_fma_f32 v[26:27], v[16:17], v[30:31], v[26:27] op_sel_hi:[1,0,1]
	s_nop 0
	v_pk_mul_f32 v[30:31], v[28:29], v[26:27] op_sel:[1,1] op_sel_hi:[1,0] neg_lo:[1,0]
	s_nop 0
	v_pk_fma_f32 v[28:29], v[28:29], v[26:27], v[30:31] op_sel_hi:[0,1,1]
	v_pk_mul_f32 v[30:31], v[16:17], v[26:27] op_sel:[1,1] op_sel_hi:[0,1] neg_lo:[0,1]
	v_pk_fma_f32 v[26:27], v[16:17], v[26:27], v[30:31] op_sel_hi:[1,0,1]
	s_nop 0
	v_pk_mul_f32 v[30:31], v[80:81], v[26:27] op_sel:[1,1] op_sel_hi:[1,0] neg_lo:[1,0]
	s_nop 0
	v_pk_fma_f32 v[30:31], v[80:81], v[26:27], v[30:31] op_sel_hi:[0,1,1]
	ds_write2_b64 v64, v[28:29], v[30:31] offset0:96 offset1:112
	v_pk_mul_f32 v[28:29], v[16:17], v[26:27] op_sel:[1,1] op_sel_hi:[0,1] neg_lo:[0,1]
	v_pk_fma_f32 v[26:27], v[16:17], v[26:27], v[28:29] op_sel_hi:[1,0,1]
	s_nop 0
	v_pk_mul_f32 v[28:29], v[22:23], v[26:27] op_sel:[1,1] op_sel_hi:[1,0] neg_lo:[1,0]
	s_nop 0
	v_pk_fma_f32 v[22:23], v[22:23], v[26:27], v[28:29] op_sel_hi:[0,1,1]
	v_pk_mul_f32 v[28:29], v[16:17], v[26:27] op_sel:[1,1] op_sel_hi:[0,1] neg_lo:[0,1]
	v_pk_fma_f32 v[26:27], v[16:17], v[26:27], v[28:29] op_sel_hi:[1,0,1]
	s_nop 0
	v_pk_mul_f32 v[28:29], v[40:41], v[26:27] op_sel:[1,1] op_sel_hi:[1,0] neg_lo:[1,0]
	s_nop 0
	v_pk_fma_f32 v[28:29], v[40:41], v[26:27], v[28:29] op_sel_hi:[0,1,1]
	ds_write2_b64 v63, v[22:23], v[28:29] offset0:128 offset1:144
	v_pk_mul_f32 v[22:23], v[16:17], v[26:27] op_sel:[1,1] op_sel_hi:[0,1] neg_lo:[0,1]
	v_pk_fma_f32 v[22:23], v[16:17], v[26:27], v[22:23] op_sel_hi:[1,0,1]
	s_nop 0
	v_pk_mul_f32 v[26:27], v[24:25], v[22:23] op_sel:[1,1] op_sel_hi:[1,0] neg_lo:[1,0]
	s_nop 0
	v_pk_fma_f32 v[24:25], v[24:25], v[22:23], v[26:27] op_sel_hi:[0,1,1]
	v_pk_mul_f32 v[26:27], v[16:17], v[22:23] op_sel:[1,1] op_sel_hi:[0,1] neg_lo:[0,1]
	v_pk_fma_f32 v[22:23], v[16:17], v[22:23], v[26:27] op_sel_hi:[1,0,1]
	s_nop 0
	v_pk_mul_f32 v[26:27], v[44:45], v[22:23] op_sel:[1,1] op_sel_hi:[1,0] neg_lo:[1,0]
	s_nop 0
	v_pk_fma_f32 v[26:27], v[44:45], v[22:23], v[26:27] op_sel_hi:[0,1,1]
	ds_write2_b64 v62, v[24:25], v[26:27] offset0:160 offset1:176
	v_pk_mul_f32 v[24:25], v[16:17], v[22:23] op_sel:[1,1] op_sel_hi:[0,1] neg_lo:[0,1]
	v_pk_fma_f32 v[22:23], v[16:17], v[22:23], v[24:25] op_sel_hi:[1,0,1]
	s_nop 0
	v_pk_mul_f32 v[24:25], v[18:19], v[22:23] op_sel:[1,1] op_sel_hi:[1,0] neg_lo:[1,0]
	s_nop 0
	v_pk_fma_f32 v[18:19], v[18:19], v[22:23], v[24:25] op_sel_hi:[0,1,1]
	v_pk_mul_f32 v[24:25], v[16:17], v[22:23] op_sel:[1,1] op_sel_hi:[0,1] neg_lo:[0,1]
	v_pk_fma_f32 v[22:23], v[16:17], v[22:23], v[24:25] op_sel_hi:[1,0,1]
	s_nop 0
	v_pk_mul_f32 v[24:25], v[32:33], v[22:23] op_sel:[1,1] op_sel_hi:[1,0] neg_lo:[1,0]
	s_nop 0
	v_pk_fma_f32 v[24:25], v[32:33], v[22:23], v[24:25] op_sel_hi:[0,1,1]
	ds_write2_b64 v15, v[18:19], v[24:25] offset0:192 offset1:208
	v_pk_mul_f32 v[18:19], v[16:17], v[22:23] op_sel:[1,1] op_sel_hi:[0,1] neg_lo:[0,1]
	v_pk_fma_f32 v[18:19], v[16:17], v[22:23], v[18:19] op_sel_hi:[1,0,1]
	s_nop 0
	v_pk_mul_f32 v[22:23], v[20:21], v[18:19] op_sel:[1,1] op_sel_hi:[1,0] neg_lo:[1,0]
	s_nop 0
	v_pk_fma_f32 v[20:21], v[20:21], v[18:19], v[22:23] op_sel_hi:[0,1,1]
	v_pk_mul_f32 v[22:23], v[16:17], v[18:19] op_sel:[1,1] op_sel_hi:[0,1] neg_lo:[0,1]
	v_pk_fma_f32 v[16:17], v[16:17], v[18:19], v[22:23] op_sel_hi:[1,0,1]
	s_nop 0
	v_pk_mul_f32 v[18:19], v[36:37], v[16:17] op_sel:[1,1] op_sel_hi:[1,0] neg_lo:[1,0]
	s_nop 0
	v_pk_fma_f32 v[16:17], v[36:37], v[16:17], v[18:19] op_sel_hi:[0,1,1]
	ds_write2_b64 v13, v[20:21], v[16:17] offset0:224 offset1:240
	v_mov_b32_e32 v16, v182
	v_mov_b32_e32 v10, v176
	v_mov_b32_e32 v17, v175
	s_waitcnt lgkmcnt(0)
	s_barrier
	v_lshlrev_b32_e32 v190, 3, v16
	v_add_u32_e32 v190, 0x1000, v190
	global_load_dwordx2 v[202:203], v190, s[46:47] offset:-4096
	global_load_dwordx2 v[204:205], v190, s[46:47]
	v_add_u32_e32 v190, 0x2000, v190
	global_load_dwordx2 v[206:207], v190, s[46:47] offset:-4096
	global_load_dwordx2 v[208:209], v190, s[46:47]
	v_add_u32_e32 v190, 0x2000, v190
	global_load_dwordx2 v[210:211], v190, s[46:47] offset:-4096
	global_load_dwordx2 v[212:213], v190, s[46:47]
	v_add_u32_e32 v190, 0x2000, v190
	global_load_dwordx2 v[214:215], v190, s[46:47] offset:-4096
	global_load_dwordx2 v[216:217], v190, s[46:47]
	v_add_u32_e32 v190, 0x2000, v190
	global_load_dwordx2 v[218:219], v190, s[46:47] offset:-4096
	global_load_dwordx2 v[220:221], v190, s[46:47]
	v_add_u32_e32 v190, 0x2000, v190
	global_load_dwordx2 v[222:223], v190, s[46:47] offset:-4096
	global_load_dwordx2 v[224:225], v190, s[46:47]
	v_add_u32_e32 v190, 0x2000, v190
	global_load_dwordx2 v[226:227], v190, s[46:47] offset:-4096
	global_load_dwordx2 v[228:229], v190, s[46:47]
	v_add_u32_e32 v190, 0x2000, v190
	global_load_dwordx2 v[230:231], v190, s[46:47] offset:-4096
	global_load_dwordx2 v[232:233], v190, s[46:47]
	v_mov_b32_e32 v50, v165
	v_lshlrev_b32_e32 v13, 3, v17
	v_lshlrev_b32_e32 v48, 3, v10
	v_add3_u32 v10, 0, v13, v48
	v_xor_b32_e32 v13, 1, v17
	v_xor_b32_e32 v34, 8, v17
	v_xor_b32_e32 v36, 9, v17
	v_lshlrev_b32_e32 v13, 3, v13
	v_xor_b32_e32 v15, 2, v17
	v_xor_b32_e32 v24, 3, v17
	v_xor_b32_e32 v26, 4, v17
	v_xor_b32_e32 v28, 5, v17
	v_xor_b32_e32 v30, 6, v17
	v_xor_b32_e32 v32, 7, v17
	v_lshlrev_b32_e32 v34, 3, v34
	v_lshlrev_b32_e32 v36, 3, v36
	v_xor_b32_e32 v38, 10, v17
	v_xor_b32_e32 v40, 11, v17
	v_xor_b32_e32 v42, 12, v17
	v_xor_b32_e32 v44, 13, v17
	v_xor_b32_e32 v46, 14, v17
	v_xor_b32_e32 v17, 15, v17
	v_add3_u32 v13, 0, v13, v48
	v_lshlrev_b32_e32 v15, 3, v15
	v_lshlrev_b32_e32 v24, 3, v24
	v_lshlrev_b32_e32 v26, 3, v26
	v_lshlrev_b32_e32 v28, 3, v28
	v_lshlrev_b32_e32 v30, 3, v30
	v_lshlrev_b32_e32 v32, 3, v32
	v_add3_u32 v57, 0, v34, v48
	v_add3_u32 v58, 0, v36, v48
	v_lshlrev_b32_e32 v38, 3, v38
	v_lshlrev_b32_e32 v40, 3, v40
	v_lshlrev_b32_e32 v42, 3, v42
	v_lshlrev_b32_e32 v44, 3, v44
	v_lshlrev_b32_e32 v46, 3, v46
	v_lshlrev_b32_e32 v17, 3, v17
	ds_read_b64 v[18:19], v10
	ds_read_b64 v[20:21], v13
	v_add3_u32 v15, 0, v15, v48
	v_add3_u32 v52, 0, v24, v48
	v_add3_u32 v53, 0, v26, v48
	v_add3_u32 v54, 0, v28, v48
	v_add3_u32 v55, 0, v30, v48
	v_add3_u32 v56, 0, v32, v48
	ds_read_b64 v[34:35], v57
	ds_read_b64 v[36:37], v58
	v_add3_u32 v59, 0, v38, v48
	v_add3_u32 v60, 0, v40, v48
	v_add3_u32 v61, 0, v42, v48
	v_add3_u32 v62, 0, v44, v48
	v_add3_u32 v63, 0, v46, v48
	v_add3_u32 v64, 0, v17, v48
	v_mov_b32_e32 v17, v1
	ds_read_b64 v[22:23], v15
	ds_read_b64 v[24:25], v52
	ds_read_b64 v[26:27], v53
	ds_read_b64 v[28:29], v54
	ds_read_b64 v[30:31], v55
	ds_read_b64 v[32:33], v56
	ds_read_b64 v[38:39], v59
	ds_read_b64 v[40:41], v60
	ds_read_b64 v[42:43], v61
	ds_read_b64 v[44:45], v62
	ds_read_b64 v[46:47], v63
	ds_read_b64 v[48:49], v64
	s_waitcnt lgkmcnt(13)
	v_pk_add_f32 v[70:71], v[18:19], v[34:35]
	v_mov_b32_e32 v17, v164
	v_pk_add_f32 v[18:19], v[18:19], v[34:35] neg_lo:[0,1] neg_hi:[0,1]
	v_mov_b32_e32 v17, v166
	s_waitcnt lgkmcnt(12)
	v_pk_add_f32 v[34:35], v[20:21], v[36:37]
	v_pk_add_f32 v[20:21], v[20:21], v[36:37] neg_lo:[0,1] neg_hi:[0,1]
	v_mov_b32_e32 v66, v167
	v_mov_b32_e32 v17, v168
	v_mov_b32_e32 v68, v169
	s_nop 0
	v_pk_mul_f32 v[36:37], v[20:21], v[68:69] op_sel:[1,0] op_sel_hi:[0,0] neg_lo:[1,1] neg_hi:[0,1]
	v_mov_b32_e32 v17, v170
	v_pk_fma_f32 v[20:21], v[20:21], v[50:51], v[36:37] op_sel_hi:[1,0,1]
	s_waitcnt lgkmcnt(5)
	v_pk_add_f32 v[36:37], v[22:23], v[38:39]
	v_pk_add_f32 v[22:23], v[22:23], v[38:39] neg_lo:[0,1] neg_hi:[0,1]
	s_nop 0
	v_pk_mul_f32 v[38:39], v[22:23], v[66:67] op_sel:[1,0] op_sel_hi:[0,0] neg_lo:[1,1] neg_hi:[0,1]
	v_mov_b32_e32 v17, v171
	v_pk_fma_f32 v[22:23], v[22:23], v[66:67], v[38:39] op_sel_hi:[1,0,1]
	s_waitcnt lgkmcnt(4)
	v_pk_add_f32 v[38:39], v[24:25], v[40:41]
	v_pk_add_f32 v[24:25], v[24:25], v[40:41] neg_lo:[0,1] neg_hi:[0,1]
	s_nop 0
	v_pk_mul_f32 v[40:41], v[24:25], v[68:69] op_sel_hi:[1,0]
	s_nop 0
	v_pk_fma_f32 v[24:25], v[24:25], v[50:51], v[40:41] op_sel:[1,0,0] op_sel_hi:[0,0,1] neg_lo:[1,1,0] neg_hi:[0,1,0]
	s_waitcnt lgkmcnt(3)
	v_pk_add_f32 v[40:41], v[26:27], v[42:43]
	v_pk_add_f32 v[26:27], v[26:27], v[42:43] neg_lo:[0,1] neg_hi:[0,1]
	v_ashrrev_i32_e32 v17, 31, v16
	v_xor_b32_e32 v73, 0x80000000, v26
	v_mov_b32_e32 v72, v27
	s_waitcnt lgkmcnt(2)
	v_pk_add_f32 v[26:27], v[28:29], v[44:45]
	v_pk_add_f32 v[28:29], v[28:29], v[44:45] neg_lo:[0,1] neg_hi:[0,1]
	s_nop 0
	v_pk_mul_f32 v[42:43], v[28:29], v[68:69] op_sel_hi:[1,0] neg_lo:[0,1] neg_hi:[0,1]
	s_nop 0
	v_pk_fma_f32 v[28:29], v[28:29], v[50:51], v[42:43] op_sel:[1,0,0] op_sel_hi:[0,0,1] neg_lo:[1,1,0] neg_hi:[0,1,0]
	s_waitcnt lgkmcnt(1)
	v_pk_add_f32 v[42:43], v[30:31], v[46:47]
	v_pk_add_f32 v[30:31], v[30:31], v[46:47] neg_lo:[0,1] neg_hi:[0,1]
	s_nop 0
	v_pk_mul_f32 v[44:45], v[30:31], v[66:67] op_sel:[1,0] op_sel_hi:[0,0] neg_lo:[1,1] neg_hi:[0,1]
	s_nop 0
	v_pk_fma_f32 v[30:31], v[30:31], v[66:67], v[44:45] op_sel_hi:[1,0,1] neg_lo:[0,1,0] neg_hi:[0,1,0]
	s_waitcnt lgkmcnt(0)
	v_pk_add_f32 v[44:45], v[32:33], v[48:49]
	v_pk_add_f32 v[32:33], v[32:33], v[48:49] neg_lo:[0,1] neg_hi:[0,1]
	v_pk_add_f32 v[48:49], v[34:35], v[26:27]
	v_pk_add_f32 v[26:27], v[34:35], v[26:27] neg_lo:[0,1] neg_hi:[0,1]
	s_nop 0
	v_pk_mul_f32 v[34:35], v[26:27], v[66:67] op_sel:[1,0] op_sel_hi:[0,0] neg_lo:[1,1] neg_hi:[0,1]
	v_pk_fma_f32 v[26:27], v[26:27], v[66:67], v[34:35] op_sel_hi:[1,0,1]
	v_pk_add_f32 v[34:35], v[36:37], v[42:43]
	v_pk_add_f32 v[36:37], v[36:37], v[42:43] neg_lo:[0,1] neg_hi:[0,1]
	v_pk_mul_f32 v[46:47], v[32:33], v[68:69] op_sel:[1,0] op_sel_hi:[0,0] neg_lo:[1,1] neg_hi:[0,1]
	v_xor_b32_e32 v43, 0x80000000, v36
	v_mov_b32_e32 v42, v37
	v_pk_add_f32 v[36:37], v[38:39], v[44:45]
	v_pk_add_f32 v[38:39], v[38:39], v[44:45] neg_lo:[0,1] neg_hi:[0,1]
	v_pk_fma_f32 v[46:47], v[32:33], v[50:51], v[46:47] op_sel_hi:[1,0,1] neg_lo:[0,1,0] neg_hi:[0,1,0]
	v_pk_add_f32 v[32:33], v[70:71], v[40:41]
	v_pk_mul_f32 v[44:45], v[38:39], v[66:67] op_sel:[1,0] op_sel_hi:[0,0] neg_lo:[1,1] neg_hi:[0,1]
	v_pk_add_f32 v[40:41], v[70:71], v[40:41] neg_lo:[0,1] neg_hi:[0,1]
	v_pk_fma_f32 v[38:39], v[38:39], v[66:67], v[44:45] op_sel_hi:[1,0,1] neg_lo:[0,1,0] neg_hi:[0,1,0]
	v_pk_add_f32 v[44:45], v[32:33], v[34:35]
	v_pk_add_f32 v[32:33], v[32:33], v[34:35] neg_lo:[0,1] neg_hi:[0,1]
	v_pk_add_f32 v[34:35], v[48:49], v[36:37]
	v_pk_add_f32 v[36:37], v[48:49], v[36:37] neg_lo:[0,1] neg_hi:[0,1]
	v_pk_add_f32 v[50:51], v[44:45], v[34:35]
	v_xor_b32_e32 v49, 0x80000000, v36
	v_mov_b32_e32 v48, v37
	v_pk_add_f32 v[36:37], v[44:45], v[34:35] neg_lo:[0,1] neg_hi:[0,1]
	v_pk_add_f32 v[68:69], v[32:33], v[48:49]
	v_pk_add_f32 v[44:45], v[32:33], v[48:49] neg_lo:[0,1] neg_hi:[0,1]
	v_pk_add_f32 v[32:33], v[40:41], v[42:43]
	v_pk_add_f32 v[34:35], v[40:41], v[42:43] neg_lo:[0,1] neg_hi:[0,1]
	v_pk_add_f32 v[40:41], v[26:27], v[38:39]
	v_pk_add_f32 v[26:27], v[26:27], v[38:39] neg_lo:[0,1] neg_hi:[0,1]
	v_pk_add_f32 v[42:43], v[32:33], v[40:41] neg_lo:[0,1] neg_hi:[0,1]
	v_xor_b32_e32 v39, 0x80000000, v26
	v_mov_b32_e32 v38, v27
	v_pk_add_f32 v[26:27], v[32:33], v[40:41]
	v_pk_add_f32 v[40:41], v[20:21], v[28:29]
	v_pk_add_f32 v[20:21], v[20:21], v[28:29] neg_lo:[0,1] neg_hi:[0,1]
	v_pk_add_f32 v[32:33], v[34:35], v[38:39]
	v_pk_mul_f32 v[28:29], v[66:67], v[20:21] op_sel:[0,1] op_sel_hi:[0,0] neg_lo:[1,1] neg_hi:[1,0]
	v_pk_fma_f32 v[20:21], v[66:67], v[20:21], v[28:29] op_sel_hi:[0,1,1]
	v_pk_add_f32 v[28:29], v[22:23], v[30:31]
	v_pk_add_f32 v[22:23], v[22:23], v[30:31] neg_lo:[0,1] neg_hi:[0,1]
	v_pk_add_f32 v[38:39], v[34:35], v[38:39] neg_lo:[0,1] neg_hi:[0,1]
	v_xor_b32_e32 v31, 0x80000000, v22
	v_mov_b32_e32 v30, v23
	v_pk_add_f32 v[22:23], v[24:25], v[46:47]
	v_pk_add_f32 v[24:25], v[24:25], v[46:47] neg_lo:[0,1] neg_hi:[0,1]
	v_pk_add_f32 v[34:35], v[18:19], v[72:73]
	v_pk_mul_f32 v[46:47], v[66:67], v[24:25] op_sel:[0,1] op_sel_hi:[0,0] neg_lo:[1,1] neg_hi:[1,0]
	v_pk_fma_f32 v[24:25], v[66:67], v[24:25], v[46:47] op_sel_hi:[0,1,1] neg_lo:[1,0,0] neg_hi:[1,0,0]
	v_pk_add_f32 v[46:47], v[34:35], v[28:29]
	v_pk_add_f32 v[28:29], v[34:35], v[28:29] neg_lo:[0,1] neg_hi:[0,1]
	v_pk_add_f32 v[34:35], v[40:41], v[22:23]
	v_pk_add_f32 v[22:23], v[40:41], v[22:23] neg_lo:[0,1] neg_hi:[0,1]
	v_pk_add_f32 v[18:19], v[18:19], v[72:73] neg_lo:[0,1] neg_hi:[0,1]
	v_pk_add_f32 v[66:67], v[28:29], v[22:23] op_sel:[0,1] op_sel_hi:[1,0] neg_hi:[0,1]
	v_pk_add_f32 v[48:49], v[28:29], v[22:23] op_sel:[0,1] op_sel_hi:[1,0] neg_lo:[0,1]
	v_pk_add_f32 v[28:29], v[18:19], v[30:31]
	v_pk_add_f32 v[18:19], v[18:19], v[30:31] neg_lo:[0,1] neg_hi:[0,1]
	v_pk_add_f32 v[30:31], v[20:21], v[24:25]
	v_pk_add_f32 v[20:21], v[20:21], v[24:25] neg_lo:[0,1] neg_hi:[0,1]
	v_pk_add_f32 v[22:23], v[46:47], v[34:35]
	v_xor_b32_e32 v25, 0x80000000, v20
	v_mov_b32_e32 v24, v21
	v_lshl_add_u64 v[20:21], v[16:17], 3, s[46:47]
	s_waitcnt vmcnt(0)
	v_pk_add_f32 v[40:41], v[46:47], v[34:35] neg_lo:[0,1] neg_hi:[0,1]
	v_pk_add_f32 v[34:35], v[18:19], v[24:25]
	v_pk_add_f32 v[18:19], v[18:19], v[24:25] neg_lo:[0,1] neg_hi:[0,1]
	v_pk_add_f32 v[70:71], v[28:29], v[30:31]
	v_pk_add_f32 v[46:47], v[28:29], v[30:31] neg_lo:[0,1] neg_hi:[0,1]
	v_mov_b32_e32 v17, v1
	s_nop 0
	v_pk_mul_f32 v[24:25], v[50:51], v[202:203] op_sel:[1,1] op_sel_hi:[1,0] neg_lo:[1,0]
	s_nop 0
	v_pk_fma_f32 v[20:21], v[50:51], v[202:203], v[24:25] op_sel_hi:[0,1,1]
	v_add_u32_e32 v24, 0x200, v16
	v_ashrrev_i32_e32 v25, 31, v24
	v_lshl_add_u64 v[24:25], v[24:25], 3, s[46:47]
	s_nop 0
	v_pk_mul_f32 v[28:29], v[204:205], v[22:23] op_sel:[1,1] op_sel_hi:[0,1] neg_lo:[0,1]
	v_pk_fma_f32 v[22:23], v[204:205], v[22:23], v[28:29] op_sel_hi:[1,0,1]
	v_add_u32_e32 v24, 0x400, v16
	v_ashrrev_i32_e32 v25, 31, v24
	v_lshl_add_u64 v[24:25], v[24:25], 3, s[46:47]
	s_nop 0
	v_pk_mul_f32 v[28:29], v[26:27], v[206:207] op_sel:[1,1] op_sel_hi:[1,0] neg_lo:[1,0]
	s_nop 0
	v_pk_fma_f32 v[24:25], v[26:27], v[206:207], v[28:29] op_sel_hi:[0,1,1]
	v_add_u32_e32 v26, 0x600, v16
	v_ashrrev_i32_e32 v27, 31, v26
	v_lshl_add_u64 v[26:27], v[26:27], 3, s[46:47]
	s_nop 0
	v_pk_mul_f32 v[28:29], v[208:209], v[70:71] op_sel:[1,1] op_sel_hi:[0,1] neg_lo:[0,1]
	v_pk_fma_f32 v[26:27], v[208:209], v[70:71], v[28:29] op_sel_hi:[1,0,1]
	v_add_u32_e32 v28, 0x800, v16
	v_ashrrev_i32_e32 v29, 31, v28
	v_lshl_add_u64 v[28:29], v[28:29], 3, s[46:47]
	s_nop 0
	v_pk_mul_f32 v[30:31], v[68:69], v[210:211] op_sel:[1,1] op_sel_hi:[1,0] neg_lo:[1,0]
	s_nop 0
	v_pk_fma_f32 v[28:29], v[68:69], v[210:211], v[30:31] op_sel_hi:[0,1,1]
	v_add_u32_e32 v30, 0xa00, v16
	v_ashrrev_i32_e32 v31, 31, v30
	v_lshl_add_u64 v[30:31], v[30:31], 3, s[46:47]
	v_mov_b32_e32 v68, v169
	s_nop 0
	v_pk_mul_f32 v[50:51], v[212:213], v[66:67] op_sel:[1,1] op_sel_hi:[0,1] neg_lo:[0,1]
	v_pk_fma_f32 v[30:31], v[212:213], v[66:67], v[50:51] op_sel_hi:[1,0,1]
	v_add_u32_e32 v50, 0xc00, v16
	v_ashrrev_i32_e32 v51, 31, v50
	v_lshl_add_u64 v[50:51], v[50:51], 3, s[46:47]
	s_nop 0
	v_pk_mul_f32 v[66:67], v[32:33], v[214:215] op_sel:[1,1] op_sel_hi:[1,0] neg_lo:[1,0]
	s_nop 0
	v_pk_fma_f32 v[32:33], v[32:33], v[214:215], v[66:67] op_sel_hi:[0,1,1]
	v_add_u32_e32 v50, 0xe00, v16
	v_ashrrev_i32_e32 v51, 31, v50
	v_lshl_add_u64 v[50:51], v[50:51], 3, s[46:47]
	s_nop 0
	v_pk_mul_f32 v[66:67], v[216:217], v[34:35] op_sel:[1,1] op_sel_hi:[0,1] neg_lo:[0,1]
	v_pk_fma_f32 v[34:35], v[216:217], v[34:35], v[66:67] op_sel_hi:[1,0,1]
	v_add_u32_e32 v50, 0x1000, v16
	v_ashrrev_i32_e32 v51, 31, v50
	v_lshl_add_u64 v[50:51], v[50:51], 3, s[46:47]
	s_nop 0
	v_pk_mul_f32 v[66:67], v[36:37], v[218:219] op_sel:[1,1] op_sel_hi:[1,0] neg_lo:[1,0]
	s_nop 0
	v_pk_fma_f32 v[36:37], v[36:37], v[218:219], v[66:67] op_sel_hi:[0,1,1]
	v_add_u32_e32 v50, 0x1200, v16
	v_ashrrev_i32_e32 v51, 31, v50
	v_lshl_add_u64 v[50:51], v[50:51], 3, s[46:47]
	v_pk_add_f32 v[70:71], v[20:21], v[36:37]
	v_pk_add_f32 v[20:21], v[20:21], v[36:37] neg_lo:[0,1] neg_hi:[0,1]
	s_nop 0
	v_pk_mul_f32 v[66:67], v[40:41], v[220:221] op_sel:[1,1] op_sel_hi:[1,0] neg_lo:[1,0]
	s_nop 0
	v_pk_fma_f32 v[40:41], v[40:41], v[220:221], v[66:67] op_sel_hi:[0,1,1]
	v_add_u32_e32 v50, 0x1400, v16
	v_ashrrev_i32_e32 v51, 31, v50
	v_lshl_add_u64 v[50:51], v[50:51], 3, s[46:47]
	v_pk_add_f32 v[36:37], v[22:23], v[40:41]
	v_pk_add_f32 v[22:23], v[22:23], v[40:41] neg_lo:[0,1] neg_hi:[0,1]
	s_nop 0
	v_pk_mul_f32 v[66:67], v[42:43], v[222:223] op_sel:[1,1] op_sel_hi:[1,0] neg_lo:[1,0]
	s_nop 0
	v_pk_fma_f32 v[42:43], v[42:43], v[222:223], v[66:67] op_sel_hi:[0,1,1]
	v_add_u32_e32 v50, 0x1600, v16
	v_ashrrev_i32_e32 v51, 31, v50
	v_lshl_add_u64 v[50:51], v[50:51], 3, s[46:47]
	s_nop 0
	v_pk_mul_f32 v[66:67], v[46:47], v[224:225] op_sel:[1,1] op_sel_hi:[1,0] neg_lo:[1,0]
	s_nop 0
	v_pk_fma_f32 v[46:47], v[46:47], v[224:225], v[66:67] op_sel_hi:[0,1,1]
	v_add_u32_e32 v50, 0x1800, v16
	v_ashrrev_i32_e32 v51, 31, v50
	v_lshl_add_u64 v[50:51], v[50:51], 3, s[46:47]
	s_nop 0
	v_pk_mul_f32 v[66:67], v[44:45], v[226:227] op_sel:[1,1] op_sel_hi:[1,0] neg_lo:[1,0]
	s_nop 0
	v_pk_fma_f32 v[44:45], v[44:45], v[226:227], v[66:67] op_sel_hi:[0,1,1]
	v_add_u32_e32 v50, 0x1a00, v16
	v_ashrrev_i32_e32 v51, 31, v50
	v_lshl_add_u64 v[50:51], v[50:51], 3, s[46:47]
	s_nop 0
	v_pk_mul_f32 v[66:67], v[48:49], v[228:229] op_sel:[1,1] op_sel_hi:[1,0] neg_lo:[1,0]
	s_nop 0
	v_pk_fma_f32 v[48:49], v[48:49], v[228:229], v[66:67] op_sel_hi:[0,1,1]
	v_add_u32_e32 v50, 0x1c00, v16
	v_ashrrev_i32_e32 v51, 31, v50
	v_lshl_add_u64 v[50:51], v[50:51], 3, s[46:47]
	s_nop 0
	v_pk_mul_f32 v[66:67], v[38:39], v[230:231] op_sel:[1,1] op_sel_hi:[1,0] neg_lo:[1,0]
	s_nop 0
	v_pk_fma_f32 v[38:39], v[38:39], v[230:231], v[66:67] op_sel_hi:[0,1,1]
	v_add_u32_e32 v50, 0x1e00, v16
	v_ashrrev_i32_e32 v51, 31, v50
	v_lshl_add_u64 v[50:51], v[50:51], 3, s[46:47]
	v_mov_b32_e32 v50, v232
	v_mov_b32_e32 v51, v233
	v_lshlrev_b32_e32 v190, 3, v16
	v_add_u32_e32 v190, 0x11000, v190
	global_load_dwordx2 v[202:203], v190, s[46:47] offset:-4096
	global_load_dwordx2 v[204:205], v190, s[46:47]
	v_add_u32_e32 v190, 0x2000, v190
	global_load_dwordx2 v[206:207], v190, s[46:47] offset:-4096
	global_load_dwordx2 v[208:209], v190, s[46:47]
	v_add_u32_e32 v190, 0x2000, v190
	global_load_dwordx2 v[210:211], v190, s[46:47] offset:-4096
	global_load_dwordx2 v[212:213], v190, s[46:47]
	v_add_u32_e32 v190, 0x2000, v190
	global_load_dwordx2 v[214:215], v190, s[46:47] offset:-4096
	global_load_dwordx2 v[216:217], v190, s[46:47]
	v_add_u32_e32 v190, 0x2000, v190
	global_load_dwordx2 v[218:219], v190, s[46:47] offset:-4096
	global_load_dwordx2 v[220:221], v190, s[46:47]
	v_add_u32_e32 v190, 0x2000, v190
	global_load_dwordx2 v[222:223], v190, s[46:47] offset:-4096
	global_load_dwordx2 v[224:225], v190, s[46:47]
	v_add_u32_e32 v190, 0x2000, v190
	global_load_dwordx2 v[226:227], v190, s[46:47] offset:-4096
	global_load_dwordx2 v[228:229], v190, s[46:47]
	v_add_u32_e32 v190, 0x2000, v190
	global_load_dwordx2 v[230:231], v190, s[46:47] offset:-4096
	global_load_dwordx2 v[232:233], v190, s[46:47]
	v_mov_b32_e32 v17, v164
	s_nop 0
	v_pk_mul_f32 v[66:67], v[18:19], v[50:51] op_sel:[1,1] op_sel_hi:[1,0] neg_lo:[1,0]
	s_nop 0
	v_pk_fma_f32 v[18:19], v[18:19], v[50:51], v[66:67] op_sel_hi:[0,1,1]
	v_mov_b32_e32 v50, v165
	v_mov_b32_e32 v17, v166
	v_mov_b32_e32 v66, v167
	v_mov_b32_e32 v17, v168
	s_nop 0
	v_pk_mul_f32 v[40:41], v[22:23], v[68:69] op_sel:[1,0] op_sel_hi:[0,0] neg_lo:[1,0]
	v_mov_b32_e32 v17, v170
	v_pk_fma_f32 v[22:23], v[22:23], v[50:51], v[40:41] op_sel_hi:[1,0,1]
	v_pk_add_f32 v[40:41], v[24:25], v[42:43]
	v_pk_add_f32 v[24:25], v[24:25], v[42:43] neg_lo:[0,1] neg_hi:[0,1]
	s_nop 0
	v_pk_mul_f32 v[42:43], v[24:25], v[66:67] op_sel:[1,0] op_sel_hi:[0,0] neg_lo:[1,0]
	v_mov_b32_e32 v17, v171
	v_pk_fma_f32 v[24:25], v[24:25], v[66:67], v[42:43] op_sel_hi:[1,0,1]
	v_pk_add_f32 v[42:43], v[26:27], v[46:47]
	v_pk_add_f32 v[26:27], v[26:27], v[46:47] neg_lo:[0,1] neg_hi:[0,1]
	s_nop 0
	v_pk_mul_f32 v[46:47], v[26:27], v[68:69] op_sel_hi:[1,0]
	s_nop 0
	v_pk_fma_f32 v[26:27], v[26:27], v[50:51], v[46:47] op_sel:[1,0,0] op_sel_hi:[0,0,1] neg_lo:[1,0,0]
	v_pk_add_f32 v[46:47], v[28:29], v[44:45]
	v_pk_add_f32 v[28:29], v[28:29], v[44:45] neg_lo:[0,1] neg_hi:[0,1]
	v_mov_b32_e32 v17, v175
	v_xor_b32_e32 v44, 0x80000000, v29
	v_mov_b32_e32 v45, v28
	v_pk_add_f32 v[28:29], v[30:31], v[48:49]
	v_pk_add_f32 v[30:31], v[30:31], v[48:49] neg_lo:[0,1] neg_hi:[0,1]
	s_nop 0
	v_pk_mul_f32 v[48:49], v[30:31], v[68:69] op_sel_hi:[1,0] neg_lo:[0,1] neg_hi:[0,1]
	s_nop 0
	v_pk_fma_f32 v[30:31], v[30:31], v[50:51], v[48:49] op_sel:[1,0,0] op_sel_hi:[0,0,1] neg_lo:[1,0,0]
	v_pk_add_f32 v[48:49], v[32:33], v[38:39]
	v_pk_add_f32 v[32:33], v[32:33], v[38:39] neg_lo:[0,1] neg_hi:[0,1]
	s_nop 0
	v_pk_mul_f32 v[38:39], v[32:33], v[66:67] op_sel:[1,0] op_sel_hi:[0,0] neg_lo:[1,0]
	s_nop 0
	v_pk_fma_f32 v[32:33], v[32:33], v[66:67], v[38:39] op_sel_hi:[1,0,1] neg_lo:[0,1,0] neg_hi:[0,1,0]
	v_pk_add_f32 v[38:39], v[34:35], v[18:19]
	v_pk_add_f32 v[18:19], v[34:35], v[18:19] neg_lo:[0,1] neg_hi:[0,1]
	s_nop 0
	v_pk_mul_f32 v[34:35], v[18:19], v[68:69] op_sel:[1,0] op_sel_hi:[0,0] neg_lo:[1,0]
	v_mov_b32_e32 v68, v169
	v_pk_fma_f32 v[18:19], v[18:19], v[50:51], v[34:35] op_sel_hi:[1,0,1] neg_lo:[0,1,0] neg_hi:[0,1,0]
	v_pk_add_f32 v[50:51], v[36:37], v[28:29]
	v_pk_add_f32 v[28:29], v[36:37], v[28:29] neg_lo:[0,1] neg_hi:[0,1]
	v_pk_add_f32 v[34:35], v[70:71], v[46:47]
	v_pk_mul_f32 v[36:37], v[28:29], v[66:67] op_sel:[1,0] op_sel_hi:[0,0] neg_lo:[1,0]
	v_pk_add_f32 v[46:47], v[70:71], v[46:47] neg_lo:[0,1] neg_hi:[0,1]
	v_pk_fma_f32 v[28:29], v[28:29], v[66:67], v[36:37] op_sel_hi:[1,0,1]
	v_pk_add_f32 v[36:37], v[40:41], v[48:49]
	v_pk_add_f32 v[40:41], v[40:41], v[48:49] neg_lo:[0,1] neg_hi:[0,1]
	s_nop 0
	v_xor_b32_e32 v48, 0x80000000, v41
	v_mov_b32_e32 v49, v40
	v_pk_add_f32 v[40:41], v[42:43], v[38:39]
	v_pk_add_f32 v[38:39], v[42:43], v[38:39] neg_lo:[0,1] neg_hi:[0,1]
	s_nop 0
	v_pk_mul_f32 v[42:43], v[66:67], v[38:39] op_sel:[0,1] op_sel_hi:[0,0] neg_lo:[0,1]
	v_pk_fma_f32 v[38:39], v[38:39], v[66:67], v[42:43] op_sel_hi:[1,0,1] neg_lo:[0,1,0] neg_hi:[0,1,0]
	v_pk_add_f32 v[42:43], v[34:35], v[36:37]
	v_pk_add_f32 v[34:35], v[34:35], v[36:37] neg_lo:[0,1] neg_hi:[0,1]
	v_pk_add_f32 v[36:37], v[50:51], v[40:41]
	v_pk_add_f32 v[40:41], v[50:51], v[40:41] neg_lo:[0,1] neg_hi:[0,1]
	s_nop 0
	v_xor_b32_e32 v50, 0x80000000, v41
	v_mov_b32_e32 v51, v40
	v_pk_add_f32 v[40:41], v[42:43], v[36:37]
	v_pk_add_f32 v[36:37], v[42:43], v[36:37] neg_lo:[0,1] neg_hi:[0,1]
	v_pk_add_f32 v[42:43], v[34:35], v[50:51]
	v_pk_add_f32 v[34:35], v[34:35], v[50:51] neg_lo:[0,1] neg_hi:[0,1]
	v_pk_add_f32 v[50:51], v[46:47], v[48:49]
	v_pk_add_f32 v[46:47], v[46:47], v[48:49] neg_lo:[0,1] neg_hi:[0,1]
	v_pk_add_f32 v[48:49], v[28:29], v[38:39]
	v_pk_add_f32 v[28:29], v[28:29], v[38:39] neg_lo:[0,1] neg_hi:[0,1]
	s_nop 0
	v_xor_b32_e32 v38, 0x80000000, v29
	v_mov_b32_e32 v39, v28
	v_pk_add_f32 v[28:29], v[50:51], v[48:49]
	v_pk_add_f32 v[48:49], v[50:51], v[48:49] neg_lo:[0,1] neg_hi:[0,1]
	v_pk_add_f32 v[50:51], v[46:47], v[38:39]
	v_pk_add_f32 v[38:39], v[46:47], v[38:39] neg_lo:[0,1] neg_hi:[0,1]
	v_pk_add_f32 v[46:47], v[20:21], v[44:45]
	v_pk_add_f32 v[20:21], v[20:21], v[44:45] neg_lo:[0,1] neg_hi:[0,1]
	v_pk_add_f32 v[44:45], v[22:23], v[30:31]
	v_pk_add_f32 v[22:23], v[22:23], v[30:31] neg_lo:[0,1] neg_hi:[0,1]
	s_nop 0
	v_pk_mul_f32 v[30:31], v[66:67], v[22:23] op_sel:[0,1] op_sel_hi:[0,0] neg_lo:[0,1]
	v_pk_fma_f32 v[22:23], v[66:67], v[22:23], v[30:31] op_sel_hi:[0,1,1]
	v_pk_add_f32 v[30:31], v[24:25], v[32:33]
	v_pk_add_f32 v[24:25], v[24:25], v[32:33] neg_lo:[0,1] neg_hi:[0,1]
	s_nop 0
	v_xor_b32_e32 v32, 0x80000000, v25
	v_mov_b32_e32 v33, v24
	v_pk_add_f32 v[24:25], v[26:27], v[18:19]
	v_pk_add_f32 v[18:19], v[26:27], v[18:19] neg_lo:[0,1] neg_hi:[0,1]
	s_nop 0
	v_pk_mul_f32 v[26:27], v[66:67], v[18:19] op_sel:[0,1] op_sel_hi:[0,0] neg_lo:[0,1]
	v_pk_fma_f32 v[18:19], v[66:67], v[18:19], v[26:27] op_sel_hi:[0,1,1] neg_lo:[1,0,0] neg_hi:[1,0,0]
	v_pk_add_f32 v[26:27], v[46:47], v[30:31]
	v_pk_add_f32 v[30:31], v[46:47], v[30:31] neg_lo:[0,1] neg_hi:[0,1]
	v_pk_add_f32 v[46:47], v[44:45], v[24:25]
	v_pk_add_f32 v[24:25], v[44:45], v[24:25] neg_lo:[0,1] neg_hi:[0,1]
	v_mov_b32_e32 v66, v167
	v_xor_b32_e32 v44, 0x80000000, v25
	v_mov_b32_e32 v45, v24
	v_pk_add_f32 v[24:25], v[26:27], v[46:47]
	v_pk_add_f32 v[26:27], v[26:27], v[46:47] neg_lo:[0,1] neg_hi:[0,1]
	v_pk_add_f32 v[46:47], v[30:31], v[44:45]
	v_pk_add_f32 v[30:31], v[30:31], v[44:45] neg_lo:[0,1] neg_hi:[0,1]
	v_pk_add_f32 v[44:45], v[20:21], v[32:33]
	v_pk_add_f32 v[20:21], v[20:21], v[32:33] neg_lo:[0,1] neg_hi:[0,1]
	v_pk_add_f32 v[32:33], v[22:23], v[18:19]
	v_pk_add_f32 v[18:19], v[22:23], v[18:19] neg_lo:[0,1] neg_hi:[0,1]
	s_nop 0
	v_xor_b32_e32 v22, 0x80000000, v19
	v_mov_b32_e32 v23, v18
	v_pk_add_f32 v[18:19], v[44:45], v[32:33]
	v_pk_add_f32 v[32:33], v[44:45], v[32:33] neg_lo:[0,1] neg_hi:[0,1]
	v_pk_add_f32 v[44:45], v[20:21], v[22:23]
	v_pk_add_f32 v[20:21], v[20:21], v[22:23] neg_lo:[0,1] neg_hi:[0,1]
	ds_write_b64 v10, v[40:41]
	ds_write_b64 v13, v[24:25]
	ds_write_b64 v15, v[28:29]
	ds_write_b64 v52, v[18:19]
	ds_write_b64 v53, v[42:43]
	ds_write_b64 v54, v[46:47]
	ds_write_b64 v55, v[50:51]
	ds_write_b64 v56, v[44:45]
	ds_write_b64 v57, v[36:37]
	ds_write_b64 v58, v[26:27]
	ds_write_b64 v59, v[48:49]
	ds_write_b64 v60, v[32:33]
	ds_write_b64 v61, v[34:35]
	ds_write_b64 v62, v[30:31]
	ds_write_b64 v63, v[38:39]
	ds_write_b64 v64, v[20:21]
	v_mov_b32_e32 v10, v177
	v_mov_b32_e32 v64, v165
	v_lshlrev_b32_e32 v13, 3, v17
	v_lshlrev_b32_e32 v48, 3, v10
	v_add3_u32 v10, 0, v13, v48
	v_xor_b32_e32 v13, 1, v17
	v_xor_b32_e32 v34, 8, v17
	v_xor_b32_e32 v36, 9, v17
	v_lshlrev_b32_e32 v13, 3, v13
	v_xor_b32_e32 v15, 2, v17
	v_xor_b32_e32 v24, 3, v17
	v_xor_b32_e32 v26, 4, v17
	v_xor_b32_e32 v28, 5, v17
	v_xor_b32_e32 v30, 6, v17
	v_xor_b32_e32 v32, 7, v17
	v_lshlrev_b32_e32 v34, 3, v34
	v_lshlrev_b32_e32 v36, 3, v36
	v_xor_b32_e32 v38, 10, v17
	v_xor_b32_e32 v40, 11, v17
	v_xor_b32_e32 v42, 12, v17
	v_xor_b32_e32 v44, 13, v17
	v_xor_b32_e32 v46, 14, v17
	v_xor_b32_e32 v17, 15, v17
	v_add3_u32 v13, 0, v13, v48
	v_lshlrev_b32_e32 v15, 3, v15
	v_lshlrev_b32_e32 v24, 3, v24
	v_lshlrev_b32_e32 v26, 3, v26
	v_lshlrev_b32_e32 v28, 3, v28
	v_lshlrev_b32_e32 v30, 3, v30
	v_lshlrev_b32_e32 v32, 3, v32
	v_add3_u32 v55, 0, v34, v48
	v_add3_u32 v56, 0, v36, v48
	v_lshlrev_b32_e32 v38, 3, v38
	v_lshlrev_b32_e32 v40, 3, v40
	v_lshlrev_b32_e32 v42, 3, v42
	v_lshlrev_b32_e32 v44, 3, v44
	v_lshlrev_b32_e32 v46, 3, v46
	v_lshlrev_b32_e32 v17, 3, v17
	ds_read_b64 v[18:19], v10
	ds_read_b64 v[20:21], v13
	v_add3_u32 v15, 0, v15, v48
	v_add3_u32 v50, 0, v24, v48
	v_add3_u32 v51, 0, v26, v48
	v_add3_u32 v52, 0, v28, v48
	v_add3_u32 v53, 0, v30, v48
	v_add3_u32 v54, 0, v32, v48
	ds_read_b64 v[34:35], v55
	ds_read_b64 v[36:37], v56
	v_add3_u32 v57, 0, v38, v48
	v_add3_u32 v58, 0, v40, v48
	v_add3_u32 v59, 0, v42, v48
	v_add3_u32 v60, 0, v44, v48
	v_add3_u32 v61, 0, v46, v48
	v_add3_u32 v62, 0, v17, v48
	v_mov_b32_e32 v17, v1
	ds_read_b64 v[22:23], v15
	ds_read_b64 v[24:25], v50
	ds_read_b64 v[26:27], v51
	ds_read_b64 v[28:29], v52
	ds_read_b64 v[30:31], v53
	ds_read_b64 v[32:33], v54
	ds_read_b64 v[38:39], v57
	ds_read_b64 v[40:41], v58
	ds_read_b64 v[42:43], v59
	ds_read_b64 v[44:45], v60
	ds_read_b64 v[46:47], v61
	ds_read_b64 v[48:49], v62
	s_waitcnt lgkmcnt(13)
	v_pk_add_f32 v[70:71], v[18:19], v[34:35]
	v_mov_b32_e32 v17, v164
	v_pk_add_f32 v[18:19], v[18:19], v[34:35] neg_lo:[0,1] neg_hi:[0,1]
	v_mov_b32_e32 v17, v166
	s_waitcnt lgkmcnt(12)
	v_pk_add_f32 v[34:35], v[20:21], v[36:37]
	v_pk_add_f32 v[20:21], v[20:21], v[36:37] neg_lo:[0,1] neg_hi:[0,1]
	v_mov_b32_e32 v17, v168
	s_nop 0
	v_pk_mul_f32 v[36:37], v[20:21], v[68:69] op_sel:[1,0] op_sel_hi:[0,0] neg_lo:[1,1] neg_hi:[0,1]
	v_mov_b32_e32 v17, v170
	v_pk_fma_f32 v[20:21], v[20:21], v[64:65], v[36:37] op_sel_hi:[1,0,1]
	s_waitcnt lgkmcnt(5)
	v_pk_add_f32 v[36:37], v[22:23], v[38:39]
	v_pk_add_f32 v[22:23], v[22:23], v[38:39] neg_lo:[0,1] neg_hi:[0,1]
	s_nop 0
	v_pk_mul_f32 v[38:39], v[22:23], v[66:67] op_sel:[1,0] op_sel_hi:[0,0] neg_lo:[1,1] neg_hi:[0,1]
	v_mov_b32_e32 v17, v171
	v_pk_fma_f32 v[22:23], v[22:23], v[66:67], v[38:39] op_sel_hi:[1,0,1]
	s_waitcnt lgkmcnt(4)
	v_pk_add_f32 v[38:39], v[24:25], v[40:41]
	v_pk_add_f32 v[24:25], v[24:25], v[40:41] neg_lo:[0,1] neg_hi:[0,1]
	s_nop 0
	v_pk_mul_f32 v[40:41], v[24:25], v[68:69] op_sel_hi:[1,0]
	s_nop 0
	v_pk_fma_f32 v[24:25], v[24:25], v[64:65], v[40:41] op_sel:[1,0,0] op_sel_hi:[0,0,1] neg_lo:[1,1,0] neg_hi:[0,1,0]
	s_waitcnt lgkmcnt(3)
	v_pk_add_f32 v[40:41], v[26:27], v[42:43]
	v_pk_add_f32 v[26:27], v[26:27], v[42:43] neg_lo:[0,1] neg_hi:[0,1]
	s_nop 0
	v_xor_b32_e32 v73, 0x80000000, v26
	v_mov_b32_e32 v72, v27
	s_waitcnt lgkmcnt(2)
	v_pk_add_f32 v[26:27], v[28:29], v[44:45]
	v_pk_add_f32 v[28:29], v[28:29], v[44:45] neg_lo:[0,1] neg_hi:[0,1]
	s_nop 0
	v_pk_mul_f32 v[42:43], v[28:29], v[68:69] op_sel_hi:[1,0] neg_lo:[0,1] neg_hi:[0,1]
	s_nop 0
	v_pk_fma_f32 v[28:29], v[28:29], v[64:65], v[42:43] op_sel:[1,0,0] op_sel_hi:[0,0,1] neg_lo:[1,1,0] neg_hi:[0,1,0]
	s_waitcnt lgkmcnt(1)
	v_pk_add_f32 v[42:43], v[30:31], v[46:47]
	v_pk_add_f32 v[30:31], v[30:31], v[46:47] neg_lo:[0,1] neg_hi:[0,1]
	s_nop 0
	v_pk_mul_f32 v[44:45], v[30:31], v[66:67] op_sel:[1,0] op_sel_hi:[0,0] neg_lo:[1,1] neg_hi:[0,1]
	s_nop 0
	v_pk_fma_f32 v[30:31], v[30:31], v[66:67], v[44:45] op_sel_hi:[1,0,1] neg_lo:[0,1,0] neg_hi:[0,1,0]
	s_waitcnt lgkmcnt(0)
	v_pk_add_f32 v[44:45], v[32:33], v[48:49]
	v_pk_add_f32 v[32:33], v[32:33], v[48:49] neg_lo:[0,1] neg_hi:[0,1]
	v_pk_add_f32 v[48:49], v[34:35], v[26:27]
	v_pk_add_f32 v[26:27], v[34:35], v[26:27] neg_lo:[0,1] neg_hi:[0,1]
	s_nop 0
	v_pk_mul_f32 v[34:35], v[26:27], v[66:67] op_sel:[1,0] op_sel_hi:[0,0] neg_lo:[1,1] neg_hi:[0,1]
	v_pk_fma_f32 v[26:27], v[26:27], v[66:67], v[34:35] op_sel_hi:[1,0,1]
	v_pk_add_f32 v[34:35], v[36:37], v[42:43]
	v_pk_add_f32 v[36:37], v[36:37], v[42:43] neg_lo:[0,1] neg_hi:[0,1]
	v_pk_mul_f32 v[46:47], v[32:33], v[68:69] op_sel:[1,0] op_sel_hi:[0,0] neg_lo:[1,1] neg_hi:[0,1]
	v_xor_b32_e32 v43, 0x80000000, v36
	v_mov_b32_e32 v42, v37
	v_pk_add_f32 v[36:37], v[38:39], v[44:45]
	v_pk_add_f32 v[38:39], v[38:39], v[44:45] neg_lo:[0,1] neg_hi:[0,1]
	v_pk_fma_f32 v[46:47], v[32:33], v[64:65], v[46:47] op_sel_hi:[1,0,1] neg_lo:[0,1,0] neg_hi:[0,1,0]
	v_pk_add_f32 v[32:33], v[70:71], v[40:41]
	v_pk_mul_f32 v[44:45], v[38:39], v[66:67] op_sel:[1,0] op_sel_hi:[0,0] neg_lo:[1,1] neg_hi:[0,1]
	v_pk_add_f32 v[40:41], v[70:71], v[40:41] neg_lo:[0,1] neg_hi:[0,1]
	v_pk_fma_f32 v[38:39], v[38:39], v[66:67], v[44:45] op_sel_hi:[1,0,1] neg_lo:[0,1,0] neg_hi:[0,1,0]
	v_pk_add_f32 v[44:45], v[32:33], v[34:35]
	v_pk_add_f32 v[32:33], v[32:33], v[34:35] neg_lo:[0,1] neg_hi:[0,1]
	v_pk_add_f32 v[34:35], v[48:49], v[36:37]
	v_pk_add_f32 v[36:37], v[48:49], v[36:37] neg_lo:[0,1] neg_hi:[0,1]
	v_pk_add_f32 v[64:65], v[44:45], v[34:35]
	v_xor_b32_e32 v49, 0x80000000, v36
	v_mov_b32_e32 v48, v37
	v_pk_add_f32 v[36:37], v[44:45], v[34:35] neg_lo:[0,1] neg_hi:[0,1]
	v_pk_add_f32 v[68:69], v[32:33], v[48:49]
	v_pk_add_f32 v[44:45], v[32:33], v[48:49] neg_lo:[0,1] neg_hi:[0,1]
	v_pk_add_f32 v[32:33], v[40:41], v[42:43]
	v_pk_add_f32 v[34:35], v[40:41], v[42:43] neg_lo:[0,1] neg_hi:[0,1]
	v_pk_add_f32 v[40:41], v[26:27], v[38:39]
	v_pk_add_f32 v[26:27], v[26:27], v[38:39] neg_lo:[0,1] neg_hi:[0,1]
	v_pk_add_f32 v[42:43], v[32:33], v[40:41] neg_lo:[0,1] neg_hi:[0,1]
	v_xor_b32_e32 v39, 0x80000000, v26
	v_mov_b32_e32 v38, v27
	v_pk_add_f32 v[26:27], v[32:33], v[40:41]
	v_pk_add_f32 v[40:41], v[20:21], v[28:29]
	v_pk_add_f32 v[20:21], v[20:21], v[28:29] neg_lo:[0,1] neg_hi:[0,1]
	v_pk_add_f32 v[32:33], v[34:35], v[38:39]
	v_pk_mul_f32 v[28:29], v[66:67], v[20:21] op_sel:[0,1] op_sel_hi:[0,0] neg_lo:[1,1] neg_hi:[1,0]
	v_pk_fma_f32 v[20:21], v[66:67], v[20:21], v[28:29] op_sel_hi:[0,1,1]
	v_pk_add_f32 v[28:29], v[22:23], v[30:31]
	v_pk_add_f32 v[22:23], v[22:23], v[30:31] neg_lo:[0,1] neg_hi:[0,1]
	v_pk_add_f32 v[38:39], v[34:35], v[38:39] neg_lo:[0,1] neg_hi:[0,1]
	v_xor_b32_e32 v31, 0x80000000, v22
	v_mov_b32_e32 v30, v23
	v_pk_add_f32 v[22:23], v[24:25], v[46:47]
	v_pk_add_f32 v[24:25], v[24:25], v[46:47] neg_lo:[0,1] neg_hi:[0,1]
	v_pk_add_f32 v[34:35], v[18:19], v[72:73]
	v_pk_mul_f32 v[46:47], v[66:67], v[24:25] op_sel:[0,1] op_sel_hi:[0,0] neg_lo:[1,1] neg_hi:[1,0]
	v_pk_fma_f32 v[24:25], v[66:67], v[24:25], v[46:47] op_sel_hi:[0,1,1] neg_lo:[1,0,0] neg_hi:[1,0,0]
	v_pk_add_f32 v[46:47], v[34:35], v[28:29]
	v_pk_add_f32 v[28:29], v[34:35], v[28:29] neg_lo:[0,1] neg_hi:[0,1]
	v_pk_add_f32 v[34:35], v[40:41], v[22:23]
	v_pk_add_f32 v[22:23], v[40:41], v[22:23] neg_lo:[0,1] neg_hi:[0,1]
	v_pk_add_f32 v[18:19], v[18:19], v[72:73] neg_lo:[0,1] neg_hi:[0,1]
	v_pk_add_f32 v[66:67], v[28:29], v[22:23] op_sel:[0,1] op_sel_hi:[1,0] neg_hi:[0,1]
	v_pk_add_f32 v[48:49], v[28:29], v[22:23] op_sel:[0,1] op_sel_hi:[1,0] neg_lo:[0,1]
	v_pk_add_f32 v[28:29], v[18:19], v[30:31]
	v_pk_add_f32 v[18:19], v[18:19], v[30:31] neg_lo:[0,1] neg_hi:[0,1]
	v_pk_add_f32 v[30:31], v[20:21], v[24:25]
	v_pk_add_f32 v[20:21], v[20:21], v[24:25] neg_lo:[0,1] neg_hi:[0,1]
	v_pk_add_f32 v[22:23], v[46:47], v[34:35]
	v_xor_b32_e32 v25, 0x80000000, v20
	v_add_u32_e32 v20, 0x2000, v16
	v_mov_b32_e32 v24, v21
	v_ashrrev_i32_e32 v21, 31, v20
	v_lshl_add_u64 v[20:21], v[20:21], 3, s[46:47]
	s_waitcnt vmcnt(0)
	v_pk_add_f32 v[40:41], v[46:47], v[34:35] neg_lo:[0,1] neg_hi:[0,1]
	v_pk_add_f32 v[34:35], v[18:19], v[24:25]
	v_pk_add_f32 v[18:19], v[18:19], v[24:25] neg_lo:[0,1] neg_hi:[0,1]
	v_pk_add_f32 v[70:71], v[28:29], v[30:31]
	v_pk_add_f32 v[46:47], v[28:29], v[30:31] neg_lo:[0,1] neg_hi:[0,1]
	s_nop 0
	v_pk_mul_f32 v[24:25], v[64:65], v[202:203] op_sel:[1,1] op_sel_hi:[1,0] neg_lo:[1,0]
	s_nop 0
	v_pk_fma_f32 v[20:21], v[64:65], v[202:203], v[24:25] op_sel_hi:[0,1,1]
	v_add_u32_e32 v24, 0x2200, v16
	v_ashrrev_i32_e32 v25, 31, v24
	v_lshl_add_u64 v[24:25], v[24:25], 3, s[46:47]
	s_nop 0
	v_pk_mul_f32 v[28:29], v[204:205], v[22:23] op_sel:[1,1] op_sel_hi:[0,1] neg_lo:[0,1]
	v_pk_fma_f32 v[22:23], v[204:205], v[22:23], v[28:29] op_sel_hi:[1,0,1]
	v_add_u32_e32 v24, 0x2400, v16
	v_ashrrev_i32_e32 v25, 31, v24
	v_lshl_add_u64 v[24:25], v[24:25], 3, s[46:47]
	s_nop 0
	v_pk_mul_f32 v[28:29], v[26:27], v[206:207] op_sel:[1,1] op_sel_hi:[1,0] neg_lo:[1,0]
	s_nop 0
	v_pk_fma_f32 v[24:25], v[26:27], v[206:207], v[28:29] op_sel_hi:[0,1,1]
	v_add_u32_e32 v26, 0x2600, v16
	v_ashrrev_i32_e32 v27, 31, v26
	v_lshl_add_u64 v[26:27], v[26:27], 3, s[46:47]
	s_nop 0
	v_pk_mul_f32 v[28:29], v[208:209], v[70:71] op_sel:[1,1] op_sel_hi:[0,1] neg_lo:[0,1]
	v_pk_fma_f32 v[26:27], v[208:209], v[70:71], v[28:29] op_sel_hi:[1,0,1]
	v_add_u32_e32 v28, 0x2800, v16
	v_ashrrev_i32_e32 v29, 31, v28
	v_lshl_add_u64 v[28:29], v[28:29], 3, s[46:47]
	s_nop 0
	v_pk_mul_f32 v[30:31], v[68:69], v[210:211] op_sel:[1,1] op_sel_hi:[1,0] neg_lo:[1,0]
	s_nop 0
	v_pk_fma_f32 v[28:29], v[68:69], v[210:211], v[30:31] op_sel_hi:[0,1,1]
	v_add_u32_e32 v30, 0x2a00, v16
	v_ashrrev_i32_e32 v31, 31, v30
	v_lshl_add_u64 v[30:31], v[30:31], 3, s[46:47]
	s_nop 0
	v_pk_mul_f32 v[64:65], v[212:213], v[66:67] op_sel:[1,1] op_sel_hi:[0,1] neg_lo:[0,1]
	v_pk_fma_f32 v[30:31], v[212:213], v[66:67], v[64:65] op_sel_hi:[1,0,1]
	v_add_u32_e32 v64, 0x2c00, v16
	v_ashrrev_i32_e32 v65, 31, v64
	v_lshl_add_u64 v[64:65], v[64:65], 3, s[46:47]
	s_nop 0
	v_pk_mul_f32 v[66:67], v[32:33], v[214:215] op_sel:[1,1] op_sel_hi:[1,0] neg_lo:[1,0]
	s_nop 0
	v_pk_fma_f32 v[32:33], v[32:33], v[214:215], v[66:67] op_sel_hi:[0,1,1]
	v_add_u32_e32 v64, 0x2e00, v16
	v_ashrrev_i32_e32 v65, 31, v64
	v_lshl_add_u64 v[64:65], v[64:65], 3, s[46:47]
	s_nop 0
	v_pk_mul_f32 v[66:67], v[216:217], v[34:35] op_sel:[1,1] op_sel_hi:[0,1] neg_lo:[0,1]
	v_pk_fma_f32 v[34:35], v[216:217], v[34:35], v[66:67] op_sel_hi:[1,0,1]
	v_add_u32_e32 v64, 0x3000, v16
	v_ashrrev_i32_e32 v65, 31, v64
	v_lshl_add_u64 v[64:65], v[64:65], 3, s[46:47]
	s_nop 0
	v_pk_mul_f32 v[66:67], v[36:37], v[218:219] op_sel:[1,1] op_sel_hi:[1,0] neg_lo:[1,0]
	s_nop 0
	v_pk_fma_f32 v[36:37], v[36:37], v[218:219], v[66:67] op_sel_hi:[0,1,1]
	v_add_u32_e32 v64, 0x3200, v16
	v_ashrrev_i32_e32 v65, 31, v64
	v_lshl_add_u64 v[64:65], v[64:65], 3, s[46:47]
	v_pk_add_f32 v[68:69], v[20:21], v[36:37]
	v_pk_add_f32 v[20:21], v[20:21], v[36:37] neg_lo:[0,1] neg_hi:[0,1]
	s_nop 0
	v_pk_mul_f32 v[66:67], v[40:41], v[220:221] op_sel:[1,1] op_sel_hi:[1,0] neg_lo:[1,0]
	s_nop 0
	v_pk_fma_f32 v[40:41], v[40:41], v[220:221], v[66:67] op_sel_hi:[0,1,1]
	v_add_u32_e32 v64, 0x3400, v16
	v_ashrrev_i32_e32 v65, 31, v64
	v_lshl_add_u64 v[64:65], v[64:65], 3, s[46:47]
	v_pk_add_f32 v[36:37], v[22:23], v[40:41]
	v_pk_add_f32 v[22:23], v[22:23], v[40:41] neg_lo:[0,1] neg_hi:[0,1]
	s_nop 0
	v_pk_mul_f32 v[66:67], v[42:43], v[222:223] op_sel:[1,1] op_sel_hi:[1,0] neg_lo:[1,0]
	s_nop 0
	v_pk_fma_f32 v[42:43], v[42:43], v[222:223], v[66:67] op_sel_hi:[0,1,1]
	v_add_u32_e32 v64, 0x3600, v16
	v_ashrrev_i32_e32 v65, 31, v64
	v_lshl_add_u64 v[64:65], v[64:65], 3, s[46:47]
	s_nop 0
	v_pk_mul_f32 v[66:67], v[46:47], v[224:225] op_sel:[1,1] op_sel_hi:[1,0] neg_lo:[1,0]
	s_nop 0
	v_pk_fma_f32 v[46:47], v[46:47], v[224:225], v[66:67] op_sel_hi:[0,1,1]
	v_add_u32_e32 v64, 0x3800, v16
	v_ashrrev_i32_e32 v65, 31, v64
	v_lshl_add_u64 v[64:65], v[64:65], 3, s[46:47]
	s_nop 0
	v_pk_mul_f32 v[66:67], v[44:45], v[226:227] op_sel:[1,1] op_sel_hi:[1,0] neg_lo:[1,0]
	s_nop 0
	v_pk_fma_f32 v[44:45], v[44:45], v[226:227], v[66:67] op_sel_hi:[0,1,1]
	v_add_u32_e32 v64, 0x3a00, v16
	v_ashrrev_i32_e32 v65, 31, v64
	v_lshl_add_u64 v[64:65], v[64:65], 3, s[46:47]
	s_nop 0
	v_pk_mul_f32 v[66:67], v[48:49], v[228:229] op_sel:[1,1] op_sel_hi:[1,0] neg_lo:[1,0]
	s_nop 0
	v_pk_fma_f32 v[48:49], v[48:49], v[228:229], v[66:67] op_sel_hi:[0,1,1]
	v_add_u32_e32 v64, 0x3c00, v16
	v_ashrrev_i32_e32 v65, 31, v64
	v_lshl_add_u64 v[64:65], v[64:65], 3, s[46:47]
	v_add_u32_e32 v16, 0x3e00, v16
	v_ashrrev_i32_e32 v17, 31, v16
	v_lshl_add_u64 v[16:17], v[16:17], 3, s[46:47]
	s_nop 0
	v_pk_mul_f32 v[66:67], v[38:39], v[230:231] op_sel:[1,1] op_sel_hi:[1,0] neg_lo:[1,0]
	s_nop 0
	v_pk_fma_f32 v[38:39], v[38:39], v[230:231], v[66:67] op_sel_hi:[0,1,1]
	s_nop 0
	v_pk_mul_f32 v[64:65], v[18:19], v[232:233] op_sel:[1,1] op_sel_hi:[1,0] neg_lo:[1,0]
	v_mov_b32_e32 v66, v169
	v_pk_fma_f32 v[16:17], v[18:19], v[232:233], v[64:65] op_sel_hi:[0,1,1]
	v_mov_b32_e32 v18, v1
	v_mov_b32_e32 v19, v166
	v_mov_b32_e32 v18, v164
	v_mov_b32_e32 v64, v167
	v_mov_b32_e32 v18, v165
	s_nop 0
	v_mov_b32_e32 v19, v168
	s_nop 0
	v_mov_b32_e32 v19, v170
	v_pk_mul_f32 v[40:41], v[22:23], v[66:67] op_sel:[1,0] op_sel_hi:[0,0] neg_lo:[1,0]
	v_mov_b32_e32 v19, v171
	s_nop 0
	v_pk_fma_f32 v[22:23], v[22:23], v[18:19], v[40:41] op_sel_hi:[1,0,1]
	v_pk_add_f32 v[40:41], v[24:25], v[42:43]
	v_pk_add_f32 v[24:25], v[24:25], v[42:43] neg_lo:[0,1] neg_hi:[0,1]
	s_nop 0
	v_pk_mul_f32 v[42:43], v[24:25], v[64:65] op_sel:[1,0] op_sel_hi:[0,0] neg_lo:[1,0]
	s_nop 0
	v_pk_fma_f32 v[24:25], v[24:25], v[64:65], v[42:43] op_sel_hi:[1,0,1]
	v_pk_add_f32 v[42:43], v[26:27], v[46:47]
	v_pk_add_f32 v[26:27], v[26:27], v[46:47] neg_lo:[0,1] neg_hi:[0,1]
	s_nop 0
	v_pk_mul_f32 v[46:47], v[26:27], v[66:67] op_sel_hi:[1,0]
	s_nop 0
	v_pk_fma_f32 v[26:27], v[26:27], v[18:19], v[46:47] op_sel:[1,0,0] op_sel_hi:[0,0,1] neg_lo:[1,0,0]
	v_pk_add_f32 v[46:47], v[28:29], v[44:45]
	v_pk_add_f32 v[28:29], v[28:29], v[44:45] neg_lo:[0,1] neg_hi:[0,1]
	s_nop 0
	v_xor_b32_e32 v44, 0x80000000, v29
	v_mov_b32_e32 v45, v28
	v_pk_add_f32 v[28:29], v[30:31], v[48:49]
	v_pk_add_f32 v[30:31], v[30:31], v[48:49] neg_lo:[0,1] neg_hi:[0,1]
	s_nop 0
	v_pk_mul_f32 v[48:49], v[30:31], v[66:67] op_sel_hi:[1,0] neg_lo:[0,1] neg_hi:[0,1]
	s_nop 0
	v_pk_fma_f32 v[30:31], v[30:31], v[18:19], v[48:49] op_sel:[1,0,0] op_sel_hi:[0,0,1] neg_lo:[1,0,0]
	v_pk_add_f32 v[48:49], v[32:33], v[38:39]
	v_pk_add_f32 v[32:33], v[32:33], v[38:39] neg_lo:[0,1] neg_hi:[0,1]
	s_nop 0
	v_pk_mul_f32 v[38:39], v[32:33], v[64:65] op_sel:[1,0] op_sel_hi:[0,0] neg_lo:[1,0]
	s_nop 0
	v_pk_fma_f32 v[32:33], v[32:33], v[64:65], v[38:39] op_sel_hi:[1,0,1] neg_lo:[0,1,0] neg_hi:[0,1,0]
	v_pk_add_f32 v[38:39], v[34:35], v[16:17]
	v_pk_add_f32 v[16:17], v[34:35], v[16:17] neg_lo:[0,1] neg_hi:[0,1]
	s_nop 0
	v_pk_mul_f32 v[34:35], v[16:17], v[66:67] op_sel:[1,0] op_sel_hi:[0,0] neg_lo:[1,0]
	s_nop 0
	v_pk_fma_f32 v[16:17], v[16:17], v[18:19], v[34:35] op_sel_hi:[1,0,1] neg_lo:[0,1,0] neg_hi:[0,1,0]
	v_pk_add_f32 v[18:19], v[68:69], v[46:47]
	v_pk_add_f32 v[34:35], v[68:69], v[46:47] neg_lo:[0,1] neg_hi:[0,1]
	v_pk_add_f32 v[46:47], v[36:37], v[28:29]
	v_pk_add_f32 v[28:29], v[36:37], v[28:29] neg_lo:[0,1] neg_hi:[0,1]
	s_nop 0
	v_pk_mul_f32 v[36:37], v[28:29], v[64:65] op_sel:[1,0] op_sel_hi:[0,0] neg_lo:[1,0]
	s_nop 0
	v_pk_fma_f32 v[28:29], v[28:29], v[64:65], v[36:37] op_sel_hi:[1,0,1]
	v_pk_add_f32 v[36:37], v[40:41], v[48:49]
	v_pk_add_f32 v[40:41], v[40:41], v[48:49] neg_lo:[0,1] neg_hi:[0,1]
	s_nop 0
	v_xor_b32_e32 v48, 0x80000000, v41
	v_mov_b32_e32 v49, v40
	v_pk_add_f32 v[40:41], v[42:43], v[38:39]
	v_pk_add_f32 v[38:39], v[42:43], v[38:39] neg_lo:[0,1] neg_hi:[0,1]
	s_nop 0
	v_pk_mul_f32 v[42:43], v[64:65], v[38:39] op_sel:[0,1] op_sel_hi:[0,0] neg_lo:[0,1]
	v_pk_fma_f32 v[38:39], v[38:39], v[64:65], v[42:43] op_sel_hi:[1,0,1] neg_lo:[0,1,0] neg_hi:[0,1,0]
	v_pk_add_f32 v[42:43], v[18:19], v[36:37]
	v_pk_add_f32 v[18:19], v[18:19], v[36:37] neg_lo:[0,1] neg_hi:[0,1]
	v_pk_add_f32 v[36:37], v[46:47], v[40:41]
	v_pk_add_f32 v[40:41], v[46:47], v[40:41] neg_lo:[0,1] neg_hi:[0,1]
	s_nop 0
	v_xor_b32_e32 v46, 0x80000000, v41
	v_mov_b32_e32 v47, v40
	v_pk_add_f32 v[40:41], v[42:43], v[36:37]
	v_pk_add_f32 v[36:37], v[42:43], v[36:37] neg_lo:[0,1] neg_hi:[0,1]
	v_pk_add_f32 v[42:43], v[18:19], v[46:47]
	v_pk_add_f32 v[18:19], v[18:19], v[46:47] neg_lo:[0,1] neg_hi:[0,1]
	v_pk_add_f32 v[46:47], v[34:35], v[48:49]
	v_pk_add_f32 v[34:35], v[34:35], v[48:49] neg_lo:[0,1] neg_hi:[0,1]
	v_pk_add_f32 v[48:49], v[28:29], v[38:39]
	v_pk_add_f32 v[28:29], v[28:29], v[38:39] neg_lo:[0,1] neg_hi:[0,1]
	s_nop 0
	v_xor_b32_e32 v38, 0x80000000, v29
	v_mov_b32_e32 v39, v28
	v_pk_add_f32 v[28:29], v[46:47], v[48:49]
	v_pk_add_f32 v[46:47], v[46:47], v[48:49] neg_lo:[0,1] neg_hi:[0,1]
	v_pk_add_f32 v[48:49], v[34:35], v[38:39]
	v_pk_add_f32 v[34:35], v[34:35], v[38:39] neg_lo:[0,1] neg_hi:[0,1]
	v_pk_add_f32 v[38:39], v[20:21], v[44:45]
	v_pk_add_f32 v[20:21], v[20:21], v[44:45] neg_lo:[0,1] neg_hi:[0,1]
	v_pk_add_f32 v[44:45], v[22:23], v[30:31]
	v_pk_add_f32 v[22:23], v[22:23], v[30:31] neg_lo:[0,1] neg_hi:[0,1]
	s_nop 0
	v_pk_mul_f32 v[30:31], v[64:65], v[22:23] op_sel:[0,1] op_sel_hi:[0,0] neg_lo:[0,1]
	v_pk_fma_f32 v[22:23], v[64:65], v[22:23], v[30:31] op_sel_hi:[0,1,1]
	v_pk_add_f32 v[30:31], v[24:25], v[32:33]
	v_pk_add_f32 v[24:25], v[24:25], v[32:33] neg_lo:[0,1] neg_hi:[0,1]
	s_nop 0
	v_xor_b32_e32 v32, 0x80000000, v25
	v_mov_b32_e32 v33, v24
	v_pk_add_f32 v[24:25], v[26:27], v[16:17]
	v_pk_add_f32 v[16:17], v[26:27], v[16:17] neg_lo:[0,1] neg_hi:[0,1]
	s_nop 0
	v_pk_mul_f32 v[26:27], v[64:65], v[16:17] op_sel:[0,1] op_sel_hi:[0,0] neg_lo:[0,1]
	v_pk_fma_f32 v[16:17], v[64:65], v[16:17], v[26:27] op_sel_hi:[0,1,1] neg_lo:[1,0,0] neg_hi:[1,0,0]
	v_pk_add_f32 v[26:27], v[38:39], v[30:31]
	v_pk_add_f32 v[30:31], v[38:39], v[30:31] neg_lo:[0,1] neg_hi:[0,1]
	v_pk_add_f32 v[38:39], v[44:45], v[24:25]
	v_pk_add_f32 v[24:25], v[44:45], v[24:25] neg_lo:[0,1] neg_hi:[0,1]
	s_nop 0
	v_xor_b32_e32 v44, 0x80000000, v25
	v_mov_b32_e32 v45, v24
	v_pk_add_f32 v[24:25], v[26:27], v[38:39]
	v_pk_add_f32 v[26:27], v[26:27], v[38:39] neg_lo:[0,1] neg_hi:[0,1]
	v_pk_add_f32 v[38:39], v[30:31], v[44:45]
	v_pk_add_f32 v[30:31], v[30:31], v[44:45] neg_lo:[0,1] neg_hi:[0,1]
	v_pk_add_f32 v[44:45], v[20:21], v[32:33]
	v_pk_add_f32 v[20:21], v[20:21], v[32:33] neg_lo:[0,1] neg_hi:[0,1]
	v_pk_add_f32 v[32:33], v[22:23], v[16:17]
	v_pk_add_f32 v[16:17], v[22:23], v[16:17] neg_lo:[0,1] neg_hi:[0,1]
	s_nop 0
	v_xor_b32_e32 v22, 0x80000000, v17
	v_mov_b32_e32 v23, v16
	v_pk_add_f32 v[16:17], v[44:45], v[32:33]
	v_pk_add_f32 v[32:33], v[44:45], v[32:33] neg_lo:[0,1] neg_hi:[0,1]
	v_pk_add_f32 v[44:45], v[20:21], v[22:23]
	v_pk_add_f32 v[20:21], v[20:21], v[22:23] neg_lo:[0,1] neg_hi:[0,1]
	ds_write_b64 v10, v[40:41]
	ds_write_b64 v13, v[24:25]
	ds_write_b64 v15, v[28:29]
	ds_write_b64 v50, v[16:17]
	ds_write_b64 v51, v[42:43]
	ds_write_b64 v52, v[38:39]
	ds_write_b64 v53, v[48:49]
	ds_write_b64 v54, v[44:45]
	ds_write_b64 v55, v[36:37]
	ds_write_b64 v56, v[26:27]
	ds_write_b64 v57, v[46:47]
	ds_write_b64 v58, v[32:33]
	ds_write_b64 v59, v[18:19]
	ds_write_b64 v60, v[30:31]
	ds_write_b64 v61, v[34:35]
	ds_write_b64 v62, v[20:21]
	v_mov_b32_e32 v10, v174
	v_mov_b32_e32 v50, v172
	s_waitcnt lgkmcnt(0)
	s_barrier
	v_add_u32_e32 v13, v50, v10
	v_lshl_add_u32 v13, v13, 3, 0
	ds_read2_b64 v[16:19], v13 offset1:16
	v_xad_u32 v15, v50, 1, v10
	v_lshl_add_u32 v15, v15, 3, 0
	s_waitcnt lgkmcnt(0)
	v_pk_fma_f32 v[16:17], v[16:17], 0, v[16:17] op_sel:[1,0,0] op_sel_hi:[0,0,1] neg_hi:[1,0,0]
	v_pk_fma_f32 v[22:23], v[180:181], s[90:91], v[180:181] op_sel:[1,0,0] op_sel_hi:[0,1,1]
	v_pk_mul_f32 v[24:25], v[22:23], v[18:19] op_sel:[1,1] op_sel_hi:[1,0] neg_hi:[0,1]
	s_nop 0
	v_pk_fma_f32 v[18:19], v[18:19], v[22:23], v[24:25] op_sel_hi:[1,0,1]
	v_pk_mul_f32 v[24:25], v[180:181], v[22:23] op_sel:[1,1] op_sel_hi:[0,1] neg_lo:[0,1]
	v_pk_fma_f32 v[26:27], v[180:181], v[22:23], v[24:25] op_sel_hi:[1,0,1]
	ds_read2_b64 v[22:25], v15 offset0:32 offset1:48
	s_waitcnt lgkmcnt(0)
	v_pk_mul_f32 v[28:29], v[22:23], v[26:27] op_sel:[1,1] op_sel_hi:[0,1] neg_hi:[1,0]
	s_nop 0
	v_pk_fma_f32 v[22:23], v[22:23], v[26:27], v[28:29] op_sel_hi:[1,0,1]
	v_pk_mul_f32 v[28:29], v[180:181], v[26:27] op_sel:[1,1] op_sel_hi:[0,1] neg_lo:[0,1]
	v_pk_fma_f32 v[26:27], v[180:181], v[26:27], v[28:29] op_sel_hi:[1,0,1]
	s_nop 0
	v_pk_mul_f32 v[28:29], v[24:25], v[26:27] op_sel:[1,1] op_sel_hi:[0,1] neg_hi:[1,0]
	s_nop 0
	v_pk_fma_f32 v[24:25], v[24:25], v[26:27], v[28:29] op_sel_hi:[1,0,1]
	v_pk_mul_f32 v[28:29], v[180:181], v[26:27] op_sel:[1,1] op_sel_hi:[0,1] neg_lo:[0,1]
	v_pk_fma_f32 v[26:27], v[180:181], v[26:27], v[28:29] op_sel_hi:[1,0,1]
	v_xad_u32 v28, v50, 2, v10
	v_lshl_add_u32 v51, v28, 3, 0
	ds_read2_b64 v[28:31], v51 offset0:64 offset1:80
	v_pk_mul_f32 v[32:33], v[180:181], v[26:27] op_sel:[1,1] op_sel_hi:[0,1] neg_lo:[0,1]
	s_waitcnt lgkmcnt(0)
	v_pk_mul_f32 v[34:35], v[28:29], v[26:27] op_sel:[1,1] op_sel_hi:[0,1] neg_hi:[1,0]
	s_nop 0
	v_pk_fma_f32 v[28:29], v[28:29], v[26:27], v[34:35] op_sel_hi:[1,0,1]
	v_pk_fma_f32 v[34:35], v[180:181], v[26:27], v[32:33] op_sel_hi:[1,0,1]
	s_nop 0
	v_pk_mul_f32 v[26:27], v[30:31], v[34:35] op_sel:[1,1] op_sel_hi:[0,1] neg_hi:[1,0]
	v_pk_fma_f32 v[26:27], v[30:31], v[34:35], v[26:27] op_sel_hi:[1,0,1]
	v_xad_u32 v30, v50, 3, v10
	v_lshl_add_u32 v54, v30, 3, 0
	ds_read2_b64 v[30:33], v54 offset0:96 offset1:112
	v_pk_mul_f32 v[36:37], v[180:181], v[34:35] op_sel:[1,1] op_sel_hi:[0,1] neg_lo:[0,1]
	v_pk_fma_f32 v[34:35], v[180:181], v[34:35], v[36:37] op_sel_hi:[1,0,1]
	s_waitcnt lgkmcnt(0)
	v_pk_mul_f32 v[36:37], v[30:31], v[34:35] op_sel:[1,1] op_sel_hi:[0,1] neg_hi:[1,0]
	s_nop 0
	v_pk_fma_f32 v[30:31], v[30:31], v[34:35], v[36:37] op_sel_hi:[1,0,1]
	v_pk_mul_f32 v[36:37], v[180:181], v[34:35] op_sel:[1,1] op_sel_hi:[0,1] neg_lo:[0,1]
	v_pk_fma_f32 v[34:35], v[180:181], v[34:35], v[36:37] op_sel_hi:[1,0,1]
	s_nop 0
	v_pk_mul_f32 v[36:37], v[32:33], v[34:35] op_sel:[1,1] op_sel_hi:[0,1] neg_hi:[1,0]
	s_nop 0
	v_pk_fma_f32 v[32:33], v[32:33], v[34:35], v[36:37] op_sel_hi:[1,0,1]
	v_pk_mul_f32 v[36:37], v[180:181], v[34:35] op_sel:[1,1] op_sel_hi:[0,1] neg_lo:[0,1]
	v_pk_fma_f32 v[38:39], v[180:181], v[34:35], v[36:37] op_sel_hi:[1,0,1]
	v_xad_u32 v34, v50, 4, v10
	v_lshl_add_u32 v55, v34, 3, 0
	ds_read2_b64 v[34:37], v55 offset0:128 offset1:144
	v_pk_mul_f32 v[40:41], v[180:181], v[38:39] op_sel:[1,1] op_sel_hi:[0,1] neg_lo:[0,1]
	s_waitcnt lgkmcnt(0)
	v_pk_mul_f32 v[42:43], v[34:35], v[38:39] op_sel:[1,1] op_sel_hi:[0,1] neg_hi:[1,0]
	s_nop 0
	v_pk_fma_f32 v[34:35], v[34:35], v[38:39], v[42:43] op_sel_hi:[1,0,1]
	v_pk_fma_f32 v[42:43], v[180:181], v[38:39], v[40:41] op_sel_hi:[1,0,1]
	s_nop 0
	v_pk_mul_f32 v[38:39], v[36:37], v[42:43] op_sel:[1,1] op_sel_hi:[0,1] neg_hi:[1,0]
	v_pk_fma_f32 v[36:37], v[36:37], v[42:43], v[38:39] op_sel_hi:[1,0,1]
	v_xad_u32 v38, v50, 5, v10
	v_lshl_add_u32 v56, v38, 3, 0
	ds_read2_b64 v[38:41], v56 offset0:160 offset1:176
	v_pk_mul_f32 v[44:45], v[180:181], v[42:43] op_sel:[1,1] op_sel_hi:[0,1] neg_lo:[0,1]
	v_pk_fma_f32 v[42:43], v[180:181], v[42:43], v[44:45] op_sel_hi:[1,0,1]
	s_waitcnt lgkmcnt(0)
	v_pk_mul_f32 v[44:45], v[38:39], v[42:43] op_sel:[1,1] op_sel_hi:[0,1] neg_hi:[1,0]
	s_nop 0
	v_pk_fma_f32 v[38:39], v[38:39], v[42:43], v[44:45] op_sel_hi:[1,0,1]
	v_pk_mul_f32 v[44:45], v[180:181], v[42:43] op_sel:[1,1] op_sel_hi:[0,1] neg_lo:[0,1]
	v_pk_fma_f32 v[42:43], v[180:181], v[42:43], v[44:45] op_sel_hi:[1,0,1]
	s_nop 0
	v_pk_mul_f32 v[44:45], v[40:41], v[42:43] op_sel:[1,1] op_sel_hi:[0,1] neg_hi:[1,0]
	s_nop 0
	v_pk_fma_f32 v[40:41], v[40:41], v[42:43], v[44:45] op_sel_hi:[1,0,1]
	v_pk_mul_f32 v[44:45], v[180:181], v[42:43] op_sel:[1,1] op_sel_hi:[0,1] neg_lo:[0,1]
	v_pk_fma_f32 v[42:43], v[180:181], v[42:43], v[44:45] op_sel_hi:[1,0,1]
	v_xad_u32 v44, v50, 6, v10
	v_lshl_add_u32 v57, v44, 3, 0
	ds_read2_b64 v[44:47], v57 offset0:192 offset1:208
	v_pk_mul_f32 v[48:49], v[180:181], v[42:43] op_sel:[1,1] op_sel_hi:[0,1] neg_lo:[0,1]
	s_waitcnt lgkmcnt(0)
	v_pk_mul_f32 v[52:53], v[44:45], v[42:43] op_sel:[1,1] op_sel_hi:[0,1] neg_hi:[1,0]
	s_nop 0
	v_pk_fma_f32 v[44:45], v[44:45], v[42:43], v[52:53] op_sel_hi:[1,0,1]
	v_pk_fma_f32 v[52:53], v[180:181], v[42:43], v[48:49] op_sel_hi:[1,0,1]
	s_nop 0
	v_pk_mul_f32 v[42:43], v[46:47], v[52:53] op_sel:[1,1] op_sel_hi:[0,1] neg_hi:[1,0]
	v_pk_fma_f32 v[42:43], v[46:47], v[52:53], v[42:43] op_sel_hi:[1,0,1]
	v_xad_u32 v46, v50, 7, v10
	v_lshl_add_u32 v58, v46, 3, 0
	ds_read2_b64 v[46:49], v58 offset0:224 offset1:240
	v_pk_mul_f32 v[60:61], v[180:181], v[52:53] op_sel:[1,1] op_sel_hi:[0,1] neg_lo:[0,1]
	v_pk_fma_f32 v[52:53], v[180:181], v[52:53], v[60:61] op_sel_hi:[1,0,1]
	s_waitcnt lgkmcnt(0)
	v_pk_mul_f32 v[60:61], v[46:47], v[52:53] op_sel:[1,1] op_sel_hi:[0,1] neg_hi:[1,0]
	s_nop 0
	v_pk_fma_f32 v[46:47], v[46:47], v[52:53], v[60:61] op_sel_hi:[1,0,1]
	v_pk_mul_f32 v[60:61], v[180:181], v[52:53] op_sel:[1,1] op_sel_hi:[0,1] neg_lo:[0,1]
	v_pk_fma_f32 v[52:53], v[180:181], v[52:53], v[60:61] op_sel_hi:[1,0,1]
	s_nop 0
	v_pk_mul_f32 v[60:61], v[48:49], v[52:53] op_sel:[1,1] op_sel_hi:[0,1] neg_hi:[1,0]
	s_nop 0
	v_pk_fma_f32 v[48:49], v[48:49], v[52:53], v[60:61] op_sel_hi:[1,0,1]
	v_pk_mul_f32 v[60:61], v[180:181], v[52:53] op_sel:[1,1] op_sel_hi:[0,1] neg_lo:[0,1]
	v_pk_fma_f32 v[64:65], v[180:181], v[52:53], v[60:61] op_sel_hi:[1,0,1]
	v_xad_u32 v52, v50, 8, v10
	v_lshl_add_u32 v52, v52, 3, 0
	v_add_u32_e32 v59, 0x800, v52
	ds_read2_b64 v[60:63], v59 offset1:16
	v_pk_mul_f32 v[66:67], v[180:181], v[64:65] op_sel:[1,1] op_sel_hi:[0,1] neg_lo:[0,1]
	v_pk_fma_f32 v[66:67], v[180:181], v[64:65], v[66:67] op_sel_hi:[1,0,1]
	s_waitcnt lgkmcnt(0)
	v_pk_mul_f32 v[52:53], v[60:61], v[64:65] op_sel:[1,1] op_sel_hi:[0,1] neg_hi:[1,0]
	v_pk_fma_f32 v[52:53], v[60:61], v[64:65], v[52:53] op_sel_hi:[1,0,1]
	v_pk_mul_f32 v[60:61], v[62:63], v[66:67] op_sel:[1,1] op_sel_hi:[0,1] neg_hi:[1,0]
	v_pk_fma_f32 v[70:71], v[62:63], v[66:67], v[60:61] op_sel_hi:[1,0,1]
	v_xad_u32 v60, v50, 9, v10
	v_lshl_add_u32 v60, v60, 3, 0
	v_add_u32_e32 v60, 0x800, v60
	ds_read2_b64 v[62:65], v60 offset0:32 offset1:48
	v_pk_mul_f32 v[68:69], v[180:181], v[66:67] op_sel:[1,1] op_sel_hi:[0,1] neg_lo:[0,1]
	v_pk_fma_f32 v[66:67], v[180:181], v[66:67], v[68:69] op_sel_hi:[1,0,1]
	s_waitcnt lgkmcnt(0)
	v_pk_mul_f32 v[68:69], v[62:63], v[66:67] op_sel:[1,1] op_sel_hi:[0,1] neg_hi:[1,0]
	s_nop 0
	v_pk_fma_f32 v[72:73], v[62:63], v[66:67], v[68:69] op_sel_hi:[1,0,1]
	v_pk_mul_f32 v[62:63], v[180:181], v[66:67] op_sel:[1,1] op_sel_hi:[0,1] neg_lo:[0,1]
	v_pk_fma_f32 v[62:63], v[180:181], v[66:67], v[62:63] op_sel_hi:[1,0,1]
	s_nop 0
	v_pk_mul_f32 v[66:67], v[64:65], v[62:63] op_sel:[1,1] op_sel_hi:[0,1] neg_hi:[1,0]
	s_nop 0
	v_pk_fma_f32 v[74:75], v[64:65], v[62:63], v[66:67] op_sel_hi:[1,0,1]
	v_pk_mul_f32 v[64:65], v[180:181], v[62:63] op_sel:[1,1] op_sel_hi:[0,1] neg_lo:[0,1]
	v_pk_fma_f32 v[66:67], v[180:181], v[62:63], v[64:65] op_sel_hi:[1,0,1]
	v_xad_u32 v61, v50, 10, v10
	v_lshl_add_u32 v61, v61, 3, 0
	v_add_u32_e32 v61, 0x800, v61
	ds_read2_b64 v[62:65], v61 offset0:64 offset1:80
	v_pk_mul_f32 v[68:69], v[180:181], v[66:67] op_sel:[1,1] op_sel_hi:[0,1] neg_lo:[0,1]
	v_pk_fma_f32 v[68:69], v[180:181], v[66:67], v[68:69] op_sel_hi:[1,0,1]
	s_waitcnt lgkmcnt(0)
	v_pk_mul_f32 v[76:77], v[62:63], v[66:67] op_sel:[1,1] op_sel_hi:[0,1] neg_hi:[1,0]
	v_pk_fma_f32 v[76:77], v[62:63], v[66:67], v[76:77] op_sel_hi:[1,0,1]
	v_pk_mul_f32 v[62:63], v[64:65], v[68:69] op_sel:[1,1] op_sel_hi:[0,1] neg_hi:[1,0]
	v_pk_fma_f32 v[78:79], v[64:65], v[68:69], v[62:63] op_sel_hi:[1,0,1]
	v_xad_u32 v62, v50, 11, v10
	v_lshl_add_u32 v62, v62, 3, 0
	v_add_u32_e32 v62, 0x800, v62
	ds_read2_b64 v[64:67], v62 offset0:96 offset1:112
	v_pk_mul_f32 v[80:81], v[180:181], v[68:69] op_sel:[1,1] op_sel_hi:[0,1] neg_lo:[0,1]
	v_pk_fma_f32 v[68:69], v[180:181], v[68:69], v[80:81] op_sel_hi:[1,0,1]
	s_waitcnt lgkmcnt(0)
	v_pk_mul_f32 v[80:81], v[64:65], v[68:69] op_sel:[1,1] op_sel_hi:[0,1] neg_hi:[1,0]
	s_nop 0
	v_pk_fma_f32 v[80:81], v[64:65], v[68:69], v[80:81] op_sel_hi:[1,0,1]
	v_pk_mul_f32 v[64:65], v[180:181], v[68:69] op_sel:[1,1] op_sel_hi:[0,1] neg_lo:[0,1]
	v_pk_fma_f32 v[64:65], v[180:181], v[68:69], v[64:65] op_sel_hi:[1,0,1]
	s_nop 0
	v_pk_mul_f32 v[68:69], v[66:67], v[64:65] op_sel:[1,1] op_sel_hi:[0,1] neg_hi:[1,0]
	s_nop 0
	v_pk_fma_f32 v[82:83], v[66:67], v[64:65], v[68:69] op_sel_hi:[1,0,1]
	v_pk_mul_f32 v[66:67], v[180:181], v[64:65] op_sel:[1,1] op_sel_hi:[0,1] neg_lo:[0,1]
	v_pk_fma_f32 v[68:69], v[180:181], v[64:65], v[66:67] op_sel_hi:[1,0,1]
	v_xad_u32 v63, v50, 12, v10
	v_lshl_add_u32 v63, v63, 3, 0
	v_add_u32_e32 v63, 0x800, v63
	ds_read2_b64 v[64:67], v63 offset0:128 offset1:144
	v_pk_mul_f32 v[84:85], v[180:181], v[68:69] op_sel:[1,1] op_sel_hi:[0,1] neg_lo:[0,1]
	v_pk_fma_f32 v[84:85], v[180:181], v[68:69], v[84:85] op_sel_hi:[1,0,1]
	s_waitcnt lgkmcnt(0)
	v_pk_mul_f32 v[86:87], v[64:65], v[68:69] op_sel:[1,1] op_sel_hi:[0,1] neg_hi:[1,0]
	v_pk_fma_f32 v[86:87], v[64:65], v[68:69], v[86:87] op_sel_hi:[1,0,1]
	v_pk_mul_f32 v[64:65], v[66:67], v[84:85] op_sel:[1,1] op_sel_hi:[0,1] neg_hi:[1,0]
	v_pk_fma_f32 v[88:89], v[66:67], v[84:85], v[64:65] op_sel_hi:[1,0,1]
	v_xad_u32 v64, v50, 13, v10
	v_lshl_add_u32 v64, v64, 3, 0
	v_add_u32_e32 v64, 0x800, v64
	ds_read2_b64 v[66:69], v64 offset0:160 offset1:176
	v_pk_mul_f32 v[90:91], v[180:181], v[84:85] op_sel:[1,1] op_sel_hi:[0,1] neg_lo:[0,1]
	v_pk_fma_f32 v[84:85], v[180:181], v[84:85], v[90:91] op_sel_hi:[1,0,1]
	s_waitcnt lgkmcnt(0)
	v_pk_mul_f32 v[90:91], v[66:67], v[84:85] op_sel:[1,1] op_sel_hi:[0,1] neg_hi:[1,0]
	s_nop 0
	v_pk_fma_f32 v[90:91], v[66:67], v[84:85], v[90:91] op_sel_hi:[1,0,1]
	v_pk_mul_f32 v[66:67], v[180:181], v[84:85] op_sel:[1,1] op_sel_hi:[0,1] neg_lo:[0,1]
	v_pk_fma_f32 v[66:67], v[180:181], v[84:85], v[66:67] op_sel_hi:[1,0,1]
	s_nop 0
	v_pk_mul_f32 v[84:85], v[68:69], v[66:67] op_sel:[1,1] op_sel_hi:[0,1] neg_hi:[1,0]
	s_nop 0
	v_pk_fma_f32 v[84:85], v[68:69], v[66:67], v[84:85] op_sel_hi:[1,0,1]
	v_pk_mul_f32 v[68:69], v[180:181], v[66:67] op_sel:[1,1] op_sel_hi:[0,1] neg_lo:[0,1]
	v_pk_fma_f32 v[92:93], v[180:181], v[66:67], v[68:69] op_sel_hi:[1,0,1]
	v_xad_u32 v65, v50, 14, v10
	v_lshl_add_u32 v65, v65, 3, 0
	v_add_u32_e32 v65, 0x800, v65
	ds_read2_b64 v[66:69], v65 offset0:192 offset1:208
	v_pk_mul_f32 v[94:95], v[180:181], v[92:93] op_sel:[1,1] op_sel_hi:[0,1] neg_lo:[0,1]
	v_xad_u32 v10, v50, 15, v10
	s_waitcnt lgkmcnt(0)
	v_pk_mul_f32 v[96:97], v[66:67], v[92:93] op_sel:[1,1] op_sel_hi:[0,1] neg_hi:[1,0]
	v_lshl_add_u32 v10, v10, 3, 0
	v_pk_fma_f32 v[96:97], v[66:67], v[92:93], v[96:97] op_sel_hi:[1,0,1]
	v_pk_fma_f32 v[92:93], v[180:181], v[92:93], v[94:95] op_sel_hi:[1,0,1]
	s_nop 0
	v_pk_mul_f32 v[66:67], v[68:69], v[92:93] op_sel:[1,1] op_sel_hi:[0,1] neg_hi:[1,0]
	v_add_u32_e32 v101, 0x800, v10
	v_pk_fma_f32 v[94:95], v[68:69], v[92:93], v[66:67] op_sel_hi:[1,0,1]
	ds_read2_b64 v[66:69], v101 offset0:224 offset1:240
	v_pk_mul_f32 v[98:99], v[180:181], v[92:93] op_sel:[1,1] op_sel_hi:[0,1] neg_lo:[0,1]
	v_pk_fma_f32 v[92:93], v[180:181], v[92:93], v[98:99] op_sel_hi:[1,0,1]
	s_waitcnt lgkmcnt(0)
	v_pk_mul_f32 v[98:99], v[66:67], v[92:93] op_sel:[1,1] op_sel_hi:[0,1] neg_hi:[1,0]
	s_nop 0
	v_pk_fma_f32 v[66:67], v[66:67], v[92:93], v[98:99] op_sel_hi:[1,0,1]
	v_pk_mul_f32 v[98:99], v[180:181], v[92:93] op_sel:[1,1] op_sel_hi:[0,1] neg_lo:[0,1]
	v_pk_fma_f32 v[20:21], v[180:181], v[92:93], v[98:99] op_sel_hi:[1,0,1]
	s_nop 0
	v_pk_mul_f32 v[92:93], v[68:69], v[20:21] op_sel:[1,1] op_sel_hi:[0,1] neg_hi:[1,0]
	s_nop 0
	v_pk_fma_f32 v[68:69], v[68:69], v[20:21], v[92:93] op_sel_hi:[1,0,1]
	v_mov_b32_e32 v10, v1
	v_pk_add_f32 v[104:105], v[16:17], v[52:53]
	v_pk_add_f32 v[16:17], v[16:17], v[52:53] neg_lo:[0,1] neg_hi:[0,1]
	v_pk_add_f32 v[52:53], v[18:19], v[70:71]
	v_pk_add_f32 v[18:19], v[18:19], v[70:71] neg_lo:[0,1] neg_hi:[0,1]
	v_mov_b32_e32 v92, v164
	v_mov_b32_e32 v20, v165
	v_mov_b32_e32 v98, v166
	v_mov_b32_e32 v10, v167
	v_mov_b32_e32 v100, v168
	v_mov_b32_e32 v50, v169
	v_mov_b32_e32 v102, v170
	v_mov_b32_e32 v21, v171
	v_pk_mul_f32 v[70:71], v[102:103], v[18:19] op_sel:[0,1] op_sel_hi:[0,0] neg_lo:[0,1]
	v_pk_fma_f32 v[18:19], v[92:93], v[18:19], v[70:71] op_sel_hi:[0,1,1]
	v_pk_add_f32 v[70:71], v[22:23], v[72:73]
	v_pk_add_f32 v[22:23], v[22:23], v[72:73] neg_lo:[0,1] neg_hi:[0,1]
	s_nop 0
	v_pk_mul_f32 v[72:73], v[50:51], v[22:23] op_sel:[0,1] op_sel_hi:[0,0] neg_lo:[0,1]
	v_pk_fma_f32 v[22:23], v[20:21], v[22:23], v[72:73] op_sel_hi:[0,1,1]
	v_pk_add_f32 v[72:73], v[24:25], v[74:75]
	v_pk_add_f32 v[24:25], v[24:25], v[74:75] neg_lo:[0,1] neg_hi:[0,1]
	s_nop 0
	v_pk_mul_f32 v[74:75], v[100:101], v[24:25] op_sel:[0,1] op_sel_hi:[0,0] neg_lo:[0,1]
	v_pk_fma_f32 v[24:25], v[98:99], v[24:25], v[74:75] op_sel_hi:[0,1,1]
	v_pk_add_f32 v[74:75], v[28:29], v[76:77]
	v_pk_add_f32 v[28:29], v[28:29], v[76:77] neg_lo:[0,1] neg_hi:[0,1]
	s_nop 0
	v_pk_mul_f32 v[76:77], v[10:11], v[28:29] op_sel:[0,1] op_sel_hi:[0,0] neg_lo:[0,1]
	v_pk_fma_f32 v[28:29], v[10:11], v[28:29], v[76:77] op_sel_hi:[0,1,1]
	v_pk_add_f32 v[76:77], v[26:27], v[78:79]
	v_pk_add_f32 v[26:27], v[26:27], v[78:79] neg_lo:[0,1] neg_hi:[0,1]
	s_nop 0
	v_pk_mul_f32 v[78:79], v[98:99], v[26:27] op_sel:[0,1] op_sel_hi:[0,0] neg_lo:[0,1]
	v_pk_fma_f32 v[26:27], v[100:101], v[26:27], v[78:79] op_sel_hi:[0,1,1]
	v_pk_add_f32 v[78:79], v[30:31], v[80:81]
	v_pk_add_f32 v[30:31], v[30:31], v[80:81] neg_lo:[0,1] neg_hi:[0,1]
	s_nop 0
	v_pk_mul_f32 v[80:81], v[20:21], v[30:31] op_sel:[0,1] op_sel_hi:[0,0] neg_lo:[0,1]
	v_pk_fma_f32 v[30:31], v[50:51], v[30:31], v[80:81] op_sel_hi:[0,1,1]
	v_pk_add_f32 v[80:81], v[32:33], v[82:83]
	v_pk_add_f32 v[32:33], v[32:33], v[82:83] neg_lo:[0,1] neg_hi:[0,1]
	s_nop 0
	v_pk_mul_f32 v[82:83], v[92:93], v[32:33] op_sel:[0,1] op_sel_hi:[0,0] neg_lo:[0,1]
	v_pk_fma_f32 v[32:33], v[102:103], v[32:33], v[82:83] op_sel_hi:[0,1,1]
	v_pk_add_f32 v[82:83], v[34:35], v[86:87]
	v_pk_add_f32 v[34:35], v[34:35], v[86:87] neg_lo:[0,1] neg_hi:[0,1]
	s_nop 0
	v_xor_b32_e32 v86, 0x80000000, v35
	v_mov_b32_e32 v87, v34
	v_pk_add_f32 v[34:35], v[36:37], v[88:89]
	v_pk_add_f32 v[36:37], v[36:37], v[88:89] neg_lo:[0,1] neg_hi:[0,1]
	s_nop 0
	v_pk_mul_f32 v[88:89], v[92:93], v[36:37] op_sel:[0,1] op_sel_hi:[0,0] neg_lo:[0,1]
	v_pk_fma_f32 v[36:37], v[102:103], v[36:37], v[88:89] op_sel_hi:[0,1,1] neg_lo:[1,0,0] neg_hi:[1,0,0]
	v_pk_add_f32 v[88:89], v[38:39], v[90:91]
	v_pk_add_f32 v[38:39], v[38:39], v[90:91] neg_lo:[0,1] neg_hi:[0,1]
	s_nop 0
	v_pk_mul_f32 v[90:91], v[20:21], v[38:39] op_sel:[0,1] op_sel_hi:[0,0] neg_lo:[0,1]
	v_pk_fma_f32 v[38:39], v[50:51], v[38:39], v[90:91] op_sel_hi:[0,1,1] neg_lo:[1,0,0] neg_hi:[1,0,0]
	v_pk_add_f32 v[90:91], v[40:41], v[84:85]
	v_pk_add_f32 v[40:41], v[40:41], v[84:85] neg_lo:[0,1] neg_hi:[0,1]
	s_nop 0
	v_pk_mul_f32 v[84:85], v[98:99], v[40:41] op_sel:[0,1] op_sel_hi:[0,0] neg_lo:[0,1]
	v_pk_fma_f32 v[40:41], v[100:101], v[40:41], v[84:85] op_sel_hi:[0,1,1] neg_lo:[1,0,0] neg_hi:[1,0,0]
	v_pk_add_f32 v[84:85], v[44:45], v[96:97]
	v_pk_add_f32 v[44:45], v[44:45], v[96:97] neg_lo:[0,1] neg_hi:[0,1]
	s_nop 0
	v_pk_mul_f32 v[96:97], v[10:11], v[44:45] op_sel:[0,1] op_sel_hi:[0,0] neg_lo:[0,1]
	v_pk_fma_f32 v[44:45], v[10:11], v[44:45], v[96:97] op_sel_hi:[0,1,1] neg_lo:[1,0,0] neg_hi:[1,0,0]
	v_pk_add_f32 v[96:97], v[42:43], v[94:95]
	v_pk_add_f32 v[42:43], v[42:43], v[94:95] neg_lo:[0,1] neg_hi:[0,1]
	s_nop 0
	v_pk_mul_f32 v[94:95], v[100:101], v[42:43] op_sel:[0,1] op_sel_hi:[0,0] neg_lo:[0,1]
	v_pk_fma_f32 v[42:43], v[98:99], v[42:43], v[94:95] op_sel_hi:[0,1,1] neg_lo:[1,0,0] neg_hi:[1,0,0]
	v_pk_add_f32 v[94:95], v[46:47], v[66:67]
	v_pk_add_f32 v[46:47], v[46:47], v[66:67] neg_lo:[0,1] neg_hi:[0,1]
	s_nop 0
	v_pk_mul_f32 v[66:67], v[50:51], v[46:47] op_sel:[0,1] op_sel_hi:[0,0] neg_lo:[0,1]
	v_pk_fma_f32 v[46:47], v[20:21], v[46:47], v[66:67] op_sel_hi:[0,1,1] neg_lo:[1,0,0] neg_hi:[1,0,0]
	v_pk_add_f32 v[66:67], v[48:49], v[68:69]
	v_pk_add_f32 v[48:49], v[48:49], v[68:69] neg_lo:[0,1] neg_hi:[0,1]
	s_nop 0
	v_pk_mul_f32 v[68:69], v[102:103], v[48:49] op_sel:[0,1] op_sel_hi:[0,0] neg_lo:[0,1]
	v_pk_fma_f32 v[48:49], v[92:93], v[48:49], v[68:69] op_sel_hi:[0,1,1] neg_lo:[1,0,0] neg_hi:[1,0,0]
	v_pk_add_f32 v[92:93], v[52:53], v[34:35]
	v_pk_add_f32 v[34:35], v[52:53], v[34:35] neg_lo:[0,1] neg_hi:[0,1]
	v_pk_add_f32 v[68:69], v[104:105], v[82:83]
	v_pk_mul_f32 v[52:53], v[50:51], v[34:35] op_sel:[0,1] op_sel_hi:[0,0] neg_lo:[0,1]
	v_pk_fma_f32 v[34:35], v[20:21], v[34:35], v[52:53] op_sel_hi:[0,1,1]
	v_pk_add_f32 v[52:53], v[70:71], v[88:89]
	v_pk_add_f32 v[70:71], v[70:71], v[88:89] neg_lo:[0,1] neg_hi:[0,1]
	v_pk_add_f32 v[82:83], v[104:105], v[82:83] neg_lo:[0,1] neg_hi:[0,1]
	v_pk_mul_f32 v[88:89], v[10:11], v[70:71] op_sel:[0,1] op_sel_hi:[0,0] neg_lo:[0,1]
	v_pk_fma_f32 v[70:71], v[10:11], v[70:71], v[88:89] op_sel_hi:[0,1,1]
	v_pk_add_f32 v[88:89], v[72:73], v[90:91]
	v_pk_add_f32 v[72:73], v[72:73], v[90:91] neg_lo:[0,1] neg_hi:[0,1]
	s_nop 0
	v_pk_mul_f32 v[90:91], v[20:21], v[72:73] op_sel:[0,1] op_sel_hi:[0,0] neg_lo:[0,1]
	v_pk_fma_f32 v[72:73], v[50:51], v[72:73], v[90:91] op_sel_hi:[0,1,1]
	v_pk_add_f32 v[90:91], v[74:75], v[84:85]
	v_pk_add_f32 v[74:75], v[74:75], v[84:85] neg_lo:[0,1] neg_hi:[0,1]
	s_nop 0
	v_xor_b32_e32 v84, 0x80000000, v75
	v_mov_b32_e32 v85, v74
	v_pk_add_f32 v[74:75], v[76:77], v[96:97]
	v_pk_add_f32 v[76:77], v[76:77], v[96:97] neg_lo:[0,1] neg_hi:[0,1]
	s_nop 0
	v_pk_mul_f32 v[96:97], v[20:21], v[76:77] op_sel:[0,1] op_sel_hi:[0,0] neg_lo:[0,1]
	v_pk_fma_f32 v[76:77], v[50:51], v[76:77], v[96:97] op_sel_hi:[0,1,1] neg_lo:[1,0,0] neg_hi:[1,0,0]
	v_pk_add_f32 v[96:97], v[78:79], v[94:95]
	v_pk_add_f32 v[78:79], v[78:79], v[94:95] neg_lo:[0,1] neg_hi:[0,1]
	s_nop 0
	v_pk_mul_f32 v[94:95], v[10:11], v[78:79] op_sel:[0,1] op_sel_hi:[0,0] neg_lo:[0,1]
	v_pk_fma_f32 v[78:79], v[10:11], v[78:79], v[94:95] op_sel_hi:[0,1,1] neg_lo:[1,0,0] neg_hi:[1,0,0]
	v_pk_add_f32 v[94:95], v[80:81], v[66:67]
	v_pk_add_f32 v[66:67], v[80:81], v[66:67] neg_lo:[0,1] neg_hi:[0,1]
	s_nop 0
	v_pk_mul_f32 v[80:81], v[50:51], v[66:67] op_sel:[0,1] op_sel_hi:[0,0] neg_lo:[0,1]
	v_pk_fma_f32 v[66:67], v[20:21], v[66:67], v[80:81] op_sel_hi:[0,1,1] neg_lo:[1,0,0] neg_hi:[1,0,0]
	v_pk_add_f32 v[80:81], v[68:69], v[90:91]
	v_pk_add_f32 v[68:69], v[68:69], v[90:91] neg_lo:[0,1] neg_hi:[0,1]
	v_pk_add_f32 v[90:91], v[92:93], v[74:75]
	v_pk_add_f32 v[74:75], v[92:93], v[74:75] neg_lo:[0,1] neg_hi:[0,1]
	s_nop 0
	v_pk_mul_f32 v[92:93], v[10:11], v[74:75] op_sel:[0,1] op_sel_hi:[0,0] neg_lo:[0,1]
	v_pk_fma_f32 v[74:75], v[10:11], v[74:75], v[92:93] op_sel_hi:[0,1,1]
	v_pk_add_f32 v[92:93], v[52:53], v[96:97]
	v_pk_add_f32 v[52:53], v[52:53], v[96:97] neg_lo:[0,1] neg_hi:[0,1]
	s_nop 0
	v_xor_b32_e32 v96, 0x80000000, v53
	v_mov_b32_e32 v97, v52
	v_pk_add_f32 v[52:53], v[88:89], v[94:95]
	v_pk_add_f32 v[88:89], v[88:89], v[94:95] neg_lo:[0,1] neg_hi:[0,1]
	s_nop 0
	v_pk_mul_f32 v[94:95], v[10:11], v[88:89] op_sel:[0,1] op_sel_hi:[0,0] neg_lo:[0,1]
	v_pk_fma_f32 v[88:89], v[10:11], v[88:89], v[94:95] op_sel_hi:[0,1,1] neg_lo:[1,0,0] neg_hi:[1,0,0]
	v_pk_add_f32 v[94:95], v[80:81], v[92:93]
	v_pk_add_f32 v[80:81], v[80:81], v[92:93] neg_lo:[0,1] neg_hi:[0,1]
	v_pk_add_f32 v[92:93], v[90:91], v[52:53]
	v_pk_add_f32 v[52:53], v[90:91], v[52:53] neg_lo:[0,1] neg_hi:[0,1]
	s_nop 0
	v_xor_b32_e32 v90, 0x80000000, v53
	v_mov_b32_e32 v91, v52
	v_pk_add_f32 v[52:53], v[94:95], v[92:93]
	v_pk_add_f32 v[92:93], v[94:95], v[92:93] neg_lo:[0,1] neg_hi:[0,1]
	v_pk_add_f32 v[94:95], v[80:81], v[90:91]
	v_pk_add_f32 v[80:81], v[80:81], v[90:91] neg_lo:[0,1] neg_hi:[0,1]
	v_pk_add_f32 v[90:91], v[68:69], v[96:97]
	v_pk_add_f32 v[68:69], v[68:69], v[96:97] neg_lo:[0,1] neg_hi:[0,1]
	v_pk_add_f32 v[96:97], v[74:75], v[88:89]
	v_pk_add_f32 v[74:75], v[74:75], v[88:89] neg_lo:[0,1] neg_hi:[0,1]
	s_nop 0
	v_xor_b32_e32 v88, 0x80000000, v75
	v_mov_b32_e32 v89, v74
	v_pk_add_f32 v[74:75], v[90:91], v[96:97]
	v_pk_add_f32 v[90:91], v[90:91], v[96:97] neg_lo:[0,1] neg_hi:[0,1]
	v_pk_add_f32 v[96:97], v[68:69], v[88:89]
	v_pk_add_f32 v[68:69], v[68:69], v[88:89] neg_lo:[0,1] neg_hi:[0,1]
	v_pk_add_f32 v[88:89], v[82:83], v[84:85]
	v_pk_add_f32 v[82:83], v[82:83], v[84:85] neg_lo:[0,1] neg_hi:[0,1]
	v_pk_add_f32 v[84:85], v[34:35], v[76:77]
	v_pk_add_f32 v[34:35], v[34:35], v[76:77] neg_lo:[0,1] neg_hi:[0,1]
	s_nop 0
	v_pk_mul_f32 v[76:77], v[10:11], v[34:35] op_sel:[0,1] op_sel_hi:[0,0] neg_lo:[0,1]
	v_pk_fma_f32 v[34:35], v[10:11], v[34:35], v[76:77] op_sel_hi:[0,1,1]
	v_pk_add_f32 v[76:77], v[70:71], v[78:79]
	v_pk_add_f32 v[70:71], v[70:71], v[78:79] neg_lo:[0,1] neg_hi:[0,1]
	s_nop 0
	v_xor_b32_e32 v78, 0x80000000, v71
	v_mov_b32_e32 v79, v70
	v_pk_add_f32 v[70:71], v[72:73], v[66:67]
	v_pk_add_f32 v[66:67], v[72:73], v[66:67] neg_lo:[0,1] neg_hi:[0,1]
	s_nop 0
	v_pk_mul_f32 v[72:73], v[10:11], v[66:67] op_sel:[0,1] op_sel_hi:[0,0] neg_lo:[0,1]
	v_pk_fma_f32 v[66:67], v[10:11], v[66:67], v[72:73] op_sel_hi:[0,1,1] neg_lo:[1,0,0] neg_hi:[1,0,0]
	v_pk_add_f32 v[72:73], v[88:89], v[76:77]
	v_pk_add_f32 v[76:77], v[88:89], v[76:77] neg_lo:[0,1] neg_hi:[0,1]
	v_pk_add_f32 v[88:89], v[84:85], v[70:71]
	v_pk_add_f32 v[70:71], v[84:85], v[70:71] neg_lo:[0,1] neg_hi:[0,1]
	s_nop 0
	v_xor_b32_e32 v84, 0x80000000, v71
	v_mov_b32_e32 v85, v70
	v_pk_add_f32 v[70:71], v[72:73], v[88:89]
	v_pk_add_f32 v[72:73], v[72:73], v[88:89] neg_lo:[0,1] neg_hi:[0,1]
	v_pk_add_f32 v[88:89], v[76:77], v[84:85]
	v_pk_add_f32 v[76:77], v[76:77], v[84:85] neg_lo:[0,1] neg_hi:[0,1]
	v_pk_add_f32 v[84:85], v[82:83], v[78:79]
	v_pk_add_f32 v[78:79], v[82:83], v[78:79] neg_lo:[0,1] neg_hi:[0,1]
	v_pk_add_f32 v[82:83], v[34:35], v[66:67]
	v_pk_add_f32 v[34:35], v[34:35], v[66:67] neg_lo:[0,1] neg_hi:[0,1]
	s_nop 0
	v_xor_b32_e32 v66, 0x80000000, v35
	v_mov_b32_e32 v67, v34
	v_pk_add_f32 v[34:35], v[84:85], v[82:83]
	v_pk_add_f32 v[82:83], v[84:85], v[82:83] neg_lo:[0,1] neg_hi:[0,1]
	v_pk_add_f32 v[84:85], v[78:79], v[66:67]
	v_pk_add_f32 v[66:67], v[78:79], v[66:67] neg_lo:[0,1] neg_hi:[0,1]
	v_pk_add_f32 v[78:79], v[16:17], v[86:87]
	v_pk_add_f32 v[16:17], v[16:17], v[86:87] neg_lo:[0,1] neg_hi:[0,1]
	v_pk_add_f32 v[86:87], v[18:19], v[36:37]
	v_pk_add_f32 v[18:19], v[18:19], v[36:37] neg_lo:[0,1] neg_hi:[0,1]
	s_nop 0
	v_pk_mul_f32 v[36:37], v[50:51], v[18:19] op_sel:[0,1] op_sel_hi:[0,0] neg_lo:[0,1]
	v_pk_fma_f32 v[18:19], v[20:21], v[18:19], v[36:37] op_sel_hi:[0,1,1]
	v_pk_add_f32 v[36:37], v[22:23], v[38:39]
	v_pk_add_f32 v[22:23], v[22:23], v[38:39] neg_lo:[0,1] neg_hi:[0,1]
	s_nop 0
	v_pk_mul_f32 v[38:39], v[10:11], v[22:23] op_sel:[0,1] op_sel_hi:[0,0] neg_lo:[0,1]
	v_pk_fma_f32 v[22:23], v[10:11], v[22:23], v[38:39] op_sel_hi:[0,1,1]
	v_pk_add_f32 v[38:39], v[24:25], v[40:41]
	v_pk_add_f32 v[24:25], v[24:25], v[40:41] neg_lo:[0,1] neg_hi:[0,1]
	s_nop 0
	v_pk_mul_f32 v[40:41], v[20:21], v[24:25] op_sel:[0,1] op_sel_hi:[0,0] neg_lo:[0,1]
	v_pk_fma_f32 v[24:25], v[50:51], v[24:25], v[40:41] op_sel_hi:[0,1,1]
	v_pk_add_f32 v[40:41], v[28:29], v[44:45]
	v_pk_add_f32 v[28:29], v[28:29], v[44:45] neg_lo:[0,1] neg_hi:[0,1]
	s_nop 0
	v_xor_b32_e32 v44, 0x80000000, v29
	v_mov_b32_e32 v45, v28
	v_pk_add_f32 v[28:29], v[26:27], v[42:43]
	v_pk_add_f32 v[26:27], v[26:27], v[42:43] neg_lo:[0,1] neg_hi:[0,1]
	s_nop 0
	v_pk_mul_f32 v[42:43], v[20:21], v[26:27] op_sel:[0,1] op_sel_hi:[0,0] neg_lo:[0,1]
	v_pk_fma_f32 v[26:27], v[50:51], v[26:27], v[42:43] op_sel_hi:[0,1,1] neg_lo:[1,0,0] neg_hi:[1,0,0]
	v_pk_add_f32 v[42:43], v[30:31], v[46:47]
	v_pk_add_f32 v[30:31], v[30:31], v[46:47] neg_lo:[0,1] neg_hi:[0,1]
	s_nop 0
	v_pk_mul_f32 v[46:47], v[10:11], v[30:31] op_sel:[0,1] op_sel_hi:[0,0] neg_lo:[0,1]
	v_pk_fma_f32 v[30:31], v[10:11], v[30:31], v[46:47] op_sel_hi:[0,1,1] neg_lo:[1,0,0] neg_hi:[1,0,0]
	v_pk_add_f32 v[46:47], v[32:33], v[48:49]
	v_pk_add_f32 v[32:33], v[32:33], v[48:49] neg_lo:[0,1] neg_hi:[0,1]
	s_nop 0
	v_pk_mul_f32 v[48:49], v[50:51], v[32:33] op_sel:[0,1] op_sel_hi:[0,0] neg_lo:[0,1]
	v_pk_fma_f32 v[20:21], v[20:21], v[32:33], v[48:49] op_sel_hi:[0,1,1] neg_lo:[1,0,0] neg_hi:[1,0,0]
	v_pk_add_f32 v[48:49], v[86:87], v[28:29]
	v_pk_add_f32 v[28:29], v[86:87], v[28:29] neg_lo:[0,1] neg_hi:[0,1]
	v_pk_add_f32 v[32:33], v[78:79], v[40:41]
	v_pk_add_f32 v[40:41], v[78:79], v[40:41] neg_lo:[0,1] neg_hi:[0,1]
	v_pk_mul_f32 v[78:79], v[10:11], v[28:29] op_sel:[0,1] op_sel_hi:[0,0] neg_lo:[0,1]
	v_pk_fma_f32 v[28:29], v[10:11], v[28:29], v[78:79] op_sel_hi:[0,1,1]
	v_pk_add_f32 v[78:79], v[36:37], v[42:43]
	v_pk_add_f32 v[36:37], v[36:37], v[42:43] neg_lo:[0,1] neg_hi:[0,1]
	s_nop 0
	v_xor_b32_e32 v42, 0x80000000, v37
	v_mov_b32_e32 v43, v36
	v_pk_add_f32 v[36:37], v[38:39], v[46:47]
	v_pk_add_f32 v[38:39], v[38:39], v[46:47] neg_lo:[0,1] neg_hi:[0,1]
	s_nop 0
	v_pk_mul_f32 v[46:47], v[10:11], v[38:39] op_sel:[0,1] op_sel_hi:[0,0] neg_lo:[0,1]
	v_pk_fma_f32 v[38:39], v[10:11], v[38:39], v[46:47] op_sel_hi:[0,1,1] neg_lo:[1,0,0] neg_hi:[1,0,0]
	v_pk_add_f32 v[46:47], v[32:33], v[78:79]
	v_pk_add_f32 v[32:33], v[32:33], v[78:79] neg_lo:[0,1] neg_hi:[0,1]
	v_pk_add_f32 v[78:79], v[48:49], v[36:37]
	v_pk_add_f32 v[36:37], v[48:49], v[36:37] neg_lo:[0,1] neg_hi:[0,1]
	s_nop 0
	v_pk_add_f32 v[86:87], v[32:33], v[36:37] op_sel:[0,1] op_sel_hi:[1,0] neg_lo:[0,1]
	v_pk_add_f32 v[32:33], v[32:33], v[36:37] op_sel:[0,1] op_sel_hi:[1,0] neg_hi:[0,1]
	v_pk_add_f32 v[48:49], v[40:41], v[42:43]
	v_pk_add_f32 v[40:41], v[40:41], v[42:43] neg_lo:[0,1] neg_hi:[0,1]
	v_pk_add_f32 v[42:43], v[28:29], v[38:39]
	v_pk_add_f32 v[28:29], v[28:29], v[38:39] neg_lo:[0,1] neg_hi:[0,1]
	v_pk_add_f32 v[36:37], v[46:47], v[78:79] neg_lo:[0,1] neg_hi:[0,1]
	v_xor_b32_e32 v38, 0x80000000, v29
	v_mov_b32_e32 v39, v28
	v_pk_add_f32 v[28:29], v[48:49], v[42:43]
	v_pk_add_f32 v[42:43], v[48:49], v[42:43] neg_lo:[0,1] neg_hi:[0,1]
	v_pk_add_f32 v[48:49], v[40:41], v[38:39]
	v_pk_add_f32 v[38:39], v[40:41], v[38:39] neg_lo:[0,1] neg_hi:[0,1]
	v_pk_add_f32 v[40:41], v[16:17], v[44:45]
	v_pk_add_f32 v[16:17], v[16:17], v[44:45] neg_lo:[0,1] neg_hi:[0,1]
	v_pk_add_f32 v[44:45], v[18:19], v[26:27]
	v_pk_add_f32 v[18:19], v[18:19], v[26:27] neg_lo:[0,1] neg_hi:[0,1]
	s_nop 0
	v_pk_mul_f32 v[26:27], v[10:11], v[18:19] op_sel:[0,1] op_sel_hi:[0,0] neg_lo:[0,1]
	v_pk_fma_f32 v[18:19], v[10:11], v[18:19], v[26:27] op_sel_hi:[0,1,1]
	v_pk_add_f32 v[26:27], v[22:23], v[30:31]
	v_pk_add_f32 v[22:23], v[22:23], v[30:31] neg_lo:[0,1] neg_hi:[0,1]
	s_nop 0
	v_xor_b32_e32 v30, 0x80000000, v23
	v_mov_b32_e32 v31, v22
	v_pk_add_f32 v[22:23], v[24:25], v[20:21]
	v_pk_add_f32 v[20:21], v[24:25], v[20:21] neg_lo:[0,1] neg_hi:[0,1]
	s_nop 0
	v_pk_mul_f32 v[24:25], v[10:11], v[20:21] op_sel:[0,1] op_sel_hi:[0,0] neg_lo:[0,1]
	v_pk_fma_f32 v[20:21], v[10:11], v[20:21], v[24:25] op_sel_hi:[0,1,1] neg_lo:[1,0,0] neg_hi:[1,0,0]
	v_pk_add_f32 v[24:25], v[40:41], v[26:27]
	v_pk_add_f32 v[26:27], v[40:41], v[26:27] neg_lo:[0,1] neg_hi:[0,1]
	v_pk_add_f32 v[40:41], v[44:45], v[22:23]
	v_pk_add_f32 v[22:23], v[44:45], v[22:23] neg_lo:[0,1] neg_hi:[0,1]
	s_nop 0
	v_xor_b32_e32 v44, 0x80000000, v23
	v_mov_b32_e32 v45, v22
	v_pk_add_f32 v[22:23], v[24:25], v[40:41]
	v_pk_add_f32 v[24:25], v[24:25], v[40:41] neg_lo:[0,1] neg_hi:[0,1]
	v_pk_add_f32 v[40:41], v[26:27], v[44:45]
	v_pk_add_f32 v[26:27], v[26:27], v[44:45] neg_lo:[0,1] neg_hi:[0,1]
	v_pk_add_f32 v[44:45], v[16:17], v[30:31]
	v_pk_add_f32 v[16:17], v[16:17], v[30:31] neg_lo:[0,1] neg_hi:[0,1]
	v_pk_add_f32 v[30:31], v[18:19], v[20:21]
	v_pk_add_f32 v[18:19], v[18:19], v[20:21] neg_lo:[0,1] neg_hi:[0,1]
	s_nop 0
	v_xor_b32_e32 v20, 0x80000000, v19
	v_mov_b32_e32 v21, v18
	v_pk_add_f32 v[18:19], v[44:45], v[30:31]
	v_pk_add_f32 v[30:31], v[44:45], v[30:31] neg_lo:[0,1] neg_hi:[0,1]
	v_pk_add_f32 v[44:45], v[16:17], v[20:21]
	v_pk_add_f32 v[16:17], v[16:17], v[20:21] neg_lo:[0,1] neg_hi:[0,1]
	v_pk_add_f32 v[20:21], v[46:47], v[78:79]
	ds_write2_b64 v13, v[52:53], v[20:21] offset1:16
	ds_write2_b64 v15, v[70:71], v[22:23] offset0:32 offset1:48
	ds_write2_b64 v51, v[74:75], v[28:29] offset0:64 offset1:80
	ds_write2_b64 v54, v[34:35], v[18:19] offset0:96 offset1:112
	ds_write2_b64 v55, v[94:95], v[86:87] offset0:128 offset1:144
	ds_write2_b64 v56, v[88:89], v[40:41] offset0:160 offset1:176
	ds_write2_b64 v57, v[96:97], v[48:49] offset0:192 offset1:208
	ds_write2_b64 v58, v[84:85], v[44:45] offset0:224 offset1:240
	ds_write2_b64 v59, v[92:93], v[36:37] offset1:16
	ds_write2_b64 v60, v[72:73], v[24:25] offset0:32 offset1:48
	ds_write2_b64 v61, v[90:91], v[42:43] offset0:64 offset1:80
	ds_write2_b64 v62, v[82:83], v[30:31] offset0:96 offset1:112
	ds_write2_b64 v63, v[80:81], v[32:33] offset0:128 offset1:144
	ds_write2_b64 v64, v[76:77], v[26:27] offset0:160 offset1:176
	ds_write2_b64 v65, v[68:69], v[38:39] offset0:192 offset1:208
	ds_write2_b64 v101, v[66:67], v[16:17] offset0:224 offset1:240
	v_mov_b32_e32 v10, v173
	s_waitcnt lgkmcnt(0)
	s_barrier
	v_lshl_add_u32 v10, v10, 3, 0
	ds_read_b64 v[16:17], v10
	ds_read_b64 v[80:81], v10 offset:4224
	ds_read_b64 v[78:79], v10 offset:8448
	ds_read_b64 v[76:77], v10 offset:12672
	ds_read_b64 v[74:75], v10 offset:16896
	ds_read_b64 v[72:73], v10 offset:21120
	ds_read_b64 v[70:71], v10 offset:25344
	ds_read_b64 v[68:69], v10 offset:29568
	ds_read_b64 v[24:25], v10 offset:33792
	ds_read_b64 v[62:63], v10 offset:38016
	ds_read_b64 v[60:61], v10 offset:42240
	ds_read_b64 v[58:59], v10 offset:46464
	ds_read_b64 v[54:55], v10 offset:50688
	ds_read_b64 v[50:51], v10 offset:54912
	ds_read_b64 v[46:47], v10 offset:59136
	ds_read_b64 v[44:45], v10 offset:63360
	v_add_u32_e32 v13, 0x10800, v10
	v_add_u32_e32 v15, 0x11880, v10
	v_add_u32_e32 v20, 0x12900, v10
	v_add_u32_e32 v21, 0x13980, v10
	ds_read_b64 v[18:19], v13
	ds_read_b64 v[66:67], v15
	ds_read_b64 v[64:65], v20
	ds_read_b64 v[38:39], v21
	v_add_u32_e32 v13, 0x14a00, v10
	v_add_u32_e32 v15, 0x15a80, v10
	v_add_u32_e32 v20, 0x16b00, v10
	v_add_u32_e32 v21, 0x17b80, v10
	ds_read_b64 v[30:31], v13
	ds_read_b64 v[56:57], v15
	ds_read_b64 v[52:53], v20
	ds_read_b64 v[48:49], v21
	v_add_u32_e32 v13, 0x18c00, v10
	v_add_u32_e32 v15, 0x19c80, v10
	v_add_u32_e32 v20, 0x1ad00, v10
	v_add_u32_e32 v21, 0x1bd80, v10
	ds_read_b64 v[82:83], v13
	ds_read_b64 v[42:43], v15
	ds_read_b64 v[40:41], v20
	ds_read_b64 v[36:37], v21
	v_add_u32_e32 v13, 0x1ce00, v10
	v_add_u32_e32 v15, 0x1de80, v10
	v_add_u32_e32 v20, 0x1ef00, v10
	v_add_u32_e32 v10, 0x1ff80, v10
	ds_read_b64 v[34:35], v13
	ds_read_b64 v[32:33], v15
	ds_read_b64 v[28:29], v20
	ds_read_b64 v[26:27], v10
	v_pk_fma_f32 v[84:85], v[178:179], s[90:91], v[178:179] op_sel:[1,0,0] op_sel_hi:[0,1,1]
	v_pk_mul_f32 v[20:21], v[178:179], v[84:85] op_sel:[1,1] op_sel_hi:[0,1] neg_lo:[0,1]
	v_pk_fma_f32 v[86:87], v[178:179], v[84:85], v[20:21] op_sel_hi:[1,0,1]
	v_mov_b32_e32 v10, v1
	v_pk_mul_f32 v[20:21], v[178:179], v[86:87] op_sel:[1,1] op_sel_hi:[0,1] neg_lo:[0,1]
	v_pk_fma_f32 v[88:89], v[178:179], v[86:87], v[20:21] op_sel_hi:[1,0,1]
	v_mov_b32_e32 v13, v171
	v_pk_mul_f32 v[20:21], v[178:179], v[88:89] op_sel:[1,1] op_sel_hi:[0,1] neg_lo:[0,1]
	v_pk_fma_f32 v[90:91], v[178:179], v[88:89], v[20:21] op_sel_hi:[1,0,1]
	v_mov_b32_e32 v10, v164
	v_pk_mul_f32 v[20:21], v[178:179], v[90:91] op_sel:[1,1] op_sel_hi:[0,1] neg_lo:[0,1]
	v_pk_fma_f32 v[92:93], v[178:179], v[90:91], v[20:21] op_sel_hi:[1,0,1]
	s_waitcnt lgkmcnt(14)
	v_fmac_f32_e32 v16, 0, v17
	v_pk_mul_f32 v[20:21], v[178:179], v[92:93] op_sel:[1,1] op_sel_hi:[0,1] neg_lo:[0,1]
	v_pk_fma_f32 v[94:95], v[178:179], v[92:93], v[20:21] op_sel_hi:[1,0,1]
	v_readlane_b32 s70, v251, 22
	v_pk_mul_f32 v[20:21], v[178:179], v[94:95] op_sel:[1,1] op_sel_hi:[0,1] neg_lo:[0,1]
	v_pk_fma_f32 v[96:97], v[178:179], v[94:95], v[20:21] op_sel_hi:[1,0,1]
	v_readlane_b32 s71, v251, 23
	v_pk_mul_f32 v[20:21], v[178:179], v[96:97] op_sel:[1,1] op_sel_hi:[0,1] neg_lo:[0,1]
	v_pk_fma_f32 v[98:99], v[178:179], v[96:97], v[20:21] op_sel_hi:[1,0,1]
	s_movk_i32 s10, 0x1000
	v_pk_mul_f32 v[20:21], v[178:179], v[98:99] op_sel:[1,1] op_sel_hi:[0,1] neg_lo:[0,1]
	v_pk_fma_f32 v[100:101], v[178:179], v[98:99], v[20:21] op_sel_hi:[1,0,1]
	s_movk_i32 s11, 0x2000
	v_pk_mul_f32 v[20:21], v[178:179], v[100:101] op_sel:[1,1] op_sel_hi:[0,1] neg_lo:[0,1]
	v_pk_fma_f32 v[102:103], v[178:179], v[100:101], v[20:21] op_sel_hi:[1,0,1]
	s_movk_i32 s13, 0x5000
	v_pk_mul_f32 v[20:21], v[178:179], v[102:103] op_sel:[1,1] op_sel_hi:[0,1] neg_lo:[0,1]
	v_pk_fma_f32 v[104:105], v[178:179], v[102:103], v[20:21] op_sel_hi:[1,0,1]
	s_movk_i32 s12, 0x6000
	v_pk_mul_f32 v[20:21], v[178:179], v[104:105] op_sel:[1,1] op_sel_hi:[0,1] neg_lo:[0,1]
	v_pk_fma_f32 v[106:107], v[178:179], v[104:105], v[20:21] op_sel_hi:[1,0,1]
	s_movk_i32 s16, 0x7000
	v_pk_mul_f32 v[20:21], v[178:179], v[106:107] op_sel:[1,1] op_sel_hi:[0,1] neg_lo:[0,1]
	v_pk_fma_f32 v[108:109], v[178:179], v[106:107], v[20:21] op_sel_hi:[1,0,1]
	s_mov_b32 s80, 0x3f74fa0b
	v_pk_mul_f32 v[20:21], v[178:179], v[108:109] op_sel:[1,1] op_sel_hi:[0,1] neg_lo:[0,1]
	v_pk_fma_f32 v[110:111], v[178:179], v[108:109], v[20:21] op_sel_hi:[1,0,1]
	s_mov_b32 s81, 0xbe94a031
	v_pk_mul_f32 v[20:21], v[178:179], v[110:111] op_sel:[1,1] op_sel_hi:[0,1] neg_lo:[0,1]
	v_pk_fma_f32 v[112:113], v[178:179], v[110:111], v[20:21] op_sel_hi:[1,0,1]
	s_mov_b32 s20, 0x3f61c598
	v_pk_mul_f32 v[20:21], v[178:179], v[112:113] op_sel:[1,1] op_sel_hi:[0,1] neg_lo:[0,1]
	v_pk_fma_f32 v[20:21], v[178:179], v[112:113], v[20:21] op_sel_hi:[1,0,1]
	s_mov_b32 s21, 0xbef15aea
	v_pk_mul_f32 v[114:115], v[178:179], v[20:21] op_sel:[1,1] op_sel_hi:[0,1] neg_lo:[0,1]
	v_pk_fma_f32 v[114:115], v[178:179], v[20:21], v[114:115] op_sel_hi:[1,0,1]
	v_mul_f32_e32 v18, v18, v20
	v_pk_mul_f32 v[116:117], v[178:179], v[114:115] op_sel:[1,1] op_sel_hi:[0,1] neg_lo:[0,1]
	v_pk_fma_f32 v[116:117], v[178:179], v[114:115], v[116:117] op_sel_hi:[1,0,1]
	v_fmac_f32_e32 v18, v19, v21
	v_pk_mul_f32 v[118:119], v[178:179], v[116:117] op_sel:[1,1] op_sel_hi:[0,1] neg_lo:[0,1]
	v_pk_fma_f32 v[118:119], v[178:179], v[116:117], v[118:119] op_sel_hi:[1,0,1]
	v_add_f32_e32 v17, v16, v18
	v_pk_mul_f32 v[120:121], v[178:179], v[118:119] op_sel:[1,1] op_sel_hi:[0,1] neg_lo:[0,1]
	v_pk_fma_f32 v[120:121], v[178:179], v[118:119], v[120:121] op_sel_hi:[1,0,1]
	s_mov_b32 s40, s45
	v_pk_mul_f32 v[122:123], v[178:179], v[120:121] op_sel:[1,1] op_sel_hi:[0,1] neg_lo:[0,1]
	v_pk_fma_f32 v[122:123], v[178:179], v[120:121], v[122:123] op_sel_hi:[1,0,1]
	s_mov_b32 s41, s94
	v_pk_mul_f32 v[124:125], v[178:179], v[122:123] op_sel:[1,1] op_sel_hi:[0,1] neg_lo:[0,1]
	v_pk_fma_f32 v[124:125], v[178:179], v[122:123], v[124:125] op_sel_hi:[1,0,1]
	s_mov_b32 s86, 0x3f226799
	v_pk_mul_f32 v[126:127], v[178:179], v[124:125] op_sel:[1,1] op_sel_hi:[0,1] neg_lo:[0,1]
	v_pk_fma_f32 v[126:127], v[178:179], v[124:125], v[126:127] op_sel_hi:[1,0,1]
	s_mov_b32 s87, 0xbf45e403
	v_pk_mul_f32 v[128:129], v[178:179], v[126:127] op_sel:[1,1] op_sel_hi:[0,1] neg_lo:[0,1]
	v_pk_fma_f32 v[128:129], v[178:179], v[126:127], v[128:129] op_sel_hi:[1,0,1]
	s_mov_b32 s24, 0x3f0e39da
	v_pk_mul_f32 v[130:131], v[178:179], v[128:129] op_sel:[1,1] op_sel_hi:[0,1] neg_lo:[0,1]
	v_pk_fma_f32 v[130:131], v[178:179], v[128:129], v[130:131] op_sel_hi:[1,0,1]
	s_mov_b32 s25, 0xbf54db31
	v_pk_mul_f32 v[132:133], v[178:179], v[130:131] op_sel:[1,1] op_sel_hi:[0,1] neg_lo:[0,1]
	v_pk_fma_f32 v[132:133], v[178:179], v[130:131], v[132:133] op_sel_hi:[1,0,1]
	s_mov_b32 s88, 0x3ef15aea
	v_pk_mul_f32 v[134:135], v[178:179], v[132:133] op_sel:[1,1] op_sel_hi:[0,1] neg_lo:[0,1]
	v_pk_fma_f32 v[134:135], v[178:179], v[132:133], v[134:135] op_sel_hi:[1,0,1]
	s_mov_b32 s89, 0xbf61c598
	v_pk_mul_f32 v[136:137], v[178:179], v[134:135] op_sel:[1,1] op_sel_hi:[0,1] neg_lo:[0,1]
	v_pk_fma_f32 v[136:137], v[178:179], v[134:135], v[136:137] op_sel_hi:[1,0,1]
	s_mov_b32 s18, 0x3ec3ef15
	v_pk_mul_f32 v[138:139], v[178:179], v[136:137] op_sel:[1,1] op_sel_hi:[0,1] neg_lo:[0,1]
	v_pk_fma_f32 v[138:139], v[178:179], v[136:137], v[138:139] op_sel_hi:[1,0,1]
	s_mov_b32 s19, 0xbf6c835e
	v_pk_mul_f32 v[140:141], v[178:179], v[138:139] op_sel:[1,1] op_sel_hi:[0,1] neg_lo:[0,1]
	v_pk_fma_f32 v[140:141], v[178:179], v[138:139], v[140:141] op_sel_hi:[1,0,1]
	s_mov_b32 s92, 0x3e94a031
	v_pk_mul_f32 v[142:143], v[178:179], v[140:141] op_sel:[1,1] op_sel_hi:[0,1] neg_lo:[0,1]
	v_pk_fma_f32 v[22:23], v[178:179], v[140:141], v[142:143] op_sel_hi:[1,0,1]
	s_waitcnt lgkmcnt(0)
	v_pk_mul_f32 v[142:143], v[26:27], v[22:23] op_sel:[1,1] op_sel_hi:[0,1] neg_hi:[1,0]
	s_mov_b32 s93, 0xbf74fa0b
	v_pk_fma_f32 v[26:27], v[26:27], v[22:23], v[142:143] op_sel_hi:[1,0,1]
	v_pk_mul_f32 v[22:23], v[28:29], v[140:141] op_sel:[1,1] op_sel_hi:[0,1] neg_hi:[1,0]
	s_mov_b32 s82, 0x3f54db31
	v_pk_fma_f32 v[28:29], v[28:29], v[140:141], v[22:23] op_sel_hi:[1,0,1]
	v_pk_mul_f32 v[22:23], v[32:33], v[138:139] op_sel:[1,1] op_sel_hi:[0,1] neg_hi:[1,0]
	s_mov_b32 s83, 0xbf0e39da
	v_pk_fma_f32 v[32:33], v[32:33], v[138:139], v[22:23] op_sel_hi:[1,0,1]
	v_pk_mul_f32 v[22:23], v[34:35], v[136:137] op_sel:[1,1] op_sel_hi:[0,1] neg_hi:[1,0]
	s_mov_b32 s28, 0x3f45e403
	v_pk_fma_f32 v[34:35], v[34:35], v[136:137], v[22:23] op_sel_hi:[1,0,1]
	v_pk_mul_f32 v[22:23], v[36:37], v[134:135] op_sel:[1,1] op_sel_hi:[0,1] neg_hi:[1,0]
	s_mov_b32 s29, 0xbf226799
	v_pk_fma_f32 v[36:37], v[36:37], v[134:135], v[22:23] op_sel_hi:[1,0,1]
	v_pk_mul_f32 v[22:23], v[40:41], v[132:133] op_sel:[1,1] op_sel_hi:[0,1] neg_hi:[1,0]
	s_mov_b32 s36, s97
	v_pk_fma_f32 v[40:41], v[40:41], v[132:133], v[22:23] op_sel_hi:[1,0,1]
	v_pk_mul_f32 v[22:23], v[42:43], v[130:131] op_sel:[1,1] op_sel_hi:[0,1] neg_hi:[1,0]
	s_mov_b32 s37, s95
	v_pk_fma_f32 v[42:43], v[42:43], v[130:131], v[22:23] op_sel_hi:[1,0,1]
	v_pk_mul_f32 v[22:23], v[82:83], v[128:129] op_sel:[1,1] op_sel_hi:[0,1] neg_hi:[1,0]
	s_mov_b32 s96, s95
	v_pk_fma_f32 v[22:23], v[82:83], v[128:129], v[22:23] op_sel_hi:[1,0,1]
	v_pk_mul_f32 v[82:83], v[48:49], v[126:127] op_sel:[1,1] op_sel_hi:[0,1] neg_hi:[1,0]
	s_mov_b32 s23, s25
	v_pk_fma_f32 v[48:49], v[48:49], v[126:127], v[82:83] op_sel_hi:[1,0,1]
	v_pk_mul_f32 v[82:83], v[52:53], v[124:125] op_sel:[1,1] op_sel_hi:[0,1] neg_hi:[1,0]
	s_mov_b32 s22, s83
	v_pk_fma_f32 v[52:53], v[52:53], v[124:125], v[82:83] op_sel_hi:[1,0,1]
	v_pk_mul_f32 v[82:83], v[56:57], v[122:123] op_sel:[1,1] op_sel_hi:[0,1] neg_hi:[1,0]
	s_mov_b32 s26, s29
	v_pk_fma_f32 v[56:57], v[56:57], v[122:123], v[82:83] op_sel_hi:[1,0,1]
	v_pk_mul_f32 v[82:83], v[30:31], v[120:121] op_sel:[1,1] op_sel_hi:[0,1] neg_hi:[1,0]
	s_mov_b32 s27, s87
	v_pk_fma_f32 v[30:31], v[30:31], v[120:121], v[82:83] op_sel_hi:[1,0,1]
	v_pk_mul_f32 v[82:83], v[38:39], v[118:119] op_sel:[1,1] op_sel_hi:[0,1] neg_hi:[1,0]
	s_movk_i32 s39, 0x2000
	v_pk_fma_f32 v[38:39], v[38:39], v[118:119], v[82:83] op_sel_hi:[1,0,1]
	v_pk_mul_f32 v[82:83], v[64:65], v[116:117] op_sel:[1,1] op_sel_hi:[0,1] neg_hi:[1,0]
	s_mov_b32 s44, s94
	v_pk_fma_f32 v[64:65], v[64:65], v[116:117], v[82:83] op_sel_hi:[1,0,1]
	v_pk_mul_f32 v[82:83], v[66:67], v[114:115] op_sel:[1,1] op_sel_hi:[0,1] neg_hi:[1,0]
	v_mov_b32_e32 v118, v164
	v_pk_fma_f32 v[66:67], v[66:67], v[114:115], v[82:83] op_sel_hi:[1,0,1]
	v_pk_mul_f32 v[82:83], v[44:45], v[112:113] op_sel:[1,1] op_sel_hi:[0,1] neg_hi:[1,0]
	v_mov_b32_e32 v120, v166
	v_pk_fma_f32 v[44:45], v[44:45], v[112:113], v[82:83] op_sel_hi:[1,0,1]
	v_pk_mul_f32 v[82:83], v[46:47], v[110:111] op_sel:[1,1] op_sel_hi:[0,1] neg_hi:[1,0]
	v_mov_b32_e32 v122, v168
	v_pk_fma_f32 v[46:47], v[46:47], v[110:111], v[82:83] op_sel_hi:[1,0,1]
	v_pk_mul_f32 v[82:83], v[50:51], v[108:109] op_sel:[1,1] op_sel_hi:[0,1] neg_hi:[1,0]
	v_mov_b32_e32 v124, v170
	v_pk_fma_f32 v[50:51], v[50:51], v[108:109], v[82:83] op_sel_hi:[1,0,1]
	v_pk_mul_f32 v[82:83], v[54:55], v[106:107] op_sel:[1,1] op_sel_hi:[0,1] neg_hi:[1,0]
	s_movk_i32 s33, 0x5000
	v_pk_fma_f32 v[54:55], v[54:55], v[106:107], v[82:83] op_sel_hi:[1,0,1]
	v_pk_mul_f32 v[82:83], v[58:59], v[104:105] op_sel:[1,1] op_sel_hi:[0,1] neg_hi:[1,0]
	s_nop 0
	v_pk_fma_f32 v[58:59], v[58:59], v[104:105], v[82:83] op_sel_hi:[1,0,1]
	v_pk_mul_f32 v[82:83], v[60:61], v[102:103] op_sel:[1,1] op_sel_hi:[0,1] neg_hi:[1,0]
	s_nop 0
	v_pk_fma_f32 v[60:61], v[60:61], v[102:103], v[82:83] op_sel_hi:[1,0,1]
	v_pk_mul_f32 v[82:83], v[62:63], v[100:101] op_sel:[1,1] op_sel_hi:[0,1] neg_hi:[1,0]
	s_nop 0
	v_pk_fma_f32 v[62:63], v[62:63], v[100:101], v[82:83] op_sel_hi:[1,0,1]
	v_pk_mul_f32 v[82:83], v[24:25], v[98:99] op_sel:[1,1] op_sel_hi:[0,1] neg_hi:[1,0]
	s_nop 0
	v_pk_fma_f32 v[24:25], v[24:25], v[98:99], v[82:83] op_sel_hi:[1,0,1]
	v_pk_mul_f32 v[82:83], v[68:69], v[96:97] op_sel:[1,1] op_sel_hi:[0,1] neg_hi:[1,0]
	v_add_f32_e32 v22, v24, v22
	v_pk_fma_f32 v[68:69], v[68:69], v[96:97], v[82:83] op_sel_hi:[1,0,1]
	v_pk_mul_f32 v[82:83], v[70:71], v[94:95] op_sel:[1,1] op_sel_hi:[0,1] neg_hi:[1,0]
	v_add_f32_e32 v20, v17, v22
	v_pk_fma_f32 v[70:71], v[70:71], v[94:95], v[82:83] op_sel_hi:[1,0,1]
	v_pk_mul_f32 v[82:83], v[72:73], v[92:93] op_sel:[1,1] op_sel_hi:[0,1] neg_hi:[1,0]
	v_mov_b32_e32 v94, v170
	v_pk_fma_f32 v[72:73], v[72:73], v[92:93], v[82:83] op_sel_hi:[1,0,1]
	v_pk_mul_f32 v[82:83], v[74:75], v[90:91] op_sel:[1,1] op_sel_hi:[0,1] neg_hi:[1,0]
	v_mov_b32_e32 v92, v169
	v_pk_fma_f32 v[74:75], v[74:75], v[90:91], v[82:83] op_sel_hi:[1,0,1]
	v_pk_mul_f32 v[82:83], v[76:77], v[88:89] op_sel:[1,1] op_sel_hi:[0,1] neg_hi:[1,0]
	v_mov_b32_e32 v90, v168
	v_pk_fma_f32 v[76:77], v[76:77], v[88:89], v[82:83] op_sel_hi:[1,0,1]
	v_pk_mul_f32 v[82:83], v[78:79], v[86:87] op_sel:[1,1] op_sel_hi:[0,1] neg_hi:[1,0]
	v_mov_b32_e32 v88, v167
	v_pk_fma_f32 v[78:79], v[78:79], v[86:87], v[82:83] op_sel_hi:[1,0,1]
	v_pk_mul_f32 v[82:83], v[84:85], v[80:81] op_sel:[1,1] op_sel_hi:[1,0] neg_hi:[0,1]
	v_mov_b32_e32 v86, v166
	v_pk_fma_f32 v[80:81], v[80:81], v[84:85], v[82:83] op_sel_hi:[1,0,1]
	v_mov_b32_e32 v84, v165
	v_pk_add_f32 v[96:97], v[80:81], v[66:67]
	v_pk_add_f32 v[66:67], v[80:81], v[66:67] neg_lo:[0,1] neg_hi:[0,1]
	s_nop 0
	v_sub_f32_e32 v82, v25, v23
	v_pk_mul_f32 v[80:81], v[94:95], v[66:67] op_sel:[0,1] op_sel_hi:[0,0] neg_lo:[0,1]
	v_pk_fma_f32 v[80:81], v[10:11], v[66:67], v[80:81] op_sel_hi:[0,1,1]
	v_pk_add_f32 v[66:67], v[78:79], v[64:65]
	v_pk_add_f32 v[64:65], v[78:79], v[64:65] neg_lo:[0,1] neg_hi:[0,1]
	s_nop 0
	v_pk_mul_f32 v[78:79], v[92:93], v[64:65] op_sel:[0,1] op_sel_hi:[0,0] neg_lo:[0,1]
	v_pk_fma_f32 v[64:65], v[84:85], v[64:65], v[78:79] op_sel_hi:[0,1,1]
	v_pk_add_f32 v[78:79], v[76:77], v[38:39]
	v_pk_add_f32 v[38:39], v[76:77], v[38:39] neg_lo:[0,1] neg_hi:[0,1]
	s_barrier
	v_pk_mul_f32 v[76:77], v[90:91], v[38:39] op_sel:[0,1] op_sel_hi:[0,0] neg_lo:[0,1]
	v_pk_fma_f32 v[76:77], v[86:87], v[38:39], v[76:77] op_sel_hi:[0,1,1]
	v_pk_add_f32 v[38:39], v[74:75], v[30:31]
	v_pk_add_f32 v[30:31], v[74:75], v[30:31] neg_lo:[0,1] neg_hi:[0,1]
	s_nop 0
	v_pk_mul_f32 v[74:75], v[88:89], v[30:31] op_sel:[0,1] op_sel_hi:[0,0] neg_lo:[0,1]
	v_pk_fma_f32 v[30:31], v[88:89], v[30:31], v[74:75] op_sel_hi:[0,1,1]
	v_pk_add_f32 v[74:75], v[72:73], v[56:57]
	v_pk_add_f32 v[56:57], v[72:73], v[56:57] neg_lo:[0,1] neg_hi:[0,1]
	v_sub_f32_e32 v22, v17, v22
	v_pk_mul_f32 v[72:73], v[86:87], v[56:57] op_sel:[0,1] op_sel_hi:[0,0] neg_lo:[0,1]
	v_pk_fma_f32 v[72:73], v[90:91], v[56:57], v[72:73] op_sel_hi:[0,1,1]
	v_pk_add_f32 v[56:57], v[70:71], v[52:53]
	v_pk_add_f32 v[52:53], v[70:71], v[52:53] neg_lo:[0,1] neg_hi:[0,1]
	v_ashrrev_i32_e32 v15, 31, v14
	v_pk_mul_f32 v[70:71], v[84:85], v[52:53] op_sel:[0,1] op_sel_hi:[0,0] neg_lo:[0,1]
	v_pk_fma_f32 v[52:53], v[92:93], v[52:53], v[70:71] op_sel_hi:[0,1,1]
	v_pk_add_f32 v[70:71], v[68:69], v[48:49]
	v_pk_add_f32 v[48:49], v[68:69], v[48:49] neg_lo:[0,1] neg_hi:[0,1]
	v_lshl_add_u64 v[14:15], v[14:15], 2, s[70:71]
	v_pk_mul_f32 v[68:69], v[10:11], v[48:49] op_sel:[0,1] op_sel_hi:[0,0] neg_lo:[0,1]
	v_pk_fma_f32 v[98:99], v[94:95], v[48:49], v[68:69] op_sel_hi:[0,1,1]
	v_pk_add_f32 v[48:49], v[62:63], v[42:43]
	v_pk_add_f32 v[42:43], v[62:63], v[42:43] neg_lo:[0,1] neg_hi:[0,1]
	s_nop 0
	v_pk_mul_f32 v[62:63], v[10:11], v[42:43] op_sel:[0,1] op_sel_hi:[0,0] neg_lo:[0,1]
	v_pk_fma_f32 v[62:63], v[94:95], v[42:43], v[62:63] op_sel_hi:[0,1,1] neg_lo:[1,0,0] neg_hi:[1,0,0]
	v_pk_add_f32 v[42:43], v[60:61], v[40:41]
	v_pk_add_f32 v[40:41], v[60:61], v[40:41] neg_lo:[0,1] neg_hi:[0,1]
	s_nop 0
	v_pk_mul_f32 v[60:61], v[84:85], v[40:41] op_sel:[0,1] op_sel_hi:[0,0] neg_lo:[0,1]
	v_pk_fma_f32 v[100:101], v[92:93], v[40:41], v[60:61] op_sel_hi:[0,1,1] neg_lo:[1,0,0] neg_hi:[1,0,0]
	v_pk_add_f32 v[60:61], v[58:59], v[36:37]
	v_pk_add_f32 v[36:37], v[58:59], v[36:37] neg_lo:[0,1] neg_hi:[0,1]
	s_nop 0
	v_pk_mul_f32 v[40:41], v[86:87], v[36:37] op_sel:[0,1] op_sel_hi:[0,0] neg_lo:[0,1]
	v_pk_fma_f32 v[58:59], v[90:91], v[36:37], v[40:41] op_sel_hi:[0,1,1] neg_lo:[1,0,0] neg_hi:[1,0,0]
	v_pk_add_f32 v[40:41], v[54:55], v[34:35]
	v_pk_add_f32 v[34:35], v[54:55], v[34:35] neg_lo:[0,1] neg_hi:[0,1]
	v_pk_add_f32 v[54:55], v[46:47], v[28:29]
	v_pk_mul_f32 v[36:37], v[88:89], v[34:35] op_sel:[0,1] op_sel_hi:[0,0] neg_lo:[0,1]
	v_pk_fma_f32 v[34:35], v[88:89], v[34:35], v[36:37] op_sel_hi:[0,1,1] neg_lo:[1,0,0] neg_hi:[1,0,0]
	v_pk_add_f32 v[36:37], v[50:51], v[32:33]
	v_pk_add_f32 v[32:33], v[50:51], v[32:33] neg_lo:[0,1] neg_hi:[0,1]
	v_pk_add_f32 v[28:29], v[46:47], v[28:29] neg_lo:[0,1] neg_hi:[0,1]
	v_pk_mul_f32 v[50:51], v[90:91], v[32:33] op_sel:[0,1] op_sel_hi:[0,0] neg_lo:[0,1]
	v_pk_fma_f32 v[86:87], v[86:87], v[32:33], v[50:51] op_sel_hi:[0,1,1] neg_lo:[1,0,0] neg_hi:[1,0,0]
	v_pk_mul_f32 v[32:33], v[92:93], v[28:29] op_sel:[0,1] op_sel_hi:[0,0] neg_lo:[0,1]
	v_pk_fma_f32 v[46:47], v[84:85], v[28:29], v[32:33] op_sel_hi:[0,1,1] neg_lo:[1,0,0] neg_hi:[1,0,0]
	v_pk_add_f32 v[28:29], v[44:45], v[26:27]
	v_pk_add_f32 v[26:27], v[44:45], v[26:27] neg_lo:[0,1] neg_hi:[0,1]
	v_pk_add_f32 v[50:51], v[66:67], v[42:43]
	v_pk_mul_f32 v[32:33], v[94:95], v[26:27] op_sel:[0,1] op_sel_hi:[0,0] neg_lo:[0,1]
	v_pk_fma_f32 v[90:91], v[10:11], v[26:27], v[32:33] op_sel_hi:[0,1,1] neg_lo:[1,0,0] neg_hi:[1,0,0]
	v_pk_add_f32 v[32:33], v[96:97], v[48:49] neg_lo:[0,1] neg_hi:[0,1]
	v_pk_add_f32 v[26:27], v[96:97], v[48:49]
	v_pk_mul_f32 v[44:45], v[92:93], v[32:33] op_sel:[0,1] op_sel_hi:[0,0] neg_lo:[0,1]
	v_pk_fma_f32 v[48:49], v[84:85], v[32:33], v[44:45] op_sel_hi:[0,1,1]
	v_pk_add_f32 v[32:33], v[66:67], v[42:43] neg_lo:[0,1] neg_hi:[0,1]
	v_pk_add_f32 v[44:45], v[78:79], v[60:61] neg_lo:[0,1] neg_hi:[0,1]
	v_pk_mul_f32 v[42:43], v[88:89], v[32:33] op_sel:[0,1] op_sel_hi:[0,0] neg_lo:[0,1]
	v_pk_fma_f32 v[32:33], v[88:89], v[32:33], v[42:43] op_sel_hi:[0,1,1]
	v_pk_add_f32 v[42:43], v[78:79], v[60:61]
	v_pk_mul_f32 v[60:61], v[84:85], v[44:45] op_sel:[0,1] op_sel_hi:[0,0] neg_lo:[0,1]
	v_pk_add_f32 v[78:79], v[74:75], v[36:37]
	v_pk_add_f32 v[36:37], v[74:75], v[36:37] neg_lo:[0,1] neg_hi:[0,1]
	v_pk_fma_f32 v[68:69], v[92:93], v[44:45], v[60:61] op_sel_hi:[0,1,1]
	v_pk_mul_f32 v[44:45], v[84:85], v[36:37] op_sel:[0,1] op_sel_hi:[0,0] neg_lo:[0,1]
	v_pk_fma_f32 v[74:75], v[92:93], v[36:37], v[44:45] op_sel_hi:[0,1,1] neg_lo:[1,0,0] neg_hi:[1,0,0]
	v_pk_add_f32 v[36:37], v[56:57], v[54:55] neg_lo:[0,1] neg_hi:[0,1]
	v_pk_add_f32 v[60:61], v[56:57], v[54:55]
	v_pk_mul_f32 v[44:45], v[88:89], v[36:37] op_sel:[0,1] op_sel_hi:[0,0] neg_lo:[0,1]
	v_pk_fma_f32 v[44:45], v[88:89], v[36:37], v[44:45] op_sel_hi:[0,1,1] neg_lo:[1,0,0] neg_hi:[1,0,0]
	v_pk_add_f32 v[36:37], v[70:71], v[28:29]
	v_pk_add_f32 v[28:29], v[70:71], v[28:29] neg_lo:[0,1] neg_hi:[0,1]
	v_pk_add_f32 v[66:67], v[26:27], v[78:79]
	v_pk_mul_f32 v[54:55], v[92:93], v[28:29] op_sel:[0,1] op_sel_hi:[0,0] neg_lo:[0,1]
	v_pk_add_f32 v[26:27], v[26:27], v[78:79] neg_lo:[0,1] neg_hi:[0,1]
	v_pk_fma_f32 v[94:95], v[84:85], v[28:29], v[54:55] op_sel_hi:[0,1,1] neg_lo:[1,0,0] neg_hi:[1,0,0]
	v_pk_mul_f32 v[28:29], v[88:89], v[26:27] op_sel:[0,1] op_sel_hi:[0,0] neg_lo:[0,1]
	v_pk_fma_f32 v[26:27], v[88:89], v[26:27], v[28:29] op_sel_hi:[0,1,1]
	v_pk_add_f32 v[28:29], v[42:43], v[36:37] neg_lo:[0,1] neg_hi:[0,1]
	v_pk_add_f32 v[70:71], v[42:43], v[36:37]
	v_pk_mul_f32 v[36:37], v[88:89], v[28:29] op_sel:[0,1] op_sel_hi:[0,0] neg_lo:[0,1]
	v_pk_fma_f32 v[36:37], v[88:89], v[28:29], v[36:37] op_sel_hi:[0,1,1] neg_lo:[1,0,0] neg_hi:[1,0,0]
	v_pk_add_f32 v[28:29], v[48:49], v[74:75] neg_lo:[0,1] neg_hi:[0,1]
	v_pk_add_f32 v[54:55], v[48:49], v[74:75]
	v_pk_mul_f32 v[42:43], v[88:89], v[28:29] op_sel:[0,1] op_sel_hi:[0,0] neg_lo:[0,1]
	v_pk_fma_f32 v[28:29], v[88:89], v[28:29], v[42:43] op_sel_hi:[0,1,1]
	v_pk_add_f32 v[42:43], v[68:69], v[94:95] neg_lo:[0,1] neg_hi:[0,1]
	v_pk_add_f32 v[74:75], v[80:81], v[62:63]
	v_pk_mul_f32 v[48:49], v[88:89], v[42:43] op_sel:[0,1] op_sel_hi:[0,0] neg_lo:[0,1]
	v_pk_fma_f32 v[42:43], v[88:89], v[42:43], v[48:49] op_sel_hi:[0,1,1] neg_lo:[1,0,0] neg_hi:[1,0,0]
	v_pk_add_f32 v[48:49], v[80:81], v[62:63] neg_lo:[0,1] neg_hi:[0,1]
	v_pk_add_f32 v[56:57], v[68:69], v[94:95]
	v_pk_mul_f32 v[62:63], v[92:93], v[48:49] op_sel:[0,1] op_sel_hi:[0,0] neg_lo:[0,1]
	v_pk_fma_f32 v[94:95], v[84:85], v[48:49], v[62:63] op_sel_hi:[0,1,1]
	v_pk_add_f32 v[48:49], v[64:65], v[100:101] neg_lo:[0,1] neg_hi:[0,1]
	v_pk_add_f32 v[68:69], v[64:65], v[100:101]
	v_pk_mul_f32 v[62:63], v[88:89], v[48:49] op_sel:[0,1] op_sel_hi:[0,0] neg_lo:[0,1]
	v_pk_add_f32 v[64:65], v[76:77], v[58:59]
	v_pk_add_f32 v[58:59], v[76:77], v[58:59] neg_lo:[0,1] neg_hi:[0,1]
	v_pk_fma_f32 v[48:49], v[88:89], v[48:49], v[62:63] op_sel_hi:[0,1,1]
	v_pk_mul_f32 v[62:63], v[84:85], v[58:59] op_sel:[0,1] op_sel_hi:[0,0] neg_lo:[0,1]
	v_pk_fma_f32 v[96:97], v[92:93], v[58:59], v[62:63] op_sel_hi:[0,1,1]
	v_pk_add_f32 v[58:59], v[72:73], v[86:87] neg_lo:[0,1] neg_hi:[0,1]
	v_pk_add_f32 v[76:77], v[52:53], v[46:47]
	v_pk_add_f32 v[46:47], v[52:53], v[46:47] neg_lo:[0,1] neg_hi:[0,1]
	v_pk_add_f32 v[62:63], v[72:73], v[86:87]
	v_pk_mul_f32 v[72:73], v[84:85], v[58:59] op_sel:[0,1] op_sel_hi:[0,0] neg_lo:[0,1]
	v_pk_mul_f32 v[52:53], v[88:89], v[46:47] op_sel:[0,1] op_sel_hi:[0,0] neg_lo:[0,1]
	v_pk_fma_f32 v[86:87], v[92:93], v[58:59], v[72:73] op_sel_hi:[0,1,1] neg_lo:[1,0,0] neg_hi:[1,0,0]
	v_pk_fma_f32 v[58:59], v[88:89], v[46:47], v[52:53] op_sel_hi:[0,1,1] neg_lo:[1,0,0] neg_hi:[1,0,0]
	v_pk_add_f32 v[46:47], v[98:99], v[90:91]
	v_pk_add_f32 v[52:53], v[98:99], v[90:91] neg_lo:[0,1] neg_hi:[0,1]
	v_pk_add_f32 v[80:81], v[64:65], v[46:47]
	v_pk_add_f32 v[46:47], v[64:65], v[46:47] neg_lo:[0,1] neg_hi:[0,1]
	s_nop 0
	v_pk_mul_f32 v[64:65], v[88:89], v[46:47] op_sel:[0,1] op_sel_hi:[0,0] neg_lo:[0,1]
	v_pk_fma_f32 v[64:65], v[88:89], v[46:47], v[64:65] op_sel_hi:[0,1,1] neg_lo:[1,0,0] neg_hi:[1,0,0]
	v_pk_add_f32 v[46:47], v[94:95], v[86:87] neg_lo:[0,1] neg_hi:[0,1]
	v_pk_mul_f32 v[72:73], v[92:93], v[52:53] op_sel:[0,1] op_sel_hi:[0,0] neg_lo:[0,1]
	v_pk_add_f32 v[78:79], v[74:75], v[62:63]
	v_pk_add_f32 v[62:63], v[74:75], v[62:63] neg_lo:[0,1] neg_hi:[0,1]
	v_pk_fma_f32 v[52:53], v[84:85], v[52:53], v[72:73] op_sel_hi:[0,1,1] neg_lo:[1,0,0] neg_hi:[1,0,0]
	v_pk_mul_f32 v[74:75], v[88:89], v[46:47] op_sel:[0,1] op_sel_hi:[0,0] neg_lo:[0,1]
	v_pk_fma_f32 v[46:47], v[88:89], v[46:47], v[74:75] op_sel_hi:[0,1,1]
	v_pk_add_f32 v[74:75], v[96:97], v[52:53]
	v_pk_add_f32 v[52:53], v[96:97], v[52:53] neg_lo:[0,1] neg_hi:[0,1]
	v_add_f32_e32 v30, v30, v34
	v_pk_mul_f32 v[84:85], v[88:89], v[52:53] op_sel:[0,1] op_sel_hi:[0,0] neg_lo:[0,1]
	v_sub_f32_e32 v34, v16, v18
	v_sub_f32_e32 v13, v51, v61
	v_pk_fma_f32 v[52:53], v[88:89], v[52:53], v[84:85] op_sel_hi:[0,1,1] neg_lo:[1,0,0] neg_hi:[1,0,0]
	v_sub_f32_e32 v51, v34, v82
	v_sub_f32_e32 v25, v29, v43
	v_sub_f32_e32 v43, v31, v35
	v_sub_f32_e32 v35, v49, v59
	v_sub_f32_e32 v10, v47, v53
	v_add_f32_e32 v49, v50, v60
	v_add_f32_e32 v50, v68, v76
	v_add_f32_e32 v53, v51, v30
	v_sub_f32_e32 v23, v27, v37
	v_sub_f32_e32 v27, v55, v57
	v_add_f32_e32 v38, v38, v40
	v_add_f32_e32 v40, v78, v80
	v_add_f32_e32 v55, v53, v50
	v_add_f32_e32 v16, v55, v40
	v_sub_f32_e32 v41, v39, v41
	v_add_f32_e32 v21, v20, v38
	global_store_dword v[14:15], v16, off offset:2048
	v_add_co_u32_e32 v16, vcc, s10, v14
	v_add_f32_e32 v47, v66, v70
	v_add_f32_e32 v24, v21, v49
	v_add_f32_e32 v32, v32, v44
	v_sub_f32_e32 v44, v22, v41
	v_addc_co_u32_e32 v17, vcc, 0, v15, vcc
	v_pk_mul_f32 v[72:73], v[88:89], v[62:63] op_sel:[0,1] op_sel_hi:[0,0] neg_lo:[0,1]
	v_add_f32_e32 v19, v24, v47
	v_add_f32_e32 v54, v54, v56
	v_add_f32_e32 v56, v44, v32
	v_add_co_u32_e32 v18, vcc, s11, v14
	v_add_f32_e32 v34, v34, v82
	v_pk_fma_f32 v[62:63], v[88:89], v[62:63], v[72:73] op_sel_hi:[0,1,1]
	v_pk_add_f32 v[72:73], v[94:95], v[86:87]
	global_store_dword v[14:15], v19, off
	v_add_f32_e32 v57, v56, v54
	v_addc_co_u32_e32 v19, vcc, 0, v15, vcc
	v_add_f32_e32 v48, v48, v58
	v_sub_f32_e32 v58, v34, v43
	global_store_dword v[18:19], v57, off offset:-4096
	v_add_f32_e32 v57, v72, v74
	v_add_f32_e32 v59, v58, v48
	v_sub_f32_e32 v20, v20, v38
	v_sub_f32_e32 v37, v33, v45
	v_sub_f32_e32 v45, v69, v77
	v_add_f32_e32 v60, v59, v57
	v_add_f32_e32 v26, v26, v36
	v_sub_f32_e32 v36, v20, v13
	v_sub_f32_e32 v30, v51, v30
	global_store_dword v[16:17], v60, off offset:2048
	v_add_f32_e32 v16, v36, v26
	v_add_f32_e32 v38, v62, v64
	v_sub_f32_e32 v51, v30, v45
	global_store_dword v[18:19], v16, off
	v_add_f32_e32 v16, v51, v38
	global_store_dword v[18:19], v16, off offset:2048
	v_add_co_u32_e32 v16, vcc, s78, v14
	v_add_f32_e32 v22, v22, v41
	s_nop 0
	v_addc_co_u32_e32 v17, vcc, 0, v15, vcc
	v_add_f32_e32 v28, v28, v42
	v_sub_f32_e32 v41, v22, v37
	v_add_co_u32_e32 v18, vcc, s43, v14
	v_add_f32_e32 v42, v41, v28
	s_nop 0
	v_addc_co_u32_e32 v19, vcc, 0, v15, vcc
	v_add_f32_e32 v34, v34, v43
	global_store_dword v[18:19], v42, off offset:-4096
	v_add_f32_e32 v42, v46, v52
	v_sub_f32_e32 v43, v34, v35
	v_sub_f32_e32 v39, v67, v71
	v_add_f32_e32 v46, v43, v42
	v_sub_f32_e32 v21, v21, v49
	v_sub_f32_e32 v33, v79, v81
	global_store_dword v[16:17], v46, off offset:2048
	v_sub_f32_e32 v16, v21, v39
	v_sub_f32_e32 v46, v53, v50
	global_store_dword v[18:19], v16, off
	v_sub_f32_e32 v16, v46, v33
	global_store_dword v[18:19], v16, off offset:2048
	v_add_co_u32_e32 v16, vcc, s13, v14
	v_sub_f32_e32 v32, v44, v32
	s_nop 0
	v_addc_co_u32_e32 v17, vcc, 0, v15, vcc
	v_add_co_u32_e32 v18, vcc, s12, v14
	v_sub_f32_e32 v44, v32, v27
	s_nop 0
	v_addc_co_u32_e32 v19, vcc, 0, v15, vcc
	v_sub_f32_e32 v31, v73, v75
	global_store_dword v[18:19], v44, off offset:-4096
	v_sub_f32_e32 v44, v58, v48
	v_sub_f32_e32 v48, v44, v31
	v_add_f32_e32 v20, v20, v13
	v_sub_f32_e32 v29, v63, v65
	global_store_dword v[16:17], v48, off offset:2048
	v_sub_f32_e32 v13, v20, v23
	v_add_f32_e32 v30, v30, v45
	v_add_co_u32_e32 v16, vcc, s16, v14
	global_store_dword v[18:19], v13, off
	v_sub_f32_e32 v13, v30, v29
	v_addc_co_u32_e32 v17, vcc, 0, v15, vcc
	global_store_dword v[18:19], v13, off offset:2048
	v_add_f32_e32 v22, v22, v37
	v_add_co_u32_e32 v18, vcc, s8, v14
	v_sub_f32_e32 v13, v22, v25
	s_nop 0
	v_addc_co_u32_e32 v19, vcc, 0, v15, vcc
	global_store_dword v[18:19], v13, off offset:-4096
	v_add_f32_e32 v13, v34, v35
	v_sub_f32_e32 v34, v13, v10
	global_store_dword v[16:17], v34, off offset:2048
	v_sub_f32_e32 v16, v24, v47
	global_store_dword v[18:19], v16, off
	v_sub_f32_e32 v16, v55, v40
	global_store_dword v[18:19], v16, off offset:2048
	v_add_co_u32_e32 v16, vcc, s9, v14
	v_sub_f32_e32 v24, v56, v54
	s_nop 0
	v_addc_co_u32_e32 v17, vcc, 0, v15, vcc
	v_add_co_u32_e32 v18, vcc, s7, v14
	v_add_f32_e32 v10, v13, v10
	s_nop 0
	v_addc_co_u32_e32 v19, vcc, 0, v15, vcc
	global_store_dword v[18:19], v24, off offset:-4096
	v_sub_f32_e32 v24, v59, v57
	global_store_dword v[16:17], v24, off offset:2048
	v_sub_f32_e32 v16, v36, v26
	global_store_dword v[18:19], v16, off
	v_sub_f32_e32 v16, v51, v38
	global_store_dword v[18:19], v16, off offset:2048
	v_add_co_u32_e32 v16, vcc, s5, v14
	v_sub_f32_e32 v24, v41, v28
	s_nop 0
	v_addc_co_u32_e32 v17, vcc, 0, v15, vcc
	v_add_co_u32_e32 v18, vcc, s6, v14
	s_nop 1
	v_addc_co_u32_e32 v19, vcc, 0, v15, vcc
	global_store_dword v[18:19], v24, off offset:-4096
	v_sub_f32_e32 v24, v43, v42
	global_store_dword v[16:17], v24, off offset:2048
	v_add_f32_e32 v16, v21, v39
	global_store_dword v[18:19], v16, off
	v_add_f32_e32 v16, v46, v33
	global_store_dword v[18:19], v16, off offset:2048
	v_add_co_u32_e32 v16, vcc, s4, v14
	v_add_f32_e32 v21, v32, v27
	s_nop 0
	v_addc_co_u32_e32 v17, vcc, 0, v15, vcc
	v_add_co_u32_e32 v18, vcc, s1, v14
	s_nop 1
	v_addc_co_u32_e32 v19, vcc, 0, v15, vcc
	global_store_dword v[18:19], v21, off offset:-4096
	v_add_f32_e32 v21, v44, v31
	global_store_dword v[16:17], v21, off offset:2048
	v_add_f32_e32 v16, v20, v23
	global_store_dword v[18:19], v16, off
	v_add_f32_e32 v16, v30, v29
	v_add_co_u32_e32 v14, vcc, s0, v14
	global_store_dword v[18:19], v16, off offset:2048
	v_add_f32_e32 v16, v22, v25
	v_addc_co_u32_e32 v15, vcc, 0, v15, vcc
	global_store_dword v[14:15], v16, off
	global_store_dword v[14:15], v10, off offset:2048
	v_mov_b32_e32 v10, v183
	v_mov_b32_e32 v14, v184
	v_mov_b32_e32 v18, v182
	s_movk_i32 s0, 0xfe00
	v_sub_u32_e32 v13, 0x4000, v18
	v_cmp_eq_u32_e32 vcc, 0, v18
	v_cmp_eq_u32_e64 s[0:1], s0, v18
	v_cmp_eq_u32_e64 s[4:5], s48, v18
	v_cndmask_b32_e64 v20, v13, 0, vcc
	v_sub_u32_e32 v13, 0x3e00, v18
	v_cndmask_b32_e64 v22, v13, 0, s[0:1]
	v_sub_u32_e32 v13, 0x3c00, v18
	v_ashrrev_i32_e32 v21, 31, v20
	v_ashrrev_i32_e32 v23, 31, v22
	v_cndmask_b32_e64 v24, v13, 0, s[4:5]
	v_lshl_add_u64 v[20:21], v[20:21], 1, s[2:3]
	v_lshl_add_u64 v[22:23], v[22:23], 1, s[2:3]
	v_ashrrev_i32_e32 v25, 31, v24
	v_sub_u32_e32 v13, 0x3a00, v18
	v_cmp_eq_u32_e64 s[6:7], s49, v18
	v_lshl_add_u64 v[24:25], v[24:25], 1, s[2:3]
	global_load_ushort v15, v[20:21], off
	s_nop 0
	global_load_ushort v22, v[22:23], off
	s_nop 0
	global_load_ushort v23, v[24:25], off
	v_cndmask_b32_e64 v20, v13, 0, s[6:7]
	v_ashrrev_i32_e32 v21, 31, v20
	v_ashrrev_i32_e32 v19, 31, v18
	v_lshl_add_u64 v[20:21], v[20:21], 1, s[2:3]
	v_lshl_add_u64 v[16:17], v[18:19], 1, s[76:77]
	global_load_ushort v20, v[20:21], off
	s_nop 0
	global_load_ushort v13, v[16:17], off offset:3072
	v_sub_u32_e32 v24, 0x3800, v18
	v_sub_u32_e32 v26, 0x3600, v18
	v_sub_u32_e32 v28, 0x3400, v18
	v_sub_u32_e32 v32, 0x3200, v18
	v_cmp_eq_u32_e64 s[8:9], s59, v18
	s_mov_b32 s48, s21
	s_mov_b32 s49, s20
	s_mov_b32 s59, s82
	s_waitcnt vmcnt(4)
	v_lshlrev_b32_e32 v15, 16, v15
	v_cndmask_b32_e64 v19, -v15, v15, vcc
	s_waitcnt vmcnt(3)
	v_lshlrev_b32_e32 v15, 16, v22
	v_cndmask_b32_e64 v31, -v15, v15, s[0:1]
	s_waitcnt vmcnt(2)
	v_lshlrev_b32_e32 v15, 16, v23
	v_cndmask_b32_e64 v30, -v15, v15, s[4:5]
	v_cmp_eq_u32_e64 s[4:5], s51, v18
	s_waitcnt vmcnt(1)
	v_lshlrev_b32_e32 v15, 16, v20
	v_add_co_u32_e32 v20, vcc, s10, v16
	v_cndmask_b32_e64 v15, -v15, v15, s[6:7]
	s_nop 0
	v_addc_co_u32_e32 v21, vcc, 0, v17, vcc
	v_add_co_u32_e32 v22, vcc, s11, v16
	v_cmp_eq_u32_e64 s[6:7], s50, v18
	s_nop 0
	v_addc_co_u32_e32 v23, vcc, 0, v17, vcc
	v_cmp_eq_u32_e64 s[0:1], s57, v18
	v_cndmask_b32_e64 v24, v24, 0, s[6:7]
	v_cndmask_b32_e64 v26, v26, 0, s[4:5]
	v_cndmask_b32_e64 v28, v28, 0, s[0:1]
	v_cmp_eq_u32_e32 vcc, s58, v18
	v_ashrrev_i32_e32 v25, 31, v24
	v_ashrrev_i32_e32 v27, 31, v26
	v_ashrrev_i32_e32 v29, 31, v28
	v_cndmask_b32_e64 v32, v32, 0, vcc
	v_lshl_add_u64 v[24:25], v[24:25], 1, s[2:3]
	v_lshl_add_u64 v[26:27], v[26:27], 1, s[2:3]
	v_lshl_add_u64 v[28:29], v[28:29], 1, s[2:3]
	v_ashrrev_i32_e32 v33, 31, v32
	v_lshl_add_u64 v[32:33], v[32:33], 1, s[2:3]
	global_load_ushort v34, v[24:25], off
	s_nop 0
	global_load_ushort v26, v[26:27], off
	s_nop 0
	global_load_ushort v27, v[28:29], off
	s_nop 0
	global_load_ushort v28, v[32:33], off
	v_sub_u32_e32 v24, 0x3000, v18
	v_cndmask_b32_e64 v24, v24, 0, s[8:9]
	v_ashrrev_i32_e32 v25, 31, v24
	v_lshl_add_u64 v[24:25], v[24:25], 1, s[2:3]
	global_load_ushort v24, v[24:25], off
	s_nop 0
	global_load_ushort v32, v[20:21], off offset:3072
	v_cmp_eq_u32_e64 s[10:11], s79, v18
	s_mov_b32 s79, s80
	s_waitcnt vmcnt(6)
	v_lshlrev_b32_e32 v13, 16, v13
	s_mov_b32 s57, s18
	s_mov_b32 s58, s83
	s_waitcnt vmcnt(5)
	v_lshlrev_b32_e32 v25, 16, v34
	v_cndmask_b32_e64 v33, -v25, v25, s[6:7]
	s_waitcnt vmcnt(4)
	v_lshlrev_b32_e32 v25, 16, v26
	v_cndmask_b32_e64 v34, -v25, v25, s[4:5]
	s_waitcnt vmcnt(3)
	v_lshlrev_b32_e32 v25, 16, v27
	v_cndmask_b32_e64 v35, -v25, v25, s[0:1]
	v_add_co_u32_e64 v26, s[0:1], s78, v16
	s_waitcnt vmcnt(2)
	v_lshlrev_b32_e32 v25, 16, v28
	s_waitcnt vmcnt(1)
	v_lshlrev_b32_e32 v24, 16, v24
	v_addc_co_u32_e64 v27, s[0:1], 0, v17, s[0:1]
	v_cndmask_b32_e64 v36, -v25, v25, vcc
	v_cndmask_b32_e64 v37, -v24, v24, s[8:9]
	v_sub_u32_e32 v24, 0x2e00, v18
	v_cmp_eq_u32_e32 vcc, s60, v18
	v_sub_u32_e32 v28, 0x2c00, v18
	v_cmp_eq_u32_e64 s[0:1], s61, v18
	v_cndmask_b32_e64 v24, v24, 0, vcc
	v_ashrrev_i32_e32 v25, 31, v24
	v_cndmask_b32_e64 v28, v28, 0, s[0:1]
	v_ashrrev_i32_e32 v29, 31, v28
	v_lshl_add_u64 v[24:25], v[24:25], 1, s[2:3]
	v_lshl_add_u64 v[28:29], v[28:29], 1, s[2:3]
	global_load_ushort v41, v[24:25], off
	s_nop 0
	global_load_ushort v28, v[28:29], off
	v_sub_u32_e32 v24, 0x2a00, v18
	v_cmp_eq_u32_e64 s[4:5], s62, v18
	v_cmp_eq_u32_e64 s[6:7], s63, v18
	v_cmp_eq_u32_e64 s[8:9], s68, v18
	v_cndmask_b32_e64 v24, v24, 0, s[4:5]
	v_ashrrev_i32_e32 v25, 31, v24
	v_lshl_add_u64 v[24:25], v[24:25], 1, s[2:3]
	global_load_ushort v29, v[24:25], off
	v_sub_u32_e32 v24, 0x2800, v18
	v_cndmask_b32_e64 v24, v24, 0, s[6:7]
	v_ashrrev_i32_e32 v25, 31, v24
	v_lshl_add_u64 v[24:25], v[24:25], 1, s[2:3]
	global_load_ushort v38, v[26:27], off offset:1024
	global_load_ushort v40, v[26:27], off offset:2048
	global_load_ushort v39, v[26:27], off offset:3072
	global_load_ushort v44, v[24:25], off
	v_sub_u32_e32 v26, 0x2600, v18
	s_mov_b32 s78, s81
	s_mov_b32 s60, s87
	s_mov_b32 s61, s86
	s_mov_b32 s68, s89
	s_mov_b32 s62, s93
	s_mov_b32 s63, s92
	s_waitcnt vmcnt(6)
	v_lshlrev_b32_e32 v24, 16, v41
	v_cndmask_b32_e64 v43, -v24, v24, vcc
	s_waitcnt vmcnt(5)
	v_lshlrev_b32_e32 v24, 16, v28
	v_cndmask_b32_e64 v41, -v24, v24, s[0:1]
	v_add_co_u32_e64 v28, s[0:1], s13, v16
	s_waitcnt vmcnt(4)
	v_lshlrev_b32_e32 v24, 16, v29
	v_cndmask_b32_e64 v42, -v24, v24, s[4:5]
	v_add_co_u32_e32 v24, vcc, s43, v16
	v_addc_co_u32_e64 v29, s[0:1], 0, v17, s[0:1]
	s_nop 0
	v_addc_co_u32_e32 v25, vcc, 0, v17, vcc
	v_cmp_eq_u32_e32 vcc, s66, v18
	v_cmp_eq_u32_e64 s[4:5], s74, v18
	v_cmp_eq_u32_e64 s[0:1], s75, v18
	v_cndmask_b32_e64 v26, v26, 0, vcc
	v_ashrrev_i32_e32 v27, 31, v26
	v_lshl_add_u64 v[26:27], v[26:27], 1, s[2:3]
	global_load_ushort v26, v[26:27], off
	s_waitcnt vmcnt(1)
	v_lshlrev_b32_e32 v27, 16, v44
	v_sub_u32_e32 v44, 0x2200, v18
	v_cndmask_b32_e64 v45, -v27, v27, s[6:7]
	v_cndmask_b32_e64 v46, v44, 0, s[8:9]
	v_sub_u32_e32 v44, 0x2000, v18
	v_cmp_eq_u32_e64 s[6:7], s69, v18
	v_ashrrev_i32_e32 v47, 31, v46
	v_lshl_add_u64 v[46:47], v[46:47], 1, s[2:3]
	v_cndmask_b32_e64 v50, v44, 0, s[6:7]
	v_sub_u32_e32 v44, 0x1e00, v18
	v_cndmask_b32_e64 v52, v44, 0, s[4:5]
	v_sub_u32_e32 v44, 0x1c00, v18
	v_ashrrev_i32_e32 v51, 31, v50
	v_cndmask_b32_e64 v54, v44, 0, s[0:1]
	v_lshl_add_u64 v[50:51], v[50:51], 1, s[2:3]
	v_ashrrev_i32_e32 v53, 31, v52
	v_ashrrev_i32_e32 v55, 31, v54
	v_lshl_add_u64 v[52:53], v[52:53], 1, s[2:3]
	v_lshl_add_u64 v[54:55], v[54:55], 1, s[2:3]
	s_mov_b32 s66, s25
	s_mov_b32 s69, s88
	s_mov_b32 s74, s29
	s_mov_b32 s75, s28
	s_movk_i32 s43, 0x6000
	s_waitcnt vmcnt(0)
	v_lshlrev_b32_e32 v26, 16, v26
	v_cndmask_b32_e64 v49, -v26, v26, vcc
	v_sub_u32_e32 v26, 0x2400, v18
	v_cmp_eq_u32_e32 vcc, s67, v18
	s_mov_b32 s67, s24
	s_nop 0
	v_cndmask_b32_e64 v26, v26, 0, vcc
	v_ashrrev_i32_e32 v27, 31, v26
	v_lshl_add_u64 v[26:27], v[26:27], 1, s[2:3]
	global_load_ushort v44, v[26:27], off
	s_nop 0
	global_load_ushort v46, v[46:47], off
	s_nop 0
	global_load_ushort v47, v[50:51], off
	global_load_ushort v48, v[52:53], off
	s_nop 0
	global_load_ushort v50, v[54:55], off
	v_sub_u32_e32 v26, 0x1a00, v18
	v_cndmask_b32_e64 v26, v26, 0, s[10:11]
	v_ashrrev_i32_e32 v27, 31, v26
	v_lshl_add_u64 v[26:27], v[26:27], 1, s[2:3]
	global_load_ushort v26, v[26:27], off
	s_nop 0
	global_load_ushort v53, v[28:29], off offset:1024
	global_load_ushort v51, v[28:29], off offset:2048
	s_waitcnt vmcnt(7)
	v_lshlrev_b32_e32 v27, 16, v44
	v_cndmask_b32_e64 v61, -v27, v27, vcc
	s_waitcnt vmcnt(6)
	v_lshlrev_b32_e32 v27, 16, v46
	v_cndmask_b32_e64 v63, -v27, v27, s[8:9]
	s_waitcnt vmcnt(5)
	v_lshlrev_b32_e32 v27, 16, v47
	v_cndmask_b32_e64 v90, -v27, v27, s[6:7]
	s_waitcnt vmcnt(4)
	v_lshlrev_b32_e32 v27, 16, v48
	v_cndmask_b32_e64 v59, -v27, v27, s[4:5]
	s_waitcnt vmcnt(3)
	v_lshlrev_b32_e32 v27, 16, v50
	v_cndmask_b32_e64 v57, -v27, v27, s[0:1]
	v_sub_u32_e32 v44, 0x1800, v18
	v_cmp_eq_u32_e64 s[8:9], s56, v18
	s_movk_i32 s0, 0xd600
	s_waitcnt vmcnt(2)
	v_lshlrev_b32_e32 v26, 16, v26
	v_cndmask_b32_e64 v46, v44, 0, s[8:9]
	v_sub_u32_e32 v44, 0x1600, v18
	v_cmp_eq_u32_e64 s[6:7], s0, v18
	s_movk_i32 s0, 0xd400
	v_cndmask_b32_e64 v55, -v26, v26, s[10:11]
	v_add_co_u32_e32 v26, vcc, s12, v16
	v_cndmask_b32_e64 v64, v44, 0, s[6:7]
	v_sub_u32_e32 v44, 0x1400, v18
	v_cmp_eq_u32_e64 s[4:5], s0, v18
	s_movk_i32 s0, 0xd200
	v_addc_co_u32_e32 v27, vcc, 0, v17, vcc
	v_cndmask_b32_e64 v66, v44, 0, s[4:5]
	v_sub_u32_e32 v44, 0x1200, v18
	v_cmp_eq_u32_e64 s[0:1], s0, v18
	s_movk_i32 s10, 0xd000
	v_cmp_eq_u32_e32 vcc, s10, v18
	v_cndmask_b32_e64 v68, v44, 0, s[0:1]
	v_sub_u32_e32 v44, 0x1000, v18
	v_ashrrev_i32_e32 v47, 31, v46
	v_cndmask_b32_e64 v70, v44, 0, vcc
	v_lshl_add_u64 v[46:47], v[46:47], 1, s[2:3]
	v_ashrrev_i32_e32 v65, 31, v64
	v_ashrrev_i32_e32 v67, 31, v66
	v_ashrrev_i32_e32 v69, 31, v68
	v_ashrrev_i32_e32 v71, 31, v70
	v_lshl_add_u64 v[64:65], v[64:65], 1, s[2:3]
	v_lshl_add_u64 v[66:67], v[66:67], 1, s[2:3]
	v_lshl_add_u64 v[68:69], v[68:69], 1, s[2:3]
	v_lshl_add_u64 v[70:71], v[70:71], 1, s[2:3]
	global_load_ushort v44, v[46:47], off
	global_load_ushort v48, v[64:65], off
	global_load_ushort v50, v[66:67], off
	global_load_ushort v52, v[68:69], off
	global_load_ushort v54, v[70:71], off
	v_sub_u32_e32 v46, 0xe00, v18
	v_cmp_eq_u32_e64 s[12:13], s84, v18
	s_movk_i32 s10, 0xcc00
	v_cmp_eq_u32_e64 s[10:11], s10, v18
	v_cndmask_b32_e64 v46, v46, 0, s[12:13]
	v_ashrrev_i32_e32 v47, 31, v46
	v_lshl_add_u64 v[46:47], v[46:47], 1, s[2:3]
	global_load_ushort v56, v[46:47], off
	v_sub_u32_e32 v46, 0xc00, v18
	v_cndmask_b32_e64 v46, v46, 0, s[10:11]
	v_ashrrev_i32_e32 v47, 31, v46
	v_lshl_add_u64 v[46:47], v[46:47], 1, s[2:3]
	global_load_ushort v46, v[46:47], off
	s_nop 0
	global_load_ushort v91, v[28:29], off offset:3072
	s_mov_b32 s84, 0x3f3504f3
	s_mov_b32 s85, 0xbf3504f3
	s_mov_b32 s54, s85
	s_mov_b32 s55, s84
	s_mov_b32 s56, s19
	s_mov_b32 s38, s85
	s_waitcnt vmcnt(7)
	v_lshlrev_b32_e32 v28, 16, v44
	v_cndmask_b32_e64 v97, -v28, v28, s[8:9]
	s_waitcnt vmcnt(6)
	v_lshlrev_b32_e32 v28, 16, v48
	v_cndmask_b32_e64 v96, -v28, v28, s[6:7]
	s_waitcnt vmcnt(5)
	v_lshlrev_b32_e32 v28, 16, v50
	v_cndmask_b32_e64 v94, -v28, v28, s[4:5]
	s_waitcnt vmcnt(4)
	v_lshlrev_b32_e32 v28, 16, v52
	v_cndmask_b32_e64 v93, -v28, v28, s[0:1]
	s_waitcnt vmcnt(3)
	v_lshlrev_b32_e32 v28, 16, v54
	v_cndmask_b32_e64 v92, -v28, v28, vcc
	s_movk_i32 s0, 0xca00
	v_cmp_eq_u32_e64 s[0:1], s0, v18
	s_waitcnt vmcnt(2)
	v_lshlrev_b32_e32 v28, 16, v56
	v_cndmask_b32_e64 v95, -v28, v28, s[12:13]
	v_sub_u32_e32 v28, 0xa00, v18
	v_cndmask_b32_e64 v28, v28, 0, s[0:1]
	v_ashrrev_i32_e32 v29, 31, v28
	v_lshl_add_u64 v[28:29], v[28:29], 1, s[2:3]
	global_load_ushort v44, v[28:29], off
	s_waitcnt vmcnt(2)
	v_lshlrev_b32_e32 v28, 16, v46
	v_cndmask_b32_e64 v106, -v28, v28, s[10:11]
	v_add_co_u32_e32 v28, vcc, s16, v16
	s_movk_i32 s4, 0xc400
	s_nop 0
	v_addc_co_u32_e32 v29, vcc, 0, v17, vcc
	v_sub_u32_e32 v46, 0x400, v18
	v_cmp_eq_u32_e32 vcc, s4, v18
	s_movk_i32 s4, 0xc800
	v_sub_u32_e32 v48, 0x800, v18
	v_cndmask_b32_e64 v46, v46, 0, vcc
	v_cmp_eq_u32_e64 s[4:5], s4, v18
	v_ashrrev_i32_e32 v47, 31, v46
	v_lshl_add_u64 v[46:47], v[46:47], 1, s[2:3]
	v_cndmask_b32_e64 v64, v48, 0, s[4:5]
	v_ashrrev_i32_e32 v65, 31, v64
	v_lshl_add_u64 v[64:65], v[64:65], 1, s[2:3]
	global_load_ushort v48, v[46:47], off
	s_nop 0
	global_load_ushort v46, v[64:65], off
	global_load_ushort v110, v[28:29], off
	global_load_ushort v112, v[28:29], off offset:1024
	global_load_ushort v114, v[28:29], off offset:2048
	global_load_ushort v116, v[28:29], off offset:3072
	s_mov_b32 s6, 0x3f7b14be
	s_mov_b32 s7, 0xbe47c5c2
	s_mov_b32 s16, 0x3f6c835e
	s_mov_b32 s17, 0xbec3ef15
	s_mov_b32 s50, s17
	s_mov_b32 s51, s16
	v_add_f32_e32 v50, v15, v13
	s_mov_b32 s8, 0x3e47c5c2
	s_mov_b32 s9, 0xbf7b14be
	s_mov_b32 s30, s9
	s_mov_b32 s31, s8
	s_mov_b32 s10, s93
	s_mov_b32 s11, s81
	s_mov_b32 s12, s17
	s_mov_b32 s13, s19
	s_waitcnt vmcnt(6)
	v_lshlrev_b32_e32 v28, 16, v44
	v_cndmask_b32_e64 v108, -v28, v28, s[0:1]
	s_movk_i32 s0, 0xc600
	v_sub_u32_e32 v28, 0x600, v18
	v_sub_u32_e32 v44, 0x200, v18
	s_waitcnt vmcnt(4)
	v_lshlrev_b32_e32 v29, 16, v46
	v_cndmask_b32_e64 v111, -v29, v29, s[4:5]
	v_cmp_eq_u32_e64 s[4:5], s0, v18
	s_movk_i32 s0, 0xc200
	v_cmp_eq_u32_e64 s[0:1], s0, v18
	v_cndmask_b32_e64 v28, v28, 0, s[4:5]
	v_ashrrev_i32_e32 v29, 31, v28
	v_cndmask_b32_e64 v46, v44, 0, s[0:1]
	v_lshl_add_u64 v[28:29], v[28:29], 1, s[2:3]
	v_ashrrev_i32_e32 v47, 31, v46
	v_lshl_add_u64 v[46:47], v[46:47], 1, s[2:3]
	global_load_ushort v18, v[16:17], off
	s_nop 0
	global_load_ushort v28, v[28:29], off
	s_nop 0
	global_load_ushort v29, v[16:17], off offset:1024
	s_nop 0
	global_load_ushort v17, v[16:17], off offset:2048
	s_nop 0
	global_load_ushort v44, v[46:47], off
	global_load_ushort v58, v[22:23], off offset:1024
	global_load_ushort v62, v[22:23], off offset:2048
	global_load_ushort v68, v[22:23], off offset:3072
	global_load_ushort v69, v[24:25], off offset:-4096
	global_load_ushort v98, v[24:25], off
	global_load_ushort v52, v[22:23], off offset:-4096
	global_load_ushort v54, v[20:21], off offset:1024
	s_nop 0
	global_load_ushort v21, v[20:21], off offset:2048
	s_nop 0
	global_load_ushort v56, v[22:23], off
	s_mov_b32 s2, 0x3f7ec46d
	s_mov_b32 s3, 0xbdc8bd36
	v_lshlrev_b32_e32 v22, 16, v48
	s_mov_b32 s76, s3
	s_mov_b32 s77, s2
	v_cndmask_b32_e64 v115, -v22, v22, vcc
	v_pk_mul_f32 v[22:23], v[14:15], s[76:77] op_sel_hi:[0,1] neg_lo:[1,0]
	s_mov_b64 vcc, s[64:65]
	s_mov_b32 s64, s7
	s_mov_b32 s65, s6
	s_waitcnt vmcnt(13)
	v_lshlrev_b32_e32 v16, 16, v18
	s_waitcnt vmcnt(12)
	v_lshlrev_b32_e32 v18, 16, v28
	s_waitcnt vmcnt(11)
	v_lshlrev_b32_e32 v20, 16, v29
	s_waitcnt vmcnt(10)
	v_lshlrev_b32_e32 v17, 16, v17
	v_add_f32_e32 v20, v31, v20
	v_pk_fma_f32 v[28:29], v[10:11], s[2:3], v[22:23] op_sel_hi:[0,1,1]
	v_add_f32_e32 v22, v30, v17
	v_pk_mul_f32 v[30:31], v[14:15], s[64:65] op_sel_hi:[0,1] neg_lo:[1,0]
	v_pk_fma_f32 v[46:47], v[10:11], s[6:7], v[30:31] op_sel_hi:[0,1,1]
	v_pk_mul_f32 v[30:31], v[14:15], s[78:79] op_sel_hi:[0,1] neg_lo:[1,0]
	v_pk_fma_f32 v[88:89], v[10:11], s[80:81], v[30:31] op_sel_hi:[0,1,1]
	s_waitcnt vmcnt(3)
	v_lshlrev_b32_e32 v13, 16, v52
	v_pk_mul_f32 v[30:31], v[14:15], s[50:51] op_sel_hi:[0,1] neg_lo:[1,0]
	v_add_f32_e32 v16, v19, v16
	v_cndmask_b32_e64 v113, -v18, v18, s[4:5]
	v_pk_mul_f32 v[18:19], v[14:15], s[40:41] op_sel_hi:[0,1] neg_lo:[1,0]
	v_add_f32_e32 v52, v33, v13
	v_pk_fma_f32 v[84:85], v[10:11], s[16:17], v[30:31] op_sel_hi:[0,1,1]
	s_waitcnt vmcnt(2)
	v_lshlrev_b32_e32 v13, 16, v54
	v_pk_mul_f32 v[30:31], v[14:15], s[48:49] op_sel_hi:[0,1] neg_lo:[1,0]
	s_waitcnt vmcnt(1)
	v_lshlrev_b32_e32 v15, 16, v21
	v_lshlrev_b32_e32 v17, 16, v44
	v_add_f32_e32 v44, v34, v13
	global_load_ushort v13, v[24:25], off offset:1024
	global_load_ushort v33, v[26:27], off
	v_add_f32_e32 v48, v35, v15
	global_load_ushort v15, v[24:25], off offset:2048
	v_lshlrev_b32_e32 v21, 16, v32
	s_waitcnt vmcnt(3)
	v_lshlrev_b32_e32 v23, 16, v56
	v_add_f32_e32 v54, v36, v21
	global_load_ushort v21, v[24:25], off offset:3072
	v_add_f32_e32 v56, v37, v23
	v_lshlrev_b32_e32 v23, 16, v58
	v_add_f32_e32 v60, v43, v23
	global_load_ushort v23, v[26:27], off offset:-4096
	v_pk_fma_f32 v[64:65], v[10:11], s[20:21], v[30:31] op_sel_hi:[0,1,1]
	s_mov_b32 s4, 0x3dc8bd36
	s_mov_b32 s5, 0xbf7ec46d
	s_mov_b32 s34, s5
	s_mov_b32 s35, s4
	s_mov_b32 s2, s5
	v_cndmask_b32_e64 v17, -v17, v17, s[0:1]
	s_mov_b32 s0, s3
	s_mov_b32 s1, s5
	s_mov_b32 s6, s9
	s_mov_b32 s16, s19
	s_mov_b32 s20, s89
	v_pk_fma_f32 v[18:19], v[10:11], s[44:45], v[18:19] op_sel_hi:[0,1,1]
	s_waitcnt vmcnt(4)
	v_lshlrev_b32_e32 v13, 16, v13
	s_waitcnt vmcnt(2)
	v_pk_mul_f32 v[24:25], v[14:15], s[54:55] op_sel_hi:[0,1] neg_lo:[1,0]
	v_pk_fma_f32 v[78:79], v[10:11], s[84:85], v[24:25] op_sel_hi:[0,1,1]
	v_pk_mul_f32 v[24:25], v[14:15], s[60:61] op_sel_hi:[0,1] neg_lo:[1,0]
	v_pk_fma_f32 v[86:87], v[10:11], s[86:87], v[24:25] op_sel_hi:[0,1,1]
	v_lshlrev_b32_e32 v24, 16, v62
	v_add_f32_e32 v62, v41, v24
	v_pk_mul_f32 v[24:25], v[14:15], s[66:67] op_sel_hi:[0,1] neg_lo:[1,0]
	v_pk_fma_f32 v[82:83], v[10:11], s[24:25], v[24:25] op_sel_hi:[0,1,1]
	v_lshlrev_b32_e32 v24, 16, v68
	v_add_f32_e32 v58, v42, v24
	v_pk_mul_f32 v[24:25], v[14:15], s[68:69] op_sel_hi:[0,1] neg_lo:[1,0]
	v_pk_fma_f32 v[80:81], v[10:11], s[88:89], v[24:25] op_sel_hi:[0,1,1]
	v_lshlrev_b32_e32 v24, 16, v69
	v_add_f32_e32 v42, v45, v24
	v_pk_mul_f32 v[24:25], v[14:15], s[56:57] op_sel_hi:[0,1] neg_lo:[1,0]
	v_pk_fma_f32 v[74:75], v[10:11], s[18:19], v[24:25] op_sel_hi:[0,1,1]
	v_lshlrev_b32_e32 v24, 16, v38
	v_add_f32_e32 v38, v49, v24
	v_pk_mul_f32 v[24:25], v[14:15], s[62:63] op_sel_hi:[0,1] neg_lo:[1,0]
	v_pk_fma_f32 v[72:73], v[10:11], s[92:93], v[24:25] op_sel_hi:[0,1,1]
	v_lshlrev_b32_e32 v25, 16, v39
	v_add_f32_e32 v32, v63, v25
	global_load_ushort v25, v[26:27], off offset:1024
	global_load_ushort v39, v[26:27], off offset:2048
	v_lshlrev_b32_e32 v24, 16, v40
	global_load_ushort v40, v[26:27], off offset:3072
	v_pk_mul_f32 v[30:31], v[14:15], s[58:59] op_sel_hi:[0,1] neg_lo:[1,0]
	v_pk_fma_f32 v[66:67], v[10:11], s[82:83], v[30:31] op_sel_hi:[0,1,1]
	v_pk_mul_f32 v[30:31], v[14:15], s[74:75] op_sel_hi:[0,1] neg_lo:[1,0]
	v_pk_fma_f32 v[76:77], v[10:11], s[28:29], v[30:31] op_sel_hi:[0,1,1]
	v_pk_mul_f32 v[30:31], v[14:15], s[30:31] op_sel_hi:[0,1] neg_lo:[1,0]
	v_pk_fma_f32 v[68:69], v[10:11], s[8:9], v[30:31] op_sel_hi:[0,1,1]
	v_pk_mul_f32 v[30:31], v[14:15], s[34:35] op_sel_hi:[0,1] neg_lo:[1,0]
	v_pk_fma_f32 v[70:71], v[10:11], s[4:5], v[30:31] op_sel_hi:[0,1,1]
	v_lshlrev_b32_e32 v30, 16, v98
	v_pk_mul_f32 v[34:35], v[14:15], s[36:37] op_sel_hi:[0,1] neg_lo:[1,0]
	v_add_f32_e32 v30, v90, v30
	v_pk_fma_f32 v[34:35], v[10:11], s[96:97], v[34:35] op_sel_hi:[0,1,1]
	v_pk_mul_f32 v[36:37], v[34:35], v[30:31] op_sel_hi:[1,0]
	v_pk_mul_f32 v[30:31], v[14:15], s[2:3] op_sel_hi:[0,1] neg_lo:[1,0]
	v_add_f32_e32 v26, v59, v13
	v_pk_fma_f32 v[30:31], v[10:11], s[0:1], v[30:31] op_sel_hi:[0,1,1]
	v_lshlrev_b32_e32 v13, 16, v15
	s_mov_b32 s4, s7
	s_mov_b32 s5, s9
	v_pk_mul_f32 v[34:35], v[14:15], s[6:7] op_sel_hi:[0,1] neg_lo:[1,0]
	v_pk_mul_f32 v[26:27], v[30:31], v[26:27] op_sel_hi:[1,0]
	v_add_f32_e32 v30, v57, v13
	v_pk_fma_f32 v[34:35], v[10:11], s[4:5], v[34:35] op_sel_hi:[0,1,1]
	v_pk_mul_f32 v[98:99], v[34:35], v[30:31] op_sel_hi:[1,0]
	s_waitcnt vmcnt(4)
	v_lshlrev_b32_e32 v13, 16, v21
	s_mov_b32 s8, s81
	s_mov_b32 s9, s93
	v_pk_mul_f32 v[34:35], v[14:15], s[10:11] op_sel_hi:[0,1] neg_lo:[1,0]
	v_add_f32_e32 v30, v55, v13
	v_pk_fma_f32 v[34:35], v[10:11], s[8:9], v[34:35] op_sel_hi:[0,1,1]
	v_pk_mul_f32 v[100:101], v[34:35], v[30:31] op_sel_hi:[1,0]
	s_waitcnt vmcnt(3)
	v_lshlrev_b32_e32 v13, 16, v23
	v_pk_mul_f32 v[34:35], v[14:15], s[16:17] op_sel_hi:[0,1] neg_lo:[1,0]
	v_add_f32_e32 v30, v97, v13
	v_pk_fma_f32 v[34:35], v[10:11], s[12:13], v[34:35] op_sel_hi:[0,1,1]
	v_pk_mul_f32 v[102:103], v[34:35], v[30:31] op_sel_hi:[1,0]
	v_lshlrev_b32_e32 v13, 16, v53
	s_mov_b32 s18, s21
	s_mov_b32 s19, s89
	v_pk_mul_f32 v[34:35], v[14:15], s[20:21] op_sel_hi:[0,1] neg_lo:[1,0]
	v_add_f32_e32 v30, v96, v13
	v_pk_fma_f32 v[34:35], v[10:11], s[18:19], v[34:35] op_sel_hi:[0,1,1]
	s_mov_b32 s24, s25
	s_mov_b32 s25, s83
	v_pk_mul_f32 v[96:97], v[34:35], v[30:31] op_sel_hi:[1,0]
	v_lshlrev_b32_e32 v13, 16, v51
	v_pk_mul_f32 v[34:35], v[14:15], s[24:25] op_sel_hi:[0,1] neg_lo:[1,0]
	v_add_f32_e32 v30, v94, v13
	v_pk_fma_f32 v[34:35], v[10:11], s[22:23], v[34:35] op_sel_hi:[0,1,1]
	s_mov_b32 s28, s87
	v_pk_mul_f32 v[104:105], v[34:35], v[30:31] op_sel_hi:[1,0]
	v_lshlrev_b32_e32 v13, 16, v91
	v_pk_mul_f32 v[34:35], v[14:15], s[28:29] op_sel_hi:[0,1] neg_lo:[1,0]
	v_add_f32_e32 v30, v93, v13
	v_pk_fma_f32 v[34:35], v[10:11], s[26:27], v[34:35] op_sel_hi:[0,1,1]
	v_pk_mul_f32 v[90:91], v[34:35], v[30:31] op_sel_hi:[1,0]
	v_lshlrev_b32_e32 v13, 16, v33
	v_pk_mul_f32 v[34:35], v[14:15], s[84:85] op_sel_hi:[0,0] neg_lo:[1,0]
	v_add_f32_e32 v30, v92, v13
	v_pk_fma_f32 v[34:35], v[10:11], s[38:39], v[34:35] op_sel_hi:[0,0,1] neg_lo:[0,0,1] neg_hi:[0,0,1]
	v_pk_mul_f32 v[92:93], v[34:35], v[30:31] op_sel_hi:[1,0]
	v_pk_mul_f32 v[34:35], v[14:15], s[26:27] op_sel_hi:[0,1] neg_lo:[1,0]
	v_pk_fma_f32 v[34:35], v[10:11], s[28:29], v[34:35] op_sel_hi:[0,1,1]
	v_add_f32_e32 v24, v61, v24
	s_waitcnt vmcnt(2)
	v_lshlrev_b32_e32 v13, 16, v25
	v_add_f32_e32 v30, v95, v13
	v_pk_mul_f32 v[94:95], v[34:35], v[30:31] op_sel_hi:[1,0]
	s_waitcnt vmcnt(1)
	v_lshlrev_b32_e32 v13, 16, v39
	v_pk_mul_f32 v[34:35], v[14:15], s[22:23] op_sel_hi:[0,1] neg_lo:[1,0]
	v_add_f32_e32 v30, v106, v13
	v_pk_fma_f32 v[34:35], v[10:11], s[24:25], v[34:35] op_sel_hi:[0,1,1]
	v_pk_mul_f32 v[106:107], v[34:35], v[30:31] op_sel_hi:[1,0]
	s_waitcnt vmcnt(0)
	v_lshlrev_b32_e32 v13, 16, v40
	v_pk_mul_f32 v[34:35], v[14:15], s[18:19] op_sel_hi:[0,1] neg_lo:[1,0]
	v_add_f32_e32 v30, v108, v13
	v_pk_fma_f32 v[34:35], v[10:11], s[20:21], v[34:35] op_sel_hi:[0,1,1]
	v_pk_mul_f32 v[108:109], v[34:35], v[30:31] op_sel_hi:[1,0]
	v_lshlrev_b32_e32 v13, 16, v110
	v_pk_mul_f32 v[34:35], v[14:15], s[12:13] op_sel_hi:[0,1] neg_lo:[1,0]
	v_add_f32_e32 v30, v111, v13
	v_pk_fma_f32 v[34:35], v[10:11], s[16:17], v[34:35] op_sel_hi:[0,1,1]
	v_pk_mul_f32 v[110:111], v[34:35], v[30:31] op_sel_hi:[1,0]
	v_lshlrev_b32_e32 v13, 16, v112
	v_pk_mul_f32 v[34:35], v[14:15], s[8:9] op_sel_hi:[0,1] neg_lo:[1,0]
	v_add_f32_e32 v30, v113, v13
	v_pk_fma_f32 v[34:35], v[10:11], s[10:11], v[34:35] op_sel_hi:[0,1,1]
	v_pk_mul_f32 v[112:113], v[34:35], v[30:31] op_sel_hi:[1,0]
	v_lshlrev_b32_e32 v13, 16, v114
	v_pk_mul_f32 v[34:35], v[14:15], s[4:5] op_sel_hi:[0,1] neg_lo:[1,0]
	v_add_f32_e32 v30, v115, v13
	v_pk_fma_f32 v[34:35], v[10:11], s[6:7], v[34:35] op_sel_hi:[0,1,1]
	v_lshlrev_b32_e32 v13, 16, v116
	v_pk_mul_f32 v[14:15], v[14:15], s[0:1] op_sel_hi:[0,1] neg_lo:[1,0]
	v_pk_mul_f32 v[114:115], v[34:35], v[30:31] op_sel_hi:[1,0]
	v_add_f32_e32 v30, v17, v13
	v_pk_fma_f32 v[14:15], v[10:11], s[2:3], v[14:15] op_sel_hi:[0,1,1]
	v_pk_mul_f32 v[116:117], v[14:15], v[30:31] op_sel_hi:[1,0]
	v_mov_b32_e32 v13, v173
	v_mov_b32_e32 v10, v1
	v_mov_b32_e32 v30, v165
	v_mov_b32_e32 v10, v167
	v_mov_b32_e32 v34, v169
	v_mov_b32_e32 v17, v171
	s_nop 0
	v_pk_fma_f32 v[126:127], v[18:19], v[16:17], v[36:37] op_sel_hi:[1,0,1]
	v_pk_fma_f32 v[36:37], v[18:19], v[16:17], v[36:37] op_sel_hi:[1,0,1] neg_lo:[0,0,1] neg_hi:[0,0,1]
	v_pk_fma_f32 v[18:19], v[28:29], v[20:21], v[26:27] op_sel_hi:[1,0,1] neg_lo:[0,0,1] neg_hi:[0,0,1]
	v_pk_fma_f32 v[16:17], v[28:29], v[20:21], v[26:27] op_sel_hi:[1,0,1]
	v_pk_mul_f32 v[20:21], v[18:19], v[124:125] op_sel:[1,0] op_sel_hi:[0,0] neg_lo:[1,1] neg_hi:[0,1]
	s_nop 0
	v_pk_fma_f32 v[40:41], v[18:19], v[118:119], v[20:21] op_sel_hi:[1,0,1]
	v_pk_fma_f32 v[20:21], v[46:47], v[22:23], v[98:99] op_sel_hi:[1,0,1] neg_lo:[0,0,1] neg_hi:[0,0,1]
	v_pk_fma_f32 v[18:19], v[46:47], v[22:23], v[98:99] op_sel_hi:[1,0,1]
	v_pk_mul_f32 v[22:23], v[20:21], v[34:35] op_sel:[1,0] op_sel_hi:[0,0] neg_lo:[1,1] neg_hi:[0,1]
	s_nop 0
	v_pk_fma_f32 v[46:47], v[20:21], v[30:31], v[22:23] op_sel_hi:[1,0,1]
	v_pk_fma_f32 v[22:23], v[88:89], v[50:51], v[100:101] op_sel_hi:[1,0,1] neg_lo:[0,0,1] neg_hi:[0,0,1]
	v_pk_fma_f32 v[20:21], v[88:89], v[50:51], v[100:101] op_sel_hi:[1,0,1]
	v_pk_mul_f32 v[26:27], v[22:23], v[122:123] op_sel:[1,0] op_sel_hi:[0,0] neg_lo:[1,1] neg_hi:[0,1]
	s_nop 0
	v_pk_fma_f32 v[50:51], v[22:23], v[120:121], v[26:27] op_sel_hi:[1,0,1]
	v_pk_fma_f32 v[26:27], v[84:85], v[52:53], v[102:103] op_sel_hi:[1,0,1] neg_lo:[0,0,1] neg_hi:[0,0,1]
	v_pk_fma_f32 v[22:23], v[84:85], v[52:53], v[102:103] op_sel_hi:[1,0,1]
	v_pk_mul_f32 v[28:29], v[26:27], v[10:11] op_sel:[1,0] op_sel_hi:[0,0] neg_lo:[1,1] neg_hi:[0,1]
	s_nop 0
	v_pk_fma_f32 v[52:53], v[26:27], v[10:11], v[28:29] op_sel_hi:[1,0,1]
	v_pk_fma_f32 v[28:29], v[64:65], v[44:45], v[96:97] op_sel_hi:[1,0,1] neg_lo:[0,0,1] neg_hi:[0,0,1]
	v_pk_fma_f32 v[26:27], v[64:65], v[44:45], v[96:97] op_sel_hi:[1,0,1]
	v_pk_mul_f32 v[44:45], v[28:29], v[122:123] op_sel_hi:[1,0]
	s_nop 0
	v_pk_fma_f32 v[64:65], v[28:29], v[120:121], v[44:45] op_sel:[1,0,0] op_sel_hi:[0,0,1] neg_lo:[1,1,0] neg_hi:[0,1,0]
	v_pk_fma_f32 v[44:45], v[66:67], v[48:49], v[104:105] op_sel_hi:[1,0,1] neg_lo:[0,0,1] neg_hi:[0,0,1]
	v_pk_fma_f32 v[28:29], v[66:67], v[48:49], v[104:105] op_sel_hi:[1,0,1]
	v_pk_mul_f32 v[48:49], v[44:45], v[34:35] op_sel_hi:[1,0]
	s_nop 0
	v_pk_fma_f32 v[66:67], v[44:45], v[30:31], v[48:49] op_sel:[1,0,0] op_sel_hi:[0,0,1] neg_lo:[1,1,0] neg_hi:[0,1,0]
	v_pk_fma_f32 v[48:49], v[76:77], v[54:55], v[90:91] op_sel_hi:[1,0,1] neg_lo:[0,0,1] neg_hi:[0,0,1]
	v_pk_fma_f32 v[44:45], v[76:77], v[54:55], v[90:91] op_sel_hi:[1,0,1]
	v_pk_mul_f32 v[54:55], v[48:49], v[124:125] op_sel_hi:[1,0]
	v_xor_b32_e32 v76, 0x80000000, v49
	v_mov_b32_e32 v77, v48
	v_pk_fma_f32 v[48:49], v[78:79], v[56:57], v[92:93] op_sel_hi:[1,0,1]
	v_pk_fma_f32 v[56:57], v[78:79], v[56:57], v[92:93] op_sel_hi:[1,0,1] neg_lo:[0,0,1] neg_hi:[0,0,1]
	v_pk_fma_f32 v[54:55], v[76:77], v[118:119], v[54:55] op_sel_hi:[1,0,1] neg_lo:[0,1,0] neg_hi:[0,1,0]
	v_xor_b32_e32 v77, 0x80000000, v56
	v_mov_b32_e32 v76, v57
	v_pk_fma_f32 v[56:57], v[86:87], v[60:61], v[94:95] op_sel_hi:[1,0,1]
	v_pk_fma_f32 v[60:61], v[86:87], v[60:61], v[94:95] op_sel_hi:[1,0,1] neg_lo:[0,0,1] neg_hi:[0,0,1]
	s_nop 0
	v_pk_mul_f32 v[78:79], v[60:61], v[124:125] op_sel_hi:[1,0] neg_lo:[0,1] neg_hi:[0,1]
	s_nop 0
	v_pk_fma_f32 v[60:61], v[60:61], v[118:119], v[78:79] op_sel:[1,0,0] op_sel_hi:[0,0,1] neg_lo:[1,1,0] neg_hi:[0,1,0]
	v_pk_fma_f32 v[78:79], v[82:83], v[62:63], v[106:107] op_sel_hi:[1,0,1]
	v_pk_fma_f32 v[62:63], v[82:83], v[62:63], v[106:107] op_sel_hi:[1,0,1] neg_lo:[0,0,1] neg_hi:[0,0,1]
	s_nop 0
	v_pk_mul_f32 v[82:83], v[62:63], v[34:35] op_sel_hi:[1,0] neg_lo:[0,1] neg_hi:[0,1]
	s_nop 0
	v_pk_fma_f32 v[62:63], v[62:63], v[30:31], v[82:83] op_sel:[1,0,0] op_sel_hi:[0,0,1] neg_lo:[1,1,0] neg_hi:[0,1,0]
	v_pk_fma_f32 v[82:83], v[80:81], v[58:59], v[108:109] op_sel_hi:[1,0,1]
	v_pk_fma_f32 v[58:59], v[80:81], v[58:59], v[108:109] op_sel_hi:[1,0,1] neg_lo:[0,0,1] neg_hi:[0,0,1]
	s_nop 0
	v_pk_mul_f32 v[80:81], v[58:59], v[122:123] op_sel_hi:[1,0] neg_lo:[0,1] neg_hi:[0,1]
	s_nop 0
	v_pk_fma_f32 v[58:59], v[58:59], v[120:121], v[80:81] op_sel:[1,0,0] op_sel_hi:[0,0,1] neg_lo:[1,1,0] neg_hi:[0,1,0]
	v_pk_add_f32 v[84:85], v[16:17], v[56:57]
	v_pk_add_f32 v[16:17], v[16:17], v[56:57] neg_lo:[0,1] neg_hi:[0,1]
	v_pk_fma_f32 v[80:81], v[74:75], v[42:43], v[110:111] op_sel_hi:[1,0,1]
	v_pk_mul_f32 v[56:57], v[16:17], v[34:35] op_sel:[1,0] op_sel_hi:[0,0] neg_lo:[1,1] neg_hi:[0,1]
	v_pk_fma_f32 v[42:43], v[74:75], v[42:43], v[110:111] op_sel_hi:[1,0,1] neg_lo:[0,0,1] neg_hi:[0,0,1]
	v_pk_fma_f32 v[56:57], v[16:17], v[30:31], v[56:57] op_sel_hi:[1,0,1]
	v_pk_add_f32 v[16:17], v[18:19], v[78:79]
	v_pk_add_f32 v[18:19], v[18:19], v[78:79] neg_lo:[0,1] neg_hi:[0,1]
	v_pk_mul_f32 v[74:75], v[42:43], v[10:11] op_sel:[1,0] op_sel_hi:[0,0] neg_lo:[1,1] neg_hi:[0,1]
	v_pk_mul_f32 v[78:79], v[18:19], v[10:11] op_sel:[1,0] op_sel_hi:[0,0] neg_lo:[1,1] neg_hi:[0,1]
	v_pk_fma_f32 v[74:75], v[42:43], v[10:11], v[74:75] op_sel_hi:[1,0,1] neg_lo:[0,1,0] neg_hi:[0,1,0]
	v_pk_fma_f32 v[42:43], v[72:73], v[38:39], v[112:113] op_sel_hi:[1,0,1]
	v_pk_fma_f32 v[38:39], v[72:73], v[38:39], v[112:113] op_sel_hi:[1,0,1] neg_lo:[0,0,1] neg_hi:[0,0,1]
	v_pk_fma_f32 v[18:19], v[18:19], v[10:11], v[78:79] op_sel_hi:[1,0,1]
	v_pk_add_f32 v[78:79], v[20:21], v[82:83]
	v_pk_add_f32 v[20:21], v[20:21], v[82:83] neg_lo:[0,1] neg_hi:[0,1]
	s_nop 0
	v_pk_mul_f32 v[82:83], v[20:21], v[34:35] op_sel_hi:[1,0]
	v_xor_b32_e32 v86, 0x80000000, v21
	v_mov_b32_e32 v87, v20
	v_pk_add_f32 v[20:21], v[22:23], v[80:81]
	v_pk_add_f32 v[22:23], v[22:23], v[80:81] neg_lo:[0,1] neg_hi:[0,1]
	v_pk_mul_f32 v[72:73], v[38:39], v[122:123] op_sel:[1,0] op_sel_hi:[0,0] neg_lo:[1,1] neg_hi:[0,1]
	v_xor_b32_e32 v81, 0x80000000, v22
	v_mov_b32_e32 v80, v23
	v_pk_add_f32 v[22:23], v[26:27], v[42:43]
	v_pk_add_f32 v[26:27], v[26:27], v[42:43] neg_lo:[0,1] neg_hi:[0,1]
	v_pk_fma_f32 v[72:73], v[38:39], v[120:121], v[72:73] op_sel_hi:[1,0,1] neg_lo:[0,1,0] neg_hi:[0,1,0]
	v_pk_fma_f32 v[38:39], v[68:69], v[24:25], v[114:115] op_sel_hi:[1,0,1]
	v_pk_fma_f32 v[24:25], v[68:69], v[24:25], v[114:115] op_sel_hi:[1,0,1] neg_lo:[0,0,1] neg_hi:[0,0,1]
	v_pk_fma_f32 v[82:83], v[86:87], v[30:31], v[82:83] op_sel_hi:[1,0,1] neg_lo:[0,1,0] neg_hi:[0,1,0]
	v_pk_mul_f32 v[42:43], v[26:27], v[34:35] op_sel_hi:[1,0] neg_lo:[0,1] neg_hi:[0,1]
	s_nop 0
	v_pk_fma_f32 v[26:27], v[30:31], v[26:27], v[42:43] op_sel:[0,1,0] op_sel_hi:[0,0,1] neg_lo:[1,1,0] neg_hi:[1,0,0]
	v_pk_add_f32 v[42:43], v[28:29], v[38:39]
	v_pk_add_f32 v[28:29], v[28:29], v[38:39] neg_lo:[0,1] neg_hi:[0,1]
	v_pk_mul_f32 v[68:69], v[24:25], v[34:35] op_sel:[1,0] op_sel_hi:[0,0] neg_lo:[1,1] neg_hi:[0,1]
	v_pk_fma_f32 v[68:69], v[24:25], v[30:31], v[68:69] op_sel_hi:[1,0,1] neg_lo:[0,1,0] neg_hi:[0,1,0]
	v_pk_fma_f32 v[24:25], v[70:71], v[32:33], v[116:117] op_sel_hi:[1,0,1]
	v_pk_fma_f32 v[32:33], v[70:71], v[32:33], v[116:117] op_sel_hi:[1,0,1] neg_lo:[0,0,1] neg_hi:[0,0,1]
	v_pk_mul_f32 v[38:39], v[10:11], v[28:29] op_sel:[0,1] op_sel_hi:[0,0] neg_lo:[1,1] neg_hi:[1,0]
	v_pk_fma_f32 v[86:87], v[28:29], v[10:11], v[38:39] op_sel_hi:[1,0,1] neg_lo:[0,1,0] neg_hi:[0,1,0]
	v_pk_add_f32 v[28:29], v[44:45], v[24:25]
	v_pk_add_f32 v[24:25], v[44:45], v[24:25] neg_lo:[0,1] neg_hi:[0,1]
	v_pk_mul_f32 v[70:71], v[32:33], v[124:125] op_sel:[1,0] op_sel_hi:[0,0] neg_lo:[1,1] neg_hi:[0,1]
	v_pk_fma_f32 v[70:71], v[118:119], v[32:33], v[70:71] op_sel_hi:[0,1,1] neg_lo:[1,0,0] neg_hi:[1,0,0]
	v_pk_add_f32 v[32:33], v[126:127], v[48:49]
	v_pk_mul_f32 v[38:39], v[34:35], v[24:25] op_sel:[0,1] op_sel_hi:[0,0] neg_lo:[1,1] neg_hi:[1,0]
	v_pk_fma_f32 v[88:89], v[30:31], v[24:25], v[38:39] op_sel_hi:[0,1,1] neg_lo:[1,0,0] neg_hi:[1,0,0]
	v_pk_add_f32 v[24:25], v[32:33], v[20:21]
	v_pk_add_f32 v[32:33], v[32:33], v[20:21] neg_lo:[0,1] neg_hi:[0,1]
	v_pk_add_f32 v[20:21], v[84:85], v[22:23]
	v_pk_add_f32 v[22:23], v[84:85], v[22:23] neg_lo:[0,1] neg_hi:[0,1]
	v_pk_add_f32 v[48:49], v[126:127], v[48:49] neg_lo:[0,1] neg_hi:[0,1]
	v_pk_mul_f32 v[38:39], v[10:11], v[22:23] op_sel:[0,1] op_sel_hi:[0,0] neg_lo:[1,1] neg_hi:[1,0]
	v_pk_fma_f32 v[22:23], v[22:23], v[10:11], v[38:39] op_sel_hi:[1,0,1]
	v_pk_add_f32 v[38:39], v[16:17], v[42:43]
	v_pk_add_f32 v[16:17], v[16:17], v[42:43] neg_lo:[0,1] neg_hi:[0,1]
	s_nop 0
	v_xor_b32_e32 v43, 0x80000000, v16
	v_mov_b32_e32 v42, v17
	v_pk_add_f32 v[16:17], v[78:79], v[28:29]
	v_pk_add_f32 v[28:29], v[78:79], v[28:29] neg_lo:[0,1] neg_hi:[0,1]
	s_nop 0
	v_pk_mul_f32 v[44:45], v[10:11], v[28:29] op_sel:[0,1] op_sel_hi:[0,0] neg_lo:[1,1] neg_hi:[1,0]
	v_pk_fma_f32 v[78:79], v[10:11], v[28:29], v[44:45] op_sel_hi:[0,1,1] neg_lo:[1,0,0] neg_hi:[1,0,0]
	v_pk_add_f32 v[28:29], v[24:25], v[38:39]
	v_pk_add_f32 v[24:25], v[24:25], v[38:39] neg_lo:[0,1] neg_hi:[0,1]
	v_pk_add_f32 v[38:39], v[20:21], v[16:17]
	v_pk_add_f32 v[16:17], v[20:21], v[16:17] neg_lo:[0,1] neg_hi:[0,1]
	v_pk_add_f32 v[84:85], v[28:29], v[38:39]
	v_pk_add_f32 v[44:45], v[24:25], v[16:17] op_sel:[0,1] op_sel_hi:[1,0] neg_hi:[0,1]
	v_pk_add_f32 v[20:21], v[24:25], v[16:17] op_sel:[0,1] op_sel_hi:[1,0] neg_lo:[0,1]
	v_pk_add_f32 v[24:25], v[22:23], v[78:79]
	v_pk_add_f32 v[22:23], v[22:23], v[78:79] neg_lo:[0,1] neg_hi:[0,1]
	v_pk_add_f32 v[16:17], v[32:33], v[42:43]
	v_pk_add_f32 v[32:33], v[32:33], v[42:43] neg_lo:[0,1] neg_hi:[0,1]
	v_pk_add_f32 v[28:29], v[28:29], v[38:39] neg_lo:[0,1] neg_hi:[0,1]
	v_pk_add_f32 v[78:79], v[16:17], v[24:25]
	v_pk_add_f32 v[24:25], v[16:17], v[24:25] neg_lo:[0,1] neg_hi:[0,1]
	v_pk_add_f32 v[38:39], v[32:33], v[22:23] op_sel:[0,1] op_sel_hi:[1,0] neg_hi:[0,1]
	v_pk_add_f32 v[16:17], v[32:33], v[22:23] op_sel:[0,1] op_sel_hi:[1,0] neg_lo:[0,1]
	v_pk_add_f32 v[32:33], v[56:57], v[26:27]
	v_pk_add_f32 v[26:27], v[56:57], v[26:27] neg_lo:[0,1] neg_hi:[0,1]
	v_pk_add_f32 v[22:23], v[48:49], v[80:81]
	v_pk_add_f32 v[42:43], v[48:49], v[80:81] neg_lo:[0,1] neg_hi:[0,1]
	v_pk_mul_f32 v[48:49], v[10:11], v[26:27] op_sel:[0,1] op_sel_hi:[0,0] neg_lo:[1,1] neg_hi:[1,0]
	v_pk_fma_f32 v[26:27], v[10:11], v[26:27], v[48:49] op_sel_hi:[0,1,1]
	v_pk_add_f32 v[48:49], v[18:19], v[86:87]
	v_pk_add_f32 v[18:19], v[18:19], v[86:87] neg_lo:[0,1] neg_hi:[0,1]
	v_pk_add_f32 v[80:81], v[82:83], v[88:89] neg_lo:[0,1] neg_hi:[0,1]
	v_xor_b32_e32 v57, 0x80000000, v18
	v_mov_b32_e32 v56, v19
	v_pk_add_f32 v[18:19], v[82:83], v[88:89]
	v_pk_mul_f32 v[82:83], v[10:11], v[80:81] op_sel:[0,1] op_sel_hi:[0,0] neg_lo:[1,1] neg_hi:[1,0]
	v_pk_fma_f32 v[80:81], v[10:11], v[80:81], v[82:83] op_sel_hi:[0,1,1] neg_lo:[1,0,0] neg_hi:[1,0,0]
	v_pk_add_f32 v[82:83], v[22:23], v[48:49]
	v_pk_add_f32 v[22:23], v[22:23], v[48:49] neg_lo:[0,1] neg_hi:[0,1]
	v_pk_add_f32 v[48:49], v[32:33], v[18:19]
	v_pk_add_f32 v[18:19], v[32:33], v[18:19] neg_lo:[0,1] neg_hi:[0,1]
	v_pk_add_f32 v[88:89], v[82:83], v[48:49]
	v_xor_b32_e32 v87, 0x80000000, v18
	v_mov_b32_e32 v86, v19
	v_pk_add_f32 v[18:19], v[42:43], v[56:57]
	v_pk_add_f32 v[56:57], v[42:43], v[56:57] neg_lo:[0,1] neg_hi:[0,1]
	v_pk_add_f32 v[42:43], v[26:27], v[80:81]
	v_pk_add_f32 v[26:27], v[26:27], v[80:81] neg_lo:[0,1] neg_hi:[0,1]
	v_pk_add_f32 v[32:33], v[82:83], v[48:49] neg_lo:[0,1] neg_hi:[0,1]
	v_xor_b32_e32 v81, 0x80000000, v26
	v_mov_b32_e32 v80, v27
	v_pk_add_f32 v[82:83], v[18:19], v[42:43]
	v_pk_add_f32 v[26:27], v[18:19], v[42:43] neg_lo:[0,1] neg_hi:[0,1]
	v_pk_add_f32 v[42:43], v[56:57], v[80:81]
	v_pk_add_f32 v[18:19], v[56:57], v[80:81] neg_lo:[0,1] neg_hi:[0,1]
	v_pk_add_f32 v[56:57], v[36:37], v[76:77]
	v_pk_add_f32 v[76:77], v[36:37], v[76:77] neg_lo:[0,1] neg_hi:[0,1]
	v_pk_add_f32 v[36:37], v[40:41], v[60:61]
	v_pk_add_f32 v[40:41], v[40:41], v[60:61] neg_lo:[0,1] neg_hi:[0,1]
	v_pk_add_f32 v[48:49], v[22:23], v[86:87]
	v_pk_mul_f32 v[60:61], v[34:35], v[40:41] op_sel:[0,1] op_sel_hi:[0,0] neg_lo:[1,1] neg_hi:[1,0]
	v_pk_fma_f32 v[40:41], v[30:31], v[40:41], v[60:61] op_sel_hi:[0,1,1]
	v_pk_add_f32 v[60:61], v[46:47], v[62:63]
	v_pk_add_f32 v[46:47], v[46:47], v[62:63] neg_lo:[0,1] neg_hi:[0,1]
	v_pk_add_f32 v[22:23], v[22:23], v[86:87] neg_lo:[0,1] neg_hi:[0,1]
	v_pk_mul_f32 v[62:63], v[10:11], v[46:47] op_sel:[0,1] op_sel_hi:[0,0] neg_lo:[1,1] neg_hi:[1,0]
	v_pk_fma_f32 v[62:63], v[10:11], v[46:47], v[62:63] op_sel_hi:[0,1,1]
	v_pk_add_f32 v[46:47], v[50:51], v[58:59]
	v_pk_add_f32 v[50:51], v[50:51], v[58:59] neg_lo:[0,1] neg_hi:[0,1]
	s_nop 0
	v_pk_mul_f32 v[58:59], v[30:31], v[50:51] op_sel:[0,1] op_sel_hi:[0,0] neg_lo:[1,1] neg_hi:[1,0]
	v_pk_fma_f32 v[50:51], v[34:35], v[50:51], v[58:59] op_sel_hi:[0,1,1]
	v_pk_add_f32 v[58:59], v[52:53], v[74:75]
	v_pk_add_f32 v[52:53], v[52:53], v[74:75] neg_lo:[0,1] neg_hi:[0,1]
	s_nop 0
	v_xor_b32_e32 v75, 0x80000000, v52
	v_mov_b32_e32 v74, v53
	v_pk_add_f32 v[52:53], v[64:65], v[72:73]
	v_pk_add_f32 v[64:65], v[64:65], v[72:73] neg_lo:[0,1] neg_hi:[0,1]
	s_nop 0
	v_pk_mul_f32 v[72:73], v[30:31], v[64:65] op_sel:[0,1] op_sel_hi:[0,0] neg_lo:[1,1] neg_hi:[1,0]
	v_pk_fma_f32 v[64:65], v[34:35], v[64:65], v[72:73] op_sel_hi:[0,1,1] neg_lo:[1,0,0] neg_hi:[1,0,0]
	v_pk_add_f32 v[72:73], v[66:67], v[68:69]
	v_pk_add_f32 v[66:67], v[66:67], v[68:69] neg_lo:[0,1] neg_hi:[0,1]
	s_nop 0
	v_pk_mul_f32 v[68:69], v[10:11], v[66:67] op_sel:[0,1] op_sel_hi:[0,0] neg_lo:[1,1] neg_hi:[1,0]
	v_pk_fma_f32 v[66:67], v[10:11], v[66:67], v[68:69] op_sel_hi:[0,1,1] neg_lo:[1,0,0] neg_hi:[1,0,0]
	v_pk_add_f32 v[68:69], v[54:55], v[70:71]
	v_pk_add_f32 v[54:55], v[54:55], v[70:71] neg_lo:[0,1] neg_hi:[0,1]
	s_nop 0
	v_pk_mul_f32 v[34:35], v[34:35], v[54:55] op_sel:[0,1] op_sel_hi:[0,0] neg_lo:[1,1] neg_hi:[1,0]
	v_pk_fma_f32 v[34:35], v[30:31], v[54:55], v[34:35] op_sel_hi:[0,1,1] neg_lo:[1,0,0] neg_hi:[1,0,0]
	v_pk_add_f32 v[30:31], v[56:57], v[58:59]
	v_pk_add_f32 v[54:55], v[56:57], v[58:59] neg_lo:[0,1] neg_hi:[0,1]
	v_pk_add_f32 v[56:57], v[52:53], v[36:37]
	v_pk_add_f32 v[36:37], v[36:37], v[52:53] neg_lo:[0,1] neg_hi:[0,1]
	s_nop 0
	v_pk_mul_f32 v[52:53], v[10:11], v[36:37] op_sel:[0,1] op_sel_hi:[0,0] neg_lo:[1,1] neg_hi:[1,0]
	v_pk_fma_f32 v[58:59], v[10:11], v[36:37], v[52:53] op_sel_hi:[0,1,1]
	v_pk_add_f32 v[52:53], v[60:61], v[72:73] neg_lo:[0,1] neg_hi:[0,1]
	v_pk_add_f32 v[36:37], v[60:61], v[72:73]
	v_xor_b32_e32 v61, 0x80000000, v52
	v_mov_b32_e32 v60, v53
	v_pk_add_f32 v[52:53], v[46:47], v[68:69]
	v_pk_add_f32 v[46:47], v[46:47], v[68:69] neg_lo:[0,1] neg_hi:[0,1]
	v_pk_add_f32 v[72:73], v[64:65], v[40:41]
	v_pk_add_f32 v[40:41], v[40:41], v[64:65] neg_lo:[0,1] neg_hi:[0,1]
	v_pk_mul_f32 v[68:69], v[10:11], v[46:47] op_sel:[0,1] op_sel_hi:[0,0] neg_lo:[1,1] neg_hi:[1,0]
	v_pk_fma_f32 v[46:47], v[10:11], v[46:47], v[68:69] op_sel_hi:[0,1,1] neg_lo:[1,0,0] neg_hi:[1,0,0]
	v_pk_add_f32 v[68:69], v[30:31], v[36:37]
	v_pk_add_f32 v[30:31], v[30:31], v[36:37] neg_lo:[0,1] neg_hi:[0,1]
	v_pk_add_f32 v[36:37], v[56:57], v[52:53]
	v_pk_add_f32 v[52:53], v[56:57], v[52:53] neg_lo:[0,1] neg_hi:[0,1]
	v_pk_mul_f32 v[64:65], v[10:11], v[40:41] op_sel:[0,1] op_sel_hi:[0,0] neg_lo:[1,1] neg_hi:[1,0]
	v_xor_b32_e32 v57, 0x80000000, v52
	v_mov_b32_e32 v56, v53
	v_pk_fma_f32 v[64:65], v[10:11], v[40:41], v[64:65] op_sel_hi:[0,1,1]
	v_pk_add_f32 v[40:41], v[62:63], v[66:67]
	v_pk_add_f32 v[62:63], v[62:63], v[66:67] neg_lo:[0,1] neg_hi:[0,1]
	v_pk_add_f32 v[70:71], v[68:69], v[36:37]
	v_pk_add_f32 v[52:53], v[68:69], v[36:37] neg_lo:[0,1] neg_hi:[0,1]
	v_pk_add_f32 v[68:69], v[30:31], v[56:57]
	v_pk_add_f32 v[36:37], v[30:31], v[56:57] neg_lo:[0,1] neg_hi:[0,1]
	v_pk_add_f32 v[56:57], v[58:59], v[46:47]
	v_pk_add_f32 v[46:47], v[58:59], v[46:47] neg_lo:[0,1] neg_hi:[0,1]
	v_xor_b32_e32 v67, 0x80000000, v62
	v_mov_b32_e32 v66, v63
	v_pk_add_f32 v[62:63], v[50:51], v[34:35]
	v_pk_add_f32 v[34:35], v[50:51], v[34:35] neg_lo:[0,1] neg_hi:[0,1]
	v_pk_add_f32 v[30:31], v[54:55], v[60:61]
	v_pk_add_f32 v[54:55], v[54:55], v[60:61] neg_lo:[0,1] neg_hi:[0,1]
	v_xor_b32_e32 v59, 0x80000000, v46
	v_mov_b32_e32 v58, v47
	v_pk_add_f32 v[60:61], v[30:31], v[56:57]
	v_pk_add_f32 v[46:47], v[30:31], v[56:57] neg_lo:[0,1] neg_hi:[0,1]
	v_pk_add_f32 v[56:57], v[54:55], v[58:59]
	v_pk_add_f32 v[30:31], v[54:55], v[58:59] neg_lo:[0,1] neg_hi:[0,1]
	v_pk_add_f32 v[54:55], v[76:77], v[74:75]
	v_pk_mul_f32 v[50:51], v[10:11], v[34:35] op_sel:[0,1] op_sel_hi:[0,0] neg_lo:[1,1] neg_hi:[1,0]
	v_pk_add_f32 v[58:59], v[76:77], v[74:75] neg_lo:[0,1] neg_hi:[0,1]
	v_pk_fma_f32 v[34:35], v[10:11], v[34:35], v[50:51] op_sel_hi:[0,1,1] neg_lo:[1,0,0] neg_hi:[1,0,0]
	v_pk_add_f32 v[50:51], v[54:55], v[40:41]
	v_pk_add_f32 v[40:41], v[54:55], v[40:41] neg_lo:[0,1] neg_hi:[0,1]
	v_pk_add_f32 v[54:55], v[72:73], v[62:63]
	v_pk_add_f32 v[62:63], v[72:73], v[62:63] neg_lo:[0,1] neg_hi:[0,1]
	v_lshl_add_u32 v10, v13, 3, 0
	v_xor_b32_e32 v73, 0x80000000, v62
	v_mov_b32_e32 v72, v63
	v_pk_add_f32 v[62:63], v[50:51], v[54:55]
	v_pk_add_f32 v[54:55], v[50:51], v[54:55] neg_lo:[0,1] neg_hi:[0,1]
	v_pk_add_f32 v[50:51], v[58:59], v[66:67]
	v_pk_add_f32 v[58:59], v[58:59], v[66:67] neg_lo:[0,1] neg_hi:[0,1]
	v_pk_add_f32 v[66:67], v[64:65], v[34:35]
	v_pk_add_f32 v[34:35], v[64:65], v[34:35] neg_lo:[0,1] neg_hi:[0,1]
	v_pk_add_f32 v[74:75], v[40:41], v[72:73]
	v_pk_add_f32 v[40:41], v[40:41], v[72:73] neg_lo:[0,1] neg_hi:[0,1]
	v_pk_add_f32 v[72:73], v[50:51], v[66:67]
	v_pk_add_f32 v[50:51], v[50:51], v[66:67] neg_lo:[0,1] neg_hi:[0,1]
	v_pk_add_f32 v[66:67], v[58:59], v[34:35] op_sel:[0,1] op_sel_hi:[1,0] neg_hi:[0,1]
	v_pk_add_f32 v[34:35], v[58:59], v[34:35] op_sel:[0,1] op_sel_hi:[1,0] neg_lo:[0,1]
	v_pk_mul_f32 v[58:59], v[84:85], s[14:15] op_sel:[1,0] neg_lo:[1,0]
	s_nop 0
	v_pk_fma_f32 v[58:59], v[84:85], s[94:95], v[58:59] op_sel_hi:[0,1,1]
	ds_write_b64 v10, v[58:59]
	v_pk_fma_f32 v[58:59], v[178:179], s[90:91], v[178:179] op_sel:[1,0,0] op_sel_hi:[0,1,1]
	v_pk_mul_f32 v[64:65], v[58:59], v[70:71] op_sel:[1,1] op_sel_hi:[0,1] neg_lo:[0,1]
	v_pk_fma_f32 v[64:65], v[58:59], v[70:71], v[64:65] op_sel_hi:[1,0,1]
	ds_write_b64 v10, v[64:65] offset:4224
	v_pk_mul_f32 v[64:65], v[178:179], v[58:59] op_sel:[1,1] op_sel_hi:[0,1] neg_lo:[0,1]
	v_pk_fma_f32 v[58:59], v[178:179], v[58:59], v[64:65] op_sel_hi:[1,0,1]
	s_nop 0
	v_pk_mul_f32 v[64:65], v[58:59], v[88:89] op_sel:[1,1] op_sel_hi:[0,1] neg_lo:[0,1]
	v_pk_fma_f32 v[64:65], v[58:59], v[88:89], v[64:65] op_sel_hi:[1,0,1]
	ds_write_b64 v10, v[64:65] offset:8448
	v_pk_mul_f32 v[64:65], v[178:179], v[58:59] op_sel:[1,1] op_sel_hi:[0,1] neg_lo:[0,1]
	v_pk_fma_f32 v[58:59], v[178:179], v[58:59], v[64:65] op_sel_hi:[1,0,1]
	s_nop 0
	v_pk_mul_f32 v[64:65], v[58:59], v[62:63] op_sel:[1,1] op_sel_hi:[0,1] neg_lo:[0,1]
	v_pk_fma_f32 v[62:63], v[58:59], v[62:63], v[64:65] op_sel_hi:[1,0,1]
	ds_write_b64 v10, v[62:63] offset:12672
	v_pk_mul_f32 v[62:63], v[178:179], v[58:59] op_sel:[1,1] op_sel_hi:[0,1] neg_lo:[0,1]
	v_pk_fma_f32 v[58:59], v[178:179], v[58:59], v[62:63] op_sel_hi:[1,0,1]
	s_nop 0
	v_pk_mul_f32 v[62:63], v[58:59], v[78:79] op_sel:[1,1] op_sel_hi:[0,1] neg_lo:[0,1]
	v_pk_fma_f32 v[62:63], v[58:59], v[78:79], v[62:63] op_sel_hi:[1,0,1]
	ds_write_b64 v10, v[62:63] offset:16896
	v_pk_mul_f32 v[62:63], v[178:179], v[58:59] op_sel:[1,1] op_sel_hi:[0,1] neg_lo:[0,1]
	v_pk_fma_f32 v[58:59], v[178:179], v[58:59], v[62:63] op_sel_hi:[1,0,1]
	s_nop 0
	v_pk_mul_f32 v[62:63], v[58:59], v[60:61] op_sel:[1,1] op_sel_hi:[0,1] neg_lo:[0,1]
	v_pk_fma_f32 v[60:61], v[58:59], v[60:61], v[62:63] op_sel_hi:[1,0,1]
	ds_write_b64 v10, v[60:61] offset:21120
	v_pk_mul_f32 v[60:61], v[178:179], v[58:59] op_sel:[1,1] op_sel_hi:[0,1] neg_lo:[0,1]
	v_pk_fma_f32 v[58:59], v[178:179], v[58:59], v[60:61] op_sel_hi:[1,0,1]
	s_nop 0
	v_pk_mul_f32 v[60:61], v[82:83], v[58:59] op_sel:[1,1] op_sel_hi:[1,0] neg_lo:[1,0]
	s_nop 0
	v_pk_fma_f32 v[60:61], v[82:83], v[58:59], v[60:61] op_sel_hi:[0,1,1]
	ds_write_b64 v10, v[60:61] offset:25344
	v_pk_mul_f32 v[60:61], v[178:179], v[58:59] op_sel:[1,1] op_sel_hi:[0,1] neg_lo:[0,1]
	v_pk_fma_f32 v[58:59], v[178:179], v[58:59], v[60:61] op_sel_hi:[1,0,1]
	s_nop 0
	v_pk_mul_f32 v[60:61], v[72:73], v[58:59] op_sel:[1,1] op_sel_hi:[1,0] neg_lo:[1,0]
	s_nop 0
	v_pk_fma_f32 v[60:61], v[72:73], v[58:59], v[60:61] op_sel_hi:[0,1,1]
	ds_write_b64 v10, v[60:61] offset:29568
	v_pk_mul_f32 v[60:61], v[178:179], v[58:59] op_sel:[1,1] op_sel_hi:[0,1] neg_lo:[0,1]
	v_pk_fma_f32 v[58:59], v[178:179], v[58:59], v[60:61] op_sel_hi:[1,0,1]
	s_nop 0
	v_pk_mul_f32 v[60:61], v[44:45], v[58:59] op_sel:[1,1] op_sel_hi:[1,0] neg_lo:[1,0]
	s_nop 0
	v_pk_fma_f32 v[44:45], v[44:45], v[58:59], v[60:61] op_sel_hi:[0,1,1]
	ds_write_b64 v10, v[44:45] offset:33792
	v_pk_mul_f32 v[44:45], v[178:179], v[58:59] op_sel:[1,1] op_sel_hi:[0,1] neg_lo:[0,1]
	v_pk_fma_f32 v[44:45], v[178:179], v[58:59], v[44:45] op_sel_hi:[1,0,1]
	s_nop 0
	v_pk_mul_f32 v[58:59], v[68:69], v[44:45] op_sel:[1,1] op_sel_hi:[1,0] neg_lo:[1,0]
	s_nop 0
	v_pk_fma_f32 v[58:59], v[68:69], v[44:45], v[58:59] op_sel_hi:[0,1,1]
	ds_write_b64 v10, v[58:59] offset:38016
	v_pk_mul_f32 v[58:59], v[178:179], v[44:45] op_sel:[1,1] op_sel_hi:[0,1] neg_lo:[0,1]
	v_pk_fma_f32 v[44:45], v[178:179], v[44:45], v[58:59] op_sel_hi:[1,0,1]
	s_nop 0
	v_pk_mul_f32 v[58:59], v[48:49], v[44:45] op_sel:[1,1] op_sel_hi:[1,0] neg_lo:[1,0]
	s_nop 0
	v_pk_fma_f32 v[48:49], v[48:49], v[44:45], v[58:59] op_sel_hi:[0,1,1]
	ds_write_b64 v10, v[48:49] offset:42240
	v_pk_mul_f32 v[48:49], v[178:179], v[44:45] op_sel:[1,1] op_sel_hi:[0,1] neg_lo:[0,1]
	v_pk_fma_f32 v[44:45], v[178:179], v[44:45], v[48:49] op_sel_hi:[1,0,1]
	s_nop 0
	v_pk_mul_f32 v[48:49], v[74:75], v[44:45] op_sel:[1,1] op_sel_hi:[1,0] neg_lo:[1,0]
	s_nop 0
	v_pk_fma_f32 v[48:49], v[74:75], v[44:45], v[48:49] op_sel_hi:[0,1,1]
	ds_write_b64 v10, v[48:49] offset:46464
	v_pk_mul_f32 v[48:49], v[178:179], v[44:45] op_sel:[1,1] op_sel_hi:[0,1] neg_lo:[0,1]
	v_pk_fma_f32 v[44:45], v[178:179], v[44:45], v[48:49] op_sel_hi:[1,0,1]
	s_nop 0
	v_pk_mul_f32 v[48:49], v[38:39], v[44:45] op_sel:[1,1] op_sel_hi:[1,0] neg_lo:[1,0]
	s_nop 0
	v_pk_fma_f32 v[38:39], v[38:39], v[44:45], v[48:49] op_sel_hi:[0,1,1]
	ds_write_b64 v10, v[38:39] offset:50688
	v_pk_mul_f32 v[38:39], v[178:179], v[44:45] op_sel:[1,1] op_sel_hi:[0,1] neg_lo:[0,1]
	v_pk_fma_f32 v[38:39], v[178:179], v[44:45], v[38:39] op_sel_hi:[1,0,1]
	s_nop 0
	v_pk_mul_f32 v[44:45], v[56:57], v[38:39] op_sel:[1,1] op_sel_hi:[1,0] neg_lo:[1,0]
	s_nop 0
	v_pk_fma_f32 v[44:45], v[56:57], v[38:39], v[44:45] op_sel_hi:[0,1,1]
	ds_write_b64 v10, v[44:45] offset:54912
	v_pk_mul_f32 v[44:45], v[178:179], v[38:39] op_sel:[1,1] op_sel_hi:[0,1] neg_lo:[0,1]
	v_pk_fma_f32 v[38:39], v[178:179], v[38:39], v[44:45] op_sel_hi:[1,0,1]
	s_nop 0
	v_pk_mul_f32 v[44:45], v[42:43], v[38:39] op_sel:[1,1] op_sel_hi:[1,0] neg_lo:[1,0]
	s_nop 0
	v_pk_fma_f32 v[42:43], v[42:43], v[38:39], v[44:45] op_sel_hi:[0,1,1]
	ds_write_b64 v10, v[42:43] offset:59136
	v_pk_mul_f32 v[42:43], v[178:179], v[38:39] op_sel:[1,1] op_sel_hi:[0,1] neg_lo:[0,1]
	v_pk_fma_f32 v[38:39], v[178:179], v[38:39], v[42:43] op_sel_hi:[1,0,1]
	s_nop 0
	v_pk_mul_f32 v[42:43], v[66:67], v[38:39] op_sel:[1,1] op_sel_hi:[1,0] neg_lo:[1,0]
	s_nop 0
	v_pk_fma_f32 v[42:43], v[66:67], v[38:39], v[42:43] op_sel_hi:[0,1,1]
	ds_write_b64 v10, v[42:43] offset:63360
	v_pk_mul_f32 v[42:43], v[178:179], v[38:39] op_sel:[1,1] op_sel_hi:[0,1] neg_lo:[0,1]
	v_pk_fma_f32 v[38:39], v[178:179], v[38:39], v[42:43] op_sel_hi:[1,0,1]
	s_nop 0
	v_pk_mul_f32 v[42:43], v[28:29], v[38:39] op_sel:[1,1] op_sel_hi:[1,0] neg_lo:[1,0]
	v_add_u32_e32 v13, 0x10800, v10
	v_pk_fma_f32 v[28:29], v[28:29], v[38:39], v[42:43] op_sel_hi:[0,1,1]
	ds_write_b64 v13, v[28:29]
	v_pk_mul_f32 v[28:29], v[178:179], v[38:39] op_sel:[1,1] op_sel_hi:[0,1] neg_lo:[0,1]
	v_pk_fma_f32 v[28:29], v[178:179], v[38:39], v[28:29] op_sel_hi:[1,0,1]
	s_nop 0
	v_pk_mul_f32 v[38:39], v[52:53], v[28:29] op_sel:[1,1] op_sel_hi:[1,0] neg_lo:[1,0]
	v_add_u32_e32 v13, 0x11880, v10
	v_pk_fma_f32 v[38:39], v[52:53], v[28:29], v[38:39] op_sel_hi:[0,1,1]
	ds_write_b64 v13, v[38:39]
	v_pk_mul_f32 v[38:39], v[178:179], v[28:29] op_sel:[1,1] op_sel_hi:[0,1] neg_lo:[0,1]
	v_pk_fma_f32 v[28:29], v[178:179], v[28:29], v[38:39] op_sel_hi:[1,0,1]
	s_nop 0
	v_pk_mul_f32 v[38:39], v[32:33], v[28:29] op_sel:[1,1] op_sel_hi:[1,0] neg_lo:[1,0]
	v_add_u32_e32 v13, 0x12900, v10
	v_pk_fma_f32 v[32:33], v[32:33], v[28:29], v[38:39] op_sel_hi:[0,1,1]
	ds_write_b64 v13, v[32:33]
	v_pk_mul_f32 v[32:33], v[178:179], v[28:29] op_sel:[1,1] op_sel_hi:[0,1] neg_lo:[0,1]
	v_pk_fma_f32 v[28:29], v[178:179], v[28:29], v[32:33] op_sel_hi:[1,0,1]
	s_nop 0
	v_pk_mul_f32 v[32:33], v[54:55], v[28:29] op_sel:[1,1] op_sel_hi:[1,0] neg_lo:[1,0]
	v_add_u32_e32 v13, 0x13980, v10
	v_pk_fma_f32 v[32:33], v[54:55], v[28:29], v[32:33] op_sel_hi:[0,1,1]
	ds_write_b64 v13, v[32:33]
	v_pk_mul_f32 v[32:33], v[178:179], v[28:29] op_sel:[1,1] op_sel_hi:[0,1] neg_lo:[0,1]
	v_pk_fma_f32 v[28:29], v[178:179], v[28:29], v[32:33] op_sel_hi:[1,0,1]
	s_nop 0
	v_pk_mul_f32 v[32:33], v[24:25], v[28:29] op_sel:[1,1] op_sel_hi:[1,0] neg_lo:[1,0]
	v_add_u32_e32 v13, 0x14a00, v10
	v_pk_fma_f32 v[24:25], v[24:25], v[28:29], v[32:33] op_sel_hi:[0,1,1]
	ds_write_b64 v13, v[24:25]
	v_pk_mul_f32 v[24:25], v[178:179], v[28:29] op_sel:[1,1] op_sel_hi:[0,1] neg_lo:[0,1]
	v_pk_fma_f32 v[24:25], v[178:179], v[28:29], v[24:25] op_sel_hi:[1,0,1]
	s_nop 0
	v_pk_mul_f32 v[28:29], v[46:47], v[24:25] op_sel:[1,1] op_sel_hi:[1,0] neg_lo:[1,0]
	v_add_u32_e32 v13, 0x15a80, v10
	v_pk_fma_f32 v[28:29], v[46:47], v[24:25], v[28:29] op_sel_hi:[0,1,1]
	ds_write_b64 v13, v[28:29]
	v_pk_mul_f32 v[28:29], v[178:179], v[24:25] op_sel:[1,1] op_sel_hi:[0,1] neg_lo:[0,1]
	v_pk_fma_f32 v[24:25], v[178:179], v[24:25], v[28:29] op_sel_hi:[1,0,1]
	s_nop 0
	v_pk_mul_f32 v[28:29], v[26:27], v[24:25] op_sel:[1,1] op_sel_hi:[1,0] neg_lo:[1,0]
	v_add_u32_e32 v13, 0x16b00, v10
	v_pk_fma_f32 v[26:27], v[26:27], v[24:25], v[28:29] op_sel_hi:[0,1,1]
	ds_write_b64 v13, v[26:27]
	v_pk_mul_f32 v[26:27], v[178:179], v[24:25] op_sel:[1,1] op_sel_hi:[0,1] neg_lo:[0,1]
	v_pk_fma_f32 v[24:25], v[178:179], v[24:25], v[26:27] op_sel_hi:[1,0,1]
	s_nop 0
	v_pk_mul_f32 v[26:27], v[50:51], v[24:25] op_sel:[1,1] op_sel_hi:[1,0] neg_lo:[1,0]
	v_add_u32_e32 v13, 0x17b80, v10
	v_pk_fma_f32 v[26:27], v[50:51], v[24:25], v[26:27] op_sel_hi:[0,1,1]
	ds_write_b64 v13, v[26:27]
	v_pk_mul_f32 v[26:27], v[178:179], v[24:25] op_sel:[1,1] op_sel_hi:[0,1] neg_lo:[0,1]
	v_pk_fma_f32 v[24:25], v[178:179], v[24:25], v[26:27] op_sel_hi:[1,0,1]
	s_nop 0
	v_pk_mul_f32 v[26:27], v[20:21], v[24:25] op_sel:[1,1] op_sel_hi:[1,0] neg_lo:[1,0]
	v_add_u32_e32 v13, 0x18c00, v10
	v_pk_fma_f32 v[20:21], v[20:21], v[24:25], v[26:27] op_sel_hi:[0,1,1]
	ds_write_b64 v13, v[20:21]
	v_pk_mul_f32 v[20:21], v[178:179], v[24:25] op_sel:[1,1] op_sel_hi:[0,1] neg_lo:[0,1]
	v_pk_fma_f32 v[20:21], v[178:179], v[24:25], v[20:21] op_sel_hi:[1,0,1]
	s_nop 0
	v_pk_mul_f32 v[24:25], v[36:37], v[20:21] op_sel:[1,1] op_sel_hi:[1,0] neg_lo:[1,0]
	v_add_u32_e32 v13, 0x19c80, v10
	v_pk_fma_f32 v[24:25], v[36:37], v[20:21], v[24:25] op_sel_hi:[0,1,1]
	ds_write_b64 v13, v[24:25]
	v_pk_mul_f32 v[24:25], v[178:179], v[20:21] op_sel:[1,1] op_sel_hi:[0,1] neg_lo:[0,1]
	v_pk_fma_f32 v[20:21], v[178:179], v[20:21], v[24:25] op_sel_hi:[1,0,1]
	s_nop 0
	v_pk_mul_f32 v[24:25], v[22:23], v[20:21] op_sel:[1,1] op_sel_hi:[1,0] neg_lo:[1,0]
	v_add_u32_e32 v13, 0x1ad00, v10
	v_pk_fma_f32 v[22:23], v[22:23], v[20:21], v[24:25] op_sel_hi:[0,1,1]
	ds_write_b64 v13, v[22:23]
	v_pk_mul_f32 v[22:23], v[178:179], v[20:21] op_sel:[1,1] op_sel_hi:[0,1] neg_lo:[0,1]
	v_pk_fma_f32 v[20:21], v[178:179], v[20:21], v[22:23] op_sel_hi:[1,0,1]
	s_nop 0
	v_pk_mul_f32 v[22:23], v[40:41], v[20:21] op_sel:[1,1] op_sel_hi:[1,0] neg_lo:[1,0]
	v_add_u32_e32 v13, 0x1bd80, v10
	v_pk_fma_f32 v[22:23], v[40:41], v[20:21], v[22:23] op_sel_hi:[0,1,1]
	ds_write_b64 v13, v[22:23]
	v_pk_mul_f32 v[22:23], v[178:179], v[20:21] op_sel:[1,1] op_sel_hi:[0,1] neg_lo:[0,1]
	v_pk_fma_f32 v[20:21], v[178:179], v[20:21], v[22:23] op_sel_hi:[1,0,1]
	s_nop 0
	v_pk_mul_f32 v[22:23], v[16:17], v[20:21] op_sel:[1,1] op_sel_hi:[1,0] neg_lo:[1,0]
	v_add_u32_e32 v13, 0x1ce00, v10
	v_pk_fma_f32 v[16:17], v[16:17], v[20:21], v[22:23] op_sel_hi:[0,1,1]
	ds_write_b64 v13, v[16:17]
	v_pk_mul_f32 v[16:17], v[178:179], v[20:21] op_sel:[1,1] op_sel_hi:[0,1] neg_lo:[0,1]
	v_pk_fma_f32 v[16:17], v[178:179], v[20:21], v[16:17] op_sel_hi:[1,0,1]
	s_nop 0
	v_pk_mul_f32 v[20:21], v[30:31], v[16:17] op_sel:[1,1] op_sel_hi:[1,0] neg_lo:[1,0]
	v_add_u32_e32 v13, 0x1de80, v10
	v_pk_fma_f32 v[20:21], v[30:31], v[16:17], v[20:21] op_sel_hi:[0,1,1]
	ds_write_b64 v13, v[20:21]
	v_pk_mul_f32 v[20:21], v[178:179], v[16:17] op_sel:[1,1] op_sel_hi:[0,1] neg_lo:[0,1]
	v_pk_fma_f32 v[16:17], v[178:179], v[16:17], v[20:21] op_sel_hi:[1,0,1]
	s_nop 0
	v_pk_mul_f32 v[20:21], v[18:19], v[16:17] op_sel:[1,1] op_sel_hi:[1,0] neg_lo:[1,0]
	v_add_u32_e32 v13, 0x1ef00, v10
	v_pk_fma_f32 v[18:19], v[18:19], v[16:17], v[20:21] op_sel_hi:[0,1,1]
	ds_write_b64 v13, v[18:19]
	v_pk_mul_f32 v[18:19], v[178:179], v[16:17] op_sel:[1,1] op_sel_hi:[0,1] neg_lo:[0,1]
	v_pk_fma_f32 v[14:15], v[178:179], v[16:17], v[18:19] op_sel_hi:[1,0,1]
	s_nop 0
	v_pk_mul_f32 v[16:17], v[34:35], v[14:15] op_sel:[1,1] op_sel_hi:[1,0] neg_lo:[1,0]
	v_add_u32_e32 v10, 0x1ff80, v10
	v_pk_fma_f32 v[14:15], v[34:35], v[14:15], v[16:17] op_sel_hi:[0,1,1]
	ds_write_b64 v10, v[14:15]
	v_mov_b32_e32 v10, v174
	v_mov_b32_e32 v13, v172
	s_waitcnt lgkmcnt(0)
	s_barrier
	v_mov_b32_e32 v14, v180
	v_xad_u32 v28, v13, 3, v10
	v_lshl_add_u32 v71, v28, 3, 0
	v_xad_u32 v28, v13, 4, v10
	v_lshl_add_u32 v70, v28, 3, 0
	v_xad_u32 v28, v13, 5, v10
	v_lshl_add_u32 v69, v28, 3, 0
	v_xad_u32 v28, v13, 6, v10
	v_lshl_add_u32 v68, v28, 3, 0
	v_xad_u32 v28, v13, 7, v10
	v_lshl_add_u32 v67, v28, 3, 0
	v_xad_u32 v28, v13, 8, v10
	v_lshl_add_u32 v28, v28, 3, 0
	v_add_u32_e32 v66, 0x800, v28
	v_xad_u32 v28, v13, 9, v10
	v_lshl_add_u32 v28, v28, 3, 0
	v_add_u32_e32 v65, 0x800, v28
	v_xad_u32 v28, v13, 10, v10
	v_lshl_add_u32 v28, v28, 3, 0
	v_add_u32_e32 v64, 0x800, v28
	v_xad_u32 v28, v13, 11, v10
	v_lshl_add_u32 v28, v28, 3, 0
	v_add_u32_e32 v16, v13, v10
	v_add_u32_e32 v63, 0x800, v28
	v_xad_u32 v28, v13, 12, v10
	v_mov_b32_e32 v15, v181
	v_lshl_add_u32 v74, v16, 3, 0
	v_lshl_add_u32 v28, v28, 3, 0
	ds_read2_b64 v[16:19], v74 offset1:16
	ds_read2_b64 v[38:41], v66 offset1:16
	v_add_u32_e32 v62, 0x800, v28
	v_xad_u32 v28, v13, 13, v10
	v_xad_u32 v20, v13, 1, v10
	v_lshl_add_u32 v28, v28, 3, 0
	v_lshl_add_u32 v73, v20, 3, 0
	v_xad_u32 v24, v13, 2, v10
	v_add_u32_e32 v61, 0x800, v28
	v_xad_u32 v28, v13, 14, v10
	v_xad_u32 v10, v13, 15, v10
	ds_read2_b64 v[20:23], v73 offset0:32 offset1:48
	ds_read2_b64 v[46:49], v65 offset0:32 offset1:48
	v_lshl_add_u32 v28, v28, 3, 0
	v_lshl_add_u32 v10, v10, 3, 0
	v_lshl_add_u32 v72, v24, 3, 0
	v_add_u32_e32 v60, 0x800, v28
	v_add_u32_e32 v13, 0x800, v10
	v_mov_b32_e32 v10, v1
	ds_read2_b64 v[24:27], v72 offset0:64 offset1:80
	ds_read2_b64 v[56:59], v71 offset0:96 offset1:112
	ds_read2_b64 v[76:79], v70 offset0:128 offset1:144
	ds_read2_b64 v[80:83], v69 offset0:160 offset1:176
	ds_read2_b64 v[84:87], v68 offset0:192 offset1:208
	ds_read2_b64 v[88:91], v67 offset0:224 offset1:240
	ds_read2_b64 v[52:55], v64 offset0:64 offset1:80
	ds_read2_b64 v[92:95], v63 offset0:96 offset1:112
	ds_read2_b64 v[96:99], v62 offset0:128 offset1:144
	ds_read2_b64 v[100:103], v61 offset0:160 offset1:176
	ds_read2_b64 v[104:107], v60 offset0:192 offset1:208
	ds_read2_b64 v[108:111], v13 offset0:224 offset1:240
	s_waitcnt lgkmcnt(14)
	v_pk_add_f32 v[112:113], v[16:17], v[38:39]
	v_pk_add_f32 v[38:39], v[16:17], v[38:39] neg_lo:[0,1] neg_hi:[0,1]
	v_pk_add_f32 v[16:17], v[18:19], v[40:41]
	v_pk_add_f32 v[18:19], v[18:19], v[40:41] neg_lo:[0,1] neg_hi:[0,1]
	v_mov_b32_e32 v28, v164
	v_mov_b32_e32 v30, v165
	v_mov_b32_e32 v32, v166
	v_mov_b32_e32 v10, v167
	v_mov_b32_e32 v36, v168
	v_mov_b32_e32 v34, v169
	v_mov_b32_e32 v44, v170
	v_mov_b32_e32 v29, v171
	v_pk_mul_f32 v[40:41], v[18:19], v[44:45] op_sel:[1,0] op_sel_hi:[0,0] neg_lo:[1,1] neg_hi:[0,1]
	s_nop 0
	v_pk_fma_f32 v[42:43], v[18:19], v[28:29], v[40:41] op_sel_hi:[1,0,1]
	s_waitcnt lgkmcnt(12)
	v_pk_add_f32 v[18:19], v[20:21], v[46:47]
	v_pk_add_f32 v[20:21], v[20:21], v[46:47] neg_lo:[0,1] neg_hi:[0,1]
	s_nop 0
	v_pk_mul_f32 v[40:41], v[20:21], v[34:35] op_sel:[1,0] op_sel_hi:[0,0] neg_lo:[1,1] neg_hi:[0,1]
	s_nop 0
	v_pk_fma_f32 v[46:47], v[20:21], v[30:31], v[40:41] op_sel_hi:[1,0,1]
	v_pk_add_f32 v[20:21], v[22:23], v[48:49]
	v_pk_add_f32 v[22:23], v[22:23], v[48:49] neg_lo:[0,1] neg_hi:[0,1]
	s_nop 0
	v_pk_mul_f32 v[40:41], v[22:23], v[36:37] op_sel:[1,0] op_sel_hi:[0,0] neg_lo:[1,1] neg_hi:[0,1]
	s_nop 0
	v_pk_fma_f32 v[50:51], v[22:23], v[32:33], v[40:41] op_sel_hi:[1,0,1]
	s_waitcnt lgkmcnt(5)
	v_pk_add_f32 v[22:23], v[24:25], v[52:53]
	v_pk_add_f32 v[24:25], v[24:25], v[52:53] neg_lo:[0,1] neg_hi:[0,1]
	s_nop 0
	v_pk_mul_f32 v[40:41], v[24:25], v[10:11] op_sel:[1,0] op_sel_hi:[0,0] neg_lo:[1,1] neg_hi:[0,1]
	s_nop 0
	v_pk_fma_f32 v[52:53], v[24:25], v[10:11], v[40:41] op_sel_hi:[1,0,1]
	v_pk_add_f32 v[24:25], v[26:27], v[54:55]
	v_pk_add_f32 v[26:27], v[26:27], v[54:55] neg_lo:[0,1] neg_hi:[0,1]
	s_nop 0
	v_pk_mul_f32 v[40:41], v[26:27], v[36:37] op_sel_hi:[1,0]
	s_nop 0
	v_pk_fma_f32 v[54:55], v[26:27], v[32:33], v[40:41] op_sel:[1,0,0] op_sel_hi:[0,0,1] neg_lo:[1,1,0] neg_hi:[0,1,0]
	s_waitcnt lgkmcnt(4)
	v_pk_add_f32 v[40:41], v[56:57], v[92:93] neg_lo:[0,1] neg_hi:[0,1]
	v_pk_add_f32 v[26:27], v[56:57], v[92:93]
	v_pk_mul_f32 v[48:49], v[40:41], v[34:35] op_sel_hi:[1,0]
	s_nop 0
	v_pk_fma_f32 v[56:57], v[40:41], v[30:31], v[48:49] op_sel:[1,0,0] op_sel_hi:[0,0,1] neg_lo:[1,1,0] neg_hi:[0,1,0]
	v_pk_add_f32 v[48:49], v[58:59], v[94:95] neg_lo:[0,1] neg_hi:[0,1]
	v_pk_add_f32 v[40:41], v[58:59], v[94:95]
	v_pk_mul_f32 v[58:59], v[48:49], v[44:45] op_sel_hi:[1,0]
	v_xor_b32_e32 v92, 0x80000000, v49
	v_mov_b32_e32 v93, v48
	s_waitcnt lgkmcnt(3)
	v_pk_add_f32 v[48:49], v[76:77], v[96:97]
	v_pk_add_f32 v[76:77], v[76:77], v[96:97] neg_lo:[0,1] neg_hi:[0,1]
	v_pk_fma_f32 v[58:59], v[92:93], v[28:29], v[58:59] op_sel_hi:[1,0,1] neg_lo:[0,1,0] neg_hi:[0,1,0]
	v_xor_b32_e32 v93, 0x80000000, v76
	v_mov_b32_e32 v92, v77
	v_pk_add_f32 v[76:77], v[78:79], v[98:99]
	v_pk_add_f32 v[78:79], v[78:79], v[98:99] neg_lo:[0,1] neg_hi:[0,1]
	s_nop 0
	v_pk_mul_f32 v[94:95], v[78:79], v[44:45] op_sel_hi:[1,0] neg_lo:[0,1] neg_hi:[0,1]
	s_nop 0
	v_pk_fma_f32 v[78:79], v[78:79], v[28:29], v[94:95] op_sel:[1,0,0] op_sel_hi:[0,0,1] neg_lo:[1,1,0] neg_hi:[0,1,0]
	s_waitcnt lgkmcnt(2)
	v_pk_add_f32 v[94:95], v[80:81], v[100:101]
	v_pk_add_f32 v[80:81], v[80:81], v[100:101] neg_lo:[0,1] neg_hi:[0,1]
	s_nop 0
	v_pk_mul_f32 v[96:97], v[80:81], v[34:35] op_sel_hi:[1,0] neg_lo:[0,1] neg_hi:[0,1]
	s_nop 0
	v_pk_fma_f32 v[80:81], v[80:81], v[30:31], v[96:97] op_sel:[1,0,0] op_sel_hi:[0,0,1] neg_lo:[1,1,0] neg_hi:[0,1,0]
	v_pk_add_f32 v[96:97], v[82:83], v[102:103]
	v_pk_add_f32 v[82:83], v[82:83], v[102:103] neg_lo:[0,1] neg_hi:[0,1]
	s_nop 0
	v_pk_mul_f32 v[98:99], v[82:83], v[36:37] op_sel_hi:[1,0] neg_lo:[0,1] neg_hi:[0,1]
	s_nop 0
	v_pk_fma_f32 v[82:83], v[82:83], v[32:33], v[98:99] op_sel:[1,0,0] op_sel_hi:[0,0,1] neg_lo:[1,1,0] neg_hi:[0,1,0]
	s_waitcnt lgkmcnt(1)
	v_pk_add_f32 v[98:99], v[84:85], v[104:105]
	v_pk_add_f32 v[84:85], v[84:85], v[104:105] neg_lo:[0,1] neg_hi:[0,1]
	s_nop 0
	v_pk_mul_f32 v[100:101], v[84:85], v[10:11] op_sel:[1,0] op_sel_hi:[0,0] neg_lo:[1,1] neg_hi:[0,1]
	s_nop 0
	v_pk_fma_f32 v[84:85], v[84:85], v[10:11], v[100:101] op_sel_hi:[1,0,1] neg_lo:[0,1,0] neg_hi:[0,1,0]
	v_pk_add_f32 v[100:101], v[86:87], v[106:107]
	v_pk_add_f32 v[86:87], v[86:87], v[106:107] neg_lo:[0,1] neg_hi:[0,1]
	s_nop 0
	v_pk_mul_f32 v[36:37], v[86:87], v[36:37] op_sel:[1,0] op_sel_hi:[0,0] neg_lo:[1,1] neg_hi:[0,1]
	s_nop 0
	v_pk_fma_f32 v[86:87], v[86:87], v[32:33], v[36:37] op_sel_hi:[1,0,1] neg_lo:[0,1,0] neg_hi:[0,1,0]
	s_waitcnt lgkmcnt(0)
	v_pk_add_f32 v[36:37], v[88:89], v[108:109] neg_lo:[0,1] neg_hi:[0,1]
	v_pk_add_f32 v[32:33], v[88:89], v[108:109]
	v_pk_mul_f32 v[88:89], v[36:37], v[34:35] op_sel:[1,0] op_sel_hi:[0,0] neg_lo:[1,1] neg_hi:[0,1]
	s_nop 0
	v_pk_fma_f32 v[88:89], v[36:37], v[30:31], v[88:89] op_sel_hi:[1,0,1] neg_lo:[0,1,0] neg_hi:[0,1,0]
	v_pk_add_f32 v[36:37], v[90:91], v[110:111]
	v_pk_add_f32 v[90:91], v[90:91], v[110:111] neg_lo:[0,1] neg_hi:[0,1]
	s_nop 0
	v_pk_mul_f32 v[44:45], v[90:91], v[44:45] op_sel:[1,0] op_sel_hi:[0,0] neg_lo:[1,1] neg_hi:[0,1]
	s_nop 0
	v_pk_fma_f32 v[90:91], v[90:91], v[28:29], v[44:45] op_sel_hi:[1,0,1] neg_lo:[0,1,0] neg_hi:[0,1,0]
	v_pk_add_f32 v[44:45], v[16:17], v[76:77]
	v_pk_add_f32 v[16:17], v[16:17], v[76:77] neg_lo:[0,1] neg_hi:[0,1]
	v_pk_add_f32 v[28:29], v[112:113], v[48:49]
	v_pk_mul_f32 v[76:77], v[16:17], v[34:35] op_sel:[1,0] op_sel_hi:[0,0] neg_lo:[1,1] neg_hi:[0,1]
	v_pk_add_f32 v[48:49], v[112:113], v[48:49] neg_lo:[0,1] neg_hi:[0,1]
	v_pk_fma_f32 v[76:77], v[16:17], v[30:31], v[76:77] op_sel_hi:[1,0,1]
	v_pk_add_f32 v[16:17], v[18:19], v[94:95]
	v_pk_add_f32 v[18:19], v[18:19], v[94:95] neg_lo:[0,1] neg_hi:[0,1]
	s_nop 0
	v_pk_mul_f32 v[94:95], v[18:19], v[10:11] op_sel:[1,0] op_sel_hi:[0,0] neg_lo:[1,1] neg_hi:[0,1]
	s_nop 0
	v_pk_fma_f32 v[18:19], v[18:19], v[10:11], v[94:95] op_sel_hi:[1,0,1]
	v_pk_add_f32 v[94:95], v[20:21], v[96:97]
	v_pk_add_f32 v[20:21], v[20:21], v[96:97] neg_lo:[0,1] neg_hi:[0,1]
	s_nop 0
	v_pk_mul_f32 v[96:97], v[20:21], v[34:35] op_sel_hi:[1,0]
	v_xor_b32_e32 v102, 0x80000000, v21
	v_mov_b32_e32 v103, v20
	v_pk_add_f32 v[20:21], v[22:23], v[98:99]
	v_pk_add_f32 v[22:23], v[22:23], v[98:99] neg_lo:[0,1] neg_hi:[0,1]
	v_pk_fma_f32 v[96:97], v[102:103], v[30:31], v[96:97] op_sel_hi:[1,0,1] neg_lo:[0,1,0] neg_hi:[0,1,0]
	v_xor_b32_e32 v99, 0x80000000, v22
	v_mov_b32_e32 v98, v23
	v_pk_add_f32 v[22:23], v[24:25], v[100:101]
	v_pk_add_f32 v[24:25], v[24:25], v[100:101] neg_lo:[0,1] neg_hi:[0,1]
	s_nop 0
	v_pk_mul_f32 v[100:101], v[24:25], v[34:35] op_sel_hi:[1,0] neg_lo:[0,1] neg_hi:[0,1]
	v_xor_b32_e32 v102, 0x80000000, v25
	v_mov_b32_e32 v103, v24
	v_pk_add_f32 v[24:25], v[26:27], v[32:33]
	v_pk_add_f32 v[26:27], v[26:27], v[32:33] neg_lo:[0,1] neg_hi:[0,1]
	v_pk_fma_f32 v[100:101], v[102:103], v[30:31], v[100:101] op_sel_hi:[1,0,1] neg_lo:[0,1,0] neg_hi:[0,1,0]
	v_pk_mul_f32 v[32:33], v[26:27], v[10:11] op_sel:[1,0] op_sel_hi:[0,0] neg_lo:[1,1] neg_hi:[0,1]
	v_pk_add_f32 v[102:103], v[28:29], v[20:21] neg_lo:[0,1] neg_hi:[0,1]
	v_pk_fma_f32 v[26:27], v[26:27], v[10:11], v[32:33] op_sel_hi:[1,0,1] neg_lo:[0,1,0] neg_hi:[0,1,0]
	v_pk_add_f32 v[32:33], v[40:41], v[36:37]
	v_pk_add_f32 v[36:37], v[40:41], v[36:37] neg_lo:[0,1] neg_hi:[0,1]
	s_nop 0
	v_pk_mul_f32 v[40:41], v[36:37], v[34:35] op_sel:[1,0] op_sel_hi:[0,0] neg_lo:[1,1] neg_hi:[0,1]
	s_nop 0
	v_pk_fma_f32 v[40:41], v[36:37], v[30:31], v[40:41] op_sel_hi:[1,0,1] neg_lo:[0,1,0] neg_hi:[0,1,0]
	v_pk_add_f32 v[36:37], v[28:29], v[20:21]
	v_pk_add_f32 v[20:21], v[44:45], v[22:23]
	v_pk_add_f32 v[22:23], v[44:45], v[22:23] neg_lo:[0,1] neg_hi:[0,1]
	s_nop 0
	v_pk_mul_f32 v[28:29], v[22:23], v[10:11] op_sel:[1,0] op_sel_hi:[0,0] neg_lo:[1,1] neg_hi:[0,1]
	s_nop 0
	v_pk_fma_f32 v[22:23], v[22:23], v[10:11], v[28:29] op_sel_hi:[1,0,1]
	v_pk_add_f32 v[28:29], v[16:17], v[24:25]
	v_pk_add_f32 v[16:17], v[16:17], v[24:25] neg_lo:[0,1] neg_hi:[0,1]
	s_nop 0
	v_xor_b32_e32 v25, 0x80000000, v16
	v_mov_b32_e32 v24, v17
	v_pk_add_f32 v[16:17], v[94:95], v[32:33]
	v_pk_add_f32 v[32:33], v[94:95], v[32:33] neg_lo:[0,1] neg_hi:[0,1]
	s_nop 0
	v_pk_mul_f32 v[44:45], v[32:33], v[10:11] op_sel:[1,0] op_sel_hi:[0,0] neg_lo:[1,1] neg_hi:[0,1]
	s_nop 0
	v_pk_fma_f32 v[32:33], v[32:33], v[10:11], v[44:45] op_sel_hi:[1,0,1] neg_lo:[0,1,0] neg_hi:[0,1,0]
	v_pk_add_f32 v[44:45], v[36:37], v[28:29]
	v_pk_add_f32 v[36:37], v[36:37], v[28:29] neg_lo:[0,1] neg_hi:[0,1]
	v_pk_add_f32 v[28:29], v[20:21], v[16:17]
	v_pk_add_f32 v[16:17], v[20:21], v[16:17] neg_lo:[0,1] neg_hi:[0,1]
	v_pk_add_f32 v[94:95], v[44:45], v[28:29]
	v_xor_b32_e32 v21, 0x80000000, v16
	v_mov_b32_e32 v20, v17
	v_pk_add_f32 v[16:17], v[102:103], v[24:25]
	v_pk_add_f32 v[102:103], v[102:103], v[24:25] neg_lo:[0,1] neg_hi:[0,1]
	v_pk_add_f32 v[24:25], v[22:23], v[32:33]
	v_pk_add_f32 v[22:23], v[22:23], v[32:33] neg_lo:[0,1] neg_hi:[0,1]
	v_pk_add_f32 v[28:29], v[44:45], v[28:29] neg_lo:[0,1] neg_hi:[0,1]
	v_xor_b32_e32 v33, 0x80000000, v22
	v_mov_b32_e32 v32, v23
	v_pk_add_f32 v[22:23], v[48:49], v[98:99]
	v_pk_add_f32 v[98:99], v[48:49], v[98:99] neg_lo:[0,1] neg_hi:[0,1]
	v_pk_add_f32 v[48:49], v[76:77], v[100:101] neg_lo:[0,1] neg_hi:[0,1]
	v_pk_add_f32 v[44:45], v[36:37], v[20:21]
	v_pk_add_f32 v[20:21], v[36:37], v[20:21] neg_lo:[0,1] neg_hi:[0,1]
	v_pk_add_f32 v[104:105], v[16:17], v[24:25]
	v_pk_add_f32 v[24:25], v[16:17], v[24:25] neg_lo:[0,1] neg_hi:[0,1]
	v_pk_add_f32 v[36:37], v[102:103], v[32:33]
	v_pk_add_f32 v[16:17], v[102:103], v[32:33] neg_lo:[0,1] neg_hi:[0,1]
	v_pk_add_f32 v[32:33], v[76:77], v[100:101]
	v_pk_mul_f32 v[76:77], v[10:11], v[48:49] op_sel:[0,1] op_sel_hi:[0,0] neg_lo:[1,1] neg_hi:[1,0]
	v_pk_fma_f32 v[76:77], v[10:11], v[48:49], v[76:77] op_sel_hi:[0,1,1]
	v_pk_add_f32 v[48:49], v[18:19], v[26:27]
	v_pk_add_f32 v[18:19], v[18:19], v[26:27] neg_lo:[0,1] neg_hi:[0,1]
	s_nop 0
	v_xor_b32_e32 v27, 0x80000000, v18
	v_mov_b32_e32 v26, v19
	v_pk_add_f32 v[18:19], v[96:97], v[40:41]
	v_pk_add_f32 v[40:41], v[96:97], v[40:41] neg_lo:[0,1] neg_hi:[0,1]
	s_nop 0
	v_pk_mul_f32 v[96:97], v[10:11], v[40:41] op_sel:[0,1] op_sel_hi:[0,0] neg_lo:[1,1] neg_hi:[1,0]
	v_pk_fma_f32 v[40:41], v[10:11], v[40:41], v[96:97] op_sel_hi:[0,1,1] neg_lo:[1,0,0] neg_hi:[1,0,0]
	v_pk_add_f32 v[96:97], v[22:23], v[48:49]
	v_pk_add_f32 v[22:23], v[22:23], v[48:49] neg_lo:[0,1] neg_hi:[0,1]
	v_pk_add_f32 v[48:49], v[32:33], v[18:19]
	v_pk_add_f32 v[18:19], v[32:33], v[18:19] neg_lo:[0,1] neg_hi:[0,1]
	v_pk_add_f32 v[102:103], v[96:97], v[48:49]
	v_xor_b32_e32 v101, 0x80000000, v18
	v_mov_b32_e32 v100, v19
	v_pk_add_f32 v[32:33], v[96:97], v[48:49] neg_lo:[0,1] neg_hi:[0,1]
	v_pk_add_f32 v[18:19], v[98:99], v[26:27]
	v_pk_add_f32 v[96:97], v[98:99], v[26:27] neg_lo:[0,1] neg_hi:[0,1]
	v_pk_add_f32 v[26:27], v[76:77], v[40:41]
	v_pk_add_f32 v[40:41], v[76:77], v[40:41] neg_lo:[0,1] neg_hi:[0,1]
	v_pk_add_f32 v[98:99], v[18:19], v[26:27]
	v_xor_b32_e32 v77, 0x80000000, v40
	v_mov_b32_e32 v76, v41
	v_pk_add_f32 v[26:27], v[18:19], v[26:27] neg_lo:[0,1] neg_hi:[0,1]
	v_pk_add_f32 v[40:41], v[96:97], v[76:77]
	v_pk_add_f32 v[18:19], v[96:97], v[76:77] neg_lo:[0,1] neg_hi:[0,1]
	v_pk_add_f32 v[76:77], v[38:39], v[92:93]
	v_pk_add_f32 v[92:93], v[38:39], v[92:93] neg_lo:[0,1] neg_hi:[0,1]
	v_pk_add_f32 v[38:39], v[42:43], v[78:79]
	v_pk_add_f32 v[42:43], v[42:43], v[78:79] neg_lo:[0,1] neg_hi:[0,1]
	v_pk_add_f32 v[48:49], v[22:23], v[100:101]
	v_pk_mul_f32 v[78:79], v[34:35], v[42:43] op_sel:[0,1] op_sel_hi:[0,0] neg_lo:[1,1] neg_hi:[1,0]
	v_pk_fma_f32 v[42:43], v[30:31], v[42:43], v[78:79] op_sel_hi:[0,1,1]
	v_pk_add_f32 v[78:79], v[46:47], v[80:81]
	v_pk_add_f32 v[46:47], v[46:47], v[80:81] neg_lo:[0,1] neg_hi:[0,1]
	v_pk_add_f32 v[22:23], v[22:23], v[100:101] neg_lo:[0,1] neg_hi:[0,1]
	v_pk_mul_f32 v[80:81], v[10:11], v[46:47] op_sel:[0,1] op_sel_hi:[0,0] neg_lo:[1,1] neg_hi:[1,0]
	v_pk_fma_f32 v[80:81], v[10:11], v[46:47], v[80:81] op_sel_hi:[0,1,1]
	v_pk_add_f32 v[46:47], v[50:51], v[82:83]
	v_pk_add_f32 v[50:51], v[50:51], v[82:83] neg_lo:[0,1] neg_hi:[0,1]
	s_nop 0
	v_pk_mul_f32 v[82:83], v[30:31], v[50:51] op_sel:[0,1] op_sel_hi:[0,0] neg_lo:[1,1] neg_hi:[1,0]
	v_pk_fma_f32 v[50:51], v[34:35], v[50:51], v[82:83] op_sel_hi:[0,1,1]
	v_pk_add_f32 v[82:83], v[52:53], v[84:85]
	v_pk_add_f32 v[52:53], v[52:53], v[84:85] neg_lo:[0,1] neg_hi:[0,1]
	s_nop 0
	v_xor_b32_e32 v85, 0x80000000, v52
	v_mov_b32_e32 v84, v53
	v_pk_add_f32 v[52:53], v[54:55], v[86:87]
	v_pk_add_f32 v[54:55], v[54:55], v[86:87] neg_lo:[0,1] neg_hi:[0,1]
	s_nop 0
	v_pk_mul_f32 v[86:87], v[30:31], v[54:55] op_sel:[0,1] op_sel_hi:[0,0] neg_lo:[1,1] neg_hi:[1,0]
	v_pk_fma_f32 v[54:55], v[34:35], v[54:55], v[86:87] op_sel_hi:[0,1,1] neg_lo:[1,0,0] neg_hi:[1,0,0]
	v_pk_add_f32 v[86:87], v[56:57], v[88:89]
	v_pk_add_f32 v[56:57], v[56:57], v[88:89] neg_lo:[0,1] neg_hi:[0,1]
	s_nop 0
	v_pk_mul_f32 v[88:89], v[10:11], v[56:57] op_sel:[0,1] op_sel_hi:[0,0] neg_lo:[1,1] neg_hi:[1,0]
	v_pk_fma_f32 v[56:57], v[10:11], v[56:57], v[88:89] op_sel_hi:[0,1,1] neg_lo:[1,0,0] neg_hi:[1,0,0]
	v_pk_add_f32 v[88:89], v[58:59], v[90:91]
	v_pk_add_f32 v[58:59], v[58:59], v[90:91] neg_lo:[0,1] neg_hi:[0,1]
	s_nop 0
	v_pk_mul_f32 v[34:35], v[34:35], v[58:59] op_sel:[0,1] op_sel_hi:[0,0] neg_lo:[1,1] neg_hi:[1,0]
	v_pk_fma_f32 v[34:35], v[30:31], v[58:59], v[34:35] op_sel_hi:[0,1,1] neg_lo:[1,0,0] neg_hi:[1,0,0]
	v_pk_add_f32 v[30:31], v[76:77], v[82:83]
	v_pk_add_f32 v[58:59], v[76:77], v[82:83] neg_lo:[0,1] neg_hi:[0,1]
	v_pk_add_f32 v[76:77], v[52:53], v[38:39]
	v_pk_add_f32 v[38:39], v[38:39], v[52:53] neg_lo:[0,1] neg_hi:[0,1]
	s_nop 0
	v_pk_mul_f32 v[52:53], v[10:11], v[38:39] op_sel:[0,1] op_sel_hi:[0,0] neg_lo:[1,1] neg_hi:[1,0]
	v_pk_fma_f32 v[52:53], v[10:11], v[38:39], v[52:53] op_sel_hi:[0,1,1]
	v_pk_add_f32 v[38:39], v[78:79], v[86:87]
	v_pk_add_f32 v[78:79], v[78:79], v[86:87] neg_lo:[0,1] neg_hi:[0,1]
	s_nop 0
	v_xor_b32_e32 v83, 0x80000000, v78
	v_mov_b32_e32 v82, v79
	v_pk_add_f32 v[78:79], v[46:47], v[88:89]
	v_pk_add_f32 v[46:47], v[46:47], v[88:89] neg_lo:[0,1] neg_hi:[0,1]
	v_pk_add_f32 v[88:89], v[76:77], v[78:79]
	v_pk_mul_f32 v[86:87], v[10:11], v[46:47] op_sel:[0,1] op_sel_hi:[0,0] neg_lo:[1,1] neg_hi:[1,0]
	v_pk_fma_f32 v[46:47], v[10:11], v[46:47], v[86:87] op_sel_hi:[0,1,1] neg_lo:[1,0,0] neg_hi:[1,0,0]
	v_pk_add_f32 v[86:87], v[30:31], v[38:39]
	v_pk_add_f32 v[30:31], v[30:31], v[38:39] neg_lo:[0,1] neg_hi:[0,1]
	v_pk_add_f32 v[38:39], v[76:77], v[78:79] neg_lo:[0,1] neg_hi:[0,1]
	v_pk_add_f32 v[78:79], v[86:87], v[88:89] neg_lo:[0,1] neg_hi:[0,1]
	v_pk_add_f32 v[90:91], v[30:31], v[38:39] op_sel:[0,1] op_sel_hi:[1,0] neg_hi:[0,1]
	v_pk_add_f32 v[38:39], v[30:31], v[38:39] op_sel:[0,1] op_sel_hi:[1,0] neg_lo:[0,1]
	v_pk_add_f32 v[76:77], v[52:53], v[46:47]
	v_pk_add_f32 v[46:47], v[52:53], v[46:47] neg_lo:[0,1] neg_hi:[0,1]
	v_pk_add_f32 v[30:31], v[58:59], v[82:83]
	v_pk_add_f32 v[58:59], v[58:59], v[82:83] neg_lo:[0,1] neg_hi:[0,1]
	v_xor_b32_e32 v53, 0x80000000, v46
	v_mov_b32_e32 v52, v47
	v_pk_add_f32 v[82:83], v[30:31], v[76:77]
	v_pk_add_f32 v[46:47], v[30:31], v[76:77] neg_lo:[0,1] neg_hi:[0,1]
	v_pk_add_f32 v[76:77], v[58:59], v[52:53]
	v_pk_add_f32 v[30:31], v[58:59], v[52:53] neg_lo:[0,1] neg_hi:[0,1]
	v_pk_add_f32 v[52:53], v[92:93], v[84:85]
	v_pk_add_f32 v[58:59], v[92:93], v[84:85] neg_lo:[0,1] neg_hi:[0,1]
	v_pk_add_f32 v[84:85], v[54:55], v[42:43]
	v_pk_add_f32 v[42:43], v[42:43], v[54:55] neg_lo:[0,1] neg_hi:[0,1]
	v_pk_add_f32 v[86:87], v[86:87], v[88:89]
	v_pk_mul_f32 v[54:55], v[10:11], v[42:43] op_sel:[0,1] op_sel_hi:[0,0] neg_lo:[1,1] neg_hi:[1,0]
	v_pk_fma_f32 v[54:55], v[10:11], v[42:43], v[54:55] op_sel_hi:[0,1,1]
	v_pk_add_f32 v[42:43], v[80:81], v[56:57]
	v_pk_add_f32 v[56:57], v[80:81], v[56:57] neg_lo:[0,1] neg_hi:[0,1]
	s_nop 0
	v_xor_b32_e32 v81, 0x80000000, v56
	v_mov_b32_e32 v80, v57
	v_pk_add_f32 v[56:57], v[50:51], v[34:35]
	v_pk_add_f32 v[34:35], v[50:51], v[34:35] neg_lo:[0,1] neg_hi:[0,1]
	s_nop 0
	v_pk_mul_f32 v[50:51], v[10:11], v[34:35] op_sel:[0,1] op_sel_hi:[0,0] neg_lo:[1,1] neg_hi:[1,0]
	v_pk_fma_f32 v[34:35], v[10:11], v[34:35], v[50:51] op_sel_hi:[0,1,1] neg_lo:[1,0,0] neg_hi:[1,0,0]
	v_pk_add_f32 v[50:51], v[52:53], v[42:43]
	v_pk_add_f32 v[42:43], v[52:53], v[42:43] neg_lo:[0,1] neg_hi:[0,1]
	v_pk_add_f32 v[52:53], v[84:85], v[56:57]
	v_pk_add_f32 v[56:57], v[84:85], v[56:57] neg_lo:[0,1] neg_hi:[0,1]
	s_nop 0
	v_xor_b32_e32 v85, 0x80000000, v56
	v_mov_b32_e32 v84, v57
	v_pk_add_f32 v[56:57], v[50:51], v[52:53]
	v_pk_add_f32 v[50:51], v[50:51], v[52:53] neg_lo:[0,1] neg_hi:[0,1]
	v_pk_add_f32 v[52:53], v[42:43], v[84:85]
	v_pk_add_f32 v[42:43], v[42:43], v[84:85] neg_lo:[0,1] neg_hi:[0,1]
	v_pk_add_f32 v[84:85], v[58:59], v[80:81]
	v_pk_add_f32 v[58:59], v[58:59], v[80:81] neg_lo:[0,1] neg_hi:[0,1]
	v_pk_add_f32 v[80:81], v[54:55], v[34:35]
	v_pk_add_f32 v[34:35], v[54:55], v[34:35] neg_lo:[0,1] neg_hi:[0,1]
	v_pk_add_f32 v[92:93], v[84:85], v[80:81]
	v_pk_add_f32 v[80:81], v[84:85], v[80:81] neg_lo:[0,1] neg_hi:[0,1]
	v_pk_add_f32 v[84:85], v[58:59], v[34:35] op_sel:[0,1] op_sel_hi:[1,0] neg_hi:[0,1]
	v_pk_add_f32 v[34:35], v[58:59], v[34:35] op_sel:[0,1] op_sel_hi:[1,0] neg_lo:[0,1]
	v_pk_fma_f32 v[58:59], v[14:15], s[90:91], v[14:15] op_sel:[1,0,0] op_sel_hi:[0,1,1]
	v_pk_mul_f32 v[54:55], v[94:95], s[14:15] op_sel:[1,0] neg_lo:[1,0]
	v_pk_mul_f32 v[88:89], v[58:59], v[86:87] op_sel:[1,1] op_sel_hi:[0,1] neg_lo:[0,1]
	v_pk_fma_f32 v[54:55], v[94:95], s[94:95], v[54:55] op_sel_hi:[0,1,1]
	v_pk_fma_f32 v[86:87], v[58:59], v[86:87], v[88:89] op_sel_hi:[1,0,1]
	ds_write2_b64 v74, v[54:55], v[86:87] offset1:16
	v_pk_mul_f32 v[54:55], v[14:15], v[58:59] op_sel:[1,1] op_sel_hi:[0,1] neg_lo:[0,1]
	v_pk_fma_f32 v[54:55], v[14:15], v[58:59], v[54:55] op_sel_hi:[1,0,1]
	s_nop 0
	v_pk_mul_f32 v[58:59], v[54:55], v[102:103] op_sel:[1,1] op_sel_hi:[0,1] neg_lo:[0,1]
	v_pk_mul_f32 v[74:75], v[14:15], v[54:55] op_sel:[1,1] op_sel_hi:[0,1] neg_lo:[0,1]
	v_pk_fma_f32 v[58:59], v[54:55], v[102:103], v[58:59] op_sel_hi:[1,0,1]
	v_pk_fma_f32 v[54:55], v[14:15], v[54:55], v[74:75] op_sel_hi:[1,0,1]
	s_nop 0
	v_pk_mul_f32 v[74:75], v[54:55], v[56:57] op_sel:[1,1] op_sel_hi:[0,1] neg_lo:[0,1]
	v_pk_fma_f32 v[56:57], v[54:55], v[56:57], v[74:75] op_sel_hi:[1,0,1]
	ds_write2_b64 v73, v[58:59], v[56:57] offset0:32 offset1:48
	v_pk_mul_f32 v[56:57], v[14:15], v[54:55] op_sel:[1,1] op_sel_hi:[0,1] neg_lo:[0,1]
	v_pk_fma_f32 v[54:55], v[14:15], v[54:55], v[56:57] op_sel_hi:[1,0,1]
	s_nop 0
	v_pk_mul_f32 v[56:57], v[54:55], v[104:105] op_sel:[1,1] op_sel_hi:[0,1] neg_lo:[0,1]
	v_pk_mul_f32 v[58:59], v[14:15], v[54:55] op_sel:[1,1] op_sel_hi:[0,1] neg_lo:[0,1]
	v_pk_fma_f32 v[56:57], v[54:55], v[104:105], v[56:57] op_sel_hi:[1,0,1]
	v_pk_fma_f32 v[54:55], v[14:15], v[54:55], v[58:59] op_sel_hi:[1,0,1]
	s_nop 0
	v_pk_mul_f32 v[58:59], v[54:55], v[82:83] op_sel:[1,1] op_sel_hi:[0,1] neg_lo:[0,1]
	v_pk_fma_f32 v[58:59], v[54:55], v[82:83], v[58:59] op_sel_hi:[1,0,1]
	ds_write2_b64 v72, v[56:57], v[58:59] offset0:64 offset1:80
	v_pk_mul_f32 v[56:57], v[14:15], v[54:55] op_sel:[1,1] op_sel_hi:[0,1] neg_lo:[0,1]
	v_pk_fma_f32 v[54:55], v[14:15], v[54:55], v[56:57] op_sel_hi:[1,0,1]
	s_nop 0
	v_pk_mul_f32 v[56:57], v[54:55], v[98:99] op_sel:[1,1] op_sel_hi:[0,1] neg_lo:[0,1]
	v_pk_mul_f32 v[58:59], v[14:15], v[54:55] op_sel:[1,1] op_sel_hi:[0,1] neg_lo:[0,1]
	v_pk_fma_f32 v[56:57], v[54:55], v[98:99], v[56:57] op_sel_hi:[1,0,1]
	v_pk_fma_f32 v[54:55], v[14:15], v[54:55], v[58:59] op_sel_hi:[1,0,1]
	s_nop 0
	v_pk_mul_f32 v[58:59], v[54:55], v[92:93] op_sel:[1,1] op_sel_hi:[0,1] neg_lo:[0,1]
	v_pk_fma_f32 v[58:59], v[54:55], v[92:93], v[58:59] op_sel_hi:[1,0,1]
	ds_write2_b64 v71, v[56:57], v[58:59] offset0:96 offset1:112
	v_pk_mul_f32 v[56:57], v[14:15], v[54:55] op_sel:[1,1] op_sel_hi:[0,1] neg_lo:[0,1]
	v_pk_fma_f32 v[54:55], v[14:15], v[54:55], v[56:57] op_sel_hi:[1,0,1]
	s_nop 0
	v_pk_mul_f32 v[56:57], v[54:55], v[44:45] op_sel:[1,1] op_sel_hi:[0,1] neg_lo:[0,1]
	v_pk_fma_f32 v[44:45], v[54:55], v[44:45], v[56:57] op_sel_hi:[1,0,1]
	v_pk_mul_f32 v[56:57], v[14:15], v[54:55] op_sel:[1,1] op_sel_hi:[0,1] neg_lo:[0,1]
	v_pk_fma_f32 v[54:55], v[14:15], v[54:55], v[56:57] op_sel_hi:[1,0,1]
	s_nop 0
	v_pk_mul_f32 v[56:57], v[54:55], v[90:91] op_sel:[1,1] op_sel_hi:[0,1] neg_lo:[0,1]
	v_pk_fma_f32 v[56:57], v[54:55], v[90:91], v[56:57] op_sel_hi:[1,0,1]
	ds_write2_b64 v70, v[44:45], v[56:57] offset0:128 offset1:144
	v_pk_mul_f32 v[44:45], v[14:15], v[54:55] op_sel:[1,1] op_sel_hi:[0,1] neg_lo:[0,1]
	v_pk_fma_f32 v[44:45], v[14:15], v[54:55], v[44:45] op_sel_hi:[1,0,1]
	s_nop 0
	v_pk_mul_f32 v[54:55], v[44:45], v[48:49] op_sel:[1,1] op_sel_hi:[0,1] neg_lo:[0,1]
	v_pk_fma_f32 v[48:49], v[44:45], v[48:49], v[54:55] op_sel_hi:[1,0,1]
	v_pk_mul_f32 v[54:55], v[14:15], v[44:45] op_sel:[1,1] op_sel_hi:[0,1] neg_lo:[0,1]
	v_pk_fma_f32 v[44:45], v[14:15], v[44:45], v[54:55] op_sel_hi:[1,0,1]
	s_nop 0
	v_pk_mul_f32 v[54:55], v[44:45], v[52:53] op_sel:[1,1] op_sel_hi:[0,1] neg_lo:[0,1]
	v_pk_fma_f32 v[52:53], v[44:45], v[52:53], v[54:55] op_sel_hi:[1,0,1]
	ds_write2_b64 v69, v[48:49], v[52:53] offset0:160 offset1:176
	v_pk_mul_f32 v[48:49], v[14:15], v[44:45] op_sel:[1,1] op_sel_hi:[0,1] neg_lo:[0,1]
	v_pk_fma_f32 v[44:45], v[14:15], v[44:45], v[48:49] op_sel_hi:[1,0,1]
	s_nop 0
	v_pk_mul_f32 v[48:49], v[36:37], v[44:45] op_sel:[1,1] op_sel_hi:[1,0] neg_lo:[1,0]
	s_nop 0
	v_pk_fma_f32 v[36:37], v[36:37], v[44:45], v[48:49] op_sel_hi:[0,1,1]
	v_pk_mul_f32 v[48:49], v[14:15], v[44:45] op_sel:[1,1] op_sel_hi:[0,1] neg_lo:[0,1]
	v_pk_fma_f32 v[44:45], v[14:15], v[44:45], v[48:49] op_sel_hi:[1,0,1]
	s_nop 0
	v_pk_mul_f32 v[48:49], v[44:45], v[76:77] op_sel:[1,1] op_sel_hi:[0,1] neg_lo:[0,1]
	v_pk_fma_f32 v[48:49], v[44:45], v[76:77], v[48:49] op_sel_hi:[1,0,1]
	ds_write2_b64 v68, v[36:37], v[48:49] offset0:192 offset1:208
	v_pk_mul_f32 v[36:37], v[14:15], v[44:45] op_sel:[1,1] op_sel_hi:[0,1] neg_lo:[0,1]
	v_pk_fma_f32 v[36:37], v[14:15], v[44:45], v[36:37] op_sel_hi:[1,0,1]
	s_nop 0
	v_pk_mul_f32 v[44:45], v[40:41], v[36:37] op_sel:[1,1] op_sel_hi:[1,0] neg_lo:[1,0]
	s_nop 0
	v_pk_fma_f32 v[40:41], v[40:41], v[36:37], v[44:45] op_sel_hi:[0,1,1]
	v_pk_mul_f32 v[44:45], v[14:15], v[36:37] op_sel:[1,1] op_sel_hi:[0,1] neg_lo:[0,1]
	v_pk_fma_f32 v[36:37], v[14:15], v[36:37], v[44:45] op_sel_hi:[1,0,1]
	s_nop 0
	v_pk_mul_f32 v[44:45], v[36:37], v[84:85] op_sel:[1,1] op_sel_hi:[0,1] neg_lo:[0,1]
	v_pk_fma_f32 v[44:45], v[36:37], v[84:85], v[44:45] op_sel_hi:[1,0,1]
	ds_write2_b64 v67, v[40:41], v[44:45] offset0:224 offset1:240
	v_pk_mul_f32 v[40:41], v[14:15], v[36:37] op_sel:[1,1] op_sel_hi:[0,1] neg_lo:[0,1]
	v_pk_fma_f32 v[36:37], v[14:15], v[36:37], v[40:41] op_sel_hi:[1,0,1]
	s_nop 0
	v_pk_mul_f32 v[40:41], v[28:29], v[36:37] op_sel:[1,1] op_sel_hi:[1,0] neg_lo:[1,0]
	s_nop 0
	v_pk_fma_f32 v[28:29], v[28:29], v[36:37], v[40:41] op_sel_hi:[0,1,1]
	v_pk_mul_f32 v[40:41], v[14:15], v[36:37] op_sel:[1,1] op_sel_hi:[0,1] neg_lo:[0,1]
	v_pk_fma_f32 v[36:37], v[14:15], v[36:37], v[40:41] op_sel_hi:[1,0,1]
	s_nop 0
	v_pk_mul_f32 v[40:41], v[78:79], v[36:37] op_sel:[1,1] op_sel_hi:[1,0] neg_lo:[1,0]
	s_nop 0
	v_pk_fma_f32 v[40:41], v[78:79], v[36:37], v[40:41] op_sel_hi:[0,1,1]
	ds_write2_b64 v66, v[28:29], v[40:41] offset1:16
	v_pk_mul_f32 v[28:29], v[14:15], v[36:37] op_sel:[1,1] op_sel_hi:[0,1] neg_lo:[0,1]
	v_pk_fma_f32 v[28:29], v[14:15], v[36:37], v[28:29] op_sel_hi:[1,0,1]
	s_nop 0
	v_pk_mul_f32 v[36:37], v[32:33], v[28:29] op_sel:[1,1] op_sel_hi:[1,0] neg_lo:[1,0]
	s_nop 0
	v_pk_fma_f32 v[32:33], v[32:33], v[28:29], v[36:37] op_sel_hi:[0,1,1]
	v_pk_mul_f32 v[36:37], v[14:15], v[28:29] op_sel:[1,1] op_sel_hi:[0,1] neg_lo:[0,1]
	v_pk_fma_f32 v[28:29], v[14:15], v[28:29], v[36:37] op_sel_hi:[1,0,1]
	s_nop 0
	v_pk_mul_f32 v[36:37], v[50:51], v[28:29] op_sel:[1,1] op_sel_hi:[1,0] neg_lo:[1,0]
	s_nop 0
	v_pk_fma_f32 v[36:37], v[50:51], v[28:29], v[36:37] op_sel_hi:[0,1,1]
	ds_write2_b64 v65, v[32:33], v[36:37] offset0:32 offset1:48
	v_pk_mul_f32 v[32:33], v[14:15], v[28:29] op_sel:[1,1] op_sel_hi:[0,1] neg_lo:[0,1]
	v_pk_fma_f32 v[28:29], v[14:15], v[28:29], v[32:33] op_sel_hi:[1,0,1]
	s_nop 0
	v_pk_mul_f32 v[32:33], v[24:25], v[28:29] op_sel:[1,1] op_sel_hi:[1,0] neg_lo:[1,0]
	s_nop 0
	v_pk_fma_f32 v[24:25], v[24:25], v[28:29], v[32:33] op_sel_hi:[0,1,1]
	v_pk_mul_f32 v[32:33], v[14:15], v[28:29] op_sel:[1,1] op_sel_hi:[0,1] neg_lo:[0,1]
	v_pk_fma_f32 v[28:29], v[14:15], v[28:29], v[32:33] op_sel_hi:[1,0,1]
	s_nop 0
	v_pk_mul_f32 v[32:33], v[46:47], v[28:29] op_sel:[1,1] op_sel_hi:[1,0] neg_lo:[1,0]
	s_nop 0
	v_pk_fma_f32 v[32:33], v[46:47], v[28:29], v[32:33] op_sel_hi:[0,1,1]
	ds_write2_b64 v64, v[24:25], v[32:33] offset0:64 offset1:80
	v_pk_mul_f32 v[24:25], v[14:15], v[28:29] op_sel:[1,1] op_sel_hi:[0,1] neg_lo:[0,1]
	v_pk_fma_f32 v[24:25], v[14:15], v[28:29], v[24:25] op_sel_hi:[1,0,1]
	s_nop 0
	v_pk_mul_f32 v[28:29], v[26:27], v[24:25] op_sel:[1,1] op_sel_hi:[1,0] neg_lo:[1,0]
	s_nop 0
	v_pk_fma_f32 v[26:27], v[26:27], v[24:25], v[28:29] op_sel_hi:[0,1,1]
	v_pk_mul_f32 v[28:29], v[14:15], v[24:25] op_sel:[1,1] op_sel_hi:[0,1] neg_lo:[0,1]
	v_pk_fma_f32 v[24:25], v[14:15], v[24:25], v[28:29] op_sel_hi:[1,0,1]
	s_nop 0
	v_pk_mul_f32 v[28:29], v[80:81], v[24:25] op_sel:[1,1] op_sel_hi:[1,0] neg_lo:[1,0]
	s_nop 0
	v_pk_fma_f32 v[28:29], v[80:81], v[24:25], v[28:29] op_sel_hi:[0,1,1]
	ds_write2_b64 v63, v[26:27], v[28:29] offset0:96 offset1:112
	v_pk_mul_f32 v[26:27], v[14:15], v[24:25] op_sel:[1,1] op_sel_hi:[0,1] neg_lo:[0,1]
	v_pk_fma_f32 v[24:25], v[14:15], v[24:25], v[26:27] op_sel_hi:[1,0,1]
	s_nop 0
	v_pk_mul_f32 v[26:27], v[20:21], v[24:25] op_sel:[1,1] op_sel_hi:[1,0] neg_lo:[1,0]
	s_nop 0
	v_pk_fma_f32 v[20:21], v[20:21], v[24:25], v[26:27] op_sel_hi:[0,1,1]
	v_pk_mul_f32 v[26:27], v[14:15], v[24:25] op_sel:[1,1] op_sel_hi:[0,1] neg_lo:[0,1]
	v_pk_fma_f32 v[24:25], v[14:15], v[24:25], v[26:27] op_sel_hi:[1,0,1]
	s_nop 0
	v_pk_mul_f32 v[26:27], v[38:39], v[24:25] op_sel:[1,1] op_sel_hi:[1,0] neg_lo:[1,0]
	s_nop 0
	v_pk_fma_f32 v[26:27], v[38:39], v[24:25], v[26:27] op_sel_hi:[0,1,1]
	ds_write2_b64 v62, v[20:21], v[26:27] offset0:128 offset1:144
	v_pk_mul_f32 v[20:21], v[14:15], v[24:25] op_sel:[1,1] op_sel_hi:[0,1] neg_lo:[0,1]
	v_pk_fma_f32 v[20:21], v[14:15], v[24:25], v[20:21] op_sel_hi:[1,0,1]
	s_nop 0
	v_pk_mul_f32 v[24:25], v[22:23], v[20:21] op_sel:[1,1] op_sel_hi:[1,0] neg_lo:[1,0]
	s_nop 0
	v_pk_fma_f32 v[22:23], v[22:23], v[20:21], v[24:25] op_sel_hi:[0,1,1]
	v_pk_mul_f32 v[24:25], v[14:15], v[20:21] op_sel:[1,1] op_sel_hi:[0,1] neg_lo:[0,1]
	v_pk_fma_f32 v[20:21], v[14:15], v[20:21], v[24:25] op_sel_hi:[1,0,1]
	s_nop 0
	v_pk_mul_f32 v[24:25], v[42:43], v[20:21] op_sel:[1,1] op_sel_hi:[1,0] neg_lo:[1,0]
	s_nop 0
	v_pk_fma_f32 v[24:25], v[42:43], v[20:21], v[24:25] op_sel_hi:[0,1,1]
	ds_write2_b64 v61, v[22:23], v[24:25] offset0:160 offset1:176
	v_pk_mul_f32 v[22:23], v[14:15], v[20:21] op_sel:[1,1] op_sel_hi:[0,1] neg_lo:[0,1]
	v_pk_fma_f32 v[20:21], v[14:15], v[20:21], v[22:23] op_sel_hi:[1,0,1]
	s_nop 0
	v_pk_mul_f32 v[22:23], v[16:17], v[20:21] op_sel:[1,1] op_sel_hi:[1,0] neg_lo:[1,0]
	s_nop 0
	v_pk_fma_f32 v[16:17], v[16:17], v[20:21], v[22:23] op_sel_hi:[0,1,1]
	v_pk_mul_f32 v[22:23], v[14:15], v[20:21] op_sel:[1,1] op_sel_hi:[0,1] neg_lo:[0,1]
	v_pk_fma_f32 v[20:21], v[14:15], v[20:21], v[22:23] op_sel_hi:[1,0,1]
	s_nop 0
	v_pk_mul_f32 v[22:23], v[30:31], v[20:21] op_sel:[1,1] op_sel_hi:[1,0] neg_lo:[1,0]
	s_nop 0
	v_pk_fma_f32 v[22:23], v[30:31], v[20:21], v[22:23] op_sel_hi:[0,1,1]
	ds_write2_b64 v60, v[16:17], v[22:23] offset0:192 offset1:208
	v_pk_mul_f32 v[16:17], v[14:15], v[20:21] op_sel:[1,1] op_sel_hi:[0,1] neg_lo:[0,1]
	v_pk_fma_f32 v[16:17], v[14:15], v[20:21], v[16:17] op_sel_hi:[1,0,1]
	s_nop 0
	v_pk_mul_f32 v[20:21], v[18:19], v[16:17] op_sel:[1,1] op_sel_hi:[1,0] neg_lo:[1,0]
	s_nop 0
	v_pk_fma_f32 v[18:19], v[18:19], v[16:17], v[20:21] op_sel_hi:[0,1,1]
	v_pk_mul_f32 v[20:21], v[14:15], v[16:17] op_sel:[1,1] op_sel_hi:[0,1] neg_lo:[0,1]
	v_pk_fma_f32 v[14:15], v[14:15], v[16:17], v[20:21] op_sel_hi:[1,0,1]
	s_nop 0
	v_pk_mul_f32 v[16:17], v[34:35], v[14:15] op_sel:[1,1] op_sel_hi:[1,0] neg_lo:[1,0]
	s_nop 0
	v_pk_fma_f32 v[14:15], v[34:35], v[14:15], v[16:17] op_sel_hi:[0,1,1]
	ds_write2_b64 v13, v[18:19], v[14:15] offset0:224 offset1:240
	v_mov_b32_e32 v14, v182
	v_mov_b32_e32 v10, v176
	v_mov_b32_e32 v13, v175
	s_waitcnt lgkmcnt(0)
	s_barrier
	v_mov_b32_e32 v48, v167
	v_xor_b32_e32 v16, 1, v13
	v_lshlrev_b32_e32 v10, 3, v10
	v_lshlrev_b32_e32 v16, 3, v16
	v_add3_u32 v18, 0, v16, v10
	v_xor_b32_e32 v16, 2, v13
	v_lshlrev_b32_e32 v16, 3, v16
	v_xor_b32_e32 v24, 5, v13
	v_add3_u32 v20, 0, v16, v10
	v_xor_b32_e32 v16, 3, v13
	v_lshlrev_b32_e32 v24, 3, v24
	v_lshlrev_b32_e32 v15, 3, v13
	v_lshlrev_b32_e32 v16, 3, v16
	v_add3_u32 v26, 0, v24, v10
	v_xor_b32_e32 v24, 6, v13
	v_add3_u32 v15, 0, v15, v10
	v_add3_u32 v22, 0, v16, v10
	v_lshlrev_b32_e32 v24, 3, v24
	v_xor_b32_e32 v32, 9, v13
	ds_read_b64 v[16:17], v15
	ds_read_b64 v[18:19], v18
	ds_read_b64 v[20:21], v20
	ds_read_b64 v[22:23], v22
	v_xor_b32_e32 v15, 4, v13
	v_add3_u32 v28, 0, v24, v10
	v_xor_b32_e32 v24, 7, v13
	v_lshlrev_b32_e32 v32, 3, v32
	v_lshlrev_b32_e32 v15, 3, v15
	v_lshlrev_b32_e32 v24, 3, v24
	v_add3_u32 v34, 0, v32, v10
	v_xor_b32_e32 v32, 10, v13
	v_add3_u32 v15, 0, v15, v10
	v_add3_u32 v30, 0, v24, v10
	v_lshlrev_b32_e32 v32, 3, v32
	ds_read_b64 v[24:25], v15
	ds_read_b64 v[26:27], v26
	ds_read_b64 v[28:29], v28
	ds_read_b64 v[30:31], v30
	v_xor_b32_e32 v15, 8, v13
	v_add3_u32 v36, 0, v32, v10
	v_xor_b32_e32 v32, 11, v13
	v_lshlrev_b32_e32 v15, 3, v15
	v_lshlrev_b32_e32 v32, 3, v32
	v_xor_b32_e32 v40, 13, v13
	v_add3_u32 v15, 0, v15, v10
	v_add3_u32 v38, 0, v32, v10
	v_lshlrev_b32_e32 v40, 3, v40
	ds_read_b64 v[32:33], v15
	ds_read_b64 v[34:35], v34
	ds_read_b64 v[36:37], v36
	ds_read_b64 v[38:39], v38
	v_xor_b32_e32 v15, 12, v13
	v_add3_u32 v42, 0, v40, v10
	v_xor_b32_e32 v40, 14, v13
	v_xor_b32_e32 v13, 15, v13
	v_lshlrev_b32_e32 v15, 3, v15
	v_lshlrev_b32_e32 v40, 3, v40
	v_lshlrev_b32_e32 v13, 3, v13
	v_add3_u32 v15, 0, v15, v10
	v_add3_u32 v44, 0, v40, v10
	v_add3_u32 v10, 0, v13, v10
	ds_read_b64 v[40:41], v15
	ds_read_b64 v[42:43], v42
	ds_read_b64 v[44:45], v44
	ds_read_b64 v[46:47], v10
	v_mov_b32_e32 v10, v1
	v_mov_b32_e32 v13, v166
	v_mov_b32_e32 v10, v164
	s_waitcnt lgkmcnt(7)
	v_pk_add_f32 v[52:53], v[16:17], v[32:33]
	v_mov_b32_e32 v10, v165
	v_pk_add_f32 v[16:17], v[16:17], v[32:33] neg_lo:[0,1] neg_hi:[0,1]
	s_waitcnt lgkmcnt(6)
	v_pk_add_f32 v[32:33], v[18:19], v[34:35]
	v_pk_add_f32 v[18:19], v[18:19], v[34:35] neg_lo:[0,1] neg_hi:[0,1]
	v_mov_b32_e32 v13, v168
	v_mov_b32_e32 v50, v169
	v_ashrrev_i32_e32 v15, 31, v14
	v_pk_mul_f32 v[34:35], v[18:19], v[50:51] op_sel:[1,0] op_sel_hi:[0,0] neg_lo:[1,1] neg_hi:[0,1]
	v_mov_b32_e32 v13, v170
	v_pk_fma_f32 v[18:19], v[18:19], v[10:11], v[34:35] op_sel_hi:[1,0,1]
	s_waitcnt lgkmcnt(5)
	v_pk_add_f32 v[34:35], v[20:21], v[36:37]
	v_pk_add_f32 v[20:21], v[20:21], v[36:37] neg_lo:[0,1] neg_hi:[0,1]
	s_nop 0
	v_pk_mul_f32 v[36:37], v[20:21], v[48:49] op_sel:[1,0] op_sel_hi:[0,0] neg_lo:[1,1] neg_hi:[0,1]
	v_mov_b32_e32 v13, v171
	v_pk_fma_f32 v[20:21], v[20:21], v[48:49], v[36:37] op_sel_hi:[1,0,1]
	s_waitcnt lgkmcnt(4)
	v_pk_add_f32 v[36:37], v[22:23], v[38:39]
	v_pk_add_f32 v[22:23], v[22:23], v[38:39] neg_lo:[0,1] neg_hi:[0,1]
	s_nop 0
	v_pk_mul_f32 v[38:39], v[22:23], v[50:51] op_sel_hi:[1,0]
	s_nop 0
	v_pk_fma_f32 v[22:23], v[22:23], v[10:11], v[38:39] op_sel:[1,0,0] op_sel_hi:[0,0,1] neg_lo:[1,1,0] neg_hi:[0,1,0]
	s_waitcnt lgkmcnt(3)
	v_pk_add_f32 v[38:39], v[24:25], v[40:41]
	v_pk_add_f32 v[24:25], v[24:25], v[40:41] neg_lo:[0,1] neg_hi:[0,1]
	v_mov_b32_e32 v13, v175
	v_xor_b32_e32 v41, 0x80000000, v24
	v_mov_b32_e32 v40, v25
	s_waitcnt lgkmcnt(2)
	v_pk_add_f32 v[24:25], v[26:27], v[42:43]
	v_pk_add_f32 v[26:27], v[26:27], v[42:43] neg_lo:[0,1] neg_hi:[0,1]
	s_nop 0
	v_pk_mul_f32 v[42:43], v[26:27], v[50:51] op_sel_hi:[1,0] neg_lo:[0,1] neg_hi:[0,1]
	s_nop 0
	v_pk_fma_f32 v[26:27], v[26:27], v[10:11], v[42:43] op_sel:[1,0,0] op_sel_hi:[0,0,1] neg_lo:[1,1,0] neg_hi:[0,1,0]
	s_waitcnt lgkmcnt(1)
	v_pk_add_f32 v[42:43], v[28:29], v[44:45]
	v_pk_add_f32 v[28:29], v[28:29], v[44:45] neg_lo:[0,1] neg_hi:[0,1]
	s_nop 0
	v_pk_mul_f32 v[44:45], v[28:29], v[48:49] op_sel:[1,0] op_sel_hi:[0,0] neg_lo:[1,1] neg_hi:[0,1]
	s_nop 0
	v_pk_fma_f32 v[28:29], v[28:29], v[48:49], v[44:45] op_sel_hi:[1,0,1] neg_lo:[0,1,0] neg_hi:[0,1,0]
	s_waitcnt lgkmcnt(0)
	v_pk_add_f32 v[44:45], v[30:31], v[46:47]
	v_pk_add_f32 v[30:31], v[30:31], v[46:47] neg_lo:[0,1] neg_hi:[0,1]
	s_nop 0
	v_pk_mul_f32 v[46:47], v[30:31], v[50:51] op_sel:[1,0] op_sel_hi:[0,0] neg_lo:[1,1] neg_hi:[0,1]
	v_pk_add_f32 v[50:51], v[32:33], v[24:25]
	v_pk_add_f32 v[24:25], v[32:33], v[24:25] neg_lo:[0,1] neg_hi:[0,1]
	v_pk_fma_f32 v[30:31], v[30:31], v[10:11], v[46:47] op_sel_hi:[1,0,1] neg_lo:[0,1,0] neg_hi:[0,1,0]
	v_pk_mul_f32 v[32:33], v[24:25], v[48:49] op_sel:[1,0] op_sel_hi:[0,0] neg_lo:[1,1] neg_hi:[0,1]
	v_pk_add_f32 v[46:47], v[52:53], v[38:39]
	v_pk_fma_f32 v[24:25], v[24:25], v[48:49], v[32:33] op_sel_hi:[1,0,1]
	v_pk_add_f32 v[32:33], v[34:35], v[42:43]
	v_pk_add_f32 v[34:35], v[34:35], v[42:43] neg_lo:[0,1] neg_hi:[0,1]
	v_pk_add_f32 v[38:39], v[52:53], v[38:39] neg_lo:[0,1] neg_hi:[0,1]
	v_xor_b32_e32 v43, 0x80000000, v34
	v_mov_b32_e32 v42, v35
	v_pk_add_f32 v[34:35], v[36:37], v[44:45]
	v_pk_add_f32 v[36:37], v[36:37], v[44:45] neg_lo:[0,1] neg_hi:[0,1]
	v_mov_b32_e32 v10, v177
	v_pk_mul_f32 v[44:45], v[36:37], v[48:49] op_sel:[1,0] op_sel_hi:[0,0] neg_lo:[1,1] neg_hi:[0,1]
	s_nop 0
	v_pk_fma_f32 v[36:37], v[36:37], v[48:49], v[44:45] op_sel_hi:[1,0,1] neg_lo:[0,1,0] neg_hi:[0,1,0]
	v_pk_add_f32 v[44:45], v[46:47], v[32:33]
	v_pk_add_f32 v[32:33], v[46:47], v[32:33] neg_lo:[0,1] neg_hi:[0,1]
	v_pk_add_f32 v[46:47], v[50:51], v[34:35]
	v_pk_add_f32 v[34:35], v[50:51], v[34:35] neg_lo:[0,1] neg_hi:[0,1]
	s_nop 0
	v_xor_b32_e32 v51, 0x80000000, v34
	v_mov_b32_e32 v50, v35
	v_pk_add_f32 v[34:35], v[44:45], v[46:47]
	v_pk_add_f32 v[44:45], v[44:45], v[46:47] neg_lo:[0,1] neg_hi:[0,1]
	v_pk_add_f32 v[46:47], v[32:33], v[50:51]
	v_pk_add_f32 v[32:33], v[32:33], v[50:51] neg_lo:[0,1] neg_hi:[0,1]
	v_pk_add_f32 v[50:51], v[38:39], v[42:43]
	v_pk_add_f32 v[38:39], v[38:39], v[42:43] neg_lo:[0,1] neg_hi:[0,1]
	v_pk_add_f32 v[42:43], v[24:25], v[36:37]
	v_pk_add_f32 v[24:25], v[24:25], v[36:37] neg_lo:[0,1] neg_hi:[0,1]
	s_nop 0
	v_xor_b32_e32 v37, 0x80000000, v24
	v_mov_b32_e32 v36, v25
	v_pk_add_f32 v[24:25], v[50:51], v[42:43]
	v_pk_add_f32 v[42:43], v[50:51], v[42:43] neg_lo:[0,1] neg_hi:[0,1]
	v_pk_add_f32 v[50:51], v[38:39], v[36:37]
	v_pk_add_f32 v[36:37], v[38:39], v[36:37] neg_lo:[0,1] neg_hi:[0,1]
	v_pk_add_f32 v[38:39], v[16:17], v[40:41]
	v_pk_add_f32 v[16:17], v[16:17], v[40:41] neg_lo:[0,1] neg_hi:[0,1]
	v_pk_add_f32 v[40:41], v[18:19], v[26:27]
	v_pk_add_f32 v[18:19], v[18:19], v[26:27] neg_lo:[0,1] neg_hi:[0,1]
	s_nop 0
	v_pk_mul_f32 v[26:27], v[48:49], v[18:19] op_sel:[0,1] op_sel_hi:[0,0] neg_lo:[1,1] neg_hi:[1,0]
	v_pk_fma_f32 v[18:19], v[48:49], v[18:19], v[26:27] op_sel_hi:[0,1,1]
	v_pk_add_f32 v[26:27], v[20:21], v[28:29]
	v_pk_add_f32 v[20:21], v[20:21], v[28:29] neg_lo:[0,1] neg_hi:[0,1]
	s_nop 0
	v_xor_b32_e32 v29, 0x80000000, v20
	v_mov_b32_e32 v28, v21
	v_pk_add_f32 v[20:21], v[22:23], v[30:31]
	v_pk_add_f32 v[22:23], v[22:23], v[30:31] neg_lo:[0,1] neg_hi:[0,1]
	s_nop 0
	v_pk_mul_f32 v[30:31], v[48:49], v[22:23] op_sel:[0,1] op_sel_hi:[0,0] neg_lo:[1,1] neg_hi:[1,0]
	v_pk_fma_f32 v[22:23], v[48:49], v[22:23], v[30:31] op_sel_hi:[0,1,1] neg_lo:[1,0,0] neg_hi:[1,0,0]
	v_pk_add_f32 v[30:31], v[38:39], v[26:27]
	v_pk_add_f32 v[26:27], v[38:39], v[26:27] neg_lo:[0,1] neg_hi:[0,1]
	v_pk_add_f32 v[38:39], v[40:41], v[20:21]
	v_pk_add_f32 v[20:21], v[40:41], v[20:21] neg_lo:[0,1] neg_hi:[0,1]
	v_mov_b32_e32 v48, v167
	v_xor_b32_e32 v41, 0x80000000, v20
	v_mov_b32_e32 v40, v21
	v_pk_add_f32 v[20:21], v[30:31], v[38:39]
	v_pk_add_f32 v[30:31], v[30:31], v[38:39] neg_lo:[0,1] neg_hi:[0,1]
	v_pk_add_f32 v[38:39], v[26:27], v[40:41]
	v_pk_add_f32 v[26:27], v[26:27], v[40:41] neg_lo:[0,1] neg_hi:[0,1]
	v_pk_add_f32 v[40:41], v[16:17], v[28:29]
	v_pk_add_f32 v[16:17], v[16:17], v[28:29] neg_lo:[0,1] neg_hi:[0,1]
	v_pk_add_f32 v[28:29], v[18:19], v[22:23]
	v_pk_add_f32 v[18:19], v[18:19], v[22:23] neg_lo:[0,1] neg_hi:[0,1]
	s_nop 0
	v_xor_b32_e32 v23, 0x80000000, v18
	v_mov_b32_e32 v22, v19
	v_pk_add_f32 v[18:19], v[40:41], v[28:29]
	v_pk_add_f32 v[28:29], v[40:41], v[28:29] neg_lo:[0,1] neg_hi:[0,1]
	v_pk_add_f32 v[40:41], v[16:17], v[22:23]
	v_pk_add_f32 v[16:17], v[16:17], v[22:23] neg_lo:[0,1] neg_hi:[0,1]
	v_lshl_add_u64 v[22:23], v[14:15], 3, s[46:47]
	global_store_dwordx2 v[22:23], v[34:35], off
	v_add_u32_e32 v22, 0x200, v14
	v_ashrrev_i32_e32 v23, 31, v22
	v_lshl_add_u64 v[22:23], v[22:23], 3, s[46:47]
	global_store_dwordx2 v[22:23], v[20:21], off
	v_add_u32_e32 v20, 0x400, v14
	v_ashrrev_i32_e32 v21, 31, v20
	v_lshl_add_u64 v[20:21], v[20:21], 3, s[46:47]
	global_store_dwordx2 v[20:21], v[24:25], off
	v_add_u32_e32 v20, 0x600, v14
	v_ashrrev_i32_e32 v21, 31, v20
	v_lshl_add_u64 v[20:21], v[20:21], 3, s[46:47]
	global_store_dwordx2 v[20:21], v[18:19], off
	v_add_u32_e32 v18, 0x800, v14
	v_ashrrev_i32_e32 v19, 31, v18
	v_lshl_add_u64 v[18:19], v[18:19], 3, s[46:47]
	global_store_dwordx2 v[18:19], v[46:47], off
	v_add_u32_e32 v18, 0xa00, v14
	v_ashrrev_i32_e32 v19, 31, v18
	v_lshl_add_u64 v[18:19], v[18:19], 3, s[46:47]
	global_store_dwordx2 v[18:19], v[38:39], off
	v_add_u32_e32 v18, 0xc00, v14
	v_ashrrev_i32_e32 v19, 31, v18
	v_lshl_add_u64 v[18:19], v[18:19], 3, s[46:47]
	global_store_dwordx2 v[18:19], v[50:51], off
	v_add_u32_e32 v18, 0xe00, v14
	v_ashrrev_i32_e32 v19, 31, v18
	v_lshl_add_u64 v[18:19], v[18:19], 3, s[46:47]
	global_store_dwordx2 v[18:19], v[40:41], off
	v_add_u32_e32 v18, 0x1000, v14
	v_ashrrev_i32_e32 v19, 31, v18
	v_lshl_add_u64 v[18:19], v[18:19], 3, s[46:47]
	global_store_dwordx2 v[18:19], v[44:45], off
	v_add_u32_e32 v18, 0x1200, v14
	v_ashrrev_i32_e32 v19, 31, v18
	v_lshl_add_u64 v[18:19], v[18:19], 3, s[46:47]
	global_store_dwordx2 v[18:19], v[30:31], off
	v_add_u32_e32 v18, 0x1400, v14
	v_ashrrev_i32_e32 v19, 31, v18
	v_lshl_add_u64 v[18:19], v[18:19], 3, s[46:47]
	global_store_dwordx2 v[18:19], v[42:43], off
	v_add_u32_e32 v18, 0x1600, v14
	v_ashrrev_i32_e32 v19, 31, v18
	v_lshl_add_u64 v[18:19], v[18:19], 3, s[46:47]
	global_store_dwordx2 v[18:19], v[28:29], off
	v_add_u32_e32 v18, 0x1800, v14
	v_ashrrev_i32_e32 v19, 31, v18
	v_lshl_add_u64 v[18:19], v[18:19], 3, s[46:47]
	global_store_dwordx2 v[18:19], v[32:33], off
	v_add_u32_e32 v18, 0x1a00, v14
	v_ashrrev_i32_e32 v19, 31, v18
	v_lshl_add_u64 v[18:19], v[18:19], 3, s[46:47]
	global_store_dwordx2 v[18:19], v[26:27], off
	v_add_u32_e32 v18, 0x1c00, v14
	v_ashrrev_i32_e32 v19, 31, v18
	v_lshl_add_u64 v[18:19], v[18:19], 3, s[46:47]
	global_store_dwordx2 v[18:19], v[36:37], off
	v_add_u32_e32 v18, 0x1e00, v14
	v_ashrrev_i32_e32 v19, 31, v18
	v_lshl_add_u64 v[18:19], v[18:19], 3, s[46:47]
	global_store_dwordx2 v[18:19], v[16:17], off
	v_mov_b32_e32 v50, v169
	v_xor_b32_e32 v16, 1, v13
	v_lshlrev_b32_e32 v10, 3, v10
	v_lshlrev_b32_e32 v16, 3, v16
	v_add3_u32 v18, 0, v16, v10
	v_xor_b32_e32 v16, 2, v13
	v_lshlrev_b32_e32 v16, 3, v16
	v_xor_b32_e32 v24, 5, v13
	v_add3_u32 v20, 0, v16, v10
	v_xor_b32_e32 v16, 3, v13
	v_lshlrev_b32_e32 v24, 3, v24
	v_lshlrev_b32_e32 v15, 3, v13
	v_lshlrev_b32_e32 v16, 3, v16
	v_add3_u32 v26, 0, v24, v10
	v_xor_b32_e32 v24, 6, v13
	v_add3_u32 v15, 0, v15, v10
	v_add3_u32 v22, 0, v16, v10
	v_lshlrev_b32_e32 v24, 3, v24
	v_xor_b32_e32 v32, 9, v13
	ds_read_b64 v[16:17], v15
	ds_read_b64 v[18:19], v18
	ds_read_b64 v[20:21], v20
	ds_read_b64 v[22:23], v22
	v_xor_b32_e32 v15, 4, v13
	v_add3_u32 v28, 0, v24, v10
	v_xor_b32_e32 v24, 7, v13
	v_lshlrev_b32_e32 v32, 3, v32
	v_lshlrev_b32_e32 v15, 3, v15
	v_lshlrev_b32_e32 v24, 3, v24
	v_add3_u32 v34, 0, v32, v10
	v_xor_b32_e32 v32, 10, v13
	v_add3_u32 v15, 0, v15, v10
	v_add3_u32 v30, 0, v24, v10
	v_lshlrev_b32_e32 v32, 3, v32
	ds_read_b64 v[24:25], v15
	ds_read_b64 v[26:27], v26
	ds_read_b64 v[28:29], v28
	ds_read_b64 v[30:31], v30
	v_xor_b32_e32 v15, 8, v13
	v_add3_u32 v36, 0, v32, v10
	v_xor_b32_e32 v32, 11, v13
	v_lshlrev_b32_e32 v15, 3, v15
	v_lshlrev_b32_e32 v32, 3, v32
	v_xor_b32_e32 v40, 13, v13
	v_add3_u32 v15, 0, v15, v10
	v_add3_u32 v38, 0, v32, v10
	v_lshlrev_b32_e32 v40, 3, v40
	ds_read_b64 v[32:33], v15
	ds_read_b64 v[34:35], v34
	ds_read_b64 v[36:37], v36
	ds_read_b64 v[38:39], v38
	v_xor_b32_e32 v15, 12, v13
	v_add3_u32 v42, 0, v40, v10
	v_xor_b32_e32 v40, 14, v13
	v_xor_b32_e32 v13, 15, v13
	v_lshlrev_b32_e32 v15, 3, v15
	v_lshlrev_b32_e32 v40, 3, v40
	v_lshlrev_b32_e32 v13, 3, v13
	v_add3_u32 v15, 0, v15, v10
	v_add3_u32 v44, 0, v40, v10
	v_add3_u32 v10, 0, v13, v10
	ds_read_b64 v[40:41], v15
	ds_read_b64 v[42:43], v42
	ds_read_b64 v[44:45], v44
	ds_read_b64 v[46:47], v10
	v_mov_b32_e32 v10, v1
	v_mov_b32_e32 v13, v166
	v_mov_b32_e32 v10, v164
	s_waitcnt lgkmcnt(7)
	v_pk_add_f32 v[52:53], v[16:17], v[32:33]
	v_mov_b32_e32 v10, v165
	v_pk_add_f32 v[16:17], v[16:17], v[32:33] neg_lo:[0,1] neg_hi:[0,1]
	s_waitcnt lgkmcnt(6)
	v_pk_add_f32 v[32:33], v[18:19], v[34:35]
	v_pk_add_f32 v[18:19], v[18:19], v[34:35] neg_lo:[0,1] neg_hi:[0,1]
	v_mov_b32_e32 v13, v168
	s_nop 0
	v_pk_mul_f32 v[34:35], v[18:19], v[50:51] op_sel:[1,0] op_sel_hi:[0,0] neg_lo:[1,1] neg_hi:[0,1]
	v_mov_b32_e32 v13, v170
	v_pk_fma_f32 v[18:19], v[18:19], v[10:11], v[34:35] op_sel_hi:[1,0,1]
	s_waitcnt lgkmcnt(5)
	v_pk_add_f32 v[34:35], v[20:21], v[36:37]
	v_pk_add_f32 v[20:21], v[20:21], v[36:37] neg_lo:[0,1] neg_hi:[0,1]
	s_nop 0
	v_pk_mul_f32 v[36:37], v[20:21], v[48:49] op_sel:[1,0] op_sel_hi:[0,0] neg_lo:[1,1] neg_hi:[0,1]
	v_mov_b32_e32 v13, v171
	v_pk_fma_f32 v[20:21], v[20:21], v[48:49], v[36:37] op_sel_hi:[1,0,1]
	s_waitcnt lgkmcnt(4)
	v_pk_add_f32 v[36:37], v[22:23], v[38:39]
	v_pk_add_f32 v[22:23], v[22:23], v[38:39] neg_lo:[0,1] neg_hi:[0,1]
	s_nop 0
	v_pk_mul_f32 v[38:39], v[22:23], v[50:51] op_sel_hi:[1,0]
	s_nop 0
	v_pk_fma_f32 v[22:23], v[22:23], v[10:11], v[38:39] op_sel:[1,0,0] op_sel_hi:[0,0,1] neg_lo:[1,1,0] neg_hi:[0,1,0]
	s_waitcnt lgkmcnt(3)
	v_pk_add_f32 v[38:39], v[24:25], v[40:41]
	v_pk_add_f32 v[24:25], v[24:25], v[40:41] neg_lo:[0,1] neg_hi:[0,1]
	v_mov_b32_e32 v13, v173
	v_xor_b32_e32 v41, 0x80000000, v24
	v_mov_b32_e32 v40, v25
	s_waitcnt lgkmcnt(2)
	v_pk_add_f32 v[24:25], v[26:27], v[42:43]
	v_pk_add_f32 v[26:27], v[26:27], v[42:43] neg_lo:[0,1] neg_hi:[0,1]
	s_nop 0
	v_pk_mul_f32 v[42:43], v[26:27], v[50:51] op_sel_hi:[1,0] neg_lo:[0,1] neg_hi:[0,1]
	s_nop 0
	v_pk_fma_f32 v[26:27], v[26:27], v[10:11], v[42:43] op_sel:[1,0,0] op_sel_hi:[0,0,1] neg_lo:[1,1,0] neg_hi:[0,1,0]
	s_waitcnt lgkmcnt(1)
	v_pk_add_f32 v[42:43], v[28:29], v[44:45]
	v_pk_add_f32 v[28:29], v[28:29], v[44:45] neg_lo:[0,1] neg_hi:[0,1]
	s_nop 0
	v_pk_mul_f32 v[44:45], v[28:29], v[48:49] op_sel:[1,0] op_sel_hi:[0,0] neg_lo:[1,1] neg_hi:[0,1]
	s_nop 0
	v_pk_fma_f32 v[28:29], v[28:29], v[48:49], v[44:45] op_sel_hi:[1,0,1] neg_lo:[0,1,0] neg_hi:[0,1,0]
	s_waitcnt lgkmcnt(0)
	v_pk_add_f32 v[44:45], v[30:31], v[46:47]
	v_pk_add_f32 v[30:31], v[30:31], v[46:47] neg_lo:[0,1] neg_hi:[0,1]
	s_nop 0
	v_pk_mul_f32 v[46:47], v[30:31], v[50:51] op_sel:[1,0] op_sel_hi:[0,0] neg_lo:[1,1] neg_hi:[0,1]
	v_pk_add_f32 v[50:51], v[32:33], v[24:25]
	v_pk_add_f32 v[24:25], v[32:33], v[24:25] neg_lo:[0,1] neg_hi:[0,1]
	v_pk_fma_f32 v[30:31], v[30:31], v[10:11], v[46:47] op_sel_hi:[1,0,1] neg_lo:[0,1,0] neg_hi:[0,1,0]
	v_pk_mul_f32 v[32:33], v[24:25], v[48:49] op_sel:[1,0] op_sel_hi:[0,0] neg_lo:[1,1] neg_hi:[0,1]
	v_pk_add_f32 v[46:47], v[52:53], v[38:39]
	v_pk_fma_f32 v[24:25], v[24:25], v[48:49], v[32:33] op_sel_hi:[1,0,1]
	v_pk_add_f32 v[32:33], v[34:35], v[42:43]
	v_pk_add_f32 v[34:35], v[34:35], v[42:43] neg_lo:[0,1] neg_hi:[0,1]
	v_pk_add_f32 v[38:39], v[52:53], v[38:39] neg_lo:[0,1] neg_hi:[0,1]
	v_xor_b32_e32 v43, 0x80000000, v34
	v_mov_b32_e32 v42, v35
	v_pk_add_f32 v[34:35], v[36:37], v[44:45]
	v_pk_add_f32 v[36:37], v[36:37], v[44:45] neg_lo:[0,1] neg_hi:[0,1]
	v_mov_b32_e32 v10, v183
	v_pk_mul_f32 v[44:45], v[36:37], v[48:49] op_sel:[1,0] op_sel_hi:[0,0] neg_lo:[1,1] neg_hi:[0,1]
	s_nop 0
	v_pk_fma_f32 v[36:37], v[36:37], v[48:49], v[44:45] op_sel_hi:[1,0,1] neg_lo:[0,1,0] neg_hi:[0,1,0]
	v_pk_add_f32 v[44:45], v[46:47], v[32:33]
	v_pk_add_f32 v[32:33], v[46:47], v[32:33] neg_lo:[0,1] neg_hi:[0,1]
	v_pk_add_f32 v[46:47], v[50:51], v[34:35]
	v_pk_add_f32 v[34:35], v[50:51], v[34:35] neg_lo:[0,1] neg_hi:[0,1]
	s_nop 0
	v_xor_b32_e32 v51, 0x80000000, v34
	v_mov_b32_e32 v50, v35
	v_pk_add_f32 v[34:35], v[44:45], v[46:47]
	v_pk_add_f32 v[44:45], v[44:45], v[46:47] neg_lo:[0,1] neg_hi:[0,1]
	v_pk_add_f32 v[46:47], v[32:33], v[50:51]
	v_pk_add_f32 v[32:33], v[32:33], v[50:51] neg_lo:[0,1] neg_hi:[0,1]
	v_pk_add_f32 v[50:51], v[38:39], v[42:43]
	v_pk_add_f32 v[38:39], v[38:39], v[42:43] neg_lo:[0,1] neg_hi:[0,1]
	v_pk_add_f32 v[42:43], v[24:25], v[36:37]
	v_pk_add_f32 v[24:25], v[24:25], v[36:37] neg_lo:[0,1] neg_hi:[0,1]
	s_nop 0
	v_xor_b32_e32 v37, 0x80000000, v24
	v_mov_b32_e32 v36, v25
	v_pk_add_f32 v[24:25], v[50:51], v[42:43]
	v_pk_add_f32 v[42:43], v[50:51], v[42:43] neg_lo:[0,1] neg_hi:[0,1]
	v_pk_add_f32 v[50:51], v[38:39], v[36:37]
	v_pk_add_f32 v[36:37], v[38:39], v[36:37] neg_lo:[0,1] neg_hi:[0,1]
	v_pk_add_f32 v[38:39], v[16:17], v[40:41]
	v_pk_add_f32 v[16:17], v[16:17], v[40:41] neg_lo:[0,1] neg_hi:[0,1]
	v_pk_add_f32 v[40:41], v[18:19], v[26:27]
	v_pk_add_f32 v[18:19], v[18:19], v[26:27] neg_lo:[0,1] neg_hi:[0,1]
	s_nop 0
	v_pk_mul_f32 v[26:27], v[48:49], v[18:19] op_sel:[0,1] op_sel_hi:[0,0] neg_lo:[1,1] neg_hi:[1,0]
	v_pk_fma_f32 v[18:19], v[48:49], v[18:19], v[26:27] op_sel_hi:[0,1,1]
	v_pk_add_f32 v[26:27], v[20:21], v[28:29]
	v_pk_add_f32 v[20:21], v[20:21], v[28:29] neg_lo:[0,1] neg_hi:[0,1]
	s_nop 0
	v_xor_b32_e32 v29, 0x80000000, v20
	v_mov_b32_e32 v28, v21
	v_pk_add_f32 v[20:21], v[22:23], v[30:31]
	v_pk_add_f32 v[22:23], v[22:23], v[30:31] neg_lo:[0,1] neg_hi:[0,1]
	s_nop 0
	v_pk_mul_f32 v[30:31], v[48:49], v[22:23] op_sel:[0,1] op_sel_hi:[0,0] neg_lo:[1,1] neg_hi:[1,0]
	v_pk_fma_f32 v[22:23], v[48:49], v[22:23], v[30:31] op_sel_hi:[0,1,1] neg_lo:[1,0,0] neg_hi:[1,0,0]
	v_pk_add_f32 v[30:31], v[38:39], v[26:27]
	v_pk_add_f32 v[26:27], v[38:39], v[26:27] neg_lo:[0,1] neg_hi:[0,1]
	v_pk_add_f32 v[38:39], v[40:41], v[20:21]
	v_pk_add_f32 v[20:21], v[40:41], v[20:21] neg_lo:[0,1] neg_hi:[0,1]
	s_nop 0
	v_xor_b32_e32 v41, 0x80000000, v20
	v_mov_b32_e32 v40, v21
	v_pk_add_f32 v[20:21], v[30:31], v[38:39]
	v_pk_add_f32 v[30:31], v[30:31], v[38:39] neg_lo:[0,1] neg_hi:[0,1]
	v_pk_add_f32 v[38:39], v[26:27], v[40:41]
	v_pk_add_f32 v[26:27], v[26:27], v[40:41] neg_lo:[0,1] neg_hi:[0,1]
	v_pk_add_f32 v[40:41], v[16:17], v[28:29]
	v_pk_add_f32 v[16:17], v[16:17], v[28:29] neg_lo:[0,1] neg_hi:[0,1]
	v_pk_add_f32 v[28:29], v[18:19], v[22:23]
	v_pk_add_f32 v[18:19], v[18:19], v[22:23] neg_lo:[0,1] neg_hi:[0,1]
	s_nop 0
	v_xor_b32_e32 v23, 0x80000000, v18
	v_mov_b32_e32 v22, v19
	v_pk_add_f32 v[18:19], v[40:41], v[28:29]
	v_pk_add_f32 v[28:29], v[40:41], v[28:29] neg_lo:[0,1] neg_hi:[0,1]
	v_pk_add_f32 v[40:41], v[16:17], v[22:23]
	v_pk_add_f32 v[16:17], v[16:17], v[22:23] neg_lo:[0,1] neg_hi:[0,1]
	v_add_u32_e32 v22, 0x2000, v14
	v_ashrrev_i32_e32 v23, 31, v22
	v_lshl_add_u64 v[22:23], v[22:23], 3, s[46:47]
	global_store_dwordx2 v[22:23], v[34:35], off
	v_add_u32_e32 v22, 0x2200, v14
	v_ashrrev_i32_e32 v23, 31, v22
	v_lshl_add_u64 v[22:23], v[22:23], 3, s[46:47]
	global_store_dwordx2 v[22:23], v[20:21], off
	v_add_u32_e32 v20, 0x2400, v14
	v_ashrrev_i32_e32 v21, 31, v20
	v_lshl_add_u64 v[20:21], v[20:21], 3, s[46:47]
	global_store_dwordx2 v[20:21], v[24:25], off
	v_add_u32_e32 v20, 0x2600, v14
	v_ashrrev_i32_e32 v21, 31, v20
	v_lshl_add_u64 v[20:21], v[20:21], 3, s[46:47]
	global_store_dwordx2 v[20:21], v[18:19], off
	v_add_u32_e32 v18, 0x2800, v14
	v_ashrrev_i32_e32 v19, 31, v18
	v_lshl_add_u64 v[18:19], v[18:19], 3, s[46:47]
	global_store_dwordx2 v[18:19], v[46:47], off
	v_add_u32_e32 v18, 0x2a00, v14
	v_ashrrev_i32_e32 v19, 31, v18
	v_lshl_add_u64 v[18:19], v[18:19], 3, s[46:47]
	global_store_dwordx2 v[18:19], v[38:39], off
	v_add_u32_e32 v18, 0x2c00, v14
	v_ashrrev_i32_e32 v19, 31, v18
	v_lshl_add_u64 v[18:19], v[18:19], 3, s[46:47]
	global_store_dwordx2 v[18:19], v[50:51], off
	v_add_u32_e32 v18, 0x2e00, v14
	v_ashrrev_i32_e32 v19, 31, v18
	v_lshl_add_u64 v[18:19], v[18:19], 3, s[46:47]
	global_store_dwordx2 v[18:19], v[40:41], off
	v_add_u32_e32 v18, 0x3000, v14
	v_ashrrev_i32_e32 v19, 31, v18
	v_lshl_add_u64 v[18:19], v[18:19], 3, s[46:47]
	global_store_dwordx2 v[18:19], v[44:45], off
	v_add_u32_e32 v18, 0x3200, v14
	v_ashrrev_i32_e32 v19, 31, v18
	v_lshl_add_u64 v[18:19], v[18:19], 3, s[46:47]
	global_store_dwordx2 v[18:19], v[30:31], off
	v_add_u32_e32 v18, 0x3400, v14
	v_ashrrev_i32_e32 v19, 31, v18
	v_lshl_add_u64 v[18:19], v[18:19], 3, s[46:47]
	global_store_dwordx2 v[18:19], v[42:43], off
	v_add_u32_e32 v18, 0x3600, v14
	v_ashrrev_i32_e32 v19, 31, v18
	v_lshl_add_u64 v[18:19], v[18:19], 3, s[46:47]
	global_store_dwordx2 v[18:19], v[28:29], off
	v_add_u32_e32 v18, 0x3800, v14
	v_ashrrev_i32_e32 v19, 31, v18
	v_lshl_add_u64 v[18:19], v[18:19], 3, s[46:47]
	global_store_dwordx2 v[18:19], v[32:33], off
	v_add_u32_e32 v18, 0x3a00, v14
	v_ashrrev_i32_e32 v19, 31, v18
	v_lshl_add_u64 v[18:19], v[18:19], 3, s[46:47]
	global_store_dwordx2 v[18:19], v[26:27], off
	v_add_u32_e32 v18, 0x3c00, v14
	v_add_u32_e32 v14, 0x3e00, v14
	v_ashrrev_i32_e32 v15, 31, v14
	v_ashrrev_i32_e32 v19, 31, v18
	v_lshl_add_u64 v[14:15], v[14:15], 3, s[46:47]
	v_lshl_add_u64 v[18:19], v[18:19], 3, s[46:47]
	global_store_dwordx2 v[14:15], v[16:17], off
	v_mov_b32_e32 v16, v184
	v_mov_b32_e32 v14, v182
	global_store_dwordx2 v[18:19], v[36:37], off
	s_barrier
	s_nop 0
	v_pk_mul_f32 v[36:37], v[16:17], s[64:65] op_sel_hi:[0,1] neg_lo:[1,0]
	s_mov_b64 s[64:65], vcc
	v_ashrrev_i32_e32 v15, 31, v14
	v_lshl_add_u64 v[18:19], v[14:15], 2, s[64:65]
	s_movk_i32 vcc_lo, 0x1000
	v_add_co_u32_e32 v28, vcc, vcc_lo, v18
	v_pk_mul_f32 v[40:41], v[16:17], s[78:79] op_sel_hi:[0,1] neg_lo:[1,0]
	s_nop 0
	v_addc_co_u32_e32 v29, vcc, 0, v19, vcc
	v_add_co_u32_e32 v20, vcc, s39, v18
	s_movk_i32 s78, 0x3000
	s_nop 0
	v_addc_co_u32_e32 v21, vcc, 0, v19, vcc
	v_add_co_u32_e32 v48, vcc, s78, v18
	v_pk_mul_f32 v[32:33], v[16:17], s[40:41] op_sel_hi:[0,1] neg_lo:[1,0]
	s_nop 0
	v_addc_co_u32_e32 v49, vcc, 0, v19, vcc
	v_add_co_u32_e32 v22, vcc, s72, v18
	s_mov_b32 s40, 0x3f7ec46d
	s_nop 0
	v_addc_co_u32_e32 v23, vcc, 0, v19, vcc
	v_add_co_u32_e32 v58, vcc, s33, v18
	s_mov_b32 s33, 0x8000
	s_nop 0
	v_addc_co_u32_e32 v59, vcc, 0, v19, vcc
	v_add_co_u32_e32 v60, vcc, s43, v18
	s_mov_b32 s41, 0xbdc8bd36
	s_nop 0
	v_addc_co_u32_e32 v61, vcc, 0, v19, vcc
	v_add_co_u32_e32 v64, vcc, s73, v18
	v_pk_mul_f32 v[34:35], v[16:17], s[76:77] op_sel_hi:[0,1] neg_lo:[1,0]
	s_nop 0
	v_addc_co_u32_e32 v65, vcc, 0, v19, vcc
	v_add_co_u32_e32 v68, vcc, s33, v18
	s_mov_b32 s33, 0x9000
	s_nop 0
	v_addc_co_u32_e32 v69, vcc, 0, v19, vcc
	v_add_co_u32_e32 v24, vcc, s33, v18
	s_mov_b32 s33, 0xa000
	s_nop 0
	v_addc_co_u32_e32 v25, vcc, 0, v19, vcc
	v_add_co_u32_e32 v26, vcc, s33, v18
	s_mov_b32 s33, 0xb000
	s_nop 0
	v_addc_co_u32_e32 v27, vcc, 0, v19, vcc
	v_add_co_u32_e32 v30, vcc, s33, v18
	s_mov_b32 s33, 0xc000
	s_nop 0
	v_addc_co_u32_e32 v31, vcc, 0, v19, vcc
	v_add_co_u32_e32 v38, vcc, s33, v18
	s_mov_b32 s33, 0xd000
	s_nop 0
	v_addc_co_u32_e32 v39, vcc, 0, v19, vcc
	v_add_co_u32_e32 v44, vcc, s33, v18
	s_mov_b32 s33, 0xe000
	s_nop 0
	v_addc_co_u32_e32 v45, vcc, 0, v19, vcc
	v_add_co_u32_e32 v50, vcc, s33, v18
	s_mov_b32 s33, 0xf000
	s_nop 0
	v_addc_co_u32_e32 v51, vcc, 0, v19, vcc
	v_add_co_u32_e32 v70, vcc, s33, v18
	v_pk_mul_f32 v[92:93], v[16:17], s[62:63] op_sel_hi:[0,1] neg_lo:[1,0]
	s_nop 0
	v_addc_co_u32_e32 v71, vcc, 0, v19, vcc
	global_load_dword v94, v[68:69], off
	global_load_dword v96, v[68:69], off offset:2048
	global_load_dword v98, v[26:27], off offset:-4096
	global_load_dword v100, v[24:25], off offset:2048
	global_load_dword v102, v[26:27], off
	global_load_dword v104, v[26:27], off offset:2048
	global_load_dword v106, v[38:39], off offset:-4096
	global_load_dword v108, v[30:31], off offset:2048
	global_load_dword v110, v[38:39], off
	global_load_dword v112, v[38:39], off offset:2048
	global_load_dword v114, v[50:51], off offset:-4096
	global_load_dword v116, v[44:45], off offset:2048
	global_load_dword v118, v[50:51], off
	global_load_dword v120, v[50:51], off offset:2048
	global_load_dword v122, v[70:71], off
	global_load_dword v56, v[20:21], off
	s_nop 0
	global_load_dword v50, v[20:21], off offset:2048
	global_load_dword v124, v[70:71], off offset:2048
	global_load_dword v44, v[22:23], off offset:-4096
	global_load_dword v38, v[22:23], off
	global_load_dword v72, v[20:21], off offset:-4096
	global_load_dword v30, v[22:23], off offset:2048
	global_load_dword v26, v[60:61], off offset:-4096
	global_load_dword v24, v[60:61], off
	s_nop 0
	global_load_dword v22, v[60:61], off offset:2048
	global_load_dword v20, v[68:69], off offset:-4096
	global_load_dword v74, v[18:19], off
	global_load_dword v78, v[18:19], off offset:2048
	s_nop 0
	global_load_dword v68, v[28:29], off offset:2048
	s_nop 0
	global_load_dword v48, v[48:49], off offset:2048
	s_nop 0
	global_load_dword v28, v[58:59], off offset:2048
	global_load_dword v18, v[64:65], off offset:2048
	v_pk_mul_f32 v[52:53], v[16:17], s[58:59] op_sel_hi:[0,1] neg_lo:[1,0]
	v_pk_fma_f32 v[82:83], v[10:11], s[40:41], v[34:35] op_sel_hi:[0,1,1]
	v_pk_fma_f32 v[34:35], v[10:11], s[92:93], v[92:93] op_sel_hi:[0,1,1]
	s_mov_b32 s92, 0x3e47c5c2
	v_pk_mul_f32 v[66:67], v[16:17], s[60:61] op_sel_hi:[0,1] neg_lo:[1,0]
	v_pk_fma_f32 v[84:85], v[10:11], s[44:45], v[32:33] op_sel_hi:[0,1,1]
	v_pk_fma_f32 v[60:61], v[10:11], s[82:83], v[52:53] op_sel_hi:[0,1,1]
	s_mov_b32 s82, 0x3f45e403
	s_mov_b32 s93, 0xbf7b14be
	v_pk_mul_f32 v[32:33], v[16:17], s[30:31] op_sel_hi:[0,1] neg_lo:[1,0]
	s_mov_b32 s30, 0x3dc8bd36
	v_pk_mul_f32 v[54:55], v[16:17], s[74:75] op_sel_hi:[0,1] neg_lo:[1,0]
	v_pk_mul_f32 v[62:63], v[16:17], s[54:55] op_sel_hi:[0,1] neg_lo:[1,0]
	s_mov_b32 s83, 0xbf226799
	v_pk_fma_f32 v[52:53], v[10:11], s[86:87], v[66:67] op_sel_hi:[0,1,1]
	s_mov_b32 s31, 0xbf7ec46d
	v_pk_fma_f32 v[66:67], v[10:11], s[92:93], v[32:33] op_sel_hi:[0,1,1]
	v_pk_mul_f32 v[32:33], v[16:17], s[34:35] op_sel_hi:[0,1] neg_lo:[1,0]
	v_pk_fma_f32 v[76:77], v[10:11], s[80:81], v[40:41] op_sel_hi:[0,1,1]
	s_mov_b32 s80, 0x3f61c598
	v_pk_fma_f32 v[58:59], v[10:11], s[82:83], v[54:55] op_sel_hi:[0,1,1]
	v_pk_fma_f32 v[54:55], v[10:11], s[84:85], v[62:63] op_sel_hi:[0,1,1]
	s_mov_b32 s86, 0x3f0e39da
	v_pk_fma_f32 v[62:63], v[10:11], s[30:31], v[32:33] op_sel_hi:[0,1,1]
	v_pk_mul_f32 v[32:33], v[16:17], s[36:37] op_sel_hi:[0,1] neg_lo:[1,0]
	v_pk_mul_f32 v[46:47], v[16:17], s[48:49] op_sel_hi:[0,1] neg_lo:[1,0]
	v_pk_mul_f32 v[86:87], v[16:17], s[66:67] op_sel_hi:[0,1] neg_lo:[1,0]
	s_mov_b32 s81, 0xbef15aea
	s_mov_b32 s87, 0xbf54db31
	v_pk_fma_f32 v[32:33], v[10:11], s[96:97], v[32:33] op_sel_hi:[0,1,1]
	s_mov_b32 s54, 0x3f6c835e
	v_pk_fma_f32 v[64:65], v[10:11], s[80:81], v[46:47] op_sel_hi:[0,1,1]
	v_pk_fma_f32 v[46:47], v[10:11], s[86:87], v[86:87] op_sel_hi:[0,1,1]
	v_pk_mul_f32 v[42:43], v[16:17], s[50:51] op_sel_hi:[0,1] neg_lo:[1,0]
	v_pk_mul_f32 v[88:89], v[16:17], s[68:69] op_sel_hi:[0,1] neg_lo:[1,0]
	s_mov_b32 s55, 0xbec3ef15
	v_pk_fma_f32 v[70:71], v[10:11], s[54:55], v[42:43] op_sel_hi:[0,1,1]
	v_pk_fma_f32 v[42:43], v[10:11], s[88:89], v[88:89] op_sel_hi:[0,1,1]
	s_mov_b32 s88, 0x3ec3ef15
	v_pk_mul_f32 v[90:91], v[16:17], s[56:57] op_sel_hi:[0,1] neg_lo:[1,0]
	s_mov_b32 s89, 0xbf6c835e
	v_pk_fma_f32 v[40:41], v[10:11], s[88:89], v[90:91] op_sel_hi:[0,1,1]
	s_mov_b32 s76, 0x3f7b14be
	s_mov_b32 s77, 0xbe47c5c2
	v_pk_fma_f32 v[80:81], v[10:11], s[76:77], v[36:37] op_sel_hi:[0,1,1]
	v_mov_b32_e32 v36, v169
	v_mov_b32_e32 v15, v171
	s_waitcnt vmcnt(31)
	v_pk_mul_f32 v[86:87], v[32:33], v[94:95] op_sel_hi:[1,0]
	v_pk_mul_f32 v[32:33], v[16:17], s[2:3] op_sel_hi:[0,1] neg_lo:[1,0]
	v_pk_fma_f32 v[32:33], v[10:11], s[0:1], v[32:33] op_sel_hi:[0,1,1]
	s_waitcnt vmcnt(30)
	v_pk_mul_f32 v[88:89], v[32:33], v[96:97] op_sel_hi:[1,0]
	v_pk_mul_f32 v[32:33], v[16:17], s[6:7] op_sel_hi:[0,1] neg_lo:[1,0]
	v_pk_fma_f32 v[32:33], v[10:11], s[4:5], v[32:33] op_sel_hi:[0,1,1]
	s_waitcnt vmcnt(29)
	v_pk_mul_f32 v[90:91], v[32:33], v[98:99] op_sel_hi:[1,0]
	v_pk_mul_f32 v[32:33], v[16:17], s[10:11] op_sel_hi:[0,1] neg_lo:[1,0]
	v_pk_fma_f32 v[32:33], v[10:11], s[8:9], v[32:33] op_sel_hi:[0,1,1]
	s_waitcnt vmcnt(28)
	v_pk_mul_f32 v[92:93], v[32:33], v[100:101] op_sel_hi:[1,0]
	v_pk_mul_f32 v[32:33], v[16:17], s[16:17] op_sel_hi:[0,1] neg_lo:[1,0]
	v_pk_fma_f32 v[32:33], v[10:11], s[12:13], v[32:33] op_sel_hi:[0,1,1]
	s_waitcnt vmcnt(27)
	v_pk_mul_f32 v[94:95], v[32:33], v[102:103] op_sel_hi:[1,0]
	v_pk_mul_f32 v[32:33], v[16:17], s[20:21] op_sel_hi:[0,1] neg_lo:[1,0]
	v_pk_fma_f32 v[32:33], v[10:11], s[18:19], v[32:33] op_sel_hi:[0,1,1]
	s_waitcnt vmcnt(26)
	v_pk_mul_f32 v[96:97], v[32:33], v[104:105] op_sel_hi:[1,0]
	v_pk_mul_f32 v[32:33], v[16:17], s[24:25] op_sel_hi:[0,1] neg_lo:[1,0]
	v_pk_fma_f32 v[32:33], v[10:11], s[22:23], v[32:33] op_sel_hi:[0,1,1]
	s_waitcnt vmcnt(25)
	v_pk_mul_f32 v[98:99], v[32:33], v[106:107] op_sel_hi:[1,0]
	v_pk_mul_f32 v[32:33], v[16:17], s[28:29] op_sel_hi:[0,1] neg_lo:[1,0]
	v_pk_fma_f32 v[32:33], v[10:11], s[26:27], v[32:33] op_sel_hi:[0,1,1]
	s_waitcnt vmcnt(24)
	v_pk_mul_f32 v[100:101], v[32:33], v[108:109] op_sel_hi:[1,0]
	v_pk_mul_f32 v[32:33], v[16:17], s[84:85] op_sel_hi:[0,0] neg_lo:[1,0]
	v_pk_fma_f32 v[32:33], v[10:11], s[38:39], v[32:33] op_sel_hi:[0,0,1] neg_lo:[0,0,1] neg_hi:[0,0,1]
	s_waitcnt vmcnt(23)
	v_pk_mul_f32 v[102:103], v[32:33], v[110:111] op_sel_hi:[1,0]
	v_pk_mul_f32 v[32:33], v[16:17], s[26:27] op_sel_hi:[0,1] neg_lo:[1,0]
	v_pk_fma_f32 v[32:33], v[10:11], s[28:29], v[32:33] op_sel_hi:[0,1,1]
	s_waitcnt vmcnt(22)
	v_pk_mul_f32 v[104:105], v[32:33], v[112:113] op_sel_hi:[1,0]
	v_pk_mul_f32 v[32:33], v[16:17], s[22:23] op_sel_hi:[0,1] neg_lo:[1,0]
	v_pk_fma_f32 v[32:33], v[10:11], s[24:25], v[32:33] op_sel_hi:[0,1,1]
	s_waitcnt vmcnt(21)
	v_pk_mul_f32 v[106:107], v[32:33], v[114:115] op_sel_hi:[1,0]
	v_pk_mul_f32 v[32:33], v[16:17], s[18:19] op_sel_hi:[0,1] neg_lo:[1,0]
	v_pk_fma_f32 v[32:33], v[10:11], s[20:21], v[32:33] op_sel_hi:[0,1,1]
	s_waitcnt vmcnt(20)
	v_pk_mul_f32 v[108:109], v[32:33], v[116:117] op_sel_hi:[1,0]
	v_pk_mul_f32 v[32:33], v[16:17], s[12:13] op_sel_hi:[0,1] neg_lo:[1,0]
	v_pk_fma_f32 v[32:33], v[10:11], s[16:17], v[32:33] op_sel_hi:[0,1,1]
	s_waitcnt vmcnt(19)
	v_pk_mul_f32 v[110:111], v[32:33], v[118:119] op_sel_hi:[1,0]
	v_pk_mul_f32 v[32:33], v[16:17], s[8:9] op_sel_hi:[0,1] neg_lo:[1,0]
	v_pk_fma_f32 v[32:33], v[10:11], s[10:11], v[32:33] op_sel_hi:[0,1,1]
	s_waitcnt vmcnt(18)
	v_pk_mul_f32 v[112:113], v[32:33], v[120:121] op_sel_hi:[1,0]
	v_pk_mul_f32 v[32:33], v[16:17], s[4:5] op_sel_hi:[0,1] neg_lo:[1,0]
	v_pk_mul_f32 v[16:17], v[16:17], s[0:1] op_sel_hi:[0,1] neg_lo:[1,0]
	v_pk_fma_f32 v[16:17], v[10:11], s[2:3], v[16:17] op_sel_hi:[0,1,1]
	v_pk_fma_f32 v[32:33], v[10:11], s[6:7], v[32:33] op_sel_hi:[0,1,1]
	s_waitcnt vmcnt(14)
	v_pk_mul_f32 v[116:117], v[16:17], v[124:125] op_sel_hi:[1,0]
	v_mov_b32_e32 v10, v1
	s_waitcnt vmcnt(5)
	v_pk_fma_f32 v[126:127], v[74:75], v[84:85], v[86:87] op_sel_hi:[0,1,1]
	v_pk_fma_f32 v[74:75], v[74:75], v[84:85], v[86:87] op_sel_hi:[0,1,1] neg_lo:[0,0,1] neg_hi:[0,0,1]
	s_waitcnt vmcnt(4)
	v_pk_fma_f32 v[84:85], v[82:83], v[78:79], v[88:89] op_sel_hi:[1,0,1]
	v_pk_fma_f32 v[78:79], v[82:83], v[78:79], v[88:89] op_sel_hi:[1,0,1] neg_lo:[0,0,1] neg_hi:[0,0,1]
	v_pk_mul_f32 v[114:115], v[32:33], v[122:123] op_sel_hi:[1,0]
	v_mov_b32_e32 v118, v164
	v_mov_b32_e32 v32, v165
	v_mov_b32_e32 v120, v166
	v_mov_b32_e32 v10, v167
	v_mov_b32_e32 v122, v168
	v_mov_b32_e32 v124, v170
	s_nop 0
	v_pk_mul_f32 v[82:83], v[78:79], v[124:125] op_sel:[1,0] op_sel_hi:[0,0] neg_lo:[1,1] neg_hi:[0,1]
	s_nop 0
	v_pk_fma_f32 v[78:79], v[78:79], v[118:119], v[82:83] op_sel_hi:[1,0,1]
	v_pk_fma_f32 v[82:83], v[80:81], v[72:73], v[90:91] op_sel_hi:[1,0,1]
	v_pk_fma_f32 v[72:73], v[80:81], v[72:73], v[90:91] op_sel_hi:[1,0,1] neg_lo:[0,0,1] neg_hi:[0,0,1]
	s_nop 0
	v_pk_mul_f32 v[80:81], v[72:73], v[36:37] op_sel:[1,0] op_sel_hi:[0,0] neg_lo:[1,1] neg_hi:[0,1]
	s_nop 0
	v_pk_fma_f32 v[72:73], v[72:73], v[32:33], v[80:81] op_sel_hi:[1,0,1]
	s_waitcnt vmcnt(3)
	v_pk_fma_f32 v[80:81], v[76:77], v[68:69], v[92:93] op_sel_hi:[1,0,1]
	v_pk_fma_f32 v[68:69], v[76:77], v[68:69], v[92:93] op_sel_hi:[1,0,1] neg_lo:[0,0,1] neg_hi:[0,0,1]
	s_nop 0
	v_pk_mul_f32 v[76:77], v[68:69], v[122:123] op_sel:[1,0] op_sel_hi:[0,0] neg_lo:[1,1] neg_hi:[0,1]
	s_nop 0
	v_pk_fma_f32 v[68:69], v[68:69], v[120:121], v[76:77] op_sel_hi:[1,0,1]
	v_pk_fma_f32 v[76:77], v[70:71], v[56:57], v[94:95] op_sel_hi:[1,0,1]
	v_pk_fma_f32 v[56:57], v[70:71], v[56:57], v[94:95] op_sel_hi:[1,0,1] neg_lo:[0,0,1] neg_hi:[0,0,1]
	s_nop 0
	v_pk_mul_f32 v[70:71], v[56:57], v[10:11] op_sel:[1,0] op_sel_hi:[0,0] neg_lo:[1,1] neg_hi:[0,1]
	s_nop 0
	v_pk_fma_f32 v[56:57], v[56:57], v[10:11], v[70:71] op_sel_hi:[1,0,1]
	v_pk_fma_f32 v[70:71], v[64:65], v[50:51], v[96:97] op_sel_hi:[1,0,1]
	v_pk_fma_f32 v[50:51], v[64:65], v[50:51], v[96:97] op_sel_hi:[1,0,1] neg_lo:[0,0,1] neg_hi:[0,0,1]
	s_nop 0
	v_pk_mul_f32 v[64:65], v[50:51], v[122:123] op_sel_hi:[1,0]
	v_xor_b32_e32 v86, 0x80000000, v51
	v_mov_b32_e32 v87, v50
	v_pk_fma_f32 v[50:51], v[60:61], v[44:45], v[98:99] op_sel_hi:[1,0,1]
	v_pk_fma_f32 v[44:45], v[60:61], v[44:45], v[98:99] op_sel_hi:[1,0,1] neg_lo:[0,0,1] neg_hi:[0,0,1]
	v_pk_fma_f32 v[64:65], v[86:87], v[120:121], v[64:65] op_sel_hi:[1,0,1] neg_lo:[0,1,0] neg_hi:[0,1,0]
	v_pk_mul_f32 v[60:61], v[44:45], v[36:37] op_sel_hi:[1,0]
	v_xor_b32_e32 v86, 0x80000000, v45
	v_mov_b32_e32 v87, v44
	s_waitcnt vmcnt(2)
	v_pk_fma_f32 v[44:45], v[58:59], v[48:49], v[100:101] op_sel_hi:[1,0,1]
	v_pk_fma_f32 v[48:49], v[58:59], v[48:49], v[100:101] op_sel_hi:[1,0,1] neg_lo:[0,0,1] neg_hi:[0,0,1]
	v_pk_fma_f32 v[60:61], v[86:87], v[32:33], v[60:61] op_sel_hi:[1,0,1] neg_lo:[0,1,0] neg_hi:[0,1,0]
	v_pk_mul_f32 v[58:59], v[48:49], v[124:125] op_sel_hi:[1,0]
	s_nop 0
	v_pk_fma_f32 v[48:49], v[48:49], v[118:119], v[58:59] op_sel:[1,0,0] op_sel_hi:[0,0,1] neg_lo:[1,1,0] neg_hi:[0,1,0]
	v_pk_fma_f32 v[58:59], v[54:55], v[38:39], v[102:103] op_sel_hi:[1,0,1]
	v_pk_fma_f32 v[38:39], v[54:55], v[38:39], v[102:103] op_sel_hi:[1,0,1] neg_lo:[0,0,1] neg_hi:[0,0,1]
	s_nop 0
	v_xor_b32_e32 v55, 0x80000000, v38
	v_mov_b32_e32 v54, v39
	v_pk_fma_f32 v[38:39], v[52:53], v[30:31], v[104:105] op_sel_hi:[1,0,1]
	v_pk_fma_f32 v[30:31], v[52:53], v[30:31], v[104:105] op_sel_hi:[1,0,1] neg_lo:[0,0,1] neg_hi:[0,0,1]
	s_nop 0
	v_pk_mul_f32 v[52:53], v[30:31], v[124:125] op_sel_hi:[1,0] neg_lo:[0,1] neg_hi:[0,1]
	v_xor_b32_e32 v86, 0x80000000, v31
	v_mov_b32_e32 v87, v30
	v_pk_fma_f32 v[30:31], v[46:47], v[26:27], v[106:107] op_sel_hi:[1,0,1]
	v_pk_fma_f32 v[26:27], v[46:47], v[26:27], v[106:107] op_sel_hi:[1,0,1] neg_lo:[0,0,1] neg_hi:[0,0,1]
	v_pk_fma_f32 v[52:53], v[86:87], v[118:119], v[52:53] op_sel_hi:[1,0,1] neg_lo:[0,1,0] neg_hi:[0,1,0]
	v_pk_mul_f32 v[46:47], v[26:27], v[36:37] op_sel_hi:[1,0] neg_lo:[0,1] neg_hi:[0,1]
	v_xor_b32_e32 v86, 0x80000000, v27
	v_mov_b32_e32 v87, v26
	s_waitcnt vmcnt(1)
	v_pk_fma_f32 v[26:27], v[42:43], v[28:29], v[108:109] op_sel_hi:[1,0,1]
	v_pk_fma_f32 v[28:29], v[42:43], v[28:29], v[108:109] op_sel_hi:[1,0,1] neg_lo:[0,0,1] neg_hi:[0,0,1]
	v_pk_fma_f32 v[86:87], v[86:87], v[32:33], v[46:47] op_sel_hi:[1,0,1] neg_lo:[0,1,0] neg_hi:[0,1,0]
	v_pk_mul_f32 v[42:43], v[28:29], v[122:123] op_sel_hi:[1,0] neg_lo:[0,1] neg_hi:[0,1]
	v_xor_b32_e32 v46, 0x80000000, v29
	v_mov_b32_e32 v47, v28
	v_pk_fma_f32 v[28:29], v[40:41], v[24:25], v[110:111] op_sel_hi:[1,0,1]
	v_pk_fma_f32 v[24:25], v[40:41], v[24:25], v[110:111] op_sel_hi:[1,0,1] neg_lo:[0,0,1] neg_hi:[0,0,1]
	v_pk_fma_f32 v[42:43], v[46:47], v[120:121], v[42:43] op_sel_hi:[1,0,1] neg_lo:[0,1,0] neg_hi:[0,1,0]
	v_pk_mul_f32 v[40:41], v[24:25], v[10:11] op_sel:[1,0] op_sel_hi:[0,0] neg_lo:[1,1] neg_hi:[0,1]
	s_nop 0
	v_pk_fma_f32 v[88:89], v[24:25], v[10:11], v[40:41] op_sel_hi:[1,0,1] neg_lo:[0,1,0] neg_hi:[0,1,0]
	v_pk_fma_f32 v[24:25], v[34:35], v[22:23], v[112:113] op_sel_hi:[1,0,1]
	v_pk_fma_f32 v[22:23], v[34:35], v[22:23], v[112:113] op_sel_hi:[1,0,1] neg_lo:[0,0,1] neg_hi:[0,0,1]
	v_pk_add_f32 v[40:41], v[84:85], v[38:39]
	v_pk_mul_f32 v[34:35], v[22:23], v[122:123] op_sel:[1,0] op_sel_hi:[0,0] neg_lo:[1,1] neg_hi:[0,1]
	v_pk_add_f32 v[38:39], v[84:85], v[38:39] neg_lo:[0,1] neg_hi:[0,1]
	v_pk_fma_f32 v[90:91], v[22:23], v[120:121], v[34:35] op_sel_hi:[1,0,1] neg_lo:[0,1,0] neg_hi:[0,1,0]
	v_pk_fma_f32 v[22:23], v[66:67], v[20:21], v[114:115] op_sel_hi:[1,0,1]
	v_pk_fma_f32 v[20:21], v[66:67], v[20:21], v[114:115] op_sel_hi:[1,0,1] neg_lo:[0,0,1] neg_hi:[0,0,1]
	s_nop 0
	v_pk_mul_f32 v[34:35], v[20:21], v[36:37] op_sel:[1,0] op_sel_hi:[0,0] neg_lo:[1,1] neg_hi:[0,1]
	v_pk_fma_f32 v[66:67], v[20:21], v[32:33], v[34:35] op_sel_hi:[1,0,1] neg_lo:[0,1,0] neg_hi:[0,1,0]
	s_waitcnt vmcnt(0)
	v_pk_fma_f32 v[20:21], v[62:63], v[18:19], v[116:117] op_sel_hi:[1,0,1]
	v_pk_fma_f32 v[18:19], v[62:63], v[18:19], v[116:117] op_sel_hi:[1,0,1] neg_lo:[0,0,1] neg_hi:[0,0,1]
	v_pk_mul_f32 v[46:47], v[38:39], v[36:37] op_sel:[1,0] op_sel_hi:[0,0] neg_lo:[1,1] neg_hi:[0,1]
	v_pk_mul_f32 v[34:35], v[18:19], v[124:125] op_sel:[1,0] op_sel_hi:[0,0] neg_lo:[1,1] neg_hi:[0,1]
	v_pk_fma_f32 v[38:39], v[38:39], v[32:33], v[46:47] op_sel_hi:[1,0,1]
	v_pk_add_f32 v[46:47], v[82:83], v[30:31]
	v_pk_add_f32 v[30:31], v[82:83], v[30:31] neg_lo:[0,1] neg_hi:[0,1]
	v_pk_fma_f32 v[62:63], v[18:19], v[118:119], v[34:35] op_sel_hi:[1,0,1] neg_lo:[0,1,0] neg_hi:[0,1,0]
	v_pk_add_f32 v[18:19], v[126:127], v[58:59]
	v_pk_add_f32 v[34:35], v[126:127], v[58:59] neg_lo:[0,1] neg_hi:[0,1]
	v_pk_mul_f32 v[58:59], v[30:31], v[10:11] op_sel:[1,0] op_sel_hi:[0,0] neg_lo:[1,1] neg_hi:[0,1]
	s_nop 0
	v_pk_fma_f32 v[58:59], v[30:31], v[10:11], v[58:59] op_sel_hi:[1,0,1]
	v_pk_add_f32 v[30:31], v[80:81], v[26:27]
	v_pk_add_f32 v[26:27], v[80:81], v[26:27] neg_lo:[0,1] neg_hi:[0,1]
	s_nop 0
	v_pk_mul_f32 v[80:81], v[26:27], v[36:37] op_sel_hi:[1,0]
	v_xor_b32_e32 v82, 0x80000000, v27
	v_mov_b32_e32 v83, v26
	v_pk_add_f32 v[26:27], v[76:77], v[28:29]
	v_pk_add_f32 v[28:29], v[76:77], v[28:29] neg_lo:[0,1] neg_hi:[0,1]
	v_pk_fma_f32 v[80:81], v[82:83], v[32:33], v[80:81] op_sel_hi:[1,0,1] neg_lo:[0,1,0] neg_hi:[0,1,0]
	v_xor_b32_e32 v77, 0x80000000, v28
	v_mov_b32_e32 v76, v29
	v_pk_add_f32 v[28:29], v[70:71], v[24:25]
	v_pk_add_f32 v[24:25], v[70:71], v[24:25] neg_lo:[0,1] neg_hi:[0,1]
	s_nop 0
	v_pk_mul_f32 v[70:71], v[24:25], v[36:37] op_sel_hi:[1,0] neg_lo:[0,1] neg_hi:[0,1]
	s_nop 0
	v_pk_fma_f32 v[24:25], v[24:25], v[32:33], v[70:71] op_sel:[1,0,0] op_sel_hi:[0,0,1] neg_lo:[1,1,0] neg_hi:[0,1,0]
	v_pk_add_f32 v[70:71], v[50:51], v[22:23]
	v_pk_add_f32 v[22:23], v[50:51], v[22:23] neg_lo:[0,1] neg_hi:[0,1]
	s_nop 0
	v_pk_mul_f32 v[50:51], v[22:23], v[10:11] op_sel:[1,0] op_sel_hi:[0,0] neg_lo:[1,1] neg_hi:[0,1]
	s_nop 0
	v_pk_fma_f32 v[50:51], v[22:23], v[10:11], v[50:51] op_sel_hi:[1,0,1] neg_lo:[0,1,0] neg_hi:[0,1,0]
	v_pk_add_f32 v[22:23], v[44:45], v[20:21]
	v_pk_add_f32 v[20:21], v[44:45], v[20:21] neg_lo:[0,1] neg_hi:[0,1]
	s_nop 0
	v_pk_mul_f32 v[44:45], v[20:21], v[36:37] op_sel:[1,0] op_sel_hi:[0,0] neg_lo:[1,1] neg_hi:[0,1]
	s_nop 0
	v_pk_fma_f32 v[20:21], v[20:21], v[32:33], v[44:45] op_sel_hi:[1,0,1] neg_lo:[0,1,0] neg_hi:[0,1,0]
	v_pk_add_f32 v[44:45], v[18:19], v[26:27]
	v_pk_add_f32 v[18:19], v[18:19], v[26:27] neg_lo:[0,1] neg_hi:[0,1]
	v_pk_add_f32 v[26:27], v[40:41], v[28:29]
	v_pk_add_f32 v[28:29], v[40:41], v[28:29] neg_lo:[0,1] neg_hi:[0,1]
	s_nop 0
	v_pk_mul_f32 v[40:41], v[28:29], v[10:11] op_sel:[1,0] op_sel_hi:[0,0] neg_lo:[1,1] neg_hi:[0,1]
	s_nop 0
	v_pk_fma_f32 v[28:29], v[28:29], v[10:11], v[40:41] op_sel_hi:[1,0,1]
	v_pk_add_f32 v[40:41], v[46:47], v[70:71]
	v_pk_add_f32 v[46:47], v[46:47], v[70:71] neg_lo:[0,1] neg_hi:[0,1]
	s_nop 0
	v_xor_b32_e32 v71, 0x80000000, v46
	v_mov_b32_e32 v70, v47
	v_pk_add_f32 v[46:47], v[30:31], v[22:23]
	v_pk_add_f32 v[22:23], v[30:31], v[22:23] neg_lo:[0,1] neg_hi:[0,1]
	s_nop 0
	v_pk_mul_f32 v[30:31], v[22:23], v[10:11] op_sel:[1,0] op_sel_hi:[0,0] neg_lo:[1,1] neg_hi:[0,1]
	s_nop 0
	v_pk_fma_f32 v[82:83], v[22:23], v[10:11], v[30:31] op_sel_hi:[1,0,1] neg_lo:[0,1,0] neg_hi:[0,1,0]
	v_pk_add_f32 v[30:31], v[26:27], v[46:47]
	v_pk_add_f32 v[26:27], v[26:27], v[46:47] neg_lo:[0,1] neg_hi:[0,1]
	v_pk_add_f32 v[22:23], v[44:45], v[40:41]
	v_pk_add_f32 v[40:41], v[44:45], v[40:41] neg_lo:[0,1] neg_hi:[0,1]
	v_pk_add_f32 v[84:85], v[22:23], v[30:31]
	v_pk_add_f32 v[30:31], v[22:23], v[30:31] neg_lo:[0,1] neg_hi:[0,1]
	v_pk_add_f32 v[46:47], v[40:41], v[26:27] op_sel:[0,1] op_sel_hi:[1,0] neg_hi:[0,1]
	v_pk_add_f32 v[22:23], v[40:41], v[26:27] op_sel:[0,1] op_sel_hi:[1,0] neg_lo:[0,1]
	v_pk_add_f32 v[40:41], v[28:29], v[82:83]
	v_pk_add_f32 v[28:29], v[28:29], v[82:83] neg_lo:[0,1] neg_hi:[0,1]
	v_pk_add_f32 v[26:27], v[18:19], v[70:71]
	v_pk_add_f32 v[18:19], v[18:19], v[70:71] neg_lo:[0,1] neg_hi:[0,1]
	v_pk_add_f32 v[70:71], v[26:27], v[40:41]
	v_pk_add_f32 v[26:27], v[26:27], v[40:41] neg_lo:[0,1] neg_hi:[0,1]
	v_pk_add_f32 v[40:41], v[18:19], v[28:29] op_sel:[0,1] op_sel_hi:[1,0] neg_hi:[0,1]
	v_pk_add_f32 v[18:19], v[18:19], v[28:29] op_sel:[0,1] op_sel_hi:[1,0] neg_lo:[0,1]
	v_pk_add_f32 v[28:29], v[34:35], v[76:77]
	v_pk_add_f32 v[44:45], v[34:35], v[76:77] neg_lo:[0,1] neg_hi:[0,1]
	v_pk_add_f32 v[34:35], v[38:39], v[24:25]
	v_pk_add_f32 v[24:25], v[38:39], v[24:25] neg_lo:[0,1] neg_hi:[0,1]
	s_nop 0
	v_pk_mul_f32 v[38:39], v[10:11], v[24:25] op_sel:[0,1] op_sel_hi:[0,0] neg_lo:[1,1] neg_hi:[1,0]
	v_pk_fma_f32 v[38:39], v[10:11], v[24:25], v[38:39] op_sel_hi:[0,1,1]
	v_pk_add_f32 v[24:25], v[58:59], v[50:51]
	v_pk_add_f32 v[50:51], v[58:59], v[50:51] neg_lo:[0,1] neg_hi:[0,1]
	s_nop 0
	v_xor_b32_e32 v59, 0x80000000, v50
	v_mov_b32_e32 v58, v51
	v_pk_add_f32 v[50:51], v[80:81], v[20:21]
	v_pk_add_f32 v[20:21], v[80:81], v[20:21] neg_lo:[0,1] neg_hi:[0,1]
	s_nop 0
	v_pk_mul_f32 v[76:77], v[10:11], v[20:21] op_sel:[0,1] op_sel_hi:[0,0] neg_lo:[1,1] neg_hi:[1,0]
	v_pk_fma_f32 v[20:21], v[10:11], v[20:21], v[76:77] op_sel_hi:[0,1,1] neg_lo:[1,0,0] neg_hi:[1,0,0]
	v_pk_add_f32 v[76:77], v[28:29], v[24:25]
	v_pk_add_f32 v[24:25], v[28:29], v[24:25] neg_lo:[0,1] neg_hi:[0,1]
	v_pk_add_f32 v[28:29], v[34:35], v[50:51]
	v_pk_add_f32 v[34:35], v[34:35], v[50:51] neg_lo:[0,1] neg_hi:[0,1]
	v_pk_add_f32 v[82:83], v[76:77], v[28:29]
	v_xor_b32_e32 v81, 0x80000000, v34
	v_mov_b32_e32 v80, v35
	v_pk_add_f32 v[34:35], v[76:77], v[28:29] neg_lo:[0,1] neg_hi:[0,1]
	v_pk_add_f32 v[28:29], v[44:45], v[58:59]
	v_pk_add_f32 v[58:59], v[44:45], v[58:59] neg_lo:[0,1] neg_hi:[0,1]
	v_pk_add_f32 v[44:45], v[38:39], v[20:21]
	v_pk_add_f32 v[20:21], v[38:39], v[20:21] neg_lo:[0,1] neg_hi:[0,1]
	v_pk_add_f32 v[76:77], v[28:29], v[44:45]
	v_pk_add_f32 v[28:29], v[28:29], v[44:45] neg_lo:[0,1] neg_hi:[0,1]
	v_pk_add_f32 v[44:45], v[58:59], v[20:21] op_sel:[0,1] op_sel_hi:[1,0] neg_hi:[0,1]
	v_pk_add_f32 v[20:21], v[58:59], v[20:21] op_sel:[0,1] op_sel_hi:[1,0] neg_lo:[0,1]
	v_pk_add_f32 v[38:39], v[74:75], v[54:55]
	v_pk_add_f32 v[58:59], v[74:75], v[54:55] neg_lo:[0,1] neg_hi:[0,1]
	v_pk_add_f32 v[54:55], v[78:79], v[52:53]
	v_pk_add_f32 v[52:53], v[78:79], v[52:53] neg_lo:[0,1] neg_hi:[0,1]
	v_pk_add_f32 v[50:51], v[24:25], v[80:81]
	v_pk_mul_f32 v[74:75], v[36:37], v[52:53] op_sel:[0,1] op_sel_hi:[0,0] neg_lo:[1,1] neg_hi:[1,0]
	v_pk_fma_f32 v[52:53], v[32:33], v[52:53], v[74:75] op_sel_hi:[0,1,1]
	v_pk_add_f32 v[74:75], v[72:73], v[86:87]
	v_pk_add_f32 v[72:73], v[72:73], v[86:87] neg_lo:[0,1] neg_hi:[0,1]
	v_pk_add_f32 v[24:25], v[24:25], v[80:81] neg_lo:[0,1] neg_hi:[0,1]
	v_pk_mul_f32 v[78:79], v[10:11], v[72:73] op_sel:[0,1] op_sel_hi:[0,0] neg_lo:[1,1] neg_hi:[1,0]
	v_pk_fma_f32 v[72:73], v[10:11], v[72:73], v[78:79] op_sel_hi:[0,1,1]
	v_pk_add_f32 v[78:79], v[68:69], v[42:43]
	v_pk_add_f32 v[42:43], v[68:69], v[42:43] neg_lo:[0,1] neg_hi:[0,1]
	s_nop 0
	v_pk_mul_f32 v[68:69], v[32:33], v[42:43] op_sel:[0,1] op_sel_hi:[0,0] neg_lo:[1,1] neg_hi:[1,0]
	v_pk_fma_f32 v[42:43], v[36:37], v[42:43], v[68:69] op_sel_hi:[0,1,1]
	v_pk_add_f32 v[68:69], v[56:57], v[88:89]
	v_pk_add_f32 v[56:57], v[56:57], v[88:89] neg_lo:[0,1] neg_hi:[0,1]
	s_nop 0
	v_xor_b32_e32 v81, 0x80000000, v56
	v_mov_b32_e32 v80, v57
	v_pk_add_f32 v[56:57], v[64:65], v[90:91]
	v_pk_add_f32 v[64:65], v[64:65], v[90:91] neg_lo:[0,1] neg_hi:[0,1]
	s_nop 0
	v_pk_mul_f32 v[86:87], v[32:33], v[64:65] op_sel:[0,1] op_sel_hi:[0,0] neg_lo:[1,1] neg_hi:[1,0]
	v_pk_fma_f32 v[64:65], v[36:37], v[64:65], v[86:87] op_sel_hi:[0,1,1] neg_lo:[1,0,0] neg_hi:[1,0,0]
	v_pk_add_f32 v[86:87], v[60:61], v[66:67]
	v_pk_add_f32 v[60:61], v[60:61], v[66:67] neg_lo:[0,1] neg_hi:[0,1]
	s_nop 0
	v_pk_mul_f32 v[66:67], v[10:11], v[60:61] op_sel:[0,1] op_sel_hi:[0,0] neg_lo:[1,1] neg_hi:[1,0]
	v_pk_fma_f32 v[60:61], v[10:11], v[60:61], v[66:67] op_sel_hi:[0,1,1] neg_lo:[1,0,0] neg_hi:[1,0,0]
	v_pk_add_f32 v[66:67], v[48:49], v[62:63]
	v_pk_add_f32 v[48:49], v[48:49], v[62:63] neg_lo:[0,1] neg_hi:[0,1]
	s_nop 0
	v_pk_mul_f32 v[36:37], v[36:37], v[48:49] op_sel:[0,1] op_sel_hi:[0,0] neg_lo:[1,1] neg_hi:[1,0]
	v_pk_fma_f32 v[36:37], v[32:33], v[48:49], v[36:37] op_sel_hi:[0,1,1] neg_lo:[1,0,0] neg_hi:[1,0,0]
	v_pk_add_f32 v[32:33], v[38:39], v[68:69]
	v_pk_add_f32 v[48:49], v[38:39], v[68:69] neg_lo:[0,1] neg_hi:[0,1]
	v_pk_add_f32 v[38:39], v[56:57], v[54:55]
	v_pk_add_f32 v[54:55], v[54:55], v[56:57] neg_lo:[0,1] neg_hi:[0,1]
	v_pk_add_f32 v[62:63], v[74:75], v[86:87] neg_lo:[0,1] neg_hi:[0,1]
	v_pk_mul_f32 v[56:57], v[10:11], v[54:55] op_sel:[0,1] op_sel_hi:[0,0] neg_lo:[1,1] neg_hi:[1,0]
	v_xor_b32_e32 v69, 0x80000000, v62
	v_mov_b32_e32 v68, v63
	v_pk_add_f32 v[62:63], v[78:79], v[66:67]
	v_pk_add_f32 v[66:67], v[78:79], v[66:67] neg_lo:[0,1] neg_hi:[0,1]
	v_pk_fma_f32 v[56:57], v[10:11], v[54:55], v[56:57] op_sel_hi:[0,1,1]
	v_pk_add_f32 v[54:55], v[74:75], v[86:87]
	v_pk_mul_f32 v[74:75], v[10:11], v[66:67] op_sel:[0,1] op_sel_hi:[0,0] neg_lo:[1,1] neg_hi:[1,0]
	v_pk_fma_f32 v[66:67], v[10:11], v[66:67], v[74:75] op_sel_hi:[0,1,1] neg_lo:[1,0,0] neg_hi:[1,0,0]
	v_pk_add_f32 v[74:75], v[32:33], v[54:55]
	v_pk_add_f32 v[32:33], v[32:33], v[54:55] neg_lo:[0,1] neg_hi:[0,1]
	v_pk_add_f32 v[54:55], v[38:39], v[62:63]
	v_pk_add_f32 v[38:39], v[38:39], v[62:63] neg_lo:[0,1] neg_hi:[0,1]
	v_pk_add_f32 v[78:79], v[74:75], v[54:55]
	v_pk_add_f32 v[54:55], v[74:75], v[54:55] neg_lo:[0,1] neg_hi:[0,1]
	v_pk_add_f32 v[74:75], v[32:33], v[38:39] op_sel:[0,1] op_sel_hi:[1,0] neg_hi:[0,1]
	v_pk_add_f32 v[38:39], v[32:33], v[38:39] op_sel:[0,1] op_sel_hi:[1,0] neg_lo:[0,1]
	v_pk_add_f32 v[32:33], v[48:49], v[68:69]
	v_pk_add_f32 v[62:63], v[48:49], v[68:69] neg_lo:[0,1] neg_hi:[0,1]
	v_pk_add_f32 v[48:49], v[56:57], v[66:67]
	v_pk_add_f32 v[56:57], v[56:57], v[66:67] neg_lo:[0,1] neg_hi:[0,1]
	s_nop 0
	v_xor_b32_e32 v67, 0x80000000, v56
	v_mov_b32_e32 v66, v57
	v_pk_add_f32 v[56:57], v[32:33], v[48:49]
	v_pk_add_f32 v[48:49], v[32:33], v[48:49] neg_lo:[0,1] neg_hi:[0,1]
	v_pk_add_f32 v[68:69], v[62:63], v[66:67]
	v_pk_add_f32 v[32:33], v[62:63], v[66:67] neg_lo:[0,1] neg_hi:[0,1]
	v_pk_add_f32 v[66:67], v[64:65], v[52:53]
	v_pk_add_f32 v[52:53], v[52:53], v[64:65] neg_lo:[0,1] neg_hi:[0,1]
	v_pk_add_f32 v[62:63], v[58:59], v[80:81]
	v_pk_mul_f32 v[64:65], v[10:11], v[52:53] op_sel:[0,1] op_sel_hi:[0,0] neg_lo:[1,1] neg_hi:[1,0]
	v_pk_fma_f32 v[52:53], v[10:11], v[52:53], v[64:65] op_sel_hi:[0,1,1]
	v_pk_add_f32 v[64:65], v[72:73], v[60:61]
	v_pk_add_f32 v[60:61], v[72:73], v[60:61] neg_lo:[0,1] neg_hi:[0,1]
	v_pk_add_f32 v[58:59], v[58:59], v[80:81] neg_lo:[0,1] neg_hi:[0,1]
	v_xor_b32_e32 v73, 0x80000000, v60
	v_mov_b32_e32 v72, v61
	v_pk_add_f32 v[60:61], v[42:43], v[36:37]
	v_pk_add_f32 v[36:37], v[42:43], v[36:37] neg_lo:[0,1] neg_hi:[0,1]
	s_nop 0
	v_pk_mul_f32 v[42:43], v[10:11], v[36:37] op_sel:[0,1] op_sel_hi:[0,0] neg_lo:[1,1] neg_hi:[1,0]
	v_pk_fma_f32 v[36:37], v[10:11], v[36:37], v[42:43] op_sel_hi:[0,1,1] neg_lo:[1,0,0] neg_hi:[1,0,0]
	v_pk_add_f32 v[42:43], v[62:63], v[64:65]
	v_pk_add_f32 v[62:63], v[62:63], v[64:65] neg_lo:[0,1] neg_hi:[0,1]
	v_pk_add_f32 v[64:65], v[66:67], v[60:61]
	v_pk_add_f32 v[60:61], v[66:67], v[60:61] neg_lo:[0,1] neg_hi:[0,1]
	v_lshl_add_u32 v10, v13, 3, 0
	v_xor_b32_e32 v67, 0x80000000, v60
	v_mov_b32_e32 v66, v61
	v_pk_add_f32 v[60:61], v[42:43], v[64:65]
	v_pk_add_f32 v[64:65], v[42:43], v[64:65] neg_lo:[0,1] neg_hi:[0,1]
	v_pk_add_f32 v[80:81], v[62:63], v[66:67]
	v_pk_add_f32 v[42:43], v[62:63], v[66:67] neg_lo:[0,1] neg_hi:[0,1]
	v_pk_add_f32 v[66:67], v[52:53], v[36:37]
	v_pk_add_f32 v[36:37], v[52:53], v[36:37] neg_lo:[0,1] neg_hi:[0,1]
	v_pk_add_f32 v[62:63], v[58:59], v[72:73]
	v_pk_add_f32 v[58:59], v[58:59], v[72:73] neg_lo:[0,1] neg_hi:[0,1]
	v_pk_add_f32 v[86:87], v[62:63], v[66:67]
	v_pk_add_f32 v[52:53], v[62:63], v[66:67] neg_lo:[0,1] neg_hi:[0,1]
	v_pk_add_f32 v[62:63], v[58:59], v[36:37] op_sel:[0,1] op_sel_hi:[1,0] neg_hi:[0,1]
	v_pk_add_f32 v[36:37], v[58:59], v[36:37] op_sel:[0,1] op_sel_hi:[1,0] neg_lo:[0,1]
	v_pk_mul_f32 v[58:59], v[84:85], s[14:15] op_sel:[1,0] neg_lo:[1,0]
	s_nop 0
	v_pk_fma_f32 v[58:59], v[84:85], s[94:95], v[58:59] op_sel_hi:[0,1,1]
	ds_write_b64 v10, v[58:59]
	v_pk_fma_f32 v[58:59], v[178:179], s[90:91], v[178:179] op_sel:[1,0,0] op_sel_hi:[0,1,1]
	v_pk_mul_f32 v[66:67], v[58:59], v[78:79] op_sel:[1,1] op_sel_hi:[0,1] neg_lo:[0,1]
	v_pk_fma_f32 v[66:67], v[58:59], v[78:79], v[66:67] op_sel_hi:[1,0,1]
	ds_write_b64 v10, v[66:67] offset:4224
	v_pk_mul_f32 v[66:67], v[178:179], v[58:59] op_sel:[1,1] op_sel_hi:[0,1] neg_lo:[0,1]
	v_pk_fma_f32 v[58:59], v[178:179], v[58:59], v[66:67] op_sel_hi:[1,0,1]
	s_nop 0
	v_pk_mul_f32 v[66:67], v[58:59], v[82:83] op_sel:[1,1] op_sel_hi:[0,1] neg_lo:[0,1]
	v_pk_fma_f32 v[66:67], v[58:59], v[82:83], v[66:67] op_sel_hi:[1,0,1]
	ds_write_b64 v10, v[66:67] offset:8448
	v_pk_mul_f32 v[66:67], v[178:179], v[58:59] op_sel:[1,1] op_sel_hi:[0,1] neg_lo:[0,1]
	v_pk_fma_f32 v[58:59], v[178:179], v[58:59], v[66:67] op_sel_hi:[1,0,1]
	s_nop 0
	v_pk_mul_f32 v[66:67], v[58:59], v[60:61] op_sel:[1,1] op_sel_hi:[0,1] neg_lo:[0,1]
	v_pk_fma_f32 v[60:61], v[58:59], v[60:61], v[66:67] op_sel_hi:[1,0,1]
	ds_write_b64 v10, v[60:61] offset:12672
	v_pk_mul_f32 v[60:61], v[178:179], v[58:59] op_sel:[1,1] op_sel_hi:[0,1] neg_lo:[0,1]
	v_pk_fma_f32 v[58:59], v[178:179], v[58:59], v[60:61] op_sel_hi:[1,0,1]
	s_nop 0
	v_pk_mul_f32 v[60:61], v[70:71], v[58:59] op_sel:[1,1] op_sel_hi:[1,0] neg_lo:[1,0]
	s_nop 0
	v_pk_fma_f32 v[60:61], v[70:71], v[58:59], v[60:61] op_sel_hi:[0,1,1]
	ds_write_b64 v10, v[60:61] offset:16896
	v_pk_mul_f32 v[60:61], v[178:179], v[58:59] op_sel:[1,1] op_sel_hi:[0,1] neg_lo:[0,1]
	v_pk_fma_f32 v[58:59], v[178:179], v[58:59], v[60:61] op_sel_hi:[1,0,1]
	s_nop 0
	v_pk_mul_f32 v[60:61], v[58:59], v[56:57] op_sel:[1,1] op_sel_hi:[0,1] neg_lo:[0,1]
	v_pk_fma_f32 v[56:57], v[58:59], v[56:57], v[60:61] op_sel_hi:[1,0,1]
	ds_write_b64 v10, v[56:57] offset:21120
	v_pk_mul_f32 v[56:57], v[178:179], v[58:59] op_sel:[1,1] op_sel_hi:[0,1] neg_lo:[0,1]
	v_pk_fma_f32 v[56:57], v[178:179], v[58:59], v[56:57] op_sel_hi:[1,0,1]
	s_nop 0
	v_pk_mul_f32 v[58:59], v[76:77], v[56:57] op_sel:[1,1] op_sel_hi:[1,0] neg_lo:[1,0]
	s_nop 0
	v_pk_fma_f32 v[58:59], v[76:77], v[56:57], v[58:59] op_sel_hi:[0,1,1]
	ds_write_b64 v10, v[58:59] offset:25344
	v_pk_mul_f32 v[58:59], v[178:179], v[56:57] op_sel:[1,1] op_sel_hi:[0,1] neg_lo:[0,1]
	v_pk_fma_f32 v[56:57], v[178:179], v[56:57], v[58:59] op_sel_hi:[1,0,1]
	s_nop 0
	v_pk_mul_f32 v[58:59], v[86:87], v[56:57] op_sel:[1,1] op_sel_hi:[1,0] neg_lo:[1,0]
	s_nop 0
	v_pk_fma_f32 v[58:59], v[86:87], v[56:57], v[58:59] op_sel_hi:[0,1,1]
	ds_write_b64 v10, v[58:59] offset:29568
	v_pk_mul_f32 v[58:59], v[178:179], v[56:57] op_sel:[1,1] op_sel_hi:[0,1] neg_lo:[0,1]
	v_pk_fma_f32 v[56:57], v[178:179], v[56:57], v[58:59] op_sel_hi:[1,0,1]
	s_nop 0
	v_pk_mul_f32 v[58:59], v[46:47], v[56:57] op_sel:[1,1] op_sel_hi:[1,0] neg_lo:[1,0]
	s_nop 0
	v_pk_fma_f32 v[46:47], v[46:47], v[56:57], v[58:59] op_sel_hi:[0,1,1]
	ds_write_b64 v10, v[46:47] offset:33792
	v_pk_mul_f32 v[46:47], v[178:179], v[56:57] op_sel:[1,1] op_sel_hi:[0,1] neg_lo:[0,1]
	v_pk_fma_f32 v[46:47], v[178:179], v[56:57], v[46:47] op_sel_hi:[1,0,1]
	s_nop 0
	v_pk_mul_f32 v[56:57], v[74:75], v[46:47] op_sel:[1,1] op_sel_hi:[1,0] neg_lo:[1,0]
	s_nop 0
	v_pk_fma_f32 v[56:57], v[74:75], v[46:47], v[56:57] op_sel_hi:[0,1,1]
	ds_write_b64 v10, v[56:57] offset:38016
	v_pk_mul_f32 v[56:57], v[178:179], v[46:47] op_sel:[1,1] op_sel_hi:[0,1] neg_lo:[0,1]
	v_pk_fma_f32 v[46:47], v[178:179], v[46:47], v[56:57] op_sel_hi:[1,0,1]
	s_nop 0
	v_pk_mul_f32 v[56:57], v[50:51], v[46:47] op_sel:[1,1] op_sel_hi:[1,0] neg_lo:[1,0]
	s_nop 0
	v_pk_fma_f32 v[50:51], v[50:51], v[46:47], v[56:57] op_sel_hi:[0,1,1]
	ds_write_b64 v10, v[50:51] offset:42240
	v_pk_mul_f32 v[50:51], v[178:179], v[46:47] op_sel:[1,1] op_sel_hi:[0,1] neg_lo:[0,1]
	v_pk_fma_f32 v[46:47], v[178:179], v[46:47], v[50:51] op_sel_hi:[1,0,1]
	s_nop 0
	v_pk_mul_f32 v[50:51], v[80:81], v[46:47] op_sel:[1,1] op_sel_hi:[1,0] neg_lo:[1,0]
	s_nop 0
	v_pk_fma_f32 v[50:51], v[80:81], v[46:47], v[50:51] op_sel_hi:[0,1,1]
	ds_write_b64 v10, v[50:51] offset:46464
	v_pk_mul_f32 v[50:51], v[178:179], v[46:47] op_sel:[1,1] op_sel_hi:[0,1] neg_lo:[0,1]
	v_pk_fma_f32 v[46:47], v[178:179], v[46:47], v[50:51] op_sel_hi:[1,0,1]
	s_nop 0
	v_pk_mul_f32 v[50:51], v[40:41], v[46:47] op_sel:[1,1] op_sel_hi:[1,0] neg_lo:[1,0]
	s_nop 0
	v_pk_fma_f32 v[40:41], v[40:41], v[46:47], v[50:51] op_sel_hi:[0,1,1]
	ds_write_b64 v10, v[40:41] offset:50688
	v_pk_mul_f32 v[40:41], v[178:179], v[46:47] op_sel:[1,1] op_sel_hi:[0,1] neg_lo:[0,1]
	v_pk_fma_f32 v[40:41], v[178:179], v[46:47], v[40:41] op_sel_hi:[1,0,1]
	s_nop 0
	v_pk_mul_f32 v[46:47], v[68:69], v[40:41] op_sel:[1,1] op_sel_hi:[1,0] neg_lo:[1,0]
	s_nop 0
	v_pk_fma_f32 v[46:47], v[68:69], v[40:41], v[46:47] op_sel_hi:[0,1,1]
	ds_write_b64 v10, v[46:47] offset:54912
	v_pk_mul_f32 v[46:47], v[178:179], v[40:41] op_sel:[1,1] op_sel_hi:[0,1] neg_lo:[0,1]
	v_pk_fma_f32 v[40:41], v[178:179], v[40:41], v[46:47] op_sel_hi:[1,0,1]
	s_nop 0
	v_pk_mul_f32 v[46:47], v[44:45], v[40:41] op_sel:[1,1] op_sel_hi:[1,0] neg_lo:[1,0]
	s_nop 0
	v_pk_fma_f32 v[44:45], v[44:45], v[40:41], v[46:47] op_sel_hi:[0,1,1]
	ds_write_b64 v10, v[44:45] offset:59136
	v_pk_mul_f32 v[44:45], v[178:179], v[40:41] op_sel:[1,1] op_sel_hi:[0,1] neg_lo:[0,1]
	v_pk_fma_f32 v[40:41], v[178:179], v[40:41], v[44:45] op_sel_hi:[1,0,1]
	s_nop 0
	v_pk_mul_f32 v[44:45], v[62:63], v[40:41] op_sel:[1,1] op_sel_hi:[1,0] neg_lo:[1,0]
	s_nop 0
	v_pk_fma_f32 v[44:45], v[62:63], v[40:41], v[44:45] op_sel_hi:[0,1,1]
	ds_write_b64 v10, v[44:45] offset:63360
	v_pk_mul_f32 v[44:45], v[178:179], v[40:41] op_sel:[1,1] op_sel_hi:[0,1] neg_lo:[0,1]
	v_pk_fma_f32 v[40:41], v[178:179], v[40:41], v[44:45] op_sel_hi:[1,0,1]
	s_nop 0
	v_pk_mul_f32 v[44:45], v[30:31], v[40:41] op_sel:[1,1] op_sel_hi:[1,0] neg_lo:[1,0]
	v_add_u32_e32 v13, 0x10800, v10
	v_pk_fma_f32 v[30:31], v[30:31], v[40:41], v[44:45] op_sel_hi:[0,1,1]
	ds_write_b64 v13, v[30:31]
	v_pk_mul_f32 v[30:31], v[178:179], v[40:41] op_sel:[1,1] op_sel_hi:[0,1] neg_lo:[0,1]
	v_pk_fma_f32 v[30:31], v[178:179], v[40:41], v[30:31] op_sel_hi:[1,0,1]
	s_nop 0
	v_pk_mul_f32 v[40:41], v[54:55], v[30:31] op_sel:[1,1] op_sel_hi:[1,0] neg_lo:[1,0]
	v_add_u32_e32 v13, 0x11880, v10
	v_pk_fma_f32 v[40:41], v[54:55], v[30:31], v[40:41] op_sel_hi:[0,1,1]
	ds_write_b64 v13, v[40:41]
	v_pk_mul_f32 v[40:41], v[178:179], v[30:31] op_sel:[1,1] op_sel_hi:[0,1] neg_lo:[0,1]
	v_pk_fma_f32 v[30:31], v[178:179], v[30:31], v[40:41] op_sel_hi:[1,0,1]
	s_nop 0
	v_pk_mul_f32 v[40:41], v[34:35], v[30:31] op_sel:[1,1] op_sel_hi:[1,0] neg_lo:[1,0]
	v_add_u32_e32 v13, 0x12900, v10
	v_pk_fma_f32 v[34:35], v[34:35], v[30:31], v[40:41] op_sel_hi:[0,1,1]
	ds_write_b64 v13, v[34:35]
	v_pk_mul_f32 v[34:35], v[178:179], v[30:31] op_sel:[1,1] op_sel_hi:[0,1] neg_lo:[0,1]
	v_pk_fma_f32 v[30:31], v[178:179], v[30:31], v[34:35] op_sel_hi:[1,0,1]
	s_nop 0
	v_pk_mul_f32 v[34:35], v[64:65], v[30:31] op_sel:[1,1] op_sel_hi:[1,0] neg_lo:[1,0]
	v_add_u32_e32 v13, 0x13980, v10
	v_pk_fma_f32 v[34:35], v[64:65], v[30:31], v[34:35] op_sel_hi:[0,1,1]
	ds_write_b64 v13, v[34:35]
	v_pk_mul_f32 v[34:35], v[178:179], v[30:31] op_sel:[1,1] op_sel_hi:[0,1] neg_lo:[0,1]
	v_pk_fma_f32 v[30:31], v[178:179], v[30:31], v[34:35] op_sel_hi:[1,0,1]
	s_nop 0
	v_pk_mul_f32 v[34:35], v[26:27], v[30:31] op_sel:[1,1] op_sel_hi:[1,0] neg_lo:[1,0]
	v_add_u32_e32 v13, 0x14a00, v10
	v_pk_fma_f32 v[26:27], v[26:27], v[30:31], v[34:35] op_sel_hi:[0,1,1]
	ds_write_b64 v13, v[26:27]
	v_pk_mul_f32 v[26:27], v[178:179], v[30:31] op_sel:[1,1] op_sel_hi:[0,1] neg_lo:[0,1]
	v_pk_fma_f32 v[26:27], v[178:179], v[30:31], v[26:27] op_sel_hi:[1,0,1]
	s_nop 0
	v_pk_mul_f32 v[30:31], v[48:49], v[26:27] op_sel:[1,1] op_sel_hi:[1,0] neg_lo:[1,0]
	v_add_u32_e32 v13, 0x15a80, v10
	v_pk_fma_f32 v[30:31], v[48:49], v[26:27], v[30:31] op_sel_hi:[0,1,1]
	ds_write_b64 v13, v[30:31]
	v_pk_mul_f32 v[30:31], v[178:179], v[26:27] op_sel:[1,1] op_sel_hi:[0,1] neg_lo:[0,1]
	v_pk_fma_f32 v[26:27], v[178:179], v[26:27], v[30:31] op_sel_hi:[1,0,1]
	s_nop 0
	v_pk_mul_f32 v[30:31], v[28:29], v[26:27] op_sel:[1,1] op_sel_hi:[1,0] neg_lo:[1,0]
	v_add_u32_e32 v13, 0x16b00, v10
	v_pk_fma_f32 v[28:29], v[28:29], v[26:27], v[30:31] op_sel_hi:[0,1,1]
	ds_write_b64 v13, v[28:29]
	v_pk_mul_f32 v[28:29], v[178:179], v[26:27] op_sel:[1,1] op_sel_hi:[0,1] neg_lo:[0,1]
	v_pk_fma_f32 v[26:27], v[178:179], v[26:27], v[28:29] op_sel_hi:[1,0,1]
	s_nop 0
	v_pk_mul_f32 v[28:29], v[52:53], v[26:27] op_sel:[1,1] op_sel_hi:[1,0] neg_lo:[1,0]
	v_add_u32_e32 v13, 0x17b80, v10
	v_pk_fma_f32 v[28:29], v[52:53], v[26:27], v[28:29] op_sel_hi:[0,1,1]
	ds_write_b64 v13, v[28:29]
	v_pk_mul_f32 v[28:29], v[178:179], v[26:27] op_sel:[1,1] op_sel_hi:[0,1] neg_lo:[0,1]
	v_pk_fma_f32 v[26:27], v[178:179], v[26:27], v[28:29] op_sel_hi:[1,0,1]
	s_nop 0
	v_pk_mul_f32 v[28:29], v[22:23], v[26:27] op_sel:[1,1] op_sel_hi:[1,0] neg_lo:[1,0]
	v_add_u32_e32 v13, 0x18c00, v10
	v_pk_fma_f32 v[22:23], v[22:23], v[26:27], v[28:29] op_sel_hi:[0,1,1]
	ds_write_b64 v13, v[22:23]
	v_pk_mul_f32 v[22:23], v[178:179], v[26:27] op_sel:[1,1] op_sel_hi:[0,1] neg_lo:[0,1]
	v_pk_fma_f32 v[22:23], v[178:179], v[26:27], v[22:23] op_sel_hi:[1,0,1]
	s_nop 0
	v_pk_mul_f32 v[26:27], v[38:39], v[22:23] op_sel:[1,1] op_sel_hi:[1,0] neg_lo:[1,0]
	v_add_u32_e32 v13, 0x19c80, v10
	v_pk_fma_f32 v[26:27], v[38:39], v[22:23], v[26:27] op_sel_hi:[0,1,1]
	ds_write_b64 v13, v[26:27]
	v_pk_mul_f32 v[26:27], v[178:179], v[22:23] op_sel:[1,1] op_sel_hi:[0,1] neg_lo:[0,1]
	v_pk_fma_f32 v[22:23], v[178:179], v[22:23], v[26:27] op_sel_hi:[1,0,1]
	s_nop 0
	v_pk_mul_f32 v[26:27], v[24:25], v[22:23] op_sel:[1,1] op_sel_hi:[1,0] neg_lo:[1,0]
	v_add_u32_e32 v13, 0x1ad00, v10
	v_pk_fma_f32 v[24:25], v[24:25], v[22:23], v[26:27] op_sel_hi:[0,1,1]
	ds_write_b64 v13, v[24:25]
	v_pk_mul_f32 v[24:25], v[178:179], v[22:23] op_sel:[1,1] op_sel_hi:[0,1] neg_lo:[0,1]
	v_pk_fma_f32 v[22:23], v[178:179], v[22:23], v[24:25] op_sel_hi:[1,0,1]
	s_nop 0
	v_pk_mul_f32 v[24:25], v[42:43], v[22:23] op_sel:[1,1] op_sel_hi:[1,0] neg_lo:[1,0]
	v_add_u32_e32 v13, 0x1bd80, v10
	v_pk_fma_f32 v[24:25], v[42:43], v[22:23], v[24:25] op_sel_hi:[0,1,1]
	ds_write_b64 v13, v[24:25]
	v_pk_mul_f32 v[24:25], v[178:179], v[22:23] op_sel:[1,1] op_sel_hi:[0,1] neg_lo:[0,1]
	v_pk_fma_f32 v[22:23], v[178:179], v[22:23], v[24:25] op_sel_hi:[1,0,1]
	s_nop 0
	v_pk_mul_f32 v[24:25], v[18:19], v[22:23] op_sel:[1,1] op_sel_hi:[1,0] neg_lo:[1,0]
	v_add_u32_e32 v13, 0x1ce00, v10
	v_pk_fma_f32 v[18:19], v[18:19], v[22:23], v[24:25] op_sel_hi:[0,1,1]
	ds_write_b64 v13, v[18:19]
	v_pk_mul_f32 v[18:19], v[178:179], v[22:23] op_sel:[1,1] op_sel_hi:[0,1] neg_lo:[0,1]
	v_pk_fma_f32 v[18:19], v[178:179], v[22:23], v[18:19] op_sel_hi:[1,0,1]
	s_nop 0
	v_pk_mul_f32 v[22:23], v[32:33], v[18:19] op_sel:[1,1] op_sel_hi:[1,0] neg_lo:[1,0]
	v_add_u32_e32 v13, 0x1de80, v10
	v_pk_fma_f32 v[22:23], v[32:33], v[18:19], v[22:23] op_sel_hi:[0,1,1]
	ds_write_b64 v13, v[22:23]
	v_pk_mul_f32 v[22:23], v[178:179], v[18:19] op_sel:[1,1] op_sel_hi:[0,1] neg_lo:[0,1]
	v_pk_fma_f32 v[18:19], v[178:179], v[18:19], v[22:23] op_sel_hi:[1,0,1]
	s_nop 0
	v_pk_mul_f32 v[22:23], v[20:21], v[18:19] op_sel:[1,1] op_sel_hi:[1,0] neg_lo:[1,0]
	v_add_u32_e32 v13, 0x1ef00, v10
	v_pk_fma_f32 v[20:21], v[20:21], v[18:19], v[22:23] op_sel_hi:[0,1,1]
	ds_write_b64 v13, v[20:21]
	v_pk_mul_f32 v[20:21], v[178:179], v[18:19] op_sel:[1,1] op_sel_hi:[0,1] neg_lo:[0,1]
	v_pk_fma_f32 v[16:17], v[178:179], v[18:19], v[20:21] op_sel_hi:[1,0,1]
	s_nop 0
	v_pk_mul_f32 v[18:19], v[36:37], v[16:17] op_sel:[1,1] op_sel_hi:[1,0] neg_lo:[1,0]
	v_add_u32_e32 v10, 0x1ff80, v10
	v_pk_fma_f32 v[16:17], v[36:37], v[16:17], v[18:19] op_sel_hi:[0,1,1]
	ds_write_b64 v10, v[16:17]
	v_mov_b32_e32 v10, v174
	v_mov_b32_e32 v13, v172
	s_waitcnt lgkmcnt(0)
	s_barrier
	v_mov_b32_e32 v16, v180
	v_add_u32_e32 v15, v13, v10
	v_lshl_add_u32 v75, v15, 3, 0
	v_xad_u32 v15, v13, 1, v10
	v_lshl_add_u32 v74, v15, 3, 0
	v_xad_u32 v15, v13, 2, v10
	v_lshl_add_u32 v73, v15, 3, 0
	v_xad_u32 v15, v13, 3, v10
	v_lshl_add_u32 v72, v15, 3, 0
	v_xad_u32 v15, v13, 4, v10
	v_lshl_add_u32 v71, v15, 3, 0
	v_xad_u32 v15, v13, 5, v10
	v_lshl_add_u32 v70, v15, 3, 0
	v_xad_u32 v15, v13, 6, v10
	v_lshl_add_u32 v69, v15, 3, 0
	v_xad_u32 v15, v13, 7, v10
	v_lshl_add_u32 v68, v15, 3, 0
	v_xad_u32 v15, v13, 8, v10
	v_lshl_add_u32 v15, v15, 3, 0
	v_add_u32_e32 v67, 0x800, v15
	v_xad_u32 v15, v13, 9, v10
	v_lshl_add_u32 v15, v15, 3, 0
	v_add_u32_e32 v66, 0x800, v15
	v_xad_u32 v15, v13, 10, v10
	v_lshl_add_u32 v15, v15, 3, 0
	v_add_u32_e32 v65, 0x800, v15
	v_xad_u32 v15, v13, 11, v10
	v_lshl_add_u32 v15, v15, 3, 0
	v_add_u32_e32 v64, 0x800, v15
	v_xad_u32 v15, v13, 12, v10
	v_mov_b32_e32 v17, v181
	v_lshl_add_u32 v15, v15, 3, 0
	ds_read2_b64 v[18:21], v75 offset1:16
	ds_read2_b64 v[40:43], v67 offset1:16
	v_add_u32_e32 v63, 0x800, v15
	v_xad_u32 v15, v13, 13, v10
	v_lshl_add_u32 v15, v15, 3, 0
	v_add_u32_e32 v62, 0x800, v15
	v_xad_u32 v15, v13, 14, v10
	v_xad_u32 v10, v13, 15, v10
	ds_read2_b64 v[22:25], v74 offset0:32 offset1:48
	ds_read2_b64 v[48:51], v66 offset0:32 offset1:48
	v_lshl_add_u32 v15, v15, 3, 0
	v_lshl_add_u32 v10, v10, 3, 0
	v_add_u32_e32 v15, 0x800, v15
	v_add_u32_e32 v13, 0x800, v10
	v_mov_b32_e32 v10, v1
	ds_read2_b64 v[26:29], v73 offset0:64 offset1:80
	ds_read2_b64 v[58:61], v72 offset0:96 offset1:112
	ds_read2_b64 v[76:79], v71 offset0:128 offset1:144
	ds_read2_b64 v[80:83], v70 offset0:160 offset1:176
	ds_read2_b64 v[84:87], v69 offset0:192 offset1:208
	ds_read2_b64 v[88:91], v68 offset0:224 offset1:240
	ds_read2_b64 v[54:57], v65 offset0:64 offset1:80
	ds_read2_b64 v[92:95], v64 offset0:96 offset1:112
	ds_read2_b64 v[96:99], v63 offset0:128 offset1:144
	ds_read2_b64 v[100:103], v62 offset0:160 offset1:176
	ds_read2_b64 v[104:107], v15 offset0:192 offset1:208
	ds_read2_b64 v[108:111], v13 offset0:224 offset1:240
	s_waitcnt lgkmcnt(14)
	v_pk_add_f32 v[112:113], v[18:19], v[40:41]
	v_pk_add_f32 v[40:41], v[18:19], v[40:41] neg_lo:[0,1] neg_hi:[0,1]
	v_pk_add_f32 v[18:19], v[20:21], v[42:43]
	v_pk_add_f32 v[20:21], v[20:21], v[42:43] neg_lo:[0,1] neg_hi:[0,1]
	v_mov_b32_e32 v30, v164
	v_mov_b32_e32 v32, v165
	v_mov_b32_e32 v34, v166
	v_mov_b32_e32 v10, v167
	v_mov_b32_e32 v38, v168
	v_mov_b32_e32 v36, v169
	v_mov_b32_e32 v46, v170
	v_mov_b32_e32 v31, v171
	v_pk_mul_f32 v[42:43], v[20:21], v[46:47] op_sel:[1,0] op_sel_hi:[0,0] neg_lo:[1,1] neg_hi:[0,1]
	s_nop 0
	v_pk_fma_f32 v[44:45], v[20:21], v[30:31], v[42:43] op_sel_hi:[1,0,1]
	s_waitcnt lgkmcnt(12)
	v_pk_add_f32 v[20:21], v[22:23], v[48:49]
	v_pk_add_f32 v[22:23], v[22:23], v[48:49] neg_lo:[0,1] neg_hi:[0,1]
	s_nop 0
	v_pk_mul_f32 v[42:43], v[22:23], v[36:37] op_sel:[1,0] op_sel_hi:[0,0] neg_lo:[1,1] neg_hi:[0,1]
	s_nop 0
	v_pk_fma_f32 v[48:49], v[22:23], v[32:33], v[42:43] op_sel_hi:[1,0,1]
	v_pk_add_f32 v[22:23], v[24:25], v[50:51]
	v_pk_add_f32 v[24:25], v[24:25], v[50:51] neg_lo:[0,1] neg_hi:[0,1]
	s_nop 0
	v_pk_mul_f32 v[42:43], v[24:25], v[38:39] op_sel:[1,0] op_sel_hi:[0,0] neg_lo:[1,1] neg_hi:[0,1]
	s_nop 0
	v_pk_fma_f32 v[52:53], v[24:25], v[34:35], v[42:43] op_sel_hi:[1,0,1]
	s_waitcnt lgkmcnt(5)
	v_pk_add_f32 v[24:25], v[26:27], v[54:55]
	v_pk_add_f32 v[26:27], v[26:27], v[54:55] neg_lo:[0,1] neg_hi:[0,1]
	s_nop 0
	v_pk_mul_f32 v[42:43], v[26:27], v[10:11] op_sel:[1,0] op_sel_hi:[0,0] neg_lo:[1,1] neg_hi:[0,1]
	s_nop 0
	v_pk_fma_f32 v[54:55], v[26:27], v[10:11], v[42:43] op_sel_hi:[1,0,1]
	v_pk_add_f32 v[26:27], v[28:29], v[56:57]
	v_pk_add_f32 v[28:29], v[28:29], v[56:57] neg_lo:[0,1] neg_hi:[0,1]
	s_nop 0
	v_pk_mul_f32 v[42:43], v[28:29], v[38:39] op_sel_hi:[1,0]
	s_nop 0
	v_pk_fma_f32 v[56:57], v[28:29], v[34:35], v[42:43] op_sel:[1,0,0] op_sel_hi:[0,0,1] neg_lo:[1,1,0] neg_hi:[0,1,0]
	s_waitcnt lgkmcnt(4)
	v_pk_add_f32 v[42:43], v[58:59], v[92:93] neg_lo:[0,1] neg_hi:[0,1]
	v_pk_add_f32 v[28:29], v[58:59], v[92:93]
	v_pk_mul_f32 v[50:51], v[42:43], v[36:37] op_sel_hi:[1,0]
	s_nop 0
	v_pk_fma_f32 v[58:59], v[42:43], v[32:33], v[50:51] op_sel:[1,0,0] op_sel_hi:[0,0,1] neg_lo:[1,1,0] neg_hi:[0,1,0]
	v_pk_add_f32 v[50:51], v[60:61], v[94:95] neg_lo:[0,1] neg_hi:[0,1]
	v_pk_add_f32 v[42:43], v[60:61], v[94:95]
	v_pk_mul_f32 v[60:61], v[50:51], v[46:47] op_sel_hi:[1,0]
	v_xor_b32_e32 v92, 0x80000000, v51
	v_mov_b32_e32 v93, v50
	s_waitcnt lgkmcnt(3)
	v_pk_add_f32 v[50:51], v[76:77], v[96:97]
	v_pk_add_f32 v[76:77], v[76:77], v[96:97] neg_lo:[0,1] neg_hi:[0,1]
	v_pk_fma_f32 v[60:61], v[92:93], v[30:31], v[60:61] op_sel_hi:[1,0,1] neg_lo:[0,1,0] neg_hi:[0,1,0]
	v_xor_b32_e32 v93, 0x80000000, v76
	v_mov_b32_e32 v92, v77
	v_pk_add_f32 v[76:77], v[78:79], v[98:99]
	v_pk_add_f32 v[78:79], v[78:79], v[98:99] neg_lo:[0,1] neg_hi:[0,1]
	s_nop 0
	v_pk_mul_f32 v[94:95], v[78:79], v[46:47] op_sel_hi:[1,0] neg_lo:[0,1] neg_hi:[0,1]
	s_nop 0
	v_pk_fma_f32 v[78:79], v[78:79], v[30:31], v[94:95] op_sel:[1,0,0] op_sel_hi:[0,0,1] neg_lo:[1,1,0] neg_hi:[0,1,0]
	s_waitcnt lgkmcnt(2)
	v_pk_add_f32 v[94:95], v[80:81], v[100:101]
	v_pk_add_f32 v[80:81], v[80:81], v[100:101] neg_lo:[0,1] neg_hi:[0,1]
	s_nop 0
	v_pk_mul_f32 v[96:97], v[80:81], v[36:37] op_sel_hi:[1,0] neg_lo:[0,1] neg_hi:[0,1]
	s_nop 0
	v_pk_fma_f32 v[80:81], v[80:81], v[32:33], v[96:97] op_sel:[1,0,0] op_sel_hi:[0,0,1] neg_lo:[1,1,0] neg_hi:[0,1,0]
	v_pk_add_f32 v[96:97], v[82:83], v[102:103]
	v_pk_add_f32 v[82:83], v[82:83], v[102:103] neg_lo:[0,1] neg_hi:[0,1]
	s_nop 0
	v_pk_mul_f32 v[98:99], v[82:83], v[38:39] op_sel_hi:[1,0] neg_lo:[0,1] neg_hi:[0,1]
	s_nop 0
	v_pk_fma_f32 v[82:83], v[82:83], v[34:35], v[98:99] op_sel:[1,0,0] op_sel_hi:[0,0,1] neg_lo:[1,1,0] neg_hi:[0,1,0]
	s_waitcnt lgkmcnt(1)
	v_pk_add_f32 v[98:99], v[84:85], v[104:105]
	v_pk_add_f32 v[84:85], v[84:85], v[104:105] neg_lo:[0,1] neg_hi:[0,1]
	s_nop 0
	v_pk_mul_f32 v[100:101], v[84:85], v[10:11] op_sel:[1,0] op_sel_hi:[0,0] neg_lo:[1,1] neg_hi:[0,1]
	s_nop 0
	v_pk_fma_f32 v[84:85], v[84:85], v[10:11], v[100:101] op_sel_hi:[1,0,1] neg_lo:[0,1,0] neg_hi:[0,1,0]
	v_pk_add_f32 v[100:101], v[86:87], v[106:107]
	v_pk_add_f32 v[86:87], v[86:87], v[106:107] neg_lo:[0,1] neg_hi:[0,1]
	s_nop 0
	v_pk_mul_f32 v[38:39], v[86:87], v[38:39] op_sel:[1,0] op_sel_hi:[0,0] neg_lo:[1,1] neg_hi:[0,1]
	s_nop 0
	v_pk_fma_f32 v[86:87], v[86:87], v[34:35], v[38:39] op_sel_hi:[1,0,1] neg_lo:[0,1,0] neg_hi:[0,1,0]
	s_waitcnt lgkmcnt(0)
	v_pk_add_f32 v[38:39], v[88:89], v[108:109] neg_lo:[0,1] neg_hi:[0,1]
	v_pk_add_f32 v[34:35], v[88:89], v[108:109]
	v_pk_mul_f32 v[88:89], v[38:39], v[36:37] op_sel:[1,0] op_sel_hi:[0,0] neg_lo:[1,1] neg_hi:[0,1]
	s_nop 0
	v_pk_fma_f32 v[88:89], v[38:39], v[32:33], v[88:89] op_sel_hi:[1,0,1] neg_lo:[0,1,0] neg_hi:[0,1,0]
	v_pk_add_f32 v[38:39], v[90:91], v[110:111]
	v_pk_add_f32 v[90:91], v[90:91], v[110:111] neg_lo:[0,1] neg_hi:[0,1]
	s_nop 0
	v_pk_mul_f32 v[46:47], v[90:91], v[46:47] op_sel:[1,0] op_sel_hi:[0,0] neg_lo:[1,1] neg_hi:[0,1]
	s_nop 0
	v_pk_fma_f32 v[90:91], v[90:91], v[30:31], v[46:47] op_sel_hi:[1,0,1] neg_lo:[0,1,0] neg_hi:[0,1,0]
	v_pk_add_f32 v[46:47], v[18:19], v[76:77]
	v_pk_add_f32 v[18:19], v[18:19], v[76:77] neg_lo:[0,1] neg_hi:[0,1]
	v_pk_add_f32 v[30:31], v[112:113], v[50:51]
	v_pk_mul_f32 v[76:77], v[18:19], v[36:37] op_sel:[1,0] op_sel_hi:[0,0] neg_lo:[1,1] neg_hi:[0,1]
	v_pk_add_f32 v[50:51], v[112:113], v[50:51] neg_lo:[0,1] neg_hi:[0,1]
	v_pk_fma_f32 v[76:77], v[18:19], v[32:33], v[76:77] op_sel_hi:[1,0,1]
	v_pk_add_f32 v[18:19], v[20:21], v[94:95]
	v_pk_add_f32 v[20:21], v[20:21], v[94:95] neg_lo:[0,1] neg_hi:[0,1]
	s_nop 0
	v_pk_mul_f32 v[94:95], v[20:21], v[10:11] op_sel:[1,0] op_sel_hi:[0,0] neg_lo:[1,1] neg_hi:[0,1]
	s_nop 0
	v_pk_fma_f32 v[20:21], v[20:21], v[10:11], v[94:95] op_sel_hi:[1,0,1]
	v_pk_add_f32 v[94:95], v[22:23], v[96:97]
	v_pk_add_f32 v[22:23], v[22:23], v[96:97] neg_lo:[0,1] neg_hi:[0,1]
	s_nop 0
	v_pk_mul_f32 v[96:97], v[22:23], v[36:37] op_sel_hi:[1,0]
	v_xor_b32_e32 v102, 0x80000000, v23
	v_mov_b32_e32 v103, v22
	v_pk_add_f32 v[22:23], v[24:25], v[98:99]
	v_pk_add_f32 v[24:25], v[24:25], v[98:99] neg_lo:[0,1] neg_hi:[0,1]
	v_pk_fma_f32 v[96:97], v[102:103], v[32:33], v[96:97] op_sel_hi:[1,0,1] neg_lo:[0,1,0] neg_hi:[0,1,0]
	v_xor_b32_e32 v99, 0x80000000, v24
	v_mov_b32_e32 v98, v25
	v_pk_add_f32 v[24:25], v[26:27], v[100:101]
	v_pk_add_f32 v[26:27], v[26:27], v[100:101] neg_lo:[0,1] neg_hi:[0,1]
	s_nop 0
	v_pk_mul_f32 v[100:101], v[26:27], v[36:37] op_sel_hi:[1,0] neg_lo:[0,1] neg_hi:[0,1]
	v_xor_b32_e32 v102, 0x80000000, v27
	v_mov_b32_e32 v103, v26
	v_pk_add_f32 v[26:27], v[28:29], v[34:35]
	v_pk_add_f32 v[28:29], v[28:29], v[34:35] neg_lo:[0,1] neg_hi:[0,1]
	v_pk_fma_f32 v[100:101], v[102:103], v[32:33], v[100:101] op_sel_hi:[1,0,1] neg_lo:[0,1,0] neg_hi:[0,1,0]
	v_pk_mul_f32 v[34:35], v[28:29], v[10:11] op_sel:[1,0] op_sel_hi:[0,0] neg_lo:[1,1] neg_hi:[0,1]
	v_pk_add_f32 v[102:103], v[30:31], v[22:23] neg_lo:[0,1] neg_hi:[0,1]
	v_pk_fma_f32 v[28:29], v[28:29], v[10:11], v[34:35] op_sel_hi:[1,0,1] neg_lo:[0,1,0] neg_hi:[0,1,0]
	v_pk_add_f32 v[34:35], v[42:43], v[38:39]
	v_pk_add_f32 v[38:39], v[42:43], v[38:39] neg_lo:[0,1] neg_hi:[0,1]
	s_nop 0
	v_pk_mul_f32 v[42:43], v[38:39], v[36:37] op_sel:[1,0] op_sel_hi:[0,0] neg_lo:[1,1] neg_hi:[0,1]
	s_nop 0
	v_pk_fma_f32 v[42:43], v[38:39], v[32:33], v[42:43] op_sel_hi:[1,0,1] neg_lo:[0,1,0] neg_hi:[0,1,0]
	v_pk_add_f32 v[38:39], v[30:31], v[22:23]
	v_pk_add_f32 v[22:23], v[46:47], v[24:25]
	v_pk_add_f32 v[24:25], v[46:47], v[24:25] neg_lo:[0,1] neg_hi:[0,1]
	s_nop 0
	v_pk_mul_f32 v[30:31], v[24:25], v[10:11] op_sel:[1,0] op_sel_hi:[0,0] neg_lo:[1,1] neg_hi:[0,1]
	s_nop 0
	v_pk_fma_f32 v[24:25], v[24:25], v[10:11], v[30:31] op_sel_hi:[1,0,1]
	v_pk_add_f32 v[30:31], v[18:19], v[26:27]
	v_pk_add_f32 v[18:19], v[18:19], v[26:27] neg_lo:[0,1] neg_hi:[0,1]
	s_nop 0
	v_xor_b32_e32 v27, 0x80000000, v18
	v_mov_b32_e32 v26, v19
	v_pk_add_f32 v[18:19], v[94:95], v[34:35]
	v_pk_add_f32 v[34:35], v[94:95], v[34:35] neg_lo:[0,1] neg_hi:[0,1]
	s_nop 0
	v_pk_mul_f32 v[46:47], v[34:35], v[10:11] op_sel:[1,0] op_sel_hi:[0,0] neg_lo:[1,1] neg_hi:[0,1]
	s_nop 0
	v_pk_fma_f32 v[34:35], v[34:35], v[10:11], v[46:47] op_sel_hi:[1,0,1] neg_lo:[0,1,0] neg_hi:[0,1,0]
	v_pk_add_f32 v[46:47], v[38:39], v[30:31]
	v_pk_add_f32 v[38:39], v[38:39], v[30:31] neg_lo:[0,1] neg_hi:[0,1]
	v_pk_add_f32 v[30:31], v[22:23], v[18:19]
	v_pk_add_f32 v[18:19], v[22:23], v[18:19] neg_lo:[0,1] neg_hi:[0,1]
	v_pk_add_f32 v[94:95], v[46:47], v[30:31]
	v_xor_b32_e32 v23, 0x80000000, v18
	v_mov_b32_e32 v22, v19
	v_pk_add_f32 v[18:19], v[102:103], v[26:27]
	v_pk_add_f32 v[102:103], v[102:103], v[26:27] neg_lo:[0,1] neg_hi:[0,1]
	v_pk_add_f32 v[26:27], v[24:25], v[34:35]
	v_pk_add_f32 v[24:25], v[24:25], v[34:35] neg_lo:[0,1] neg_hi:[0,1]
	v_pk_add_f32 v[30:31], v[46:47], v[30:31] neg_lo:[0,1] neg_hi:[0,1]
	v_xor_b32_e32 v35, 0x80000000, v24
	v_mov_b32_e32 v34, v25
	v_pk_add_f32 v[24:25], v[50:51], v[98:99]
	v_pk_add_f32 v[98:99], v[50:51], v[98:99] neg_lo:[0,1] neg_hi:[0,1]
	v_pk_add_f32 v[50:51], v[76:77], v[100:101] neg_lo:[0,1] neg_hi:[0,1]
	v_pk_add_f32 v[46:47], v[38:39], v[22:23]
	v_pk_add_f32 v[22:23], v[38:39], v[22:23] neg_lo:[0,1] neg_hi:[0,1]
	v_pk_add_f32 v[104:105], v[18:19], v[26:27]
	v_pk_add_f32 v[26:27], v[18:19], v[26:27] neg_lo:[0,1] neg_hi:[0,1]
	v_pk_add_f32 v[38:39], v[102:103], v[34:35]
	v_pk_add_f32 v[18:19], v[102:103], v[34:35] neg_lo:[0,1] neg_hi:[0,1]
	v_pk_add_f32 v[34:35], v[76:77], v[100:101]
	v_pk_mul_f32 v[76:77], v[10:11], v[50:51] op_sel:[0,1] op_sel_hi:[0,0] neg_lo:[1,1] neg_hi:[1,0]
	v_pk_fma_f32 v[76:77], v[10:11], v[50:51], v[76:77] op_sel_hi:[0,1,1]
	v_pk_add_f32 v[50:51], v[20:21], v[28:29]
	v_pk_add_f32 v[20:21], v[20:21], v[28:29] neg_lo:[0,1] neg_hi:[0,1]
	s_nop 0
	v_xor_b32_e32 v29, 0x80000000, v20
	v_mov_b32_e32 v28, v21
	v_pk_add_f32 v[20:21], v[96:97], v[42:43]
	v_pk_add_f32 v[42:43], v[96:97], v[42:43] neg_lo:[0,1] neg_hi:[0,1]
	s_nop 0
	v_pk_mul_f32 v[96:97], v[10:11], v[42:43] op_sel:[0,1] op_sel_hi:[0,0] neg_lo:[1,1] neg_hi:[1,0]
	v_pk_fma_f32 v[42:43], v[10:11], v[42:43], v[96:97] op_sel_hi:[0,1,1] neg_lo:[1,0,0] neg_hi:[1,0,0]
	v_pk_add_f32 v[96:97], v[24:25], v[50:51]
	v_pk_add_f32 v[24:25], v[24:25], v[50:51] neg_lo:[0,1] neg_hi:[0,1]
	v_pk_add_f32 v[50:51], v[34:35], v[20:21]
	v_pk_add_f32 v[20:21], v[34:35], v[20:21] neg_lo:[0,1] neg_hi:[0,1]
	v_pk_add_f32 v[102:103], v[96:97], v[50:51]
	v_xor_b32_e32 v101, 0x80000000, v20
	v_mov_b32_e32 v100, v21
	v_pk_add_f32 v[34:35], v[96:97], v[50:51] neg_lo:[0,1] neg_hi:[0,1]
	v_pk_add_f32 v[20:21], v[98:99], v[28:29]
	v_pk_add_f32 v[96:97], v[98:99], v[28:29] neg_lo:[0,1] neg_hi:[0,1]
	v_pk_add_f32 v[28:29], v[76:77], v[42:43]
	v_pk_add_f32 v[42:43], v[76:77], v[42:43] neg_lo:[0,1] neg_hi:[0,1]
	v_pk_add_f32 v[98:99], v[20:21], v[28:29]
	v_xor_b32_e32 v77, 0x80000000, v42
	v_mov_b32_e32 v76, v43
	v_pk_add_f32 v[28:29], v[20:21], v[28:29] neg_lo:[0,1] neg_hi:[0,1]
	v_pk_add_f32 v[42:43], v[96:97], v[76:77]
	v_pk_add_f32 v[20:21], v[96:97], v[76:77] neg_lo:[0,1] neg_hi:[0,1]
	v_pk_add_f32 v[76:77], v[40:41], v[92:93]
	v_pk_add_f32 v[92:93], v[40:41], v[92:93] neg_lo:[0,1] neg_hi:[0,1]
	v_pk_add_f32 v[40:41], v[44:45], v[78:79]
	v_pk_add_f32 v[44:45], v[44:45], v[78:79] neg_lo:[0,1] neg_hi:[0,1]
	v_pk_add_f32 v[50:51], v[24:25], v[100:101]
	v_pk_mul_f32 v[78:79], v[36:37], v[44:45] op_sel:[0,1] op_sel_hi:[0,0] neg_lo:[1,1] neg_hi:[1,0]
	v_pk_fma_f32 v[44:45], v[32:33], v[44:45], v[78:79] op_sel_hi:[0,1,1]
	v_pk_add_f32 v[78:79], v[48:49], v[80:81]
	v_pk_add_f32 v[48:49], v[48:49], v[80:81] neg_lo:[0,1] neg_hi:[0,1]
	v_pk_add_f32 v[24:25], v[24:25], v[100:101] neg_lo:[0,1] neg_hi:[0,1]
	v_pk_mul_f32 v[80:81], v[10:11], v[48:49] op_sel:[0,1] op_sel_hi:[0,0] neg_lo:[1,1] neg_hi:[1,0]
	v_pk_fma_f32 v[80:81], v[10:11], v[48:49], v[80:81] op_sel_hi:[0,1,1]
	v_pk_add_f32 v[48:49], v[52:53], v[82:83]
	v_pk_add_f32 v[52:53], v[52:53], v[82:83] neg_lo:[0,1] neg_hi:[0,1]
	s_nop 0
	v_pk_mul_f32 v[82:83], v[32:33], v[52:53] op_sel:[0,1] op_sel_hi:[0,0] neg_lo:[1,1] neg_hi:[1,0]
	v_pk_fma_f32 v[52:53], v[36:37], v[52:53], v[82:83] op_sel_hi:[0,1,1]
	v_pk_add_f32 v[82:83], v[54:55], v[84:85]
	v_pk_add_f32 v[54:55], v[54:55], v[84:85] neg_lo:[0,1] neg_hi:[0,1]
	s_nop 0
	v_xor_b32_e32 v85, 0x80000000, v54
	v_mov_b32_e32 v84, v55
	v_pk_add_f32 v[54:55], v[56:57], v[86:87]
	v_pk_add_f32 v[56:57], v[56:57], v[86:87] neg_lo:[0,1] neg_hi:[0,1]
	s_nop 0
	v_pk_mul_f32 v[86:87], v[32:33], v[56:57] op_sel:[0,1] op_sel_hi:[0,0] neg_lo:[1,1] neg_hi:[1,0]
	v_pk_fma_f32 v[56:57], v[36:37], v[56:57], v[86:87] op_sel_hi:[0,1,1] neg_lo:[1,0,0] neg_hi:[1,0,0]
	v_pk_add_f32 v[86:87], v[58:59], v[88:89]
	v_pk_add_f32 v[58:59], v[58:59], v[88:89] neg_lo:[0,1] neg_hi:[0,1]
	s_nop 0
	v_pk_mul_f32 v[88:89], v[10:11], v[58:59] op_sel:[0,1] op_sel_hi:[0,0] neg_lo:[1,1] neg_hi:[1,0]
	v_pk_fma_f32 v[58:59], v[10:11], v[58:59], v[88:89] op_sel_hi:[0,1,1] neg_lo:[1,0,0] neg_hi:[1,0,0]
	v_pk_add_f32 v[88:89], v[60:61], v[90:91]
	v_pk_add_f32 v[60:61], v[60:61], v[90:91] neg_lo:[0,1] neg_hi:[0,1]
	s_nop 0
	v_pk_mul_f32 v[36:37], v[36:37], v[60:61] op_sel:[0,1] op_sel_hi:[0,0] neg_lo:[1,1] neg_hi:[1,0]
	v_pk_fma_f32 v[36:37], v[32:33], v[60:61], v[36:37] op_sel_hi:[0,1,1] neg_lo:[1,0,0] neg_hi:[1,0,0]
	v_pk_add_f32 v[32:33], v[76:77], v[82:83]
	v_pk_add_f32 v[60:61], v[76:77], v[82:83] neg_lo:[0,1] neg_hi:[0,1]
	v_pk_add_f32 v[76:77], v[54:55], v[40:41]
	v_pk_add_f32 v[40:41], v[40:41], v[54:55] neg_lo:[0,1] neg_hi:[0,1]
	s_nop 0
	v_pk_mul_f32 v[54:55], v[10:11], v[40:41] op_sel:[0,1] op_sel_hi:[0,0] neg_lo:[1,1] neg_hi:[1,0]
	v_pk_fma_f32 v[54:55], v[10:11], v[40:41], v[54:55] op_sel_hi:[0,1,1]
	v_pk_add_f32 v[40:41], v[78:79], v[86:87]
	v_pk_add_f32 v[78:79], v[78:79], v[86:87] neg_lo:[0,1] neg_hi:[0,1]
	s_nop 0
	v_xor_b32_e32 v83, 0x80000000, v78
	v_mov_b32_e32 v82, v79
	v_pk_add_f32 v[78:79], v[48:49], v[88:89]
	v_pk_add_f32 v[48:49], v[48:49], v[88:89] neg_lo:[0,1] neg_hi:[0,1]
	v_pk_add_f32 v[88:89], v[76:77], v[78:79]
	v_pk_mul_f32 v[86:87], v[10:11], v[48:49] op_sel:[0,1] op_sel_hi:[0,0] neg_lo:[1,1] neg_hi:[1,0]
	v_pk_fma_f32 v[48:49], v[10:11], v[48:49], v[86:87] op_sel_hi:[0,1,1] neg_lo:[1,0,0] neg_hi:[1,0,0]
	v_pk_add_f32 v[86:87], v[32:33], v[40:41]
	v_pk_add_f32 v[32:33], v[32:33], v[40:41] neg_lo:[0,1] neg_hi:[0,1]
	v_pk_add_f32 v[40:41], v[76:77], v[78:79] neg_lo:[0,1] neg_hi:[0,1]
	v_pk_add_f32 v[78:79], v[86:87], v[88:89] neg_lo:[0,1] neg_hi:[0,1]
	v_pk_add_f32 v[90:91], v[32:33], v[40:41] op_sel:[0,1] op_sel_hi:[1,0] neg_hi:[0,1]
	v_pk_add_f32 v[40:41], v[32:33], v[40:41] op_sel:[0,1] op_sel_hi:[1,0] neg_lo:[0,1]
	v_pk_add_f32 v[76:77], v[54:55], v[48:49]
	v_pk_add_f32 v[48:49], v[54:55], v[48:49] neg_lo:[0,1] neg_hi:[0,1]
	v_pk_add_f32 v[32:33], v[60:61], v[82:83]
	v_pk_add_f32 v[60:61], v[60:61], v[82:83] neg_lo:[0,1] neg_hi:[0,1]
	v_xor_b32_e32 v55, 0x80000000, v48
	v_mov_b32_e32 v54, v49
	v_pk_add_f32 v[82:83], v[32:33], v[76:77]
	v_pk_add_f32 v[48:49], v[32:33], v[76:77] neg_lo:[0,1] neg_hi:[0,1]
	v_pk_add_f32 v[76:77], v[60:61], v[54:55]
	v_pk_add_f32 v[32:33], v[60:61], v[54:55] neg_lo:[0,1] neg_hi:[0,1]
	v_pk_add_f32 v[54:55], v[92:93], v[84:85]
	v_pk_add_f32 v[60:61], v[92:93], v[84:85] neg_lo:[0,1] neg_hi:[0,1]
	v_pk_add_f32 v[84:85], v[56:57], v[44:45]
	v_pk_add_f32 v[44:45], v[44:45], v[56:57] neg_lo:[0,1] neg_hi:[0,1]
	v_pk_add_f32 v[86:87], v[86:87], v[88:89]
	v_pk_mul_f32 v[56:57], v[10:11], v[44:45] op_sel:[0,1] op_sel_hi:[0,0] neg_lo:[1,1] neg_hi:[1,0]
	v_pk_fma_f32 v[56:57], v[10:11], v[44:45], v[56:57] op_sel_hi:[0,1,1]
	v_pk_add_f32 v[44:45], v[80:81], v[58:59]
	v_pk_add_f32 v[58:59], v[80:81], v[58:59] neg_lo:[0,1] neg_hi:[0,1]
	s_nop 0
	v_xor_b32_e32 v81, 0x80000000, v58
	v_mov_b32_e32 v80, v59
	v_pk_add_f32 v[58:59], v[52:53], v[36:37]
	v_pk_add_f32 v[36:37], v[52:53], v[36:37] neg_lo:[0,1] neg_hi:[0,1]
	s_nop 0
	v_pk_mul_f32 v[52:53], v[10:11], v[36:37] op_sel:[0,1] op_sel_hi:[0,0] neg_lo:[1,1] neg_hi:[1,0]
	v_pk_fma_f32 v[36:37], v[10:11], v[36:37], v[52:53] op_sel_hi:[0,1,1] neg_lo:[1,0,0] neg_hi:[1,0,0]
	v_pk_add_f32 v[52:53], v[54:55], v[44:45]
	v_pk_add_f32 v[44:45], v[54:55], v[44:45] neg_lo:[0,1] neg_hi:[0,1]
	v_pk_add_f32 v[54:55], v[84:85], v[58:59]
	v_pk_add_f32 v[58:59], v[84:85], v[58:59] neg_lo:[0,1] neg_hi:[0,1]
	s_nop 0
	v_xor_b32_e32 v85, 0x80000000, v58
	v_mov_b32_e32 v84, v59
	v_pk_add_f32 v[58:59], v[52:53], v[54:55]
	v_pk_add_f32 v[52:53], v[52:53], v[54:55] neg_lo:[0,1] neg_hi:[0,1]
	v_pk_add_f32 v[54:55], v[44:45], v[84:85]
	v_pk_add_f32 v[44:45], v[44:45], v[84:85] neg_lo:[0,1] neg_hi:[0,1]
	v_pk_add_f32 v[84:85], v[60:61], v[80:81]
	v_pk_add_f32 v[60:61], v[60:61], v[80:81] neg_lo:[0,1] neg_hi:[0,1]
	v_pk_add_f32 v[80:81], v[56:57], v[36:37]
	v_pk_add_f32 v[36:37], v[56:57], v[36:37] neg_lo:[0,1] neg_hi:[0,1]
	v_pk_add_f32 v[92:93], v[84:85], v[80:81]
	v_pk_add_f32 v[80:81], v[84:85], v[80:81] neg_lo:[0,1] neg_hi:[0,1]
	v_pk_add_f32 v[84:85], v[60:61], v[36:37] op_sel:[0,1] op_sel_hi:[1,0] neg_hi:[0,1]
	v_pk_add_f32 v[36:37], v[60:61], v[36:37] op_sel:[0,1] op_sel_hi:[1,0] neg_lo:[0,1]
	v_pk_fma_f32 v[60:61], v[16:17], s[90:91], v[16:17] op_sel:[1,0,0] op_sel_hi:[0,1,1]
	v_pk_mul_f32 v[56:57], v[94:95], s[14:15] op_sel:[1,0] neg_lo:[1,0]
	v_pk_mul_f32 v[88:89], v[60:61], v[86:87] op_sel:[1,1] op_sel_hi:[0,1] neg_lo:[0,1]
	v_pk_fma_f32 v[56:57], v[94:95], s[94:95], v[56:57] op_sel_hi:[0,1,1]
	v_pk_fma_f32 v[86:87], v[60:61], v[86:87], v[88:89] op_sel_hi:[1,0,1]
	ds_write2_b64 v75, v[56:57], v[86:87] offset1:16
	v_pk_mul_f32 v[56:57], v[16:17], v[60:61] op_sel:[1,1] op_sel_hi:[0,1] neg_lo:[0,1]
	v_pk_fma_f32 v[56:57], v[16:17], v[60:61], v[56:57] op_sel_hi:[1,0,1]
	s_nop 0
	v_pk_mul_f32 v[60:61], v[56:57], v[102:103] op_sel:[1,1] op_sel_hi:[0,1] neg_lo:[0,1]
	v_pk_mul_f32 v[86:87], v[16:17], v[56:57] op_sel:[1,1] op_sel_hi:[0,1] neg_lo:[0,1]
	v_pk_fma_f32 v[60:61], v[56:57], v[102:103], v[60:61] op_sel_hi:[1,0,1]
	v_pk_fma_f32 v[56:57], v[16:17], v[56:57], v[86:87] op_sel_hi:[1,0,1]
	s_nop 0
	v_pk_mul_f32 v[86:87], v[56:57], v[58:59] op_sel:[1,1] op_sel_hi:[0,1] neg_lo:[0,1]
	v_pk_fma_f32 v[58:59], v[56:57], v[58:59], v[86:87] op_sel_hi:[1,0,1]
	ds_write2_b64 v74, v[60:61], v[58:59] offset0:32 offset1:48
	v_pk_mul_f32 v[58:59], v[16:17], v[56:57] op_sel:[1,1] op_sel_hi:[0,1] neg_lo:[0,1]
	v_pk_fma_f32 v[56:57], v[16:17], v[56:57], v[58:59] op_sel_hi:[1,0,1]
	s_nop 0
	v_pk_mul_f32 v[58:59], v[56:57], v[104:105] op_sel:[1,1] op_sel_hi:[0,1] neg_lo:[0,1]
	v_pk_mul_f32 v[60:61], v[16:17], v[56:57] op_sel:[1,1] op_sel_hi:[0,1] neg_lo:[0,1]
	v_pk_fma_f32 v[58:59], v[56:57], v[104:105], v[58:59] op_sel_hi:[1,0,1]
	v_pk_fma_f32 v[56:57], v[16:17], v[56:57], v[60:61] op_sel_hi:[1,0,1]
	s_nop 0
	v_pk_mul_f32 v[60:61], v[56:57], v[82:83] op_sel:[1,1] op_sel_hi:[0,1] neg_lo:[0,1]
	v_pk_fma_f32 v[60:61], v[56:57], v[82:83], v[60:61] op_sel_hi:[1,0,1]
	ds_write2_b64 v73, v[58:59], v[60:61] offset0:64 offset1:80
	v_pk_mul_f32 v[58:59], v[16:17], v[56:57] op_sel:[1,1] op_sel_hi:[0,1] neg_lo:[0,1]
	v_pk_fma_f32 v[56:57], v[16:17], v[56:57], v[58:59] op_sel_hi:[1,0,1]
	s_nop 0
	v_pk_mul_f32 v[58:59], v[56:57], v[98:99] op_sel:[1,1] op_sel_hi:[0,1] neg_lo:[0,1]
	v_pk_mul_f32 v[60:61], v[16:17], v[56:57] op_sel:[1,1] op_sel_hi:[0,1] neg_lo:[0,1]
	v_pk_fma_f32 v[58:59], v[56:57], v[98:99], v[58:59] op_sel_hi:[1,0,1]
	v_pk_fma_f32 v[56:57], v[16:17], v[56:57], v[60:61] op_sel_hi:[1,0,1]
	s_nop 0
	v_pk_mul_f32 v[60:61], v[56:57], v[92:93] op_sel:[1,1] op_sel_hi:[0,1] neg_lo:[0,1]
	v_pk_fma_f32 v[60:61], v[56:57], v[92:93], v[60:61] op_sel_hi:[1,0,1]
	ds_write2_b64 v72, v[58:59], v[60:61] offset0:96 offset1:112
	v_pk_mul_f32 v[58:59], v[16:17], v[56:57] op_sel:[1,1] op_sel_hi:[0,1] neg_lo:[0,1]
	v_pk_fma_f32 v[56:57], v[16:17], v[56:57], v[58:59] op_sel_hi:[1,0,1]
	s_nop 0
	v_pk_mul_f32 v[58:59], v[56:57], v[46:47] op_sel:[1,1] op_sel_hi:[0,1] neg_lo:[0,1]
	v_pk_fma_f32 v[46:47], v[56:57], v[46:47], v[58:59] op_sel_hi:[1,0,1]
	v_pk_mul_f32 v[58:59], v[16:17], v[56:57] op_sel:[1,1] op_sel_hi:[0,1] neg_lo:[0,1]
	v_pk_fma_f32 v[56:57], v[16:17], v[56:57], v[58:59] op_sel_hi:[1,0,1]
	s_nop 0
	v_pk_mul_f32 v[58:59], v[56:57], v[90:91] op_sel:[1,1] op_sel_hi:[0,1] neg_lo:[0,1]
	v_pk_fma_f32 v[58:59], v[56:57], v[90:91], v[58:59] op_sel_hi:[1,0,1]
	ds_write2_b64 v71, v[46:47], v[58:59] offset0:128 offset1:144
	v_pk_mul_f32 v[46:47], v[16:17], v[56:57] op_sel:[1,1] op_sel_hi:[0,1] neg_lo:[0,1]
	v_pk_fma_f32 v[46:47], v[16:17], v[56:57], v[46:47] op_sel_hi:[1,0,1]
	s_nop 0
	v_pk_mul_f32 v[56:57], v[46:47], v[50:51] op_sel:[1,1] op_sel_hi:[0,1] neg_lo:[0,1]
	v_pk_fma_f32 v[50:51], v[46:47], v[50:51], v[56:57] op_sel_hi:[1,0,1]
	v_pk_mul_f32 v[56:57], v[16:17], v[46:47] op_sel:[1,1] op_sel_hi:[0,1] neg_lo:[0,1]
	v_pk_fma_f32 v[46:47], v[16:17], v[46:47], v[56:57] op_sel_hi:[1,0,1]
	s_nop 0
	v_pk_mul_f32 v[56:57], v[46:47], v[54:55] op_sel:[1,1] op_sel_hi:[0,1] neg_lo:[0,1]
	v_pk_fma_f32 v[54:55], v[46:47], v[54:55], v[56:57] op_sel_hi:[1,0,1]
	ds_write2_b64 v70, v[50:51], v[54:55] offset0:160 offset1:176
	v_pk_mul_f32 v[50:51], v[16:17], v[46:47] op_sel:[1,1] op_sel_hi:[0,1] neg_lo:[0,1]
	v_pk_fma_f32 v[46:47], v[16:17], v[46:47], v[50:51] op_sel_hi:[1,0,1]
	s_nop 0
	v_pk_mul_f32 v[50:51], v[38:39], v[46:47] op_sel:[1,1] op_sel_hi:[1,0] neg_lo:[1,0]
	s_nop 0
	v_pk_fma_f32 v[38:39], v[38:39], v[46:47], v[50:51] op_sel_hi:[0,1,1]
	v_pk_mul_f32 v[50:51], v[16:17], v[46:47] op_sel:[1,1] op_sel_hi:[0,1] neg_lo:[0,1]
	v_pk_fma_f32 v[46:47], v[16:17], v[46:47], v[50:51] op_sel_hi:[1,0,1]
	s_nop 0
	v_pk_mul_f32 v[50:51], v[46:47], v[76:77] op_sel:[1,1] op_sel_hi:[0,1] neg_lo:[0,1]
	v_pk_fma_f32 v[50:51], v[46:47], v[76:77], v[50:51] op_sel_hi:[1,0,1]
	ds_write2_b64 v69, v[38:39], v[50:51] offset0:192 offset1:208
	v_pk_mul_f32 v[38:39], v[16:17], v[46:47] op_sel:[1,1] op_sel_hi:[0,1] neg_lo:[0,1]
	v_pk_fma_f32 v[38:39], v[16:17], v[46:47], v[38:39] op_sel_hi:[1,0,1]
	s_nop 0
	v_pk_mul_f32 v[46:47], v[42:43], v[38:39] op_sel:[1,1] op_sel_hi:[1,0] neg_lo:[1,0]
	s_nop 0
	v_pk_fma_f32 v[42:43], v[42:43], v[38:39], v[46:47] op_sel_hi:[0,1,1]
	v_pk_mul_f32 v[46:47], v[16:17], v[38:39] op_sel:[1,1] op_sel_hi:[0,1] neg_lo:[0,1]
	v_pk_fma_f32 v[38:39], v[16:17], v[38:39], v[46:47] op_sel_hi:[1,0,1]
	s_nop 0
	v_pk_mul_f32 v[46:47], v[38:39], v[84:85] op_sel:[1,1] op_sel_hi:[0,1] neg_lo:[0,1]
	v_pk_fma_f32 v[46:47], v[38:39], v[84:85], v[46:47] op_sel_hi:[1,0,1]
	ds_write2_b64 v68, v[42:43], v[46:47] offset0:224 offset1:240
	v_pk_mul_f32 v[42:43], v[16:17], v[38:39] op_sel:[1,1] op_sel_hi:[0,1] neg_lo:[0,1]
	v_pk_fma_f32 v[38:39], v[16:17], v[38:39], v[42:43] op_sel_hi:[1,0,1]
	s_nop 0
	v_pk_mul_f32 v[42:43], v[30:31], v[38:39] op_sel:[1,1] op_sel_hi:[1,0] neg_lo:[1,0]
	s_nop 0
	v_pk_fma_f32 v[30:31], v[30:31], v[38:39], v[42:43] op_sel_hi:[0,1,1]
	v_pk_mul_f32 v[42:43], v[16:17], v[38:39] op_sel:[1,1] op_sel_hi:[0,1] neg_lo:[0,1]
	v_pk_fma_f32 v[38:39], v[16:17], v[38:39], v[42:43] op_sel_hi:[1,0,1]
	s_nop 0
	v_pk_mul_f32 v[42:43], v[78:79], v[38:39] op_sel:[1,1] op_sel_hi:[1,0] neg_lo:[1,0]
	s_nop 0
	v_pk_fma_f32 v[42:43], v[78:79], v[38:39], v[42:43] op_sel_hi:[0,1,1]
	ds_write2_b64 v67, v[30:31], v[42:43] offset1:16
	v_pk_mul_f32 v[30:31], v[16:17], v[38:39] op_sel:[1,1] op_sel_hi:[0,1] neg_lo:[0,1]
	v_pk_fma_f32 v[30:31], v[16:17], v[38:39], v[30:31] op_sel_hi:[1,0,1]
	s_nop 0
	v_pk_mul_f32 v[38:39], v[34:35], v[30:31] op_sel:[1,1] op_sel_hi:[1,0] neg_lo:[1,0]
	s_nop 0
	v_pk_fma_f32 v[34:35], v[34:35], v[30:31], v[38:39] op_sel_hi:[0,1,1]
	v_pk_mul_f32 v[38:39], v[16:17], v[30:31] op_sel:[1,1] op_sel_hi:[0,1] neg_lo:[0,1]
	v_pk_fma_f32 v[30:31], v[16:17], v[30:31], v[38:39] op_sel_hi:[1,0,1]
	s_nop 0
	v_pk_mul_f32 v[38:39], v[52:53], v[30:31] op_sel:[1,1] op_sel_hi:[1,0] neg_lo:[1,0]
	s_nop 0
	v_pk_fma_f32 v[38:39], v[52:53], v[30:31], v[38:39] op_sel_hi:[0,1,1]
	ds_write2_b64 v66, v[34:35], v[38:39] offset0:32 offset1:48
	v_pk_mul_f32 v[34:35], v[16:17], v[30:31] op_sel:[1,1] op_sel_hi:[0,1] neg_lo:[0,1]
	v_pk_fma_f32 v[30:31], v[16:17], v[30:31], v[34:35] op_sel_hi:[1,0,1]
	s_nop 0
	v_pk_mul_f32 v[34:35], v[26:27], v[30:31] op_sel:[1,1] op_sel_hi:[1,0] neg_lo:[1,0]
	s_nop 0
	v_pk_fma_f32 v[26:27], v[26:27], v[30:31], v[34:35] op_sel_hi:[0,1,1]
	v_pk_mul_f32 v[34:35], v[16:17], v[30:31] op_sel:[1,1] op_sel_hi:[0,1] neg_lo:[0,1]
	v_pk_fma_f32 v[30:31], v[16:17], v[30:31], v[34:35] op_sel_hi:[1,0,1]
	s_nop 0
	v_pk_mul_f32 v[34:35], v[48:49], v[30:31] op_sel:[1,1] op_sel_hi:[1,0] neg_lo:[1,0]
	s_nop 0
	v_pk_fma_f32 v[34:35], v[48:49], v[30:31], v[34:35] op_sel_hi:[0,1,1]
	ds_write2_b64 v65, v[26:27], v[34:35] offset0:64 offset1:80
	v_pk_mul_f32 v[26:27], v[16:17], v[30:31] op_sel:[1,1] op_sel_hi:[0,1] neg_lo:[0,1]
	v_pk_fma_f32 v[26:27], v[16:17], v[30:31], v[26:27] op_sel_hi:[1,0,1]
	s_nop 0
	v_pk_mul_f32 v[30:31], v[28:29], v[26:27] op_sel:[1,1] op_sel_hi:[1,0] neg_lo:[1,0]
	s_nop 0
	v_pk_fma_f32 v[28:29], v[28:29], v[26:27], v[30:31] op_sel_hi:[0,1,1]
	v_pk_mul_f32 v[30:31], v[16:17], v[26:27] op_sel:[1,1] op_sel_hi:[0,1] neg_lo:[0,1]
	v_pk_fma_f32 v[26:27], v[16:17], v[26:27], v[30:31] op_sel_hi:[1,0,1]
	s_nop 0
	v_pk_mul_f32 v[30:31], v[80:81], v[26:27] op_sel:[1,1] op_sel_hi:[1,0] neg_lo:[1,0]
	s_nop 0
	v_pk_fma_f32 v[30:31], v[80:81], v[26:27], v[30:31] op_sel_hi:[0,1,1]
	ds_write2_b64 v64, v[28:29], v[30:31] offset0:96 offset1:112
	v_pk_mul_f32 v[28:29], v[16:17], v[26:27] op_sel:[1,1] op_sel_hi:[0,1] neg_lo:[0,1]
	v_pk_fma_f32 v[26:27], v[16:17], v[26:27], v[28:29] op_sel_hi:[1,0,1]
	s_nop 0
	v_pk_mul_f32 v[28:29], v[22:23], v[26:27] op_sel:[1,1] op_sel_hi:[1,0] neg_lo:[1,0]
	s_nop 0
	v_pk_fma_f32 v[22:23], v[22:23], v[26:27], v[28:29] op_sel_hi:[0,1,1]
	v_pk_mul_f32 v[28:29], v[16:17], v[26:27] op_sel:[1,1] op_sel_hi:[0,1] neg_lo:[0,1]
	v_pk_fma_f32 v[26:27], v[16:17], v[26:27], v[28:29] op_sel_hi:[1,0,1]
	s_nop 0
	v_pk_mul_f32 v[28:29], v[40:41], v[26:27] op_sel:[1,1] op_sel_hi:[1,0] neg_lo:[1,0]
	s_nop 0
	v_pk_fma_f32 v[28:29], v[40:41], v[26:27], v[28:29] op_sel_hi:[0,1,1]
	ds_write2_b64 v63, v[22:23], v[28:29] offset0:128 offset1:144
	v_pk_mul_f32 v[22:23], v[16:17], v[26:27] op_sel:[1,1] op_sel_hi:[0,1] neg_lo:[0,1]
	v_pk_fma_f32 v[22:23], v[16:17], v[26:27], v[22:23] op_sel_hi:[1,0,1]
	s_nop 0
	v_pk_mul_f32 v[26:27], v[24:25], v[22:23] op_sel:[1,1] op_sel_hi:[1,0] neg_lo:[1,0]
	s_nop 0
	v_pk_fma_f32 v[24:25], v[24:25], v[22:23], v[26:27] op_sel_hi:[0,1,1]
	v_pk_mul_f32 v[26:27], v[16:17], v[22:23] op_sel:[1,1] op_sel_hi:[0,1] neg_lo:[0,1]
	v_pk_fma_f32 v[22:23], v[16:17], v[22:23], v[26:27] op_sel_hi:[1,0,1]
	s_nop 0
	v_pk_mul_f32 v[26:27], v[44:45], v[22:23] op_sel:[1,1] op_sel_hi:[1,0] neg_lo:[1,0]
	s_nop 0
	v_pk_fma_f32 v[26:27], v[44:45], v[22:23], v[26:27] op_sel_hi:[0,1,1]
	ds_write2_b64 v62, v[24:25], v[26:27] offset0:160 offset1:176
	v_pk_mul_f32 v[24:25], v[16:17], v[22:23] op_sel:[1,1] op_sel_hi:[0,1] neg_lo:[0,1]
	v_pk_fma_f32 v[22:23], v[16:17], v[22:23], v[24:25] op_sel_hi:[1,0,1]
	s_nop 0
	v_pk_mul_f32 v[24:25], v[18:19], v[22:23] op_sel:[1,1] op_sel_hi:[1,0] neg_lo:[1,0]
	s_nop 0
	v_pk_fma_f32 v[18:19], v[18:19], v[22:23], v[24:25] op_sel_hi:[0,1,1]
	v_pk_mul_f32 v[24:25], v[16:17], v[22:23] op_sel:[1,1] op_sel_hi:[0,1] neg_lo:[0,1]
	v_pk_fma_f32 v[22:23], v[16:17], v[22:23], v[24:25] op_sel_hi:[1,0,1]
	s_nop 0
	v_pk_mul_f32 v[24:25], v[32:33], v[22:23] op_sel:[1,1] op_sel_hi:[1,0] neg_lo:[1,0]
	s_nop 0
	v_pk_fma_f32 v[24:25], v[32:33], v[22:23], v[24:25] op_sel_hi:[0,1,1]
	ds_write2_b64 v15, v[18:19], v[24:25] offset0:192 offset1:208
	v_pk_mul_f32 v[18:19], v[16:17], v[22:23] op_sel:[1,1] op_sel_hi:[0,1] neg_lo:[0,1]
	v_pk_fma_f32 v[18:19], v[16:17], v[22:23], v[18:19] op_sel_hi:[1,0,1]
	s_nop 0
	v_pk_mul_f32 v[22:23], v[20:21], v[18:19] op_sel:[1,1] op_sel_hi:[1,0] neg_lo:[1,0]
	s_nop 0
	v_pk_fma_f32 v[20:21], v[20:21], v[18:19], v[22:23] op_sel_hi:[0,1,1]
	v_pk_mul_f32 v[22:23], v[16:17], v[18:19] op_sel:[1,1] op_sel_hi:[0,1] neg_lo:[0,1]
	v_pk_fma_f32 v[16:17], v[16:17], v[18:19], v[22:23] op_sel_hi:[1,0,1]
	s_nop 0
	v_pk_mul_f32 v[18:19], v[36:37], v[16:17] op_sel:[1,1] op_sel_hi:[1,0] neg_lo:[1,0]
	s_nop 0
	v_pk_fma_f32 v[16:17], v[36:37], v[16:17], v[18:19] op_sel_hi:[0,1,1]
	ds_write2_b64 v13, v[20:21], v[16:17] offset0:224 offset1:240
	v_mov_b32_e32 v16, v182
	v_mov_b32_e32 v10, v176
	v_mov_b32_e32 v17, v175
	s_waitcnt lgkmcnt(0)
	s_barrier
	v_lshlrev_b32_e32 v190, 3, v16
	v_add_u32_e32 v190, 0x1000, v190
	global_load_dwordx2 v[202:203], v190, s[46:47] offset:-4096
	global_load_dwordx2 v[204:205], v190, s[46:47]
	v_add_u32_e32 v190, 0x2000, v190
	global_load_dwordx2 v[206:207], v190, s[46:47] offset:-4096
	global_load_dwordx2 v[208:209], v190, s[46:47]
	v_add_u32_e32 v190, 0x2000, v190
	global_load_dwordx2 v[210:211], v190, s[46:47] offset:-4096
	global_load_dwordx2 v[212:213], v190, s[46:47]
	v_add_u32_e32 v190, 0x2000, v190
	global_load_dwordx2 v[214:215], v190, s[46:47] offset:-4096
	global_load_dwordx2 v[216:217], v190, s[46:47]
	v_add_u32_e32 v190, 0x2000, v190
	global_load_dwordx2 v[218:219], v190, s[46:47] offset:-4096
	global_load_dwordx2 v[220:221], v190, s[46:47]
	v_add_u32_e32 v190, 0x2000, v190
	global_load_dwordx2 v[222:223], v190, s[46:47] offset:-4096
	global_load_dwordx2 v[224:225], v190, s[46:47]
	v_add_u32_e32 v190, 0x2000, v190
	global_load_dwordx2 v[226:227], v190, s[46:47] offset:-4096
	global_load_dwordx2 v[228:229], v190, s[46:47]
	v_add_u32_e32 v190, 0x2000, v190
	global_load_dwordx2 v[230:231], v190, s[46:47] offset:-4096
	global_load_dwordx2 v[232:233], v190, s[46:47]
	v_mov_b32_e32 v50, v165
	v_lshlrev_b32_e32 v13, 3, v17
	v_lshlrev_b32_e32 v48, 3, v10
	v_add3_u32 v10, 0, v13, v48
	v_xor_b32_e32 v13, 1, v17
	v_xor_b32_e32 v34, 8, v17
	v_xor_b32_e32 v36, 9, v17
	v_lshlrev_b32_e32 v13, 3, v13
	v_xor_b32_e32 v15, 2, v17
	v_xor_b32_e32 v24, 3, v17
	v_xor_b32_e32 v26, 4, v17
	v_xor_b32_e32 v28, 5, v17
	v_xor_b32_e32 v30, 6, v17
	v_xor_b32_e32 v32, 7, v17
	v_lshlrev_b32_e32 v34, 3, v34
	v_lshlrev_b32_e32 v36, 3, v36
	v_xor_b32_e32 v38, 10, v17
	v_xor_b32_e32 v40, 11, v17
	v_xor_b32_e32 v42, 12, v17
	v_xor_b32_e32 v44, 13, v17
	v_xor_b32_e32 v46, 14, v17
	v_xor_b32_e32 v17, 15, v17
	v_add3_u32 v13, 0, v13, v48
	v_lshlrev_b32_e32 v15, 3, v15
	v_lshlrev_b32_e32 v24, 3, v24
	v_lshlrev_b32_e32 v26, 3, v26
	v_lshlrev_b32_e32 v28, 3, v28
	v_lshlrev_b32_e32 v30, 3, v30
	v_lshlrev_b32_e32 v32, 3, v32
	v_add3_u32 v57, 0, v34, v48
	v_add3_u32 v58, 0, v36, v48
	v_lshlrev_b32_e32 v38, 3, v38
	v_lshlrev_b32_e32 v40, 3, v40
	v_lshlrev_b32_e32 v42, 3, v42
	v_lshlrev_b32_e32 v44, 3, v44
	v_lshlrev_b32_e32 v46, 3, v46
	v_lshlrev_b32_e32 v17, 3, v17
	ds_read_b64 v[18:19], v10
	ds_read_b64 v[20:21], v13
	v_add3_u32 v15, 0, v15, v48
	v_add3_u32 v52, 0, v24, v48
	v_add3_u32 v53, 0, v26, v48
	v_add3_u32 v54, 0, v28, v48
	v_add3_u32 v55, 0, v30, v48
	v_add3_u32 v56, 0, v32, v48
	ds_read_b64 v[34:35], v57
	ds_read_b64 v[36:37], v58
	v_add3_u32 v59, 0, v38, v48
	v_add3_u32 v60, 0, v40, v48
	v_add3_u32 v61, 0, v42, v48
	v_add3_u32 v62, 0, v44, v48
	v_add3_u32 v63, 0, v46, v48
	v_add3_u32 v64, 0, v17, v48
	v_mov_b32_e32 v17, v1
	ds_read_b64 v[22:23], v15
	ds_read_b64 v[24:25], v52
	ds_read_b64 v[26:27], v53
	ds_read_b64 v[28:29], v54
	ds_read_b64 v[30:31], v55
	ds_read_b64 v[32:33], v56
	ds_read_b64 v[38:39], v59
	ds_read_b64 v[40:41], v60
	ds_read_b64 v[42:43], v61
	ds_read_b64 v[44:45], v62
	ds_read_b64 v[46:47], v63
	ds_read_b64 v[48:49], v64
	s_waitcnt lgkmcnt(13)
	v_pk_add_f32 v[70:71], v[18:19], v[34:35]
	v_mov_b32_e32 v17, v164
	v_pk_add_f32 v[18:19], v[18:19], v[34:35] neg_lo:[0,1] neg_hi:[0,1]
	v_mov_b32_e32 v17, v166
	s_waitcnt lgkmcnt(12)
	v_pk_add_f32 v[34:35], v[20:21], v[36:37]
	v_pk_add_f32 v[20:21], v[20:21], v[36:37] neg_lo:[0,1] neg_hi:[0,1]
	v_mov_b32_e32 v66, v167
	v_mov_b32_e32 v17, v168
	v_mov_b32_e32 v68, v169
	s_nop 0
	v_pk_mul_f32 v[36:37], v[20:21], v[68:69] op_sel:[1,0] op_sel_hi:[0,0] neg_lo:[1,1] neg_hi:[0,1]
	v_mov_b32_e32 v17, v170
	v_pk_fma_f32 v[20:21], v[20:21], v[50:51], v[36:37] op_sel_hi:[1,0,1]
	s_waitcnt lgkmcnt(5)
	v_pk_add_f32 v[36:37], v[22:23], v[38:39]
	v_pk_add_f32 v[22:23], v[22:23], v[38:39] neg_lo:[0,1] neg_hi:[0,1]
	s_nop 0
	v_pk_mul_f32 v[38:39], v[22:23], v[66:67] op_sel:[1,0] op_sel_hi:[0,0] neg_lo:[1,1] neg_hi:[0,1]
	v_mov_b32_e32 v17, v171
	v_pk_fma_f32 v[22:23], v[22:23], v[66:67], v[38:39] op_sel_hi:[1,0,1]
	s_waitcnt lgkmcnt(4)
	v_pk_add_f32 v[38:39], v[24:25], v[40:41]
	v_pk_add_f32 v[24:25], v[24:25], v[40:41] neg_lo:[0,1] neg_hi:[0,1]
	s_nop 0
	v_pk_mul_f32 v[40:41], v[24:25], v[68:69] op_sel_hi:[1,0]
	s_nop 0
	v_pk_fma_f32 v[24:25], v[24:25], v[50:51], v[40:41] op_sel:[1,0,0] op_sel_hi:[0,0,1] neg_lo:[1,1,0] neg_hi:[0,1,0]
	s_waitcnt lgkmcnt(3)
	v_pk_add_f32 v[40:41], v[26:27], v[42:43]
	v_pk_add_f32 v[26:27], v[26:27], v[42:43] neg_lo:[0,1] neg_hi:[0,1]
	v_ashrrev_i32_e32 v17, 31, v16
	v_xor_b32_e32 v73, 0x80000000, v26
	v_mov_b32_e32 v72, v27
	s_waitcnt lgkmcnt(2)
	v_pk_add_f32 v[26:27], v[28:29], v[44:45]
	v_pk_add_f32 v[28:29], v[28:29], v[44:45] neg_lo:[0,1] neg_hi:[0,1]
	s_nop 0
	v_pk_mul_f32 v[42:43], v[28:29], v[68:69] op_sel_hi:[1,0] neg_lo:[0,1] neg_hi:[0,1]
	s_nop 0
	v_pk_fma_f32 v[28:29], v[28:29], v[50:51], v[42:43] op_sel:[1,0,0] op_sel_hi:[0,0,1] neg_lo:[1,1,0] neg_hi:[0,1,0]
	s_waitcnt lgkmcnt(1)
	v_pk_add_f32 v[42:43], v[30:31], v[46:47]
	v_pk_add_f32 v[30:31], v[30:31], v[46:47] neg_lo:[0,1] neg_hi:[0,1]
	s_nop 0
	v_pk_mul_f32 v[44:45], v[30:31], v[66:67] op_sel:[1,0] op_sel_hi:[0,0] neg_lo:[1,1] neg_hi:[0,1]
	s_nop 0
	v_pk_fma_f32 v[30:31], v[30:31], v[66:67], v[44:45] op_sel_hi:[1,0,1] neg_lo:[0,1,0] neg_hi:[0,1,0]
	s_waitcnt lgkmcnt(0)
	v_pk_add_f32 v[44:45], v[32:33], v[48:49]
	v_pk_add_f32 v[32:33], v[32:33], v[48:49] neg_lo:[0,1] neg_hi:[0,1]
	v_pk_add_f32 v[48:49], v[34:35], v[26:27]
	v_pk_add_f32 v[26:27], v[34:35], v[26:27] neg_lo:[0,1] neg_hi:[0,1]
	s_nop 0
	v_pk_mul_f32 v[34:35], v[26:27], v[66:67] op_sel:[1,0] op_sel_hi:[0,0] neg_lo:[1,1] neg_hi:[0,1]
	v_pk_fma_f32 v[26:27], v[26:27], v[66:67], v[34:35] op_sel_hi:[1,0,1]
	v_pk_add_f32 v[34:35], v[36:37], v[42:43]
	v_pk_add_f32 v[36:37], v[36:37], v[42:43] neg_lo:[0,1] neg_hi:[0,1]
	v_pk_mul_f32 v[46:47], v[32:33], v[68:69] op_sel:[1,0] op_sel_hi:[0,0] neg_lo:[1,1] neg_hi:[0,1]
	v_xor_b32_e32 v43, 0x80000000, v36
	v_mov_b32_e32 v42, v37
	v_pk_add_f32 v[36:37], v[38:39], v[44:45]
	v_pk_add_f32 v[38:39], v[38:39], v[44:45] neg_lo:[0,1] neg_hi:[0,1]
	v_pk_fma_f32 v[46:47], v[32:33], v[50:51], v[46:47] op_sel_hi:[1,0,1] neg_lo:[0,1,0] neg_hi:[0,1,0]
	v_pk_add_f32 v[32:33], v[70:71], v[40:41]
	v_pk_mul_f32 v[44:45], v[38:39], v[66:67] op_sel:[1,0] op_sel_hi:[0,0] neg_lo:[1,1] neg_hi:[0,1]
	v_pk_add_f32 v[40:41], v[70:71], v[40:41] neg_lo:[0,1] neg_hi:[0,1]
	v_pk_fma_f32 v[38:39], v[38:39], v[66:67], v[44:45] op_sel_hi:[1,0,1] neg_lo:[0,1,0] neg_hi:[0,1,0]
	v_pk_add_f32 v[44:45], v[32:33], v[34:35]
	v_pk_add_f32 v[32:33], v[32:33], v[34:35] neg_lo:[0,1] neg_hi:[0,1]
	v_pk_add_f32 v[34:35], v[48:49], v[36:37]
	v_pk_add_f32 v[36:37], v[48:49], v[36:37] neg_lo:[0,1] neg_hi:[0,1]
	v_pk_add_f32 v[50:51], v[44:45], v[34:35]
	v_xor_b32_e32 v49, 0x80000000, v36
	v_mov_b32_e32 v48, v37
	v_pk_add_f32 v[36:37], v[44:45], v[34:35] neg_lo:[0,1] neg_hi:[0,1]
	v_pk_add_f32 v[68:69], v[32:33], v[48:49]
	v_pk_add_f32 v[44:45], v[32:33], v[48:49] neg_lo:[0,1] neg_hi:[0,1]
	v_pk_add_f32 v[32:33], v[40:41], v[42:43]
	v_pk_add_f32 v[34:35], v[40:41], v[42:43] neg_lo:[0,1] neg_hi:[0,1]
	v_pk_add_f32 v[40:41], v[26:27], v[38:39]
	v_pk_add_f32 v[26:27], v[26:27], v[38:39] neg_lo:[0,1] neg_hi:[0,1]
	v_pk_add_f32 v[42:43], v[32:33], v[40:41] neg_lo:[0,1] neg_hi:[0,1]
	v_xor_b32_e32 v39, 0x80000000, v26
	v_mov_b32_e32 v38, v27
	v_pk_add_f32 v[26:27], v[32:33], v[40:41]
	v_pk_add_f32 v[40:41], v[20:21], v[28:29]
	v_pk_add_f32 v[20:21], v[20:21], v[28:29] neg_lo:[0,1] neg_hi:[0,1]
	v_pk_add_f32 v[32:33], v[34:35], v[38:39]
	v_pk_mul_f32 v[28:29], v[66:67], v[20:21] op_sel:[0,1] op_sel_hi:[0,0] neg_lo:[1,1] neg_hi:[1,0]
	v_pk_fma_f32 v[20:21], v[66:67], v[20:21], v[28:29] op_sel_hi:[0,1,1]
	v_pk_add_f32 v[28:29], v[22:23], v[30:31]
	v_pk_add_f32 v[22:23], v[22:23], v[30:31] neg_lo:[0,1] neg_hi:[0,1]
	v_pk_add_f32 v[38:39], v[34:35], v[38:39] neg_lo:[0,1] neg_hi:[0,1]
	v_xor_b32_e32 v31, 0x80000000, v22
	v_mov_b32_e32 v30, v23
	v_pk_add_f32 v[22:23], v[24:25], v[46:47]
	v_pk_add_f32 v[24:25], v[24:25], v[46:47] neg_lo:[0,1] neg_hi:[0,1]
	v_pk_add_f32 v[34:35], v[18:19], v[72:73]
	v_pk_mul_f32 v[46:47], v[66:67], v[24:25] op_sel:[0,1] op_sel_hi:[0,0] neg_lo:[1,1] neg_hi:[1,0]
	v_pk_fma_f32 v[24:25], v[66:67], v[24:25], v[46:47] op_sel_hi:[0,1,1] neg_lo:[1,0,0] neg_hi:[1,0,0]
	v_pk_add_f32 v[46:47], v[34:35], v[28:29]
	v_pk_add_f32 v[28:29], v[34:35], v[28:29] neg_lo:[0,1] neg_hi:[0,1]
	v_pk_add_f32 v[34:35], v[40:41], v[22:23]
	v_pk_add_f32 v[22:23], v[40:41], v[22:23] neg_lo:[0,1] neg_hi:[0,1]
	v_pk_add_f32 v[18:19], v[18:19], v[72:73] neg_lo:[0,1] neg_hi:[0,1]
	v_pk_add_f32 v[66:67], v[28:29], v[22:23] op_sel:[0,1] op_sel_hi:[1,0] neg_hi:[0,1]
	v_pk_add_f32 v[48:49], v[28:29], v[22:23] op_sel:[0,1] op_sel_hi:[1,0] neg_lo:[0,1]
	v_pk_add_f32 v[28:29], v[18:19], v[30:31]
	v_pk_add_f32 v[18:19], v[18:19], v[30:31] neg_lo:[0,1] neg_hi:[0,1]
	v_pk_add_f32 v[30:31], v[20:21], v[24:25]
	v_pk_add_f32 v[20:21], v[20:21], v[24:25] neg_lo:[0,1] neg_hi:[0,1]
	v_pk_add_f32 v[22:23], v[46:47], v[34:35]
	v_xor_b32_e32 v25, 0x80000000, v20
	v_mov_b32_e32 v24, v21
	v_lshl_add_u64 v[20:21], v[16:17], 3, s[46:47]
	s_waitcnt vmcnt(0)
	v_pk_add_f32 v[40:41], v[46:47], v[34:35] neg_lo:[0,1] neg_hi:[0,1]
	v_pk_add_f32 v[34:35], v[18:19], v[24:25]
	v_pk_add_f32 v[18:19], v[18:19], v[24:25] neg_lo:[0,1] neg_hi:[0,1]
	v_pk_add_f32 v[70:71], v[28:29], v[30:31]
	v_pk_add_f32 v[46:47], v[28:29], v[30:31] neg_lo:[0,1] neg_hi:[0,1]
	v_mov_b32_e32 v17, v1
	s_nop 0
	v_pk_mul_f32 v[24:25], v[50:51], v[202:203] op_sel:[1,1] op_sel_hi:[1,0] neg_lo:[1,0]
	s_nop 0
	v_pk_fma_f32 v[20:21], v[50:51], v[202:203], v[24:25] op_sel_hi:[0,1,1]
	v_add_u32_e32 v24, 0x200, v16
	v_ashrrev_i32_e32 v25, 31, v24
	v_lshl_add_u64 v[24:25], v[24:25], 3, s[46:47]
	s_nop 0
	v_pk_mul_f32 v[28:29], v[204:205], v[22:23] op_sel:[1,1] op_sel_hi:[0,1] neg_lo:[0,1]
	v_pk_fma_f32 v[22:23], v[204:205], v[22:23], v[28:29] op_sel_hi:[1,0,1]
	v_add_u32_e32 v24, 0x400, v16
	v_ashrrev_i32_e32 v25, 31, v24
	v_lshl_add_u64 v[24:25], v[24:25], 3, s[46:47]
	s_nop 0
	v_pk_mul_f32 v[28:29], v[26:27], v[206:207] op_sel:[1,1] op_sel_hi:[1,0] neg_lo:[1,0]
	s_nop 0
	v_pk_fma_f32 v[24:25], v[26:27], v[206:207], v[28:29] op_sel_hi:[0,1,1]
	v_add_u32_e32 v26, 0x600, v16
	v_ashrrev_i32_e32 v27, 31, v26
	v_lshl_add_u64 v[26:27], v[26:27], 3, s[46:47]
	s_nop 0
	v_pk_mul_f32 v[28:29], v[208:209], v[70:71] op_sel:[1,1] op_sel_hi:[0,1] neg_lo:[0,1]
	v_pk_fma_f32 v[26:27], v[208:209], v[70:71], v[28:29] op_sel_hi:[1,0,1]
	v_add_u32_e32 v28, 0x800, v16
	v_ashrrev_i32_e32 v29, 31, v28
	v_lshl_add_u64 v[28:29], v[28:29], 3, s[46:47]
	s_nop 0
	v_pk_mul_f32 v[30:31], v[68:69], v[210:211] op_sel:[1,1] op_sel_hi:[1,0] neg_lo:[1,0]
	s_nop 0
	v_pk_fma_f32 v[28:29], v[68:69], v[210:211], v[30:31] op_sel_hi:[0,1,1]
	v_add_u32_e32 v30, 0xa00, v16
	v_ashrrev_i32_e32 v31, 31, v30
	v_lshl_add_u64 v[30:31], v[30:31], 3, s[46:47]
	v_mov_b32_e32 v68, v169
	s_nop 0
	v_pk_mul_f32 v[50:51], v[212:213], v[66:67] op_sel:[1,1] op_sel_hi:[0,1] neg_lo:[0,1]
	v_pk_fma_f32 v[30:31], v[212:213], v[66:67], v[50:51] op_sel_hi:[1,0,1]
	v_add_u32_e32 v50, 0xc00, v16
	v_ashrrev_i32_e32 v51, 31, v50
	v_lshl_add_u64 v[50:51], v[50:51], 3, s[46:47]
	s_nop 0
	v_pk_mul_f32 v[66:67], v[32:33], v[214:215] op_sel:[1,1] op_sel_hi:[1,0] neg_lo:[1,0]
	s_nop 0
	v_pk_fma_f32 v[32:33], v[32:33], v[214:215], v[66:67] op_sel_hi:[0,1,1]
	v_add_u32_e32 v50, 0xe00, v16
	v_ashrrev_i32_e32 v51, 31, v50
	v_lshl_add_u64 v[50:51], v[50:51], 3, s[46:47]
	s_nop 0
	v_pk_mul_f32 v[66:67], v[216:217], v[34:35] op_sel:[1,1] op_sel_hi:[0,1] neg_lo:[0,1]
	v_pk_fma_f32 v[34:35], v[216:217], v[34:35], v[66:67] op_sel_hi:[1,0,1]
	v_add_u32_e32 v50, 0x1000, v16
	v_ashrrev_i32_e32 v51, 31, v50
	v_lshl_add_u64 v[50:51], v[50:51], 3, s[46:47]
	s_nop 0
	v_pk_mul_f32 v[66:67], v[36:37], v[218:219] op_sel:[1,1] op_sel_hi:[1,0] neg_lo:[1,0]
	s_nop 0
	v_pk_fma_f32 v[36:37], v[36:37], v[218:219], v[66:67] op_sel_hi:[0,1,1]
	v_add_u32_e32 v50, 0x1200, v16
	v_ashrrev_i32_e32 v51, 31, v50
	v_lshl_add_u64 v[50:51], v[50:51], 3, s[46:47]
	v_pk_add_f32 v[70:71], v[20:21], v[36:37]
	v_pk_add_f32 v[20:21], v[20:21], v[36:37] neg_lo:[0,1] neg_hi:[0,1]
	s_nop 0
	v_pk_mul_f32 v[66:67], v[40:41], v[220:221] op_sel:[1,1] op_sel_hi:[1,0] neg_lo:[1,0]
	s_nop 0
	v_pk_fma_f32 v[40:41], v[40:41], v[220:221], v[66:67] op_sel_hi:[0,1,1]
	v_add_u32_e32 v50, 0x1400, v16
	v_ashrrev_i32_e32 v51, 31, v50
	v_lshl_add_u64 v[50:51], v[50:51], 3, s[46:47]
	v_pk_add_f32 v[36:37], v[22:23], v[40:41]
	v_pk_add_f32 v[22:23], v[22:23], v[40:41] neg_lo:[0,1] neg_hi:[0,1]
	s_nop 0
	v_pk_mul_f32 v[66:67], v[42:43], v[222:223] op_sel:[1,1] op_sel_hi:[1,0] neg_lo:[1,0]
	s_nop 0
	v_pk_fma_f32 v[42:43], v[42:43], v[222:223], v[66:67] op_sel_hi:[0,1,1]
	v_add_u32_e32 v50, 0x1600, v16
	v_ashrrev_i32_e32 v51, 31, v50
	v_lshl_add_u64 v[50:51], v[50:51], 3, s[46:47]
	s_nop 0
	v_pk_mul_f32 v[66:67], v[46:47], v[224:225] op_sel:[1,1] op_sel_hi:[1,0] neg_lo:[1,0]
	s_nop 0
	v_pk_fma_f32 v[46:47], v[46:47], v[224:225], v[66:67] op_sel_hi:[0,1,1]
	v_add_u32_e32 v50, 0x1800, v16
	v_ashrrev_i32_e32 v51, 31, v50
	v_lshl_add_u64 v[50:51], v[50:51], 3, s[46:47]
	s_nop 0
	v_pk_mul_f32 v[66:67], v[44:45], v[226:227] op_sel:[1,1] op_sel_hi:[1,0] neg_lo:[1,0]
	s_nop 0
	v_pk_fma_f32 v[44:45], v[44:45], v[226:227], v[66:67] op_sel_hi:[0,1,1]
	v_add_u32_e32 v50, 0x1a00, v16
	v_ashrrev_i32_e32 v51, 31, v50
	v_lshl_add_u64 v[50:51], v[50:51], 3, s[46:47]
	s_nop 0
	v_pk_mul_f32 v[66:67], v[48:49], v[228:229] op_sel:[1,1] op_sel_hi:[1,0] neg_lo:[1,0]
	s_nop 0
	v_pk_fma_f32 v[48:49], v[48:49], v[228:229], v[66:67] op_sel_hi:[0,1,1]
	v_add_u32_e32 v50, 0x1c00, v16
	v_ashrrev_i32_e32 v51, 31, v50
	v_lshl_add_u64 v[50:51], v[50:51], 3, s[46:47]
	s_nop 0
	v_pk_mul_f32 v[66:67], v[38:39], v[230:231] op_sel:[1,1] op_sel_hi:[1,0] neg_lo:[1,0]
	s_nop 0
	v_pk_fma_f32 v[38:39], v[38:39], v[230:231], v[66:67] op_sel_hi:[0,1,1]
	v_add_u32_e32 v50, 0x1e00, v16
	v_ashrrev_i32_e32 v51, 31, v50
	v_lshl_add_u64 v[50:51], v[50:51], 3, s[46:47]
	v_mov_b32_e32 v50, v232
	v_mov_b32_e32 v51, v233
	v_lshlrev_b32_e32 v190, 3, v16
	v_add_u32_e32 v190, 0x11000, v190
	global_load_dwordx2 v[202:203], v190, s[46:47] offset:-4096
	global_load_dwordx2 v[204:205], v190, s[46:47]
	v_add_u32_e32 v190, 0x2000, v190
	global_load_dwordx2 v[206:207], v190, s[46:47] offset:-4096
	global_load_dwordx2 v[208:209], v190, s[46:47]
	v_add_u32_e32 v190, 0x2000, v190
	global_load_dwordx2 v[210:211], v190, s[46:47] offset:-4096
	global_load_dwordx2 v[212:213], v190, s[46:47]
	v_add_u32_e32 v190, 0x2000, v190
	global_load_dwordx2 v[214:215], v190, s[46:47] offset:-4096
	global_load_dwordx2 v[216:217], v190, s[46:47]
	v_add_u32_e32 v190, 0x2000, v190
	global_load_dwordx2 v[218:219], v190, s[46:47] offset:-4096
	global_load_dwordx2 v[220:221], v190, s[46:47]
	v_add_u32_e32 v190, 0x2000, v190
	global_load_dwordx2 v[222:223], v190, s[46:47] offset:-4096
	global_load_dwordx2 v[224:225], v190, s[46:47]
	v_add_u32_e32 v190, 0x2000, v190
	global_load_dwordx2 v[226:227], v190, s[46:47] offset:-4096
	global_load_dwordx2 v[228:229], v190, s[46:47]
	v_add_u32_e32 v190, 0x2000, v190
	global_load_dwordx2 v[230:231], v190, s[46:47] offset:-4096
	global_load_dwordx2 v[232:233], v190, s[46:47]
	v_mov_b32_e32 v17, v164
	s_nop 0
	v_pk_mul_f32 v[66:67], v[18:19], v[50:51] op_sel:[1,1] op_sel_hi:[1,0] neg_lo:[1,0]
	s_nop 0
	v_pk_fma_f32 v[18:19], v[18:19], v[50:51], v[66:67] op_sel_hi:[0,1,1]
	v_mov_b32_e32 v50, v165
	v_mov_b32_e32 v17, v166
	v_mov_b32_e32 v66, v167
	v_mov_b32_e32 v17, v168
	s_nop 0
	v_pk_mul_f32 v[40:41], v[22:23], v[68:69] op_sel:[1,0] op_sel_hi:[0,0] neg_lo:[1,0]
	v_mov_b32_e32 v17, v170
	v_pk_fma_f32 v[22:23], v[22:23], v[50:51], v[40:41] op_sel_hi:[1,0,1]
	v_pk_add_f32 v[40:41], v[24:25], v[42:43]
	v_pk_add_f32 v[24:25], v[24:25], v[42:43] neg_lo:[0,1] neg_hi:[0,1]
	s_nop 0
	v_pk_mul_f32 v[42:43], v[24:25], v[66:67] op_sel:[1,0] op_sel_hi:[0,0] neg_lo:[1,0]
	v_mov_b32_e32 v17, v171
	v_pk_fma_f32 v[24:25], v[24:25], v[66:67], v[42:43] op_sel_hi:[1,0,1]
	v_pk_add_f32 v[42:43], v[26:27], v[46:47]
	v_pk_add_f32 v[26:27], v[26:27], v[46:47] neg_lo:[0,1] neg_hi:[0,1]
	s_nop 0
	v_pk_mul_f32 v[46:47], v[26:27], v[68:69] op_sel_hi:[1,0]
	s_nop 0
	v_pk_fma_f32 v[26:27], v[26:27], v[50:51], v[46:47] op_sel:[1,0,0] op_sel_hi:[0,0,1] neg_lo:[1,0,0]
	v_pk_add_f32 v[46:47], v[28:29], v[44:45]
	v_pk_add_f32 v[28:29], v[28:29], v[44:45] neg_lo:[0,1] neg_hi:[0,1]
	v_mov_b32_e32 v17, v175
	v_xor_b32_e32 v44, 0x80000000, v29
	v_mov_b32_e32 v45, v28
	v_pk_add_f32 v[28:29], v[30:31], v[48:49]
	v_pk_add_f32 v[30:31], v[30:31], v[48:49] neg_lo:[0,1] neg_hi:[0,1]
	s_nop 0
	v_pk_mul_f32 v[48:49], v[30:31], v[68:69] op_sel_hi:[1,0] neg_lo:[0,1] neg_hi:[0,1]
	s_nop 0
	v_pk_fma_f32 v[30:31], v[30:31], v[50:51], v[48:49] op_sel:[1,0,0] op_sel_hi:[0,0,1] neg_lo:[1,0,0]
	v_pk_add_f32 v[48:49], v[32:33], v[38:39]
	v_pk_add_f32 v[32:33], v[32:33], v[38:39] neg_lo:[0,1] neg_hi:[0,1]
	s_nop 0
	v_pk_mul_f32 v[38:39], v[32:33], v[66:67] op_sel:[1,0] op_sel_hi:[0,0] neg_lo:[1,0]
	s_nop 0
	v_pk_fma_f32 v[32:33], v[32:33], v[66:67], v[38:39] op_sel_hi:[1,0,1] neg_lo:[0,1,0] neg_hi:[0,1,0]
	v_pk_add_f32 v[38:39], v[34:35], v[18:19]
	v_pk_add_f32 v[18:19], v[34:35], v[18:19] neg_lo:[0,1] neg_hi:[0,1]
	s_nop 0
	v_pk_mul_f32 v[34:35], v[18:19], v[68:69] op_sel:[1,0] op_sel_hi:[0,0] neg_lo:[1,0]
	v_mov_b32_e32 v68, v169
	v_pk_fma_f32 v[18:19], v[18:19], v[50:51], v[34:35] op_sel_hi:[1,0,1] neg_lo:[0,1,0] neg_hi:[0,1,0]
	v_pk_add_f32 v[50:51], v[36:37], v[28:29]
	v_pk_add_f32 v[28:29], v[36:37], v[28:29] neg_lo:[0,1] neg_hi:[0,1]
	v_pk_add_f32 v[34:35], v[70:71], v[46:47]
	v_pk_mul_f32 v[36:37], v[28:29], v[66:67] op_sel:[1,0] op_sel_hi:[0,0] neg_lo:[1,0]
	v_pk_add_f32 v[46:47], v[70:71], v[46:47] neg_lo:[0,1] neg_hi:[0,1]
	v_pk_fma_f32 v[28:29], v[28:29], v[66:67], v[36:37] op_sel_hi:[1,0,1]
	v_pk_add_f32 v[36:37], v[40:41], v[48:49]
	v_pk_add_f32 v[40:41], v[40:41], v[48:49] neg_lo:[0,1] neg_hi:[0,1]
	s_nop 0
	v_xor_b32_e32 v48, 0x80000000, v41
	v_mov_b32_e32 v49, v40
	v_pk_add_f32 v[40:41], v[42:43], v[38:39]
	v_pk_add_f32 v[38:39], v[42:43], v[38:39] neg_lo:[0,1] neg_hi:[0,1]
	s_nop 0
	v_pk_mul_f32 v[42:43], v[66:67], v[38:39] op_sel:[0,1] op_sel_hi:[0,0] neg_lo:[0,1]
	v_pk_fma_f32 v[38:39], v[38:39], v[66:67], v[42:43] op_sel_hi:[1,0,1] neg_lo:[0,1,0] neg_hi:[0,1,0]
	v_pk_add_f32 v[42:43], v[34:35], v[36:37]
	v_pk_add_f32 v[34:35], v[34:35], v[36:37] neg_lo:[0,1] neg_hi:[0,1]
	v_pk_add_f32 v[36:37], v[50:51], v[40:41]
	v_pk_add_f32 v[40:41], v[50:51], v[40:41] neg_lo:[0,1] neg_hi:[0,1]
	s_nop 0
	v_xor_b32_e32 v50, 0x80000000, v41
	v_mov_b32_e32 v51, v40
	v_pk_add_f32 v[40:41], v[42:43], v[36:37]
	v_pk_add_f32 v[36:37], v[42:43], v[36:37] neg_lo:[0,1] neg_hi:[0,1]
	v_pk_add_f32 v[42:43], v[34:35], v[50:51]
	v_pk_add_f32 v[34:35], v[34:35], v[50:51] neg_lo:[0,1] neg_hi:[0,1]
	v_pk_add_f32 v[50:51], v[46:47], v[48:49]
	v_pk_add_f32 v[46:47], v[46:47], v[48:49] neg_lo:[0,1] neg_hi:[0,1]
	v_pk_add_f32 v[48:49], v[28:29], v[38:39]
	v_pk_add_f32 v[28:29], v[28:29], v[38:39] neg_lo:[0,1] neg_hi:[0,1]
	s_nop 0
	v_xor_b32_e32 v38, 0x80000000, v29
	v_mov_b32_e32 v39, v28
	v_pk_add_f32 v[28:29], v[50:51], v[48:49]
	v_pk_add_f32 v[48:49], v[50:51], v[48:49] neg_lo:[0,1] neg_hi:[0,1]
	v_pk_add_f32 v[50:51], v[46:47], v[38:39]
	v_pk_add_f32 v[38:39], v[46:47], v[38:39] neg_lo:[0,1] neg_hi:[0,1]
	v_pk_add_f32 v[46:47], v[20:21], v[44:45]
	v_pk_add_f32 v[20:21], v[20:21], v[44:45] neg_lo:[0,1] neg_hi:[0,1]
	v_pk_add_f32 v[44:45], v[22:23], v[30:31]
	v_pk_add_f32 v[22:23], v[22:23], v[30:31] neg_lo:[0,1] neg_hi:[0,1]
	s_nop 0
	v_pk_mul_f32 v[30:31], v[66:67], v[22:23] op_sel:[0,1] op_sel_hi:[0,0] neg_lo:[0,1]
	v_pk_fma_f32 v[22:23], v[66:67], v[22:23], v[30:31] op_sel_hi:[0,1,1]
	v_pk_add_f32 v[30:31], v[24:25], v[32:33]
	v_pk_add_f32 v[24:25], v[24:25], v[32:33] neg_lo:[0,1] neg_hi:[0,1]
	s_nop 0
	v_xor_b32_e32 v32, 0x80000000, v25
	v_mov_b32_e32 v33, v24
	v_pk_add_f32 v[24:25], v[26:27], v[18:19]
	v_pk_add_f32 v[18:19], v[26:27], v[18:19] neg_lo:[0,1] neg_hi:[0,1]
	s_nop 0
	v_pk_mul_f32 v[26:27], v[66:67], v[18:19] op_sel:[0,1] op_sel_hi:[0,0] neg_lo:[0,1]
	v_pk_fma_f32 v[18:19], v[66:67], v[18:19], v[26:27] op_sel_hi:[0,1,1] neg_lo:[1,0,0] neg_hi:[1,0,0]
	v_pk_add_f32 v[26:27], v[46:47], v[30:31]
	v_pk_add_f32 v[30:31], v[46:47], v[30:31] neg_lo:[0,1] neg_hi:[0,1]
	v_pk_add_f32 v[46:47], v[44:45], v[24:25]
	v_pk_add_f32 v[24:25], v[44:45], v[24:25] neg_lo:[0,1] neg_hi:[0,1]
	v_mov_b32_e32 v66, v167
	v_xor_b32_e32 v44, 0x80000000, v25
	v_mov_b32_e32 v45, v24
	v_pk_add_f32 v[24:25], v[26:27], v[46:47]
	v_pk_add_f32 v[26:27], v[26:27], v[46:47] neg_lo:[0,1] neg_hi:[0,1]
	v_pk_add_f32 v[46:47], v[30:31], v[44:45]
	v_pk_add_f32 v[30:31], v[30:31], v[44:45] neg_lo:[0,1] neg_hi:[0,1]
	v_pk_add_f32 v[44:45], v[20:21], v[32:33]
	v_pk_add_f32 v[20:21], v[20:21], v[32:33] neg_lo:[0,1] neg_hi:[0,1]
	v_pk_add_f32 v[32:33], v[22:23], v[18:19]
	v_pk_add_f32 v[18:19], v[22:23], v[18:19] neg_lo:[0,1] neg_hi:[0,1]
	s_nop 0
	v_xor_b32_e32 v22, 0x80000000, v19
	v_mov_b32_e32 v23, v18
	v_pk_add_f32 v[18:19], v[44:45], v[32:33]
	v_pk_add_f32 v[32:33], v[44:45], v[32:33] neg_lo:[0,1] neg_hi:[0,1]
	v_pk_add_f32 v[44:45], v[20:21], v[22:23]
	v_pk_add_f32 v[20:21], v[20:21], v[22:23] neg_lo:[0,1] neg_hi:[0,1]
	ds_write_b64 v10, v[40:41]
	ds_write_b64 v13, v[24:25]
	ds_write_b64 v15, v[28:29]
	ds_write_b64 v52, v[18:19]
	ds_write_b64 v53, v[42:43]
	ds_write_b64 v54, v[46:47]
	ds_write_b64 v55, v[50:51]
	ds_write_b64 v56, v[44:45]
	ds_write_b64 v57, v[36:37]
	ds_write_b64 v58, v[26:27]
	ds_write_b64 v59, v[48:49]
	ds_write_b64 v60, v[32:33]
	ds_write_b64 v61, v[34:35]
	ds_write_b64 v62, v[30:31]
	ds_write_b64 v63, v[38:39]
	ds_write_b64 v64, v[20:21]
	v_mov_b32_e32 v10, v177
	v_mov_b32_e32 v64, v165
	v_lshlrev_b32_e32 v13, 3, v17
	v_lshlrev_b32_e32 v48, 3, v10
	v_add3_u32 v10, 0, v13, v48
	v_xor_b32_e32 v13, 1, v17
	v_xor_b32_e32 v34, 8, v17
	v_xor_b32_e32 v36, 9, v17
	v_lshlrev_b32_e32 v13, 3, v13
	v_xor_b32_e32 v15, 2, v17
	v_xor_b32_e32 v24, 3, v17
	v_xor_b32_e32 v26, 4, v17
	v_xor_b32_e32 v28, 5, v17
	v_xor_b32_e32 v30, 6, v17
	v_xor_b32_e32 v32, 7, v17
	v_lshlrev_b32_e32 v34, 3, v34
	v_lshlrev_b32_e32 v36, 3, v36
	v_xor_b32_e32 v38, 10, v17
	v_xor_b32_e32 v40, 11, v17
	v_xor_b32_e32 v42, 12, v17
	v_xor_b32_e32 v44, 13, v17
	v_xor_b32_e32 v46, 14, v17
	v_xor_b32_e32 v17, 15, v17
	v_add3_u32 v13, 0, v13, v48
	v_lshlrev_b32_e32 v15, 3, v15
	v_lshlrev_b32_e32 v24, 3, v24
	v_lshlrev_b32_e32 v26, 3, v26
	v_lshlrev_b32_e32 v28, 3, v28
	v_lshlrev_b32_e32 v30, 3, v30
	v_lshlrev_b32_e32 v32, 3, v32
	v_add3_u32 v55, 0, v34, v48
	v_add3_u32 v56, 0, v36, v48
	v_lshlrev_b32_e32 v38, 3, v38
	v_lshlrev_b32_e32 v40, 3, v40
	v_lshlrev_b32_e32 v42, 3, v42
	v_lshlrev_b32_e32 v44, 3, v44
	v_lshlrev_b32_e32 v46, 3, v46
	v_lshlrev_b32_e32 v17, 3, v17
	ds_read_b64 v[18:19], v10
	ds_read_b64 v[20:21], v13
	v_add3_u32 v15, 0, v15, v48
	v_add3_u32 v50, 0, v24, v48
	v_add3_u32 v51, 0, v26, v48
	v_add3_u32 v52, 0, v28, v48
	v_add3_u32 v53, 0, v30, v48
	v_add3_u32 v54, 0, v32, v48
	ds_read_b64 v[34:35], v55
	ds_read_b64 v[36:37], v56
	v_add3_u32 v57, 0, v38, v48
	v_add3_u32 v58, 0, v40, v48
	v_add3_u32 v59, 0, v42, v48
	v_add3_u32 v60, 0, v44, v48
	v_add3_u32 v61, 0, v46, v48
	v_add3_u32 v62, 0, v17, v48
	v_mov_b32_e32 v17, v1
	ds_read_b64 v[22:23], v15
	ds_read_b64 v[24:25], v50
	ds_read_b64 v[26:27], v51
	ds_read_b64 v[28:29], v52
	ds_read_b64 v[30:31], v53
	ds_read_b64 v[32:33], v54
	ds_read_b64 v[38:39], v57
	ds_read_b64 v[40:41], v58
	ds_read_b64 v[42:43], v59
	ds_read_b64 v[44:45], v60
	ds_read_b64 v[46:47], v61
	ds_read_b64 v[48:49], v62
	s_waitcnt lgkmcnt(13)
	v_pk_add_f32 v[70:71], v[18:19], v[34:35]
	v_mov_b32_e32 v17, v164
	v_pk_add_f32 v[18:19], v[18:19], v[34:35] neg_lo:[0,1] neg_hi:[0,1]
	v_mov_b32_e32 v17, v166
	s_waitcnt lgkmcnt(12)
	v_pk_add_f32 v[34:35], v[20:21], v[36:37]
	v_pk_add_f32 v[20:21], v[20:21], v[36:37] neg_lo:[0,1] neg_hi:[0,1]
	v_mov_b32_e32 v17, v168
	s_nop 0
	v_pk_mul_f32 v[36:37], v[20:21], v[68:69] op_sel:[1,0] op_sel_hi:[0,0] neg_lo:[1,1] neg_hi:[0,1]
	v_mov_b32_e32 v17, v170
	v_pk_fma_f32 v[20:21], v[20:21], v[64:65], v[36:37] op_sel_hi:[1,0,1]
	s_waitcnt lgkmcnt(5)
	v_pk_add_f32 v[36:37], v[22:23], v[38:39]
	v_pk_add_f32 v[22:23], v[22:23], v[38:39] neg_lo:[0,1] neg_hi:[0,1]
	s_nop 0
	v_pk_mul_f32 v[38:39], v[22:23], v[66:67] op_sel:[1,0] op_sel_hi:[0,0] neg_lo:[1,1] neg_hi:[0,1]
	v_mov_b32_e32 v17, v171
	v_pk_fma_f32 v[22:23], v[22:23], v[66:67], v[38:39] op_sel_hi:[1,0,1]
	s_waitcnt lgkmcnt(4)
	v_pk_add_f32 v[38:39], v[24:25], v[40:41]
	v_pk_add_f32 v[24:25], v[24:25], v[40:41] neg_lo:[0,1] neg_hi:[0,1]
	s_nop 0
	v_pk_mul_f32 v[40:41], v[24:25], v[68:69] op_sel_hi:[1,0]
	s_nop 0
	v_pk_fma_f32 v[24:25], v[24:25], v[64:65], v[40:41] op_sel:[1,0,0] op_sel_hi:[0,0,1] neg_lo:[1,1,0] neg_hi:[0,1,0]
	s_waitcnt lgkmcnt(3)
	v_pk_add_f32 v[40:41], v[26:27], v[42:43]
	v_pk_add_f32 v[26:27], v[26:27], v[42:43] neg_lo:[0,1] neg_hi:[0,1]
	s_nop 0
	v_xor_b32_e32 v73, 0x80000000, v26
	v_mov_b32_e32 v72, v27
	s_waitcnt lgkmcnt(2)
	v_pk_add_f32 v[26:27], v[28:29], v[44:45]
	v_pk_add_f32 v[28:29], v[28:29], v[44:45] neg_lo:[0,1] neg_hi:[0,1]
	s_nop 0
	v_pk_mul_f32 v[42:43], v[28:29], v[68:69] op_sel_hi:[1,0] neg_lo:[0,1] neg_hi:[0,1]
	s_nop 0
	v_pk_fma_f32 v[28:29], v[28:29], v[64:65], v[42:43] op_sel:[1,0,0] op_sel_hi:[0,0,1] neg_lo:[1,1,0] neg_hi:[0,1,0]
	s_waitcnt lgkmcnt(1)
	v_pk_add_f32 v[42:43], v[30:31], v[46:47]
	v_pk_add_f32 v[30:31], v[30:31], v[46:47] neg_lo:[0,1] neg_hi:[0,1]
	s_nop 0
	v_pk_mul_f32 v[44:45], v[30:31], v[66:67] op_sel:[1,0] op_sel_hi:[0,0] neg_lo:[1,1] neg_hi:[0,1]
	s_nop 0
	v_pk_fma_f32 v[30:31], v[30:31], v[66:67], v[44:45] op_sel_hi:[1,0,1] neg_lo:[0,1,0] neg_hi:[0,1,0]
	s_waitcnt lgkmcnt(0)
	v_pk_add_f32 v[44:45], v[32:33], v[48:49]
	v_pk_add_f32 v[32:33], v[32:33], v[48:49] neg_lo:[0,1] neg_hi:[0,1]
	v_pk_add_f32 v[48:49], v[34:35], v[26:27]
	v_pk_add_f32 v[26:27], v[34:35], v[26:27] neg_lo:[0,1] neg_hi:[0,1]
	s_nop 0
	v_pk_mul_f32 v[34:35], v[26:27], v[66:67] op_sel:[1,0] op_sel_hi:[0,0] neg_lo:[1,1] neg_hi:[0,1]
	v_pk_fma_f32 v[26:27], v[26:27], v[66:67], v[34:35] op_sel_hi:[1,0,1]
	v_pk_add_f32 v[34:35], v[36:37], v[42:43]
	v_pk_add_f32 v[36:37], v[36:37], v[42:43] neg_lo:[0,1] neg_hi:[0,1]
	v_pk_mul_f32 v[46:47], v[32:33], v[68:69] op_sel:[1,0] op_sel_hi:[0,0] neg_lo:[1,1] neg_hi:[0,1]
	v_xor_b32_e32 v43, 0x80000000, v36
	v_mov_b32_e32 v42, v37
	v_pk_add_f32 v[36:37], v[38:39], v[44:45]
	v_pk_add_f32 v[38:39], v[38:39], v[44:45] neg_lo:[0,1] neg_hi:[0,1]
	v_pk_fma_f32 v[46:47], v[32:33], v[64:65], v[46:47] op_sel_hi:[1,0,1] neg_lo:[0,1,0] neg_hi:[0,1,0]
	v_pk_add_f32 v[32:33], v[70:71], v[40:41]
	v_pk_mul_f32 v[44:45], v[38:39], v[66:67] op_sel:[1,0] op_sel_hi:[0,0] neg_lo:[1,1] neg_hi:[0,1]
	v_pk_add_f32 v[40:41], v[70:71], v[40:41] neg_lo:[0,1] neg_hi:[0,1]
	v_pk_fma_f32 v[38:39], v[38:39], v[66:67], v[44:45] op_sel_hi:[1,0,1] neg_lo:[0,1,0] neg_hi:[0,1,0]
	v_pk_add_f32 v[44:45], v[32:33], v[34:35]
	v_pk_add_f32 v[32:33], v[32:33], v[34:35] neg_lo:[0,1] neg_hi:[0,1]
	v_pk_add_f32 v[34:35], v[48:49], v[36:37]
	v_pk_add_f32 v[36:37], v[48:49], v[36:37] neg_lo:[0,1] neg_hi:[0,1]
	v_pk_add_f32 v[64:65], v[44:45], v[34:35]
	v_xor_b32_e32 v49, 0x80000000, v36
	v_mov_b32_e32 v48, v37
	v_pk_add_f32 v[36:37], v[44:45], v[34:35] neg_lo:[0,1] neg_hi:[0,1]
	v_pk_add_f32 v[68:69], v[32:33], v[48:49]
	v_pk_add_f32 v[44:45], v[32:33], v[48:49] neg_lo:[0,1] neg_hi:[0,1]
	v_pk_add_f32 v[32:33], v[40:41], v[42:43]
	v_pk_add_f32 v[34:35], v[40:41], v[42:43] neg_lo:[0,1] neg_hi:[0,1]
	v_pk_add_f32 v[40:41], v[26:27], v[38:39]
	v_pk_add_f32 v[26:27], v[26:27], v[38:39] neg_lo:[0,1] neg_hi:[0,1]
	v_pk_add_f32 v[42:43], v[32:33], v[40:41] neg_lo:[0,1] neg_hi:[0,1]
	v_xor_b32_e32 v39, 0x80000000, v26
	v_mov_b32_e32 v38, v27
	v_pk_add_f32 v[26:27], v[32:33], v[40:41]
	v_pk_add_f32 v[40:41], v[20:21], v[28:29]
	v_pk_add_f32 v[20:21], v[20:21], v[28:29] neg_lo:[0,1] neg_hi:[0,1]
	v_pk_add_f32 v[32:33], v[34:35], v[38:39]
	v_pk_mul_f32 v[28:29], v[66:67], v[20:21] op_sel:[0,1] op_sel_hi:[0,0] neg_lo:[1,1] neg_hi:[1,0]
	v_pk_fma_f32 v[20:21], v[66:67], v[20:21], v[28:29] op_sel_hi:[0,1,1]
	v_pk_add_f32 v[28:29], v[22:23], v[30:31]
	v_pk_add_f32 v[22:23], v[22:23], v[30:31] neg_lo:[0,1] neg_hi:[0,1]
	v_pk_add_f32 v[38:39], v[34:35], v[38:39] neg_lo:[0,1] neg_hi:[0,1]
	v_xor_b32_e32 v31, 0x80000000, v22
	v_mov_b32_e32 v30, v23
	v_pk_add_f32 v[22:23], v[24:25], v[46:47]
	v_pk_add_f32 v[24:25], v[24:25], v[46:47] neg_lo:[0,1] neg_hi:[0,1]
	v_pk_add_f32 v[34:35], v[18:19], v[72:73]
	v_pk_mul_f32 v[46:47], v[66:67], v[24:25] op_sel:[0,1] op_sel_hi:[0,0] neg_lo:[1,1] neg_hi:[1,0]
	v_pk_fma_f32 v[24:25], v[66:67], v[24:25], v[46:47] op_sel_hi:[0,1,1] neg_lo:[1,0,0] neg_hi:[1,0,0]
	v_pk_add_f32 v[46:47], v[34:35], v[28:29]
	v_pk_add_f32 v[28:29], v[34:35], v[28:29] neg_lo:[0,1] neg_hi:[0,1]
	v_pk_add_f32 v[34:35], v[40:41], v[22:23]
	v_pk_add_f32 v[22:23], v[40:41], v[22:23] neg_lo:[0,1] neg_hi:[0,1]
	v_pk_add_f32 v[18:19], v[18:19], v[72:73] neg_lo:[0,1] neg_hi:[0,1]
	v_pk_add_f32 v[66:67], v[28:29], v[22:23] op_sel:[0,1] op_sel_hi:[1,0] neg_hi:[0,1]
	v_pk_add_f32 v[48:49], v[28:29], v[22:23] op_sel:[0,1] op_sel_hi:[1,0] neg_lo:[0,1]
	v_pk_add_f32 v[28:29], v[18:19], v[30:31]
	v_pk_add_f32 v[18:19], v[18:19], v[30:31] neg_lo:[0,1] neg_hi:[0,1]
	v_pk_add_f32 v[30:31], v[20:21], v[24:25]
	v_pk_add_f32 v[20:21], v[20:21], v[24:25] neg_lo:[0,1] neg_hi:[0,1]
	v_pk_add_f32 v[22:23], v[46:47], v[34:35]
	v_xor_b32_e32 v25, 0x80000000, v20
	v_add_u32_e32 v20, 0x2000, v16
	v_mov_b32_e32 v24, v21
	v_ashrrev_i32_e32 v21, 31, v20
	v_lshl_add_u64 v[20:21], v[20:21], 3, s[46:47]
	s_waitcnt vmcnt(0)
	v_pk_add_f32 v[40:41], v[46:47], v[34:35] neg_lo:[0,1] neg_hi:[0,1]
	v_pk_add_f32 v[34:35], v[18:19], v[24:25]
	v_pk_add_f32 v[18:19], v[18:19], v[24:25] neg_lo:[0,1] neg_hi:[0,1]
	v_pk_add_f32 v[70:71], v[28:29], v[30:31]
	v_pk_add_f32 v[46:47], v[28:29], v[30:31] neg_lo:[0,1] neg_hi:[0,1]
	s_nop 0
	v_pk_mul_f32 v[24:25], v[64:65], v[202:203] op_sel:[1,1] op_sel_hi:[1,0] neg_lo:[1,0]
	s_nop 0
	v_pk_fma_f32 v[20:21], v[64:65], v[202:203], v[24:25] op_sel_hi:[0,1,1]
	v_add_u32_e32 v24, 0x2200, v16
	v_ashrrev_i32_e32 v25, 31, v24
	v_lshl_add_u64 v[24:25], v[24:25], 3, s[46:47]
	s_nop 0
	v_pk_mul_f32 v[28:29], v[204:205], v[22:23] op_sel:[1,1] op_sel_hi:[0,1] neg_lo:[0,1]
	v_pk_fma_f32 v[22:23], v[204:205], v[22:23], v[28:29] op_sel_hi:[1,0,1]
	v_add_u32_e32 v24, 0x2400, v16
	v_ashrrev_i32_e32 v25, 31, v24
	v_lshl_add_u64 v[24:25], v[24:25], 3, s[46:47]
	s_nop 0
	v_pk_mul_f32 v[28:29], v[26:27], v[206:207] op_sel:[1,1] op_sel_hi:[1,0] neg_lo:[1,0]
	s_nop 0
	v_pk_fma_f32 v[24:25], v[26:27], v[206:207], v[28:29] op_sel_hi:[0,1,1]
	v_add_u32_e32 v26, 0x2600, v16
	v_ashrrev_i32_e32 v27, 31, v26
	v_lshl_add_u64 v[26:27], v[26:27], 3, s[46:47]
	s_nop 0
	v_pk_mul_f32 v[28:29], v[208:209], v[70:71] op_sel:[1,1] op_sel_hi:[0,1] neg_lo:[0,1]
	v_pk_fma_f32 v[26:27], v[208:209], v[70:71], v[28:29] op_sel_hi:[1,0,1]
	v_add_u32_e32 v28, 0x2800, v16
	v_ashrrev_i32_e32 v29, 31, v28
	v_lshl_add_u64 v[28:29], v[28:29], 3, s[46:47]
	s_nop 0
	v_pk_mul_f32 v[30:31], v[68:69], v[210:211] op_sel:[1,1] op_sel_hi:[1,0] neg_lo:[1,0]
	s_nop 0
	v_pk_fma_f32 v[28:29], v[68:69], v[210:211], v[30:31] op_sel_hi:[0,1,1]
	v_add_u32_e32 v30, 0x2a00, v16
	v_ashrrev_i32_e32 v31, 31, v30
	v_lshl_add_u64 v[30:31], v[30:31], 3, s[46:47]
	s_nop 0
	v_pk_mul_f32 v[64:65], v[212:213], v[66:67] op_sel:[1,1] op_sel_hi:[0,1] neg_lo:[0,1]
	v_pk_fma_f32 v[30:31], v[212:213], v[66:67], v[64:65] op_sel_hi:[1,0,1]
	v_add_u32_e32 v64, 0x2c00, v16
	v_ashrrev_i32_e32 v65, 31, v64
	v_lshl_add_u64 v[64:65], v[64:65], 3, s[46:47]
	s_nop 0
	v_pk_mul_f32 v[66:67], v[32:33], v[214:215] op_sel:[1,1] op_sel_hi:[1,0] neg_lo:[1,0]
	s_nop 0
	v_pk_fma_f32 v[32:33], v[32:33], v[214:215], v[66:67] op_sel_hi:[0,1,1]
	v_add_u32_e32 v64, 0x2e00, v16
	v_ashrrev_i32_e32 v65, 31, v64
	v_lshl_add_u64 v[64:65], v[64:65], 3, s[46:47]
	s_nop 0
	v_pk_mul_f32 v[66:67], v[216:217], v[34:35] op_sel:[1,1] op_sel_hi:[0,1] neg_lo:[0,1]
	v_pk_fma_f32 v[34:35], v[216:217], v[34:35], v[66:67] op_sel_hi:[1,0,1]
	v_add_u32_e32 v64, 0x3000, v16
	v_ashrrev_i32_e32 v65, 31, v64
	v_lshl_add_u64 v[64:65], v[64:65], 3, s[46:47]
	s_nop 0
	v_pk_mul_f32 v[66:67], v[36:37], v[218:219] op_sel:[1,1] op_sel_hi:[1,0] neg_lo:[1,0]
	s_nop 0
	v_pk_fma_f32 v[36:37], v[36:37], v[218:219], v[66:67] op_sel_hi:[0,1,1]
	v_add_u32_e32 v64, 0x3200, v16
	v_ashrrev_i32_e32 v65, 31, v64
	v_lshl_add_u64 v[64:65], v[64:65], 3, s[46:47]
	v_pk_add_f32 v[68:69], v[20:21], v[36:37]
	v_pk_add_f32 v[20:21], v[20:21], v[36:37] neg_lo:[0,1] neg_hi:[0,1]
	s_nop 0
	v_pk_mul_f32 v[66:67], v[40:41], v[220:221] op_sel:[1,1] op_sel_hi:[1,0] neg_lo:[1,0]
	s_nop 0
	v_pk_fma_f32 v[40:41], v[40:41], v[220:221], v[66:67] op_sel_hi:[0,1,1]
	v_add_u32_e32 v64, 0x3400, v16
	v_ashrrev_i32_e32 v65, 31, v64
	v_lshl_add_u64 v[64:65], v[64:65], 3, s[46:47]
	v_pk_add_f32 v[36:37], v[22:23], v[40:41]
	v_pk_add_f32 v[22:23], v[22:23], v[40:41] neg_lo:[0,1] neg_hi:[0,1]
	s_nop 0
	v_pk_mul_f32 v[66:67], v[42:43], v[222:223] op_sel:[1,1] op_sel_hi:[1,0] neg_lo:[1,0]
	s_nop 0
	v_pk_fma_f32 v[42:43], v[42:43], v[222:223], v[66:67] op_sel_hi:[0,1,1]
	v_add_u32_e32 v64, 0x3600, v16
	v_ashrrev_i32_e32 v65, 31, v64
	v_lshl_add_u64 v[64:65], v[64:65], 3, s[46:47]
	s_nop 0
	v_pk_mul_f32 v[66:67], v[46:47], v[224:225] op_sel:[1,1] op_sel_hi:[1,0] neg_lo:[1,0]
	s_nop 0
	v_pk_fma_f32 v[46:47], v[46:47], v[224:225], v[66:67] op_sel_hi:[0,1,1]
	v_add_u32_e32 v64, 0x3800, v16
	v_ashrrev_i32_e32 v65, 31, v64
	v_lshl_add_u64 v[64:65], v[64:65], 3, s[46:47]
	s_nop 0
	v_pk_mul_f32 v[66:67], v[44:45], v[226:227] op_sel:[1,1] op_sel_hi:[1,0] neg_lo:[1,0]
	s_nop 0
	v_pk_fma_f32 v[44:45], v[44:45], v[226:227], v[66:67] op_sel_hi:[0,1,1]
	v_add_u32_e32 v64, 0x3a00, v16
	v_ashrrev_i32_e32 v65, 31, v64
	v_lshl_add_u64 v[64:65], v[64:65], 3, s[46:47]
	s_nop 0
	v_pk_mul_f32 v[66:67], v[48:49], v[228:229] op_sel:[1,1] op_sel_hi:[1,0] neg_lo:[1,0]
	s_nop 0
	v_pk_fma_f32 v[48:49], v[48:49], v[228:229], v[66:67] op_sel_hi:[0,1,1]
	v_add_u32_e32 v64, 0x3c00, v16
	v_ashrrev_i32_e32 v65, 31, v64
	v_lshl_add_u64 v[64:65], v[64:65], 3, s[46:47]
	v_add_u32_e32 v16, 0x3e00, v16
	v_ashrrev_i32_e32 v17, 31, v16
	v_lshl_add_u64 v[16:17], v[16:17], 3, s[46:47]
	s_nop 0
	v_pk_mul_f32 v[66:67], v[38:39], v[230:231] op_sel:[1,1] op_sel_hi:[1,0] neg_lo:[1,0]
	s_nop 0
	v_pk_fma_f32 v[38:39], v[38:39], v[230:231], v[66:67] op_sel_hi:[0,1,1]
	s_nop 0
	v_pk_mul_f32 v[64:65], v[18:19], v[232:233] op_sel:[1,1] op_sel_hi:[1,0] neg_lo:[1,0]
	v_mov_b32_e32 v66, v169
	v_pk_fma_f32 v[16:17], v[18:19], v[232:233], v[64:65] op_sel_hi:[0,1,1]
	v_mov_b32_e32 v18, v1
	v_mov_b32_e32 v19, v166
	v_mov_b32_e32 v18, v164
	v_mov_b32_e32 v64, v167
	v_mov_b32_e32 v18, v165
	s_nop 0
	v_mov_b32_e32 v19, v168
	s_nop 0
	v_mov_b32_e32 v19, v170
	v_pk_mul_f32 v[40:41], v[22:23], v[66:67] op_sel:[1,0] op_sel_hi:[0,0] neg_lo:[1,0]
	v_mov_b32_e32 v19, v171
	s_nop 0
	v_pk_fma_f32 v[22:23], v[22:23], v[18:19], v[40:41] op_sel_hi:[1,0,1]
	v_pk_add_f32 v[40:41], v[24:25], v[42:43]
	v_pk_add_f32 v[24:25], v[24:25], v[42:43] neg_lo:[0,1] neg_hi:[0,1]
	s_nop 0
	v_pk_mul_f32 v[42:43], v[24:25], v[64:65] op_sel:[1,0] op_sel_hi:[0,0] neg_lo:[1,0]
	s_nop 0
	v_pk_fma_f32 v[24:25], v[24:25], v[64:65], v[42:43] op_sel_hi:[1,0,1]
	v_pk_add_f32 v[42:43], v[26:27], v[46:47]
	v_pk_add_f32 v[26:27], v[26:27], v[46:47] neg_lo:[0,1] neg_hi:[0,1]
	s_nop 0
	v_pk_mul_f32 v[46:47], v[26:27], v[66:67] op_sel_hi:[1,0]
	s_nop 0
	v_pk_fma_f32 v[26:27], v[26:27], v[18:19], v[46:47] op_sel:[1,0,0] op_sel_hi:[0,0,1] neg_lo:[1,0,0]
	v_pk_add_f32 v[46:47], v[28:29], v[44:45]
	v_pk_add_f32 v[28:29], v[28:29], v[44:45] neg_lo:[0,1] neg_hi:[0,1]
	s_nop 0
	v_xor_b32_e32 v44, 0x80000000, v29
	v_mov_b32_e32 v45, v28
	v_pk_add_f32 v[28:29], v[30:31], v[48:49]
	v_pk_add_f32 v[30:31], v[30:31], v[48:49] neg_lo:[0,1] neg_hi:[0,1]
	s_nop 0
	v_pk_mul_f32 v[48:49], v[30:31], v[66:67] op_sel_hi:[1,0] neg_lo:[0,1] neg_hi:[0,1]
	s_nop 0
	v_pk_fma_f32 v[30:31], v[30:31], v[18:19], v[48:49] op_sel:[1,0,0] op_sel_hi:[0,0,1] neg_lo:[1,0,0]
	v_pk_add_f32 v[48:49], v[32:33], v[38:39]
	v_pk_add_f32 v[32:33], v[32:33], v[38:39] neg_lo:[0,1] neg_hi:[0,1]
	s_nop 0
	v_pk_mul_f32 v[38:39], v[32:33], v[64:65] op_sel:[1,0] op_sel_hi:[0,0] neg_lo:[1,0]
	s_nop 0
	v_pk_fma_f32 v[32:33], v[32:33], v[64:65], v[38:39] op_sel_hi:[1,0,1] neg_lo:[0,1,0] neg_hi:[0,1,0]
	v_pk_add_f32 v[38:39], v[34:35], v[16:17]
	v_pk_add_f32 v[16:17], v[34:35], v[16:17] neg_lo:[0,1] neg_hi:[0,1]
	s_nop 0
	v_pk_mul_f32 v[34:35], v[16:17], v[66:67] op_sel:[1,0] op_sel_hi:[0,0] neg_lo:[1,0]
	s_nop 0
	v_pk_fma_f32 v[16:17], v[16:17], v[18:19], v[34:35] op_sel_hi:[1,0,1] neg_lo:[0,1,0] neg_hi:[0,1,0]
	v_pk_add_f32 v[18:19], v[68:69], v[46:47]
	v_pk_add_f32 v[34:35], v[68:69], v[46:47] neg_lo:[0,1] neg_hi:[0,1]
	v_pk_add_f32 v[46:47], v[36:37], v[28:29]
	v_pk_add_f32 v[28:29], v[36:37], v[28:29] neg_lo:[0,1] neg_hi:[0,1]
	s_nop 0
	v_pk_mul_f32 v[36:37], v[28:29], v[64:65] op_sel:[1,0] op_sel_hi:[0,0] neg_lo:[1,0]
	s_nop 0
	v_pk_fma_f32 v[28:29], v[28:29], v[64:65], v[36:37] op_sel_hi:[1,0,1]
	v_pk_add_f32 v[36:37], v[40:41], v[48:49]
	v_pk_add_f32 v[40:41], v[40:41], v[48:49] neg_lo:[0,1] neg_hi:[0,1]
	s_nop 0
	v_xor_b32_e32 v48, 0x80000000, v41
	v_mov_b32_e32 v49, v40
	v_pk_add_f32 v[40:41], v[42:43], v[38:39]
	v_pk_add_f32 v[38:39], v[42:43], v[38:39] neg_lo:[0,1] neg_hi:[0,1]
	s_nop 0
	v_pk_mul_f32 v[42:43], v[64:65], v[38:39] op_sel:[0,1] op_sel_hi:[0,0] neg_lo:[0,1]
	v_pk_fma_f32 v[38:39], v[38:39], v[64:65], v[42:43] op_sel_hi:[1,0,1] neg_lo:[0,1,0] neg_hi:[0,1,0]
	v_pk_add_f32 v[42:43], v[18:19], v[36:37]
	v_pk_add_f32 v[18:19], v[18:19], v[36:37] neg_lo:[0,1] neg_hi:[0,1]
	v_pk_add_f32 v[36:37], v[46:47], v[40:41]
	v_pk_add_f32 v[40:41], v[46:47], v[40:41] neg_lo:[0,1] neg_hi:[0,1]
	s_nop 0
	v_xor_b32_e32 v46, 0x80000000, v41
	v_mov_b32_e32 v47, v40
	v_pk_add_f32 v[40:41], v[42:43], v[36:37]
	v_pk_add_f32 v[36:37], v[42:43], v[36:37] neg_lo:[0,1] neg_hi:[0,1]
	v_pk_add_f32 v[42:43], v[18:19], v[46:47]
	v_pk_add_f32 v[18:19], v[18:19], v[46:47] neg_lo:[0,1] neg_hi:[0,1]
	v_pk_add_f32 v[46:47], v[34:35], v[48:49]
	v_pk_add_f32 v[34:35], v[34:35], v[48:49] neg_lo:[0,1] neg_hi:[0,1]
	v_pk_add_f32 v[48:49], v[28:29], v[38:39]
	v_pk_add_f32 v[28:29], v[28:29], v[38:39] neg_lo:[0,1] neg_hi:[0,1]
	s_nop 0
	v_xor_b32_e32 v38, 0x80000000, v29
	v_mov_b32_e32 v39, v28
	v_pk_add_f32 v[28:29], v[46:47], v[48:49]
	v_pk_add_f32 v[46:47], v[46:47], v[48:49] neg_lo:[0,1] neg_hi:[0,1]
	v_pk_add_f32 v[48:49], v[34:35], v[38:39]
	v_pk_add_f32 v[34:35], v[34:35], v[38:39] neg_lo:[0,1] neg_hi:[0,1]
	v_pk_add_f32 v[38:39], v[20:21], v[44:45]
	v_pk_add_f32 v[20:21], v[20:21], v[44:45] neg_lo:[0,1] neg_hi:[0,1]
	v_pk_add_f32 v[44:45], v[22:23], v[30:31]
	v_pk_add_f32 v[22:23], v[22:23], v[30:31] neg_lo:[0,1] neg_hi:[0,1]
	s_nop 0
	v_pk_mul_f32 v[30:31], v[64:65], v[22:23] op_sel:[0,1] op_sel_hi:[0,0] neg_lo:[0,1]
	v_pk_fma_f32 v[22:23], v[64:65], v[22:23], v[30:31] op_sel_hi:[0,1,1]
	v_pk_add_f32 v[30:31], v[24:25], v[32:33]
	v_pk_add_f32 v[24:25], v[24:25], v[32:33] neg_lo:[0,1] neg_hi:[0,1]
	s_nop 0
	v_xor_b32_e32 v32, 0x80000000, v25
	v_mov_b32_e32 v33, v24
	v_pk_add_f32 v[24:25], v[26:27], v[16:17]
	v_pk_add_f32 v[16:17], v[26:27], v[16:17] neg_lo:[0,1] neg_hi:[0,1]
	s_nop 0
	v_pk_mul_f32 v[26:27], v[64:65], v[16:17] op_sel:[0,1] op_sel_hi:[0,0] neg_lo:[0,1]
	v_pk_fma_f32 v[16:17], v[64:65], v[16:17], v[26:27] op_sel_hi:[0,1,1] neg_lo:[1,0,0] neg_hi:[1,0,0]
	v_pk_add_f32 v[26:27], v[38:39], v[30:31]
	v_pk_add_f32 v[30:31], v[38:39], v[30:31] neg_lo:[0,1] neg_hi:[0,1]
	v_pk_add_f32 v[38:39], v[44:45], v[24:25]
	v_pk_add_f32 v[24:25], v[44:45], v[24:25] neg_lo:[0,1] neg_hi:[0,1]
	s_nop 0
	v_xor_b32_e32 v44, 0x80000000, v25
	v_mov_b32_e32 v45, v24
	v_pk_add_f32 v[24:25], v[26:27], v[38:39]
	v_pk_add_f32 v[26:27], v[26:27], v[38:39] neg_lo:[0,1] neg_hi:[0,1]
	v_pk_add_f32 v[38:39], v[30:31], v[44:45]
	v_pk_add_f32 v[30:31], v[30:31], v[44:45] neg_lo:[0,1] neg_hi:[0,1]
	v_pk_add_f32 v[44:45], v[20:21], v[32:33]
	v_pk_add_f32 v[20:21], v[20:21], v[32:33] neg_lo:[0,1] neg_hi:[0,1]
	v_pk_add_f32 v[32:33], v[22:23], v[16:17]
	v_pk_add_f32 v[16:17], v[22:23], v[16:17] neg_lo:[0,1] neg_hi:[0,1]
	s_nop 0
	v_xor_b32_e32 v22, 0x80000000, v17
	v_mov_b32_e32 v23, v16
	v_pk_add_f32 v[16:17], v[44:45], v[32:33]
	v_pk_add_f32 v[32:33], v[44:45], v[32:33] neg_lo:[0,1] neg_hi:[0,1]
	v_pk_add_f32 v[44:45], v[20:21], v[22:23]
	v_pk_add_f32 v[20:21], v[20:21], v[22:23] neg_lo:[0,1] neg_hi:[0,1]
	ds_write_b64 v10, v[40:41]
	ds_write_b64 v13, v[24:25]
	ds_write_b64 v15, v[28:29]
	ds_write_b64 v50, v[16:17]
	ds_write_b64 v51, v[42:43]
	ds_write_b64 v52, v[38:39]
	ds_write_b64 v53, v[48:49]
	ds_write_b64 v54, v[44:45]
	ds_write_b64 v55, v[36:37]
	ds_write_b64 v56, v[26:27]
	ds_write_b64 v57, v[46:47]
	ds_write_b64 v58, v[32:33]
	ds_write_b64 v59, v[18:19]
	ds_write_b64 v60, v[30:31]
	ds_write_b64 v61, v[34:35]
	ds_write_b64 v62, v[20:21]
	v_mov_b32_e32 v10, v174
	v_mov_b32_e32 v50, v172
	s_waitcnt lgkmcnt(0)
	s_barrier
	v_add_u32_e32 v13, v50, v10
	v_lshl_add_u32 v13, v13, 3, 0
	ds_read2_b64 v[16:19], v13 offset1:16
	v_xad_u32 v15, v50, 1, v10
	v_lshl_add_u32 v15, v15, 3, 0
	s_waitcnt lgkmcnt(0)
	v_pk_fma_f32 v[16:17], v[16:17], 0, v[16:17] op_sel:[1,0,0] op_sel_hi:[0,0,1] neg_hi:[1,0,0]
	v_pk_fma_f32 v[22:23], v[180:181], s[90:91], v[180:181] op_sel:[1,0,0] op_sel_hi:[0,1,1]
	v_pk_mul_f32 v[24:25], v[22:23], v[18:19] op_sel:[1,1] op_sel_hi:[1,0] neg_hi:[0,1]
	s_nop 0
	v_pk_fma_f32 v[18:19], v[18:19], v[22:23], v[24:25] op_sel_hi:[1,0,1]
	v_pk_mul_f32 v[24:25], v[180:181], v[22:23] op_sel:[1,1] op_sel_hi:[0,1] neg_lo:[0,1]
	v_pk_fma_f32 v[26:27], v[180:181], v[22:23], v[24:25] op_sel_hi:[1,0,1]
	ds_read2_b64 v[22:25], v15 offset0:32 offset1:48
	s_waitcnt lgkmcnt(0)
	v_pk_mul_f32 v[28:29], v[22:23], v[26:27] op_sel:[1,1] op_sel_hi:[0,1] neg_hi:[1,0]
	s_nop 0
	v_pk_fma_f32 v[22:23], v[22:23], v[26:27], v[28:29] op_sel_hi:[1,0,1]
	v_pk_mul_f32 v[28:29], v[180:181], v[26:27] op_sel:[1,1] op_sel_hi:[0,1] neg_lo:[0,1]
	v_pk_fma_f32 v[26:27], v[180:181], v[26:27], v[28:29] op_sel_hi:[1,0,1]
	s_nop 0
	v_pk_mul_f32 v[28:29], v[24:25], v[26:27] op_sel:[1,1] op_sel_hi:[0,1] neg_hi:[1,0]
	s_nop 0
	v_pk_fma_f32 v[24:25], v[24:25], v[26:27], v[28:29] op_sel_hi:[1,0,1]
	v_pk_mul_f32 v[28:29], v[180:181], v[26:27] op_sel:[1,1] op_sel_hi:[0,1] neg_lo:[0,1]
	v_pk_fma_f32 v[26:27], v[180:181], v[26:27], v[28:29] op_sel_hi:[1,0,1]
	v_xad_u32 v28, v50, 2, v10
	v_lshl_add_u32 v51, v28, 3, 0
	ds_read2_b64 v[28:31], v51 offset0:64 offset1:80
	v_pk_mul_f32 v[32:33], v[180:181], v[26:27] op_sel:[1,1] op_sel_hi:[0,1] neg_lo:[0,1]
	s_waitcnt lgkmcnt(0)
	v_pk_mul_f32 v[34:35], v[28:29], v[26:27] op_sel:[1,1] op_sel_hi:[0,1] neg_hi:[1,0]
	s_nop 0
	v_pk_fma_f32 v[28:29], v[28:29], v[26:27], v[34:35] op_sel_hi:[1,0,1]
	v_pk_fma_f32 v[34:35], v[180:181], v[26:27], v[32:33] op_sel_hi:[1,0,1]
	s_nop 0
	v_pk_mul_f32 v[26:27], v[30:31], v[34:35] op_sel:[1,1] op_sel_hi:[0,1] neg_hi:[1,0]
	v_pk_fma_f32 v[26:27], v[30:31], v[34:35], v[26:27] op_sel_hi:[1,0,1]
	v_xad_u32 v30, v50, 3, v10
	v_lshl_add_u32 v54, v30, 3, 0
	ds_read2_b64 v[30:33], v54 offset0:96 offset1:112
	v_pk_mul_f32 v[36:37], v[180:181], v[34:35] op_sel:[1,1] op_sel_hi:[0,1] neg_lo:[0,1]
	v_pk_fma_f32 v[34:35], v[180:181], v[34:35], v[36:37] op_sel_hi:[1,0,1]
	s_waitcnt lgkmcnt(0)
	v_pk_mul_f32 v[36:37], v[30:31], v[34:35] op_sel:[1,1] op_sel_hi:[0,1] neg_hi:[1,0]
	s_nop 0
	v_pk_fma_f32 v[30:31], v[30:31], v[34:35], v[36:37] op_sel_hi:[1,0,1]
	v_pk_mul_f32 v[36:37], v[180:181], v[34:35] op_sel:[1,1] op_sel_hi:[0,1] neg_lo:[0,1]
	v_pk_fma_f32 v[34:35], v[180:181], v[34:35], v[36:37] op_sel_hi:[1,0,1]
	s_nop 0
	v_pk_mul_f32 v[36:37], v[32:33], v[34:35] op_sel:[1,1] op_sel_hi:[0,1] neg_hi:[1,0]
	s_nop 0
	v_pk_fma_f32 v[32:33], v[32:33], v[34:35], v[36:37] op_sel_hi:[1,0,1]
	v_pk_mul_f32 v[36:37], v[180:181], v[34:35] op_sel:[1,1] op_sel_hi:[0,1] neg_lo:[0,1]
	v_pk_fma_f32 v[38:39], v[180:181], v[34:35], v[36:37] op_sel_hi:[1,0,1]
	v_xad_u32 v34, v50, 4, v10
	v_lshl_add_u32 v55, v34, 3, 0
	ds_read2_b64 v[34:37], v55 offset0:128 offset1:144
	v_pk_mul_f32 v[40:41], v[180:181], v[38:39] op_sel:[1,1] op_sel_hi:[0,1] neg_lo:[0,1]
	s_waitcnt lgkmcnt(0)
	v_pk_mul_f32 v[42:43], v[34:35], v[38:39] op_sel:[1,1] op_sel_hi:[0,1] neg_hi:[1,0]
	s_nop 0
	v_pk_fma_f32 v[34:35], v[34:35], v[38:39], v[42:43] op_sel_hi:[1,0,1]
	v_pk_fma_f32 v[42:43], v[180:181], v[38:39], v[40:41] op_sel_hi:[1,0,1]
	s_nop 0
	v_pk_mul_f32 v[38:39], v[36:37], v[42:43] op_sel:[1,1] op_sel_hi:[0,1] neg_hi:[1,0]
	v_pk_fma_f32 v[36:37], v[36:37], v[42:43], v[38:39] op_sel_hi:[1,0,1]
	v_xad_u32 v38, v50, 5, v10
	v_lshl_add_u32 v56, v38, 3, 0
	ds_read2_b64 v[38:41], v56 offset0:160 offset1:176
	v_pk_mul_f32 v[44:45], v[180:181], v[42:43] op_sel:[1,1] op_sel_hi:[0,1] neg_lo:[0,1]
	v_pk_fma_f32 v[42:43], v[180:181], v[42:43], v[44:45] op_sel_hi:[1,0,1]
	s_waitcnt lgkmcnt(0)
	v_pk_mul_f32 v[44:45], v[38:39], v[42:43] op_sel:[1,1] op_sel_hi:[0,1] neg_hi:[1,0]
	s_nop 0
	v_pk_fma_f32 v[38:39], v[38:39], v[42:43], v[44:45] op_sel_hi:[1,0,1]
	v_pk_mul_f32 v[44:45], v[180:181], v[42:43] op_sel:[1,1] op_sel_hi:[0,1] neg_lo:[0,1]
	v_pk_fma_f32 v[42:43], v[180:181], v[42:43], v[44:45] op_sel_hi:[1,0,1]
	s_nop 0
	v_pk_mul_f32 v[44:45], v[40:41], v[42:43] op_sel:[1,1] op_sel_hi:[0,1] neg_hi:[1,0]
	s_nop 0
	v_pk_fma_f32 v[40:41], v[40:41], v[42:43], v[44:45] op_sel_hi:[1,0,1]
	v_pk_mul_f32 v[44:45], v[180:181], v[42:43] op_sel:[1,1] op_sel_hi:[0,1] neg_lo:[0,1]
	v_pk_fma_f32 v[42:43], v[180:181], v[42:43], v[44:45] op_sel_hi:[1,0,1]
	v_xad_u32 v44, v50, 6, v10
	v_lshl_add_u32 v57, v44, 3, 0
	ds_read2_b64 v[44:47], v57 offset0:192 offset1:208
	v_pk_mul_f32 v[48:49], v[180:181], v[42:43] op_sel:[1,1] op_sel_hi:[0,1] neg_lo:[0,1]
	s_waitcnt lgkmcnt(0)
	v_pk_mul_f32 v[52:53], v[44:45], v[42:43] op_sel:[1,1] op_sel_hi:[0,1] neg_hi:[1,0]
	s_nop 0
	v_pk_fma_f32 v[44:45], v[44:45], v[42:43], v[52:53] op_sel_hi:[1,0,1]
	v_pk_fma_f32 v[52:53], v[180:181], v[42:43], v[48:49] op_sel_hi:[1,0,1]
	s_nop 0
	v_pk_mul_f32 v[42:43], v[46:47], v[52:53] op_sel:[1,1] op_sel_hi:[0,1] neg_hi:[1,0]
	v_pk_fma_f32 v[42:43], v[46:47], v[52:53], v[42:43] op_sel_hi:[1,0,1]
	v_xad_u32 v46, v50, 7, v10
	v_lshl_add_u32 v58, v46, 3, 0
	ds_read2_b64 v[46:49], v58 offset0:224 offset1:240
	v_pk_mul_f32 v[60:61], v[180:181], v[52:53] op_sel:[1,1] op_sel_hi:[0,1] neg_lo:[0,1]
	v_pk_fma_f32 v[52:53], v[180:181], v[52:53], v[60:61] op_sel_hi:[1,0,1]
	s_waitcnt lgkmcnt(0)
	v_pk_mul_f32 v[60:61], v[46:47], v[52:53] op_sel:[1,1] op_sel_hi:[0,1] neg_hi:[1,0]
	s_nop 0
	v_pk_fma_f32 v[46:47], v[46:47], v[52:53], v[60:61] op_sel_hi:[1,0,1]
	v_pk_mul_f32 v[60:61], v[180:181], v[52:53] op_sel:[1,1] op_sel_hi:[0,1] neg_lo:[0,1]
	v_pk_fma_f32 v[52:53], v[180:181], v[52:53], v[60:61] op_sel_hi:[1,0,1]
	s_nop 0
	v_pk_mul_f32 v[60:61], v[48:49], v[52:53] op_sel:[1,1] op_sel_hi:[0,1] neg_hi:[1,0]
	s_nop 0
	v_pk_fma_f32 v[48:49], v[48:49], v[52:53], v[60:61] op_sel_hi:[1,0,1]
	v_pk_mul_f32 v[60:61], v[180:181], v[52:53] op_sel:[1,1] op_sel_hi:[0,1] neg_lo:[0,1]
	v_pk_fma_f32 v[64:65], v[180:181], v[52:53], v[60:61] op_sel_hi:[1,0,1]
	v_xad_u32 v52, v50, 8, v10
	v_lshl_add_u32 v52, v52, 3, 0
	v_add_u32_e32 v59, 0x800, v52
	ds_read2_b64 v[60:63], v59 offset1:16
	v_pk_mul_f32 v[66:67], v[180:181], v[64:65] op_sel:[1,1] op_sel_hi:[0,1] neg_lo:[0,1]
	v_pk_fma_f32 v[66:67], v[180:181], v[64:65], v[66:67] op_sel_hi:[1,0,1]
	s_waitcnt lgkmcnt(0)
	v_pk_mul_f32 v[52:53], v[60:61], v[64:65] op_sel:[1,1] op_sel_hi:[0,1] neg_hi:[1,0]
	v_pk_fma_f32 v[52:53], v[60:61], v[64:65], v[52:53] op_sel_hi:[1,0,1]
	v_pk_mul_f32 v[60:61], v[62:63], v[66:67] op_sel:[1,1] op_sel_hi:[0,1] neg_hi:[1,0]
	v_pk_fma_f32 v[70:71], v[62:63], v[66:67], v[60:61] op_sel_hi:[1,0,1]
	v_xad_u32 v60, v50, 9, v10
	v_lshl_add_u32 v60, v60, 3, 0
	v_add_u32_e32 v60, 0x800, v60
	ds_read2_b64 v[62:65], v60 offset0:32 offset1:48
	v_pk_mul_f32 v[68:69], v[180:181], v[66:67] op_sel:[1,1] op_sel_hi:[0,1] neg_lo:[0,1]
	v_pk_fma_f32 v[66:67], v[180:181], v[66:67], v[68:69] op_sel_hi:[1,0,1]
	s_waitcnt lgkmcnt(0)
	v_pk_mul_f32 v[68:69], v[62:63], v[66:67] op_sel:[1,1] op_sel_hi:[0,1] neg_hi:[1,0]
	s_nop 0
	v_pk_fma_f32 v[72:73], v[62:63], v[66:67], v[68:69] op_sel_hi:[1,0,1]
	v_pk_mul_f32 v[62:63], v[180:181], v[66:67] op_sel:[1,1] op_sel_hi:[0,1] neg_lo:[0,1]
	v_pk_fma_f32 v[62:63], v[180:181], v[66:67], v[62:63] op_sel_hi:[1,0,1]
	s_nop 0
	v_pk_mul_f32 v[66:67], v[64:65], v[62:63] op_sel:[1,1] op_sel_hi:[0,1] neg_hi:[1,0]
	s_nop 0
	v_pk_fma_f32 v[74:75], v[64:65], v[62:63], v[66:67] op_sel_hi:[1,0,1]
	v_pk_mul_f32 v[64:65], v[180:181], v[62:63] op_sel:[1,1] op_sel_hi:[0,1] neg_lo:[0,1]
	v_pk_fma_f32 v[66:67], v[180:181], v[62:63], v[64:65] op_sel_hi:[1,0,1]
	v_xad_u32 v61, v50, 10, v10
	v_lshl_add_u32 v61, v61, 3, 0
	v_add_u32_e32 v61, 0x800, v61
	ds_read2_b64 v[62:65], v61 offset0:64 offset1:80
	v_pk_mul_f32 v[68:69], v[180:181], v[66:67] op_sel:[1,1] op_sel_hi:[0,1] neg_lo:[0,1]
	v_pk_fma_f32 v[68:69], v[180:181], v[66:67], v[68:69] op_sel_hi:[1,0,1]
	s_waitcnt lgkmcnt(0)
	v_pk_mul_f32 v[76:77], v[62:63], v[66:67] op_sel:[1,1] op_sel_hi:[0,1] neg_hi:[1,0]
	v_pk_fma_f32 v[76:77], v[62:63], v[66:67], v[76:77] op_sel_hi:[1,0,1]
	v_pk_mul_f32 v[62:63], v[64:65], v[68:69] op_sel:[1,1] op_sel_hi:[0,1] neg_hi:[1,0]
	v_pk_fma_f32 v[78:79], v[64:65], v[68:69], v[62:63] op_sel_hi:[1,0,1]
	v_xad_u32 v62, v50, 11, v10
	v_lshl_add_u32 v62, v62, 3, 0
	v_add_u32_e32 v62, 0x800, v62
	ds_read2_b64 v[64:67], v62 offset0:96 offset1:112
	v_pk_mul_f32 v[80:81], v[180:181], v[68:69] op_sel:[1,1] op_sel_hi:[0,1] neg_lo:[0,1]
	v_pk_fma_f32 v[68:69], v[180:181], v[68:69], v[80:81] op_sel_hi:[1,0,1]
	s_waitcnt lgkmcnt(0)
	v_pk_mul_f32 v[80:81], v[64:65], v[68:69] op_sel:[1,1] op_sel_hi:[0,1] neg_hi:[1,0]
	s_nop 0
	v_pk_fma_f32 v[80:81], v[64:65], v[68:69], v[80:81] op_sel_hi:[1,0,1]
	v_pk_mul_f32 v[64:65], v[180:181], v[68:69] op_sel:[1,1] op_sel_hi:[0,1] neg_lo:[0,1]
	v_pk_fma_f32 v[64:65], v[180:181], v[68:69], v[64:65] op_sel_hi:[1,0,1]
	s_nop 0
	v_pk_mul_f32 v[68:69], v[66:67], v[64:65] op_sel:[1,1] op_sel_hi:[0,1] neg_hi:[1,0]
	s_nop 0
	v_pk_fma_f32 v[82:83], v[66:67], v[64:65], v[68:69] op_sel_hi:[1,0,1]
	v_pk_mul_f32 v[66:67], v[180:181], v[64:65] op_sel:[1,1] op_sel_hi:[0,1] neg_lo:[0,1]
	v_pk_fma_f32 v[68:69], v[180:181], v[64:65], v[66:67] op_sel_hi:[1,0,1]
	v_xad_u32 v63, v50, 12, v10
	v_lshl_add_u32 v63, v63, 3, 0
	v_add_u32_e32 v63, 0x800, v63
	ds_read2_b64 v[64:67], v63 offset0:128 offset1:144
	v_pk_mul_f32 v[84:85], v[180:181], v[68:69] op_sel:[1,1] op_sel_hi:[0,1] neg_lo:[0,1]
	v_pk_fma_f32 v[84:85], v[180:181], v[68:69], v[84:85] op_sel_hi:[1,0,1]
	s_waitcnt lgkmcnt(0)
	v_pk_mul_f32 v[86:87], v[64:65], v[68:69] op_sel:[1,1] op_sel_hi:[0,1] neg_hi:[1,0]
	v_pk_fma_f32 v[86:87], v[64:65], v[68:69], v[86:87] op_sel_hi:[1,0,1]
	v_pk_mul_f32 v[64:65], v[66:67], v[84:85] op_sel:[1,1] op_sel_hi:[0,1] neg_hi:[1,0]
	v_pk_fma_f32 v[88:89], v[66:67], v[84:85], v[64:65] op_sel_hi:[1,0,1]
	v_xad_u32 v64, v50, 13, v10
	v_lshl_add_u32 v64, v64, 3, 0
	v_add_u32_e32 v64, 0x800, v64
	ds_read2_b64 v[66:69], v64 offset0:160 offset1:176
	v_pk_mul_f32 v[90:91], v[180:181], v[84:85] op_sel:[1,1] op_sel_hi:[0,1] neg_lo:[0,1]
	v_pk_fma_f32 v[84:85], v[180:181], v[84:85], v[90:91] op_sel_hi:[1,0,1]
	s_waitcnt lgkmcnt(0)
	v_pk_mul_f32 v[90:91], v[66:67], v[84:85] op_sel:[1,1] op_sel_hi:[0,1] neg_hi:[1,0]
	s_nop 0
	v_pk_fma_f32 v[90:91], v[66:67], v[84:85], v[90:91] op_sel_hi:[1,0,1]
	v_pk_mul_f32 v[66:67], v[180:181], v[84:85] op_sel:[1,1] op_sel_hi:[0,1] neg_lo:[0,1]
	v_pk_fma_f32 v[66:67], v[180:181], v[84:85], v[66:67] op_sel_hi:[1,0,1]
	s_nop 0
	v_pk_mul_f32 v[84:85], v[68:69], v[66:67] op_sel:[1,1] op_sel_hi:[0,1] neg_hi:[1,0]
	s_nop 0
	v_pk_fma_f32 v[84:85], v[68:69], v[66:67], v[84:85] op_sel_hi:[1,0,1]
	v_pk_mul_f32 v[68:69], v[180:181], v[66:67] op_sel:[1,1] op_sel_hi:[0,1] neg_lo:[0,1]
	v_pk_fma_f32 v[92:93], v[180:181], v[66:67], v[68:69] op_sel_hi:[1,0,1]
	v_xad_u32 v65, v50, 14, v10
	v_lshl_add_u32 v65, v65, 3, 0
	v_add_u32_e32 v65, 0x800, v65
	ds_read2_b64 v[66:69], v65 offset0:192 offset1:208
	v_pk_mul_f32 v[94:95], v[180:181], v[92:93] op_sel:[1,1] op_sel_hi:[0,1] neg_lo:[0,1]
	v_xad_u32 v10, v50, 15, v10
	s_waitcnt lgkmcnt(0)
	v_pk_mul_f32 v[96:97], v[66:67], v[92:93] op_sel:[1,1] op_sel_hi:[0,1] neg_hi:[1,0]
	v_lshl_add_u32 v10, v10, 3, 0
	v_pk_fma_f32 v[96:97], v[66:67], v[92:93], v[96:97] op_sel_hi:[1,0,1]
	v_pk_fma_f32 v[92:93], v[180:181], v[92:93], v[94:95] op_sel_hi:[1,0,1]
	s_nop 0
	v_pk_mul_f32 v[66:67], v[68:69], v[92:93] op_sel:[1,1] op_sel_hi:[0,1] neg_hi:[1,0]
	v_add_u32_e32 v101, 0x800, v10
	v_pk_fma_f32 v[94:95], v[68:69], v[92:93], v[66:67] op_sel_hi:[1,0,1]
	ds_read2_b64 v[66:69], v101 offset0:224 offset1:240
	v_pk_mul_f32 v[98:99], v[180:181], v[92:93] op_sel:[1,1] op_sel_hi:[0,1] neg_lo:[0,1]
	v_pk_fma_f32 v[92:93], v[180:181], v[92:93], v[98:99] op_sel_hi:[1,0,1]
	s_waitcnt lgkmcnt(0)
	v_pk_mul_f32 v[98:99], v[66:67], v[92:93] op_sel:[1,1] op_sel_hi:[0,1] neg_hi:[1,0]
	s_nop 0
	v_pk_fma_f32 v[66:67], v[66:67], v[92:93], v[98:99] op_sel_hi:[1,0,1]
	v_pk_mul_f32 v[98:99], v[180:181], v[92:93] op_sel:[1,1] op_sel_hi:[0,1] neg_lo:[0,1]
	v_pk_fma_f32 v[20:21], v[180:181], v[92:93], v[98:99] op_sel_hi:[1,0,1]
	s_nop 0
	v_pk_mul_f32 v[92:93], v[68:69], v[20:21] op_sel:[1,1] op_sel_hi:[0,1] neg_hi:[1,0]
	s_nop 0
	v_pk_fma_f32 v[68:69], v[68:69], v[20:21], v[92:93] op_sel_hi:[1,0,1]
	v_mov_b32_e32 v10, v1
	v_pk_add_f32 v[104:105], v[16:17], v[52:53]
	v_pk_add_f32 v[16:17], v[16:17], v[52:53] neg_lo:[0,1] neg_hi:[0,1]
	v_pk_add_f32 v[52:53], v[18:19], v[70:71]
	v_pk_add_f32 v[18:19], v[18:19], v[70:71] neg_lo:[0,1] neg_hi:[0,1]
	v_mov_b32_e32 v92, v164
	v_mov_b32_e32 v20, v165
	v_mov_b32_e32 v98, v166
	v_mov_b32_e32 v10, v167
	v_mov_b32_e32 v100, v168
	v_mov_b32_e32 v50, v169
	v_mov_b32_e32 v102, v170
	v_mov_b32_e32 v21, v171
	v_pk_mul_f32 v[70:71], v[102:103], v[18:19] op_sel:[0,1] op_sel_hi:[0,0] neg_lo:[0,1]
	v_pk_fma_f32 v[18:19], v[92:93], v[18:19], v[70:71] op_sel_hi:[0,1,1]
	v_pk_add_f32 v[70:71], v[22:23], v[72:73]
	v_pk_add_f32 v[22:23], v[22:23], v[72:73] neg_lo:[0,1] neg_hi:[0,1]
	s_nop 0
	v_pk_mul_f32 v[72:73], v[50:51], v[22:23] op_sel:[0,1] op_sel_hi:[0,0] neg_lo:[0,1]
	v_pk_fma_f32 v[22:23], v[20:21], v[22:23], v[72:73] op_sel_hi:[0,1,1]
	v_pk_add_f32 v[72:73], v[24:25], v[74:75]
	v_pk_add_f32 v[24:25], v[24:25], v[74:75] neg_lo:[0,1] neg_hi:[0,1]
	s_nop 0
	v_pk_mul_f32 v[74:75], v[100:101], v[24:25] op_sel:[0,1] op_sel_hi:[0,0] neg_lo:[0,1]
	v_pk_fma_f32 v[24:25], v[98:99], v[24:25], v[74:75] op_sel_hi:[0,1,1]
	v_pk_add_f32 v[74:75], v[28:29], v[76:77]
	v_pk_add_f32 v[28:29], v[28:29], v[76:77] neg_lo:[0,1] neg_hi:[0,1]
	s_nop 0
	v_pk_mul_f32 v[76:77], v[10:11], v[28:29] op_sel:[0,1] op_sel_hi:[0,0] neg_lo:[0,1]
	v_pk_fma_f32 v[28:29], v[10:11], v[28:29], v[76:77] op_sel_hi:[0,1,1]
	v_pk_add_f32 v[76:77], v[26:27], v[78:79]
	v_pk_add_f32 v[26:27], v[26:27], v[78:79] neg_lo:[0,1] neg_hi:[0,1]
	s_nop 0
	v_pk_mul_f32 v[78:79], v[98:99], v[26:27] op_sel:[0,1] op_sel_hi:[0,0] neg_lo:[0,1]
	v_pk_fma_f32 v[26:27], v[100:101], v[26:27], v[78:79] op_sel_hi:[0,1,1]
	v_pk_add_f32 v[78:79], v[30:31], v[80:81]
	v_pk_add_f32 v[30:31], v[30:31], v[80:81] neg_lo:[0,1] neg_hi:[0,1]
	s_nop 0
	v_pk_mul_f32 v[80:81], v[20:21], v[30:31] op_sel:[0,1] op_sel_hi:[0,0] neg_lo:[0,1]
	v_pk_fma_f32 v[30:31], v[50:51], v[30:31], v[80:81] op_sel_hi:[0,1,1]
	v_pk_add_f32 v[80:81], v[32:33], v[82:83]
	v_pk_add_f32 v[32:33], v[32:33], v[82:83] neg_lo:[0,1] neg_hi:[0,1]
	s_nop 0
	v_pk_mul_f32 v[82:83], v[92:93], v[32:33] op_sel:[0,1] op_sel_hi:[0,0] neg_lo:[0,1]
	v_pk_fma_f32 v[32:33], v[102:103], v[32:33], v[82:83] op_sel_hi:[0,1,1]
	v_pk_add_f32 v[82:83], v[34:35], v[86:87]
	v_pk_add_f32 v[34:35], v[34:35], v[86:87] neg_lo:[0,1] neg_hi:[0,1]
	s_nop 0
	v_xor_b32_e32 v86, 0x80000000, v35
	v_mov_b32_e32 v87, v34
	v_pk_add_f32 v[34:35], v[36:37], v[88:89]
	v_pk_add_f32 v[36:37], v[36:37], v[88:89] neg_lo:[0,1] neg_hi:[0,1]
	s_nop 0
	v_pk_mul_f32 v[88:89], v[92:93], v[36:37] op_sel:[0,1] op_sel_hi:[0,0] neg_lo:[0,1]
	v_pk_fma_f32 v[36:37], v[102:103], v[36:37], v[88:89] op_sel_hi:[0,1,1] neg_lo:[1,0,0] neg_hi:[1,0,0]
	v_pk_add_f32 v[88:89], v[38:39], v[90:91]
	v_pk_add_f32 v[38:39], v[38:39], v[90:91] neg_lo:[0,1] neg_hi:[0,1]
	s_nop 0
	v_pk_mul_f32 v[90:91], v[20:21], v[38:39] op_sel:[0,1] op_sel_hi:[0,0] neg_lo:[0,1]
	v_pk_fma_f32 v[38:39], v[50:51], v[38:39], v[90:91] op_sel_hi:[0,1,1] neg_lo:[1,0,0] neg_hi:[1,0,0]
	v_pk_add_f32 v[90:91], v[40:41], v[84:85]
	v_pk_add_f32 v[40:41], v[40:41], v[84:85] neg_lo:[0,1] neg_hi:[0,1]
	s_nop 0
	v_pk_mul_f32 v[84:85], v[98:99], v[40:41] op_sel:[0,1] op_sel_hi:[0,0] neg_lo:[0,1]
	v_pk_fma_f32 v[40:41], v[100:101], v[40:41], v[84:85] op_sel_hi:[0,1,1] neg_lo:[1,0,0] neg_hi:[1,0,0]
	v_pk_add_f32 v[84:85], v[44:45], v[96:97]
	v_pk_add_f32 v[44:45], v[44:45], v[96:97] neg_lo:[0,1] neg_hi:[0,1]
	s_nop 0
	v_pk_mul_f32 v[96:97], v[10:11], v[44:45] op_sel:[0,1] op_sel_hi:[0,0] neg_lo:[0,1]
	v_pk_fma_f32 v[44:45], v[10:11], v[44:45], v[96:97] op_sel_hi:[0,1,1] neg_lo:[1,0,0] neg_hi:[1,0,0]
	v_pk_add_f32 v[96:97], v[42:43], v[94:95]
	v_pk_add_f32 v[42:43], v[42:43], v[94:95] neg_lo:[0,1] neg_hi:[0,1]
	s_nop 0
	v_pk_mul_f32 v[94:95], v[100:101], v[42:43] op_sel:[0,1] op_sel_hi:[0,0] neg_lo:[0,1]
	v_pk_fma_f32 v[42:43], v[98:99], v[42:43], v[94:95] op_sel_hi:[0,1,1] neg_lo:[1,0,0] neg_hi:[1,0,0]
	v_pk_add_f32 v[94:95], v[46:47], v[66:67]
	v_pk_add_f32 v[46:47], v[46:47], v[66:67] neg_lo:[0,1] neg_hi:[0,1]
	s_nop 0
	v_pk_mul_f32 v[66:67], v[50:51], v[46:47] op_sel:[0,1] op_sel_hi:[0,0] neg_lo:[0,1]
	v_pk_fma_f32 v[46:47], v[20:21], v[46:47], v[66:67] op_sel_hi:[0,1,1] neg_lo:[1,0,0] neg_hi:[1,0,0]
	v_pk_add_f32 v[66:67], v[48:49], v[68:69]
	v_pk_add_f32 v[48:49], v[48:49], v[68:69] neg_lo:[0,1] neg_hi:[0,1]
	s_nop 0
	v_pk_mul_f32 v[68:69], v[102:103], v[48:49] op_sel:[0,1] op_sel_hi:[0,0] neg_lo:[0,1]
	v_pk_fma_f32 v[48:49], v[92:93], v[48:49], v[68:69] op_sel_hi:[0,1,1] neg_lo:[1,0,0] neg_hi:[1,0,0]
	v_pk_add_f32 v[92:93], v[52:53], v[34:35]
	v_pk_add_f32 v[34:35], v[52:53], v[34:35] neg_lo:[0,1] neg_hi:[0,1]
	v_pk_add_f32 v[68:69], v[104:105], v[82:83]
	v_pk_mul_f32 v[52:53], v[50:51], v[34:35] op_sel:[0,1] op_sel_hi:[0,0] neg_lo:[0,1]
	v_pk_fma_f32 v[34:35], v[20:21], v[34:35], v[52:53] op_sel_hi:[0,1,1]
	v_pk_add_f32 v[52:53], v[70:71], v[88:89]
	v_pk_add_f32 v[70:71], v[70:71], v[88:89] neg_lo:[0,1] neg_hi:[0,1]
	v_pk_add_f32 v[82:83], v[104:105], v[82:83] neg_lo:[0,1] neg_hi:[0,1]
	v_pk_mul_f32 v[88:89], v[10:11], v[70:71] op_sel:[0,1] op_sel_hi:[0,0] neg_lo:[0,1]
	v_pk_fma_f32 v[70:71], v[10:11], v[70:71], v[88:89] op_sel_hi:[0,1,1]
	v_pk_add_f32 v[88:89], v[72:73], v[90:91]
	v_pk_add_f32 v[72:73], v[72:73], v[90:91] neg_lo:[0,1] neg_hi:[0,1]
	s_nop 0
	v_pk_mul_f32 v[90:91], v[20:21], v[72:73] op_sel:[0,1] op_sel_hi:[0,0] neg_lo:[0,1]
	v_pk_fma_f32 v[72:73], v[50:51], v[72:73], v[90:91] op_sel_hi:[0,1,1]
	v_pk_add_f32 v[90:91], v[74:75], v[84:85]
	v_pk_add_f32 v[74:75], v[74:75], v[84:85] neg_lo:[0,1] neg_hi:[0,1]
	s_nop 0
	v_xor_b32_e32 v84, 0x80000000, v75
	v_mov_b32_e32 v85, v74
	v_pk_add_f32 v[74:75], v[76:77], v[96:97]
	v_pk_add_f32 v[76:77], v[76:77], v[96:97] neg_lo:[0,1] neg_hi:[0,1]
	s_nop 0
	v_pk_mul_f32 v[96:97], v[20:21], v[76:77] op_sel:[0,1] op_sel_hi:[0,0] neg_lo:[0,1]
	v_pk_fma_f32 v[76:77], v[50:51], v[76:77], v[96:97] op_sel_hi:[0,1,1] neg_lo:[1,0,0] neg_hi:[1,0,0]
	v_pk_add_f32 v[96:97], v[78:79], v[94:95]
	v_pk_add_f32 v[78:79], v[78:79], v[94:95] neg_lo:[0,1] neg_hi:[0,1]
	s_nop 0
	v_pk_mul_f32 v[94:95], v[10:11], v[78:79] op_sel:[0,1] op_sel_hi:[0,0] neg_lo:[0,1]
	v_pk_fma_f32 v[78:79], v[10:11], v[78:79], v[94:95] op_sel_hi:[0,1,1] neg_lo:[1,0,0] neg_hi:[1,0,0]
	v_pk_add_f32 v[94:95], v[80:81], v[66:67]
	v_pk_add_f32 v[66:67], v[80:81], v[66:67] neg_lo:[0,1] neg_hi:[0,1]
	s_nop 0
	v_pk_mul_f32 v[80:81], v[50:51], v[66:67] op_sel:[0,1] op_sel_hi:[0,0] neg_lo:[0,1]
	v_pk_fma_f32 v[66:67], v[20:21], v[66:67], v[80:81] op_sel_hi:[0,1,1] neg_lo:[1,0,0] neg_hi:[1,0,0]
	v_pk_add_f32 v[80:81], v[68:69], v[90:91]
	v_pk_add_f32 v[68:69], v[68:69], v[90:91] neg_lo:[0,1] neg_hi:[0,1]
	v_pk_add_f32 v[90:91], v[92:93], v[74:75]
	v_pk_add_f32 v[74:75], v[92:93], v[74:75] neg_lo:[0,1] neg_hi:[0,1]
	s_nop 0
	v_pk_mul_f32 v[92:93], v[10:11], v[74:75] op_sel:[0,1] op_sel_hi:[0,0] neg_lo:[0,1]
	v_pk_fma_f32 v[74:75], v[10:11], v[74:75], v[92:93] op_sel_hi:[0,1,1]
	v_pk_add_f32 v[92:93], v[52:53], v[96:97]
	v_pk_add_f32 v[52:53], v[52:53], v[96:97] neg_lo:[0,1] neg_hi:[0,1]
	s_nop 0
	v_xor_b32_e32 v96, 0x80000000, v53
	v_mov_b32_e32 v97, v52
	v_pk_add_f32 v[52:53], v[88:89], v[94:95]
	v_pk_add_f32 v[88:89], v[88:89], v[94:95] neg_lo:[0,1] neg_hi:[0,1]
	s_nop 0
	v_pk_mul_f32 v[94:95], v[10:11], v[88:89] op_sel:[0,1] op_sel_hi:[0,0] neg_lo:[0,1]
	v_pk_fma_f32 v[88:89], v[10:11], v[88:89], v[94:95] op_sel_hi:[0,1,1] neg_lo:[1,0,0] neg_hi:[1,0,0]
	v_pk_add_f32 v[94:95], v[80:81], v[92:93]
	v_pk_add_f32 v[80:81], v[80:81], v[92:93] neg_lo:[0,1] neg_hi:[0,1]
	v_pk_add_f32 v[92:93], v[90:91], v[52:53]
	v_pk_add_f32 v[52:53], v[90:91], v[52:53] neg_lo:[0,1] neg_hi:[0,1]
	s_nop 0
	v_xor_b32_e32 v90, 0x80000000, v53
	v_mov_b32_e32 v91, v52
	v_pk_add_f32 v[52:53], v[94:95], v[92:93]
	v_pk_add_f32 v[92:93], v[94:95], v[92:93] neg_lo:[0,1] neg_hi:[0,1]
	v_pk_add_f32 v[94:95], v[80:81], v[90:91]
	v_pk_add_f32 v[80:81], v[80:81], v[90:91] neg_lo:[0,1] neg_hi:[0,1]
	v_pk_add_f32 v[90:91], v[68:69], v[96:97]
	v_pk_add_f32 v[68:69], v[68:69], v[96:97] neg_lo:[0,1] neg_hi:[0,1]
	v_pk_add_f32 v[96:97], v[74:75], v[88:89]
	v_pk_add_f32 v[74:75], v[74:75], v[88:89] neg_lo:[0,1] neg_hi:[0,1]
	s_nop 0
	v_xor_b32_e32 v88, 0x80000000, v75
	v_mov_b32_e32 v89, v74
	v_pk_add_f32 v[74:75], v[90:91], v[96:97]
	v_pk_add_f32 v[90:91], v[90:91], v[96:97] neg_lo:[0,1] neg_hi:[0,1]
	v_pk_add_f32 v[96:97], v[68:69], v[88:89]
	v_pk_add_f32 v[68:69], v[68:69], v[88:89] neg_lo:[0,1] neg_hi:[0,1]
	v_pk_add_f32 v[88:89], v[82:83], v[84:85]
	v_pk_add_f32 v[82:83], v[82:83], v[84:85] neg_lo:[0,1] neg_hi:[0,1]
	v_pk_add_f32 v[84:85], v[34:35], v[76:77]
	v_pk_add_f32 v[34:35], v[34:35], v[76:77] neg_lo:[0,1] neg_hi:[0,1]
	s_nop 0
	v_pk_mul_f32 v[76:77], v[10:11], v[34:35] op_sel:[0,1] op_sel_hi:[0,0] neg_lo:[0,1]
	v_pk_fma_f32 v[34:35], v[10:11], v[34:35], v[76:77] op_sel_hi:[0,1,1]
	v_pk_add_f32 v[76:77], v[70:71], v[78:79]
	v_pk_add_f32 v[70:71], v[70:71], v[78:79] neg_lo:[0,1] neg_hi:[0,1]
	s_nop 0
	v_xor_b32_e32 v78, 0x80000000, v71
	v_mov_b32_e32 v79, v70
	v_pk_add_f32 v[70:71], v[72:73], v[66:67]
	v_pk_add_f32 v[66:67], v[72:73], v[66:67] neg_lo:[0,1] neg_hi:[0,1]
	s_nop 0
	v_pk_mul_f32 v[72:73], v[10:11], v[66:67] op_sel:[0,1] op_sel_hi:[0,0] neg_lo:[0,1]
	v_pk_fma_f32 v[66:67], v[10:11], v[66:67], v[72:73] op_sel_hi:[0,1,1] neg_lo:[1,0,0] neg_hi:[1,0,0]
	v_pk_add_f32 v[72:73], v[88:89], v[76:77]
	v_pk_add_f32 v[76:77], v[88:89], v[76:77] neg_lo:[0,1] neg_hi:[0,1]
	v_pk_add_f32 v[88:89], v[84:85], v[70:71]
	v_pk_add_f32 v[70:71], v[84:85], v[70:71] neg_lo:[0,1] neg_hi:[0,1]
	s_nop 0
	v_xor_b32_e32 v84, 0x80000000, v71
	v_mov_b32_e32 v85, v70
	v_pk_add_f32 v[70:71], v[72:73], v[88:89]
	v_pk_add_f32 v[72:73], v[72:73], v[88:89] neg_lo:[0,1] neg_hi:[0,1]
	v_pk_add_f32 v[88:89], v[76:77], v[84:85]
	v_pk_add_f32 v[76:77], v[76:77], v[84:85] neg_lo:[0,1] neg_hi:[0,1]
	v_pk_add_f32 v[84:85], v[82:83], v[78:79]
	v_pk_add_f32 v[78:79], v[82:83], v[78:79] neg_lo:[0,1] neg_hi:[0,1]
	v_pk_add_f32 v[82:83], v[34:35], v[66:67]
	v_pk_add_f32 v[34:35], v[34:35], v[66:67] neg_lo:[0,1] neg_hi:[0,1]
	s_nop 0
	v_xor_b32_e32 v66, 0x80000000, v35
	v_mov_b32_e32 v67, v34
	v_pk_add_f32 v[34:35], v[84:85], v[82:83]
	v_pk_add_f32 v[82:83], v[84:85], v[82:83] neg_lo:[0,1] neg_hi:[0,1]
	v_pk_add_f32 v[84:85], v[78:79], v[66:67]
	v_pk_add_f32 v[66:67], v[78:79], v[66:67] neg_lo:[0,1] neg_hi:[0,1]
	v_pk_add_f32 v[78:79], v[16:17], v[86:87]
	v_pk_add_f32 v[16:17], v[16:17], v[86:87] neg_lo:[0,1] neg_hi:[0,1]
	v_pk_add_f32 v[86:87], v[18:19], v[36:37]
	v_pk_add_f32 v[18:19], v[18:19], v[36:37] neg_lo:[0,1] neg_hi:[0,1]
	s_nop 0
	v_pk_mul_f32 v[36:37], v[50:51], v[18:19] op_sel:[0,1] op_sel_hi:[0,0] neg_lo:[0,1]
	v_pk_fma_f32 v[18:19], v[20:21], v[18:19], v[36:37] op_sel_hi:[0,1,1]
	v_pk_add_f32 v[36:37], v[22:23], v[38:39]
	v_pk_add_f32 v[22:23], v[22:23], v[38:39] neg_lo:[0,1] neg_hi:[0,1]
	s_nop 0
	v_pk_mul_f32 v[38:39], v[10:11], v[22:23] op_sel:[0,1] op_sel_hi:[0,0] neg_lo:[0,1]
	v_pk_fma_f32 v[22:23], v[10:11], v[22:23], v[38:39] op_sel_hi:[0,1,1]
	v_pk_add_f32 v[38:39], v[24:25], v[40:41]
	v_pk_add_f32 v[24:25], v[24:25], v[40:41] neg_lo:[0,1] neg_hi:[0,1]
	s_nop 0
	v_pk_mul_f32 v[40:41], v[20:21], v[24:25] op_sel:[0,1] op_sel_hi:[0,0] neg_lo:[0,1]
	v_pk_fma_f32 v[24:25], v[50:51], v[24:25], v[40:41] op_sel_hi:[0,1,1]
	v_pk_add_f32 v[40:41], v[28:29], v[44:45]
	v_pk_add_f32 v[28:29], v[28:29], v[44:45] neg_lo:[0,1] neg_hi:[0,1]
	s_nop 0
	v_xor_b32_e32 v44, 0x80000000, v29
	v_mov_b32_e32 v45, v28
	v_pk_add_f32 v[28:29], v[26:27], v[42:43]
	v_pk_add_f32 v[26:27], v[26:27], v[42:43] neg_lo:[0,1] neg_hi:[0,1]
	s_nop 0
	v_pk_mul_f32 v[42:43], v[20:21], v[26:27] op_sel:[0,1] op_sel_hi:[0,0] neg_lo:[0,1]
	v_pk_fma_f32 v[26:27], v[50:51], v[26:27], v[42:43] op_sel_hi:[0,1,1] neg_lo:[1,0,0] neg_hi:[1,0,0]
	v_pk_add_f32 v[42:43], v[30:31], v[46:47]
	v_pk_add_f32 v[30:31], v[30:31], v[46:47] neg_lo:[0,1] neg_hi:[0,1]
	s_nop 0
	v_pk_mul_f32 v[46:47], v[10:11], v[30:31] op_sel:[0,1] op_sel_hi:[0,0] neg_lo:[0,1]
	v_pk_fma_f32 v[30:31], v[10:11], v[30:31], v[46:47] op_sel_hi:[0,1,1] neg_lo:[1,0,0] neg_hi:[1,0,0]
	v_pk_add_f32 v[46:47], v[32:33], v[48:49]
	v_pk_add_f32 v[32:33], v[32:33], v[48:49] neg_lo:[0,1] neg_hi:[0,1]
	s_nop 0
	v_pk_mul_f32 v[48:49], v[50:51], v[32:33] op_sel:[0,1] op_sel_hi:[0,0] neg_lo:[0,1]
	v_pk_fma_f32 v[20:21], v[20:21], v[32:33], v[48:49] op_sel_hi:[0,1,1] neg_lo:[1,0,0] neg_hi:[1,0,0]
	v_pk_add_f32 v[48:49], v[86:87], v[28:29]
	v_pk_add_f32 v[28:29], v[86:87], v[28:29] neg_lo:[0,1] neg_hi:[0,1]
	v_pk_add_f32 v[32:33], v[78:79], v[40:41]
	v_pk_add_f32 v[40:41], v[78:79], v[40:41] neg_lo:[0,1] neg_hi:[0,1]
	v_pk_mul_f32 v[78:79], v[10:11], v[28:29] op_sel:[0,1] op_sel_hi:[0,0] neg_lo:[0,1]
	v_pk_fma_f32 v[28:29], v[10:11], v[28:29], v[78:79] op_sel_hi:[0,1,1]
	v_pk_add_f32 v[78:79], v[36:37], v[42:43]
	v_pk_add_f32 v[36:37], v[36:37], v[42:43] neg_lo:[0,1] neg_hi:[0,1]
	s_nop 0
	v_xor_b32_e32 v42, 0x80000000, v37
	v_mov_b32_e32 v43, v36
	v_pk_add_f32 v[36:37], v[38:39], v[46:47]
	v_pk_add_f32 v[38:39], v[38:39], v[46:47] neg_lo:[0,1] neg_hi:[0,1]
	s_nop 0
	v_pk_mul_f32 v[46:47], v[10:11], v[38:39] op_sel:[0,1] op_sel_hi:[0,0] neg_lo:[0,1]
	v_pk_fma_f32 v[38:39], v[10:11], v[38:39], v[46:47] op_sel_hi:[0,1,1] neg_lo:[1,0,0] neg_hi:[1,0,0]
	v_pk_add_f32 v[46:47], v[32:33], v[78:79]
	v_pk_add_f32 v[32:33], v[32:33], v[78:79] neg_lo:[0,1] neg_hi:[0,1]
	v_pk_add_f32 v[78:79], v[48:49], v[36:37]
	v_pk_add_f32 v[36:37], v[48:49], v[36:37] neg_lo:[0,1] neg_hi:[0,1]
	s_nop 0
	v_pk_add_f32 v[86:87], v[32:33], v[36:37] op_sel:[0,1] op_sel_hi:[1,0] neg_lo:[0,1]
	v_pk_add_f32 v[32:33], v[32:33], v[36:37] op_sel:[0,1] op_sel_hi:[1,0] neg_hi:[0,1]
	v_pk_add_f32 v[48:49], v[40:41], v[42:43]
	v_pk_add_f32 v[40:41], v[40:41], v[42:43] neg_lo:[0,1] neg_hi:[0,1]
	v_pk_add_f32 v[42:43], v[28:29], v[38:39]
	v_pk_add_f32 v[28:29], v[28:29], v[38:39] neg_lo:[0,1] neg_hi:[0,1]
	v_pk_add_f32 v[36:37], v[46:47], v[78:79] neg_lo:[0,1] neg_hi:[0,1]
	v_xor_b32_e32 v38, 0x80000000, v29
	v_mov_b32_e32 v39, v28
	v_pk_add_f32 v[28:29], v[48:49], v[42:43]
	v_pk_add_f32 v[42:43], v[48:49], v[42:43] neg_lo:[0,1] neg_hi:[0,1]
	v_pk_add_f32 v[48:49], v[40:41], v[38:39]
	v_pk_add_f32 v[38:39], v[40:41], v[38:39] neg_lo:[0,1] neg_hi:[0,1]
	v_pk_add_f32 v[40:41], v[16:17], v[44:45]
	v_pk_add_f32 v[16:17], v[16:17], v[44:45] neg_lo:[0,1] neg_hi:[0,1]
	v_pk_add_f32 v[44:45], v[18:19], v[26:27]
	v_pk_add_f32 v[18:19], v[18:19], v[26:27] neg_lo:[0,1] neg_hi:[0,1]
	s_nop 0
	v_pk_mul_f32 v[26:27], v[10:11], v[18:19] op_sel:[0,1] op_sel_hi:[0,0] neg_lo:[0,1]
	v_pk_fma_f32 v[18:19], v[10:11], v[18:19], v[26:27] op_sel_hi:[0,1,1]
	v_pk_add_f32 v[26:27], v[22:23], v[30:31]
	v_pk_add_f32 v[22:23], v[22:23], v[30:31] neg_lo:[0,1] neg_hi:[0,1]
	s_nop 0
	v_xor_b32_e32 v30, 0x80000000, v23
	v_mov_b32_e32 v31, v22
	v_pk_add_f32 v[22:23], v[24:25], v[20:21]
	v_pk_add_f32 v[20:21], v[24:25], v[20:21] neg_lo:[0,1] neg_hi:[0,1]
	s_nop 0
	v_pk_mul_f32 v[24:25], v[10:11], v[20:21] op_sel:[0,1] op_sel_hi:[0,0] neg_lo:[0,1]
	v_pk_fma_f32 v[20:21], v[10:11], v[20:21], v[24:25] op_sel_hi:[0,1,1] neg_lo:[1,0,0] neg_hi:[1,0,0]
	v_pk_add_f32 v[24:25], v[40:41], v[26:27]
	v_pk_add_f32 v[26:27], v[40:41], v[26:27] neg_lo:[0,1] neg_hi:[0,1]
	v_pk_add_f32 v[40:41], v[44:45], v[22:23]
	v_pk_add_f32 v[22:23], v[44:45], v[22:23] neg_lo:[0,1] neg_hi:[0,1]
	s_nop 0
	v_xor_b32_e32 v44, 0x80000000, v23
	v_mov_b32_e32 v45, v22
	v_pk_add_f32 v[22:23], v[24:25], v[40:41]
	v_pk_add_f32 v[24:25], v[24:25], v[40:41] neg_lo:[0,1] neg_hi:[0,1]
	v_pk_add_f32 v[40:41], v[26:27], v[44:45]
	v_pk_add_f32 v[26:27], v[26:27], v[44:45] neg_lo:[0,1] neg_hi:[0,1]
	v_pk_add_f32 v[44:45], v[16:17], v[30:31]
	v_pk_add_f32 v[16:17], v[16:17], v[30:31] neg_lo:[0,1] neg_hi:[0,1]
	v_pk_add_f32 v[30:31], v[18:19], v[20:21]
	v_pk_add_f32 v[18:19], v[18:19], v[20:21] neg_lo:[0,1] neg_hi:[0,1]
	s_nop 0
	v_xor_b32_e32 v20, 0x80000000, v19
	v_mov_b32_e32 v21, v18
	v_pk_add_f32 v[18:19], v[44:45], v[30:31]
	v_pk_add_f32 v[30:31], v[44:45], v[30:31] neg_lo:[0,1] neg_hi:[0,1]
	v_pk_add_f32 v[44:45], v[16:17], v[20:21]
	v_pk_add_f32 v[16:17], v[16:17], v[20:21] neg_lo:[0,1] neg_hi:[0,1]
	v_pk_add_f32 v[20:21], v[46:47], v[78:79]
	ds_write2_b64 v13, v[52:53], v[20:21] offset1:16
	ds_write2_b64 v15, v[70:71], v[22:23] offset0:32 offset1:48
	ds_write2_b64 v51, v[74:75], v[28:29] offset0:64 offset1:80
	ds_write2_b64 v54, v[34:35], v[18:19] offset0:96 offset1:112
	ds_write2_b64 v55, v[94:95], v[86:87] offset0:128 offset1:144
	ds_write2_b64 v56, v[88:89], v[40:41] offset0:160 offset1:176
	ds_write2_b64 v57, v[96:97], v[48:49] offset0:192 offset1:208
	ds_write2_b64 v58, v[84:85], v[44:45] offset0:224 offset1:240
	ds_write2_b64 v59, v[92:93], v[36:37] offset1:16
	ds_write2_b64 v60, v[72:73], v[24:25] offset0:32 offset1:48
	ds_write2_b64 v61, v[90:91], v[42:43] offset0:64 offset1:80
	ds_write2_b64 v62, v[82:83], v[30:31] offset0:96 offset1:112
	ds_write2_b64 v63, v[80:81], v[32:33] offset0:128 offset1:144
	ds_write2_b64 v64, v[76:77], v[26:27] offset0:160 offset1:176
	ds_write2_b64 v65, v[68:69], v[38:39] offset0:192 offset1:208
	ds_write2_b64 v101, v[66:67], v[16:17] offset0:224 offset1:240
	v_mov_b32_e32 v10, v173
	s_waitcnt lgkmcnt(0)
	s_barrier
	v_mov_b32_e32 v58, v178
	v_mov_b32_e32 v59, v179
	v_lshl_add_u32 v10, v10, 3, 0
	ds_read_b64 v[34:35], v10
	ds_read_b64 v[36:37], v10 offset:4224
	ds_read_b64 v[38:39], v10 offset:8448
	ds_read_b64 v[40:41], v10 offset:12672
	ds_read_b64 v[42:43], v10 offset:16896
	ds_read_b64 v[44:45], v10 offset:21120
	ds_read_b64 v[50:51], v10 offset:25344
	ds_read_b64 v[52:53], v10 offset:29568
	ds_read_b64 v[54:55], v10 offset:33792
	ds_read_b64 v[56:57], v10 offset:38016
	ds_read_b64 v[64:65], v10 offset:42240
	ds_read_b64 v[74:75], v10 offset:46464
	ds_read_b64 v[76:77], v10 offset:50688
	ds_read_b64 v[78:79], v10 offset:54912
	ds_read_b64 v[80:81], v10 offset:59136
	ds_read_b64 v[82:83], v10 offset:63360
	v_add_u32_e32 v13, 0x10800, v10
	v_add_u32_e32 v15, 0x11880, v10
	v_add_u32_e32 v16, 0x12900, v10
	v_add_u32_e32 v17, 0x13980, v10
	ds_read_b64 v[84:85], v13
	ds_read_b64 v[86:87], v15
	ds_read_b64 v[88:89], v16
	ds_read_b64 v[92:93], v17
	v_add_u32_e32 v13, 0x14a00, v10
	v_add_u32_e32 v15, 0x15a80, v10
	v_add_u32_e32 v16, 0x16b00, v10
	v_add_u32_e32 v17, 0x17b80, v10
	ds_read_b64 v[96:97], v13
	ds_read_b64 v[98:99], v15
	ds_read_b64 v[94:95], v16
	ds_read_b64 v[90:91], v17
	v_add_u32_e32 v13, 0x18c00, v10
	v_add_u32_e32 v15, 0x19c80, v10
	v_add_u32_e32 v16, 0x1ad00, v10
	v_add_u32_e32 v17, 0x1bd80, v10
	ds_read_b64 v[72:73], v13
	ds_read_b64 v[70:71], v15
	ds_read_b64 v[68:69], v16
	ds_read_b64 v[66:67], v17
	v_add_u32_e32 v13, 0x1ce00, v10
	v_add_u32_e32 v15, 0x1de80, v10
	v_add_u32_e32 v16, 0x1ef00, v10
	v_add_u32_e32 v10, 0x1ff80, v10
	ds_read_b64 v[62:63], v13
	ds_read_b64 v[60:61], v15
	ds_read_b64 v[100:101], v16
	ds_read_b64 v[102:103], v10
	s_mov_b32 s43, s95
	v_mov_b32_e32 v10, v1
	s_lshl_b64 s[0:1], s[42:43], 2
	v_readlane_b32 s2, v251, 46
	s_add_u32 s0, s2, s0
	v_readlane_b32 s2, v251, 48
	v_readlane_b32 s6, v251, 52
	v_mov_b32_e32 v24, v164
	v_mov_b32_e32 v32, v165
	v_mov_b32_e32 v28, v166
	v_mov_b32_e32 v46, v167
	v_mov_b32_e32 v48, v168
	v_mov_b32_e32 v30, v169
	v_mov_b32_e32 v26, v170
	v_mov_b32_e32 v10, v171
	v_mov_b32_e32 v16, v183
	v_mov_b32_e32 v19, v184
	s_addc_u32 s1, s2, s1
	v_readlane_b32 s7, v251, 53
	s_waitcnt lgkmcnt(0)
	s_barrier
	global_load_dword v13, v11, s[0:1]
	s_and_b64 s[0:1], s[6:7], exec
	s_movk_i32 s0, 0x800
	s_cselect_b32 s2, 0x400, s0
	v_readlane_b32 s24, v251, 50
	s_add_i32 s4, s2, s24
	s_mul_i32 s0, s4, 0x8200
	v_readlane_b32 s3, v251, 18
	s_mul_hi_i32 s1, s4, 0x8200
	s_add_u32 s0, s3, s0
	v_readlane_b32 s3, v251, 20
	s_addc_u32 s1, s3, s1
	s_lshl_b32 s2, s2, 2
	v_mov_b32_e32 v10, s2
	v_readlane_b32 s2, v251, 42
	v_readlane_b32 s3, v251, 43
	v_readlane_b32 s8, v250, 23
	v_readlane_b32 s9, v250, 24
	v_ashrrev_i32_e32 v15, 31, v14
	v_lshl_add_u64 v[22:23], v[14:15], 2, s[70:71]
	v_readlane_b32 s22, v250, 37
	global_load_dword v197, v10, s[2:3]
	s_add_i32 s2, s4, 0xc00
	s_ashr_i32 s3, s2, 31
	s_lshl_b64 s[2:3], s[2:3], 2
	s_add_u32 s2, s8, s2
	s_addc_u32 s3, s9, s3
	global_load_dword v198, v11, s[2:3]
	s_add_i32 s2, s4, 0x1800
	s_ashr_i32 s3, s2, 31
	s_lshl_b64 s[2:3], s[2:3], 2
	s_add_u32 s2, s8, s2
	s_addc_u32 s3, s9, s3
	global_load_dword v199, v11, s[2:3]
	v_readlane_b32 s2, v251, 40
	v_readlane_b32 s3, v251, 41
	v_cmp_lt_i32_e32 vcc, 0, v14
	v_mov_b32_e32 v17, 0
	v_lshl_add_u64 v[20:21], v[14:15], 1, s[0:1]
	v_mov_b32_e32 v18, 0
	v_readlane_b32 s25, v251, 51
	global_load_dword v200, v10, s[2:3]
	v_readlane_b32 s10, v250, 25
	v_lshlrev_b32_e32 v241, 1, v14
	v_lshlrev_b32_e32 v242, 2, v14
	v_add_u32_e32 v242, 0x1000, v242
	global_load_dword v190, v242, s[70:71] offset:-4096
	global_load_ushort v202, v241, s[0:1] offset:-2
	global_load_ushort v203, v241, s[0:1]
	global_load_ushort v204, v241, s[0:1] offset:2
	global_load_dword v205, v242, s[64:65] offset:-4096
	global_load_dword v206, v242, s[70:71] offset:-2048
	global_load_ushort v207, v241, s[0:1] offset:1022
	global_load_ushort v208, v241, s[0:1] offset:1024
	global_load_ushort v209, v241, s[0:1] offset:1026
	global_load_dword v210, v242, s[64:65] offset:-2048
	global_load_dword v211, v242, s[70:71]
	global_load_ushort v212, v241, s[0:1] offset:2046
	global_load_ushort v213, v241, s[0:1] offset:2048
	global_load_ushort v214, v241, s[0:1] offset:2050
	global_load_dword v215, v242, s[64:65]
	global_load_dword v216, v242, s[70:71] offset:2048
	global_load_ushort v217, v241, s[0:1] offset:3070
	global_load_ushort v218, v241, s[0:1] offset:3072
	global_load_ushort v219, v241, s[0:1] offset:3074
	global_load_dword v220, v242, s[64:65] offset:2048
	v_lshlrev_b32_e32 v241, 1, v14
	v_add_u32_e32 v241, 0x1000, v241
	v_lshlrev_b32_e32 v242, 2, v14
	v_add_u32_e32 v242, 0x3000, v242
	global_load_dword v221, v242, s[70:71] offset:-4096
	global_load_ushort v222, v241, s[0:1] offset:-2
	global_load_ushort v223, v241, s[0:1]
	global_load_ushort v224, v241, s[0:1] offset:2
	global_load_dword v225, v242, s[64:65] offset:-4096
	global_load_dword v226, v242, s[70:71] offset:-2048
	global_load_ushort v227, v241, s[0:1] offset:1022
	global_load_ushort v228, v241, s[0:1] offset:1024
	global_load_ushort v229, v241, s[0:1] offset:1026
	global_load_dword v230, v242, s[64:65] offset:-2048
	global_load_dword v231, v242, s[70:71]
	global_load_ushort v232, v241, s[0:1] offset:2046
	global_load_ushort v233, v241, s[0:1] offset:2048
	global_load_ushort v234, v241, s[0:1] offset:2050
	global_load_dword v235, v242, s[64:65]
	global_load_dword v236, v242, s[70:71] offset:2048
	global_load_ushort v237, v241, s[0:1] offset:3070
	global_load_ushort v238, v241, s[0:1] offset:3072
	global_load_ushort v239, v241, s[0:1] offset:3074
	global_load_dword v240, v242, s[64:65] offset:2048
	s_waitcnt vmcnt(20)
	v_mov_b32_e32 v10, v190
	v_readlane_b32 s11, v250, 26
	v_readlane_b32 s12, v250, 27
	v_readlane_b32 s13, v250, 28
	v_readlane_b32 s14, v250, 29
	v_readlane_b32 s15, v250, 30
	v_readlane_b32 s16, v250, 31
	v_readlane_b32 s17, v250, 32
	v_readlane_b32 s18, v250, 33
	v_readlane_b32 s19, v250, 34
	v_readlane_b32 s20, v250, 35
	v_readlane_b32 s21, v250, 36
	v_readlane_b32 s23, v250, 38
	s_and_saveexec_b64 s[2:3], vcc
	s_movk_i32 s22, 0x3fff
	s_cbranch_execz .LBB0_636
	v_mov_b32_e32 v18, v202
	s_nop 0
	v_lshlrev_b32_e32 v18, 16, v18

.LBB0_2283:
	s_add_u32 s29, s20, s28
	s_addc_u32 s39, s21, 0
	s_add_u32 s34, s29, 0x100
	s_addc_u32 s35, s39, 0
	s_and_b64 s[30:31], s[26:27], exec
	s_cselect_b32 s35, s13, s35
	s_cselect_b32 s34, s59, s34
	s_add_u32 s28, s22, s28
	s_addc_u32 s30, s23, 0
	s_add_u32 s28, s28, 0x100
	s_addc_u32 s30, s30, 0
	s_and_b64 s[26:27], s[26:27], exec
	s_cselect_b32 s37, s11, s30
	s_cselect_b32 s36, s60, s28
	s_add_u32 s38, s29, 0x10080
	s_addc_u32 s39, s39, 0
	s_add_i32 s70, s56, s46
	s_add_i32 m0, s19, 0xc000
	s_add_i32 s71, s19, 0xe000
	s_add_i32 s69, s70, 0x2000
	s_add_u32 s30, s36, 0x10000
	s_addc_u32 s31, s37, 0
	s_add_i32 s68, s57, s46
	ds_read_b128 v[144:147], v151
	ds_read_b128 v[156:159], v151 offset:1024
	ds_read_b128 v[160:163], v151 offset:2048
	ds_read_b128 v[164:167], v151 offset:3072
	s_add_i32 s67, s68, 0x2000
	s_add_i32 s66, 0, 0x18000
	s_add_u32 s28, s34, 0x10000
	s_addc_u32 s29, s35, 0
	s_add_i32 s65, s66, s46
	s_add_i32 s64, 0, 0x1c000
	s_add_i32 s63, s65, 0x2000
	s_add_u32 s26, s36, 0x10080
	s_addc_u32 s27, s37, 0
	s_add_i32 s62, s64, s46
	s_add_i32 s61, s62, 0x2000
	v_lshl_add_u64 v[148:149], s[38:39], 0, v[136:137]
	ds_read_b128 v[168:171], v152
	ds_read_b128 v[172:175], v152 offset:1024
	ds_read_b128 v[176:179], v152 offset:2048
	ds_read_b128 v[180:183], v152 offset:3072
	ds_read_b128 v[184:187], v152 offset:4096
	ds_read_b128 v[188:191], v152 offset:5120
	ds_read_b128 v[192:195], v152 offset:6144
	ds_read_b128 v[196:199], v152 offset:7168
	global_load_lds_dwordx4 v[148:149], off
	v_lshl_add_u64 v[148:149], s[38:39], 0, v[132:133]
	s_mov_b32 m0, s71
	s_nop 0
	global_load_lds_dwordx4 v[148:149], off
	s_waitcnt lgkmcnt(8)
	s_barrier
	s_waitcnt lgkmcnt(0)
	s_setprio 1
	s_waitcnt lgkmcnt(0)
	v_mfma_f32_16x16x32_bf16 v[126:129], v[144:147], v[168:171], v[126:129]
	v_mfma_f32_16x16x32_bf16 v[122:125], v[160:163], v[168:171], v[122:125]
	v_mfma_f32_16x16x32_bf16 v[110:113], v[144:147], v[176:179], v[110:113]
	v_mfma_f32_16x16x32_bf16 v[106:109], v[160:163], v[176:179], v[106:109]
	v_mfma_f32_16x16x32_bf16 v[94:97], v[144:147], v[184:187], v[94:97]
	v_mfma_f32_16x16x32_bf16 v[90:93], v[160:163], v[184:187], v[90:93]
	v_mfma_f32_16x16x32_bf16 v[78:81], v[144:147], v[192:195], v[78:81]
	v_mfma_f32_16x16x32_bf16 v[74:77], v[160:163], v[192:195], v[74:77]
	v_mfma_f32_16x16x32_bf16 v[126:129], v[156:159], v[172:175], v[126:129]
	v_mfma_f32_16x16x32_bf16 v[122:125], v[164:167], v[172:175], v[122:125]
	v_mfma_f32_16x16x32_bf16 v[110:113], v[156:159], v[180:183], v[110:113]
	v_mfma_f32_16x16x32_bf16 v[106:109], v[164:167], v[180:183], v[106:109]
	v_mfma_f32_16x16x32_bf16 v[94:97], v[156:159], v[188:191], v[94:97]
	v_mfma_f32_16x16x32_bf16 v[90:93], v[164:167], v[188:191], v[90:93]
	v_mfma_f32_16x16x32_bf16 v[78:81], v[156:159], v[196:199], v[78:81]
	v_mfma_f32_16x16x32_bf16 v[74:77], v[164:167], v[196:199], v[74:77]
	s_setprio 0
	s_barrier
	s_mov_b32 m0, s70
	v_lshl_add_u64 v[148:149], s[36:37], 0, v[138:139]
	ds_read_b128 v[200:203], v153
	ds_read_b128 v[204:207], v153 offset:1024
	ds_read_b128 v[208:211], v153 offset:2048
	ds_read_b128 v[212:215], v153 offset:3072
	global_load_lds_dwordx4 v[148:149], off
	v_lshl_add_u64 v[216:217], s[36:37], 0, v[134:135]
	s_mov_b32 m0, s69
	s_nop 0
	global_load_lds_dwordx4 v[216:217], off
	s_barrier
	s_waitcnt lgkmcnt(0)
	s_setprio 1
	s_waitcnt lgkmcnt(0)
	v_mfma_f32_16x16x32_bf16 v[118:121], v[200:203], v[168:171], v[118:121]
	v_mfma_f32_16x16x32_bf16 v[114:117], v[208:211], v[168:171], v[114:117]
	v_mfma_f32_16x16x32_bf16 v[102:105], v[200:203], v[176:179], v[102:105]
	v_mfma_f32_16x16x32_bf16 v[98:101], v[208:211], v[176:179], v[98:101]
	v_mfma_f32_16x16x32_bf16 v[86:89], v[200:203], v[184:187], v[86:89]
	v_mfma_f32_16x16x32_bf16 v[82:85], v[208:211], v[184:187], v[82:85]
	v_mfma_f32_16x16x32_bf16 v[70:73], v[200:203], v[192:195], v[70:73]
	v_mfma_f32_16x16x32_bf16 v[66:69], v[208:211], v[192:195], v[66:69]
	v_mfma_f32_16x16x32_bf16 v[118:121], v[204:207], v[172:175], v[118:121]
	v_mfma_f32_16x16x32_bf16 v[114:117], v[212:215], v[172:175], v[114:117]
	v_mfma_f32_16x16x32_bf16 v[102:105], v[204:207], v[180:183], v[102:105]
	v_mfma_f32_16x16x32_bf16 v[98:101], v[212:215], v[180:183], v[98:101]
	v_mfma_f32_16x16x32_bf16 v[86:89], v[204:207], v[188:191], v[86:89]
	v_mfma_f32_16x16x32_bf16 v[82:85], v[212:215], v[188:191], v[82:85]
	v_mfma_f32_16x16x32_bf16 v[70:73], v[204:207], v[196:199], v[70:73]
	v_mfma_f32_16x16x32_bf16 v[66:69], v[212:215], v[196:199], v[66:69]
	s_setprio 0
	s_mov_b32 m0, s19
	v_lshl_add_u64 v[218:219], s[34:35], 0, v[136:137]
	s_barrier
	ds_read_b128 v[168:171], v152 offset:16384
	ds_read_b128 v[172:175], v152 offset:17408
	ds_read_b128 v[176:179], v152 offset:18432
	ds_read_b128 v[180:183], v152 offset:19456
	ds_read_b128 v[184:187], v152 offset:20480
	ds_read_b128 v[188:191], v152 offset:21504
	ds_read_b128 v[192:195], v152 offset:22528
	ds_read_b128 v[196:199], v152 offset:23552
	global_load_lds_dwordx4 v[218:219], off
	v_lshl_add_u64 v[220:221], s[34:35], 0, v[132:133]
	s_mov_b32 m0, s49
	s_nop 0
	global_load_lds_dwordx4 v[220:221], off
	s_barrier
	s_waitcnt lgkmcnt(0)
	s_setprio 1
	s_waitcnt lgkmcnt(0)
	v_mfma_f32_16x16x32_bf16 v[62:65], v[144:147], v[168:171], v[62:65]
	v_mfma_f32_16x16x32_bf16 v[58:61], v[160:163], v[168:171], v[58:61]
	v_mfma_f32_16x16x32_bf16 v[46:49], v[144:147], v[176:179], v[46:49]
	v_mfma_f32_16x16x32_bf16 v[42:45], v[160:163], v[176:179], v[42:45]
	v_mfma_f32_16x16x32_bf16 v[30:33], v[144:147], v[184:187], v[30:33]
	v_mfma_f32_16x16x32_bf16 v[26:29], v[160:163], v[184:187], v[26:29]
	v_mfma_f32_16x16x32_bf16 v[14:17], v[144:147], v[192:195], v[14:17]
	v_mfma_f32_16x16x32_bf16 v[10:13], v[160:163], v[192:195], v[10:13]
	v_mfma_f32_16x16x32_bf16 v[62:65], v[156:159], v[172:175], v[62:65]
	v_mfma_f32_16x16x32_bf16 v[58:61], v[164:167], v[172:175], v[58:61]
	v_mfma_f32_16x16x32_bf16 v[46:49], v[156:159], v[180:183], v[46:49]
	v_mfma_f32_16x16x32_bf16 v[42:45], v[164:167], v[180:183], v[42:45]
	v_mfma_f32_16x16x32_bf16 v[30:33], v[156:159], v[188:191], v[30:33]
	v_mfma_f32_16x16x32_bf16 v[26:29], v[164:167], v[188:191], v[26:29]
	v_mfma_f32_16x16x32_bf16 v[14:17], v[156:159], v[196:199], v[14:17]
	v_mfma_f32_16x16x32_bf16 v[10:13], v[164:167], v[196:199], v[10:13]
	s_setprio 0
	s_barrier
	s_mov_b32 m0, s68
	v_lshl_add_u64 v[144:145], s[30:31], 0, v[138:139]
	global_load_lds_dwordx4 v[144:145], off
	v_lshl_add_u64 v[144:145], s[30:31], 0, v[134:135]
	s_mov_b32 m0, s67
	s_nop 0
	global_load_lds_dwordx4 v[144:145], off
	s_waitcnt vmcnt(6)
	s_barrier
	s_setprio 1
	v_mfma_f32_16x16x32_bf16 v[54:57], v[200:203], v[168:171], v[54:57]
	v_mfma_f32_16x16x32_bf16 v[50:53], v[208:211], v[168:171], v[50:53]
	v_mfma_f32_16x16x32_bf16 v[38:41], v[200:203], v[176:179], v[38:41]
	v_mfma_f32_16x16x32_bf16 v[34:37], v[208:211], v[176:179], v[34:37]
	v_mfma_f32_16x16x32_bf16 v[22:25], v[200:203], v[184:187], v[22:25]
	v_mfma_f32_16x16x32_bf16 v[18:21], v[208:211], v[184:187], v[18:21]
	v_mfma_f32_16x16x32_bf16 v[6:9], v[200:203], v[192:195], v[6:9]
	v_mfma_f32_16x16x32_bf16 v[2:5], v[208:211], v[192:195], v[2:5]
	v_mfma_f32_16x16x32_bf16 v[54:57], v[204:207], v[172:175], v[54:57]
	v_mfma_f32_16x16x32_bf16 v[50:53], v[212:215], v[172:175], v[50:53]
	v_mfma_f32_16x16x32_bf16 v[38:41], v[204:207], v[180:183], v[38:41]
	v_mfma_f32_16x16x32_bf16 v[34:37], v[212:215], v[180:183], v[34:37]
	v_mfma_f32_16x16x32_bf16 v[22:25], v[204:207], v[188:191], v[22:25]
	v_mfma_f32_16x16x32_bf16 v[18:21], v[212:215], v[188:191], v[18:21]
	v_mfma_f32_16x16x32_bf16 v[6:9], v[204:207], v[196:199], v[6:9]
	v_mfma_f32_16x16x32_bf16 v[2:5], v[212:215], v[196:199], v[2:5]
	s_setprio 0
	v_add_u32_e32 v164, s66, v131
	s_barrier
	ds_read_b128 v[144:147], v164
	ds_read_b128 v[156:159], v164 offset:1024
	ds_read_b128 v[160:163], v164 offset:2048
	ds_read_b128 v[164:167], v164 offset:3072
	s_mov_b32 m0, s50
	v_lshl_add_u64 v[200:201], s[28:29], 0, v[136:137]
	ds_read_b128 v[168:171], v152 offset:32768
	ds_read_b128 v[172:175], v152 offset:33792
	ds_read_b128 v[176:179], v152 offset:34816
	ds_read_b128 v[180:183], v152 offset:35840
	ds_read_b128 v[184:187], v152 offset:36864
	ds_read_b128 v[188:191], v152 offset:37888
	ds_read_b128 v[192:195], v152 offset:38912
	ds_read_b128 v[196:199], v152 offset:39936
	global_load_lds_dwordx4 v[200:201], off
	v_lshl_add_u64 v[200:201], s[28:29], 0, v[132:133]
	s_mov_b32 m0, s51
	s_nop 0
	global_load_lds_dwordx4 v[200:201], off
	s_waitcnt lgkmcnt(8)
	s_barrier
	s_waitcnt lgkmcnt(0)
	s_setprio 1
	s_waitcnt lgkmcnt(0)
	v_mfma_f32_16x16x32_bf16 v[126:129], v[144:147], v[168:171], v[126:129]
	v_mfma_f32_16x16x32_bf16 v[122:125], v[160:163], v[168:171], v[122:125]
	v_mfma_f32_16x16x32_bf16 v[110:113], v[144:147], v[176:179], v[110:113]
	v_mfma_f32_16x16x32_bf16 v[106:109], v[160:163], v[176:179], v[106:109]
	v_mfma_f32_16x16x32_bf16 v[94:97], v[144:147], v[184:187], v[94:97]
	v_mfma_f32_16x16x32_bf16 v[90:93], v[160:163], v[184:187], v[90:93]
	v_mfma_f32_16x16x32_bf16 v[78:81], v[144:147], v[192:195], v[78:81]
	v_mfma_f32_16x16x32_bf16 v[74:77], v[160:163], v[192:195], v[74:77]
	v_mfma_f32_16x16x32_bf16 v[126:129], v[156:159], v[172:175], v[126:129]
	v_mfma_f32_16x16x32_bf16 v[122:125], v[164:167], v[172:175], v[122:125]
	v_mfma_f32_16x16x32_bf16 v[110:113], v[156:159], v[180:183], v[110:113]
	v_mfma_f32_16x16x32_bf16 v[106:109], v[164:167], v[180:183], v[106:109]
	v_mfma_f32_16x16x32_bf16 v[94:97], v[156:159], v[188:191], v[94:97]
	v_mfma_f32_16x16x32_bf16 v[90:93], v[164:167], v[188:191], v[90:93]
	v_mfma_f32_16x16x32_bf16 v[78:81], v[156:159], v[196:199], v[78:81]
	v_mfma_f32_16x16x32_bf16 v[74:77], v[164:167], v[196:199], v[74:77]
	s_setprio 0
	s_barrier
	s_mov_b32 m0, s65
	v_add_u32_e32 v212, s64, v131
	v_lshl_add_u64 v[148:149], v[148:149], 0, s[8:9]
	ds_read_b128 v[200:203], v212
	ds_read_b128 v[204:207], v212 offset:1024
	ds_read_b128 v[208:211], v212 offset:2048
	ds_read_b128 v[212:215], v212 offset:3072
	global_load_lds_dwordx4 v[148:149], off
	v_lshl_add_u64 v[148:149], v[216:217], 0, s[8:9]
	s_mov_b32 m0, s63
	s_nop 0
	global_load_lds_dwordx4 v[148:149], off
	s_barrier
	s_waitcnt lgkmcnt(0)
	s_setprio 1
	s_waitcnt lgkmcnt(0)
	v_mfma_f32_16x16x32_bf16 v[118:121], v[200:203], v[168:171], v[118:121]
	v_mfma_f32_16x16x32_bf16 v[114:117], v[208:211], v[168:171], v[114:117]
	v_mfma_f32_16x16x32_bf16 v[102:105], v[200:203], v[176:179], v[102:105]
	v_mfma_f32_16x16x32_bf16 v[98:101], v[208:211], v[176:179], v[98:101]
	v_mfma_f32_16x16x32_bf16 v[86:89], v[200:203], v[184:187], v[86:89]
	v_mfma_f32_16x16x32_bf16 v[82:85], v[208:211], v[184:187], v[82:85]
	v_mfma_f32_16x16x32_bf16 v[70:73], v[200:203], v[192:195], v[70:73]
	v_mfma_f32_16x16x32_bf16 v[66:69], v[208:211], v[192:195], v[66:69]
	v_mfma_f32_16x16x32_bf16 v[118:121], v[204:207], v[172:175], v[118:121]
	v_mfma_f32_16x16x32_bf16 v[114:117], v[212:215], v[172:175], v[114:117]
	v_mfma_f32_16x16x32_bf16 v[102:105], v[204:207], v[180:183], v[102:105]
	v_mfma_f32_16x16x32_bf16 v[98:101], v[212:215], v[180:183], v[98:101]
	v_mfma_f32_16x16x32_bf16 v[86:89], v[204:207], v[188:191], v[86:89]
	v_mfma_f32_16x16x32_bf16 v[82:85], v[212:215], v[188:191], v[82:85]
	v_mfma_f32_16x16x32_bf16 v[70:73], v[204:207], v[196:199], v[70:73]
	v_mfma_f32_16x16x32_bf16 v[66:69], v[212:215], v[196:199], v[66:69]
	s_setprio 0
	s_mov_b32 m0, s53
	v_lshl_add_u64 v[148:149], v[218:219], 0, s[8:9]
	s_barrier
	ds_read_b128 v[168:171], v152 offset:49152
	ds_read_b128 v[172:175], v152 offset:50176
	ds_read_b128 v[176:179], v152 offset:51200
	ds_read_b128 v[180:183], v152 offset:52224
	ds_read_b128 v[184:187], v152 offset:53248
	ds_read_b128 v[188:191], v152 offset:54272
	ds_read_b128 v[192:195], v152 offset:55296
	ds_read_b128 v[196:199], v152 offset:56320
	global_load_lds_dwordx4 v[148:149], off
	v_lshl_add_u64 v[148:149], v[220:221], 0, s[8:9]
	s_mov_b32 m0, s54
	s_nop 0
	global_load_lds_dwordx4 v[148:149], off
	s_barrier
	s_waitcnt lgkmcnt(0)
	s_setprio 1
	s_waitcnt lgkmcnt(0)
	v_mfma_f32_16x16x32_bf16 v[62:65], v[144:147], v[168:171], v[62:65]
	v_mfma_f32_16x16x32_bf16 v[58:61], v[160:163], v[168:171], v[58:61]
	v_mfma_f32_16x16x32_bf16 v[46:49], v[144:147], v[176:179], v[46:49]
	v_mfma_f32_16x16x32_bf16 v[42:45], v[160:163], v[176:179], v[42:45]
	v_mfma_f32_16x16x32_bf16 v[30:33], v[144:147], v[184:187], v[30:33]
	v_mfma_f32_16x16x32_bf16 v[26:29], v[160:163], v[184:187], v[26:29]
	v_mfma_f32_16x16x32_bf16 v[14:17], v[144:147], v[192:195], v[14:17]
	v_mfma_f32_16x16x32_bf16 v[10:13], v[160:163], v[192:195], v[10:13]
	v_mfma_f32_16x16x32_bf16 v[62:65], v[156:159], v[172:175], v[62:65]
	v_mfma_f32_16x16x32_bf16 v[58:61], v[164:167], v[172:175], v[58:61]
	v_mfma_f32_16x16x32_bf16 v[46:49], v[156:159], v[180:183], v[46:49]
	v_mfma_f32_16x16x32_bf16 v[42:45], v[164:167], v[180:183], v[42:45]
	v_mfma_f32_16x16x32_bf16 v[30:33], v[156:159], v[188:191], v[30:33]
	v_mfma_f32_16x16x32_bf16 v[26:29], v[164:167], v[188:191], v[26:29]
	v_mfma_f32_16x16x32_bf16 v[14:17], v[156:159], v[196:199], v[14:17]
	v_mfma_f32_16x16x32_bf16 v[10:13], v[164:167], v[196:199], v[10:13]
	s_setprio 0
	s_barrier
	s_mov_b32 m0, s62
	v_lshl_add_u64 v[144:145], s[26:27], 0, v[138:139]
	global_load_lds_dwordx4 v[144:145], off
	v_lshl_add_u64 v[144:145], s[26:27], 0, v[134:135]
	s_mov_b32 m0, s61
	s_nop 0
	global_load_lds_dwordx4 v[144:145], off
	s_waitcnt vmcnt(6)
	s_barrier
	s_setprio 1
	v_mfma_f32_16x16x32_bf16 v[54:57], v[200:203], v[168:171], v[54:57]
	v_mfma_f32_16x16x32_bf16 v[50:53], v[208:211], v[168:171], v[50:53]
	v_mfma_f32_16x16x32_bf16 v[38:41], v[200:203], v[176:179], v[38:41]
	v_mfma_f32_16x16x32_bf16 v[34:37], v[208:211], v[176:179], v[34:37]
	v_mfma_f32_16x16x32_bf16 v[22:25], v[200:203], v[184:187], v[22:25]
	v_mfma_f32_16x16x32_bf16 v[18:21], v[208:211], v[184:187], v[18:21]
	v_mfma_f32_16x16x32_bf16 v[6:9], v[200:203], v[192:195], v[6:9]
	v_mfma_f32_16x16x32_bf16 v[2:5], v[208:211], v[192:195], v[2:5]
	v_mfma_f32_16x16x32_bf16 v[54:57], v[204:207], v[172:175], v[54:57]
	v_mfma_f32_16x16x32_bf16 v[50:53], v[212:215], v[172:175], v[50:53]
	v_mfma_f32_16x16x32_bf16 v[38:41], v[204:207], v[180:183], v[38:41]
	v_mfma_f32_16x16x32_bf16 v[34:37], v[212:215], v[180:183], v[34:37]
	v_mfma_f32_16x16x32_bf16 v[22:25], v[204:207], v[188:191], v[22:25]
	v_mfma_f32_16x16x32_bf16 v[18:21], v[212:215], v[188:191], v[18:21]
	v_mfma_f32_16x16x32_bf16 v[6:9], v[204:207], v[196:199], v[6:9]
	v_mfma_f32_16x16x32_bf16 v[2:5], v[212:215], v[196:199], v[2:5]
	s_setprio 0
	s_movk_i32 s28, 0x100
	s_andn2_b64 vcc, exec, s[24:25]
	s_mov_b64 s[26:27], -1
	s_mov_b64 s[24:25], 0
	s_barrier
	s_cbranch_vccz .LBB0_2283
	v_lshl_add_u32 v144, s18, 8, v1
	v_ashrrev_i32_e32 v145, 31, v144
	v_lshl_add_u64 v[146:147], v[144:145], 2, s[2:3]
	global_load_dword v168, v[146:147], off
	global_load_dword v178, v[146:147], off offset:64
	global_load_dword v179, v[146:147], off offset:128
	global_load_dword v180, v[146:147], off offset:192
	global_load_dword v181, v[146:147], off offset:512
	global_load_dword v182, v[146:147], off offset:576
	global_load_dword v183, v[146:147], off offset:640
	global_load_dword v184, v[146:147], off offset:704
	s_lshl_b32 s11, s58, 8
	s_cmp_eq_u32 s58, 64
	s_cselect_b64 vcc, -1, 0
	s_mov_b32 s13, 0x17c0000
	s_and_b64 s[20:21], vcc, exec
	s_cselect_b32 s18, 0, s11
	s_cselect_b32 s13, s13, 0x22940000
	s_cselect_b32 s11, 8, 14
	v_or_b32_e32 v164, s18, v150
	s_add_u32 s20, s6, s13
	v_lshlrev_b64 v[156:157], s11, v[144:145]
	s_addc_u32 s21, s7, 0
	v_ashrrev_i32_e32 v165, 31, v164
	v_cvt_f32_i32_e32 v145, v164
	v_or_b32_e32 v158, 1, v164
	v_or_b32_e32 v159, 2, v164
	v_or_b32_e32 v161, 4, v164
	v_or_b32_e32 v166, 7, v164
	v_or_b32_e32 v160, 3, v164
	v_or_b32_e32 v162, 5, v164
	v_or_b32_e32 v163, 6, v164
	v_or_b32_e32 v167, 0x80, v164
	v_lshl_add_u64 v[148:149], v[164:165], 1, s[20:21]
	v_cvt_f32_i32_e32 v158, v158
	v_cvt_f32_i32_e32 v159, v159
	v_cvt_f32_i32_e32 v165, v161
	v_cvt_f32_i32_e32 v172, v166
	v_cvt_f32_i32_e32 v160, v160
	v_cvt_f32_i32_e32 v170, v162
	v_cvt_f32_i32_e32 v171, v163
	v_cvt_f32_i32_e32 v173, v167
	v_cndmask_b32_e32 v169, v154, v155, vcc
	v_mul_f32_e64 v163, v169, -v145
	v_lshl_add_u64 v[166:167], v[156:157], 1, v[148:149]
	v_mul_f32_e64 v162, v169, -v158
	v_mul_f32_e64 v161, v169, -v159
	v_mul_f32_e64 v159, v169, -v165
	v_mul_f32_e64 v156, v169, -v172
	v_mul_f32_e64 v160, v169, -v160
	v_mul_f32_e64 v158, v169, -v170
	v_mul_f32_e64 v157, v169, -v171
	v_mul_f32_e64 v145, v169, -v173
	s_and_b64 vcc, exec, s[0:1]
	s_mov_b32 s58, s10
	s_mov_b32 s18, s12
	s_mov_b64 s[22:23], s[16:17]
	s_mov_b64 s[20:21], s[14:15]
	s_waitcnt vmcnt(0)
	v_mul_f32_e64 v165, v163, |v168|
	v_mul_f32_e64 v170, v162, |v168|
	v_mul_f32_e64 v173, v159, |v168|
	v_mul_f32_e64 v176, v156, |v168|
	v_mul_f32_e32 v165, 0x3fb8aa3b, v165
	v_mul_f32_e64 v171, v161, |v168|
	v_mul_f32_e64 v172, v160, |v168|
	v_mul_f32_e64 v174, v158, |v168|
	v_mul_f32_e64 v175, v157, |v168|
	v_mul_f32_e32 v170, 0x3fb8aa3b, v170
	v_mul_f32_e32 v173, 0x3fb8aa3b, v173
	v_mul_f32_e32 v176, 0x3fb8aa3b, v176
	v_exp_f32_e32 v165, v165
	v_mul_f32_e64 v177, v145, |v168|
	v_mul_f32_e32 v171, 0x3fb8aa3b, v171
	v_mul_f32_e32 v172, 0x3fb8aa3b, v172
	v_mul_f32_e32 v174, 0x3fb8aa3b, v174
	v_mul_f32_e32 v175, 0x3fb8aa3b, v175
	v_exp_f32_e32 v170, v170
	v_exp_f32_e32 v173, v173
	v_exp_f32_e32 v176, v176
	v_mul_f32_e32 v177, 0x3fb8aa3b, v177
	v_exp_f32_e32 v171, v171
	v_exp_f32_e32 v172, v172
	v_exp_f32_e32 v174, v174
	v_exp_f32_e32 v175, v175
	v_exp_f32_e32 v177, v177
	v_add_f32_e32 v165, 0x3d4ccccd, v165
	v_add_f32_e32 v170, 0x3d4ccccd, v170
	v_add_f32_e32 v173, 0x3d4ccccd, v173
	v_add_f32_e32 v176, 0x3d4ccccd, v176
	v_mul_f32_e32 v126, v126, v165
	v_add_f32_e32 v171, 0x3d4ccccd, v171
	v_add_f32_e32 v172, 0x3d4ccccd, v172
	v_add_f32_e32 v174, 0x3d4ccccd, v174
	v_add_f32_e32 v175, 0x3d4ccccd, v175
	v_mul_f32_e32 v127, v127, v170
	v_mul_f32_e32 v165, v122, v173
	v_mul_f32_e32 v125, v125, v176
	v_cvt_pk_bf16_f32 v122, v126, v127
	v_or_b32_e32 v126, 0x81, v164
	v_mul_f32_e32 v128, v128, v171
	v_mul_f32_e32 v129, v129, v172
	v_mul_f32_e32 v170, v123, v174
	v_mul_f32_e32 v171, v124, v175
	v_cvt_pk_bf16_f32 v123, v128, v129
	v_cvt_pk_bf16_f32 v124, v165, v170
	v_cvt_pk_bf16_f32 v125, v171, v125
	v_cvt_f32_i32_e32 v126, v126
	global_store_dwordx4 v[166:167], v[122:125], off
	v_or_b32_e32 v129, 0x86, v164
	v_cvt_f32_i32_e32 v129, v129
	v_add_f32_e32 v122, 0x3d4ccccd, v177
	v_mul_f32_e32 v124, v118, v122
	v_or_b32_e32 v122, 0x82, v164
	v_cvt_f32_i32_e32 v122, v122
	v_mul_f32_e64 v118, v169, -v126
	v_mul_f32_e64 v123, v118, |v168|
	v_mul_f32_e32 v123, 0x3fb8aa3b, v123
	v_mul_f32_e64 v122, v169, -v122
	v_exp_f32_e32 v123, v123
	v_mul_f32_e64 v125, v122, |v168|
	v_or_b32_e32 v126, 0x83, v164
	v_mul_f32_e32 v125, 0x3fb8aa3b, v125
	v_cvt_f32_i32_e32 v126, v126
	v_exp_f32_e32 v125, v125
	v_add_f32_e32 v123, 0x3d4ccccd, v123
	v_mul_f32_e32 v127, v119, v123
	v_mul_f32_e64 v119, v169, -v126
	v_add_f32_e32 v123, 0x3d4ccccd, v125
	v_mul_f32_e64 v125, v119, |v168|
	v_mul_f32_e32 v125, 0x3fb8aa3b, v125
	v_exp_f32_e32 v125, v125
	v_or_b32_e32 v126, 0x84, v164
	v_cvt_f32_i32_e32 v126, v126
	v_mul_f32_e32 v128, v120, v123
	v_add_f32_e32 v120, 0x3d4ccccd, v125
	v_mul_f32_e32 v125, v121, v120
	v_mul_f32_e64 v120, v169, -v126
	v_mul_f32_e64 v123, v120, |v168|
	v_mul_f32_e32 v123, 0x3fb8aa3b, v123
	v_exp_f32_e32 v123, v123
	v_or_b32_e32 v121, 0x85, v164
	v_cvt_f32_i32_e32 v121, v121
	v_cvt_pk_bf16_f32 v124, v124, v127
	v_add_f32_e32 v123, 0x3d4ccccd, v123
	v_mul_f32_e32 v165, v114, v123
	v_or_b32_e32 v114, 0x87, v164
	v_cvt_f32_i32_e32 v114, v114
	v_mul_f32_e64 v121, v169, -v121
	v_mul_f32_e64 v126, v121, |v168|
	v_mul_f32_e64 v123, v169, -v129
	v_mul_f32_e32 v126, 0x3fb8aa3b, v126
	v_mul_f32_e64 v129, v123, |v168|
	v_mul_f32_e64 v114, v169, -v114
	v_exp_f32_e32 v126, v126
	v_mul_f32_e32 v129, 0x3fb8aa3b, v129
	v_mul_f32_e64 v164, v114, |v168|
	v_exp_f32_e32 v129, v129
	v_mul_f32_e32 v164, 0x3fb8aa3b, v164
	v_exp_f32_e32 v164, v164
	v_add_f32_e32 v126, 0x3d4ccccd, v126
	v_mul_f32_e32 v115, v115, v126
	v_add_f32_e32 v126, 0x3d4ccccd, v129
	v_mul_f32_e32 v116, v116, v126
	v_add_f32_e32 v126, 0x3d4ccccd, v164
	v_mul_f32_e32 v117, v117, v126
	v_cvt_pk_bf16_f32 v125, v128, v125
	v_cvt_pk_bf16_f32 v126, v165, v115
	v_cvt_pk_bf16_f32 v127, v116, v117
	v_or_b32_e32 v116, 16, v144
	v_ashrrev_i32_e32 v117, 31, v116
	global_store_dwordx4 v[166:167], v[124:127], off offset:256
	s_nop 1
	v_lshl_add_u64 v[124:125], v[116:117], 2, s[2:3]
	s_nop 1
	v_mov_b32_e32 v115, v178
	v_lshlrev_b64 v[116:117], s11, v[116:117]
	v_lshl_add_u64 v[116:117], v[116:117], 1, v[148:149]
	s_nop 0
	v_mul_f32_e64 v124, v163, |v115|
	v_mul_f32_e64 v125, v162, |v115|
	v_mul_f32_e32 v124, 0x3fb8aa3b, v124
	v_mul_f32_e32 v125, 0x3fb8aa3b, v125
	v_exp_f32_e32 v124, v124
	v_exp_f32_e32 v125, v125
	v_mul_f32_e64 v128, v159, |v115|
	v_mul_f32_e64 v126, v161, |v115|
	v_add_f32_e32 v124, 0x3d4ccccd, v124
	v_add_f32_e32 v125, 0x3d4ccccd, v125
	v_mul_f32_e32 v110, v110, v124
	v_mul_f32_e32 v111, v111, v125
	v_mul_f32_e32 v124, 0x3fb8aa3b, v128
	v_mul_f32_e64 v125, v158, |v115|
	v_mul_f32_e32 v126, 0x3fb8aa3b, v126
	v_exp_f32_e32 v124, v124
	v_mul_f32_e32 v125, 0x3fb8aa3b, v125
	v_exp_f32_e32 v126, v126
	v_exp_f32_e32 v125, v125
	v_mul_f32_e64 v127, v160, |v115|
	v_add_f32_e32 v124, 0x3d4ccccd, v124
	v_mul_f32_e32 v127, 0x3fb8aa3b, v127
	v_add_f32_e32 v126, 0x3d4ccccd, v126
	v_mul_f32_e32 v124, v106, v124
	v_add_f32_e32 v106, 0x3d4ccccd, v125
	v_mul_f32_e64 v125, v157, |v115|
	v_exp_f32_e32 v127, v127
	v_mul_f32_e32 v112, v112, v126
	v_mul_f32_e32 v125, 0x3fb8aa3b, v125
	v_mul_f32_e64 v126, v156, |v115|
	v_exp_f32_e32 v125, v125
	v_mul_f32_e32 v126, 0x3fb8aa3b, v126
	v_exp_f32_e32 v126, v126
	v_add_f32_e32 v127, 0x3d4ccccd, v127
	v_mul_f32_e32 v113, v113, v127
	v_mul_f32_e32 v127, v107, v106
	v_add_f32_e32 v106, 0x3d4ccccd, v125
	v_mul_f32_e32 v125, v108, v106
	v_add_f32_e32 v106, 0x3d4ccccd, v126
	v_mul_f32_e32 v109, v109, v106
	v_cvt_pk_bf16_f32 v106, v110, v111
	v_mul_f32_e64 v110, v145, |v115|
	v_cvt_pk_bf16_f32 v107, v112, v113
	v_mul_f32_e32 v110, 0x3fb8aa3b, v110
	v_mul_f32_e64 v111, v118, |v115|
	v_cvt_pk_bf16_f32 v108, v124, v127
	v_cvt_pk_bf16_f32 v109, v125, v109
	v_exp_f32_e32 v110, v110
	v_mul_f32_e32 v111, 0x3fb8aa3b, v111
	global_store_dwordx4 v[116:117], v[106:109], off
	v_exp_f32_e32 v111, v111
	s_nop 0
	v_mul_f32_e64 v107, v122, |v115|
	v_mul_f32_e32 v107, 0x3fb8aa3b, v107
	v_mul_f32_e64 v108, v119, |v115|
	v_exp_f32_e32 v107, v107
	v_mul_f32_e32 v108, 0x3fb8aa3b, v108
	v_exp_f32_e32 v108, v108
	v_add_f32_e32 v106, 0x3d4ccccd, v110
	v_mul_f32_e32 v102, v102, v106
	v_add_f32_e32 v106, 0x3d4ccccd, v111
	v_mul_f32_e32 v103, v103, v106
	v_add_f32_e32 v106, 0x3d4ccccd, v107
	v_mul_f32_e64 v107, v120, |v115|
	v_mul_f32_e32 v104, v104, v106
	v_add_f32_e32 v106, 0x3d4ccccd, v108
	v_mul_f32_e32 v107, 0x3fb8aa3b, v107
	v_mul_f32_e64 v108, v121, |v115|
	v_exp_f32_e32 v107, v107
	v_mul_f32_e32 v108, 0x3fb8aa3b, v108
	v_exp_f32_e32 v108, v108
	v_mul_f32_e32 v105, v105, v106
	v_add_f32_e32 v106, 0x3d4ccccd, v107
	v_mul_f32_e64 v107, v123, |v115|
	v_mul_f32_e32 v106, v98, v106
	v_add_f32_e32 v98, 0x3d4ccccd, v108
	v_mul_f32_e32 v107, 0x3fb8aa3b, v107
	v_mul_f32_e64 v108, v114, |v115|
	v_exp_f32_e32 v107, v107
	v_mul_f32_e32 v108, 0x3fb8aa3b, v108
	v_exp_f32_e32 v108, v108
	v_mul_f32_e32 v109, v99, v98
	v_add_f32_e32 v98, 0x3d4ccccd, v107
	v_mul_f32_e32 v107, v100, v98
	v_add_f32_e32 v98, 0x3d4ccccd, v108
	v_mul_f32_e32 v101, v101, v98
	v_cvt_pk_bf16_f32 v98, v102, v103
	v_cvt_pk_bf16_f32 v99, v104, v105
	v_cvt_pk_bf16_f32 v100, v106, v109
	v_cvt_pk_bf16_f32 v101, v107, v101
	global_store_dwordx4 v[116:117], v[98:101], off offset:256
	s_nop 1
	v_or_b32_e32 v98, 32, v144
	v_ashrrev_i32_e32 v99, 31, v98
	v_lshl_add_u64 v[100:101], v[98:99], 2, s[2:3]
	s_nop 1
	v_mov_b32_e32 v100, v179
	v_lshlrev_b64 v[98:99], s11, v[98:99]
	v_lshl_add_u64 v[98:99], v[98:99], 1, v[148:149]
	s_nop 0
	v_mul_f32_e64 v102, v162, |v100|
	v_mul_f32_e64 v101, v163, |v100|
	v_mul_f32_e32 v102, 0x3fb8aa3b, v102
	v_mul_f32_e64 v103, v161, |v100|
	v_mul_f32_e32 v101, 0x3fb8aa3b, v101
	v_exp_f32_e32 v102, v102
	v_mul_f32_e32 v103, 0x3fb8aa3b, v103
	v_exp_f32_e32 v101, v101
	v_exp_f32_e32 v103, v103
	v_mul_f32_e64 v104, v160, |v100|
	v_add_f32_e32 v102, 0x3d4ccccd, v102
	v_mul_f32_e32 v104, 0x3fb8aa3b, v104
	v_add_f32_e32 v101, 0x3d4ccccd, v101
	v_mul_f32_e32 v95, v95, v102
	v_mul_f32_e64 v102, v159, |v100|
	v_exp_f32_e32 v104, v104
	v_mul_f32_e32 v94, v94, v101
	v_add_f32_e32 v101, 0x3d4ccccd, v103
	v_mul_f32_e32 v102, 0x3fb8aa3b, v102
	v_mul_f32_e64 v103, v158, |v100|
	v_exp_f32_e32 v102, v102
	v_mul_f32_e32 v103, 0x3fb8aa3b, v103
	v_exp_f32_e32 v103, v103
	v_mul_f32_e32 v96, v96, v101
	v_add_f32_e32 v101, 0x3d4ccccd, v104
	v_mul_f32_e32 v97, v97, v101
	v_add_f32_e32 v101, 0x3d4ccccd, v102
	v_mul_f32_e64 v102, v157, |v100|
	v_mul_f32_e32 v101, v90, v101
	v_add_f32_e32 v90, 0x3d4ccccd, v103
	v_mul_f32_e32 v102, 0x3fb8aa3b, v102
	v_mul_f32_e64 v103, v156, |v100|
	v_exp_f32_e32 v102, v102
	v_mul_f32_e32 v103, 0x3fb8aa3b, v103
	v_exp_f32_e32 v103, v103
	v_mul_f32_e32 v104, v91, v90
	v_add_f32_e32 v90, 0x3d4ccccd, v102
	v_mul_f32_e32 v102, v92, v90
	v_add_f32_e32 v90, 0x3d4ccccd, v103
	v_mul_f32_e32 v93, v93, v90
	v_cvt_pk_bf16_f32 v90, v94, v95
	v_mul_f32_e64 v94, v145, |v100|
	v_cvt_pk_bf16_f32 v91, v96, v97
	v_mul_f32_e32 v94, 0x3fb8aa3b, v94
	v_mul_f32_e64 v95, v118, |v100|
	v_cvt_pk_bf16_f32 v92, v101, v104
	v_cvt_pk_bf16_f32 v93, v102, v93
	v_exp_f32_e32 v94, v94
	v_mul_f32_e32 v95, 0x3fb8aa3b, v95
	global_store_dwordx4 v[98:99], v[90:93], off
	v_exp_f32_e32 v95, v95
	s_nop 0
	v_mul_f32_e64 v91, v122, |v100|
	v_mul_f32_e32 v91, 0x3fb8aa3b, v91
	v_mul_f32_e64 v92, v119, |v100|
	v_exp_f32_e32 v91, v91
	v_mul_f32_e32 v92, 0x3fb8aa3b, v92
	v_exp_f32_e32 v92, v92
	v_add_f32_e32 v90, 0x3d4ccccd, v94
	v_mul_f32_e32 v86, v86, v90
	v_add_f32_e32 v90, 0x3d4ccccd, v95
	v_mul_f32_e32 v87, v87, v90
	v_add_f32_e32 v90, 0x3d4ccccd, v91
	v_mul_f32_e64 v91, v120, |v100|
	v_mul_f32_e32 v88, v88, v90
	v_add_f32_e32 v90, 0x3d4ccccd, v92
	v_mul_f32_e32 v91, 0x3fb8aa3b, v91
	v_mul_f32_e64 v92, v121, |v100|
	v_exp_f32_e32 v91, v91
	v_mul_f32_e32 v92, 0x3fb8aa3b, v92
	v_exp_f32_e32 v92, v92
	v_mul_f32_e32 v89, v89, v90
	v_add_f32_e32 v90, 0x3d4ccccd, v91
	v_mul_f32_e64 v91, v123, |v100|
	v_mul_f32_e32 v90, v82, v90
	v_add_f32_e32 v82, 0x3d4ccccd, v92
	v_mul_f32_e32 v91, 0x3fb8aa3b, v91
	v_mul_f32_e64 v92, v114, |v100|
	v_exp_f32_e32 v91, v91
	v_mul_f32_e32 v92, 0x3fb8aa3b, v92
	v_exp_f32_e32 v92, v92
	v_mul_f32_e32 v93, v83, v82
	v_add_f32_e32 v82, 0x3d4ccccd, v91
	v_mul_f32_e32 v91, v84, v82
	v_add_f32_e32 v82, 0x3d4ccccd, v92
	v_mul_f32_e32 v85, v85, v82
	v_cvt_pk_bf16_f32 v82, v86, v87
	v_cvt_pk_bf16_f32 v83, v88, v89
	v_cvt_pk_bf16_f32 v84, v90, v93
	v_cvt_pk_bf16_f32 v85, v91, v85
	global_store_dwordx4 v[98:99], v[82:85], off offset:256
	s_nop 1
	v_or_b32_e32 v82, 48, v144
	v_ashrrev_i32_e32 v83, 31, v82
	v_lshl_add_u64 v[84:85], v[82:83], 2, s[2:3]
	s_nop 1
	v_mov_b32_e32 v84, v180
	v_lshlrev_b64 v[82:83], s11, v[82:83]
	v_lshl_add_u64 v[82:83], v[82:83], 1, v[148:149]
	s_nop 0
	v_mul_f32_e64 v85, v163, |v84|
	v_mul_f32_e32 v85, 0x3fb8aa3b, v85
	v_exp_f32_e32 v85, v85
	v_mul_f32_e64 v86, v162, |v84|
	v_mul_f32_e32 v86, 0x3fb8aa3b, v86
	v_mul_f32_e64 v87, v161, |v84|
	v_add_f32_e32 v85, 0x3d4ccccd, v85
	v_exp_f32_e32 v86, v86
	v_mul_f32_e32 v78, v78, v85
	v_mul_f32_e32 v85, 0x3fb8aa3b, v87
	v_mul_f32_e64 v87, v160, |v84|
	v_exp_f32_e32 v85, v85
	v_mul_f32_e32 v87, 0x3fb8aa3b, v87
	v_exp_f32_e32 v87, v87
	v_add_f32_e32 v86, 0x3d4ccccd, v86
	v_mul_f32_e32 v79, v79, v86
	v_add_f32_e32 v85, 0x3d4ccccd, v85
	v_mul_f32_e64 v86, v159, |v84|
	v_mul_f32_e32 v80, v80, v85
	v_add_f32_e32 v85, 0x3d4ccccd, v87
	v_mul_f32_e32 v86, 0x3fb8aa3b, v86
	v_mul_f32_e64 v87, v158, |v84|
	v_exp_f32_e32 v86, v86
	v_mul_f32_e32 v87, 0x3fb8aa3b, v87
	v_exp_f32_e32 v87, v87
	v_mul_f32_e32 v81, v81, v85
	v_add_f32_e32 v85, 0x3d4ccccd, v86
	v_mul_f32_e64 v86, v157, |v84|
	v_mul_f32_e32 v85, v74, v85
	v_add_f32_e32 v74, 0x3d4ccccd, v87
	v_mul_f32_e32 v86, 0x3fb8aa3b, v86
	v_mul_f32_e64 v87, v156, |v84|
	v_exp_f32_e32 v86, v86
	v_mul_f32_e32 v87, 0x3fb8aa3b, v87
	v_exp_f32_e32 v87, v87
	v_mul_f32_e32 v88, v75, v74
	v_add_f32_e32 v74, 0x3d4ccccd, v86
	v_mul_f32_e32 v86, v76, v74
	v_add_f32_e32 v74, 0x3d4ccccd, v87
	v_mul_f32_e32 v77, v77, v74
	v_cvt_pk_bf16_f32 v74, v78, v79
	v_mul_f32_e64 v78, v145, |v84|
	v_cvt_pk_bf16_f32 v75, v80, v81
	v_mul_f32_e32 v78, 0x3fb8aa3b, v78
	v_mul_f32_e64 v79, v118, |v84|
	v_cvt_pk_bf16_f32 v76, v85, v88
	v_cvt_pk_bf16_f32 v77, v86, v77
	v_exp_f32_e32 v78, v78
	v_mul_f32_e32 v79, 0x3fb8aa3b, v79
	global_store_dwordx4 v[82:83], v[74:77], off
	v_exp_f32_e32 v79, v79
	s_nop 0
	v_mul_f32_e64 v75, v122, |v84|
	v_mul_f32_e32 v75, 0x3fb8aa3b, v75
	v_mul_f32_e64 v76, v119, |v84|
	v_exp_f32_e32 v75, v75
	v_mul_f32_e32 v76, 0x3fb8aa3b, v76
	v_exp_f32_e32 v76, v76
	v_add_f32_e32 v74, 0x3d4ccccd, v78
	v_mul_f32_e32 v70, v70, v74
	v_add_f32_e32 v74, 0x3d4ccccd, v79
	v_mul_f32_e32 v71, v71, v74
	v_add_f32_e32 v74, 0x3d4ccccd, v75
	v_mul_f32_e64 v75, v120, |v84|
	v_mul_f32_e32 v72, v72, v74
	v_add_f32_e32 v74, 0x3d4ccccd, v76
	v_mul_f32_e32 v75, 0x3fb8aa3b, v75
	v_mul_f32_e64 v76, v121, |v84|
	v_exp_f32_e32 v75, v75
	v_mul_f32_e32 v76, 0x3fb8aa3b, v76
	v_exp_f32_e32 v76, v76
	v_mul_f32_e32 v73, v73, v74
	v_add_f32_e32 v74, 0x3d4ccccd, v75
	v_mul_f32_e64 v75, v123, |v84|
	v_mul_f32_e32 v74, v66, v74
	v_add_f32_e32 v66, 0x3d4ccccd, v76
	v_mul_f32_e32 v75, 0x3fb8aa3b, v75
	v_mul_f32_e64 v76, v114, |v84|
	v_exp_f32_e32 v75, v75
	v_mul_f32_e32 v76, 0x3fb8aa3b, v76
	v_exp_f32_e32 v76, v76
	v_mul_f32_e32 v77, v67, v66
	v_add_f32_e32 v66, 0x3d4ccccd, v75
	v_mul_f32_e32 v75, v68, v66
	v_add_f32_e32 v66, 0x3d4ccccd, v76
	v_mul_f32_e32 v69, v69, v66
	v_cvt_pk_bf16_f32 v66, v70, v71
	v_cvt_pk_bf16_f32 v67, v72, v73
	v_cvt_pk_bf16_f32 v68, v74, v77
	v_cvt_pk_bf16_f32 v69, v75, v69
	global_store_dwordx4 v[82:83], v[66:69], off offset:256
	s_nop 1
	v_mov_b32_e32 v68, v181
	s_nop 0
	v_mul_f32_e64 v70, v162, |v68|
	v_mul_f32_e64 v69, v163, |v68|
	v_mul_f32_e32 v69, 0x3fb8aa3b, v69
	v_exp_f32_e32 v69, v69
	v_mul_f32_e32 v70, 0x3fb8aa3b, v70
	v_exp_f32_e32 v70, v70
	v_mul_f32_e64 v71, v160, |v68|
	v_add_f32_e32 v69, 0x3d4ccccd, v69
	v_mul_f32_e32 v62, v62, v69
	v_add_f32_e32 v69, 0x3d4ccccd, v70
	v_mul_f32_e64 v70, v161, |v68|
	v_mul_f32_e32 v70, 0x3fb8aa3b, v70
	v_exp_f32_e32 v70, v70
	v_mul_f32_e32 v71, 0x3fb8aa3b, v71
	v_exp_f32_e32 v71, v71
	v_mul_f32_e32 v63, v63, v69
	v_add_f32_e32 v69, 0x3d4ccccd, v70
	v_mul_f32_e64 v70, v159, |v68|
	v_mul_f32_e32 v64, v64, v69
	v_add_f32_e32 v69, 0x3d4ccccd, v71
	v_mul_f32_e32 v70, 0x3fb8aa3b, v70
	v_mul_f32_e64 v71, v158, |v68|
	v_exp_f32_e32 v70, v70
	v_mul_f32_e32 v71, 0x3fb8aa3b, v71
	v_exp_f32_e32 v71, v71
	v_mul_f32_e32 v65, v65, v69
	v_add_f32_e32 v69, 0x3d4ccccd, v70
	v_mul_f32_e64 v70, v157, |v68|
	v_mul_f32_e32 v69, v58, v69
	v_add_f32_e32 v58, 0x3d4ccccd, v71
	v_mul_f32_e32 v70, 0x3fb8aa3b, v70
	v_mul_f32_e64 v71, v156, |v68|
	v_exp_f32_e32 v70, v70
	v_mul_f32_e32 v71, 0x3fb8aa3b, v71
	v_exp_f32_e32 v71, v71
	v_add_u32_e32 v66, 0x80, v144
	v_mul_f32_e32 v72, v59, v58
	v_add_f32_e32 v58, 0x3d4ccccd, v70
	v_ashrrev_i32_e32 v67, 31, v66
	v_mul_f32_e32 v70, v60, v58
	v_add_f32_e32 v58, 0x3d4ccccd, v71
	v_lshlrev_b64 v[66:67], s11, v[66:67]
	v_mul_f32_e32 v61, v61, v58
	v_cvt_pk_bf16_f32 v58, v62, v63
	v_mul_f32_e64 v62, v145, |v68|
	v_lshl_add_u64 v[66:67], v[66:67], 1, v[148:149]
	v_cvt_pk_bf16_f32 v59, v64, v65
	v_mul_f32_e32 v62, 0x3fb8aa3b, v62
	v_mul_f32_e64 v63, v118, |v68|
	v_cvt_pk_bf16_f32 v60, v69, v72
	v_cvt_pk_bf16_f32 v61, v70, v61
	v_exp_f32_e32 v62, v62
	v_mul_f32_e32 v63, 0x3fb8aa3b, v63
	global_store_dwordx4 v[66:67], v[58:61], off
	v_exp_f32_e32 v63, v63
	s_nop 0
	v_mul_f32_e64 v59, v122, |v68|
	v_mul_f32_e32 v59, 0x3fb8aa3b, v59
	v_mul_f32_e64 v60, v119, |v68|
	v_exp_f32_e32 v59, v59
	v_mul_f32_e32 v60, 0x3fb8aa3b, v60
	v_exp_f32_e32 v60, v60
	v_add_f32_e32 v58, 0x3d4ccccd, v62
	v_mul_f32_e32 v54, v54, v58
	v_add_f32_e32 v58, 0x3d4ccccd, v63
	v_mul_f32_e32 v55, v55, v58
	v_add_f32_e32 v58, 0x3d4ccccd, v59
	v_mul_f32_e64 v59, v120, |v68|
	v_mul_f32_e32 v56, v56, v58
	v_add_f32_e32 v58, 0x3d4ccccd, v60
	v_mul_f32_e32 v59, 0x3fb8aa3b, v59
	v_mul_f32_e64 v60, v121, |v68|
	v_exp_f32_e32 v59, v59
	v_mul_f32_e32 v60, 0x3fb8aa3b, v60
	v_exp_f32_e32 v60, v60
	v_mul_f32_e32 v57, v57, v58
	v_add_f32_e32 v58, 0x3d4ccccd, v59
	v_mul_f32_e64 v59, v123, |v68|
	v_mul_f32_e32 v58, v50, v58
	v_add_f32_e32 v50, 0x3d4ccccd, v60
	v_mul_f32_e32 v59, 0x3fb8aa3b, v59
	v_mul_f32_e64 v60, v114, |v68|
	v_exp_f32_e32 v59, v59
	v_mul_f32_e32 v60, 0x3fb8aa3b, v60
	v_exp_f32_e32 v60, v60
	v_mul_f32_e32 v61, v51, v50
	v_add_f32_e32 v50, 0x3d4ccccd, v59
	v_mul_f32_e32 v59, v52, v50
	v_add_f32_e32 v50, 0x3d4ccccd, v60
	v_mul_f32_e32 v53, v53, v50
	v_cvt_pk_bf16_f32 v50, v54, v55
	v_cvt_pk_bf16_f32 v51, v56, v57
	v_cvt_pk_bf16_f32 v52, v58, v61
	v_cvt_pk_bf16_f32 v53, v59, v53
	global_store_dwordx4 v[66:67], v[50:53], off offset:256
	s_nop 1
	v_mov_b32_e32 v52, v182
	s_nop 0
	v_mul_f32_e64 v54, v162, |v52|
	v_mul_f32_e64 v53, v163, |v52|
	v_mul_f32_e32 v53, 0x3fb8aa3b, v53
	v_exp_f32_e32 v53, v53
	v_mul_f32_e32 v54, 0x3fb8aa3b, v54
	v_exp_f32_e32 v54, v54
	v_mul_f32_e64 v55, v160, |v52|
	v_add_f32_e32 v53, 0x3d4ccccd, v53
	v_mul_f32_e32 v46, v46, v53
	v_add_f32_e32 v53, 0x3d4ccccd, v54
	v_mul_f32_e64 v54, v161, |v52|
	v_mul_f32_e32 v54, 0x3fb8aa3b, v54
	v_exp_f32_e32 v54, v54
	v_mul_f32_e32 v55, 0x3fb8aa3b, v55
	v_exp_f32_e32 v55, v55
	v_mul_f32_e32 v47, v47, v53
	v_add_f32_e32 v53, 0x3d4ccccd, v54
	v_mul_f32_e64 v54, v159, |v52|
	v_mul_f32_e32 v48, v48, v53
	v_add_f32_e32 v53, 0x3d4ccccd, v55
	v_mul_f32_e32 v54, 0x3fb8aa3b, v54
	v_mul_f32_e64 v55, v158, |v52|
	v_exp_f32_e32 v54, v54
	v_mul_f32_e32 v55, 0x3fb8aa3b, v55
	v_exp_f32_e32 v55, v55
	v_mul_f32_e32 v49, v49, v53
	v_add_f32_e32 v53, 0x3d4ccccd, v54
	v_mul_f32_e64 v54, v157, |v52|
	v_mul_f32_e32 v53, v42, v53
	v_add_f32_e32 v42, 0x3d4ccccd, v55
	v_mul_f32_e32 v54, 0x3fb8aa3b, v54
	v_mul_f32_e64 v55, v156, |v52|
	v_exp_f32_e32 v54, v54
	v_mul_f32_e32 v55, 0x3fb8aa3b, v55
	v_exp_f32_e32 v55, v55
	v_add_u32_e32 v50, 0x90, v144
	v_mul_f32_e32 v56, v43, v42
	v_add_f32_e32 v42, 0x3d4ccccd, v54
	v_ashrrev_i32_e32 v51, 31, v50
	v_mul_f32_e32 v54, v44, v42
	v_add_f32_e32 v42, 0x3d4ccccd, v55
	v_lshlrev_b64 v[50:51], s11, v[50:51]
	v_mul_f32_e32 v45, v45, v42
	v_cvt_pk_bf16_f32 v42, v46, v47
	v_mul_f32_e64 v46, v145, |v52|
	v_lshl_add_u64 v[50:51], v[50:51], 1, v[148:149]
	v_cvt_pk_bf16_f32 v43, v48, v49
	v_mul_f32_e32 v46, 0x3fb8aa3b, v46
	v_mul_f32_e64 v47, v118, |v52|
	v_cvt_pk_bf16_f32 v44, v53, v56
	v_cvt_pk_bf16_f32 v45, v54, v45
	v_exp_f32_e32 v46, v46
	v_mul_f32_e32 v47, 0x3fb8aa3b, v47
	global_store_dwordx4 v[50:51], v[42:45], off
	v_exp_f32_e32 v47, v47
	s_nop 0
	v_mul_f32_e64 v43, v122, |v52|
	v_mul_f32_e32 v43, 0x3fb8aa3b, v43
	v_mul_f32_e64 v44, v119, |v52|
	v_exp_f32_e32 v43, v43
	v_mul_f32_e32 v44, 0x3fb8aa3b, v44
	v_exp_f32_e32 v44, v44
	v_add_f32_e32 v42, 0x3d4ccccd, v46
	v_mul_f32_e32 v38, v38, v42
	v_add_f32_e32 v42, 0x3d4ccccd, v47
	v_mul_f32_e32 v39, v39, v42
	v_add_f32_e32 v42, 0x3d4ccccd, v43
	v_mul_f32_e64 v43, v120, |v52|
	v_mul_f32_e32 v40, v40, v42
	v_add_f32_e32 v42, 0x3d4ccccd, v44
	v_mul_f32_e32 v43, 0x3fb8aa3b, v43
	v_mul_f32_e64 v44, v121, |v52|
	v_exp_f32_e32 v43, v43
	v_mul_f32_e32 v44, 0x3fb8aa3b, v44
	v_exp_f32_e32 v44, v44
	v_mul_f32_e32 v41, v41, v42
	v_add_f32_e32 v42, 0x3d4ccccd, v43
	v_mul_f32_e64 v43, v123, |v52|
	v_mul_f32_e32 v42, v34, v42
	v_add_f32_e32 v34, 0x3d4ccccd, v44
	v_mul_f32_e32 v43, 0x3fb8aa3b, v43
	v_mul_f32_e64 v44, v114, |v52|
	v_exp_f32_e32 v43, v43
	v_mul_f32_e32 v44, 0x3fb8aa3b, v44
	v_exp_f32_e32 v44, v44
	v_mul_f32_e32 v45, v35, v34
	v_add_f32_e32 v34, 0x3d4ccccd, v43
	v_mul_f32_e32 v43, v36, v34
	v_add_f32_e32 v34, 0x3d4ccccd, v44
	v_mul_f32_e32 v37, v37, v34
	v_cvt_pk_bf16_f32 v34, v38, v39
	v_cvt_pk_bf16_f32 v35, v40, v41
	v_cvt_pk_bf16_f32 v36, v42, v45
	v_cvt_pk_bf16_f32 v37, v43, v37
	global_store_dwordx4 v[50:51], v[34:37], off offset:256
	s_nop 1
	v_mov_b32_e32 v36, v183
	s_nop 0
	v_mul_f32_e64 v38, v162, |v36|
	v_mul_f32_e64 v37, v163, |v36|
	v_mul_f32_e32 v37, 0x3fb8aa3b, v37
	v_exp_f32_e32 v37, v37
	v_mul_f32_e32 v38, 0x3fb8aa3b, v38
	v_exp_f32_e32 v38, v38
	v_mul_f32_e64 v39, v160, |v36|
	v_add_f32_e32 v37, 0x3d4ccccd, v37
	v_mul_f32_e32 v30, v30, v37
	v_add_f32_e32 v37, 0x3d4ccccd, v38
	v_mul_f32_e64 v38, v161, |v36|
	v_mul_f32_e32 v38, 0x3fb8aa3b, v38
	v_exp_f32_e32 v38, v38
	v_mul_f32_e32 v39, 0x3fb8aa3b, v39
	v_exp_f32_e32 v39, v39
	v_mul_f32_e32 v31, v31, v37
	v_add_f32_e32 v37, 0x3d4ccccd, v38
	v_mul_f32_e64 v38, v159, |v36|
	v_mul_f32_e32 v32, v32, v37
	v_add_f32_e32 v37, 0x3d4ccccd, v39
	v_mul_f32_e32 v38, 0x3fb8aa3b, v38
	v_mul_f32_e64 v39, v158, |v36|
	v_exp_f32_e32 v38, v38
	v_mul_f32_e32 v39, 0x3fb8aa3b, v39
	v_exp_f32_e32 v39, v39
	v_mul_f32_e32 v33, v33, v37
	v_add_f32_e32 v37, 0x3d4ccccd, v38
	v_mul_f32_e64 v38, v157, |v36|
	v_mul_f32_e32 v37, v26, v37
	v_add_f32_e32 v26, 0x3d4ccccd, v39
	v_mul_f32_e32 v38, 0x3fb8aa3b, v38
	v_mul_f32_e64 v39, v156, |v36|
	v_exp_f32_e32 v38, v38
	v_mul_f32_e32 v39, 0x3fb8aa3b, v39
	v_exp_f32_e32 v39, v39
	v_add_u32_e32 v34, 0xa0, v144
	v_mul_f32_e32 v40, v27, v26
	v_add_f32_e32 v26, 0x3d4ccccd, v38
	v_ashrrev_i32_e32 v35, 31, v34
	v_mul_f32_e32 v38, v28, v26
	v_add_f32_e32 v26, 0x3d4ccccd, v39
	v_lshlrev_b64 v[34:35], s11, v[34:35]
	v_mul_f32_e32 v29, v29, v26
	v_cvt_pk_bf16_f32 v26, v30, v31
	v_mul_f32_e64 v30, v145, |v36|
	v_lshl_add_u64 v[34:35], v[34:35], 1, v[148:149]
	v_cvt_pk_bf16_f32 v27, v32, v33
	v_mul_f32_e32 v30, 0x3fb8aa3b, v30
	v_mul_f32_e64 v31, v118, |v36|
	v_cvt_pk_bf16_f32 v28, v37, v40
	v_cvt_pk_bf16_f32 v29, v38, v29
	v_exp_f32_e32 v30, v30
	v_mul_f32_e32 v31, 0x3fb8aa3b, v31
	global_store_dwordx4 v[34:35], v[26:29], off
	v_exp_f32_e32 v31, v31
	s_nop 0
	v_mul_f32_e64 v27, v122, |v36|
	v_mul_f32_e32 v27, 0x3fb8aa3b, v27
	v_mul_f32_e64 v28, v119, |v36|
	v_exp_f32_e32 v27, v27
	v_mul_f32_e32 v28, 0x3fb8aa3b, v28
	v_exp_f32_e32 v28, v28
	v_add_f32_e32 v26, 0x3d4ccccd, v30
	v_mul_f32_e32 v22, v22, v26
	v_add_f32_e32 v26, 0x3d4ccccd, v31
	v_mul_f32_e32 v23, v23, v26
	v_add_f32_e32 v26, 0x3d4ccccd, v27
	v_mul_f32_e64 v27, v120, |v36|
	v_mul_f32_e32 v24, v24, v26
	v_add_f32_e32 v26, 0x3d4ccccd, v28
	v_mul_f32_e32 v27, 0x3fb8aa3b, v27
	v_mul_f32_e64 v28, v121, |v36|
	v_exp_f32_e32 v27, v27
	v_mul_f32_e32 v28, 0x3fb8aa3b, v28
	v_exp_f32_e32 v28, v28
	v_mul_f32_e32 v25, v25, v26
	v_add_f32_e32 v26, 0x3d4ccccd, v27
	v_mul_f32_e64 v27, v123, |v36|
	v_mul_f32_e32 v26, v18, v26
	v_add_f32_e32 v18, 0x3d4ccccd, v28
	v_mul_f32_e32 v27, 0x3fb8aa3b, v27
	v_mul_f32_e64 v28, v114, |v36|
	v_exp_f32_e32 v27, v27
	v_mul_f32_e32 v28, 0x3fb8aa3b, v28
	v_exp_f32_e32 v28, v28
	v_mul_f32_e32 v29, v19, v18
	v_add_f32_e32 v18, 0x3d4ccccd, v27
	v_mul_f32_e32 v27, v20, v18
	v_add_f32_e32 v18, 0x3d4ccccd, v28
	v_mul_f32_e32 v21, v21, v18
	v_cvt_pk_bf16_f32 v18, v22, v23
	v_cvt_pk_bf16_f32 v19, v24, v25
	v_cvt_pk_bf16_f32 v20, v26, v29
	v_cvt_pk_bf16_f32 v21, v27, v21
	global_store_dwordx4 v[34:35], v[18:21], off offset:256
	s_nop 1
	v_mov_b32_e32 v20, v184
	s_nop 0
	v_mul_f32_e64 v22, v162, |v20|
	v_mul_f32_e64 v21, v163, |v20|
	v_mul_f32_e32 v21, 0x3fb8aa3b, v21
	v_exp_f32_e32 v21, v21
	v_mul_f32_e32 v22, 0x3fb8aa3b, v22
	v_exp_f32_e32 v22, v22
	v_mul_f32_e64 v23, v160, |v20|
	v_add_f32_e32 v21, 0x3d4ccccd, v21
	v_mul_f32_e32 v14, v14, v21
	v_add_f32_e32 v21, 0x3d4ccccd, v22
	v_mul_f32_e64 v22, v161, |v20|
	v_mul_f32_e32 v22, 0x3fb8aa3b, v22
	v_exp_f32_e32 v22, v22
	v_mul_f32_e32 v23, 0x3fb8aa3b, v23
	v_exp_f32_e32 v23, v23
	v_mul_f32_e32 v15, v15, v21
	v_add_f32_e32 v21, 0x3d4ccccd, v22
	v_mul_f32_e64 v22, v159, |v20|
	v_mul_f32_e32 v16, v16, v21
	v_add_f32_e32 v21, 0x3d4ccccd, v23
	v_mul_f32_e32 v22, 0x3fb8aa3b, v22
	v_mul_f32_e64 v23, v158, |v20|
	v_exp_f32_e32 v22, v22
	v_mul_f32_e32 v23, 0x3fb8aa3b, v23
	v_exp_f32_e32 v23, v23
	v_mul_f32_e32 v17, v17, v21
	v_add_f32_e32 v21, 0x3d4ccccd, v22
	v_mul_f32_e64 v22, v157, |v20|
	v_mul_f32_e32 v21, v10, v21
	v_add_f32_e32 v10, 0x3d4ccccd, v23
	v_mul_f32_e32 v22, 0x3fb8aa3b, v22
	v_mul_f32_e64 v23, v156, |v20|
	v_exp_f32_e32 v22, v22
	v_mul_f32_e32 v23, 0x3fb8aa3b, v23
	v_exp_f32_e32 v23, v23
	v_add_u32_e32 v18, 0xb0, v144
	v_mul_f32_e32 v24, v11, v10
	v_add_f32_e32 v10, 0x3d4ccccd, v22
	v_ashrrev_i32_e32 v19, 31, v18
	v_mul_f32_e32 v22, v12, v10
	v_add_f32_e32 v10, 0x3d4ccccd, v23
	v_lshlrev_b64 v[18:19], s11, v[18:19]
	v_mul_f32_e32 v13, v13, v10
	v_cvt_pk_bf16_f32 v10, v14, v15
	v_mul_f32_e64 v14, v123, |v20|
	v_lshl_add_u64 v[18:19], v[18:19], 1, v[148:149]
	v_cvt_pk_bf16_f32 v11, v16, v17
	v_mul_f32_e32 v14, 0x3fb8aa3b, v14
	v_mul_f32_e64 v15, v121, |v20|
	v_cvt_pk_bf16_f32 v12, v21, v24
	v_cvt_pk_bf16_f32 v13, v22, v13
	v_exp_f32_e32 v14, v14
	v_mul_f32_e32 v15, 0x3fb8aa3b, v15
	global_store_dwordx4 v[18:19], v[10:13], off
	v_exp_f32_e32 v15, v15
	s_nop 0
	v_mul_f32_e64 v11, v120, |v20|
	v_mul_f32_e32 v11, 0x3fb8aa3b, v11
	v_exp_f32_e32 v11, v11
	v_mul_f32_e64 v12, v119, |v20|
	v_add_f32_e32 v10, 0x3d4ccccd, v14
	v_mul_f32_e32 v12, 0x3fb8aa3b, v12
	v_mul_f32_e32 v10, v4, v10
	v_add_f32_e32 v4, 0x3d4ccccd, v15
	v_exp_f32_e32 v12, v12
	v_mul_f32_e32 v4, v3, v4
	v_add_f32_e32 v3, 0x3d4ccccd, v11
	v_mul_f32_e32 v11, v2, v3
	v_mul_f32_e64 v3, v122, |v20|
	v_mul_f32_e32 v3, 0x3fb8aa3b, v3
	v_add_f32_e32 v2, 0x3d4ccccd, v12
	v_exp_f32_e32 v3, v3
	v_mul_f32_e64 v12, v118, |v20|
	v_mul_f32_e32 v12, 0x3fb8aa3b, v12
	v_exp_f32_e32 v12, v12
	v_mul_f32_e32 v9, v9, v2
	v_add_f32_e32 v2, 0x3d4ccccd, v3
	v_mul_f32_e32 v3, v8, v2
	v_mul_f32_e64 v8, v145, |v20|
	v_add_f32_e32 v2, 0x3d4ccccd, v12
	v_mul_f32_e32 v8, 0x3fb8aa3b, v8
	v_mul_f32_e64 v12, v114, |v20|
	v_exp_f32_e32 v8, v8
	v_mul_f32_e32 v12, 0x3fb8aa3b, v12
	v_exp_f32_e32 v12, v12
	v_mul_f32_e32 v2, v7, v2
	v_add_f32_e32 v7, 0x3d4ccccd, v8
	v_mul_f32_e32 v6, v6, v7
	v_add_f32_e32 v7, 0x3d4ccccd, v12
	v_mul_f32_e32 v5, v5, v7
	v_cvt_pk_bf16_f32 v2, v6, v2
	v_cvt_pk_bf16_f32 v3, v3, v9
	v_cvt_pk_bf16_f32 v4, v11, v4
	v_cvt_pk_bf16_f32 v5, v10, v5
	global_store_dwordx4 v[18:19], v[2:5], off offset:256
	s_cbranch_vccz .LBB0_2280
	s_waitcnt vmcnt(0)
	s_cmpk_gt_u32 s41, 0xff
	s_cbranch_scc1 .LBB0_2287
	s_barrier
